# layer-1 w_down transposition fully moved out of the prologue: half into the layer-0 idle slot (after the early compression/conv work), half into the layer-1 in-projection idle slot
# speedup vs baseline: 1.0011x; 1.0011x over previous
; #define GAS __attribute__((address_space(1)))
; #define LAS __attribute__((address_space(3)))
; #define LDS_WAIT() asm volatile("s_waitcnt lgkmcnt(0)" ::: "memory")
; __device__ __forceinline__ unsigned pk2(float lo, float hi) { return f2bf(lo) | (f2bf(hi) << 16); }
; __device__ __forceinline__ int nat_dim(int p) { return (p >> 1) + 64 * (p & 1); }
; template <int MAP, bool KS, bool KPERM = false>
; __device__ __forceinline__ void p0_transpose_item(const float* W, int K, int Nsrc, int nblk, bf16* WT, const float* ksA, const float* ksB, int ksplit, LAS float* scr, int item, int lane) {
;     const int kb = item / nblk, nb = item % nblk, k0 = 64 * kb, n0 = 32 * nb;
;     const int nr = n0 + (lane & 31); const int sc = MAP == 1 ? src_col_in(nr) : (MAP == 2 ? nat_dim(nr) : nr);
;     float v[32];
; #pragma unroll
;     for (int i = 0; i < 32; ++i) { const int k = k0 + 2 * i + (lane >> 5); const int ksrc = KPERM ? ((k & ~127) + nat_dim(k & 127)) : k;
;         v[i] = sc >= 0 ? W[(size_t)ksrc * Nsrc + sc] : 0.f; }
; #pragma unroll
;     for (int i = 0; i < 32; ++i) { const int kk = 2 * i + (lane >> 5); const int k = k0 + kk;
;         if (KS) v[i] *= (k < ksplit ? ksA[k] : ksB[k - ksplit]);
;         scr[kk * 33 + (lane & 31)] = v[i]; }
;     LDS_WAIT(); asm volatile("" ::: "memory");
;     const int c = lane & 7;
; #pragma unroll
;     for (int j = 0; j < 4; ++j) { const int n = (lane >> 3) + 8 * j; const LAS float* s = scr + (8 * c) * 33 + n;
;         v4u o; o.x = pk2(s[0 * 33], s[1 * 33]); o.y = pk2(s[2 * 33], s[3 * 33]); o.z = pk2(s[4 * 33], s[5 * 33]); o.w = pk2(s[6 * 33], s[7 * 33]);
;         *(GAS v4u*)(WT + (size_t)(n0 + n) * K + k0 + 8 * c) = o; }
; __global__ void __launch_bounds__(NWAVES * 64, 2) hybrid_fwd(Args args) {
;     ...
;         PHASE_IDS();
;         LAS float* scr = (LAS float*)(F.lds + RING_OFF + wave * 16384);
;         constexpr int I_IN = (DM / 64) * (NPROJ / 32), I_O = (DM / 64) * (DM / 32), I_UP = (DM / 64) * (FF / 32), I_DN = (FF / 64) * (DM / 32);
;         constexpr int I_L = I_IN + I_O + I_UP + I_DN;
;         for (int rep = 0; rep < REP_PRO; ++rep)
;         for (int it = gw; it < DEPTH * I_L; it += NGW) {
.LBB0_11:
	s_or_b64 exec, exec, s[0:1]
	v_mov_b32_e32 v1, v0
	v_readlane_b32 s1, v253, 2
	v_readfirstlane_b32 s0, v1
	s_ashr_i32 s0, s0, 6
	s_lshl_b32 s1, s1, 3
	s_add_i32 s80, s0, s1
	s_lshl_b32 s0, s0, 14
	v_lshlrev_b32_e32 v2, 3, v1
	v_writelane_b32 v253, s1, 46
	s_add_i32 s1, s0, 0
	v_and_b32_e32 v18, 31, v1
	v_bfe_u32 v20, v1, 3, 3
	v_and_b32_e32 v8, 56, v2
	s_lshl_b32 s96, s83, 3
	s_lshl_b32 s76, s83, 9
	v_bfe_u32 v6, v1, 5, 1
	v_lshl_add_u32 v25, v18, 2, s1
	s_movk_i32 s0, 0x84
	v_mul_u32_u24_e32 v2, 0x84, v8
	v_lshlrev_b32_e32 v3, 2, v20
	s_cmp_gt_i32 s80, 0x2f3ff
	v_mad_u32_u24 v19, v6, s0, v25
	v_mov_b32_e32 v11, 0
	v_add3_u32 v21, s1, v2, v3
	v_or_b32_e32 v22, 8, v20
	v_or_b32_e32 v23, 16, v20
	v_or_b32_e32 v24, 24, v20
	s_cbranch_scc1 .Lco3_hop_192
	v_and_b32_e32 v249, 63, v0
	v_lshrrev_b32_e32 v250, 6, v0
	v_readlane_b32 s15, v253, 2
	s_lshr_b32 s22, s15, 3
	s_and_b32 s23, s15, 7
	v_lshrrev_b32_e32 v246, 5, v249
	v_lshl_add_u32 v247, v250, 4, v246
	v_and_b32_e32 v248, 31, v249
	v_xor_b32_e32 v248, v248, v250
	v_lshlrev_b32_e32 v248, 4, v248
	v_lshl_add_u32 v209, v247, 9, v248
	v_add_u32_e32 v210, 0x10000, v209
	v_lshlrev_b32_e32 v96, 2, v247
	v_and_b32_e32 v248, 31, v249
	v_lshlrev_b32_e32 v248, 4, v248
	s_mov_b32 s20, 0x10000
	v_mad_u32_u24 v74, v247, s20, v248
	s_mov_b32 s20, 0x4000
	v_mad_u32_u24 v75, v247, s20, v248
	s_mov_b32 s20, 0xb140
	v_mad_u32_u24 v76, v247, s20, v248
	v_and_b32_e32 v246, 7, v249
	v_lshrrev_b32_e32 v247, 5, v249
	v_lshl_add_u32 v247, v250, 2, v247
	v_xor_b32_e32 v247, v247, v246
	v_lshlrev_b32_e32 v247, 4, v247
	v_lshl_add_u32 v247, v246, 13, v247
	v_bfe_u32 v248, v249, 3, 2
	v_lshl_add_u32 v211, v248, 2, v247
	v_add_u32_e32 v212, 0x10000, v211
	v_and_b32_e32 v246, 7, v249
	v_lshrrev_b32_e32 v247, 5, v249
	v_lshl_add_u32 v247, v250, 2, v247
	v_add_u32_e32 v247, 2, v247
	v_xor_b32_e32 v247, v247, v246
	v_lshlrev_b32_e32 v247, 4, v247
	v_lshl_add_u32 v247, v246, 13, v247
	v_bfe_u32 v248, v249, 3, 2
	v_lshl_add_u32 v213, v248, 2, v247
	v_add_u32_e32 v214, 0x10000, v213
	v_and_b32_e32 v246, 15, v249
	v_lshrrev_b32_e32 v247, 1, v246
	v_lshlrev_b32_e32 v248, 2, v250
	v_xor_b32_e32 v248, v248, v247
	v_lshlrev_b32_e32 v248, 4, v248
	v_lshl_add_u32 v248, v246, 12, v248
	v_lshrrev_b32_e32 v247, 4, v249
	v_lshl_add_u32 v112, v247, 2, v248
	v_add_u32_e32 v113, 0x10000, v112
	v_and_b32_e32 v246, 15, v249
	v_lshrrev_b32_e32 v247, 1, v246
	v_lshlrev_b32_e32 v248, 2, v250
	v_add_u32_e32 v248, 1, v248
	v_xor_b32_e32 v248, v248, v247
	v_lshlrev_b32_e32 v248, 4, v248
	v_lshl_add_u32 v248, v246, 12, v248
	v_lshrrev_b32_e32 v247, 4, v249
	v_lshl_add_u32 v114, v247, 2, v248
	v_add_u32_e32 v115, 0x10000, v114
	v_and_b32_e32 v246, 15, v249
	v_lshrrev_b32_e32 v247, 1, v246
	v_lshlrev_b32_e32 v248, 2, v250
	v_add_u32_e32 v248, 2, v248
	v_xor_b32_e32 v248, v248, v247
	v_lshlrev_b32_e32 v248, 4, v248
	v_lshl_add_u32 v248, v246, 12, v248
	v_lshrrev_b32_e32 v247, 4, v249
	v_lshl_add_u32 v116, v247, 2, v248
	v_add_u32_e32 v117, 0x10000, v116
	v_and_b32_e32 v246, 15, v249
	v_lshrrev_b32_e32 v247, 1, v246
	v_lshlrev_b32_e32 v248, 2, v250
	v_add_u32_e32 v248, 3, v248
	v_xor_b32_e32 v248, v248, v247
	v_lshlrev_b32_e32 v248, 4, v248
	v_lshl_add_u32 v248, v246, 12, v248
	v_lshrrev_b32_e32 v247, 4, v249
	v_lshl_add_u32 v118, v247, 2, v248
	v_add_u32_e32 v119, 0x10000, v118
	v_lshrrev_b32_e32 v246, 3, v249
	v_lshl_add_u32 v246, v250, 4, v246
	v_and_b32_e32 v247, 7, v249
	v_lshlrev_b32_e32 v247, 4, v247
	v_lshl_add_u32 v77, v246, 12, v247
	v_lshl_add_u32 v79, v246, 14, v247
	v_and_b32_e32 v248, 63, v246
	v_lshlrev_b32_e32 v248, 1, v248
	v_lshrrev_b32_e32 v246, 6, v246
	v_or_b32_e32 v248, v248, v246
	v_lshl_add_u32 v81, v248, 12, v247
	v_lshrrev_b32_e32 v246, 3, v249
	v_lshl_add_u32 v246, v250, 4, v246
	v_add_u32_e32 v246, 8, v246
	v_and_b32_e32 v247, 7, v249
	v_lshlrev_b32_e32 v247, 4, v247
	v_lshl_add_u32 v78, v246, 12, v247
	v_lshl_add_u32 v80, v246, 14, v247
	v_and_b32_e32 v248, 63, v246
	v_lshlrev_b32_e32 v248, 1, v248
	v_lshrrev_b32_e32 v246, 6, v246
	v_or_b32_e32 v248, v248, v246
	v_lshl_add_u32 v82, v248, 12, v247
	v_lshrrev_b32_e32 v246, 4, v249
	v_lshl_add_u32 v246, v250, 4, v246
	v_and_b32_e32 v247, 15, v249
	v_lshlrev_b32_e32 v247, 4, v247
	v_lshl_add_u32 v83, v246, 13, v247
	v_and_b32_e32 v248, 63, v246
	v_lshlrev_b32_e32 v248, 1, v248
	v_lshrrev_b32_e32 v246, 6, v246
	v_or_b32_e32 v248, v248, v246
	v_lshl_add_u32 v87, v248, 13, v247
	v_lshrrev_b32_e32 v246, 4, v249
	v_lshl_add_u32 v246, v250, 4, v246
	v_add_u32_e32 v246, 4, v246
	v_and_b32_e32 v247, 15, v249
	v_lshlrev_b32_e32 v247, 4, v247
	v_lshl_add_u32 v84, v246, 13, v247
	v_and_b32_e32 v248, 63, v246
	v_lshlrev_b32_e32 v248, 1, v248
	v_lshrrev_b32_e32 v246, 6, v246
	v_or_b32_e32 v248, v248, v246
	v_lshl_add_u32 v88, v248, 13, v247
	v_lshrrev_b32_e32 v246, 4, v249
	v_lshl_add_u32 v246, v250, 4, v246
	v_add_u32_e32 v246, 8, v246
	v_and_b32_e32 v247, 15, v249
	v_lshlrev_b32_e32 v247, 4, v247
	v_lshl_add_u32 v85, v246, 13, v247
	v_and_b32_e32 v248, 63, v246
	v_lshlrev_b32_e32 v248, 1, v248
	v_lshrrev_b32_e32 v246, 6, v246
	v_or_b32_e32 v248, v248, v246
	v_lshl_add_u32 v89, v248, 13, v247
	v_lshrrev_b32_e32 v246, 4, v249
	v_lshl_add_u32 v246, v250, 4, v246
	v_add_u32_e32 v246, 12, v246
	v_and_b32_e32 v247, 15, v249
	v_lshlrev_b32_e32 v247, 4, v247
	v_lshl_add_u32 v86, v246, 13, v247
	v_and_b32_e32 v248, 63, v246
	v_lshlrev_b32_e32 v248, 1, v248
	v_lshrrev_b32_e32 v246, 6, v246
	v_or_b32_e32 v248, v248, v246
	v_lshl_add_u32 v90, v248, 13, v247
	v_mov_b32_e32 v95, 0x43e00000
	s_mov_b32 s62, 0xc3e00000
	s_mov_b32 s63, 0x7fff
	s_mov_b32 s64, 0x07060302
	v_readlane_b32 s10, v253, 5
;     const int pr = item >> 1, kb = 2 * (pr / nblk) + (item & 1), nb = pr % nblk, k0 = 64 * kb, n0 = 32 * nb;
;     const int nr = n0 + (lane & 31); const int sc = MAP == 1 ? src_col_in(nr) : nr;
;     float v[32];
; #pragma unroll
;     for (int i = 0; i < 32; ++i) v[i] = sc >= 0 ? W[(size_t)(k0 + 2 * i + (lane >> 5)) * Nsrc + sc] : 0.f;
; #pragma unroll
;     for (int i = 0; i < 32; ++i) { const int k = k0 + 2 * i + (lane >> 5); float x = v[i] * wscale; if (KS) x *= (k < ksplit ? ksA[k] : ksB[k - ksplit]); scr[(2 * i + (lane >> 5)) * 33 + (lane & 31)] = x; }
; __global__ void __launch_bounds__(NWAVES * 64, 2) hybrid_fwd(Args args) {
;     ...
;         for (int it = gw; it < DEPTH * I_L; it += NGW) {
;             const int l = it / I_L; int r = it % I_L;
;             if (r < I_IN) { if (l >= PROJ_F8_FROM) p0_transpose_item_f8<true, 1>(args.in[2] + (size_t)l * DM * NSRC, DM, NSRC, NPROJ / 32, (unsigned char*)(ws + WS_WIN + l * SZ_WIN), WUP8_SCALE, args.in[1] + l * DM, args.in[1] + l * DM, DM, scr, r, lane);
;                 else p0_transpose_item<1, true>(args.in[2] + (size_t)l * DM * NSRC, DM, NSRC, NPROJ / 32, (bf16*)(ws + WS_WIN + l * SZ_WIN), args.in[1] + l * DM, args.in[1] + l * DM, DM, scr, r, lane); continue; } r -= I_IN;
;             if (r < I_O) { if (l >= WO_F8_FROM) p0_transpose_item_f8<true>(args.in[13] + (size_t)l * DM * DM, DM, DM, DM / 32, (unsigned char*)(ws + WS_WO + l * SZ_WO), 64.f, args.in[6] + l * 2048, args.in[12] + l * 2048, 2048, scr, r, lane);
;                 else p0_transpose_item<0, true>(args.in[13] + (size_t)l * DM * DM, DM, DM, DM / 32, (bf16*)(ws + WS_WO + l * SZ_WO), args.in[6] + l * 2048, args.in[12] + l * 2048, 2048, scr, r, lane); continue; } r -= I_O;
;             if (r < I_UP) { p0_transpose_item_f8<true>(args.in[15] + (size_t)l * DM * FF, DM, FF, FF / 32, (unsigned char*)(ws + WS_WUP + l * SZ_WUP), WUP8_SCALE, args.in[14] + l * DM, args.in[14] + l * DM, DM, scr, r, lane); continue; } r -= I_UP;
;             p0_transpose_item_f8<false>(args.in[16] + (size_t)l * FF * DM, FF, DM, DM / 32, (unsigned char*)(ws + WS_WDN + l * SZ_WDN), 128.f, args.in[16], args.in[16], 0, scr, r, lane);
	v_readlane_b32 s11, v253, 6
	s_lshl_b32 s20, s22, 9
	s_add_u32 s10, s10, s20
	s_addc_u32 s11, s11, 0
	global_load_dword v42, v96, s[10:11] offset:0
	global_load_dword v43, v96, s[10:11] offset:8
	global_load_dword v44, v96, s[10:11] offset:16
	global_load_dword v45, v96, s[10:11] offset:24
	global_load_dword v46, v96, s[10:11] offset:32
	global_load_dword v47, v96, s[10:11] offset:40
	global_load_dword v48, v96, s[10:11] offset:48
	global_load_dword v49, v96, s[10:11] offset:56
	v_readlane_b32 s10, v253, 5
	v_readlane_b32 s11, v253, 6
	s_lshl_b32 s20, s22, 9
	s_add_i32 s20, s20, 0x4000
	s_add_u32 s10, s10, s20
	s_addc_u32 s11, s11, 0
	global_load_dword v50, v96, s[10:11] offset:0
	global_load_dword v51, v96, s[10:11] offset:8
	global_load_dword v52, v96, s[10:11] offset:16
	global_load_dword v53, v96, s[10:11] offset:24
	global_load_dword v54, v96, s[10:11] offset:32
	global_load_dword v55, v96, s[10:11] offset:40
	global_load_dword v56, v96, s[10:11] offset:48
	global_load_dword v57, v96, s[10:11] offset:56
	v_readlane_b32 s10, v253, 15
	v_readlane_b32 s11, v253, 16
	v_readlane_b32 s20, v253, 27
	v_readlane_b32 s21, v253, 28
	s_sub_i32 s26, s22, 16
	s_cmp_lt_u32 s22, 16
	s_cselect_b32 s10, s10, s20
	s_cselect_b32 s11, s11, s21
	s_cselect_b32 s26, s22, s26
	s_lshl_b32 s20, s26, 9
	s_add_u32 s10, s10, s20
	s_addc_u32 s11, s11, 0
	global_load_dword v58, v96, s[10:11] offset:0
	global_load_dword v59, v96, s[10:11] offset:8
	global_load_dword v60, v96, s[10:11] offset:16
	global_load_dword v61, v96, s[10:11] offset:24
	global_load_dword v62, v96, s[10:11] offset:32
	global_load_dword v63, v96, s[10:11] offset:40
	global_load_dword v64, v96, s[10:11] offset:48
	global_load_dword v65, v96, s[10:11] offset:56
	v_readlane_b32 s10, v253, 15
	v_readlane_b32 s11, v253, 16
	v_readlane_b32 s20, v253, 27
	v_readlane_b32 s21, v253, 28
	s_sub_i32 s26, s22, 16
	s_cmp_lt_u32 s22, 16
	s_cselect_b32 s10, s10, s20
	s_cselect_b32 s11, s11, s21
	s_cselect_b32 s26, s22, s26
	s_lshl_b32 s20, s26, 9
	s_add_i32 s20, s20, 0x2000
	s_add_u32 s10, s10, s20
	s_addc_u32 s11, s11, 0
	global_load_dword v66, v96, s[10:11] offset:0
	global_load_dword v67, v96, s[10:11] offset:8
	global_load_dword v68, v96, s[10:11] offset:16
	global_load_dword v69, v96, s[10:11] offset:24
	global_load_dword v70, v96, s[10:11] offset:32
	global_load_dword v71, v96, s[10:11] offset:40
	global_load_dword v72, v96, s[10:11] offset:48
	global_load_dword v73, v96, s[10:11] offset:56
	v_readlane_b32 s10, v253, 31
	v_readlane_b32 s11, v253, 32
	s_lshl_b32 s20, s22, 9
	s_add_u32 s10, s10, s20
	s_addc_u32 s11, s11, 0
	global_load_dword v26, v96, s[10:11] offset:0
	global_load_dword v27, v96, s[10:11] offset:8
	global_load_dword v28, v96, s[10:11] offset:16
	global_load_dword v29, v96, s[10:11] offset:24
	global_load_dword v30, v96, s[10:11] offset:32
	global_load_dword v31, v96, s[10:11] offset:40
	global_load_dword v32, v96, s[10:11] offset:48
	global_load_dword v33, v96, s[10:11] offset:56
	v_readlane_b32 s10, v253, 31
	v_readlane_b32 s11, v253, 32
	s_lshl_b32 s20, s22, 9
	s_add_i32 s20, s20, 0x4000
	s_add_u32 s10, s10, s20
	s_addc_u32 s11, s11, 0
	global_load_dword v34, v96, s[10:11] offset:0
	global_load_dword v35, v96, s[10:11] offset:8
	global_load_dword v36, v96, s[10:11] offset:16
	global_load_dword v37, v96, s[10:11] offset:24
	global_load_dword v38, v96, s[10:11] offset:32
	global_load_dword v39, v96, s[10:11] offset:40
	global_load_dword v40, v96, s[10:11] offset:48
	global_load_dword v41, v96, s[10:11] offset:56
	s_waitcnt vmcnt(0)
	v_mul_f32_e32 v50, 0x42800000, v50
	v_mul_f32_e32 v51, 0x42800000, v51
	v_mul_f32_e32 v52, 0x42800000, v52
	v_mul_f32_e32 v53, 0x42800000, v53
	v_mul_f32_e32 v54, 0x42800000, v54
	v_mul_f32_e32 v55, 0x42800000, v55
	v_mul_f32_e32 v56, 0x42800000, v56
	v_mul_f32_e32 v57, 0x42800000, v57
	v_mul_f32_e32 v66, 0x42800000, v66
	v_mul_f32_e32 v67, 0x42800000, v67
	v_mul_f32_e32 v68, 0x42800000, v68
	v_mul_f32_e32 v69, 0x42800000, v69
	v_mul_f32_e32 v70, 0x42800000, v70
	v_mul_f32_e32 v71, 0x42800000, v71
	v_mul_f32_e32 v72, 0x42800000, v72
	v_mul_f32_e32 v73, 0x42800000, v73
	v_mul_f32_e32 v26, 0x42800000, v26
	v_mul_f32_e32 v27, 0x42800000, v27
	v_mul_f32_e32 v28, 0x42800000, v28
	v_mul_f32_e32 v29, 0x42800000, v29
	v_mul_f32_e32 v30, 0x42800000, v30
	v_mul_f32_e32 v31, 0x42800000, v31
	v_mul_f32_e32 v32, 0x42800000, v32
	v_mul_f32_e32 v33, 0x42800000, v33
	v_mul_f32_e32 v34, 0x42800000, v34
	v_mul_f32_e32 v35, 0x42800000, v35
	v_mul_f32_e32 v36, 0x42800000, v36
	v_mul_f32_e32 v37, 0x42800000, v37
	v_mul_f32_e32 v38, 0x42800000, v38
	v_mul_f32_e32 v39, 0x42800000, v39
	v_mul_f32_e32 v40, 0x42800000, v40
	v_mul_f32_e32 v41, 0x42800000, v41
	v_readlane_b32 s30, v253, 33
	v_readlane_b32 s31, v253, 34
	v_readlane_b32 s32, v253, 41
	v_readlane_b32 s33, v253, 42
	s_mul_i32 s20, s22, 0x800000
	s_lshl_b32 s21, s23, 9
	s_add_u32 s20, s20, s21
	s_add_u32 s30, s30, s20
	s_addc_u32 s31, s31, 0
	s_add_u32 s32, s32, 0xf600000
	s_addc_u32 s33, s33, 0
	s_lshl_b32 s20, s22, 7
	s_mul_i32 s21, s23, 0x80000
	s_add_u32 s20, s20, s21
	s_add_u32 s32, s32, s20
	s_addc_u32 s33, s33, 0
	v_readlane_b32 s34, v253, 33
	v_readlane_b32 s35, v253, 34
	v_readlane_b32 s36, v253, 41
	v_readlane_b32 s37, v253, 42
	s_add_u32 s34, s34, 0x10000000
	s_addc_u32 s35, s35, 0
	s_mul_i32 s20, s22, 0x800000
	s_lshl_b32 s21, s23, 9
	s_add_u32 s20, s20, s21
	s_add_u32 s34, s34, s20
	s_addc_u32 s35, s35, 0
	s_add_u32 s36, s36, 0x17600000
	s_addc_u32 s37, s37, 0
	s_lshl_b32 s20, s22, 7
	s_mul_i32 s21, s23, 0x80000
	s_add_u32 s20, s20, s21
	s_add_u32 s36, s36, s20
	s_addc_u32 s37, s37, 0
	v_readlane_b32 s38, v253, 35
; #define LDS_WAIT() asm volatile("s_waitcnt lgkmcnt(0)" ::: "memory")
;     const int pr = item >> 1, kb = 2 * (pr / nblk) + (item & 1), nb = pr % nblk, k0 = 64 * kb, n0 = 32 * nb;
;     const int nr = n0 + (lane & 31); const int sc = MAP == 1 ? src_col_in(nr) : nr;
;     float v[32];
; #pragma unroll
;     for (int i = 0; i < 32; ++i) v[i] = sc >= 0 ? W[(size_t)(k0 + 2 * i + (lane >> 5)) * Nsrc + sc] : 0.f;
; #pragma unroll
;     for (int i = 0; i < 32; ++i) { const int k = k0 + 2 * i + (lane >> 5); float x = v[i] * wscale; if (KS) x *= (k < ksplit ? ksA[k] : ksB[k - ksplit]); scr[(2 * i + (lane >> 5)) * 33 + (lane & 31)] = x; }
;     LDS_WAIT(); asm volatile("" ::: "memory");
; __global__ void __launch_bounds__(NWAVES * 64, 2) hybrid_fwd(Args args) {
;     ...
;             if (r < I_IN) { if (l >= PROJ_F8_FROM) p0_transpose_item_f8<true, 1>(args.in[2] + (size_t)l * DM * NSRC, DM, NSRC, NPROJ / 32, (unsigned char*)(ws + WS_WIN + l * SZ_WIN), WUP8_SCALE, args.in[1] + l * DM, args.in[1] + l * DM, DM, scr, r, lane);
;                 else p0_transpose_item<1, true>(args.in[2] + (size_t)l * DM * NSRC, DM, NSRC, NPROJ / 32, (bf16*)(ws + WS_WIN + l * SZ_WIN), args.in[1] + l * DM, args.in[1] + l * DM, DM, scr, r, lane); continue; } r -= I_IN;
;             if (r < I_O) { if (l >= WO_F8_FROM) p0_transpose_item_f8<true>(args.in[13] + (size_t)l * DM * DM, DM, DM, DM / 32, (unsigned char*)(ws + WS_WO + l * SZ_WO), 64.f, args.in[6] + l * 2048, args.in[12] + l * 2048, 2048, scr, r, lane);
;                 else p0_transpose_item<0, true>(args.in[13] + (size_t)l * DM * DM, DM, DM, DM / 32, (bf16*)(ws + WS_WO + l * SZ_WO), args.in[6] + l * 2048, args.in[12] + l * 2048, 2048, scr, r, lane); continue; } r -= I_O;
;             if (r < I_UP) { p0_transpose_item_f8<true>(args.in[15] + (size_t)l * DM * FF, DM, FF, FF / 32, (unsigned char*)(ws + WS_WUP + l * SZ_WUP), WUP8_SCALE, args.in[14] + l * DM, args.in[14] + l * DM, DM, scr, r, lane); continue; } r -= I_UP;
;             p0_transpose_item_f8<false>(args.in[16] + (size_t)l * FF * DM, FF, DM, DM / 32, (unsigned char*)(ws + WS_WDN + l * SZ_WDN), 128.f, args.in[16], args.in[16], 0, scr, r, lane);
	v_readlane_b32 s39, v253, 36
	v_readlane_b32 s40, v253, 41
	v_readlane_b32 s41, v253, 42
	s_mul_i32 s20, s22, 0x200000
	s_lshl_b32 s21, s23, 9
	s_add_u32 s20, s20, s21
	s_add_u32 s38, s38, s20
	s_addc_u32 s39, s39, 0
	s_add_u32 s40, s40, 0x1f600000
	s_addc_u32 s41, s41, 0
	s_lshl_b32 s20, s22, 7
	s_mul_i32 s21, s23, 0x200000
	s_add_u32 s20, s20, s21
	s_add_u32 s40, s40, s20
	s_addc_u32 s41, s41, 0
	v_readlane_b32 s42, v253, 35
	v_readlane_b32 s43, v253, 36
	v_readlane_b32 s44, v253, 41
	v_readlane_b32 s45, v253, 42
	s_add_u32 s42, s42, 0x10000000
	s_addc_u32 s43, s43, 0
	s_mul_i32 s20, s22, 0x200000
	s_lshl_b32 s21, s23, 9
	s_add_u32 s20, s20, s21
	s_add_u32 s42, s42, s20
	s_addc_u32 s43, s43, 0
	s_add_u32 s44, s44, 0x27600000
	s_addc_u32 s45, s45, 0
	s_lshl_b32 s20, s22, 7
	s_mul_i32 s21, s23, 0x200000
	s_add_u32 s20, s20, s21
	s_add_u32 s44, s44, s20
	s_addc_u32 s45, s45, 0
	v_readlane_b32 s46, v253, 7
	v_readlane_b32 s47, v253, 8
	v_readlane_b32 s48, v253, 41
	v_readlane_b32 s49, v253, 42
	s_mul_i32 s20, s22, 0x58a000
	s_add_u32 s46, s46, s20
	s_addc_u32 s47, s47, 0
	s_add_u32 s48, s48, 0x200000
	s_addc_u32 s49, s49, 0
	s_lshl_b32 s20, s22, 8
	s_add_u32 s48, s48, s20
	s_addc_u32 s49, s49, 0
	v_readlane_b32 s50, v253, 7
	v_readlane_b32 s51, v253, 8
	v_readlane_b32 s52, v253, 41
	v_readlane_b32 s53, v253, 42
	s_add_u32 s50, s50, 0xb140000
	s_addc_u32 s51, s51, 0
	s_mul_i32 s20, s22, 0x58a000
	s_add_u32 s50, s50, s20
	s_addc_u32 s51, s51, 0
	s_add_u32 s52, s52, 0x5c00000
	s_addc_u32 s53, s53, 0
	s_lshl_b32 s20, s22, 7
	s_add_u32 s52, s52, s20
	s_addc_u32 s53, s53, 0
	v_readlane_b32 s54, v253, 29
	v_readlane_b32 s55, v253, 30
	v_readlane_b32 s56, v253, 41
	v_readlane_b32 s57, v253, 42
	s_mul_i32 s20, s22, 0x200000
	s_lshl_b32 s21, s23, 9
	s_add_u32 s20, s20, s21
	s_add_u32 s54, s54, s20
	s_addc_u32 s55, s55, 0
	s_add_u32 s56, s56, 0xb600000
	s_addc_u32 s57, s57, 0
	s_lshl_b32 s20, s22, 8
	s_mul_i32 s21, s23, 0x100000
	s_add_u32 s20, s20, s21
	s_add_u32 s56, s56, s20
	s_addc_u32 s57, s57, 0
	v_readlane_b32 s58, v253, 29
	v_readlane_b32 s59, v253, 30
	v_readlane_b32 s60, v253, 41
	v_readlane_b32 s61, v253, 42
	s_add_u32 s58, s58, 0x4000000
	s_addc_u32 s59, s59, 0
	s_mul_i32 s20, s22, 0x200000
	s_lshl_b32 s21, s23, 9
	s_add_u32 s20, s20, s21
	s_add_u32 s58, s58, s20
	s_addc_u32 s59, s59, 0
	s_add_u32 s60, s60, 0xd600000
	s_addc_u32 s61, s61, 0
	s_lshl_b32 s20, s22, 7
	s_mul_i32 s21, s23, 0x80000
	s_add_u32 s20, s20, s21
	s_add_u32 s60, s60, s20
	s_addc_u32 s61, s61, 0
	s_mov_b64 s[8:9], s[30:31]
	global_load_dwordx4 v[144:147], v74, s[8:9]
	s_add_u32 s8, s8, 0x20000
	s_addc_u32 s9, s9, 0
	global_load_dwordx4 v[148:151], v74, s[8:9]
	s_add_u32 s8, s8, 0x20000
	s_addc_u32 s9, s9, 0
	global_load_dwordx4 v[152:155], v74, s[8:9]
	s_add_u32 s8, s8, 0x20000
	s_addc_u32 s9, s9, 0
	global_load_dwordx4 v[156:159], v74, s[8:9]
	s_add_u32 s8, s8, 0x20000
	s_addc_u32 s9, s9, 0
	global_load_dwordx4 v[160:163], v74, s[8:9]
	s_add_u32 s8, s8, 0x20000
	s_addc_u32 s9, s9, 0
	global_load_dwordx4 v[164:167], v74, s[8:9]
	s_add_u32 s8, s8, 0x20000
	s_addc_u32 s9, s9, 0
	global_load_dwordx4 v[168:171], v74, s[8:9]
	s_add_u32 s8, s8, 0x20000
	s_addc_u32 s9, s9, 0
	global_load_dwordx4 v[172:175], v74, s[8:9]
	s_add_u32 s8, s30, 0x1000
	s_addc_u32 s9, s31, 0
	global_load_dwordx4 v[176:179], v74, s[8:9]
	s_add_u32 s8, s8, 0x20000
	s_addc_u32 s9, s9, 0
	global_load_dwordx4 v[180:183], v74, s[8:9]
	s_add_u32 s8, s8, 0x20000
	s_addc_u32 s9, s9, 0
	global_load_dwordx4 v[184:187], v74, s[8:9]
	s_add_u32 s8, s8, 0x20000
	s_addc_u32 s9, s9, 0
	global_load_dwordx4 v[188:191], v74, s[8:9]
	s_add_u32 s8, s8, 0x20000
	s_addc_u32 s9, s9, 0
	global_load_dwordx4 v[192:195], v74, s[8:9]
	s_add_u32 s8, s8, 0x20000
	s_addc_u32 s9, s9, 0
	global_load_dwordx4 v[196:199], v74, s[8:9]
	s_add_u32 s8, s8, 0x20000
	s_addc_u32 s9, s9, 0
	global_load_dwordx4 v[200:203], v74, s[8:9]
	s_add_u32 s8, s8, 0x20000
	s_addc_u32 s9, s9, 0
	global_load_dwordx4 v[204:207], v74, s[8:9]
	s_waitcnt vmcnt(8)
	v_mul_f32_e32 v144, v26, v144
	v_mul_f32_e32 v145, v26, v145
	v_mul_f32_e32 v146, v26, v146
	v_mul_f32_e32 v147, v26, v147
	ds_write_b128 v209, v[144:147]
	v_mul_f32_e32 v148, v27, v148
	v_mul_f32_e32 v149, v27, v149
	v_mul_f32_e32 v150, v27, v150
	v_mul_f32_e32 v151, v27, v151
	ds_write_b128 v209, v[148:151] offset:1024
	v_mul_f32_e32 v152, v28, v152
	v_mul_f32_e32 v153, v28, v153
	v_mul_f32_e32 v154, v28, v154
	v_mul_f32_e32 v155, v28, v155
	ds_write_b128 v209, v[152:155] offset:2048
	v_mul_f32_e32 v156, v29, v156
	v_mul_f32_e32 v157, v29, v157
	v_mul_f32_e32 v158, v29, v158
	v_mul_f32_e32 v159, v29, v159
	ds_write_b128 v209, v[156:159] offset:3072
	v_mul_f32_e32 v160, v30, v160
	v_mul_f32_e32 v161, v30, v161
	v_mul_f32_e32 v162, v30, v162
	v_mul_f32_e32 v163, v30, v163
	ds_write_b128 v209, v[160:163] offset:4096
	v_mul_f32_e32 v164, v31, v164
	v_mul_f32_e32 v165, v31, v165
	v_mul_f32_e32 v166, v31, v166
	v_mul_f32_e32 v167, v31, v167
	ds_write_b128 v209, v[164:167] offset:5120
	v_mul_f32_e32 v168, v32, v168
	v_mul_f32_e32 v169, v32, v169
	v_mul_f32_e32 v170, v32, v170
	v_mul_f32_e32 v171, v32, v171
	ds_write_b128 v209, v[168:171] offset:6144
	v_mul_f32_e32 v172, v33, v172
	v_mul_f32_e32 v173, v33, v173
	v_mul_f32_e32 v174, v33, v174
	v_mul_f32_e32 v175, v33, v175
	ds_write_b128 v209, v[172:175] offset:7168
	s_waitcnt lgkmcnt(0)
	s_barrier
; #define GAS __attribute__((address_space(1)))
; #define LAS __attribute__((address_space(3)))
; #define LDS_WAIT() asm volatile("s_waitcnt lgkmcnt(0)" ::: "memory")
;     ...
; #pragma unroll
;     for (int i = 0; i < 32; ++i) v[i] = sc >= 0 ? W[(size_t)(k0 + 2 * i + (lane >> 5)) * Nsrc + sc] : 0.f;
; #pragma unroll
;     for (int i = 0; i < 32; ++i) { const int k = k0 + 2 * i + (lane >> 5); float x = v[i] * wscale; if (KS) x *= (k < ksplit ? ksA[k] : ksB[k - ksplit]); scr[(2 * i + (lane >> 5)) * 33 + (lane & 31)] = x; }
;     LDS_WAIT(); asm volatile("" ::: "memory");
;     const int c = lane & 7;
; #pragma unroll
;     for (int j = 0; j < 4; ++j) { const int n = (lane >> 3) + 8 * j; const LAS float* s = scr + (8 * c) * 33 + n;
;         const unsigned long long o = (unsigned long long)pg8::pk4_fp8(s[0 * 33], s[1 * 33], s[2 * 33], s[3 * 33]) | ((unsigned long long)pg8::pk4_fp8(s[4 * 33], s[5 * 33], s[6 * 33], s[7 * 33]) << 32);
;         *(GAS unsigned long long*)(WT + (size_t)(n0 + n) * K + k0 + 8 * c) = o; }
; __global__ void __launch_bounds__(NWAVES * 64, 2) hybrid_fwd(Args args) {
;     ...
;             if (r < I_UP) { p0_transpose_item_f8<true>(args.in[15] + (size_t)l * DM * FF, DM, FF, FF / 32, (unsigned char*)(ws + WS_WUP + l * SZ_WUP), WUP8_SCALE, args.in[14] + l * DM, args.in[14] + l * DM, DM, scr, r, lane); continue; } r -= I_UP;
	s_add_u32 s8, s30, 0x2000
	s_addc_u32 s9, s31, 0
	global_load_dwordx4 v[144:147], v74, s[8:9]
	s_add_u32 s8, s8, 0x20000
	s_addc_u32 s9, s9, 0
	global_load_dwordx4 v[148:151], v74, s[8:9]
	s_add_u32 s8, s8, 0x20000
	s_addc_u32 s9, s9, 0
	global_load_dwordx4 v[152:155], v74, s[8:9]
	s_add_u32 s8, s8, 0x20000
	s_addc_u32 s9, s9, 0
	global_load_dwordx4 v[156:159], v74, s[8:9]
	s_add_u32 s8, s8, 0x20000
	s_addc_u32 s9, s9, 0
	global_load_dwordx4 v[160:163], v74, s[8:9]
	s_add_u32 s8, s8, 0x20000
	s_addc_u32 s9, s9, 0
	global_load_dwordx4 v[164:167], v74, s[8:9]
	s_add_u32 s8, s8, 0x20000
	s_addc_u32 s9, s9, 0
	global_load_dwordx4 v[168:171], v74, s[8:9]
	s_add_u32 s8, s8, 0x20000
	s_addc_u32 s9, s9, 0
	global_load_dwordx4 v[172:175], v74, s[8:9]
	s_mov_b64 s[6:7], s[32:33]
	ds_read_b32 v226, v211
	ds_read_b32 v227, v211 offset:512
	ds_read_b32 v228, v211 offset:1024
	ds_read_b32 v229, v211 offset:1536
	ds_read_b32 v230, v211 offset:2048
	ds_read_b32 v231, v211 offset:2560
	ds_read_b32 v232, v211 offset:3072
	ds_read_b32 v233, v211 offset:3584
	ds_read_b32 v234, v211 offset:4096
	ds_read_b32 v235, v211 offset:4608
	ds_read_b32 v236, v211 offset:5120
	ds_read_b32 v237, v211 offset:5632
	ds_read_b32 v238, v211 offset:6144
	ds_read_b32 v239, v211 offset:6656
	ds_read_b32 v240, v211 offset:7168
	ds_read_b32 v241, v211 offset:7680
	s_waitcnt lgkmcnt(0)
	v_max_f32_e32 v226, v226, v226
	v_max_f32_e32 v227, v227, v227
	v_max_f32_e32 v228, v228, v228
	v_max_f32_e32 v229, v229, v229
	v_max_f32_e32 v230, v230, v230
	v_max_f32_e32 v231, v231, v231
	v_max_f32_e32 v232, v232, v232
	v_max_f32_e32 v233, v233, v233
	v_max_f32_e32 v234, v234, v234
	v_max_f32_e32 v235, v235, v235
	v_max_f32_e32 v236, v236, v236
	v_max_f32_e32 v237, v237, v237
	v_max_f32_e32 v238, v238, v238
	v_max_f32_e32 v239, v239, v239
	v_max_f32_e32 v240, v240, v240
	v_max_f32_e32 v241, v241, v241
	v_med3_f32 v226, v226, s62, v95
	v_med3_f32 v227, v227, s62, v95
	v_med3_f32 v228, v228, s62, v95
	v_med3_f32 v229, v229, s62, v95
	v_med3_f32 v230, v230, s62, v95
	v_med3_f32 v231, v231, s62, v95
	v_med3_f32 v232, v232, s62, v95
	v_med3_f32 v233, v233, s62, v95
	v_med3_f32 v234, v234, s62, v95
	v_med3_f32 v235, v235, s62, v95
	v_med3_f32 v236, v236, s62, v95
	v_med3_f32 v237, v237, s62, v95
	v_med3_f32 v238, v238, s62, v95
	v_med3_f32 v239, v239, s62, v95
	v_med3_f32 v240, v240, s62, v95
	v_med3_f32 v241, v241, s62, v95
	v_mov_b32_e32 v242, 0
	v_mov_b32_e32 v243, 0
	v_mov_b32_e32 v244, 0
	v_mov_b32_e32 v245, 0
	v_cvt_pk_fp8_f32 v242, v226, v227
	v_cvt_pk_fp8_f32 v243, v230, v231
	v_cvt_pk_fp8_f32 v244, v234, v235
	v_cvt_pk_fp8_f32 v245, v238, v239
	v_cvt_pk_fp8_f32 v242, v228, v229 op_sel:[0,0,1]
	v_cvt_pk_fp8_f32 v243, v232, v233 op_sel:[0,0,1]
	v_cvt_pk_fp8_f32 v244, v236, v237 op_sel:[0,0,1]
	v_cvt_pk_fp8_f32 v245, v240, v241 op_sel:[0,0,1]
	s_nop 0
	global_store_dwordx4 v77, v[242:245], s[6:7]
	ds_read_b32 v226, v213
	ds_read_b32 v227, v213 offset:512
	ds_read_b32 v228, v213 offset:1024
	ds_read_b32 v229, v213 offset:1536
	ds_read_b32 v230, v213 offset:2048
	ds_read_b32 v231, v213 offset:2560
	ds_read_b32 v232, v213 offset:3072
	ds_read_b32 v233, v213 offset:3584
	ds_read_b32 v234, v213 offset:4096
	ds_read_b32 v235, v213 offset:4608
	ds_read_b32 v236, v213 offset:5120
	ds_read_b32 v237, v213 offset:5632
	ds_read_b32 v238, v213 offset:6144
	ds_read_b32 v239, v213 offset:6656
	ds_read_b32 v240, v213 offset:7168
	ds_read_b32 v241, v213 offset:7680
	s_waitcnt lgkmcnt(0)
	v_max_f32_e32 v226, v226, v226
	v_max_f32_e32 v227, v227, v227
	v_max_f32_e32 v228, v228, v228
	v_max_f32_e32 v229, v229, v229
	v_max_f32_e32 v230, v230, v230
	v_max_f32_e32 v231, v231, v231
	v_max_f32_e32 v232, v232, v232
	v_max_f32_e32 v233, v233, v233
	v_max_f32_e32 v234, v234, v234
	v_max_f32_e32 v235, v235, v235
	v_max_f32_e32 v236, v236, v236
	v_max_f32_e32 v237, v237, v237
	v_max_f32_e32 v238, v238, v238
	v_max_f32_e32 v239, v239, v239
	v_max_f32_e32 v240, v240, v240
	v_max_f32_e32 v241, v241, v241
	v_med3_f32 v226, v226, s62, v95
	v_med3_f32 v227, v227, s62, v95
	v_med3_f32 v228, v228, s62, v95
	v_med3_f32 v229, v229, s62, v95
	v_med3_f32 v230, v230, s62, v95
	v_med3_f32 v231, v231, s62, v95
	v_med3_f32 v232, v232, s62, v95
	v_med3_f32 v233, v233, s62, v95
	v_med3_f32 v234, v234, s62, v95
	v_med3_f32 v235, v235, s62, v95
	v_med3_f32 v236, v236, s62, v95
	v_med3_f32 v237, v237, s62, v95
	v_med3_f32 v238, v238, s62, v95
	v_med3_f32 v239, v239, s62, v95
	v_med3_f32 v240, v240, s62, v95
	v_med3_f32 v241, v241, s62, v95
	v_mov_b32_e32 v242, 0
	v_mov_b32_e32 v243, 0
	v_mov_b32_e32 v244, 0
	v_mov_b32_e32 v245, 0
	v_cvt_pk_fp8_f32 v242, v226, v227
	v_cvt_pk_fp8_f32 v243, v230, v231
	v_cvt_pk_fp8_f32 v244, v234, v235
	v_cvt_pk_fp8_f32 v245, v238, v239
	v_cvt_pk_fp8_f32 v242, v228, v229 op_sel:[0,0,1]
	v_cvt_pk_fp8_f32 v243, v232, v233 op_sel:[0,0,1]
	v_cvt_pk_fp8_f32 v244, v236, v237 op_sel:[0,0,1]
	v_cvt_pk_fp8_f32 v245, v240, v241 op_sel:[0,0,1]
	s_nop 0
	global_store_dwordx4 v78, v[242:245], s[6:7]
	s_waitcnt vmcnt(10)
	v_mul_f32_e32 v176, v26, v176
	v_mul_f32_e32 v177, v26, v177
	v_mul_f32_e32 v178, v26, v178
	v_mul_f32_e32 v179, v26, v179
	ds_write_b128 v210, v[176:179]
	v_mul_f32_e32 v180, v27, v180
	v_mul_f32_e32 v181, v27, v181
	v_mul_f32_e32 v182, v27, v182
	v_mul_f32_e32 v183, v27, v183
	ds_write_b128 v210, v[180:183] offset:1024
	v_mul_f32_e32 v184, v28, v184
	v_mul_f32_e32 v185, v28, v185
	v_mul_f32_e32 v186, v28, v186
	v_mul_f32_e32 v187, v28, v187
	ds_write_b128 v210, v[184:187] offset:2048
	v_mul_f32_e32 v188, v29, v188
	v_mul_f32_e32 v189, v29, v189
	v_mul_f32_e32 v190, v29, v190
	v_mul_f32_e32 v191, v29, v191
	ds_write_b128 v210, v[188:191] offset:3072
	v_mul_f32_e32 v192, v30, v192
	v_mul_f32_e32 v193, v30, v193
	v_mul_f32_e32 v194, v30, v194
	v_mul_f32_e32 v195, v30, v195
	ds_write_b128 v210, v[192:195] offset:4096
	v_mul_f32_e32 v196, v31, v196
	v_mul_f32_e32 v197, v31, v197
	v_mul_f32_e32 v198, v31, v198
	v_mul_f32_e32 v199, v31, v199
	ds_write_b128 v210, v[196:199] offset:5120
	v_mul_f32_e32 v200, v32, v200
	v_mul_f32_e32 v201, v32, v201
	v_mul_f32_e32 v202, v32, v202
	v_mul_f32_e32 v203, v32, v203
	ds_write_b128 v210, v[200:203] offset:6144
	v_mul_f32_e32 v204, v33, v204
	v_mul_f32_e32 v205, v33, v205
	v_mul_f32_e32 v206, v33, v206
	v_mul_f32_e32 v207, v33, v207
	ds_write_b128 v210, v[204:207] offset:7168
	s_waitcnt lgkmcnt(0)
	s_barrier
; #define GAS __attribute__((address_space(1)))
; #define LAS __attribute__((address_space(3)))
; #define LDS_WAIT() asm volatile("s_waitcnt lgkmcnt(0)" ::: "memory")
;     ...
; #pragma unroll
;     for (int i = 0; i < 32; ++i) v[i] = sc >= 0 ? W[(size_t)(k0 + 2 * i + (lane >> 5)) * Nsrc + sc] : 0.f;
; #pragma unroll
;     for (int i = 0; i < 32; ++i) { const int k = k0 + 2 * i + (lane >> 5); float x = v[i] * wscale; if (KS) x *= (k < ksplit ? ksA[k] : ksB[k - ksplit]); scr[(2 * i + (lane >> 5)) * 33 + (lane & 31)] = x; }
;     LDS_WAIT(); asm volatile("" ::: "memory");
;     const int c = lane & 7;
; #pragma unroll
;     for (int j = 0; j < 4; ++j) { const int n = (lane >> 3) + 8 * j; const LAS float* s = scr + (8 * c) * 33 + n;
;         const unsigned long long o = (unsigned long long)pg8::pk4_fp8(s[0 * 33], s[1 * 33], s[2 * 33], s[3 * 33]) | ((unsigned long long)pg8::pk4_fp8(s[4 * 33], s[5 * 33], s[6 * 33], s[7 * 33]) << 32);
;         *(GAS unsigned long long*)(WT + (size_t)(n0 + n) * K + k0 + 8 * c) = o; }
; __global__ void __launch_bounds__(NWAVES * 64, 2) hybrid_fwd(Args args) {
;     ...
;             if (r < I_UP) { p0_transpose_item_f8<true>(args.in[15] + (size_t)l * DM * FF, DM, FF, FF / 32, (unsigned char*)(ws + WS_WUP + l * SZ_WUP), WUP8_SCALE, args.in[14] + l * DM, args.in[14] + l * DM, DM, scr, r, lane); continue; } r -= I_UP;
	s_add_u32 s8, s30, 0x3000
	s_addc_u32 s9, s31, 0
	global_load_dwordx4 v[176:179], v74, s[8:9]
	s_add_u32 s8, s8, 0x20000
	s_addc_u32 s9, s9, 0
	global_load_dwordx4 v[180:183], v74, s[8:9]
	s_add_u32 s8, s8, 0x20000
	s_addc_u32 s9, s9, 0
	global_load_dwordx4 v[184:187], v74, s[8:9]
	s_add_u32 s8, s8, 0x20000
	s_addc_u32 s9, s9, 0
	global_load_dwordx4 v[188:191], v74, s[8:9]
	s_add_u32 s8, s8, 0x20000
	s_addc_u32 s9, s9, 0
	global_load_dwordx4 v[192:195], v74, s[8:9]
	s_add_u32 s8, s8, 0x20000
	s_addc_u32 s9, s9, 0
	global_load_dwordx4 v[196:199], v74, s[8:9]
	s_add_u32 s8, s8, 0x20000
	s_addc_u32 s9, s9, 0
	global_load_dwordx4 v[200:203], v74, s[8:9]
	s_add_u32 s8, s8, 0x20000
	s_addc_u32 s9, s9, 0
	global_load_dwordx4 v[204:207], v74, s[8:9]
	s_add_u32 s6, s32, 0x400000
	s_addc_u32 s7, s33, 0
	ds_read_b32 v226, v212
	ds_read_b32 v227, v212 offset:512
	ds_read_b32 v228, v212 offset:1024
	ds_read_b32 v229, v212 offset:1536
	ds_read_b32 v230, v212 offset:2048
	ds_read_b32 v231, v212 offset:2560
	ds_read_b32 v232, v212 offset:3072
	ds_read_b32 v233, v212 offset:3584
	ds_read_b32 v234, v212 offset:4096
	ds_read_b32 v235, v212 offset:4608
	ds_read_b32 v236, v212 offset:5120
	ds_read_b32 v237, v212 offset:5632
	ds_read_b32 v238, v212 offset:6144
	ds_read_b32 v239, v212 offset:6656
	ds_read_b32 v240, v212 offset:7168
	ds_read_b32 v241, v212 offset:7680
	s_waitcnt lgkmcnt(0)
	v_max_f32_e32 v226, v226, v226
	v_max_f32_e32 v227, v227, v227
	v_max_f32_e32 v228, v228, v228
	v_max_f32_e32 v229, v229, v229
	v_max_f32_e32 v230, v230, v230
	v_max_f32_e32 v231, v231, v231
	v_max_f32_e32 v232, v232, v232
	v_max_f32_e32 v233, v233, v233
	v_max_f32_e32 v234, v234, v234
	v_max_f32_e32 v235, v235, v235
	v_max_f32_e32 v236, v236, v236
	v_max_f32_e32 v237, v237, v237
	v_max_f32_e32 v238, v238, v238
	v_max_f32_e32 v239, v239, v239
	v_max_f32_e32 v240, v240, v240
	v_max_f32_e32 v241, v241, v241
	v_med3_f32 v226, v226, s62, v95
	v_med3_f32 v227, v227, s62, v95
	v_med3_f32 v228, v228, s62, v95
	v_med3_f32 v229, v229, s62, v95
	v_med3_f32 v230, v230, s62, v95
	v_med3_f32 v231, v231, s62, v95
	v_med3_f32 v232, v232, s62, v95
	v_med3_f32 v233, v233, s62, v95
	v_med3_f32 v234, v234, s62, v95
	v_med3_f32 v235, v235, s62, v95
	v_med3_f32 v236, v236, s62, v95
	v_med3_f32 v237, v237, s62, v95
	v_med3_f32 v238, v238, s62, v95
	v_med3_f32 v239, v239, s62, v95
	v_med3_f32 v240, v240, s62, v95
	v_med3_f32 v241, v241, s62, v95
	v_mov_b32_e32 v242, 0
	v_mov_b32_e32 v243, 0
	v_mov_b32_e32 v244, 0
	v_mov_b32_e32 v245, 0
	v_cvt_pk_fp8_f32 v242, v226, v227
	v_cvt_pk_fp8_f32 v243, v230, v231
	v_cvt_pk_fp8_f32 v244, v234, v235
	v_cvt_pk_fp8_f32 v245, v238, v239
	v_cvt_pk_fp8_f32 v242, v228, v229 op_sel:[0,0,1]
	v_cvt_pk_fp8_f32 v243, v232, v233 op_sel:[0,0,1]
	v_cvt_pk_fp8_f32 v244, v236, v237 op_sel:[0,0,1]
	v_cvt_pk_fp8_f32 v245, v240, v241 op_sel:[0,0,1]
	s_nop 0
	global_store_dwordx4 v77, v[242:245], s[6:7]
	ds_read_b32 v226, v214
	ds_read_b32 v227, v214 offset:512
	ds_read_b32 v228, v214 offset:1024
	ds_read_b32 v229, v214 offset:1536
	ds_read_b32 v230, v214 offset:2048
	ds_read_b32 v231, v214 offset:2560
	ds_read_b32 v232, v214 offset:3072
	ds_read_b32 v233, v214 offset:3584
	ds_read_b32 v234, v214 offset:4096
	ds_read_b32 v235, v214 offset:4608
	ds_read_b32 v236, v214 offset:5120
	ds_read_b32 v237, v214 offset:5632
	ds_read_b32 v238, v214 offset:6144
	ds_read_b32 v239, v214 offset:6656
	ds_read_b32 v240, v214 offset:7168
	ds_read_b32 v241, v214 offset:7680
	s_waitcnt lgkmcnt(0)
	v_max_f32_e32 v226, v226, v226
	v_max_f32_e32 v227, v227, v227
	v_max_f32_e32 v228, v228, v228
	v_max_f32_e32 v229, v229, v229
	v_max_f32_e32 v230, v230, v230
	v_max_f32_e32 v231, v231, v231
	v_max_f32_e32 v232, v232, v232
	v_max_f32_e32 v233, v233, v233
	v_max_f32_e32 v234, v234, v234
	v_max_f32_e32 v235, v235, v235
	v_max_f32_e32 v236, v236, v236
	v_max_f32_e32 v237, v237, v237
	v_max_f32_e32 v238, v238, v238
	v_max_f32_e32 v239, v239, v239
	v_max_f32_e32 v240, v240, v240
	v_max_f32_e32 v241, v241, v241
	v_med3_f32 v226, v226, s62, v95
	v_med3_f32 v227, v227, s62, v95
	v_med3_f32 v228, v228, s62, v95
	v_med3_f32 v229, v229, s62, v95
	v_med3_f32 v230, v230, s62, v95
	v_med3_f32 v231, v231, s62, v95
	v_med3_f32 v232, v232, s62, v95
	v_med3_f32 v233, v233, s62, v95
	v_med3_f32 v234, v234, s62, v95
	v_med3_f32 v235, v235, s62, v95
	v_med3_f32 v236, v236, s62, v95
	v_med3_f32 v237, v237, s62, v95
	v_med3_f32 v238, v238, s62, v95
	v_med3_f32 v239, v239, s62, v95
	v_med3_f32 v240, v240, s62, v95
	v_med3_f32 v241, v241, s62, v95
	v_mov_b32_e32 v242, 0
	v_mov_b32_e32 v243, 0
	v_mov_b32_e32 v244, 0
	v_mov_b32_e32 v245, 0
	v_cvt_pk_fp8_f32 v242, v226, v227
	v_cvt_pk_fp8_f32 v243, v230, v231
	v_cvt_pk_fp8_f32 v244, v234, v235
	v_cvt_pk_fp8_f32 v245, v238, v239
	v_cvt_pk_fp8_f32 v242, v228, v229 op_sel:[0,0,1]
	v_cvt_pk_fp8_f32 v243, v232, v233 op_sel:[0,0,1]
	v_cvt_pk_fp8_f32 v244, v236, v237 op_sel:[0,0,1]
	v_cvt_pk_fp8_f32 v245, v240, v241 op_sel:[0,0,1]
	s_nop 0
	global_store_dwordx4 v78, v[242:245], s[6:7]
	s_waitcnt vmcnt(12)
	v_mul_f32_e32 v144, v26, v144
	v_mul_f32_e32 v145, v26, v145
	v_mul_f32_e32 v146, v26, v146
	v_mul_f32_e32 v147, v26, v147
	ds_write_b128 v209, v[144:147]
	v_mul_f32_e32 v148, v27, v148
	v_mul_f32_e32 v149, v27, v149
	v_mul_f32_e32 v150, v27, v150
	v_mul_f32_e32 v151, v27, v151
	ds_write_b128 v209, v[148:151] offset:1024
	v_mul_f32_e32 v152, v28, v152
	v_mul_f32_e32 v153, v28, v153
	v_mul_f32_e32 v154, v28, v154
	v_mul_f32_e32 v155, v28, v155
	ds_write_b128 v209, v[152:155] offset:2048
	v_mul_f32_e32 v156, v29, v156
	v_mul_f32_e32 v157, v29, v157
	v_mul_f32_e32 v158, v29, v158
	v_mul_f32_e32 v159, v29, v159
	ds_write_b128 v209, v[156:159] offset:3072
	v_mul_f32_e32 v160, v30, v160
	v_mul_f32_e32 v161, v30, v161
	v_mul_f32_e32 v162, v30, v162
	v_mul_f32_e32 v163, v30, v163
	ds_write_b128 v209, v[160:163] offset:4096
	v_mul_f32_e32 v164, v31, v164
	v_mul_f32_e32 v165, v31, v165
	v_mul_f32_e32 v166, v31, v166
	v_mul_f32_e32 v167, v31, v167
	ds_write_b128 v209, v[164:167] offset:5120
	v_mul_f32_e32 v168, v32, v168
	v_mul_f32_e32 v169, v32, v169
	v_mul_f32_e32 v170, v32, v170
	v_mul_f32_e32 v171, v32, v171
	ds_write_b128 v209, v[168:171] offset:6144
	v_mul_f32_e32 v172, v33, v172
	v_mul_f32_e32 v173, v33, v173
	v_mul_f32_e32 v174, v33, v174
	v_mul_f32_e32 v175, v33, v175
	ds_write_b128 v209, v[172:175] offset:7168
	s_waitcnt lgkmcnt(0)
	s_barrier
; #define GAS __attribute__((address_space(1)))
; #define LAS __attribute__((address_space(3)))
; #define LDS_WAIT() asm volatile("s_waitcnt lgkmcnt(0)" ::: "memory")
;     ...
; #pragma unroll
;     for (int i = 0; i < 32; ++i) v[i] = sc >= 0 ? W[(size_t)(k0 + 2 * i + (lane >> 5)) * Nsrc + sc] : 0.f;
; #pragma unroll
;     for (int i = 0; i < 32; ++i) { const int k = k0 + 2 * i + (lane >> 5); float x = v[i] * wscale; if (KS) x *= (k < ksplit ? ksA[k] : ksB[k - ksplit]); scr[(2 * i + (lane >> 5)) * 33 + (lane & 31)] = x; }
;     LDS_WAIT(); asm volatile("" ::: "memory");
;     const int c = lane & 7;
; #pragma unroll
;     for (int j = 0; j < 4; ++j) { const int n = (lane >> 3) + 8 * j; const LAS float* s = scr + (8 * c) * 33 + n;
;         const unsigned long long o = (unsigned long long)pg8::pk4_fp8(s[0 * 33], s[1 * 33], s[2 * 33], s[3 * 33]) | ((unsigned long long)pg8::pk4_fp8(s[4 * 33], s[5 * 33], s[6 * 33], s[7 * 33]) << 32);
;         *(GAS unsigned long long*)(WT + (size_t)(n0 + n) * K + k0 + 8 * c) = o; }
; __global__ void __launch_bounds__(NWAVES * 64, 2) hybrid_fwd(Args args) {
;     ...
;             if (r < I_UP) { p0_transpose_item_f8<true>(args.in[15] + (size_t)l * DM * FF, DM, FF, FF / 32, (unsigned char*)(ws + WS_WUP + l * SZ_WUP), WUP8_SCALE, args.in[14] + l * DM, args.in[14] + l * DM, DM, scr, r, lane); continue; } r -= I_UP;
	s_add_u32 s8, s30, 0x4000
	s_addc_u32 s9, s31, 0
	global_load_dwordx4 v[144:147], v74, s[8:9]
	s_add_u32 s8, s8, 0x20000
	s_addc_u32 s9, s9, 0
	global_load_dwordx4 v[148:151], v74, s[8:9]
	s_add_u32 s8, s8, 0x20000
	s_addc_u32 s9, s9, 0
	global_load_dwordx4 v[152:155], v74, s[8:9]
	s_add_u32 s8, s8, 0x20000
	s_addc_u32 s9, s9, 0
	global_load_dwordx4 v[156:159], v74, s[8:9]
	s_add_u32 s8, s8, 0x20000
	s_addc_u32 s9, s9, 0
	global_load_dwordx4 v[160:163], v74, s[8:9]
	s_add_u32 s8, s8, 0x20000
	s_addc_u32 s9, s9, 0
	global_load_dwordx4 v[164:167], v74, s[8:9]
	s_add_u32 s8, s8, 0x20000
	s_addc_u32 s9, s9, 0
	global_load_dwordx4 v[168:171], v74, s[8:9]
	s_add_u32 s8, s8, 0x20000
	s_addc_u32 s9, s9, 0
	global_load_dwordx4 v[172:175], v74, s[8:9]
	s_add_u32 s6, s32, 0x800000
	s_addc_u32 s7, s33, 0
	ds_read_b32 v226, v211
	ds_read_b32 v227, v211 offset:512
	ds_read_b32 v228, v211 offset:1024
	ds_read_b32 v229, v211 offset:1536
	ds_read_b32 v230, v211 offset:2048
	ds_read_b32 v231, v211 offset:2560
	ds_read_b32 v232, v211 offset:3072
	ds_read_b32 v233, v211 offset:3584
	ds_read_b32 v234, v211 offset:4096
	ds_read_b32 v235, v211 offset:4608
	ds_read_b32 v236, v211 offset:5120
	ds_read_b32 v237, v211 offset:5632
	ds_read_b32 v238, v211 offset:6144
	ds_read_b32 v239, v211 offset:6656
	ds_read_b32 v240, v211 offset:7168
	ds_read_b32 v241, v211 offset:7680
	s_waitcnt lgkmcnt(0)
	v_max_f32_e32 v226, v226, v226
	v_max_f32_e32 v227, v227, v227
	v_max_f32_e32 v228, v228, v228
	v_max_f32_e32 v229, v229, v229
	v_max_f32_e32 v230, v230, v230
	v_max_f32_e32 v231, v231, v231
	v_max_f32_e32 v232, v232, v232
	v_max_f32_e32 v233, v233, v233
	v_max_f32_e32 v234, v234, v234
	v_max_f32_e32 v235, v235, v235
	v_max_f32_e32 v236, v236, v236
	v_max_f32_e32 v237, v237, v237
	v_max_f32_e32 v238, v238, v238
	v_max_f32_e32 v239, v239, v239
	v_max_f32_e32 v240, v240, v240
	v_max_f32_e32 v241, v241, v241
	v_med3_f32 v226, v226, s62, v95
	v_med3_f32 v227, v227, s62, v95
	v_med3_f32 v228, v228, s62, v95
	v_med3_f32 v229, v229, s62, v95
	v_med3_f32 v230, v230, s62, v95
	v_med3_f32 v231, v231, s62, v95
	v_med3_f32 v232, v232, s62, v95
	v_med3_f32 v233, v233, s62, v95
	v_med3_f32 v234, v234, s62, v95
	v_med3_f32 v235, v235, s62, v95
	v_med3_f32 v236, v236, s62, v95
	v_med3_f32 v237, v237, s62, v95
	v_med3_f32 v238, v238, s62, v95
	v_med3_f32 v239, v239, s62, v95
	v_med3_f32 v240, v240, s62, v95
	v_med3_f32 v241, v241, s62, v95
	v_mov_b32_e32 v242, 0
	v_mov_b32_e32 v243, 0
	v_mov_b32_e32 v244, 0
	v_mov_b32_e32 v245, 0
	v_cvt_pk_fp8_f32 v242, v226, v227
	v_cvt_pk_fp8_f32 v243, v230, v231
	v_cvt_pk_fp8_f32 v244, v234, v235
	v_cvt_pk_fp8_f32 v245, v238, v239
	v_cvt_pk_fp8_f32 v242, v228, v229 op_sel:[0,0,1]
	v_cvt_pk_fp8_f32 v243, v232, v233 op_sel:[0,0,1]
	v_cvt_pk_fp8_f32 v244, v236, v237 op_sel:[0,0,1]
	v_cvt_pk_fp8_f32 v245, v240, v241 op_sel:[0,0,1]
	s_nop 0
	global_store_dwordx4 v77, v[242:245], s[6:7]
	ds_read_b32 v226, v213
	ds_read_b32 v227, v213 offset:512
	ds_read_b32 v228, v213 offset:1024
	ds_read_b32 v229, v213 offset:1536
	ds_read_b32 v230, v213 offset:2048
	ds_read_b32 v231, v213 offset:2560
	ds_read_b32 v232, v213 offset:3072
	ds_read_b32 v233, v213 offset:3584
	ds_read_b32 v234, v213 offset:4096
	ds_read_b32 v235, v213 offset:4608
	ds_read_b32 v236, v213 offset:5120
	ds_read_b32 v237, v213 offset:5632
	ds_read_b32 v238, v213 offset:6144
	ds_read_b32 v239, v213 offset:6656
	ds_read_b32 v240, v213 offset:7168
	ds_read_b32 v241, v213 offset:7680
	s_waitcnt lgkmcnt(0)
	v_max_f32_e32 v226, v226, v226
	v_max_f32_e32 v227, v227, v227
	v_max_f32_e32 v228, v228, v228
	v_max_f32_e32 v229, v229, v229
	v_max_f32_e32 v230, v230, v230
	v_max_f32_e32 v231, v231, v231
	v_max_f32_e32 v232, v232, v232
	v_max_f32_e32 v233, v233, v233
	v_max_f32_e32 v234, v234, v234
	v_max_f32_e32 v235, v235, v235
	v_max_f32_e32 v236, v236, v236
	v_max_f32_e32 v237, v237, v237
	v_max_f32_e32 v238, v238, v238
	v_max_f32_e32 v239, v239, v239
	v_max_f32_e32 v240, v240, v240
	v_max_f32_e32 v241, v241, v241
	v_med3_f32 v226, v226, s62, v95
	v_med3_f32 v227, v227, s62, v95
	v_med3_f32 v228, v228, s62, v95
	v_med3_f32 v229, v229, s62, v95
	v_med3_f32 v230, v230, s62, v95
	v_med3_f32 v231, v231, s62, v95
	v_med3_f32 v232, v232, s62, v95
	v_med3_f32 v233, v233, s62, v95
	v_med3_f32 v234, v234, s62, v95
	v_med3_f32 v235, v235, s62, v95
	v_med3_f32 v236, v236, s62, v95
	v_med3_f32 v237, v237, s62, v95
	v_med3_f32 v238, v238, s62, v95
	v_med3_f32 v239, v239, s62, v95
	v_med3_f32 v240, v240, s62, v95
	v_med3_f32 v241, v241, s62, v95
	v_mov_b32_e32 v242, 0
	v_mov_b32_e32 v243, 0
	v_mov_b32_e32 v244, 0
	v_mov_b32_e32 v245, 0
	v_cvt_pk_fp8_f32 v242, v226, v227
	v_cvt_pk_fp8_f32 v243, v230, v231
	v_cvt_pk_fp8_f32 v244, v234, v235
	v_cvt_pk_fp8_f32 v245, v238, v239
	v_cvt_pk_fp8_f32 v242, v228, v229 op_sel:[0,0,1]
	v_cvt_pk_fp8_f32 v243, v232, v233 op_sel:[0,0,1]
	v_cvt_pk_fp8_f32 v244, v236, v237 op_sel:[0,0,1]
	v_cvt_pk_fp8_f32 v245, v240, v241 op_sel:[0,0,1]
	s_nop 0
	global_store_dwordx4 v78, v[242:245], s[6:7]
	s_waitcnt vmcnt(12)
	v_mul_f32_e32 v176, v26, v176
	v_mul_f32_e32 v177, v26, v177
	v_mul_f32_e32 v178, v26, v178
	v_mul_f32_e32 v179, v26, v179
	ds_write_b128 v210, v[176:179]
	v_mul_f32_e32 v180, v27, v180
	v_mul_f32_e32 v181, v27, v181
	v_mul_f32_e32 v182, v27, v182
	v_mul_f32_e32 v183, v27, v183
	ds_write_b128 v210, v[180:183] offset:1024
	v_mul_f32_e32 v184, v28, v184
	v_mul_f32_e32 v185, v28, v185
	v_mul_f32_e32 v186, v28, v186
	v_mul_f32_e32 v187, v28, v187
	ds_write_b128 v210, v[184:187] offset:2048
	v_mul_f32_e32 v188, v29, v188
	v_mul_f32_e32 v189, v29, v189
	v_mul_f32_e32 v190, v29, v190
	v_mul_f32_e32 v191, v29, v191
	ds_write_b128 v210, v[188:191] offset:3072
	v_mul_f32_e32 v192, v30, v192
	v_mul_f32_e32 v193, v30, v193
	v_mul_f32_e32 v194, v30, v194
	v_mul_f32_e32 v195, v30, v195
	ds_write_b128 v210, v[192:195] offset:4096
	v_mul_f32_e32 v196, v31, v196
	v_mul_f32_e32 v197, v31, v197
	v_mul_f32_e32 v198, v31, v198
	v_mul_f32_e32 v199, v31, v199
	ds_write_b128 v210, v[196:199] offset:5120
	v_mul_f32_e32 v200, v32, v200
	v_mul_f32_e32 v201, v32, v201
	v_mul_f32_e32 v202, v32, v202
	v_mul_f32_e32 v203, v32, v203
	ds_write_b128 v210, v[200:203] offset:6144
	v_mul_f32_e32 v204, v33, v204
	v_mul_f32_e32 v205, v33, v205
	v_mul_f32_e32 v206, v33, v206
	v_mul_f32_e32 v207, v33, v207
	ds_write_b128 v210, v[204:207] offset:7168
	s_waitcnt lgkmcnt(0)
	s_barrier
; #define GAS __attribute__((address_space(1)))
; #define LAS __attribute__((address_space(3)))
; #define LDS_WAIT() asm volatile("s_waitcnt lgkmcnt(0)" ::: "memory")
;     ...
; #pragma unroll
;     for (int i = 0; i < 32; ++i) v[i] = sc >= 0 ? W[(size_t)(k0 + 2 * i + (lane >> 5)) * Nsrc + sc] : 0.f;
; #pragma unroll
;     for (int i = 0; i < 32; ++i) { const int k = k0 + 2 * i + (lane >> 5); float x = v[i] * wscale; if (KS) x *= (k < ksplit ? ksA[k] : ksB[k - ksplit]); scr[(2 * i + (lane >> 5)) * 33 + (lane & 31)] = x; }
;     LDS_WAIT(); asm volatile("" ::: "memory");
;     const int c = lane & 7;
; #pragma unroll
;     for (int j = 0; j < 4; ++j) { const int n = (lane >> 3) + 8 * j; const LAS float* s = scr + (8 * c) * 33 + n;
;         const unsigned long long o = (unsigned long long)pg8::pk4_fp8(s[0 * 33], s[1 * 33], s[2 * 33], s[3 * 33]) | ((unsigned long long)pg8::pk4_fp8(s[4 * 33], s[5 * 33], s[6 * 33], s[7 * 33]) << 32);
;         *(GAS unsigned long long*)(WT + (size_t)(n0 + n) * K + k0 + 8 * c) = o; }
; __global__ void __launch_bounds__(NWAVES * 64, 2) hybrid_fwd(Args args) {
;     ...
;             if (r < I_UP) { p0_transpose_item_f8<true>(args.in[15] + (size_t)l * DM * FF, DM, FF, FF / 32, (unsigned char*)(ws + WS_WUP + l * SZ_WUP), WUP8_SCALE, args.in[14] + l * DM, args.in[14] + l * DM, DM, scr, r, lane); continue; } r -= I_UP;
	s_add_u32 s8, s30, 0x5000
	s_addc_u32 s9, s31, 0
	global_load_dwordx4 v[176:179], v74, s[8:9]
	s_add_u32 s8, s8, 0x20000
	s_addc_u32 s9, s9, 0
	global_load_dwordx4 v[180:183], v74, s[8:9]
	s_add_u32 s8, s8, 0x20000
	s_addc_u32 s9, s9, 0
	global_load_dwordx4 v[184:187], v74, s[8:9]
	s_add_u32 s8, s8, 0x20000
	s_addc_u32 s9, s9, 0
	global_load_dwordx4 v[188:191], v74, s[8:9]
	s_add_u32 s8, s8, 0x20000
	s_addc_u32 s9, s9, 0
	global_load_dwordx4 v[192:195], v74, s[8:9]
	s_add_u32 s8, s8, 0x20000
	s_addc_u32 s9, s9, 0
	global_load_dwordx4 v[196:199], v74, s[8:9]
	s_add_u32 s8, s8, 0x20000
	s_addc_u32 s9, s9, 0
	global_load_dwordx4 v[200:203], v74, s[8:9]
	s_add_u32 s8, s8, 0x20000
	s_addc_u32 s9, s9, 0
	global_load_dwordx4 v[204:207], v74, s[8:9]
	s_add_u32 s6, s32, 0xc00000
	s_addc_u32 s7, s33, 0
	ds_read_b32 v226, v212
	ds_read_b32 v227, v212 offset:512
	ds_read_b32 v228, v212 offset:1024
	ds_read_b32 v229, v212 offset:1536
	ds_read_b32 v230, v212 offset:2048
	ds_read_b32 v231, v212 offset:2560
	ds_read_b32 v232, v212 offset:3072
	ds_read_b32 v233, v212 offset:3584
	ds_read_b32 v234, v212 offset:4096
	ds_read_b32 v235, v212 offset:4608
	ds_read_b32 v236, v212 offset:5120
	ds_read_b32 v237, v212 offset:5632
	ds_read_b32 v238, v212 offset:6144
	ds_read_b32 v239, v212 offset:6656
	ds_read_b32 v240, v212 offset:7168
	ds_read_b32 v241, v212 offset:7680
	s_waitcnt lgkmcnt(0)
	v_max_f32_e32 v226, v226, v226
	v_max_f32_e32 v227, v227, v227
	v_max_f32_e32 v228, v228, v228
	v_max_f32_e32 v229, v229, v229
	v_max_f32_e32 v230, v230, v230
	v_max_f32_e32 v231, v231, v231
	v_max_f32_e32 v232, v232, v232
	v_max_f32_e32 v233, v233, v233
	v_max_f32_e32 v234, v234, v234
	v_max_f32_e32 v235, v235, v235
	v_max_f32_e32 v236, v236, v236
	v_max_f32_e32 v237, v237, v237
	v_max_f32_e32 v238, v238, v238
	v_max_f32_e32 v239, v239, v239
	v_max_f32_e32 v240, v240, v240
	v_max_f32_e32 v241, v241, v241
	v_med3_f32 v226, v226, s62, v95
	v_med3_f32 v227, v227, s62, v95
	v_med3_f32 v228, v228, s62, v95
	v_med3_f32 v229, v229, s62, v95
	v_med3_f32 v230, v230, s62, v95
	v_med3_f32 v231, v231, s62, v95
	v_med3_f32 v232, v232, s62, v95
	v_med3_f32 v233, v233, s62, v95
	v_med3_f32 v234, v234, s62, v95
	v_med3_f32 v235, v235, s62, v95
	v_med3_f32 v236, v236, s62, v95
	v_med3_f32 v237, v237, s62, v95
	v_med3_f32 v238, v238, s62, v95
	v_med3_f32 v239, v239, s62, v95
	v_med3_f32 v240, v240, s62, v95
	v_med3_f32 v241, v241, s62, v95
	v_mov_b32_e32 v242, 0
	v_mov_b32_e32 v243, 0
	v_mov_b32_e32 v244, 0
	v_mov_b32_e32 v245, 0
	v_cvt_pk_fp8_f32 v242, v226, v227
	v_cvt_pk_fp8_f32 v243, v230, v231
	v_cvt_pk_fp8_f32 v244, v234, v235
	v_cvt_pk_fp8_f32 v245, v238, v239
	v_cvt_pk_fp8_f32 v242, v228, v229 op_sel:[0,0,1]
	v_cvt_pk_fp8_f32 v243, v232, v233 op_sel:[0,0,1]
	v_cvt_pk_fp8_f32 v244, v236, v237 op_sel:[0,0,1]
	v_cvt_pk_fp8_f32 v245, v240, v241 op_sel:[0,0,1]
	s_nop 0
	global_store_dwordx4 v77, v[242:245], s[6:7]
	ds_read_b32 v226, v214
	ds_read_b32 v227, v214 offset:512
	ds_read_b32 v228, v214 offset:1024
	ds_read_b32 v229, v214 offset:1536
	ds_read_b32 v230, v214 offset:2048
	ds_read_b32 v231, v214 offset:2560
	ds_read_b32 v232, v214 offset:3072
	ds_read_b32 v233, v214 offset:3584
	ds_read_b32 v234, v214 offset:4096
	ds_read_b32 v235, v214 offset:4608
	ds_read_b32 v236, v214 offset:5120
	ds_read_b32 v237, v214 offset:5632
	ds_read_b32 v238, v214 offset:6144
	ds_read_b32 v239, v214 offset:6656
	ds_read_b32 v240, v214 offset:7168
	ds_read_b32 v241, v214 offset:7680
	s_waitcnt lgkmcnt(0)
	v_max_f32_e32 v226, v226, v226
	v_max_f32_e32 v227, v227, v227
	v_max_f32_e32 v228, v228, v228
	v_max_f32_e32 v229, v229, v229
	v_max_f32_e32 v230, v230, v230
	v_max_f32_e32 v231, v231, v231
	v_max_f32_e32 v232, v232, v232
	v_max_f32_e32 v233, v233, v233
	v_max_f32_e32 v234, v234, v234
	v_max_f32_e32 v235, v235, v235
	v_max_f32_e32 v236, v236, v236
	v_max_f32_e32 v237, v237, v237
	v_max_f32_e32 v238, v238, v238
	v_max_f32_e32 v239, v239, v239
	v_max_f32_e32 v240, v240, v240
	v_max_f32_e32 v241, v241, v241
	v_med3_f32 v226, v226, s62, v95
	v_med3_f32 v227, v227, s62, v95
	v_med3_f32 v228, v228, s62, v95
	v_med3_f32 v229, v229, s62, v95
	v_med3_f32 v230, v230, s62, v95
	v_med3_f32 v231, v231, s62, v95
	v_med3_f32 v232, v232, s62, v95
	v_med3_f32 v233, v233, s62, v95
	v_med3_f32 v234, v234, s62, v95
	v_med3_f32 v235, v235, s62, v95
	v_med3_f32 v236, v236, s62, v95
	v_med3_f32 v237, v237, s62, v95
	v_med3_f32 v238, v238, s62, v95
	v_med3_f32 v239, v239, s62, v95
	v_med3_f32 v240, v240, s62, v95
	v_med3_f32 v241, v241, s62, v95
	v_mov_b32_e32 v242, 0
	v_mov_b32_e32 v243, 0
	v_mov_b32_e32 v244, 0
	v_mov_b32_e32 v245, 0
	v_cvt_pk_fp8_f32 v242, v226, v227
	v_cvt_pk_fp8_f32 v243, v230, v231
	v_cvt_pk_fp8_f32 v244, v234, v235
	v_cvt_pk_fp8_f32 v245, v238, v239
	v_cvt_pk_fp8_f32 v242, v228, v229 op_sel:[0,0,1]
	v_cvt_pk_fp8_f32 v243, v232, v233 op_sel:[0,0,1]
	v_cvt_pk_fp8_f32 v244, v236, v237 op_sel:[0,0,1]
	v_cvt_pk_fp8_f32 v245, v240, v241 op_sel:[0,0,1]
	s_nop 0
	global_store_dwordx4 v78, v[242:245], s[6:7]
	s_waitcnt vmcnt(12)
	v_mul_f32_e32 v144, v26, v144
	v_mul_f32_e32 v145, v26, v145
	v_mul_f32_e32 v146, v26, v146
	v_mul_f32_e32 v147, v26, v147
	ds_write_b128 v209, v[144:147]
	v_mul_f32_e32 v148, v27, v148
	v_mul_f32_e32 v149, v27, v149
	v_mul_f32_e32 v150, v27, v150
	v_mul_f32_e32 v151, v27, v151
	ds_write_b128 v209, v[148:151] offset:1024
	v_mul_f32_e32 v152, v28, v152
	v_mul_f32_e32 v153, v28, v153
	v_mul_f32_e32 v154, v28, v154
	v_mul_f32_e32 v155, v28, v155
	ds_write_b128 v209, v[152:155] offset:2048
	v_mul_f32_e32 v156, v29, v156
	v_mul_f32_e32 v157, v29, v157
	v_mul_f32_e32 v158, v29, v158
	v_mul_f32_e32 v159, v29, v159
	ds_write_b128 v209, v[156:159] offset:3072
	v_mul_f32_e32 v160, v30, v160
	v_mul_f32_e32 v161, v30, v161
	v_mul_f32_e32 v162, v30, v162
	v_mul_f32_e32 v163, v30, v163
	ds_write_b128 v209, v[160:163] offset:4096
	v_mul_f32_e32 v164, v31, v164
	v_mul_f32_e32 v165, v31, v165
	v_mul_f32_e32 v166, v31, v166
	v_mul_f32_e32 v167, v31, v167
	ds_write_b128 v209, v[164:167] offset:5120
	v_mul_f32_e32 v168, v32, v168
	v_mul_f32_e32 v169, v32, v169
	v_mul_f32_e32 v170, v32, v170
	v_mul_f32_e32 v171, v32, v171
	ds_write_b128 v209, v[168:171] offset:6144
	v_mul_f32_e32 v172, v33, v172
	v_mul_f32_e32 v173, v33, v173
	v_mul_f32_e32 v174, v33, v174
	v_mul_f32_e32 v175, v33, v175
	ds_write_b128 v209, v[172:175] offset:7168
	s_waitcnt lgkmcnt(0)
	s_barrier
; #define GAS __attribute__((address_space(1)))
; #define LAS __attribute__((address_space(3)))
; #define LDS_WAIT() asm volatile("s_waitcnt lgkmcnt(0)" ::: "memory")
;     ...
; #pragma unroll
;     for (int i = 0; i < 32; ++i) v[i] = sc >= 0 ? W[(size_t)(k0 + 2 * i + (lane >> 5)) * Nsrc + sc] : 0.f;
; #pragma unroll
;     for (int i = 0; i < 32; ++i) { const int k = k0 + 2 * i + (lane >> 5); float x = v[i] * wscale; if (KS) x *= (k < ksplit ? ksA[k] : ksB[k - ksplit]); scr[(2 * i + (lane >> 5)) * 33 + (lane & 31)] = x; }
;     LDS_WAIT(); asm volatile("" ::: "memory");
;     const int c = lane & 7;
; #pragma unroll
;     for (int j = 0; j < 4; ++j) { const int n = (lane >> 3) + 8 * j; const LAS float* s = scr + (8 * c) * 33 + n;
;         const unsigned long long o = (unsigned long long)pg8::pk4_fp8(s[0 * 33], s[1 * 33], s[2 * 33], s[3 * 33]) | ((unsigned long long)pg8::pk4_fp8(s[4 * 33], s[5 * 33], s[6 * 33], s[7 * 33]) << 32);
;         *(GAS unsigned long long*)(WT + (size_t)(n0 + n) * K + k0 + 8 * c) = o; }
; __global__ void __launch_bounds__(NWAVES * 64, 2) hybrid_fwd(Args args) {
;     ...
;             if (r < I_UP) { p0_transpose_item_f8<true>(args.in[15] + (size_t)l * DM * FF, DM, FF, FF / 32, (unsigned char*)(ws + WS_WUP + l * SZ_WUP), WUP8_SCALE, args.in[14] + l * DM, args.in[14] + l * DM, DM, scr, r, lane); continue; } r -= I_UP;
	s_add_u32 s8, s30, 0x6000
	s_addc_u32 s9, s31, 0
	global_load_dwordx4 v[144:147], v74, s[8:9]
	s_add_u32 s8, s8, 0x20000
	s_addc_u32 s9, s9, 0
	global_load_dwordx4 v[148:151], v74, s[8:9]
	s_add_u32 s8, s8, 0x20000
	s_addc_u32 s9, s9, 0
	global_load_dwordx4 v[152:155], v74, s[8:9]
	s_add_u32 s8, s8, 0x20000
	s_addc_u32 s9, s9, 0
	global_load_dwordx4 v[156:159], v74, s[8:9]
	s_add_u32 s8, s8, 0x20000
	s_addc_u32 s9, s9, 0
	global_load_dwordx4 v[160:163], v74, s[8:9]
	s_add_u32 s8, s8, 0x20000
	s_addc_u32 s9, s9, 0
	global_load_dwordx4 v[164:167], v74, s[8:9]
	s_add_u32 s8, s8, 0x20000
	s_addc_u32 s9, s9, 0
	global_load_dwordx4 v[168:171], v74, s[8:9]
	s_add_u32 s8, s8, 0x20000
	s_addc_u32 s9, s9, 0
	global_load_dwordx4 v[172:175], v74, s[8:9]
	s_add_u32 s6, s32, 0x1000000
	s_addc_u32 s7, s33, 0
	ds_read_b32 v226, v211
	ds_read_b32 v227, v211 offset:512
	ds_read_b32 v228, v211 offset:1024
	ds_read_b32 v229, v211 offset:1536
	ds_read_b32 v230, v211 offset:2048
	ds_read_b32 v231, v211 offset:2560
	ds_read_b32 v232, v211 offset:3072
	ds_read_b32 v233, v211 offset:3584
	ds_read_b32 v234, v211 offset:4096
	ds_read_b32 v235, v211 offset:4608
	ds_read_b32 v236, v211 offset:5120
	ds_read_b32 v237, v211 offset:5632
	ds_read_b32 v238, v211 offset:6144
	ds_read_b32 v239, v211 offset:6656
	ds_read_b32 v240, v211 offset:7168
	ds_read_b32 v241, v211 offset:7680
	s_waitcnt lgkmcnt(0)
	v_max_f32_e32 v226, v226, v226
	v_max_f32_e32 v227, v227, v227
	v_max_f32_e32 v228, v228, v228
	v_max_f32_e32 v229, v229, v229
	v_max_f32_e32 v230, v230, v230
	v_max_f32_e32 v231, v231, v231
	v_max_f32_e32 v232, v232, v232
	v_max_f32_e32 v233, v233, v233
	v_max_f32_e32 v234, v234, v234
	v_max_f32_e32 v235, v235, v235
	v_max_f32_e32 v236, v236, v236
	v_max_f32_e32 v237, v237, v237
	v_max_f32_e32 v238, v238, v238
	v_max_f32_e32 v239, v239, v239
	v_max_f32_e32 v240, v240, v240
	v_max_f32_e32 v241, v241, v241
	v_med3_f32 v226, v226, s62, v95
	v_med3_f32 v227, v227, s62, v95
	v_med3_f32 v228, v228, s62, v95
	v_med3_f32 v229, v229, s62, v95
	v_med3_f32 v230, v230, s62, v95
	v_med3_f32 v231, v231, s62, v95
	v_med3_f32 v232, v232, s62, v95
	v_med3_f32 v233, v233, s62, v95
	v_med3_f32 v234, v234, s62, v95
	v_med3_f32 v235, v235, s62, v95
	v_med3_f32 v236, v236, s62, v95
	v_med3_f32 v237, v237, s62, v95
	v_med3_f32 v238, v238, s62, v95
	v_med3_f32 v239, v239, s62, v95
	v_med3_f32 v240, v240, s62, v95
	v_med3_f32 v241, v241, s62, v95
	v_mov_b32_e32 v242, 0
	v_mov_b32_e32 v243, 0
	v_mov_b32_e32 v244, 0
	v_mov_b32_e32 v245, 0
	v_cvt_pk_fp8_f32 v242, v226, v227
	v_cvt_pk_fp8_f32 v243, v230, v231
	v_cvt_pk_fp8_f32 v244, v234, v235
	v_cvt_pk_fp8_f32 v245, v238, v239
	v_cvt_pk_fp8_f32 v242, v228, v229 op_sel:[0,0,1]
	v_cvt_pk_fp8_f32 v243, v232, v233 op_sel:[0,0,1]
	v_cvt_pk_fp8_f32 v244, v236, v237 op_sel:[0,0,1]
	v_cvt_pk_fp8_f32 v245, v240, v241 op_sel:[0,0,1]
	s_nop 0
	global_store_dwordx4 v77, v[242:245], s[6:7]
	ds_read_b32 v226, v213
	ds_read_b32 v227, v213 offset:512
	ds_read_b32 v228, v213 offset:1024
	ds_read_b32 v229, v213 offset:1536
	ds_read_b32 v230, v213 offset:2048
	ds_read_b32 v231, v213 offset:2560
	ds_read_b32 v232, v213 offset:3072
	ds_read_b32 v233, v213 offset:3584
	ds_read_b32 v234, v213 offset:4096
	ds_read_b32 v235, v213 offset:4608
	ds_read_b32 v236, v213 offset:5120
	ds_read_b32 v237, v213 offset:5632
	ds_read_b32 v238, v213 offset:6144
	ds_read_b32 v239, v213 offset:6656
	ds_read_b32 v240, v213 offset:7168
	ds_read_b32 v241, v213 offset:7680
	s_waitcnt lgkmcnt(0)
	v_max_f32_e32 v226, v226, v226
	v_max_f32_e32 v227, v227, v227
	v_max_f32_e32 v228, v228, v228
	v_max_f32_e32 v229, v229, v229
	v_max_f32_e32 v230, v230, v230
	v_max_f32_e32 v231, v231, v231
	v_max_f32_e32 v232, v232, v232
	v_max_f32_e32 v233, v233, v233
	v_max_f32_e32 v234, v234, v234
	v_max_f32_e32 v235, v235, v235
	v_max_f32_e32 v236, v236, v236
	v_max_f32_e32 v237, v237, v237
	v_max_f32_e32 v238, v238, v238
	v_max_f32_e32 v239, v239, v239
	v_max_f32_e32 v240, v240, v240
	v_max_f32_e32 v241, v241, v241
	v_med3_f32 v226, v226, s62, v95
	v_med3_f32 v227, v227, s62, v95
	v_med3_f32 v228, v228, s62, v95
	v_med3_f32 v229, v229, s62, v95
	v_med3_f32 v230, v230, s62, v95
	v_med3_f32 v231, v231, s62, v95
	v_med3_f32 v232, v232, s62, v95
	v_med3_f32 v233, v233, s62, v95
	v_med3_f32 v234, v234, s62, v95
	v_med3_f32 v235, v235, s62, v95
	v_med3_f32 v236, v236, s62, v95
	v_med3_f32 v237, v237, s62, v95
	v_med3_f32 v238, v238, s62, v95
	v_med3_f32 v239, v239, s62, v95
	v_med3_f32 v240, v240, s62, v95
	v_med3_f32 v241, v241, s62, v95
	v_mov_b32_e32 v242, 0
	v_mov_b32_e32 v243, 0
	v_mov_b32_e32 v244, 0
	v_mov_b32_e32 v245, 0
	v_cvt_pk_fp8_f32 v242, v226, v227
	v_cvt_pk_fp8_f32 v243, v230, v231
	v_cvt_pk_fp8_f32 v244, v234, v235
	v_cvt_pk_fp8_f32 v245, v238, v239
	v_cvt_pk_fp8_f32 v242, v228, v229 op_sel:[0,0,1]
	v_cvt_pk_fp8_f32 v243, v232, v233 op_sel:[0,0,1]
	v_cvt_pk_fp8_f32 v244, v236, v237 op_sel:[0,0,1]
	v_cvt_pk_fp8_f32 v245, v240, v241 op_sel:[0,0,1]
	s_nop 0
	global_store_dwordx4 v78, v[242:245], s[6:7]
	s_waitcnt vmcnt(12)
	v_mul_f32_e32 v176, v26, v176
	v_mul_f32_e32 v177, v26, v177
	v_mul_f32_e32 v178, v26, v178
	v_mul_f32_e32 v179, v26, v179
	ds_write_b128 v210, v[176:179]
	v_mul_f32_e32 v180, v27, v180
	v_mul_f32_e32 v181, v27, v181
	v_mul_f32_e32 v182, v27, v182
	v_mul_f32_e32 v183, v27, v183
	ds_write_b128 v210, v[180:183] offset:1024
	v_mul_f32_e32 v184, v28, v184
	v_mul_f32_e32 v185, v28, v185
	v_mul_f32_e32 v186, v28, v186
	v_mul_f32_e32 v187, v28, v187
	ds_write_b128 v210, v[184:187] offset:2048
	v_mul_f32_e32 v188, v29, v188
	v_mul_f32_e32 v189, v29, v189
	v_mul_f32_e32 v190, v29, v190
	v_mul_f32_e32 v191, v29, v191
	ds_write_b128 v210, v[188:191] offset:3072
	v_mul_f32_e32 v192, v30, v192
	v_mul_f32_e32 v193, v30, v193
	v_mul_f32_e32 v194, v30, v194
	v_mul_f32_e32 v195, v30, v195
	ds_write_b128 v210, v[192:195] offset:4096
	v_mul_f32_e32 v196, v31, v196
	v_mul_f32_e32 v197, v31, v197
	v_mul_f32_e32 v198, v31, v198
	v_mul_f32_e32 v199, v31, v199
	ds_write_b128 v210, v[196:199] offset:5120
	v_mul_f32_e32 v200, v32, v200
	v_mul_f32_e32 v201, v32, v201
	v_mul_f32_e32 v202, v32, v202
	v_mul_f32_e32 v203, v32, v203
	ds_write_b128 v210, v[200:203] offset:6144
	v_mul_f32_e32 v204, v33, v204
	v_mul_f32_e32 v205, v33, v205
	v_mul_f32_e32 v206, v33, v206
	v_mul_f32_e32 v207, v33, v207
	ds_write_b128 v210, v[204:207] offset:7168
	s_waitcnt lgkmcnt(0)
	s_barrier
; #define GAS __attribute__((address_space(1)))
; #define LAS __attribute__((address_space(3)))
; #define LDS_WAIT() asm volatile("s_waitcnt lgkmcnt(0)" ::: "memory")
;     ...
; #pragma unroll
;     for (int i = 0; i < 32; ++i) v[i] = sc >= 0 ? W[(size_t)(k0 + 2 * i + (lane >> 5)) * Nsrc + sc] : 0.f;
; #pragma unroll
;     for (int i = 0; i < 32; ++i) { const int k = k0 + 2 * i + (lane >> 5); float x = v[i] * wscale; if (KS) x *= (k < ksplit ? ksA[k] : ksB[k - ksplit]); scr[(2 * i + (lane >> 5)) * 33 + (lane & 31)] = x; }
;     LDS_WAIT(); asm volatile("" ::: "memory");
;     const int c = lane & 7;
; #pragma unroll
;     for (int j = 0; j < 4; ++j) { const int n = (lane >> 3) + 8 * j; const LAS float* s = scr + (8 * c) * 33 + n;
;         const unsigned long long o = (unsigned long long)pg8::pk4_fp8(s[0 * 33], s[1 * 33], s[2 * 33], s[3 * 33]) | ((unsigned long long)pg8::pk4_fp8(s[4 * 33], s[5 * 33], s[6 * 33], s[7 * 33]) << 32);
;         *(GAS unsigned long long*)(WT + (size_t)(n0 + n) * K + k0 + 8 * c) = o; }
; __global__ void __launch_bounds__(NWAVES * 64, 2) hybrid_fwd(Args args) {
;     ...
;             if (r < I_UP) { p0_transpose_item_f8<true>(args.in[15] + (size_t)l * DM * FF, DM, FF, FF / 32, (unsigned char*)(ws + WS_WUP + l * SZ_WUP), WUP8_SCALE, args.in[14] + l * DM, args.in[14] + l * DM, DM, scr, r, lane); continue; } r -= I_UP;
	s_add_u32 s8, s30, 0x7000
	s_addc_u32 s9, s31, 0
	global_load_dwordx4 v[176:179], v74, s[8:9]
	s_add_u32 s8, s8, 0x20000
	s_addc_u32 s9, s9, 0
	global_load_dwordx4 v[180:183], v74, s[8:9]
	s_add_u32 s8, s8, 0x20000
	s_addc_u32 s9, s9, 0
	global_load_dwordx4 v[184:187], v74, s[8:9]
	s_add_u32 s8, s8, 0x20000
	s_addc_u32 s9, s9, 0
	global_load_dwordx4 v[188:191], v74, s[8:9]
	s_add_u32 s8, s8, 0x20000
	s_addc_u32 s9, s9, 0
	global_load_dwordx4 v[192:195], v74, s[8:9]
	s_add_u32 s8, s8, 0x20000
	s_addc_u32 s9, s9, 0
	global_load_dwordx4 v[196:199], v74, s[8:9]
	s_add_u32 s8, s8, 0x20000
	s_addc_u32 s9, s9, 0
	global_load_dwordx4 v[200:203], v74, s[8:9]
	s_add_u32 s8, s8, 0x20000
	s_addc_u32 s9, s9, 0
	global_load_dwordx4 v[204:207], v74, s[8:9]
	s_add_u32 s6, s32, 0x1400000
	s_addc_u32 s7, s33, 0
	ds_read_b32 v226, v212
	ds_read_b32 v227, v212 offset:512
	ds_read_b32 v228, v212 offset:1024
	ds_read_b32 v229, v212 offset:1536
	ds_read_b32 v230, v212 offset:2048
	ds_read_b32 v231, v212 offset:2560
	ds_read_b32 v232, v212 offset:3072
	ds_read_b32 v233, v212 offset:3584
	ds_read_b32 v234, v212 offset:4096
	ds_read_b32 v235, v212 offset:4608
	ds_read_b32 v236, v212 offset:5120
	ds_read_b32 v237, v212 offset:5632
	ds_read_b32 v238, v212 offset:6144
	ds_read_b32 v239, v212 offset:6656
	ds_read_b32 v240, v212 offset:7168
	ds_read_b32 v241, v212 offset:7680
	s_waitcnt lgkmcnt(0)
	v_max_f32_e32 v226, v226, v226
	v_max_f32_e32 v227, v227, v227
	v_max_f32_e32 v228, v228, v228
	v_max_f32_e32 v229, v229, v229
	v_max_f32_e32 v230, v230, v230
	v_max_f32_e32 v231, v231, v231
	v_max_f32_e32 v232, v232, v232
	v_max_f32_e32 v233, v233, v233
	v_max_f32_e32 v234, v234, v234
	v_max_f32_e32 v235, v235, v235
	v_max_f32_e32 v236, v236, v236
	v_max_f32_e32 v237, v237, v237
	v_max_f32_e32 v238, v238, v238
	v_max_f32_e32 v239, v239, v239
	v_max_f32_e32 v240, v240, v240
	v_max_f32_e32 v241, v241, v241
	v_med3_f32 v226, v226, s62, v95
	v_med3_f32 v227, v227, s62, v95
	v_med3_f32 v228, v228, s62, v95
	v_med3_f32 v229, v229, s62, v95
	v_med3_f32 v230, v230, s62, v95
	v_med3_f32 v231, v231, s62, v95
	v_med3_f32 v232, v232, s62, v95
	v_med3_f32 v233, v233, s62, v95
	v_med3_f32 v234, v234, s62, v95
	v_med3_f32 v235, v235, s62, v95
	v_med3_f32 v236, v236, s62, v95
	v_med3_f32 v237, v237, s62, v95
	v_med3_f32 v238, v238, s62, v95
	v_med3_f32 v239, v239, s62, v95
	v_med3_f32 v240, v240, s62, v95
	v_med3_f32 v241, v241, s62, v95
	v_mov_b32_e32 v242, 0
	v_mov_b32_e32 v243, 0
	v_mov_b32_e32 v244, 0
	v_mov_b32_e32 v245, 0
	v_cvt_pk_fp8_f32 v242, v226, v227
	v_cvt_pk_fp8_f32 v243, v230, v231
	v_cvt_pk_fp8_f32 v244, v234, v235
	v_cvt_pk_fp8_f32 v245, v238, v239
	v_cvt_pk_fp8_f32 v242, v228, v229 op_sel:[0,0,1]
	v_cvt_pk_fp8_f32 v243, v232, v233 op_sel:[0,0,1]
	v_cvt_pk_fp8_f32 v244, v236, v237 op_sel:[0,0,1]
	v_cvt_pk_fp8_f32 v245, v240, v241 op_sel:[0,0,1]
	s_nop 0
	global_store_dwordx4 v77, v[242:245], s[6:7]
	ds_read_b32 v226, v214
	ds_read_b32 v227, v214 offset:512
	ds_read_b32 v228, v214 offset:1024
	ds_read_b32 v229, v214 offset:1536
	ds_read_b32 v230, v214 offset:2048
	ds_read_b32 v231, v214 offset:2560
	ds_read_b32 v232, v214 offset:3072
	ds_read_b32 v233, v214 offset:3584
	ds_read_b32 v234, v214 offset:4096
	ds_read_b32 v235, v214 offset:4608
	ds_read_b32 v236, v214 offset:5120
	ds_read_b32 v237, v214 offset:5632
	ds_read_b32 v238, v214 offset:6144
	ds_read_b32 v239, v214 offset:6656
	ds_read_b32 v240, v214 offset:7168
	ds_read_b32 v241, v214 offset:7680
	s_waitcnt lgkmcnt(0)
	v_max_f32_e32 v226, v226, v226
	v_max_f32_e32 v227, v227, v227
	v_max_f32_e32 v228, v228, v228
	v_max_f32_e32 v229, v229, v229
	v_max_f32_e32 v230, v230, v230
	v_max_f32_e32 v231, v231, v231
	v_max_f32_e32 v232, v232, v232
	v_max_f32_e32 v233, v233, v233
	v_max_f32_e32 v234, v234, v234
	v_max_f32_e32 v235, v235, v235
	v_max_f32_e32 v236, v236, v236
	v_max_f32_e32 v237, v237, v237
	v_max_f32_e32 v238, v238, v238
	v_max_f32_e32 v239, v239, v239
	v_max_f32_e32 v240, v240, v240
	v_max_f32_e32 v241, v241, v241
	v_med3_f32 v226, v226, s62, v95
	v_med3_f32 v227, v227, s62, v95
	v_med3_f32 v228, v228, s62, v95
	v_med3_f32 v229, v229, s62, v95
	v_med3_f32 v230, v230, s62, v95
	v_med3_f32 v231, v231, s62, v95
	v_med3_f32 v232, v232, s62, v95
	v_med3_f32 v233, v233, s62, v95
	v_med3_f32 v234, v234, s62, v95
	v_med3_f32 v235, v235, s62, v95
	v_med3_f32 v236, v236, s62, v95
	v_med3_f32 v237, v237, s62, v95
	v_med3_f32 v238, v238, s62, v95
	v_med3_f32 v239, v239, s62, v95
	v_med3_f32 v240, v240, s62, v95
	v_med3_f32 v241, v241, s62, v95
	v_mov_b32_e32 v242, 0
	v_mov_b32_e32 v243, 0
	v_mov_b32_e32 v244, 0
	v_mov_b32_e32 v245, 0
	v_cvt_pk_fp8_f32 v242, v226, v227
	v_cvt_pk_fp8_f32 v243, v230, v231
	v_cvt_pk_fp8_f32 v244, v234, v235
	v_cvt_pk_fp8_f32 v245, v238, v239
	v_cvt_pk_fp8_f32 v242, v228, v229 op_sel:[0,0,1]
	v_cvt_pk_fp8_f32 v243, v232, v233 op_sel:[0,0,1]
	v_cvt_pk_fp8_f32 v244, v236, v237 op_sel:[0,0,1]
	v_cvt_pk_fp8_f32 v245, v240, v241 op_sel:[0,0,1]
	s_nop 0
	global_store_dwordx4 v78, v[242:245], s[6:7]
	s_waitcnt vmcnt(12)
	v_mul_f32_e32 v144, v26, v144
	v_mul_f32_e32 v145, v26, v145
	v_mul_f32_e32 v146, v26, v146
	v_mul_f32_e32 v147, v26, v147
	ds_write_b128 v209, v[144:147]
	v_mul_f32_e32 v148, v27, v148
	v_mul_f32_e32 v149, v27, v149
	v_mul_f32_e32 v150, v27, v150
	v_mul_f32_e32 v151, v27, v151
	ds_write_b128 v209, v[148:151] offset:1024
	v_mul_f32_e32 v152, v28, v152
	v_mul_f32_e32 v153, v28, v153
	v_mul_f32_e32 v154, v28, v154
	v_mul_f32_e32 v155, v28, v155
	ds_write_b128 v209, v[152:155] offset:2048
	v_mul_f32_e32 v156, v29, v156
	v_mul_f32_e32 v157, v29, v157
	v_mul_f32_e32 v158, v29, v158
	v_mul_f32_e32 v159, v29, v159
	ds_write_b128 v209, v[156:159] offset:3072
	v_mul_f32_e32 v160, v30, v160
	v_mul_f32_e32 v161, v30, v161
	v_mul_f32_e32 v162, v30, v162
	v_mul_f32_e32 v163, v30, v163
	ds_write_b128 v209, v[160:163] offset:4096
	v_mul_f32_e32 v164, v31, v164
	v_mul_f32_e32 v165, v31, v165
	v_mul_f32_e32 v166, v31, v166
	v_mul_f32_e32 v167, v31, v167
	ds_write_b128 v209, v[164:167] offset:5120
	v_mul_f32_e32 v168, v32, v168
	v_mul_f32_e32 v169, v32, v169
	v_mul_f32_e32 v170, v32, v170
	v_mul_f32_e32 v171, v32, v171
	ds_write_b128 v209, v[168:171] offset:6144
	v_mul_f32_e32 v172, v33, v172
	v_mul_f32_e32 v173, v33, v173
	v_mul_f32_e32 v174, v33, v174
	v_mul_f32_e32 v175, v33, v175
	ds_write_b128 v209, v[172:175] offset:7168
	s_waitcnt lgkmcnt(0)
	s_barrier
; #define GAS __attribute__((address_space(1)))
; #define LAS __attribute__((address_space(3)))
; #define LDS_WAIT() asm volatile("s_waitcnt lgkmcnt(0)" ::: "memory")
;     ...
; #pragma unroll
;     for (int i = 0; i < 32; ++i) v[i] = sc >= 0 ? W[(size_t)(k0 + 2 * i + (lane >> 5)) * Nsrc + sc] : 0.f;
; #pragma unroll
;     for (int i = 0; i < 32; ++i) { const int k = k0 + 2 * i + (lane >> 5); float x = v[i] * wscale; if (KS) x *= (k < ksplit ? ksA[k] : ksB[k - ksplit]); scr[(2 * i + (lane >> 5)) * 33 + (lane & 31)] = x; }
;     LDS_WAIT(); asm volatile("" ::: "memory");
;     const int c = lane & 7;
; #pragma unroll
;     for (int j = 0; j < 4; ++j) { const int n = (lane >> 3) + 8 * j; const LAS float* s = scr + (8 * c) * 33 + n;
;         const unsigned long long o = (unsigned long long)pg8::pk4_fp8(s[0 * 33], s[1 * 33], s[2 * 33], s[3 * 33]) | ((unsigned long long)pg8::pk4_fp8(s[4 * 33], s[5 * 33], s[6 * 33], s[7 * 33]) << 32);
;         *(GAS unsigned long long*)(WT + (size_t)(n0 + n) * K + k0 + 8 * c) = o; }
; __global__ void __launch_bounds__(NWAVES * 64, 2) hybrid_fwd(Args args) {
;     ...
;             if (r < I_UP) { p0_transpose_item_f8<true>(args.in[15] + (size_t)l * DM * FF, DM, FF, FF / 32, (unsigned char*)(ws + WS_WUP + l * SZ_WUP), WUP8_SCALE, args.in[14] + l * DM, args.in[14] + l * DM, DM, scr, r, lane); continue; } r -= I_UP;
	s_add_u32 s8, s30, 0x8000
	s_addc_u32 s9, s31, 0
	global_load_dwordx4 v[144:147], v74, s[8:9]
	s_add_u32 s8, s8, 0x20000
	s_addc_u32 s9, s9, 0
	global_load_dwordx4 v[148:151], v74, s[8:9]
	s_add_u32 s8, s8, 0x20000
	s_addc_u32 s9, s9, 0
	global_load_dwordx4 v[152:155], v74, s[8:9]
	s_add_u32 s8, s8, 0x20000
	s_addc_u32 s9, s9, 0
	global_load_dwordx4 v[156:159], v74, s[8:9]
	s_add_u32 s8, s8, 0x20000
	s_addc_u32 s9, s9, 0
	global_load_dwordx4 v[160:163], v74, s[8:9]
	s_add_u32 s8, s8, 0x20000
	s_addc_u32 s9, s9, 0
	global_load_dwordx4 v[164:167], v74, s[8:9]
	s_add_u32 s8, s8, 0x20000
	s_addc_u32 s9, s9, 0
	global_load_dwordx4 v[168:171], v74, s[8:9]
	s_add_u32 s8, s8, 0x20000
	s_addc_u32 s9, s9, 0
	global_load_dwordx4 v[172:175], v74, s[8:9]
	s_add_u32 s6, s32, 0x1800000
	s_addc_u32 s7, s33, 0
	ds_read_b32 v226, v211
	ds_read_b32 v227, v211 offset:512
	ds_read_b32 v228, v211 offset:1024
	ds_read_b32 v229, v211 offset:1536
	ds_read_b32 v230, v211 offset:2048
	ds_read_b32 v231, v211 offset:2560
	ds_read_b32 v232, v211 offset:3072
	ds_read_b32 v233, v211 offset:3584
	ds_read_b32 v234, v211 offset:4096
	ds_read_b32 v235, v211 offset:4608
	ds_read_b32 v236, v211 offset:5120
	ds_read_b32 v237, v211 offset:5632
	ds_read_b32 v238, v211 offset:6144
	ds_read_b32 v239, v211 offset:6656
	ds_read_b32 v240, v211 offset:7168
	ds_read_b32 v241, v211 offset:7680
	s_waitcnt lgkmcnt(0)
	v_max_f32_e32 v226, v226, v226
	v_max_f32_e32 v227, v227, v227
	v_max_f32_e32 v228, v228, v228
	v_max_f32_e32 v229, v229, v229
	v_max_f32_e32 v230, v230, v230
	v_max_f32_e32 v231, v231, v231
	v_max_f32_e32 v232, v232, v232
	v_max_f32_e32 v233, v233, v233
	v_max_f32_e32 v234, v234, v234
	v_max_f32_e32 v235, v235, v235
	v_max_f32_e32 v236, v236, v236
	v_max_f32_e32 v237, v237, v237
	v_max_f32_e32 v238, v238, v238
	v_max_f32_e32 v239, v239, v239
	v_max_f32_e32 v240, v240, v240
	v_max_f32_e32 v241, v241, v241
	v_med3_f32 v226, v226, s62, v95
	v_med3_f32 v227, v227, s62, v95
	v_med3_f32 v228, v228, s62, v95
	v_med3_f32 v229, v229, s62, v95
	v_med3_f32 v230, v230, s62, v95
	v_med3_f32 v231, v231, s62, v95
	v_med3_f32 v232, v232, s62, v95
	v_med3_f32 v233, v233, s62, v95
	v_med3_f32 v234, v234, s62, v95
	v_med3_f32 v235, v235, s62, v95
	v_med3_f32 v236, v236, s62, v95
	v_med3_f32 v237, v237, s62, v95
	v_med3_f32 v238, v238, s62, v95
	v_med3_f32 v239, v239, s62, v95
	v_med3_f32 v240, v240, s62, v95
	v_med3_f32 v241, v241, s62, v95
	v_mov_b32_e32 v242, 0
	v_mov_b32_e32 v243, 0
	v_mov_b32_e32 v244, 0
	v_mov_b32_e32 v245, 0
	v_cvt_pk_fp8_f32 v242, v226, v227
	v_cvt_pk_fp8_f32 v243, v230, v231
	v_cvt_pk_fp8_f32 v244, v234, v235
	v_cvt_pk_fp8_f32 v245, v238, v239
	v_cvt_pk_fp8_f32 v242, v228, v229 op_sel:[0,0,1]
	v_cvt_pk_fp8_f32 v243, v232, v233 op_sel:[0,0,1]
	v_cvt_pk_fp8_f32 v244, v236, v237 op_sel:[0,0,1]
	v_cvt_pk_fp8_f32 v245, v240, v241 op_sel:[0,0,1]
	s_nop 0
	global_store_dwordx4 v77, v[242:245], s[6:7]
	ds_read_b32 v226, v213
	ds_read_b32 v227, v213 offset:512
	ds_read_b32 v228, v213 offset:1024
	ds_read_b32 v229, v213 offset:1536
	ds_read_b32 v230, v213 offset:2048
	ds_read_b32 v231, v213 offset:2560
	ds_read_b32 v232, v213 offset:3072
	ds_read_b32 v233, v213 offset:3584
	ds_read_b32 v234, v213 offset:4096
	ds_read_b32 v235, v213 offset:4608
	ds_read_b32 v236, v213 offset:5120
	ds_read_b32 v237, v213 offset:5632
	ds_read_b32 v238, v213 offset:6144
	ds_read_b32 v239, v213 offset:6656
	ds_read_b32 v240, v213 offset:7168
	ds_read_b32 v241, v213 offset:7680
	s_waitcnt lgkmcnt(0)
	v_max_f32_e32 v226, v226, v226
	v_max_f32_e32 v227, v227, v227
	v_max_f32_e32 v228, v228, v228
	v_max_f32_e32 v229, v229, v229
	v_max_f32_e32 v230, v230, v230
	v_max_f32_e32 v231, v231, v231
	v_max_f32_e32 v232, v232, v232
	v_max_f32_e32 v233, v233, v233
	v_max_f32_e32 v234, v234, v234
	v_max_f32_e32 v235, v235, v235
	v_max_f32_e32 v236, v236, v236
	v_max_f32_e32 v237, v237, v237
	v_max_f32_e32 v238, v238, v238
	v_max_f32_e32 v239, v239, v239
	v_max_f32_e32 v240, v240, v240
	v_max_f32_e32 v241, v241, v241
	v_med3_f32 v226, v226, s62, v95
	v_med3_f32 v227, v227, s62, v95
	v_med3_f32 v228, v228, s62, v95
	v_med3_f32 v229, v229, s62, v95
	v_med3_f32 v230, v230, s62, v95
	v_med3_f32 v231, v231, s62, v95
	v_med3_f32 v232, v232, s62, v95
	v_med3_f32 v233, v233, s62, v95
	v_med3_f32 v234, v234, s62, v95
	v_med3_f32 v235, v235, s62, v95
	v_med3_f32 v236, v236, s62, v95
	v_med3_f32 v237, v237, s62, v95
	v_med3_f32 v238, v238, s62, v95
	v_med3_f32 v239, v239, s62, v95
	v_med3_f32 v240, v240, s62, v95
	v_med3_f32 v241, v241, s62, v95
	v_mov_b32_e32 v242, 0
	v_mov_b32_e32 v243, 0
	v_mov_b32_e32 v244, 0
	v_mov_b32_e32 v245, 0
	v_cvt_pk_fp8_f32 v242, v226, v227
	v_cvt_pk_fp8_f32 v243, v230, v231
	v_cvt_pk_fp8_f32 v244, v234, v235
	v_cvt_pk_fp8_f32 v245, v238, v239
	v_cvt_pk_fp8_f32 v242, v228, v229 op_sel:[0,0,1]
	v_cvt_pk_fp8_f32 v243, v232, v233 op_sel:[0,0,1]
	v_cvt_pk_fp8_f32 v244, v236, v237 op_sel:[0,0,1]
	v_cvt_pk_fp8_f32 v245, v240, v241 op_sel:[0,0,1]
	s_nop 0
	global_store_dwordx4 v78, v[242:245], s[6:7]
	s_waitcnt vmcnt(12)
	v_mul_f32_e32 v176, v26, v176
	v_mul_f32_e32 v177, v26, v177
	v_mul_f32_e32 v178, v26, v178
	v_mul_f32_e32 v179, v26, v179
	ds_write_b128 v210, v[176:179]
	v_mul_f32_e32 v180, v27, v180
	v_mul_f32_e32 v181, v27, v181
	v_mul_f32_e32 v182, v27, v182
	v_mul_f32_e32 v183, v27, v183
	ds_write_b128 v210, v[180:183] offset:1024
	v_mul_f32_e32 v184, v28, v184
	v_mul_f32_e32 v185, v28, v185
	v_mul_f32_e32 v186, v28, v186
	v_mul_f32_e32 v187, v28, v187
	ds_write_b128 v210, v[184:187] offset:2048
	v_mul_f32_e32 v188, v29, v188
	v_mul_f32_e32 v189, v29, v189
	v_mul_f32_e32 v190, v29, v190
	v_mul_f32_e32 v191, v29, v191
	ds_write_b128 v210, v[188:191] offset:3072
	v_mul_f32_e32 v192, v30, v192
	v_mul_f32_e32 v193, v30, v193
	v_mul_f32_e32 v194, v30, v194
	v_mul_f32_e32 v195, v30, v195
	ds_write_b128 v210, v[192:195] offset:4096
	v_mul_f32_e32 v196, v31, v196
	v_mul_f32_e32 v197, v31, v197
	v_mul_f32_e32 v198, v31, v198
	v_mul_f32_e32 v199, v31, v199
	ds_write_b128 v210, v[196:199] offset:5120
	v_mul_f32_e32 v200, v32, v200
	v_mul_f32_e32 v201, v32, v201
	v_mul_f32_e32 v202, v32, v202
	v_mul_f32_e32 v203, v32, v203
	ds_write_b128 v210, v[200:203] offset:6144
	v_mul_f32_e32 v204, v33, v204
	v_mul_f32_e32 v205, v33, v205
	v_mul_f32_e32 v206, v33, v206
	v_mul_f32_e32 v207, v33, v207
	ds_write_b128 v210, v[204:207] offset:7168
	s_waitcnt lgkmcnt(0)
	s_barrier
; #define GAS __attribute__((address_space(1)))
; #define LAS __attribute__((address_space(3)))
; #define LDS_WAIT() asm volatile("s_waitcnt lgkmcnt(0)" ::: "memory")
;     ...
; #pragma unroll
;     for (int i = 0; i < 32; ++i) v[i] = sc >= 0 ? W[(size_t)(k0 + 2 * i + (lane >> 5)) * Nsrc + sc] : 0.f;
; #pragma unroll
;     for (int i = 0; i < 32; ++i) { const int k = k0 + 2 * i + (lane >> 5); float x = v[i] * wscale; if (KS) x *= (k < ksplit ? ksA[k] : ksB[k - ksplit]); scr[(2 * i + (lane >> 5)) * 33 + (lane & 31)] = x; }
;     LDS_WAIT(); asm volatile("" ::: "memory");
;     const int c = lane & 7;
; #pragma unroll
;     for (int j = 0; j < 4; ++j) { const int n = (lane >> 3) + 8 * j; const LAS float* s = scr + (8 * c) * 33 + n;
;         const unsigned long long o = (unsigned long long)pg8::pk4_fp8(s[0 * 33], s[1 * 33], s[2 * 33], s[3 * 33]) | ((unsigned long long)pg8::pk4_fp8(s[4 * 33], s[5 * 33], s[6 * 33], s[7 * 33]) << 32);
;         *(GAS unsigned long long*)(WT + (size_t)(n0 + n) * K + k0 + 8 * c) = o; }
; __global__ void __launch_bounds__(NWAVES * 64, 2) hybrid_fwd(Args args) {
;     ...
;             if (r < I_UP) { p0_transpose_item_f8<true>(args.in[15] + (size_t)l * DM * FF, DM, FF, FF / 32, (unsigned char*)(ws + WS_WUP + l * SZ_WUP), WUP8_SCALE, args.in[14] + l * DM, args.in[14] + l * DM, DM, scr, r, lane); continue; } r -= I_UP;
	s_add_u32 s8, s30, 0x9000
	s_addc_u32 s9, s31, 0
	global_load_dwordx4 v[176:179], v74, s[8:9]
	s_add_u32 s8, s8, 0x20000
	s_addc_u32 s9, s9, 0
	global_load_dwordx4 v[180:183], v74, s[8:9]
	s_add_u32 s8, s8, 0x20000
	s_addc_u32 s9, s9, 0
	global_load_dwordx4 v[184:187], v74, s[8:9]
	s_add_u32 s8, s8, 0x20000
	s_addc_u32 s9, s9, 0
	global_load_dwordx4 v[188:191], v74, s[8:9]
	s_add_u32 s8, s8, 0x20000
	s_addc_u32 s9, s9, 0
	global_load_dwordx4 v[192:195], v74, s[8:9]
	s_add_u32 s8, s8, 0x20000
	s_addc_u32 s9, s9, 0
	global_load_dwordx4 v[196:199], v74, s[8:9]
	s_add_u32 s8, s8, 0x20000
	s_addc_u32 s9, s9, 0
	global_load_dwordx4 v[200:203], v74, s[8:9]
	s_add_u32 s8, s8, 0x20000
	s_addc_u32 s9, s9, 0
	global_load_dwordx4 v[204:207], v74, s[8:9]
	s_add_u32 s6, s32, 0x1c00000
	s_addc_u32 s7, s33, 0
	ds_read_b32 v226, v212
	ds_read_b32 v227, v212 offset:512
	ds_read_b32 v228, v212 offset:1024
	ds_read_b32 v229, v212 offset:1536
	ds_read_b32 v230, v212 offset:2048
	ds_read_b32 v231, v212 offset:2560
	ds_read_b32 v232, v212 offset:3072
	ds_read_b32 v233, v212 offset:3584
	ds_read_b32 v234, v212 offset:4096
	ds_read_b32 v235, v212 offset:4608
	ds_read_b32 v236, v212 offset:5120
	ds_read_b32 v237, v212 offset:5632
	ds_read_b32 v238, v212 offset:6144
	ds_read_b32 v239, v212 offset:6656
	ds_read_b32 v240, v212 offset:7168
	ds_read_b32 v241, v212 offset:7680
	s_waitcnt lgkmcnt(0)
	v_max_f32_e32 v226, v226, v226
	v_max_f32_e32 v227, v227, v227
	v_max_f32_e32 v228, v228, v228
	v_max_f32_e32 v229, v229, v229
	v_max_f32_e32 v230, v230, v230
	v_max_f32_e32 v231, v231, v231
	v_max_f32_e32 v232, v232, v232
	v_max_f32_e32 v233, v233, v233
	v_max_f32_e32 v234, v234, v234
	v_max_f32_e32 v235, v235, v235
	v_max_f32_e32 v236, v236, v236
	v_max_f32_e32 v237, v237, v237
	v_max_f32_e32 v238, v238, v238
	v_max_f32_e32 v239, v239, v239
	v_max_f32_e32 v240, v240, v240
	v_max_f32_e32 v241, v241, v241
	v_med3_f32 v226, v226, s62, v95
	v_med3_f32 v227, v227, s62, v95
	v_med3_f32 v228, v228, s62, v95
	v_med3_f32 v229, v229, s62, v95
	v_med3_f32 v230, v230, s62, v95
	v_med3_f32 v231, v231, s62, v95
	v_med3_f32 v232, v232, s62, v95
	v_med3_f32 v233, v233, s62, v95
	v_med3_f32 v234, v234, s62, v95
	v_med3_f32 v235, v235, s62, v95
	v_med3_f32 v236, v236, s62, v95
	v_med3_f32 v237, v237, s62, v95
	v_med3_f32 v238, v238, s62, v95
	v_med3_f32 v239, v239, s62, v95
	v_med3_f32 v240, v240, s62, v95
	v_med3_f32 v241, v241, s62, v95
	v_mov_b32_e32 v242, 0
	v_mov_b32_e32 v243, 0
	v_mov_b32_e32 v244, 0
	v_mov_b32_e32 v245, 0
	v_cvt_pk_fp8_f32 v242, v226, v227
	v_cvt_pk_fp8_f32 v243, v230, v231
	v_cvt_pk_fp8_f32 v244, v234, v235
	v_cvt_pk_fp8_f32 v245, v238, v239
	v_cvt_pk_fp8_f32 v242, v228, v229 op_sel:[0,0,1]
	v_cvt_pk_fp8_f32 v243, v232, v233 op_sel:[0,0,1]
	v_cvt_pk_fp8_f32 v244, v236, v237 op_sel:[0,0,1]
	v_cvt_pk_fp8_f32 v245, v240, v241 op_sel:[0,0,1]
	s_nop 0
	global_store_dwordx4 v77, v[242:245], s[6:7]
	ds_read_b32 v226, v214
	ds_read_b32 v227, v214 offset:512
	ds_read_b32 v228, v214 offset:1024
	ds_read_b32 v229, v214 offset:1536
	ds_read_b32 v230, v214 offset:2048
	ds_read_b32 v231, v214 offset:2560
	ds_read_b32 v232, v214 offset:3072
	ds_read_b32 v233, v214 offset:3584
	ds_read_b32 v234, v214 offset:4096
	ds_read_b32 v235, v214 offset:4608
	ds_read_b32 v236, v214 offset:5120
	ds_read_b32 v237, v214 offset:5632
	ds_read_b32 v238, v214 offset:6144
	ds_read_b32 v239, v214 offset:6656
	ds_read_b32 v240, v214 offset:7168
	ds_read_b32 v241, v214 offset:7680
	s_waitcnt lgkmcnt(0)
	v_max_f32_e32 v226, v226, v226
	v_max_f32_e32 v227, v227, v227
	v_max_f32_e32 v228, v228, v228
	v_max_f32_e32 v229, v229, v229
	v_max_f32_e32 v230, v230, v230
	v_max_f32_e32 v231, v231, v231
	v_max_f32_e32 v232, v232, v232
	v_max_f32_e32 v233, v233, v233
	v_max_f32_e32 v234, v234, v234
	v_max_f32_e32 v235, v235, v235
	v_max_f32_e32 v236, v236, v236
	v_max_f32_e32 v237, v237, v237
	v_max_f32_e32 v238, v238, v238
	v_max_f32_e32 v239, v239, v239
	v_max_f32_e32 v240, v240, v240
	v_max_f32_e32 v241, v241, v241
	v_med3_f32 v226, v226, s62, v95
	v_med3_f32 v227, v227, s62, v95
	v_med3_f32 v228, v228, s62, v95
	v_med3_f32 v229, v229, s62, v95
	v_med3_f32 v230, v230, s62, v95
	v_med3_f32 v231, v231, s62, v95
	v_med3_f32 v232, v232, s62, v95
	v_med3_f32 v233, v233, s62, v95
	v_med3_f32 v234, v234, s62, v95
	v_med3_f32 v235, v235, s62, v95
	v_med3_f32 v236, v236, s62, v95
	v_med3_f32 v237, v237, s62, v95
	v_med3_f32 v238, v238, s62, v95
	v_med3_f32 v239, v239, s62, v95
	v_med3_f32 v240, v240, s62, v95
	v_med3_f32 v241, v241, s62, v95
	v_mov_b32_e32 v242, 0
	v_mov_b32_e32 v243, 0
	v_mov_b32_e32 v244, 0
	v_mov_b32_e32 v245, 0
	v_cvt_pk_fp8_f32 v242, v226, v227
	v_cvt_pk_fp8_f32 v243, v230, v231
	v_cvt_pk_fp8_f32 v244, v234, v235
	v_cvt_pk_fp8_f32 v245, v238, v239
	v_cvt_pk_fp8_f32 v242, v228, v229 op_sel:[0,0,1]
	v_cvt_pk_fp8_f32 v243, v232, v233 op_sel:[0,0,1]
	v_cvt_pk_fp8_f32 v244, v236, v237 op_sel:[0,0,1]
	v_cvt_pk_fp8_f32 v245, v240, v241 op_sel:[0,0,1]
	s_nop 0
	global_store_dwordx4 v78, v[242:245], s[6:7]
	s_waitcnt vmcnt(12)
	v_mul_f32_e32 v144, v26, v144
	v_mul_f32_e32 v145, v26, v145
	v_mul_f32_e32 v146, v26, v146
	v_mul_f32_e32 v147, v26, v147
	ds_write_b128 v209, v[144:147]
	v_mul_f32_e32 v148, v27, v148
	v_mul_f32_e32 v149, v27, v149
	v_mul_f32_e32 v150, v27, v150
	v_mul_f32_e32 v151, v27, v151
	ds_write_b128 v209, v[148:151] offset:1024
	v_mul_f32_e32 v152, v28, v152
	v_mul_f32_e32 v153, v28, v153
	v_mul_f32_e32 v154, v28, v154
	v_mul_f32_e32 v155, v28, v155
	ds_write_b128 v209, v[152:155] offset:2048
	v_mul_f32_e32 v156, v29, v156
	v_mul_f32_e32 v157, v29, v157
	v_mul_f32_e32 v158, v29, v158
	v_mul_f32_e32 v159, v29, v159
	ds_write_b128 v209, v[156:159] offset:3072
	v_mul_f32_e32 v160, v30, v160
	v_mul_f32_e32 v161, v30, v161
	v_mul_f32_e32 v162, v30, v162
	v_mul_f32_e32 v163, v30, v163
	ds_write_b128 v209, v[160:163] offset:4096
	v_mul_f32_e32 v164, v31, v164
	v_mul_f32_e32 v165, v31, v165
	v_mul_f32_e32 v166, v31, v166
	v_mul_f32_e32 v167, v31, v167
	ds_write_b128 v209, v[164:167] offset:5120
	v_mul_f32_e32 v168, v32, v168
	v_mul_f32_e32 v169, v32, v169
	v_mul_f32_e32 v170, v32, v170
	v_mul_f32_e32 v171, v32, v171
	ds_write_b128 v209, v[168:171] offset:6144
	v_mul_f32_e32 v172, v33, v172
	v_mul_f32_e32 v173, v33, v173
	v_mul_f32_e32 v174, v33, v174
	v_mul_f32_e32 v175, v33, v175
	ds_write_b128 v209, v[172:175] offset:7168
	s_waitcnt lgkmcnt(0)
	s_barrier
; #define GAS __attribute__((address_space(1)))
; #define LAS __attribute__((address_space(3)))
; #define LDS_WAIT() asm volatile("s_waitcnt lgkmcnt(0)" ::: "memory")
;     ...
; #pragma unroll
;     for (int i = 0; i < 32; ++i) v[i] = sc >= 0 ? W[(size_t)(k0 + 2 * i + (lane >> 5)) * Nsrc + sc] : 0.f;
; #pragma unroll
;     for (int i = 0; i < 32; ++i) { const int k = k0 + 2 * i + (lane >> 5); float x = v[i] * wscale; if (KS) x *= (k < ksplit ? ksA[k] : ksB[k - ksplit]); scr[(2 * i + (lane >> 5)) * 33 + (lane & 31)] = x; }
;     LDS_WAIT(); asm volatile("" ::: "memory");
;     const int c = lane & 7;
; #pragma unroll
;     for (int j = 0; j < 4; ++j) { const int n = (lane >> 3) + 8 * j; const LAS float* s = scr + (8 * c) * 33 + n;
;         const unsigned long long o = (unsigned long long)pg8::pk4_fp8(s[0 * 33], s[1 * 33], s[2 * 33], s[3 * 33]) | ((unsigned long long)pg8::pk4_fp8(s[4 * 33], s[5 * 33], s[6 * 33], s[7 * 33]) << 32);
;         *(GAS unsigned long long*)(WT + (size_t)(n0 + n) * K + k0 + 8 * c) = o; }
; __global__ void __launch_bounds__(NWAVES * 64, 2) hybrid_fwd(Args args) {
;     ...
;             if (r < I_UP) { p0_transpose_item_f8<true>(args.in[15] + (size_t)l * DM * FF, DM, FF, FF / 32, (unsigned char*)(ws + WS_WUP + l * SZ_WUP), WUP8_SCALE, args.in[14] + l * DM, args.in[14] + l * DM, DM, scr, r, lane); continue; } r -= I_UP;
	s_add_u32 s8, s30, 0xa000
	s_addc_u32 s9, s31, 0
	global_load_dwordx4 v[144:147], v74, s[8:9]
	s_add_u32 s8, s8, 0x20000
	s_addc_u32 s9, s9, 0
	global_load_dwordx4 v[148:151], v74, s[8:9]
	s_add_u32 s8, s8, 0x20000
	s_addc_u32 s9, s9, 0
	global_load_dwordx4 v[152:155], v74, s[8:9]
	s_add_u32 s8, s8, 0x20000
	s_addc_u32 s9, s9, 0
	global_load_dwordx4 v[156:159], v74, s[8:9]
	s_add_u32 s8, s8, 0x20000
	s_addc_u32 s9, s9, 0
	global_load_dwordx4 v[160:163], v74, s[8:9]
	s_add_u32 s8, s8, 0x20000
	s_addc_u32 s9, s9, 0
	global_load_dwordx4 v[164:167], v74, s[8:9]
	s_add_u32 s8, s8, 0x20000
	s_addc_u32 s9, s9, 0
	global_load_dwordx4 v[168:171], v74, s[8:9]
	s_add_u32 s8, s8, 0x20000
	s_addc_u32 s9, s9, 0
	global_load_dwordx4 v[172:175], v74, s[8:9]
	s_add_u32 s6, s32, 0x2000000
	s_addc_u32 s7, s33, 0
	ds_read_b32 v226, v211
	ds_read_b32 v227, v211 offset:512
	ds_read_b32 v228, v211 offset:1024
	ds_read_b32 v229, v211 offset:1536
	ds_read_b32 v230, v211 offset:2048
	ds_read_b32 v231, v211 offset:2560
	ds_read_b32 v232, v211 offset:3072
	ds_read_b32 v233, v211 offset:3584
	ds_read_b32 v234, v211 offset:4096
	ds_read_b32 v235, v211 offset:4608
	ds_read_b32 v236, v211 offset:5120
	ds_read_b32 v237, v211 offset:5632
	ds_read_b32 v238, v211 offset:6144
	ds_read_b32 v239, v211 offset:6656
	ds_read_b32 v240, v211 offset:7168
	ds_read_b32 v241, v211 offset:7680
	s_waitcnt lgkmcnt(0)
	v_max_f32_e32 v226, v226, v226
	v_max_f32_e32 v227, v227, v227
	v_max_f32_e32 v228, v228, v228
	v_max_f32_e32 v229, v229, v229
	v_max_f32_e32 v230, v230, v230
	v_max_f32_e32 v231, v231, v231
	v_max_f32_e32 v232, v232, v232
	v_max_f32_e32 v233, v233, v233
	v_max_f32_e32 v234, v234, v234
	v_max_f32_e32 v235, v235, v235
	v_max_f32_e32 v236, v236, v236
	v_max_f32_e32 v237, v237, v237
	v_max_f32_e32 v238, v238, v238
	v_max_f32_e32 v239, v239, v239
	v_max_f32_e32 v240, v240, v240
	v_max_f32_e32 v241, v241, v241
	v_med3_f32 v226, v226, s62, v95
	v_med3_f32 v227, v227, s62, v95
	v_med3_f32 v228, v228, s62, v95
	v_med3_f32 v229, v229, s62, v95
	v_med3_f32 v230, v230, s62, v95
	v_med3_f32 v231, v231, s62, v95
	v_med3_f32 v232, v232, s62, v95
	v_med3_f32 v233, v233, s62, v95
	v_med3_f32 v234, v234, s62, v95
	v_med3_f32 v235, v235, s62, v95
	v_med3_f32 v236, v236, s62, v95
	v_med3_f32 v237, v237, s62, v95
	v_med3_f32 v238, v238, s62, v95
	v_med3_f32 v239, v239, s62, v95
	v_med3_f32 v240, v240, s62, v95
	v_med3_f32 v241, v241, s62, v95
	v_mov_b32_e32 v242, 0
	v_mov_b32_e32 v243, 0
	v_mov_b32_e32 v244, 0
	v_mov_b32_e32 v245, 0
	v_cvt_pk_fp8_f32 v242, v226, v227
	v_cvt_pk_fp8_f32 v243, v230, v231
	v_cvt_pk_fp8_f32 v244, v234, v235
	v_cvt_pk_fp8_f32 v245, v238, v239
	v_cvt_pk_fp8_f32 v242, v228, v229 op_sel:[0,0,1]
	v_cvt_pk_fp8_f32 v243, v232, v233 op_sel:[0,0,1]
	v_cvt_pk_fp8_f32 v244, v236, v237 op_sel:[0,0,1]
	v_cvt_pk_fp8_f32 v245, v240, v241 op_sel:[0,0,1]
	s_nop 0
	global_store_dwordx4 v77, v[242:245], s[6:7]
	ds_read_b32 v226, v213
	ds_read_b32 v227, v213 offset:512
	ds_read_b32 v228, v213 offset:1024
	ds_read_b32 v229, v213 offset:1536
	ds_read_b32 v230, v213 offset:2048
	ds_read_b32 v231, v213 offset:2560
	ds_read_b32 v232, v213 offset:3072
	ds_read_b32 v233, v213 offset:3584
	ds_read_b32 v234, v213 offset:4096
	ds_read_b32 v235, v213 offset:4608
	ds_read_b32 v236, v213 offset:5120
	ds_read_b32 v237, v213 offset:5632
	ds_read_b32 v238, v213 offset:6144
	ds_read_b32 v239, v213 offset:6656
	ds_read_b32 v240, v213 offset:7168
	ds_read_b32 v241, v213 offset:7680
	s_waitcnt lgkmcnt(0)
	v_max_f32_e32 v226, v226, v226
	v_max_f32_e32 v227, v227, v227
	v_max_f32_e32 v228, v228, v228
	v_max_f32_e32 v229, v229, v229
	v_max_f32_e32 v230, v230, v230
	v_max_f32_e32 v231, v231, v231
	v_max_f32_e32 v232, v232, v232
	v_max_f32_e32 v233, v233, v233
	v_max_f32_e32 v234, v234, v234
	v_max_f32_e32 v235, v235, v235
	v_max_f32_e32 v236, v236, v236
	v_max_f32_e32 v237, v237, v237
	v_max_f32_e32 v238, v238, v238
	v_max_f32_e32 v239, v239, v239
	v_max_f32_e32 v240, v240, v240
	v_max_f32_e32 v241, v241, v241
	v_med3_f32 v226, v226, s62, v95
	v_med3_f32 v227, v227, s62, v95
	v_med3_f32 v228, v228, s62, v95
	v_med3_f32 v229, v229, s62, v95
	v_med3_f32 v230, v230, s62, v95
	v_med3_f32 v231, v231, s62, v95
	v_med3_f32 v232, v232, s62, v95
	v_med3_f32 v233, v233, s62, v95
	v_med3_f32 v234, v234, s62, v95
	v_med3_f32 v235, v235, s62, v95
	v_med3_f32 v236, v236, s62, v95
	v_med3_f32 v237, v237, s62, v95
	v_med3_f32 v238, v238, s62, v95
	v_med3_f32 v239, v239, s62, v95
	v_med3_f32 v240, v240, s62, v95
	v_med3_f32 v241, v241, s62, v95
	v_mov_b32_e32 v242, 0
	v_mov_b32_e32 v243, 0
	v_mov_b32_e32 v244, 0
	v_mov_b32_e32 v245, 0
	v_cvt_pk_fp8_f32 v242, v226, v227
	v_cvt_pk_fp8_f32 v243, v230, v231
	v_cvt_pk_fp8_f32 v244, v234, v235
	v_cvt_pk_fp8_f32 v245, v238, v239
	v_cvt_pk_fp8_f32 v242, v228, v229 op_sel:[0,0,1]
	v_cvt_pk_fp8_f32 v243, v232, v233 op_sel:[0,0,1]
	v_cvt_pk_fp8_f32 v244, v236, v237 op_sel:[0,0,1]
	v_cvt_pk_fp8_f32 v245, v240, v241 op_sel:[0,0,1]
	s_nop 0
	global_store_dwordx4 v78, v[242:245], s[6:7]
	s_waitcnt vmcnt(12)
	v_mul_f32_e32 v176, v26, v176
	v_mul_f32_e32 v177, v26, v177
	v_mul_f32_e32 v178, v26, v178
	v_mul_f32_e32 v179, v26, v179
	ds_write_b128 v210, v[176:179]
	v_mul_f32_e32 v180, v27, v180
	v_mul_f32_e32 v181, v27, v181
	v_mul_f32_e32 v182, v27, v182
	v_mul_f32_e32 v183, v27, v183
	ds_write_b128 v210, v[180:183] offset:1024
	v_mul_f32_e32 v184, v28, v184
	v_mul_f32_e32 v185, v28, v185
	v_mul_f32_e32 v186, v28, v186
	v_mul_f32_e32 v187, v28, v187
	ds_write_b128 v210, v[184:187] offset:2048
	v_mul_f32_e32 v188, v29, v188
	v_mul_f32_e32 v189, v29, v189
	v_mul_f32_e32 v190, v29, v190
	v_mul_f32_e32 v191, v29, v191
	ds_write_b128 v210, v[188:191] offset:3072
	v_mul_f32_e32 v192, v30, v192
	v_mul_f32_e32 v193, v30, v193
	v_mul_f32_e32 v194, v30, v194
	v_mul_f32_e32 v195, v30, v195
	ds_write_b128 v210, v[192:195] offset:4096
	v_mul_f32_e32 v196, v31, v196
	v_mul_f32_e32 v197, v31, v197
	v_mul_f32_e32 v198, v31, v198
	v_mul_f32_e32 v199, v31, v199
	ds_write_b128 v210, v[196:199] offset:5120
	v_mul_f32_e32 v200, v32, v200
	v_mul_f32_e32 v201, v32, v201
	v_mul_f32_e32 v202, v32, v202
	v_mul_f32_e32 v203, v32, v203
	ds_write_b128 v210, v[200:203] offset:6144
	v_mul_f32_e32 v204, v33, v204
	v_mul_f32_e32 v205, v33, v205
	v_mul_f32_e32 v206, v33, v206
	v_mul_f32_e32 v207, v33, v207
	ds_write_b128 v210, v[204:207] offset:7168
	s_waitcnt lgkmcnt(0)
	s_barrier
; #define GAS __attribute__((address_space(1)))
; #define LAS __attribute__((address_space(3)))
; #define LDS_WAIT() asm volatile("s_waitcnt lgkmcnt(0)" ::: "memory")
;     ...
; #pragma unroll
;     for (int i = 0; i < 32; ++i) v[i] = sc >= 0 ? W[(size_t)(k0 + 2 * i + (lane >> 5)) * Nsrc + sc] : 0.f;
; #pragma unroll
;     for (int i = 0; i < 32; ++i) { const int k = k0 + 2 * i + (lane >> 5); float x = v[i] * wscale; if (KS) x *= (k < ksplit ? ksA[k] : ksB[k - ksplit]); scr[(2 * i + (lane >> 5)) * 33 + (lane & 31)] = x; }
;     LDS_WAIT(); asm volatile("" ::: "memory");
;     const int c = lane & 7;
; #pragma unroll
;     for (int j = 0; j < 4; ++j) { const int n = (lane >> 3) + 8 * j; const LAS float* s = scr + (8 * c) * 33 + n;
;         const unsigned long long o = (unsigned long long)pg8::pk4_fp8(s[0 * 33], s[1 * 33], s[2 * 33], s[3 * 33]) | ((unsigned long long)pg8::pk4_fp8(s[4 * 33], s[5 * 33], s[6 * 33], s[7 * 33]) << 32);
;         *(GAS unsigned long long*)(WT + (size_t)(n0 + n) * K + k0 + 8 * c) = o; }
; __global__ void __launch_bounds__(NWAVES * 64, 2) hybrid_fwd(Args args) {
;     ...
;             if (r < I_UP) { p0_transpose_item_f8<true>(args.in[15] + (size_t)l * DM * FF, DM, FF, FF / 32, (unsigned char*)(ws + WS_WUP + l * SZ_WUP), WUP8_SCALE, args.in[14] + l * DM, args.in[14] + l * DM, DM, scr, r, lane); continue; } r -= I_UP;
	s_add_u32 s8, s30, 0xb000
	s_addc_u32 s9, s31, 0
	global_load_dwordx4 v[176:179], v74, s[8:9]
	s_add_u32 s8, s8, 0x20000
	s_addc_u32 s9, s9, 0
	global_load_dwordx4 v[180:183], v74, s[8:9]
	s_add_u32 s8, s8, 0x20000
	s_addc_u32 s9, s9, 0
	global_load_dwordx4 v[184:187], v74, s[8:9]
	s_add_u32 s8, s8, 0x20000
	s_addc_u32 s9, s9, 0
	global_load_dwordx4 v[188:191], v74, s[8:9]
	s_add_u32 s8, s8, 0x20000
	s_addc_u32 s9, s9, 0
	global_load_dwordx4 v[192:195], v74, s[8:9]
	s_add_u32 s8, s8, 0x20000
	s_addc_u32 s9, s9, 0
	global_load_dwordx4 v[196:199], v74, s[8:9]
	s_add_u32 s8, s8, 0x20000
	s_addc_u32 s9, s9, 0
	global_load_dwordx4 v[200:203], v74, s[8:9]
	s_add_u32 s8, s8, 0x20000
	s_addc_u32 s9, s9, 0
	global_load_dwordx4 v[204:207], v74, s[8:9]
	s_add_u32 s6, s32, 0x2400000
	s_addc_u32 s7, s33, 0
	ds_read_b32 v226, v212
	ds_read_b32 v227, v212 offset:512
	ds_read_b32 v228, v212 offset:1024
	ds_read_b32 v229, v212 offset:1536
	ds_read_b32 v230, v212 offset:2048
	ds_read_b32 v231, v212 offset:2560
	ds_read_b32 v232, v212 offset:3072
	ds_read_b32 v233, v212 offset:3584
	ds_read_b32 v234, v212 offset:4096
	ds_read_b32 v235, v212 offset:4608
	ds_read_b32 v236, v212 offset:5120
	ds_read_b32 v237, v212 offset:5632
	ds_read_b32 v238, v212 offset:6144
	ds_read_b32 v239, v212 offset:6656
	ds_read_b32 v240, v212 offset:7168
	ds_read_b32 v241, v212 offset:7680
	s_waitcnt lgkmcnt(0)
	v_max_f32_e32 v226, v226, v226
	v_max_f32_e32 v227, v227, v227
	v_max_f32_e32 v228, v228, v228
	v_max_f32_e32 v229, v229, v229
	v_max_f32_e32 v230, v230, v230
	v_max_f32_e32 v231, v231, v231
	v_max_f32_e32 v232, v232, v232
	v_max_f32_e32 v233, v233, v233
	v_max_f32_e32 v234, v234, v234
	v_max_f32_e32 v235, v235, v235
	v_max_f32_e32 v236, v236, v236
	v_max_f32_e32 v237, v237, v237
	v_max_f32_e32 v238, v238, v238
	v_max_f32_e32 v239, v239, v239
	v_max_f32_e32 v240, v240, v240
	v_max_f32_e32 v241, v241, v241
	v_med3_f32 v226, v226, s62, v95
	v_med3_f32 v227, v227, s62, v95
	v_med3_f32 v228, v228, s62, v95
	v_med3_f32 v229, v229, s62, v95
	v_med3_f32 v230, v230, s62, v95
	v_med3_f32 v231, v231, s62, v95
	v_med3_f32 v232, v232, s62, v95
	v_med3_f32 v233, v233, s62, v95
	v_med3_f32 v234, v234, s62, v95
	v_med3_f32 v235, v235, s62, v95
	v_med3_f32 v236, v236, s62, v95
	v_med3_f32 v237, v237, s62, v95
	v_med3_f32 v238, v238, s62, v95
	v_med3_f32 v239, v239, s62, v95
	v_med3_f32 v240, v240, s62, v95
	v_med3_f32 v241, v241, s62, v95
	v_mov_b32_e32 v242, 0
	v_mov_b32_e32 v243, 0
	v_mov_b32_e32 v244, 0
	v_mov_b32_e32 v245, 0
	v_cvt_pk_fp8_f32 v242, v226, v227
	v_cvt_pk_fp8_f32 v243, v230, v231
	v_cvt_pk_fp8_f32 v244, v234, v235
	v_cvt_pk_fp8_f32 v245, v238, v239
	v_cvt_pk_fp8_f32 v242, v228, v229 op_sel:[0,0,1]
	v_cvt_pk_fp8_f32 v243, v232, v233 op_sel:[0,0,1]
	v_cvt_pk_fp8_f32 v244, v236, v237 op_sel:[0,0,1]
	v_cvt_pk_fp8_f32 v245, v240, v241 op_sel:[0,0,1]
	s_nop 0
	global_store_dwordx4 v77, v[242:245], s[6:7]
	ds_read_b32 v226, v214
	ds_read_b32 v227, v214 offset:512
	ds_read_b32 v228, v214 offset:1024
	ds_read_b32 v229, v214 offset:1536
	ds_read_b32 v230, v214 offset:2048
	ds_read_b32 v231, v214 offset:2560
	ds_read_b32 v232, v214 offset:3072
	ds_read_b32 v233, v214 offset:3584
	ds_read_b32 v234, v214 offset:4096
	ds_read_b32 v235, v214 offset:4608
	ds_read_b32 v236, v214 offset:5120
	ds_read_b32 v237, v214 offset:5632
	ds_read_b32 v238, v214 offset:6144
	ds_read_b32 v239, v214 offset:6656
	ds_read_b32 v240, v214 offset:7168
	ds_read_b32 v241, v214 offset:7680
	s_waitcnt lgkmcnt(0)
	v_max_f32_e32 v226, v226, v226
	v_max_f32_e32 v227, v227, v227
	v_max_f32_e32 v228, v228, v228
	v_max_f32_e32 v229, v229, v229
	v_max_f32_e32 v230, v230, v230
	v_max_f32_e32 v231, v231, v231
	v_max_f32_e32 v232, v232, v232
	v_max_f32_e32 v233, v233, v233
	v_max_f32_e32 v234, v234, v234
	v_max_f32_e32 v235, v235, v235
	v_max_f32_e32 v236, v236, v236
	v_max_f32_e32 v237, v237, v237
	v_max_f32_e32 v238, v238, v238
	v_max_f32_e32 v239, v239, v239
	v_max_f32_e32 v240, v240, v240
	v_max_f32_e32 v241, v241, v241
	v_med3_f32 v226, v226, s62, v95
	v_med3_f32 v227, v227, s62, v95
	v_med3_f32 v228, v228, s62, v95
	v_med3_f32 v229, v229, s62, v95
	v_med3_f32 v230, v230, s62, v95
	v_med3_f32 v231, v231, s62, v95
	v_med3_f32 v232, v232, s62, v95
	v_med3_f32 v233, v233, s62, v95
	v_med3_f32 v234, v234, s62, v95
	v_med3_f32 v235, v235, s62, v95
	v_med3_f32 v236, v236, s62, v95
	v_med3_f32 v237, v237, s62, v95
	v_med3_f32 v238, v238, s62, v95
	v_med3_f32 v239, v239, s62, v95
	v_med3_f32 v240, v240, s62, v95
	v_med3_f32 v241, v241, s62, v95
	v_mov_b32_e32 v242, 0
	v_mov_b32_e32 v243, 0
	v_mov_b32_e32 v244, 0
	v_mov_b32_e32 v245, 0
	v_cvt_pk_fp8_f32 v242, v226, v227
	v_cvt_pk_fp8_f32 v243, v230, v231
	v_cvt_pk_fp8_f32 v244, v234, v235
	v_cvt_pk_fp8_f32 v245, v238, v239
	v_cvt_pk_fp8_f32 v242, v228, v229 op_sel:[0,0,1]
	v_cvt_pk_fp8_f32 v243, v232, v233 op_sel:[0,0,1]
	v_cvt_pk_fp8_f32 v244, v236, v237 op_sel:[0,0,1]
	v_cvt_pk_fp8_f32 v245, v240, v241 op_sel:[0,0,1]
	s_nop 0
	global_store_dwordx4 v78, v[242:245], s[6:7]
	s_waitcnt vmcnt(12)
	v_mul_f32_e32 v144, v26, v144
	v_mul_f32_e32 v145, v26, v145
	v_mul_f32_e32 v146, v26, v146
	v_mul_f32_e32 v147, v26, v147
	ds_write_b128 v209, v[144:147]
	v_mul_f32_e32 v148, v27, v148
	v_mul_f32_e32 v149, v27, v149
	v_mul_f32_e32 v150, v27, v150
	v_mul_f32_e32 v151, v27, v151
	ds_write_b128 v209, v[148:151] offset:1024
	v_mul_f32_e32 v152, v28, v152
	v_mul_f32_e32 v153, v28, v153
	v_mul_f32_e32 v154, v28, v154
	v_mul_f32_e32 v155, v28, v155
	ds_write_b128 v209, v[152:155] offset:2048
	v_mul_f32_e32 v156, v29, v156
	v_mul_f32_e32 v157, v29, v157
	v_mul_f32_e32 v158, v29, v158
	v_mul_f32_e32 v159, v29, v159
	ds_write_b128 v209, v[156:159] offset:3072
	v_mul_f32_e32 v160, v30, v160
	v_mul_f32_e32 v161, v30, v161
	v_mul_f32_e32 v162, v30, v162
	v_mul_f32_e32 v163, v30, v163
	ds_write_b128 v209, v[160:163] offset:4096
	v_mul_f32_e32 v164, v31, v164
	v_mul_f32_e32 v165, v31, v165
	v_mul_f32_e32 v166, v31, v166
	v_mul_f32_e32 v167, v31, v167
	ds_write_b128 v209, v[164:167] offset:5120
	v_mul_f32_e32 v168, v32, v168
	v_mul_f32_e32 v169, v32, v169
	v_mul_f32_e32 v170, v32, v170
	v_mul_f32_e32 v171, v32, v171
	ds_write_b128 v209, v[168:171] offset:6144
	v_mul_f32_e32 v172, v33, v172
	v_mul_f32_e32 v173, v33, v173
	v_mul_f32_e32 v174, v33, v174
	v_mul_f32_e32 v175, v33, v175
	ds_write_b128 v209, v[172:175] offset:7168
	s_waitcnt lgkmcnt(0)
	s_barrier
; #define GAS __attribute__((address_space(1)))
; #define LAS __attribute__((address_space(3)))
; #define LDS_WAIT() asm volatile("s_waitcnt lgkmcnt(0)" ::: "memory")
;     ...
; #pragma unroll
;     for (int i = 0; i < 32; ++i) v[i] = sc >= 0 ? W[(size_t)(k0 + 2 * i + (lane >> 5)) * Nsrc + sc] : 0.f;
; #pragma unroll
;     for (int i = 0; i < 32; ++i) { const int k = k0 + 2 * i + (lane >> 5); float x = v[i] * wscale; if (KS) x *= (k < ksplit ? ksA[k] : ksB[k - ksplit]); scr[(2 * i + (lane >> 5)) * 33 + (lane & 31)] = x; }
;     LDS_WAIT(); asm volatile("" ::: "memory");
;     const int c = lane & 7;
; #pragma unroll
;     for (int j = 0; j < 4; ++j) { const int n = (lane >> 3) + 8 * j; const LAS float* s = scr + (8 * c) * 33 + n;
;         const unsigned long long o = (unsigned long long)pg8::pk4_fp8(s[0 * 33], s[1 * 33], s[2 * 33], s[3 * 33]) | ((unsigned long long)pg8::pk4_fp8(s[4 * 33], s[5 * 33], s[6 * 33], s[7 * 33]) << 32);
;         *(GAS unsigned long long*)(WT + (size_t)(n0 + n) * K + k0 + 8 * c) = o; }
; __global__ void __launch_bounds__(NWAVES * 64, 2) hybrid_fwd(Args args) {
;     ...
;             if (r < I_UP) { p0_transpose_item_f8<true>(args.in[15] + (size_t)l * DM * FF, DM, FF, FF / 32, (unsigned char*)(ws + WS_WUP + l * SZ_WUP), WUP8_SCALE, args.in[14] + l * DM, args.in[14] + l * DM, DM, scr, r, lane); continue; } r -= I_UP;
	s_add_u32 s8, s30, 0xc000
	s_addc_u32 s9, s31, 0
	global_load_dwordx4 v[144:147], v74, s[8:9]
	s_add_u32 s8, s8, 0x20000
	s_addc_u32 s9, s9, 0
	global_load_dwordx4 v[148:151], v74, s[8:9]
	s_add_u32 s8, s8, 0x20000
	s_addc_u32 s9, s9, 0
	global_load_dwordx4 v[152:155], v74, s[8:9]
	s_add_u32 s8, s8, 0x20000
	s_addc_u32 s9, s9, 0
	global_load_dwordx4 v[156:159], v74, s[8:9]
	s_add_u32 s8, s8, 0x20000
	s_addc_u32 s9, s9, 0
	global_load_dwordx4 v[160:163], v74, s[8:9]
	s_add_u32 s8, s8, 0x20000
	s_addc_u32 s9, s9, 0
	global_load_dwordx4 v[164:167], v74, s[8:9]
	s_add_u32 s8, s8, 0x20000
	s_addc_u32 s9, s9, 0
	global_load_dwordx4 v[168:171], v74, s[8:9]
	s_add_u32 s8, s8, 0x20000
	s_addc_u32 s9, s9, 0
	global_load_dwordx4 v[172:175], v74, s[8:9]
	s_add_u32 s6, s32, 0x2800000
	s_addc_u32 s7, s33, 0
	ds_read_b32 v226, v211
	ds_read_b32 v227, v211 offset:512
	ds_read_b32 v228, v211 offset:1024
	ds_read_b32 v229, v211 offset:1536
	ds_read_b32 v230, v211 offset:2048
	ds_read_b32 v231, v211 offset:2560
	ds_read_b32 v232, v211 offset:3072
	ds_read_b32 v233, v211 offset:3584
	ds_read_b32 v234, v211 offset:4096
	ds_read_b32 v235, v211 offset:4608
	ds_read_b32 v236, v211 offset:5120
	ds_read_b32 v237, v211 offset:5632
	ds_read_b32 v238, v211 offset:6144
	ds_read_b32 v239, v211 offset:6656
	ds_read_b32 v240, v211 offset:7168
	ds_read_b32 v241, v211 offset:7680
	s_waitcnt lgkmcnt(0)
	v_max_f32_e32 v226, v226, v226
	v_max_f32_e32 v227, v227, v227
	v_max_f32_e32 v228, v228, v228
	v_max_f32_e32 v229, v229, v229
	v_max_f32_e32 v230, v230, v230
	v_max_f32_e32 v231, v231, v231
	v_max_f32_e32 v232, v232, v232
	v_max_f32_e32 v233, v233, v233
	v_max_f32_e32 v234, v234, v234
	v_max_f32_e32 v235, v235, v235
	v_max_f32_e32 v236, v236, v236
	v_max_f32_e32 v237, v237, v237
	v_max_f32_e32 v238, v238, v238
	v_max_f32_e32 v239, v239, v239
	v_max_f32_e32 v240, v240, v240
	v_max_f32_e32 v241, v241, v241
	v_med3_f32 v226, v226, s62, v95
	v_med3_f32 v227, v227, s62, v95
	v_med3_f32 v228, v228, s62, v95
	v_med3_f32 v229, v229, s62, v95
	v_med3_f32 v230, v230, s62, v95
	v_med3_f32 v231, v231, s62, v95
	v_med3_f32 v232, v232, s62, v95
	v_med3_f32 v233, v233, s62, v95
	v_med3_f32 v234, v234, s62, v95
	v_med3_f32 v235, v235, s62, v95
	v_med3_f32 v236, v236, s62, v95
	v_med3_f32 v237, v237, s62, v95
	v_med3_f32 v238, v238, s62, v95
	v_med3_f32 v239, v239, s62, v95
	v_med3_f32 v240, v240, s62, v95
	v_med3_f32 v241, v241, s62, v95
	v_mov_b32_e32 v242, 0
	v_mov_b32_e32 v243, 0
	v_mov_b32_e32 v244, 0
	v_mov_b32_e32 v245, 0
	v_cvt_pk_fp8_f32 v242, v226, v227
	v_cvt_pk_fp8_f32 v243, v230, v231
	v_cvt_pk_fp8_f32 v244, v234, v235
	v_cvt_pk_fp8_f32 v245, v238, v239
	v_cvt_pk_fp8_f32 v242, v228, v229 op_sel:[0,0,1]
	v_cvt_pk_fp8_f32 v243, v232, v233 op_sel:[0,0,1]
	v_cvt_pk_fp8_f32 v244, v236, v237 op_sel:[0,0,1]
	v_cvt_pk_fp8_f32 v245, v240, v241 op_sel:[0,0,1]
	s_nop 0
	global_store_dwordx4 v77, v[242:245], s[6:7]
	ds_read_b32 v226, v213
	ds_read_b32 v227, v213 offset:512
	ds_read_b32 v228, v213 offset:1024
	ds_read_b32 v229, v213 offset:1536
	ds_read_b32 v230, v213 offset:2048
	ds_read_b32 v231, v213 offset:2560
	ds_read_b32 v232, v213 offset:3072
	ds_read_b32 v233, v213 offset:3584
	ds_read_b32 v234, v213 offset:4096
	ds_read_b32 v235, v213 offset:4608
	ds_read_b32 v236, v213 offset:5120
	ds_read_b32 v237, v213 offset:5632
	ds_read_b32 v238, v213 offset:6144
	ds_read_b32 v239, v213 offset:6656
	ds_read_b32 v240, v213 offset:7168
	ds_read_b32 v241, v213 offset:7680
	s_waitcnt lgkmcnt(0)
	v_max_f32_e32 v226, v226, v226
	v_max_f32_e32 v227, v227, v227
	v_max_f32_e32 v228, v228, v228
	v_max_f32_e32 v229, v229, v229
	v_max_f32_e32 v230, v230, v230
	v_max_f32_e32 v231, v231, v231
	v_max_f32_e32 v232, v232, v232
	v_max_f32_e32 v233, v233, v233
	v_max_f32_e32 v234, v234, v234
	v_max_f32_e32 v235, v235, v235
	v_max_f32_e32 v236, v236, v236
	v_max_f32_e32 v237, v237, v237
	v_max_f32_e32 v238, v238, v238
	v_max_f32_e32 v239, v239, v239
	v_max_f32_e32 v240, v240, v240
	v_max_f32_e32 v241, v241, v241
	v_med3_f32 v226, v226, s62, v95
	v_med3_f32 v227, v227, s62, v95
	v_med3_f32 v228, v228, s62, v95
	v_med3_f32 v229, v229, s62, v95
	v_med3_f32 v230, v230, s62, v95
	v_med3_f32 v231, v231, s62, v95
	v_med3_f32 v232, v232, s62, v95
	v_med3_f32 v233, v233, s62, v95
	v_med3_f32 v234, v234, s62, v95
	v_med3_f32 v235, v235, s62, v95
	v_med3_f32 v236, v236, s62, v95
	v_med3_f32 v237, v237, s62, v95
	v_med3_f32 v238, v238, s62, v95
	v_med3_f32 v239, v239, s62, v95
	v_med3_f32 v240, v240, s62, v95
	v_med3_f32 v241, v241, s62, v95
	v_mov_b32_e32 v242, 0
	v_mov_b32_e32 v243, 0
	v_mov_b32_e32 v244, 0
	v_mov_b32_e32 v245, 0
	v_cvt_pk_fp8_f32 v242, v226, v227
	v_cvt_pk_fp8_f32 v243, v230, v231
	v_cvt_pk_fp8_f32 v244, v234, v235
	v_cvt_pk_fp8_f32 v245, v238, v239
	v_cvt_pk_fp8_f32 v242, v228, v229 op_sel:[0,0,1]
	v_cvt_pk_fp8_f32 v243, v232, v233 op_sel:[0,0,1]
	v_cvt_pk_fp8_f32 v244, v236, v237 op_sel:[0,0,1]
	v_cvt_pk_fp8_f32 v245, v240, v241 op_sel:[0,0,1]
	s_nop 0
	global_store_dwordx4 v78, v[242:245], s[6:7]
	s_waitcnt vmcnt(12)
	v_mul_f32_e32 v176, v26, v176
	v_mul_f32_e32 v177, v26, v177
	v_mul_f32_e32 v178, v26, v178
	v_mul_f32_e32 v179, v26, v179
	ds_write_b128 v210, v[176:179]
	v_mul_f32_e32 v180, v27, v180
	v_mul_f32_e32 v181, v27, v181
	v_mul_f32_e32 v182, v27, v182
	v_mul_f32_e32 v183, v27, v183
	ds_write_b128 v210, v[180:183] offset:1024
	v_mul_f32_e32 v184, v28, v184
	v_mul_f32_e32 v185, v28, v185
	v_mul_f32_e32 v186, v28, v186
	v_mul_f32_e32 v187, v28, v187
	ds_write_b128 v210, v[184:187] offset:2048
	v_mul_f32_e32 v188, v29, v188
	v_mul_f32_e32 v189, v29, v189
	v_mul_f32_e32 v190, v29, v190
	v_mul_f32_e32 v191, v29, v191
	ds_write_b128 v210, v[188:191] offset:3072
	v_mul_f32_e32 v192, v30, v192
	v_mul_f32_e32 v193, v30, v193
	v_mul_f32_e32 v194, v30, v194
	v_mul_f32_e32 v195, v30, v195
	ds_write_b128 v210, v[192:195] offset:4096
	v_mul_f32_e32 v196, v31, v196
	v_mul_f32_e32 v197, v31, v197
	v_mul_f32_e32 v198, v31, v198
	v_mul_f32_e32 v199, v31, v199
	ds_write_b128 v210, v[196:199] offset:5120
	v_mul_f32_e32 v200, v32, v200
	v_mul_f32_e32 v201, v32, v201
	v_mul_f32_e32 v202, v32, v202
	v_mul_f32_e32 v203, v32, v203
	ds_write_b128 v210, v[200:203] offset:6144
	v_mul_f32_e32 v204, v33, v204
	v_mul_f32_e32 v205, v33, v205
	v_mul_f32_e32 v206, v33, v206
	v_mul_f32_e32 v207, v33, v207
	ds_write_b128 v210, v[204:207] offset:7168
	s_waitcnt lgkmcnt(0)
	s_barrier
; #define GAS __attribute__((address_space(1)))
; #define LAS __attribute__((address_space(3)))
; #define LDS_WAIT() asm volatile("s_waitcnt lgkmcnt(0)" ::: "memory")
;     ...
; #pragma unroll
;     for (int i = 0; i < 32; ++i) v[i] = sc >= 0 ? W[(size_t)(k0 + 2 * i + (lane >> 5)) * Nsrc + sc] : 0.f;
; #pragma unroll
;     for (int i = 0; i < 32; ++i) { const int k = k0 + 2 * i + (lane >> 5); float x = v[i] * wscale; if (KS) x *= (k < ksplit ? ksA[k] : ksB[k - ksplit]); scr[(2 * i + (lane >> 5)) * 33 + (lane & 31)] = x; }
;     LDS_WAIT(); asm volatile("" ::: "memory");
;     const int c = lane & 7;
; #pragma unroll
;     for (int j = 0; j < 4; ++j) { const int n = (lane >> 3) + 8 * j; const LAS float* s = scr + (8 * c) * 33 + n;
;         const unsigned long long o = (unsigned long long)pg8::pk4_fp8(s[0 * 33], s[1 * 33], s[2 * 33], s[3 * 33]) | ((unsigned long long)pg8::pk4_fp8(s[4 * 33], s[5 * 33], s[6 * 33], s[7 * 33]) << 32);
;         *(GAS unsigned long long*)(WT + (size_t)(n0 + n) * K + k0 + 8 * c) = o; }
; __global__ void __launch_bounds__(NWAVES * 64, 2) hybrid_fwd(Args args) {
;     ...
;             if (r < I_UP) { p0_transpose_item_f8<true>(args.in[15] + (size_t)l * DM * FF, DM, FF, FF / 32, (unsigned char*)(ws + WS_WUP + l * SZ_WUP), WUP8_SCALE, args.in[14] + l * DM, args.in[14] + l * DM, DM, scr, r, lane); continue; } r -= I_UP;
	s_add_u32 s8, s30, 0xd000
	s_addc_u32 s9, s31, 0
	global_load_dwordx4 v[176:179], v74, s[8:9]
	s_add_u32 s8, s8, 0x20000
	s_addc_u32 s9, s9, 0
	global_load_dwordx4 v[180:183], v74, s[8:9]
	s_add_u32 s8, s8, 0x20000
	s_addc_u32 s9, s9, 0
	global_load_dwordx4 v[184:187], v74, s[8:9]
	s_add_u32 s8, s8, 0x20000
	s_addc_u32 s9, s9, 0
	global_load_dwordx4 v[188:191], v74, s[8:9]
	s_add_u32 s8, s8, 0x20000
	s_addc_u32 s9, s9, 0
	global_load_dwordx4 v[192:195], v74, s[8:9]
	s_add_u32 s8, s8, 0x20000
	s_addc_u32 s9, s9, 0
	global_load_dwordx4 v[196:199], v74, s[8:9]
	s_add_u32 s8, s8, 0x20000
	s_addc_u32 s9, s9, 0
	global_load_dwordx4 v[200:203], v74, s[8:9]
	s_add_u32 s8, s8, 0x20000
	s_addc_u32 s9, s9, 0
	global_load_dwordx4 v[204:207], v74, s[8:9]
	s_add_u32 s6, s32, 0x2c00000
	s_addc_u32 s7, s33, 0
	ds_read_b32 v226, v212
	ds_read_b32 v227, v212 offset:512
	ds_read_b32 v228, v212 offset:1024
	ds_read_b32 v229, v212 offset:1536
	ds_read_b32 v230, v212 offset:2048
	ds_read_b32 v231, v212 offset:2560
	ds_read_b32 v232, v212 offset:3072
	ds_read_b32 v233, v212 offset:3584
	ds_read_b32 v234, v212 offset:4096
	ds_read_b32 v235, v212 offset:4608
	ds_read_b32 v236, v212 offset:5120
	ds_read_b32 v237, v212 offset:5632
	ds_read_b32 v238, v212 offset:6144
	ds_read_b32 v239, v212 offset:6656
	ds_read_b32 v240, v212 offset:7168
	ds_read_b32 v241, v212 offset:7680
	s_waitcnt lgkmcnt(0)
	v_max_f32_e32 v226, v226, v226
	v_max_f32_e32 v227, v227, v227
	v_max_f32_e32 v228, v228, v228
	v_max_f32_e32 v229, v229, v229
	v_max_f32_e32 v230, v230, v230
	v_max_f32_e32 v231, v231, v231
	v_max_f32_e32 v232, v232, v232
	v_max_f32_e32 v233, v233, v233
	v_max_f32_e32 v234, v234, v234
	v_max_f32_e32 v235, v235, v235
	v_max_f32_e32 v236, v236, v236
	v_max_f32_e32 v237, v237, v237
	v_max_f32_e32 v238, v238, v238
	v_max_f32_e32 v239, v239, v239
	v_max_f32_e32 v240, v240, v240
	v_max_f32_e32 v241, v241, v241
	v_med3_f32 v226, v226, s62, v95
	v_med3_f32 v227, v227, s62, v95
	v_med3_f32 v228, v228, s62, v95
	v_med3_f32 v229, v229, s62, v95
	v_med3_f32 v230, v230, s62, v95
	v_med3_f32 v231, v231, s62, v95
	v_med3_f32 v232, v232, s62, v95
	v_med3_f32 v233, v233, s62, v95
	v_med3_f32 v234, v234, s62, v95
	v_med3_f32 v235, v235, s62, v95
	v_med3_f32 v236, v236, s62, v95
	v_med3_f32 v237, v237, s62, v95
	v_med3_f32 v238, v238, s62, v95
	v_med3_f32 v239, v239, s62, v95
	v_med3_f32 v240, v240, s62, v95
	v_med3_f32 v241, v241, s62, v95
	v_mov_b32_e32 v242, 0
	v_mov_b32_e32 v243, 0
	v_mov_b32_e32 v244, 0
	v_mov_b32_e32 v245, 0
	v_cvt_pk_fp8_f32 v242, v226, v227
	v_cvt_pk_fp8_f32 v243, v230, v231
	v_cvt_pk_fp8_f32 v244, v234, v235
	v_cvt_pk_fp8_f32 v245, v238, v239
	v_cvt_pk_fp8_f32 v242, v228, v229 op_sel:[0,0,1]
	v_cvt_pk_fp8_f32 v243, v232, v233 op_sel:[0,0,1]
	v_cvt_pk_fp8_f32 v244, v236, v237 op_sel:[0,0,1]
	v_cvt_pk_fp8_f32 v245, v240, v241 op_sel:[0,0,1]
	s_nop 0
	global_store_dwordx4 v77, v[242:245], s[6:7]
	ds_read_b32 v226, v214
	ds_read_b32 v227, v214 offset:512
	ds_read_b32 v228, v214 offset:1024
	ds_read_b32 v229, v214 offset:1536
	ds_read_b32 v230, v214 offset:2048
	ds_read_b32 v231, v214 offset:2560
	ds_read_b32 v232, v214 offset:3072
	ds_read_b32 v233, v214 offset:3584
	ds_read_b32 v234, v214 offset:4096
	ds_read_b32 v235, v214 offset:4608
	ds_read_b32 v236, v214 offset:5120
	ds_read_b32 v237, v214 offset:5632
	ds_read_b32 v238, v214 offset:6144
	ds_read_b32 v239, v214 offset:6656
	ds_read_b32 v240, v214 offset:7168
	ds_read_b32 v241, v214 offset:7680
	s_waitcnt lgkmcnt(0)
	v_max_f32_e32 v226, v226, v226
	v_max_f32_e32 v227, v227, v227
	v_max_f32_e32 v228, v228, v228
	v_max_f32_e32 v229, v229, v229
	v_max_f32_e32 v230, v230, v230
	v_max_f32_e32 v231, v231, v231
	v_max_f32_e32 v232, v232, v232
	v_max_f32_e32 v233, v233, v233
	v_max_f32_e32 v234, v234, v234
	v_max_f32_e32 v235, v235, v235
	v_max_f32_e32 v236, v236, v236
	v_max_f32_e32 v237, v237, v237
	v_max_f32_e32 v238, v238, v238
	v_max_f32_e32 v239, v239, v239
	v_max_f32_e32 v240, v240, v240
	v_max_f32_e32 v241, v241, v241
	v_med3_f32 v226, v226, s62, v95
	v_med3_f32 v227, v227, s62, v95
	v_med3_f32 v228, v228, s62, v95
	v_med3_f32 v229, v229, s62, v95
	v_med3_f32 v230, v230, s62, v95
	v_med3_f32 v231, v231, s62, v95
	v_med3_f32 v232, v232, s62, v95
	v_med3_f32 v233, v233, s62, v95
	v_med3_f32 v234, v234, s62, v95
	v_med3_f32 v235, v235, s62, v95
	v_med3_f32 v236, v236, s62, v95
	v_med3_f32 v237, v237, s62, v95
	v_med3_f32 v238, v238, s62, v95
	v_med3_f32 v239, v239, s62, v95
	v_med3_f32 v240, v240, s62, v95
	v_med3_f32 v241, v241, s62, v95
	v_mov_b32_e32 v242, 0
	v_mov_b32_e32 v243, 0
	v_mov_b32_e32 v244, 0
	v_mov_b32_e32 v245, 0
	v_cvt_pk_fp8_f32 v242, v226, v227
	v_cvt_pk_fp8_f32 v243, v230, v231
	v_cvt_pk_fp8_f32 v244, v234, v235
	v_cvt_pk_fp8_f32 v245, v238, v239
	v_cvt_pk_fp8_f32 v242, v228, v229 op_sel:[0,0,1]
	v_cvt_pk_fp8_f32 v243, v232, v233 op_sel:[0,0,1]
	v_cvt_pk_fp8_f32 v244, v236, v237 op_sel:[0,0,1]
	v_cvt_pk_fp8_f32 v245, v240, v241 op_sel:[0,0,1]
	s_nop 0
	global_store_dwordx4 v78, v[242:245], s[6:7]
	s_waitcnt vmcnt(12)
	v_mul_f32_e32 v144, v26, v144
	v_mul_f32_e32 v145, v26, v145
	v_mul_f32_e32 v146, v26, v146
	v_mul_f32_e32 v147, v26, v147
	ds_write_b128 v209, v[144:147]
	v_mul_f32_e32 v148, v27, v148
	v_mul_f32_e32 v149, v27, v149
	v_mul_f32_e32 v150, v27, v150
	v_mul_f32_e32 v151, v27, v151
	ds_write_b128 v209, v[148:151] offset:1024
	v_mul_f32_e32 v152, v28, v152
	v_mul_f32_e32 v153, v28, v153
	v_mul_f32_e32 v154, v28, v154
	v_mul_f32_e32 v155, v28, v155
	ds_write_b128 v209, v[152:155] offset:2048
	v_mul_f32_e32 v156, v29, v156
	v_mul_f32_e32 v157, v29, v157
	v_mul_f32_e32 v158, v29, v158
	v_mul_f32_e32 v159, v29, v159
	ds_write_b128 v209, v[156:159] offset:3072
	v_mul_f32_e32 v160, v30, v160
	v_mul_f32_e32 v161, v30, v161
	v_mul_f32_e32 v162, v30, v162
	v_mul_f32_e32 v163, v30, v163
	ds_write_b128 v209, v[160:163] offset:4096
	v_mul_f32_e32 v164, v31, v164
	v_mul_f32_e32 v165, v31, v165
	v_mul_f32_e32 v166, v31, v166
	v_mul_f32_e32 v167, v31, v167
	ds_write_b128 v209, v[164:167] offset:5120
	v_mul_f32_e32 v168, v32, v168
	v_mul_f32_e32 v169, v32, v169
	v_mul_f32_e32 v170, v32, v170
	v_mul_f32_e32 v171, v32, v171
	ds_write_b128 v209, v[168:171] offset:6144
	v_mul_f32_e32 v172, v33, v172
	v_mul_f32_e32 v173, v33, v173
	v_mul_f32_e32 v174, v33, v174
	v_mul_f32_e32 v175, v33, v175
	ds_write_b128 v209, v[172:175] offset:7168
	s_waitcnt lgkmcnt(0)
	s_barrier
; #define GAS __attribute__((address_space(1)))
; #define LAS __attribute__((address_space(3)))
; #define LDS_WAIT() asm volatile("s_waitcnt lgkmcnt(0)" ::: "memory")
;     ...
; #pragma unroll
;     for (int i = 0; i < 32; ++i) v[i] = sc >= 0 ? W[(size_t)(k0 + 2 * i + (lane >> 5)) * Nsrc + sc] : 0.f;
; #pragma unroll
;     for (int i = 0; i < 32; ++i) { const int k = k0 + 2 * i + (lane >> 5); float x = v[i] * wscale; if (KS) x *= (k < ksplit ? ksA[k] : ksB[k - ksplit]); scr[(2 * i + (lane >> 5)) * 33 + (lane & 31)] = x; }
;     LDS_WAIT(); asm volatile("" ::: "memory");
;     const int c = lane & 7;
; #pragma unroll
;     for (int j = 0; j < 4; ++j) { const int n = (lane >> 3) + 8 * j; const LAS float* s = scr + (8 * c) * 33 + n;
;         const unsigned long long o = (unsigned long long)pg8::pk4_fp8(s[0 * 33], s[1 * 33], s[2 * 33], s[3 * 33]) | ((unsigned long long)pg8::pk4_fp8(s[4 * 33], s[5 * 33], s[6 * 33], s[7 * 33]) << 32);
;         *(GAS unsigned long long*)(WT + (size_t)(n0 + n) * K + k0 + 8 * c) = o; }
; __global__ void __launch_bounds__(NWAVES * 64, 2) hybrid_fwd(Args args) {
;     ...
;             if (r < I_UP) { p0_transpose_item_f8<true>(args.in[15] + (size_t)l * DM * FF, DM, FF, FF / 32, (unsigned char*)(ws + WS_WUP + l * SZ_WUP), WUP8_SCALE, args.in[14] + l * DM, args.in[14] + l * DM, DM, scr, r, lane); continue; } r -= I_UP;
	s_add_u32 s8, s30, 0xe000
	s_addc_u32 s9, s31, 0
	global_load_dwordx4 v[144:147], v74, s[8:9]
	s_add_u32 s8, s8, 0x20000
	s_addc_u32 s9, s9, 0
	global_load_dwordx4 v[148:151], v74, s[8:9]
	s_add_u32 s8, s8, 0x20000
	s_addc_u32 s9, s9, 0
	global_load_dwordx4 v[152:155], v74, s[8:9]
	s_add_u32 s8, s8, 0x20000
	s_addc_u32 s9, s9, 0
	global_load_dwordx4 v[156:159], v74, s[8:9]
	s_add_u32 s8, s8, 0x20000
	s_addc_u32 s9, s9, 0
	global_load_dwordx4 v[160:163], v74, s[8:9]
	s_add_u32 s8, s8, 0x20000
	s_addc_u32 s9, s9, 0
	global_load_dwordx4 v[164:167], v74, s[8:9]
	s_add_u32 s8, s8, 0x20000
	s_addc_u32 s9, s9, 0
	global_load_dwordx4 v[168:171], v74, s[8:9]
	s_add_u32 s8, s8, 0x20000
	s_addc_u32 s9, s9, 0
	global_load_dwordx4 v[172:175], v74, s[8:9]
	s_add_u32 s6, s32, 0x3000000
	s_addc_u32 s7, s33, 0
	ds_read_b32 v226, v211
	ds_read_b32 v227, v211 offset:512
	ds_read_b32 v228, v211 offset:1024
	ds_read_b32 v229, v211 offset:1536
	ds_read_b32 v230, v211 offset:2048
	ds_read_b32 v231, v211 offset:2560
	ds_read_b32 v232, v211 offset:3072
	ds_read_b32 v233, v211 offset:3584
	ds_read_b32 v234, v211 offset:4096
	ds_read_b32 v235, v211 offset:4608
	ds_read_b32 v236, v211 offset:5120
	ds_read_b32 v237, v211 offset:5632
	ds_read_b32 v238, v211 offset:6144
	ds_read_b32 v239, v211 offset:6656
	ds_read_b32 v240, v211 offset:7168
	ds_read_b32 v241, v211 offset:7680
	s_waitcnt lgkmcnt(0)
	v_max_f32_e32 v226, v226, v226
	v_max_f32_e32 v227, v227, v227
	v_max_f32_e32 v228, v228, v228
	v_max_f32_e32 v229, v229, v229
	v_max_f32_e32 v230, v230, v230
	v_max_f32_e32 v231, v231, v231
	v_max_f32_e32 v232, v232, v232
	v_max_f32_e32 v233, v233, v233
	v_max_f32_e32 v234, v234, v234
	v_max_f32_e32 v235, v235, v235
	v_max_f32_e32 v236, v236, v236
	v_max_f32_e32 v237, v237, v237
	v_max_f32_e32 v238, v238, v238
	v_max_f32_e32 v239, v239, v239
	v_max_f32_e32 v240, v240, v240
	v_max_f32_e32 v241, v241, v241
	v_med3_f32 v226, v226, s62, v95
	v_med3_f32 v227, v227, s62, v95
	v_med3_f32 v228, v228, s62, v95
	v_med3_f32 v229, v229, s62, v95
	v_med3_f32 v230, v230, s62, v95
	v_med3_f32 v231, v231, s62, v95
	v_med3_f32 v232, v232, s62, v95
	v_med3_f32 v233, v233, s62, v95
	v_med3_f32 v234, v234, s62, v95
	v_med3_f32 v235, v235, s62, v95
	v_med3_f32 v236, v236, s62, v95
	v_med3_f32 v237, v237, s62, v95
	v_med3_f32 v238, v238, s62, v95
	v_med3_f32 v239, v239, s62, v95
	v_med3_f32 v240, v240, s62, v95
	v_med3_f32 v241, v241, s62, v95
	v_mov_b32_e32 v242, 0
	v_mov_b32_e32 v243, 0
	v_mov_b32_e32 v244, 0
	v_mov_b32_e32 v245, 0
	v_cvt_pk_fp8_f32 v242, v226, v227
	v_cvt_pk_fp8_f32 v243, v230, v231
	v_cvt_pk_fp8_f32 v244, v234, v235
	v_cvt_pk_fp8_f32 v245, v238, v239
	v_cvt_pk_fp8_f32 v242, v228, v229 op_sel:[0,0,1]
	v_cvt_pk_fp8_f32 v243, v232, v233 op_sel:[0,0,1]
	v_cvt_pk_fp8_f32 v244, v236, v237 op_sel:[0,0,1]
	v_cvt_pk_fp8_f32 v245, v240, v241 op_sel:[0,0,1]
	s_nop 0
	global_store_dwordx4 v77, v[242:245], s[6:7]
	ds_read_b32 v226, v213
	ds_read_b32 v227, v213 offset:512
	ds_read_b32 v228, v213 offset:1024
	ds_read_b32 v229, v213 offset:1536
	ds_read_b32 v230, v213 offset:2048
	ds_read_b32 v231, v213 offset:2560
	ds_read_b32 v232, v213 offset:3072
	ds_read_b32 v233, v213 offset:3584
	ds_read_b32 v234, v213 offset:4096
	ds_read_b32 v235, v213 offset:4608
	ds_read_b32 v236, v213 offset:5120
	ds_read_b32 v237, v213 offset:5632
	ds_read_b32 v238, v213 offset:6144
	ds_read_b32 v239, v213 offset:6656
	ds_read_b32 v240, v213 offset:7168
	ds_read_b32 v241, v213 offset:7680
	s_waitcnt lgkmcnt(0)
	v_max_f32_e32 v226, v226, v226
	v_max_f32_e32 v227, v227, v227
	v_max_f32_e32 v228, v228, v228
	v_max_f32_e32 v229, v229, v229
	v_max_f32_e32 v230, v230, v230
	v_max_f32_e32 v231, v231, v231
	v_max_f32_e32 v232, v232, v232
	v_max_f32_e32 v233, v233, v233
	v_max_f32_e32 v234, v234, v234
	v_max_f32_e32 v235, v235, v235
	v_max_f32_e32 v236, v236, v236
	v_max_f32_e32 v237, v237, v237
	v_max_f32_e32 v238, v238, v238
	v_max_f32_e32 v239, v239, v239
	v_max_f32_e32 v240, v240, v240
	v_max_f32_e32 v241, v241, v241
	v_med3_f32 v226, v226, s62, v95
	v_med3_f32 v227, v227, s62, v95
	v_med3_f32 v228, v228, s62, v95
	v_med3_f32 v229, v229, s62, v95
	v_med3_f32 v230, v230, s62, v95
	v_med3_f32 v231, v231, s62, v95
	v_med3_f32 v232, v232, s62, v95
	v_med3_f32 v233, v233, s62, v95
	v_med3_f32 v234, v234, s62, v95
	v_med3_f32 v235, v235, s62, v95
	v_med3_f32 v236, v236, s62, v95
	v_med3_f32 v237, v237, s62, v95
	v_med3_f32 v238, v238, s62, v95
	v_med3_f32 v239, v239, s62, v95
	v_med3_f32 v240, v240, s62, v95
	v_med3_f32 v241, v241, s62, v95
	v_mov_b32_e32 v242, 0
	v_mov_b32_e32 v243, 0
	v_mov_b32_e32 v244, 0
	v_mov_b32_e32 v245, 0
	v_cvt_pk_fp8_f32 v242, v226, v227
	v_cvt_pk_fp8_f32 v243, v230, v231
	v_cvt_pk_fp8_f32 v244, v234, v235
	v_cvt_pk_fp8_f32 v245, v238, v239
	v_cvt_pk_fp8_f32 v242, v228, v229 op_sel:[0,0,1]
	v_cvt_pk_fp8_f32 v243, v232, v233 op_sel:[0,0,1]
	v_cvt_pk_fp8_f32 v244, v236, v237 op_sel:[0,0,1]
	v_cvt_pk_fp8_f32 v245, v240, v241 op_sel:[0,0,1]
	s_nop 0
	global_store_dwordx4 v78, v[242:245], s[6:7]
	s_waitcnt vmcnt(12)
	v_mul_f32_e32 v176, v26, v176
	v_mul_f32_e32 v177, v26, v177
	v_mul_f32_e32 v178, v26, v178
	v_mul_f32_e32 v179, v26, v179
	ds_write_b128 v210, v[176:179]
	v_mul_f32_e32 v180, v27, v180
	v_mul_f32_e32 v181, v27, v181
	v_mul_f32_e32 v182, v27, v182
	v_mul_f32_e32 v183, v27, v183
	ds_write_b128 v210, v[180:183] offset:1024
	v_mul_f32_e32 v184, v28, v184
	v_mul_f32_e32 v185, v28, v185
	v_mul_f32_e32 v186, v28, v186
	v_mul_f32_e32 v187, v28, v187
	ds_write_b128 v210, v[184:187] offset:2048
	v_mul_f32_e32 v188, v29, v188
	v_mul_f32_e32 v189, v29, v189
	v_mul_f32_e32 v190, v29, v190
	v_mul_f32_e32 v191, v29, v191
	ds_write_b128 v210, v[188:191] offset:3072
	v_mul_f32_e32 v192, v30, v192
	v_mul_f32_e32 v193, v30, v193
	v_mul_f32_e32 v194, v30, v194
	v_mul_f32_e32 v195, v30, v195
	ds_write_b128 v210, v[192:195] offset:4096
	v_mul_f32_e32 v196, v31, v196
	v_mul_f32_e32 v197, v31, v197
	v_mul_f32_e32 v198, v31, v198
	v_mul_f32_e32 v199, v31, v199
	ds_write_b128 v210, v[196:199] offset:5120
	v_mul_f32_e32 v200, v32, v200
	v_mul_f32_e32 v201, v32, v201
	v_mul_f32_e32 v202, v32, v202
	v_mul_f32_e32 v203, v32, v203
	ds_write_b128 v210, v[200:203] offset:6144
	v_mul_f32_e32 v204, v33, v204
	v_mul_f32_e32 v205, v33, v205
	v_mul_f32_e32 v206, v33, v206
	v_mul_f32_e32 v207, v33, v207
	ds_write_b128 v210, v[204:207] offset:7168
	s_waitcnt lgkmcnt(0)
	s_barrier
; #define GAS __attribute__((address_space(1)))
; #define LAS __attribute__((address_space(3)))
; #define LDS_WAIT() asm volatile("s_waitcnt lgkmcnt(0)" ::: "memory")
;     const int pr = item >> 1, kb = 2 * (pr / nblk) + (item & 1), nb = pr % nblk, k0 = 64 * kb, n0 = 32 * nb;
;     const int nr = n0 + (lane & 31); const int sc = MAP == 1 ? src_col_in(nr) : nr;
;     float v[32];
; #pragma unroll
;     for (int i = 0; i < 32; ++i) v[i] = sc >= 0 ? W[(size_t)(k0 + 2 * i + (lane >> 5)) * Nsrc + sc] : 0.f;
; #pragma unroll
;     for (int i = 0; i < 32; ++i) { const int k = k0 + 2 * i + (lane >> 5); float x = v[i] * wscale; if (KS) x *= (k < ksplit ? ksA[k] : ksB[k - ksplit]); scr[(2 * i + (lane >> 5)) * 33 + (lane & 31)] = x; }
;     LDS_WAIT(); asm volatile("" ::: "memory");
;     const int c = lane & 7;
; #pragma unroll
;     for (int j = 0; j < 4; ++j) { const int n = (lane >> 3) + 8 * j; const LAS float* s = scr + (8 * c) * 33 + n;
;         const unsigned long long o = (unsigned long long)pg8::pk4_fp8(s[0 * 33], s[1 * 33], s[2 * 33], s[3 * 33]) | ((unsigned long long)pg8::pk4_fp8(s[4 * 33], s[5 * 33], s[6 * 33], s[7 * 33]) << 32);
;         *(GAS unsigned long long*)(WT + (size_t)(n0 + n) * K + k0 + 8 * c) = o; }
;     LDS_WAIT(); asm volatile("" ::: "memory");
; }
; __global__ void __launch_bounds__(NWAVES * 64, 2) hybrid_fwd(Args args) {
;     ...
;             if (r < I_UP) { p0_transpose_item_f8<true>(args.in[15] + (size_t)l * DM * FF, DM, FF, FF / 32, (unsigned char*)(ws + WS_WUP + l * SZ_WUP), WUP8_SCALE, args.in[14] + l * DM, args.in[14] + l * DM, DM, scr, r, lane); continue; } r -= I_UP;
	s_add_u32 s8, s30, 0xf000
	s_addc_u32 s9, s31, 0
	global_load_dwordx4 v[176:179], v74, s[8:9]
	s_add_u32 s8, s8, 0x20000
	s_addc_u32 s9, s9, 0
	global_load_dwordx4 v[180:183], v74, s[8:9]
	s_add_u32 s8, s8, 0x20000
	s_addc_u32 s9, s9, 0
	global_load_dwordx4 v[184:187], v74, s[8:9]
	s_add_u32 s8, s8, 0x20000
	s_addc_u32 s9, s9, 0
	global_load_dwordx4 v[188:191], v74, s[8:9]
	s_add_u32 s8, s8, 0x20000
	s_addc_u32 s9, s9, 0
	global_load_dwordx4 v[192:195], v74, s[8:9]
	s_add_u32 s8, s8, 0x20000
	s_addc_u32 s9, s9, 0
	global_load_dwordx4 v[196:199], v74, s[8:9]
	s_add_u32 s8, s8, 0x20000
	s_addc_u32 s9, s9, 0
	global_load_dwordx4 v[200:203], v74, s[8:9]
	s_add_u32 s8, s8, 0x20000
	s_addc_u32 s9, s9, 0
	global_load_dwordx4 v[204:207], v74, s[8:9]
	s_add_u32 s6, s32, 0x3400000
	s_addc_u32 s7, s33, 0
	ds_read_b32 v226, v212
	ds_read_b32 v227, v212 offset:512
	ds_read_b32 v228, v212 offset:1024
	ds_read_b32 v229, v212 offset:1536
	ds_read_b32 v230, v212 offset:2048
	ds_read_b32 v231, v212 offset:2560
	ds_read_b32 v232, v212 offset:3072
	ds_read_b32 v233, v212 offset:3584
	ds_read_b32 v234, v212 offset:4096
	ds_read_b32 v235, v212 offset:4608
	ds_read_b32 v236, v212 offset:5120
	ds_read_b32 v237, v212 offset:5632
	ds_read_b32 v238, v212 offset:6144
	ds_read_b32 v239, v212 offset:6656
	ds_read_b32 v240, v212 offset:7168
	ds_read_b32 v241, v212 offset:7680
	s_waitcnt lgkmcnt(0)
	v_max_f32_e32 v226, v226, v226
	v_max_f32_e32 v227, v227, v227
	v_max_f32_e32 v228, v228, v228
	v_max_f32_e32 v229, v229, v229
	v_max_f32_e32 v230, v230, v230
	v_max_f32_e32 v231, v231, v231
	v_max_f32_e32 v232, v232, v232
	v_max_f32_e32 v233, v233, v233
	v_max_f32_e32 v234, v234, v234
	v_max_f32_e32 v235, v235, v235
	v_max_f32_e32 v236, v236, v236
	v_max_f32_e32 v237, v237, v237
	v_max_f32_e32 v238, v238, v238
	v_max_f32_e32 v239, v239, v239
	v_max_f32_e32 v240, v240, v240
	v_max_f32_e32 v241, v241, v241
	v_med3_f32 v226, v226, s62, v95
	v_med3_f32 v227, v227, s62, v95
	v_med3_f32 v228, v228, s62, v95
	v_med3_f32 v229, v229, s62, v95
	v_med3_f32 v230, v230, s62, v95
	v_med3_f32 v231, v231, s62, v95
	v_med3_f32 v232, v232, s62, v95
	v_med3_f32 v233, v233, s62, v95
	v_med3_f32 v234, v234, s62, v95
	v_med3_f32 v235, v235, s62, v95
	v_med3_f32 v236, v236, s62, v95
	v_med3_f32 v237, v237, s62, v95
	v_med3_f32 v238, v238, s62, v95
	v_med3_f32 v239, v239, s62, v95
	v_med3_f32 v240, v240, s62, v95
	v_med3_f32 v241, v241, s62, v95
	v_mov_b32_e32 v242, 0
	v_mov_b32_e32 v243, 0
	v_mov_b32_e32 v244, 0
	v_mov_b32_e32 v245, 0
	v_cvt_pk_fp8_f32 v242, v226, v227
	v_cvt_pk_fp8_f32 v243, v230, v231
	v_cvt_pk_fp8_f32 v244, v234, v235
	v_cvt_pk_fp8_f32 v245, v238, v239
	v_cvt_pk_fp8_f32 v242, v228, v229 op_sel:[0,0,1]
	v_cvt_pk_fp8_f32 v243, v232, v233 op_sel:[0,0,1]
	v_cvt_pk_fp8_f32 v244, v236, v237 op_sel:[0,0,1]
	v_cvt_pk_fp8_f32 v245, v240, v241 op_sel:[0,0,1]
	s_nop 0
	global_store_dwordx4 v77, v[242:245], s[6:7]
	ds_read_b32 v226, v214
	ds_read_b32 v227, v214 offset:512
	ds_read_b32 v228, v214 offset:1024
	ds_read_b32 v229, v214 offset:1536
	ds_read_b32 v230, v214 offset:2048
	ds_read_b32 v231, v214 offset:2560
	ds_read_b32 v232, v214 offset:3072
	ds_read_b32 v233, v214 offset:3584
	ds_read_b32 v234, v214 offset:4096
	ds_read_b32 v235, v214 offset:4608
	ds_read_b32 v236, v214 offset:5120
	ds_read_b32 v237, v214 offset:5632
	ds_read_b32 v238, v214 offset:6144
	ds_read_b32 v239, v214 offset:6656
	ds_read_b32 v240, v214 offset:7168
	ds_read_b32 v241, v214 offset:7680
	s_waitcnt lgkmcnt(0)
	v_max_f32_e32 v226, v226, v226
	v_max_f32_e32 v227, v227, v227
	v_max_f32_e32 v228, v228, v228
	v_max_f32_e32 v229, v229, v229
	v_max_f32_e32 v230, v230, v230
	v_max_f32_e32 v231, v231, v231
	v_max_f32_e32 v232, v232, v232
	v_max_f32_e32 v233, v233, v233
	v_max_f32_e32 v234, v234, v234
	v_max_f32_e32 v235, v235, v235
	v_max_f32_e32 v236, v236, v236
	v_max_f32_e32 v237, v237, v237
	v_max_f32_e32 v238, v238, v238
	v_max_f32_e32 v239, v239, v239
	v_max_f32_e32 v240, v240, v240
	v_max_f32_e32 v241, v241, v241
	v_med3_f32 v226, v226, s62, v95
	v_med3_f32 v227, v227, s62, v95
	v_med3_f32 v228, v228, s62, v95
	v_med3_f32 v229, v229, s62, v95
	v_med3_f32 v230, v230, s62, v95
	v_med3_f32 v231, v231, s62, v95
	v_med3_f32 v232, v232, s62, v95
	v_med3_f32 v233, v233, s62, v95
	v_med3_f32 v234, v234, s62, v95
	v_med3_f32 v235, v235, s62, v95
	v_med3_f32 v236, v236, s62, v95
	v_med3_f32 v237, v237, s62, v95
	v_med3_f32 v238, v238, s62, v95
	v_med3_f32 v239, v239, s62, v95
	v_med3_f32 v240, v240, s62, v95
	v_med3_f32 v241, v241, s62, v95
	v_mov_b32_e32 v242, 0
	v_mov_b32_e32 v243, 0
	v_mov_b32_e32 v244, 0
	v_mov_b32_e32 v245, 0
	v_cvt_pk_fp8_f32 v242, v226, v227
	v_cvt_pk_fp8_f32 v243, v230, v231
	v_cvt_pk_fp8_f32 v244, v234, v235
	v_cvt_pk_fp8_f32 v245, v238, v239
	v_cvt_pk_fp8_f32 v242, v228, v229 op_sel:[0,0,1]
	v_cvt_pk_fp8_f32 v243, v232, v233 op_sel:[0,0,1]
	v_cvt_pk_fp8_f32 v244, v236, v237 op_sel:[0,0,1]
	v_cvt_pk_fp8_f32 v245, v240, v241 op_sel:[0,0,1]
	s_nop 0
	global_store_dwordx4 v78, v[242:245], s[6:7]
	s_waitcnt vmcnt(12)
	v_mul_f32_e32 v144, v26, v144
	v_mul_f32_e32 v145, v26, v145
	v_mul_f32_e32 v146, v26, v146
	v_mul_f32_e32 v147, v26, v147
	ds_write_b128 v209, v[144:147]
	v_mul_f32_e32 v148, v27, v148
	v_mul_f32_e32 v149, v27, v149
	v_mul_f32_e32 v150, v27, v150
	v_mul_f32_e32 v151, v27, v151
	ds_write_b128 v209, v[148:151] offset:1024
	v_mul_f32_e32 v152, v28, v152
	v_mul_f32_e32 v153, v28, v153
	v_mul_f32_e32 v154, v28, v154
	v_mul_f32_e32 v155, v28, v155
	ds_write_b128 v209, v[152:155] offset:2048
	v_mul_f32_e32 v156, v29, v156
	v_mul_f32_e32 v157, v29, v157
	v_mul_f32_e32 v158, v29, v158
	v_mul_f32_e32 v159, v29, v159
	ds_write_b128 v209, v[156:159] offset:3072
	v_mul_f32_e32 v160, v30, v160
	v_mul_f32_e32 v161, v30, v161
	v_mul_f32_e32 v162, v30, v162
	v_mul_f32_e32 v163, v30, v163
	ds_write_b128 v209, v[160:163] offset:4096
	v_mul_f32_e32 v164, v31, v164
	v_mul_f32_e32 v165, v31, v165
	v_mul_f32_e32 v166, v31, v166
	v_mul_f32_e32 v167, v31, v167
	ds_write_b128 v209, v[164:167] offset:5120
	v_mul_f32_e32 v168, v32, v168
	v_mul_f32_e32 v169, v32, v169
	v_mul_f32_e32 v170, v32, v170
	v_mul_f32_e32 v171, v32, v171
	ds_write_b128 v209, v[168:171] offset:6144
	v_mul_f32_e32 v172, v33, v172
	v_mul_f32_e32 v173, v33, v173
	v_mul_f32_e32 v174, v33, v174
	v_mul_f32_e32 v175, v33, v175
	ds_write_b128 v209, v[172:175] offset:7168
	s_waitcnt lgkmcnt(0)
	s_barrier
; #define GAS __attribute__((address_space(1)))
; #define LAS __attribute__((address_space(3)))
; #define LDS_WAIT() asm volatile("s_waitcnt lgkmcnt(0)" ::: "memory")
;     const int pr = item >> 1, kb = 2 * (pr / nblk) + (item & 1), nb = pr % nblk, k0 = 64 * kb, n0 = 32 * nb;
;     const int nr = n0 + (lane & 31); const int sc = MAP == 1 ? src_col_in(nr) : nr;
;     float v[32];
; #pragma unroll
;     for (int i = 0; i < 32; ++i) v[i] = sc >= 0 ? W[(size_t)(k0 + 2 * i + (lane >> 5)) * Nsrc + sc] : 0.f;
; #pragma unroll
;     for (int i = 0; i < 32; ++i) { const int k = k0 + 2 * i + (lane >> 5); float x = v[i] * wscale; if (KS) x *= (k < ksplit ? ksA[k] : ksB[k - ksplit]); scr[(2 * i + (lane >> 5)) * 33 + (lane & 31)] = x; }
;     LDS_WAIT(); asm volatile("" ::: "memory");
;     const int c = lane & 7;
; #pragma unroll
;     for (int j = 0; j < 4; ++j) { const int n = (lane >> 3) + 8 * j; const LAS float* s = scr + (8 * c) * 33 + n;
;         const unsigned long long o = (unsigned long long)pg8::pk4_fp8(s[0 * 33], s[1 * 33], s[2 * 33], s[3 * 33]) | ((unsigned long long)pg8::pk4_fp8(s[4 * 33], s[5 * 33], s[6 * 33], s[7 * 33]) << 32);
;         *(GAS unsigned long long*)(WT + (size_t)(n0 + n) * K + k0 + 8 * c) = o; }
;     LDS_WAIT(); asm volatile("" ::: "memory");
; }
; __global__ void __launch_bounds__(NWAVES * 64, 2) hybrid_fwd(Args args) {
;     ...
;             if (r < I_UP) { p0_transpose_item_f8<true>(args.in[15] + (size_t)l * DM * FF, DM, FF, FF / 32, (unsigned char*)(ws + WS_WUP + l * SZ_WUP), WUP8_SCALE, args.in[14] + l * DM, args.in[14] + l * DM, DM, scr, r, lane); continue; } r -= I_UP;
	s_mov_b64 s[8:9], s[34:35]
	global_load_dwordx4 v[144:147], v74, s[8:9]
	s_add_u32 s8, s8, 0x20000
	s_addc_u32 s9, s9, 0
	global_load_dwordx4 v[148:151], v74, s[8:9]
	s_add_u32 s8, s8, 0x20000
	s_addc_u32 s9, s9, 0
	global_load_dwordx4 v[152:155], v74, s[8:9]
	s_add_u32 s8, s8, 0x20000
	s_addc_u32 s9, s9, 0
	global_load_dwordx4 v[156:159], v74, s[8:9]
	s_add_u32 s8, s8, 0x20000
	s_addc_u32 s9, s9, 0
	global_load_dwordx4 v[160:163], v74, s[8:9]
	s_add_u32 s8, s8, 0x20000
	s_addc_u32 s9, s9, 0
	global_load_dwordx4 v[164:167], v74, s[8:9]
	s_add_u32 s8, s8, 0x20000
	s_addc_u32 s9, s9, 0
	global_load_dwordx4 v[168:171], v74, s[8:9]
	s_add_u32 s8, s8, 0x20000
	s_addc_u32 s9, s9, 0
	global_load_dwordx4 v[172:175], v74, s[8:9]
	s_add_u32 s6, s32, 0x3800000
	s_addc_u32 s7, s33, 0
	ds_read_b32 v226, v211
	ds_read_b32 v227, v211 offset:512
	ds_read_b32 v228, v211 offset:1024
	ds_read_b32 v229, v211 offset:1536
	ds_read_b32 v230, v211 offset:2048
	ds_read_b32 v231, v211 offset:2560
	ds_read_b32 v232, v211 offset:3072
	ds_read_b32 v233, v211 offset:3584
	ds_read_b32 v234, v211 offset:4096
	ds_read_b32 v235, v211 offset:4608
	ds_read_b32 v236, v211 offset:5120
	ds_read_b32 v237, v211 offset:5632
	ds_read_b32 v238, v211 offset:6144
	ds_read_b32 v239, v211 offset:6656
	ds_read_b32 v240, v211 offset:7168
	ds_read_b32 v241, v211 offset:7680
	s_waitcnt lgkmcnt(0)
	v_max_f32_e32 v226, v226, v226
	v_max_f32_e32 v227, v227, v227
	v_max_f32_e32 v228, v228, v228
	v_max_f32_e32 v229, v229, v229
	v_max_f32_e32 v230, v230, v230
	v_max_f32_e32 v231, v231, v231
	v_max_f32_e32 v232, v232, v232
	v_max_f32_e32 v233, v233, v233
	v_max_f32_e32 v234, v234, v234
	v_max_f32_e32 v235, v235, v235
	v_max_f32_e32 v236, v236, v236
	v_max_f32_e32 v237, v237, v237
	v_max_f32_e32 v238, v238, v238
	v_max_f32_e32 v239, v239, v239
	v_max_f32_e32 v240, v240, v240
	v_max_f32_e32 v241, v241, v241
	v_med3_f32 v226, v226, s62, v95
	v_med3_f32 v227, v227, s62, v95
	v_med3_f32 v228, v228, s62, v95
	v_med3_f32 v229, v229, s62, v95
	v_med3_f32 v230, v230, s62, v95
	v_med3_f32 v231, v231, s62, v95
	v_med3_f32 v232, v232, s62, v95
	v_med3_f32 v233, v233, s62, v95
	v_med3_f32 v234, v234, s62, v95
	v_med3_f32 v235, v235, s62, v95
	v_med3_f32 v236, v236, s62, v95
	v_med3_f32 v237, v237, s62, v95
	v_med3_f32 v238, v238, s62, v95
	v_med3_f32 v239, v239, s62, v95
	v_med3_f32 v240, v240, s62, v95
	v_med3_f32 v241, v241, s62, v95
	v_mov_b32_e32 v242, 0
	v_mov_b32_e32 v243, 0
	v_mov_b32_e32 v244, 0
	v_mov_b32_e32 v245, 0
	v_cvt_pk_fp8_f32 v242, v226, v227
	v_cvt_pk_fp8_f32 v243, v230, v231
	v_cvt_pk_fp8_f32 v244, v234, v235
	v_cvt_pk_fp8_f32 v245, v238, v239
	v_cvt_pk_fp8_f32 v242, v228, v229 op_sel:[0,0,1]
	v_cvt_pk_fp8_f32 v243, v232, v233 op_sel:[0,0,1]
	v_cvt_pk_fp8_f32 v244, v236, v237 op_sel:[0,0,1]
	v_cvt_pk_fp8_f32 v245, v240, v241 op_sel:[0,0,1]
	s_nop 0
	global_store_dwordx4 v77, v[242:245], s[6:7]
	ds_read_b32 v226, v213
	ds_read_b32 v227, v213 offset:512
	ds_read_b32 v228, v213 offset:1024
	ds_read_b32 v229, v213 offset:1536
	ds_read_b32 v230, v213 offset:2048
	ds_read_b32 v231, v213 offset:2560
	ds_read_b32 v232, v213 offset:3072
	ds_read_b32 v233, v213 offset:3584
	ds_read_b32 v234, v213 offset:4096
	ds_read_b32 v235, v213 offset:4608
	ds_read_b32 v236, v213 offset:5120
	ds_read_b32 v237, v213 offset:5632
	ds_read_b32 v238, v213 offset:6144
	ds_read_b32 v239, v213 offset:6656
	ds_read_b32 v240, v213 offset:7168
	ds_read_b32 v241, v213 offset:7680
	s_waitcnt lgkmcnt(0)
	v_max_f32_e32 v226, v226, v226
	v_max_f32_e32 v227, v227, v227
	v_max_f32_e32 v228, v228, v228
	v_max_f32_e32 v229, v229, v229
	v_max_f32_e32 v230, v230, v230
	v_max_f32_e32 v231, v231, v231
	v_max_f32_e32 v232, v232, v232
	v_max_f32_e32 v233, v233, v233
	v_max_f32_e32 v234, v234, v234
	v_max_f32_e32 v235, v235, v235
	v_max_f32_e32 v236, v236, v236
	v_max_f32_e32 v237, v237, v237
	v_max_f32_e32 v238, v238, v238
	v_max_f32_e32 v239, v239, v239
	v_max_f32_e32 v240, v240, v240
	v_max_f32_e32 v241, v241, v241
	v_med3_f32 v226, v226, s62, v95
	v_med3_f32 v227, v227, s62, v95
	v_med3_f32 v228, v228, s62, v95
	v_med3_f32 v229, v229, s62, v95
	v_med3_f32 v230, v230, s62, v95
	v_med3_f32 v231, v231, s62, v95
	v_med3_f32 v232, v232, s62, v95
	v_med3_f32 v233, v233, s62, v95
	v_med3_f32 v234, v234, s62, v95
	v_med3_f32 v235, v235, s62, v95
	v_med3_f32 v236, v236, s62, v95
	v_med3_f32 v237, v237, s62, v95
	v_med3_f32 v238, v238, s62, v95
	v_med3_f32 v239, v239, s62, v95
	v_med3_f32 v240, v240, s62, v95
	v_med3_f32 v241, v241, s62, v95
	v_mov_b32_e32 v242, 0
	v_mov_b32_e32 v243, 0
	v_mov_b32_e32 v244, 0
	v_mov_b32_e32 v245, 0
	v_cvt_pk_fp8_f32 v242, v226, v227
	v_cvt_pk_fp8_f32 v243, v230, v231
	v_cvt_pk_fp8_f32 v244, v234, v235
	v_cvt_pk_fp8_f32 v245, v238, v239
	v_cvt_pk_fp8_f32 v242, v228, v229 op_sel:[0,0,1]
	v_cvt_pk_fp8_f32 v243, v232, v233 op_sel:[0,0,1]
	v_cvt_pk_fp8_f32 v244, v236, v237 op_sel:[0,0,1]
	v_cvt_pk_fp8_f32 v245, v240, v241 op_sel:[0,0,1]
	s_nop 0
	global_store_dwordx4 v78, v[242:245], s[6:7]
	s_waitcnt vmcnt(12)
	v_mul_f32_e32 v176, v26, v176
	v_mul_f32_e32 v177, v26, v177
	v_mul_f32_e32 v178, v26, v178
	v_mul_f32_e32 v179, v26, v179
	ds_write_b128 v210, v[176:179]
	v_mul_f32_e32 v180, v27, v180
	v_mul_f32_e32 v181, v27, v181
	v_mul_f32_e32 v182, v27, v182
	v_mul_f32_e32 v183, v27, v183
	ds_write_b128 v210, v[180:183] offset:1024
	v_mul_f32_e32 v184, v28, v184
	v_mul_f32_e32 v185, v28, v185
	v_mul_f32_e32 v186, v28, v186
	v_mul_f32_e32 v187, v28, v187
	ds_write_b128 v210, v[184:187] offset:2048
	v_mul_f32_e32 v188, v29, v188
	v_mul_f32_e32 v189, v29, v189
	v_mul_f32_e32 v190, v29, v190
	v_mul_f32_e32 v191, v29, v191
	ds_write_b128 v210, v[188:191] offset:3072
	v_mul_f32_e32 v192, v30, v192
	v_mul_f32_e32 v193, v30, v193
	v_mul_f32_e32 v194, v30, v194
	v_mul_f32_e32 v195, v30, v195
	ds_write_b128 v210, v[192:195] offset:4096
	v_mul_f32_e32 v196, v31, v196
	v_mul_f32_e32 v197, v31, v197
	v_mul_f32_e32 v198, v31, v198
	v_mul_f32_e32 v199, v31, v199
	ds_write_b128 v210, v[196:199] offset:5120
	v_mul_f32_e32 v200, v32, v200
	v_mul_f32_e32 v201, v32, v201
	v_mul_f32_e32 v202, v32, v202
	v_mul_f32_e32 v203, v32, v203
	ds_write_b128 v210, v[200:203] offset:6144
	v_mul_f32_e32 v204, v33, v204
	v_mul_f32_e32 v205, v33, v205
	v_mul_f32_e32 v206, v33, v206
	v_mul_f32_e32 v207, v33, v207
	ds_write_b128 v210, v[204:207] offset:7168
	s_waitcnt lgkmcnt(0)
	s_barrier
; #define GAS __attribute__((address_space(1)))
; #define LAS __attribute__((address_space(3)))
; #define LDS_WAIT() asm volatile("s_waitcnt lgkmcnt(0)" ::: "memory")
;     const int pr = item >> 1, kb = 2 * (pr / nblk) + (item & 1), nb = pr % nblk, k0 = 64 * kb, n0 = 32 * nb;
;     const int nr = n0 + (lane & 31); const int sc = MAP == 1 ? src_col_in(nr) : nr;
;     float v[32];
; #pragma unroll
;     for (int i = 0; i < 32; ++i) v[i] = sc >= 0 ? W[(size_t)(k0 + 2 * i + (lane >> 5)) * Nsrc + sc] : 0.f;
; #pragma unroll
;     for (int i = 0; i < 32; ++i) { const int k = k0 + 2 * i + (lane >> 5); float x = v[i] * wscale; if (KS) x *= (k < ksplit ? ksA[k] : ksB[k - ksplit]); scr[(2 * i + (lane >> 5)) * 33 + (lane & 31)] = x; }
;     LDS_WAIT(); asm volatile("" ::: "memory");
;     const int c = lane & 7;
; #pragma unroll
;     for (int j = 0; j < 4; ++j) { const int n = (lane >> 3) + 8 * j; const LAS float* s = scr + (8 * c) * 33 + n;
;         const unsigned long long o = (unsigned long long)pg8::pk4_fp8(s[0 * 33], s[1 * 33], s[2 * 33], s[3 * 33]) | ((unsigned long long)pg8::pk4_fp8(s[4 * 33], s[5 * 33], s[6 * 33], s[7 * 33]) << 32);
;         *(GAS unsigned long long*)(WT + (size_t)(n0 + n) * K + k0 + 8 * c) = o; }
;     LDS_WAIT(); asm volatile("" ::: "memory");
; }
; __global__ void __launch_bounds__(NWAVES * 64, 2) hybrid_fwd(Args args) {
;     ...
;             if (r < I_UP) { p0_transpose_item_f8<true>(args.in[15] + (size_t)l * DM * FF, DM, FF, FF / 32, (unsigned char*)(ws + WS_WUP + l * SZ_WUP), WUP8_SCALE, args.in[14] + l * DM, args.in[14] + l * DM, DM, scr, r, lane); continue; } r -= I_UP;
	s_add_u32 s8, s34, 0x1000
	s_addc_u32 s9, s35, 0
	global_load_dwordx4 v[176:179], v74, s[8:9]
	s_add_u32 s8, s8, 0x20000
	s_addc_u32 s9, s9, 0
	global_load_dwordx4 v[180:183], v74, s[8:9]
	s_add_u32 s8, s8, 0x20000
	s_addc_u32 s9, s9, 0
	global_load_dwordx4 v[184:187], v74, s[8:9]
	s_add_u32 s8, s8, 0x20000
	s_addc_u32 s9, s9, 0
	global_load_dwordx4 v[188:191], v74, s[8:9]
	s_add_u32 s8, s8, 0x20000
	s_addc_u32 s9, s9, 0
	global_load_dwordx4 v[192:195], v74, s[8:9]
	s_add_u32 s8, s8, 0x20000
	s_addc_u32 s9, s9, 0
	global_load_dwordx4 v[196:199], v74, s[8:9]
	s_add_u32 s8, s8, 0x20000
	s_addc_u32 s9, s9, 0
	global_load_dwordx4 v[200:203], v74, s[8:9]
	s_add_u32 s8, s8, 0x20000
	s_addc_u32 s9, s9, 0
	global_load_dwordx4 v[204:207], v74, s[8:9]
	s_add_u32 s6, s32, 0x3c00000
	s_addc_u32 s7, s33, 0
	ds_read_b32 v226, v212
	ds_read_b32 v227, v212 offset:512
	ds_read_b32 v228, v212 offset:1024
	ds_read_b32 v229, v212 offset:1536
	ds_read_b32 v230, v212 offset:2048
	ds_read_b32 v231, v212 offset:2560
	ds_read_b32 v232, v212 offset:3072
	ds_read_b32 v233, v212 offset:3584
	ds_read_b32 v234, v212 offset:4096
	ds_read_b32 v235, v212 offset:4608
	ds_read_b32 v236, v212 offset:5120
	ds_read_b32 v237, v212 offset:5632
	ds_read_b32 v238, v212 offset:6144
	ds_read_b32 v239, v212 offset:6656
	ds_read_b32 v240, v212 offset:7168
	ds_read_b32 v241, v212 offset:7680
	s_waitcnt lgkmcnt(0)
	v_max_f32_e32 v226, v226, v226
	v_max_f32_e32 v227, v227, v227
	v_max_f32_e32 v228, v228, v228
	v_max_f32_e32 v229, v229, v229
	v_max_f32_e32 v230, v230, v230
	v_max_f32_e32 v231, v231, v231
	v_max_f32_e32 v232, v232, v232
	v_max_f32_e32 v233, v233, v233
	v_max_f32_e32 v234, v234, v234
	v_max_f32_e32 v235, v235, v235
	v_max_f32_e32 v236, v236, v236
	v_max_f32_e32 v237, v237, v237
	v_max_f32_e32 v238, v238, v238
	v_max_f32_e32 v239, v239, v239
	v_max_f32_e32 v240, v240, v240
	v_max_f32_e32 v241, v241, v241
	v_med3_f32 v226, v226, s62, v95
	v_med3_f32 v227, v227, s62, v95
	v_med3_f32 v228, v228, s62, v95
	v_med3_f32 v229, v229, s62, v95
	v_med3_f32 v230, v230, s62, v95
	v_med3_f32 v231, v231, s62, v95
	v_med3_f32 v232, v232, s62, v95
	v_med3_f32 v233, v233, s62, v95
	v_med3_f32 v234, v234, s62, v95
	v_med3_f32 v235, v235, s62, v95
	v_med3_f32 v236, v236, s62, v95
	v_med3_f32 v237, v237, s62, v95
	v_med3_f32 v238, v238, s62, v95
	v_med3_f32 v239, v239, s62, v95
	v_med3_f32 v240, v240, s62, v95
	v_med3_f32 v241, v241, s62, v95
	v_mov_b32_e32 v242, 0
	v_mov_b32_e32 v243, 0
	v_mov_b32_e32 v244, 0
	v_mov_b32_e32 v245, 0
	v_cvt_pk_fp8_f32 v242, v226, v227
	v_cvt_pk_fp8_f32 v243, v230, v231
	v_cvt_pk_fp8_f32 v244, v234, v235
	v_cvt_pk_fp8_f32 v245, v238, v239
	v_cvt_pk_fp8_f32 v242, v228, v229 op_sel:[0,0,1]
	v_cvt_pk_fp8_f32 v243, v232, v233 op_sel:[0,0,1]
	v_cvt_pk_fp8_f32 v244, v236, v237 op_sel:[0,0,1]
	v_cvt_pk_fp8_f32 v245, v240, v241 op_sel:[0,0,1]
	s_nop 0
	global_store_dwordx4 v77, v[242:245], s[6:7]
	ds_read_b32 v226, v214
	ds_read_b32 v227, v214 offset:512
	ds_read_b32 v228, v214 offset:1024
	ds_read_b32 v229, v214 offset:1536
	ds_read_b32 v230, v214 offset:2048
	ds_read_b32 v231, v214 offset:2560
	ds_read_b32 v232, v214 offset:3072
	ds_read_b32 v233, v214 offset:3584
	ds_read_b32 v234, v214 offset:4096
	ds_read_b32 v235, v214 offset:4608
	ds_read_b32 v236, v214 offset:5120
	ds_read_b32 v237, v214 offset:5632
	ds_read_b32 v238, v214 offset:6144
	ds_read_b32 v239, v214 offset:6656
	ds_read_b32 v240, v214 offset:7168
	ds_read_b32 v241, v214 offset:7680
	s_waitcnt lgkmcnt(0)
	v_max_f32_e32 v226, v226, v226
	v_max_f32_e32 v227, v227, v227
	v_max_f32_e32 v228, v228, v228
	v_max_f32_e32 v229, v229, v229
	v_max_f32_e32 v230, v230, v230
	v_max_f32_e32 v231, v231, v231
	v_max_f32_e32 v232, v232, v232
	v_max_f32_e32 v233, v233, v233
	v_max_f32_e32 v234, v234, v234
	v_max_f32_e32 v235, v235, v235
	v_max_f32_e32 v236, v236, v236
	v_max_f32_e32 v237, v237, v237
	v_max_f32_e32 v238, v238, v238
	v_max_f32_e32 v239, v239, v239
	v_max_f32_e32 v240, v240, v240
	v_max_f32_e32 v241, v241, v241
	v_med3_f32 v226, v226, s62, v95
	v_med3_f32 v227, v227, s62, v95
	v_med3_f32 v228, v228, s62, v95
	v_med3_f32 v229, v229, s62, v95
	v_med3_f32 v230, v230, s62, v95
	v_med3_f32 v231, v231, s62, v95
	v_med3_f32 v232, v232, s62, v95
	v_med3_f32 v233, v233, s62, v95
	v_med3_f32 v234, v234, s62, v95
	v_med3_f32 v235, v235, s62, v95
	v_med3_f32 v236, v236, s62, v95
	v_med3_f32 v237, v237, s62, v95
	v_med3_f32 v238, v238, s62, v95
	v_med3_f32 v239, v239, s62, v95
	v_med3_f32 v240, v240, s62, v95
	v_med3_f32 v241, v241, s62, v95
	v_mov_b32_e32 v242, 0
	v_mov_b32_e32 v243, 0
	v_mov_b32_e32 v244, 0
	v_mov_b32_e32 v245, 0
	v_cvt_pk_fp8_f32 v242, v226, v227
	v_cvt_pk_fp8_f32 v243, v230, v231
	v_cvt_pk_fp8_f32 v244, v234, v235
	v_cvt_pk_fp8_f32 v245, v238, v239
	v_cvt_pk_fp8_f32 v242, v228, v229 op_sel:[0,0,1]
	v_cvt_pk_fp8_f32 v243, v232, v233 op_sel:[0,0,1]
	v_cvt_pk_fp8_f32 v244, v236, v237 op_sel:[0,0,1]
	v_cvt_pk_fp8_f32 v245, v240, v241 op_sel:[0,0,1]
	s_nop 0
	global_store_dwordx4 v78, v[242:245], s[6:7]
	s_waitcnt vmcnt(12)
	v_mul_f32_e32 v144, v34, v144
	v_mul_f32_e32 v145, v34, v145
	v_mul_f32_e32 v146, v34, v146
	v_mul_f32_e32 v147, v34, v147
	ds_write_b128 v209, v[144:147]
	v_mul_f32_e32 v148, v35, v148
	v_mul_f32_e32 v149, v35, v149
	v_mul_f32_e32 v150, v35, v150
	v_mul_f32_e32 v151, v35, v151
	ds_write_b128 v209, v[148:151] offset:1024
	v_mul_f32_e32 v152, v36, v152
	v_mul_f32_e32 v153, v36, v153
	v_mul_f32_e32 v154, v36, v154
	v_mul_f32_e32 v155, v36, v155
	ds_write_b128 v209, v[152:155] offset:2048
	v_mul_f32_e32 v156, v37, v156
	v_mul_f32_e32 v157, v37, v157
	v_mul_f32_e32 v158, v37, v158
	v_mul_f32_e32 v159, v37, v159
	ds_write_b128 v209, v[156:159] offset:3072
	v_mul_f32_e32 v160, v38, v160
	v_mul_f32_e32 v161, v38, v161
	v_mul_f32_e32 v162, v38, v162
	v_mul_f32_e32 v163, v38, v163
	ds_write_b128 v209, v[160:163] offset:4096
	v_mul_f32_e32 v164, v39, v164
	v_mul_f32_e32 v165, v39, v165
	v_mul_f32_e32 v166, v39, v166
	v_mul_f32_e32 v167, v39, v167
	ds_write_b128 v209, v[164:167] offset:5120
	v_mul_f32_e32 v168, v40, v168
	v_mul_f32_e32 v169, v40, v169
	v_mul_f32_e32 v170, v40, v170
	v_mul_f32_e32 v171, v40, v171
	ds_write_b128 v209, v[168:171] offset:6144
	v_mul_f32_e32 v172, v41, v172
	v_mul_f32_e32 v173, v41, v173
	v_mul_f32_e32 v174, v41, v174
	v_mul_f32_e32 v175, v41, v175
	ds_write_b128 v209, v[172:175] offset:7168
	s_waitcnt lgkmcnt(0)
	s_barrier
; #define GAS __attribute__((address_space(1)))
; #define LAS __attribute__((address_space(3)))
; #define LDS_WAIT() asm volatile("s_waitcnt lgkmcnt(0)" ::: "memory")
;     const int pr = item >> 1, kb = 2 * (pr / nblk) + (item & 1), nb = pr % nblk, k0 = 64 * kb, n0 = 32 * nb;
;     const int nr = n0 + (lane & 31); const int sc = MAP == 1 ? src_col_in(nr) : nr;
;     float v[32];
; #pragma unroll
;     for (int i = 0; i < 32; ++i) v[i] = sc >= 0 ? W[(size_t)(k0 + 2 * i + (lane >> 5)) * Nsrc + sc] : 0.f;
; #pragma unroll
;     for (int i = 0; i < 32; ++i) { const int k = k0 + 2 * i + (lane >> 5); float x = v[i] * wscale; if (KS) x *= (k < ksplit ? ksA[k] : ksB[k - ksplit]); scr[(2 * i + (lane >> 5)) * 33 + (lane & 31)] = x; }
;     LDS_WAIT(); asm volatile("" ::: "memory");
;     const int c = lane & 7;
; #pragma unroll
;     for (int j = 0; j < 4; ++j) { const int n = (lane >> 3) + 8 * j; const LAS float* s = scr + (8 * c) * 33 + n;
;         const unsigned long long o = (unsigned long long)pg8::pk4_fp8(s[0 * 33], s[1 * 33], s[2 * 33], s[3 * 33]) | ((unsigned long long)pg8::pk4_fp8(s[4 * 33], s[5 * 33], s[6 * 33], s[7 * 33]) << 32);
;         *(GAS unsigned long long*)(WT + (size_t)(n0 + n) * K + k0 + 8 * c) = o; }
;     LDS_WAIT(); asm volatile("" ::: "memory");
; }
; __global__ void __launch_bounds__(NWAVES * 64, 2) hybrid_fwd(Args args) {
;     ...
;             if (r < I_UP) { p0_transpose_item_f8<true>(args.in[15] + (size_t)l * DM * FF, DM, FF, FF / 32, (unsigned char*)(ws + WS_WUP + l * SZ_WUP), WUP8_SCALE, args.in[14] + l * DM, args.in[14] + l * DM, DM, scr, r, lane); continue; } r -= I_UP;
	s_add_u32 s8, s34, 0x2000
	s_addc_u32 s9, s35, 0
	global_load_dwordx4 v[144:147], v74, s[8:9]
	s_add_u32 s8, s8, 0x20000
	s_addc_u32 s9, s9, 0
	global_load_dwordx4 v[148:151], v74, s[8:9]
	s_add_u32 s8, s8, 0x20000
	s_addc_u32 s9, s9, 0
	global_load_dwordx4 v[152:155], v74, s[8:9]
	s_add_u32 s8, s8, 0x20000
	s_addc_u32 s9, s9, 0
	global_load_dwordx4 v[156:159], v74, s[8:9]
	s_add_u32 s8, s8, 0x20000
	s_addc_u32 s9, s9, 0
	global_load_dwordx4 v[160:163], v74, s[8:9]
	s_add_u32 s8, s8, 0x20000
	s_addc_u32 s9, s9, 0
	global_load_dwordx4 v[164:167], v74, s[8:9]
	s_add_u32 s8, s8, 0x20000
	s_addc_u32 s9, s9, 0
	global_load_dwordx4 v[168:171], v74, s[8:9]
	s_add_u32 s8, s8, 0x20000
	s_addc_u32 s9, s9, 0
	global_load_dwordx4 v[172:175], v74, s[8:9]
	s_mov_b64 s[6:7], s[36:37]
	ds_read_b32 v226, v211
	ds_read_b32 v227, v211 offset:512
	ds_read_b32 v228, v211 offset:1024
	ds_read_b32 v229, v211 offset:1536
	ds_read_b32 v230, v211 offset:2048
	ds_read_b32 v231, v211 offset:2560
	ds_read_b32 v232, v211 offset:3072
	ds_read_b32 v233, v211 offset:3584
	ds_read_b32 v234, v211 offset:4096
	ds_read_b32 v235, v211 offset:4608
	ds_read_b32 v236, v211 offset:5120
	ds_read_b32 v237, v211 offset:5632
	ds_read_b32 v238, v211 offset:6144
	ds_read_b32 v239, v211 offset:6656
	ds_read_b32 v240, v211 offset:7168
	ds_read_b32 v241, v211 offset:7680
	s_waitcnt lgkmcnt(0)
	v_max_f32_e32 v226, v226, v226
	v_max_f32_e32 v227, v227, v227
	v_max_f32_e32 v228, v228, v228
	v_max_f32_e32 v229, v229, v229
	v_max_f32_e32 v230, v230, v230
	v_max_f32_e32 v231, v231, v231
	v_max_f32_e32 v232, v232, v232
	v_max_f32_e32 v233, v233, v233
	v_max_f32_e32 v234, v234, v234
	v_max_f32_e32 v235, v235, v235
	v_max_f32_e32 v236, v236, v236
	v_max_f32_e32 v237, v237, v237
	v_max_f32_e32 v238, v238, v238
	v_max_f32_e32 v239, v239, v239
	v_max_f32_e32 v240, v240, v240
	v_max_f32_e32 v241, v241, v241
	v_med3_f32 v226, v226, s62, v95
	v_med3_f32 v227, v227, s62, v95
	v_med3_f32 v228, v228, s62, v95
	v_med3_f32 v229, v229, s62, v95
	v_med3_f32 v230, v230, s62, v95
	v_med3_f32 v231, v231, s62, v95
	v_med3_f32 v232, v232, s62, v95
	v_med3_f32 v233, v233, s62, v95
	v_med3_f32 v234, v234, s62, v95
	v_med3_f32 v235, v235, s62, v95
	v_med3_f32 v236, v236, s62, v95
	v_med3_f32 v237, v237, s62, v95
	v_med3_f32 v238, v238, s62, v95
	v_med3_f32 v239, v239, s62, v95
	v_med3_f32 v240, v240, s62, v95
	v_med3_f32 v241, v241, s62, v95
	v_mov_b32_e32 v242, 0
	v_mov_b32_e32 v243, 0
	v_mov_b32_e32 v244, 0
	v_mov_b32_e32 v245, 0
	v_cvt_pk_fp8_f32 v242, v226, v227
	v_cvt_pk_fp8_f32 v243, v230, v231
	v_cvt_pk_fp8_f32 v244, v234, v235
	v_cvt_pk_fp8_f32 v245, v238, v239
	v_cvt_pk_fp8_f32 v242, v228, v229 op_sel:[0,0,1]
	v_cvt_pk_fp8_f32 v243, v232, v233 op_sel:[0,0,1]
	v_cvt_pk_fp8_f32 v244, v236, v237 op_sel:[0,0,1]
	v_cvt_pk_fp8_f32 v245, v240, v241 op_sel:[0,0,1]
	s_nop 0
	global_store_dwordx4 v77, v[242:245], s[6:7]
	ds_read_b32 v226, v213
	ds_read_b32 v227, v213 offset:512
	ds_read_b32 v228, v213 offset:1024
	ds_read_b32 v229, v213 offset:1536
	ds_read_b32 v230, v213 offset:2048
	ds_read_b32 v231, v213 offset:2560
	ds_read_b32 v232, v213 offset:3072
	ds_read_b32 v233, v213 offset:3584
	ds_read_b32 v234, v213 offset:4096
	ds_read_b32 v235, v213 offset:4608
	ds_read_b32 v236, v213 offset:5120
	ds_read_b32 v237, v213 offset:5632
	ds_read_b32 v238, v213 offset:6144
	ds_read_b32 v239, v213 offset:6656
	ds_read_b32 v240, v213 offset:7168
	ds_read_b32 v241, v213 offset:7680
	s_waitcnt lgkmcnt(0)
	v_max_f32_e32 v226, v226, v226
	v_max_f32_e32 v227, v227, v227
	v_max_f32_e32 v228, v228, v228
	v_max_f32_e32 v229, v229, v229
	v_max_f32_e32 v230, v230, v230
	v_max_f32_e32 v231, v231, v231
	v_max_f32_e32 v232, v232, v232
	v_max_f32_e32 v233, v233, v233
	v_max_f32_e32 v234, v234, v234
	v_max_f32_e32 v235, v235, v235
	v_max_f32_e32 v236, v236, v236
	v_max_f32_e32 v237, v237, v237
	v_max_f32_e32 v238, v238, v238
	v_max_f32_e32 v239, v239, v239
	v_max_f32_e32 v240, v240, v240
	v_max_f32_e32 v241, v241, v241
	v_med3_f32 v226, v226, s62, v95
	v_med3_f32 v227, v227, s62, v95
	v_med3_f32 v228, v228, s62, v95
	v_med3_f32 v229, v229, s62, v95
	v_med3_f32 v230, v230, s62, v95
	v_med3_f32 v231, v231, s62, v95
	v_med3_f32 v232, v232, s62, v95
	v_med3_f32 v233, v233, s62, v95
	v_med3_f32 v234, v234, s62, v95
	v_med3_f32 v235, v235, s62, v95
	v_med3_f32 v236, v236, s62, v95
	v_med3_f32 v237, v237, s62, v95
	v_med3_f32 v238, v238, s62, v95
	v_med3_f32 v239, v239, s62, v95
	v_med3_f32 v240, v240, s62, v95
	v_med3_f32 v241, v241, s62, v95
	v_mov_b32_e32 v242, 0
	v_mov_b32_e32 v243, 0
	v_mov_b32_e32 v244, 0
	v_mov_b32_e32 v245, 0
	v_cvt_pk_fp8_f32 v242, v226, v227
	v_cvt_pk_fp8_f32 v243, v230, v231
	v_cvt_pk_fp8_f32 v244, v234, v235
	v_cvt_pk_fp8_f32 v245, v238, v239
	v_cvt_pk_fp8_f32 v242, v228, v229 op_sel:[0,0,1]
	v_cvt_pk_fp8_f32 v243, v232, v233 op_sel:[0,0,1]
	v_cvt_pk_fp8_f32 v244, v236, v237 op_sel:[0,0,1]
	v_cvt_pk_fp8_f32 v245, v240, v241 op_sel:[0,0,1]
	s_nop 0
	global_store_dwordx4 v78, v[242:245], s[6:7]
	s_waitcnt vmcnt(12)
	v_mul_f32_e32 v176, v34, v176
	v_mul_f32_e32 v177, v34, v177
	v_mul_f32_e32 v178, v34, v178
	v_mul_f32_e32 v179, v34, v179
	ds_write_b128 v210, v[176:179]
	v_mul_f32_e32 v180, v35, v180
	v_mul_f32_e32 v181, v35, v181
	v_mul_f32_e32 v182, v35, v182
	v_mul_f32_e32 v183, v35, v183
	ds_write_b128 v210, v[180:183] offset:1024
	v_mul_f32_e32 v184, v36, v184
	v_mul_f32_e32 v185, v36, v185
	v_mul_f32_e32 v186, v36, v186
	v_mul_f32_e32 v187, v36, v187
	ds_write_b128 v210, v[184:187] offset:2048
	v_mul_f32_e32 v188, v37, v188
	v_mul_f32_e32 v189, v37, v189
	v_mul_f32_e32 v190, v37, v190
	v_mul_f32_e32 v191, v37, v191
	ds_write_b128 v210, v[188:191] offset:3072
	v_mul_f32_e32 v192, v38, v192
	v_mul_f32_e32 v193, v38, v193
	v_mul_f32_e32 v194, v38, v194
	v_mul_f32_e32 v195, v38, v195
	ds_write_b128 v210, v[192:195] offset:4096
	v_mul_f32_e32 v196, v39, v196
	v_mul_f32_e32 v197, v39, v197
	v_mul_f32_e32 v198, v39, v198
	v_mul_f32_e32 v199, v39, v199
	ds_write_b128 v210, v[196:199] offset:5120
	v_mul_f32_e32 v200, v40, v200
	v_mul_f32_e32 v201, v40, v201
	v_mul_f32_e32 v202, v40, v202
	v_mul_f32_e32 v203, v40, v203
	ds_write_b128 v210, v[200:203] offset:6144
	v_mul_f32_e32 v204, v41, v204
	v_mul_f32_e32 v205, v41, v205
	v_mul_f32_e32 v206, v41, v206
	v_mul_f32_e32 v207, v41, v207
	ds_write_b128 v210, v[204:207] offset:7168
	s_waitcnt lgkmcnt(0)
	s_barrier
; #define GAS __attribute__((address_space(1)))
; #define LAS __attribute__((address_space(3)))
; #define LDS_WAIT() asm volatile("s_waitcnt lgkmcnt(0)" ::: "memory")
;     const int pr = item >> 1, kb = 2 * (pr / nblk) + (item & 1), nb = pr % nblk, k0 = 64 * kb, n0 = 32 * nb;
;     const int nr = n0 + (lane & 31); const int sc = MAP == 1 ? src_col_in(nr) : nr;
;     float v[32];
; #pragma unroll
;     for (int i = 0; i < 32; ++i) v[i] = sc >= 0 ? W[(size_t)(k0 + 2 * i + (lane >> 5)) * Nsrc + sc] : 0.f;
; #pragma unroll
;     for (int i = 0; i < 32; ++i) { const int k = k0 + 2 * i + (lane >> 5); float x = v[i] * wscale; if (KS) x *= (k < ksplit ? ksA[k] : ksB[k - ksplit]); scr[(2 * i + (lane >> 5)) * 33 + (lane & 31)] = x; }
;     LDS_WAIT(); asm volatile("" ::: "memory");
;     const int c = lane & 7;
; #pragma unroll
;     for (int j = 0; j < 4; ++j) { const int n = (lane >> 3) + 8 * j; const LAS float* s = scr + (8 * c) * 33 + n;
;         const unsigned long long o = (unsigned long long)pg8::pk4_fp8(s[0 * 33], s[1 * 33], s[2 * 33], s[3 * 33]) | ((unsigned long long)pg8::pk4_fp8(s[4 * 33], s[5 * 33], s[6 * 33], s[7 * 33]) << 32);
;         *(GAS unsigned long long*)(WT + (size_t)(n0 + n) * K + k0 + 8 * c) = o; }
;     LDS_WAIT(); asm volatile("" ::: "memory");
; }
; __global__ void __launch_bounds__(NWAVES * 64, 2) hybrid_fwd(Args args) {
;     ...
;             if (r < I_UP) { p0_transpose_item_f8<true>(args.in[15] + (size_t)l * DM * FF, DM, FF, FF / 32, (unsigned char*)(ws + WS_WUP + l * SZ_WUP), WUP8_SCALE, args.in[14] + l * DM, args.in[14] + l * DM, DM, scr, r, lane); continue; } r -= I_UP;
	s_add_u32 s8, s34, 0x3000
	s_addc_u32 s9, s35, 0
	global_load_dwordx4 v[176:179], v74, s[8:9]
	s_add_u32 s8, s8, 0x20000
	s_addc_u32 s9, s9, 0
	global_load_dwordx4 v[180:183], v74, s[8:9]
	s_add_u32 s8, s8, 0x20000
	s_addc_u32 s9, s9, 0
	global_load_dwordx4 v[184:187], v74, s[8:9]
	s_add_u32 s8, s8, 0x20000
	s_addc_u32 s9, s9, 0
	global_load_dwordx4 v[188:191], v74, s[8:9]
	s_add_u32 s8, s8, 0x20000
	s_addc_u32 s9, s9, 0
	global_load_dwordx4 v[192:195], v74, s[8:9]
	s_add_u32 s8, s8, 0x20000
	s_addc_u32 s9, s9, 0
	global_load_dwordx4 v[196:199], v74, s[8:9]
	s_add_u32 s8, s8, 0x20000
	s_addc_u32 s9, s9, 0
	global_load_dwordx4 v[200:203], v74, s[8:9]
	s_add_u32 s8, s8, 0x20000
	s_addc_u32 s9, s9, 0
	global_load_dwordx4 v[204:207], v74, s[8:9]
	s_add_u32 s6, s36, 0x400000
	s_addc_u32 s7, s37, 0
	ds_read_b32 v226, v212
	ds_read_b32 v227, v212 offset:512
	ds_read_b32 v228, v212 offset:1024
	ds_read_b32 v229, v212 offset:1536
	ds_read_b32 v230, v212 offset:2048
	ds_read_b32 v231, v212 offset:2560
	ds_read_b32 v232, v212 offset:3072
	ds_read_b32 v233, v212 offset:3584
	ds_read_b32 v234, v212 offset:4096
	ds_read_b32 v235, v212 offset:4608
	ds_read_b32 v236, v212 offset:5120
	ds_read_b32 v237, v212 offset:5632
	ds_read_b32 v238, v212 offset:6144
	ds_read_b32 v239, v212 offset:6656
	ds_read_b32 v240, v212 offset:7168
	ds_read_b32 v241, v212 offset:7680
	s_waitcnt lgkmcnt(0)
	v_max_f32_e32 v226, v226, v226
	v_max_f32_e32 v227, v227, v227
	v_max_f32_e32 v228, v228, v228
	v_max_f32_e32 v229, v229, v229
	v_max_f32_e32 v230, v230, v230
	v_max_f32_e32 v231, v231, v231
	v_max_f32_e32 v232, v232, v232
	v_max_f32_e32 v233, v233, v233
	v_max_f32_e32 v234, v234, v234
	v_max_f32_e32 v235, v235, v235
	v_max_f32_e32 v236, v236, v236
	v_max_f32_e32 v237, v237, v237
	v_max_f32_e32 v238, v238, v238
	v_max_f32_e32 v239, v239, v239
	v_max_f32_e32 v240, v240, v240
	v_max_f32_e32 v241, v241, v241
	v_med3_f32 v226, v226, s62, v95
	v_med3_f32 v227, v227, s62, v95
	v_med3_f32 v228, v228, s62, v95
	v_med3_f32 v229, v229, s62, v95
	v_med3_f32 v230, v230, s62, v95
	v_med3_f32 v231, v231, s62, v95
	v_med3_f32 v232, v232, s62, v95
	v_med3_f32 v233, v233, s62, v95
	v_med3_f32 v234, v234, s62, v95
	v_med3_f32 v235, v235, s62, v95
	v_med3_f32 v236, v236, s62, v95
	v_med3_f32 v237, v237, s62, v95
	v_med3_f32 v238, v238, s62, v95
	v_med3_f32 v239, v239, s62, v95
	v_med3_f32 v240, v240, s62, v95
	v_med3_f32 v241, v241, s62, v95
	v_mov_b32_e32 v242, 0
	v_mov_b32_e32 v243, 0
	v_mov_b32_e32 v244, 0
	v_mov_b32_e32 v245, 0
	v_cvt_pk_fp8_f32 v242, v226, v227
	v_cvt_pk_fp8_f32 v243, v230, v231
	v_cvt_pk_fp8_f32 v244, v234, v235
	v_cvt_pk_fp8_f32 v245, v238, v239
	v_cvt_pk_fp8_f32 v242, v228, v229 op_sel:[0,0,1]
	v_cvt_pk_fp8_f32 v243, v232, v233 op_sel:[0,0,1]
	v_cvt_pk_fp8_f32 v244, v236, v237 op_sel:[0,0,1]
	v_cvt_pk_fp8_f32 v245, v240, v241 op_sel:[0,0,1]
	s_nop 0
	global_store_dwordx4 v77, v[242:245], s[6:7]
	ds_read_b32 v226, v214
	ds_read_b32 v227, v214 offset:512
	ds_read_b32 v228, v214 offset:1024
	ds_read_b32 v229, v214 offset:1536
	ds_read_b32 v230, v214 offset:2048
	ds_read_b32 v231, v214 offset:2560
	ds_read_b32 v232, v214 offset:3072
	ds_read_b32 v233, v214 offset:3584
	ds_read_b32 v234, v214 offset:4096
	ds_read_b32 v235, v214 offset:4608
	ds_read_b32 v236, v214 offset:5120
	ds_read_b32 v237, v214 offset:5632
	ds_read_b32 v238, v214 offset:6144
	ds_read_b32 v239, v214 offset:6656
	ds_read_b32 v240, v214 offset:7168
	ds_read_b32 v241, v214 offset:7680
	s_waitcnt lgkmcnt(0)
	v_max_f32_e32 v226, v226, v226
	v_max_f32_e32 v227, v227, v227
	v_max_f32_e32 v228, v228, v228
	v_max_f32_e32 v229, v229, v229
	v_max_f32_e32 v230, v230, v230
	v_max_f32_e32 v231, v231, v231
	v_max_f32_e32 v232, v232, v232
	v_max_f32_e32 v233, v233, v233
	v_max_f32_e32 v234, v234, v234
	v_max_f32_e32 v235, v235, v235
	v_max_f32_e32 v236, v236, v236
	v_max_f32_e32 v237, v237, v237
	v_max_f32_e32 v238, v238, v238
	v_max_f32_e32 v239, v239, v239
	v_max_f32_e32 v240, v240, v240
	v_max_f32_e32 v241, v241, v241
	v_med3_f32 v226, v226, s62, v95
	v_med3_f32 v227, v227, s62, v95
	v_med3_f32 v228, v228, s62, v95
	v_med3_f32 v229, v229, s62, v95
	v_med3_f32 v230, v230, s62, v95
	v_med3_f32 v231, v231, s62, v95
	v_med3_f32 v232, v232, s62, v95
	v_med3_f32 v233, v233, s62, v95
	v_med3_f32 v234, v234, s62, v95
	v_med3_f32 v235, v235, s62, v95
	v_med3_f32 v236, v236, s62, v95
	v_med3_f32 v237, v237, s62, v95
	v_med3_f32 v238, v238, s62, v95
	v_med3_f32 v239, v239, s62, v95
	v_med3_f32 v240, v240, s62, v95
	v_med3_f32 v241, v241, s62, v95
	v_mov_b32_e32 v242, 0
	v_mov_b32_e32 v243, 0
	v_mov_b32_e32 v244, 0
	v_mov_b32_e32 v245, 0
	v_cvt_pk_fp8_f32 v242, v226, v227
	v_cvt_pk_fp8_f32 v243, v230, v231
	v_cvt_pk_fp8_f32 v244, v234, v235
	v_cvt_pk_fp8_f32 v245, v238, v239
	v_cvt_pk_fp8_f32 v242, v228, v229 op_sel:[0,0,1]
	v_cvt_pk_fp8_f32 v243, v232, v233 op_sel:[0,0,1]
	v_cvt_pk_fp8_f32 v244, v236, v237 op_sel:[0,0,1]
	v_cvt_pk_fp8_f32 v245, v240, v241 op_sel:[0,0,1]
	s_nop 0
	global_store_dwordx4 v78, v[242:245], s[6:7]
	s_waitcnt vmcnt(12)
	v_mul_f32_e32 v144, v34, v144
	v_mul_f32_e32 v145, v34, v145
	v_mul_f32_e32 v146, v34, v146
	v_mul_f32_e32 v147, v34, v147
	ds_write_b128 v209, v[144:147]
	v_mul_f32_e32 v148, v35, v148
	v_mul_f32_e32 v149, v35, v149
	v_mul_f32_e32 v150, v35, v150
	v_mul_f32_e32 v151, v35, v151
	ds_write_b128 v209, v[148:151] offset:1024
	v_mul_f32_e32 v152, v36, v152
	v_mul_f32_e32 v153, v36, v153
	v_mul_f32_e32 v154, v36, v154
	v_mul_f32_e32 v155, v36, v155
	ds_write_b128 v209, v[152:155] offset:2048
	v_mul_f32_e32 v156, v37, v156
	v_mul_f32_e32 v157, v37, v157
	v_mul_f32_e32 v158, v37, v158
	v_mul_f32_e32 v159, v37, v159
	ds_write_b128 v209, v[156:159] offset:3072
	v_mul_f32_e32 v160, v38, v160
	v_mul_f32_e32 v161, v38, v161
	v_mul_f32_e32 v162, v38, v162
	v_mul_f32_e32 v163, v38, v163
	ds_write_b128 v209, v[160:163] offset:4096
	v_mul_f32_e32 v164, v39, v164
	v_mul_f32_e32 v165, v39, v165
	v_mul_f32_e32 v166, v39, v166
	v_mul_f32_e32 v167, v39, v167
	ds_write_b128 v209, v[164:167] offset:5120
	v_mul_f32_e32 v168, v40, v168
	v_mul_f32_e32 v169, v40, v169
	v_mul_f32_e32 v170, v40, v170
	v_mul_f32_e32 v171, v40, v171
	ds_write_b128 v209, v[168:171] offset:6144
	v_mul_f32_e32 v172, v41, v172
	v_mul_f32_e32 v173, v41, v173
	v_mul_f32_e32 v174, v41, v174
	v_mul_f32_e32 v175, v41, v175
	ds_write_b128 v209, v[172:175] offset:7168
	s_waitcnt lgkmcnt(0)
	s_barrier
; #define GAS __attribute__((address_space(1)))
; #define LAS __attribute__((address_space(3)))
; #define LDS_WAIT() asm volatile("s_waitcnt lgkmcnt(0)" ::: "memory")
;     const int pr = item >> 1, kb = 2 * (pr / nblk) + (item & 1), nb = pr % nblk, k0 = 64 * kb, n0 = 32 * nb;
;     const int nr = n0 + (lane & 31); const int sc = MAP == 1 ? src_col_in(nr) : nr;
;     float v[32];
; #pragma unroll
;     for (int i = 0; i < 32; ++i) v[i] = sc >= 0 ? W[(size_t)(k0 + 2 * i + (lane >> 5)) * Nsrc + sc] : 0.f;
; #pragma unroll
;     for (int i = 0; i < 32; ++i) { const int k = k0 + 2 * i + (lane >> 5); float x = v[i] * wscale; if (KS) x *= (k < ksplit ? ksA[k] : ksB[k - ksplit]); scr[(2 * i + (lane >> 5)) * 33 + (lane & 31)] = x; }
;     LDS_WAIT(); asm volatile("" ::: "memory");
;     const int c = lane & 7;
; #pragma unroll
;     for (int j = 0; j < 4; ++j) { const int n = (lane >> 3) + 8 * j; const LAS float* s = scr + (8 * c) * 33 + n;
;         const unsigned long long o = (unsigned long long)pg8::pk4_fp8(s[0 * 33], s[1 * 33], s[2 * 33], s[3 * 33]) | ((unsigned long long)pg8::pk4_fp8(s[4 * 33], s[5 * 33], s[6 * 33], s[7 * 33]) << 32);
;         *(GAS unsigned long long*)(WT + (size_t)(n0 + n) * K + k0 + 8 * c) = o; }
;     LDS_WAIT(); asm volatile("" ::: "memory");
; }
; __global__ void __launch_bounds__(NWAVES * 64, 2) hybrid_fwd(Args args) {
;     ...
;             if (r < I_UP) { p0_transpose_item_f8<true>(args.in[15] + (size_t)l * DM * FF, DM, FF, FF / 32, (unsigned char*)(ws + WS_WUP + l * SZ_WUP), WUP8_SCALE, args.in[14] + l * DM, args.in[14] + l * DM, DM, scr, r, lane); continue; } r -= I_UP;
	s_add_u32 s8, s34, 0x4000
	s_addc_u32 s9, s35, 0
	global_load_dwordx4 v[144:147], v74, s[8:9]
	s_add_u32 s8, s8, 0x20000
	s_addc_u32 s9, s9, 0
	global_load_dwordx4 v[148:151], v74, s[8:9]
	s_add_u32 s8, s8, 0x20000
	s_addc_u32 s9, s9, 0
	global_load_dwordx4 v[152:155], v74, s[8:9]
	s_add_u32 s8, s8, 0x20000
	s_addc_u32 s9, s9, 0
	global_load_dwordx4 v[156:159], v74, s[8:9]
	s_add_u32 s8, s8, 0x20000
	s_addc_u32 s9, s9, 0
	global_load_dwordx4 v[160:163], v74, s[8:9]
	s_add_u32 s8, s8, 0x20000
	s_addc_u32 s9, s9, 0
	global_load_dwordx4 v[164:167], v74, s[8:9]
	s_add_u32 s8, s8, 0x20000
	s_addc_u32 s9, s9, 0
	global_load_dwordx4 v[168:171], v74, s[8:9]
	s_add_u32 s8, s8, 0x20000
	s_addc_u32 s9, s9, 0
	global_load_dwordx4 v[172:175], v74, s[8:9]
	s_add_u32 s6, s36, 0x800000
	s_addc_u32 s7, s37, 0
	ds_read_b32 v226, v211
	ds_read_b32 v227, v211 offset:512
	ds_read_b32 v228, v211 offset:1024
	ds_read_b32 v229, v211 offset:1536
	ds_read_b32 v230, v211 offset:2048
	ds_read_b32 v231, v211 offset:2560
	ds_read_b32 v232, v211 offset:3072
	ds_read_b32 v233, v211 offset:3584
	ds_read_b32 v234, v211 offset:4096
	ds_read_b32 v235, v211 offset:4608
	ds_read_b32 v236, v211 offset:5120
	ds_read_b32 v237, v211 offset:5632
	ds_read_b32 v238, v211 offset:6144
	ds_read_b32 v239, v211 offset:6656
	ds_read_b32 v240, v211 offset:7168
	ds_read_b32 v241, v211 offset:7680
	s_waitcnt lgkmcnt(0)
	v_max_f32_e32 v226, v226, v226
	v_max_f32_e32 v227, v227, v227
	v_max_f32_e32 v228, v228, v228
	v_max_f32_e32 v229, v229, v229
	v_max_f32_e32 v230, v230, v230
	v_max_f32_e32 v231, v231, v231
	v_max_f32_e32 v232, v232, v232
	v_max_f32_e32 v233, v233, v233
	v_max_f32_e32 v234, v234, v234
	v_max_f32_e32 v235, v235, v235
	v_max_f32_e32 v236, v236, v236
	v_max_f32_e32 v237, v237, v237
	v_max_f32_e32 v238, v238, v238
	v_max_f32_e32 v239, v239, v239
	v_max_f32_e32 v240, v240, v240
	v_max_f32_e32 v241, v241, v241
	v_med3_f32 v226, v226, s62, v95
	v_med3_f32 v227, v227, s62, v95
	v_med3_f32 v228, v228, s62, v95
	v_med3_f32 v229, v229, s62, v95
	v_med3_f32 v230, v230, s62, v95
	v_med3_f32 v231, v231, s62, v95
	v_med3_f32 v232, v232, s62, v95
	v_med3_f32 v233, v233, s62, v95
	v_med3_f32 v234, v234, s62, v95
	v_med3_f32 v235, v235, s62, v95
	v_med3_f32 v236, v236, s62, v95
	v_med3_f32 v237, v237, s62, v95
	v_med3_f32 v238, v238, s62, v95
	v_med3_f32 v239, v239, s62, v95
	v_med3_f32 v240, v240, s62, v95
	v_med3_f32 v241, v241, s62, v95
	v_mov_b32_e32 v242, 0
	v_mov_b32_e32 v243, 0
	v_mov_b32_e32 v244, 0
	v_mov_b32_e32 v245, 0
	v_cvt_pk_fp8_f32 v242, v226, v227
	v_cvt_pk_fp8_f32 v243, v230, v231
	v_cvt_pk_fp8_f32 v244, v234, v235
	v_cvt_pk_fp8_f32 v245, v238, v239
	v_cvt_pk_fp8_f32 v242, v228, v229 op_sel:[0,0,1]
	v_cvt_pk_fp8_f32 v243, v232, v233 op_sel:[0,0,1]
	v_cvt_pk_fp8_f32 v244, v236, v237 op_sel:[0,0,1]
	v_cvt_pk_fp8_f32 v245, v240, v241 op_sel:[0,0,1]
	s_nop 0
	global_store_dwordx4 v77, v[242:245], s[6:7]
	ds_read_b32 v226, v213
	ds_read_b32 v227, v213 offset:512
	ds_read_b32 v228, v213 offset:1024
	ds_read_b32 v229, v213 offset:1536
	ds_read_b32 v230, v213 offset:2048
	ds_read_b32 v231, v213 offset:2560
	ds_read_b32 v232, v213 offset:3072
	ds_read_b32 v233, v213 offset:3584
	ds_read_b32 v234, v213 offset:4096
	ds_read_b32 v235, v213 offset:4608
	ds_read_b32 v236, v213 offset:5120
	ds_read_b32 v237, v213 offset:5632
	ds_read_b32 v238, v213 offset:6144
	ds_read_b32 v239, v213 offset:6656
	ds_read_b32 v240, v213 offset:7168
	ds_read_b32 v241, v213 offset:7680
	s_waitcnt lgkmcnt(0)
	v_max_f32_e32 v226, v226, v226
	v_max_f32_e32 v227, v227, v227
	v_max_f32_e32 v228, v228, v228
	v_max_f32_e32 v229, v229, v229
	v_max_f32_e32 v230, v230, v230
	v_max_f32_e32 v231, v231, v231
	v_max_f32_e32 v232, v232, v232
	v_max_f32_e32 v233, v233, v233
	v_max_f32_e32 v234, v234, v234
	v_max_f32_e32 v235, v235, v235
	v_max_f32_e32 v236, v236, v236
	v_max_f32_e32 v237, v237, v237
	v_max_f32_e32 v238, v238, v238
	v_max_f32_e32 v239, v239, v239
	v_max_f32_e32 v240, v240, v240
	v_max_f32_e32 v241, v241, v241
	v_med3_f32 v226, v226, s62, v95
	v_med3_f32 v227, v227, s62, v95
	v_med3_f32 v228, v228, s62, v95
	v_med3_f32 v229, v229, s62, v95
	v_med3_f32 v230, v230, s62, v95
	v_med3_f32 v231, v231, s62, v95
	v_med3_f32 v232, v232, s62, v95
	v_med3_f32 v233, v233, s62, v95
	v_med3_f32 v234, v234, s62, v95
	v_med3_f32 v235, v235, s62, v95
	v_med3_f32 v236, v236, s62, v95
	v_med3_f32 v237, v237, s62, v95
	v_med3_f32 v238, v238, s62, v95
	v_med3_f32 v239, v239, s62, v95
	v_med3_f32 v240, v240, s62, v95
	v_med3_f32 v241, v241, s62, v95
	v_mov_b32_e32 v242, 0
	v_mov_b32_e32 v243, 0
	v_mov_b32_e32 v244, 0
	v_mov_b32_e32 v245, 0
	v_cvt_pk_fp8_f32 v242, v226, v227
	v_cvt_pk_fp8_f32 v243, v230, v231
	v_cvt_pk_fp8_f32 v244, v234, v235
	v_cvt_pk_fp8_f32 v245, v238, v239
	v_cvt_pk_fp8_f32 v242, v228, v229 op_sel:[0,0,1]
	v_cvt_pk_fp8_f32 v243, v232, v233 op_sel:[0,0,1]
	v_cvt_pk_fp8_f32 v244, v236, v237 op_sel:[0,0,1]
	v_cvt_pk_fp8_f32 v245, v240, v241 op_sel:[0,0,1]
	s_nop 0
	global_store_dwordx4 v78, v[242:245], s[6:7]
	s_waitcnt vmcnt(12)
	v_mul_f32_e32 v176, v34, v176
	v_mul_f32_e32 v177, v34, v177
	v_mul_f32_e32 v178, v34, v178
	v_mul_f32_e32 v179, v34, v179
	ds_write_b128 v210, v[176:179]
	v_mul_f32_e32 v180, v35, v180
	v_mul_f32_e32 v181, v35, v181
	v_mul_f32_e32 v182, v35, v182
	v_mul_f32_e32 v183, v35, v183
	ds_write_b128 v210, v[180:183] offset:1024
	v_mul_f32_e32 v184, v36, v184
	v_mul_f32_e32 v185, v36, v185
	v_mul_f32_e32 v186, v36, v186
	v_mul_f32_e32 v187, v36, v187
	ds_write_b128 v210, v[184:187] offset:2048
	v_mul_f32_e32 v188, v37, v188
	v_mul_f32_e32 v189, v37, v189
	v_mul_f32_e32 v190, v37, v190
	v_mul_f32_e32 v191, v37, v191
	ds_write_b128 v210, v[188:191] offset:3072
	v_mul_f32_e32 v192, v38, v192
	v_mul_f32_e32 v193, v38, v193
	v_mul_f32_e32 v194, v38, v194
	v_mul_f32_e32 v195, v38, v195
	ds_write_b128 v210, v[192:195] offset:4096
	v_mul_f32_e32 v196, v39, v196
	v_mul_f32_e32 v197, v39, v197
	v_mul_f32_e32 v198, v39, v198
	v_mul_f32_e32 v199, v39, v199
	ds_write_b128 v210, v[196:199] offset:5120
	v_mul_f32_e32 v200, v40, v200
	v_mul_f32_e32 v201, v40, v201
	v_mul_f32_e32 v202, v40, v202
	v_mul_f32_e32 v203, v40, v203
	ds_write_b128 v210, v[200:203] offset:6144
	v_mul_f32_e32 v204, v41, v204
	v_mul_f32_e32 v205, v41, v205
	v_mul_f32_e32 v206, v41, v206
	v_mul_f32_e32 v207, v41, v207
	ds_write_b128 v210, v[204:207] offset:7168
	s_waitcnt lgkmcnt(0)
	s_barrier
; #define GAS __attribute__((address_space(1)))
; #define LAS __attribute__((address_space(3)))
; #define LDS_WAIT() asm volatile("s_waitcnt lgkmcnt(0)" ::: "memory")
;     const int pr = item >> 1, kb = 2 * (pr / nblk) + (item & 1), nb = pr % nblk, k0 = 64 * kb, n0 = 32 * nb;
;     const int nr = n0 + (lane & 31); const int sc = MAP == 1 ? src_col_in(nr) : nr;
;     float v[32];
; #pragma unroll
;     for (int i = 0; i < 32; ++i) v[i] = sc >= 0 ? W[(size_t)(k0 + 2 * i + (lane >> 5)) * Nsrc + sc] : 0.f;
; #pragma unroll
;     for (int i = 0; i < 32; ++i) { const int k = k0 + 2 * i + (lane >> 5); float x = v[i] * wscale; if (KS) x *= (k < ksplit ? ksA[k] : ksB[k - ksplit]); scr[(2 * i + (lane >> 5)) * 33 + (lane & 31)] = x; }
;     LDS_WAIT(); asm volatile("" ::: "memory");
;     const int c = lane & 7;
; #pragma unroll
;     for (int j = 0; j < 4; ++j) { const int n = (lane >> 3) + 8 * j; const LAS float* s = scr + (8 * c) * 33 + n;
;         const unsigned long long o = (unsigned long long)pg8::pk4_fp8(s[0 * 33], s[1 * 33], s[2 * 33], s[3 * 33]) | ((unsigned long long)pg8::pk4_fp8(s[4 * 33], s[5 * 33], s[6 * 33], s[7 * 33]) << 32);
;         *(GAS unsigned long long*)(WT + (size_t)(n0 + n) * K + k0 + 8 * c) = o; }
;     LDS_WAIT(); asm volatile("" ::: "memory");
; }
; __global__ void __launch_bounds__(NWAVES * 64, 2) hybrid_fwd(Args args) {
;     ...
;             if (r < I_UP) { p0_transpose_item_f8<true>(args.in[15] + (size_t)l * DM * FF, DM, FF, FF / 32, (unsigned char*)(ws + WS_WUP + l * SZ_WUP), WUP8_SCALE, args.in[14] + l * DM, args.in[14] + l * DM, DM, scr, r, lane); continue; } r -= I_UP;
	s_add_u32 s8, s34, 0x5000
	s_addc_u32 s9, s35, 0
	global_load_dwordx4 v[176:179], v74, s[8:9]
	s_add_u32 s8, s8, 0x20000
	s_addc_u32 s9, s9, 0
	global_load_dwordx4 v[180:183], v74, s[8:9]
	s_add_u32 s8, s8, 0x20000
	s_addc_u32 s9, s9, 0
	global_load_dwordx4 v[184:187], v74, s[8:9]
	s_add_u32 s8, s8, 0x20000
	s_addc_u32 s9, s9, 0
	global_load_dwordx4 v[188:191], v74, s[8:9]
	s_add_u32 s8, s8, 0x20000
	s_addc_u32 s9, s9, 0
	global_load_dwordx4 v[192:195], v74, s[8:9]
	s_add_u32 s8, s8, 0x20000
	s_addc_u32 s9, s9, 0
	global_load_dwordx4 v[196:199], v74, s[8:9]
	s_add_u32 s8, s8, 0x20000
	s_addc_u32 s9, s9, 0
	global_load_dwordx4 v[200:203], v74, s[8:9]
	s_add_u32 s8, s8, 0x20000
	s_addc_u32 s9, s9, 0
	global_load_dwordx4 v[204:207], v74, s[8:9]
	s_add_u32 s6, s36, 0xc00000
	s_addc_u32 s7, s37, 0
	ds_read_b32 v226, v212
	ds_read_b32 v227, v212 offset:512
	ds_read_b32 v228, v212 offset:1024
	ds_read_b32 v229, v212 offset:1536
	ds_read_b32 v230, v212 offset:2048
	ds_read_b32 v231, v212 offset:2560
	ds_read_b32 v232, v212 offset:3072
	ds_read_b32 v233, v212 offset:3584
	ds_read_b32 v234, v212 offset:4096
	ds_read_b32 v235, v212 offset:4608
	ds_read_b32 v236, v212 offset:5120
	ds_read_b32 v237, v212 offset:5632
	ds_read_b32 v238, v212 offset:6144
	ds_read_b32 v239, v212 offset:6656
	ds_read_b32 v240, v212 offset:7168
	ds_read_b32 v241, v212 offset:7680
	s_waitcnt lgkmcnt(0)
	v_max_f32_e32 v226, v226, v226
	v_max_f32_e32 v227, v227, v227
	v_max_f32_e32 v228, v228, v228
	v_max_f32_e32 v229, v229, v229
	v_max_f32_e32 v230, v230, v230
	v_max_f32_e32 v231, v231, v231
	v_max_f32_e32 v232, v232, v232
	v_max_f32_e32 v233, v233, v233
	v_max_f32_e32 v234, v234, v234
	v_max_f32_e32 v235, v235, v235
	v_max_f32_e32 v236, v236, v236
	v_max_f32_e32 v237, v237, v237
	v_max_f32_e32 v238, v238, v238
	v_max_f32_e32 v239, v239, v239
	v_max_f32_e32 v240, v240, v240
	v_max_f32_e32 v241, v241, v241
	v_med3_f32 v226, v226, s62, v95
	v_med3_f32 v227, v227, s62, v95
	v_med3_f32 v228, v228, s62, v95
	v_med3_f32 v229, v229, s62, v95
	v_med3_f32 v230, v230, s62, v95
	v_med3_f32 v231, v231, s62, v95
	v_med3_f32 v232, v232, s62, v95
	v_med3_f32 v233, v233, s62, v95
	v_med3_f32 v234, v234, s62, v95
	v_med3_f32 v235, v235, s62, v95
	v_med3_f32 v236, v236, s62, v95
	v_med3_f32 v237, v237, s62, v95
	v_med3_f32 v238, v238, s62, v95
	v_med3_f32 v239, v239, s62, v95
	v_med3_f32 v240, v240, s62, v95
	v_med3_f32 v241, v241, s62, v95
	v_mov_b32_e32 v242, 0
	v_mov_b32_e32 v243, 0
	v_mov_b32_e32 v244, 0
	v_mov_b32_e32 v245, 0
	v_cvt_pk_fp8_f32 v242, v226, v227
	v_cvt_pk_fp8_f32 v243, v230, v231
	v_cvt_pk_fp8_f32 v244, v234, v235
	v_cvt_pk_fp8_f32 v245, v238, v239
	v_cvt_pk_fp8_f32 v242, v228, v229 op_sel:[0,0,1]
	v_cvt_pk_fp8_f32 v243, v232, v233 op_sel:[0,0,1]
	v_cvt_pk_fp8_f32 v244, v236, v237 op_sel:[0,0,1]
	v_cvt_pk_fp8_f32 v245, v240, v241 op_sel:[0,0,1]
	s_nop 0
	global_store_dwordx4 v77, v[242:245], s[6:7]
	ds_read_b32 v226, v214
	ds_read_b32 v227, v214 offset:512
	ds_read_b32 v228, v214 offset:1024
	ds_read_b32 v229, v214 offset:1536
	ds_read_b32 v230, v214 offset:2048
	ds_read_b32 v231, v214 offset:2560
	ds_read_b32 v232, v214 offset:3072
	ds_read_b32 v233, v214 offset:3584
	ds_read_b32 v234, v214 offset:4096
	ds_read_b32 v235, v214 offset:4608
	ds_read_b32 v236, v214 offset:5120
	ds_read_b32 v237, v214 offset:5632
	ds_read_b32 v238, v214 offset:6144
	ds_read_b32 v239, v214 offset:6656
	ds_read_b32 v240, v214 offset:7168
	ds_read_b32 v241, v214 offset:7680
	s_waitcnt lgkmcnt(0)
	v_max_f32_e32 v226, v226, v226
	v_max_f32_e32 v227, v227, v227
	v_max_f32_e32 v228, v228, v228
	v_max_f32_e32 v229, v229, v229
	v_max_f32_e32 v230, v230, v230
	v_max_f32_e32 v231, v231, v231
	v_max_f32_e32 v232, v232, v232
	v_max_f32_e32 v233, v233, v233
	v_max_f32_e32 v234, v234, v234
	v_max_f32_e32 v235, v235, v235
	v_max_f32_e32 v236, v236, v236
	v_max_f32_e32 v237, v237, v237
	v_max_f32_e32 v238, v238, v238
	v_max_f32_e32 v239, v239, v239
	v_max_f32_e32 v240, v240, v240
	v_max_f32_e32 v241, v241, v241
	v_med3_f32 v226, v226, s62, v95
	v_med3_f32 v227, v227, s62, v95
	v_med3_f32 v228, v228, s62, v95
	v_med3_f32 v229, v229, s62, v95
	v_med3_f32 v230, v230, s62, v95
	v_med3_f32 v231, v231, s62, v95
	v_med3_f32 v232, v232, s62, v95
	v_med3_f32 v233, v233, s62, v95
	v_med3_f32 v234, v234, s62, v95
	v_med3_f32 v235, v235, s62, v95
	v_med3_f32 v236, v236, s62, v95
	v_med3_f32 v237, v237, s62, v95
	v_med3_f32 v238, v238, s62, v95
	v_med3_f32 v239, v239, s62, v95
	v_med3_f32 v240, v240, s62, v95
	v_med3_f32 v241, v241, s62, v95
	v_mov_b32_e32 v242, 0
	v_mov_b32_e32 v243, 0
	v_mov_b32_e32 v244, 0
	v_mov_b32_e32 v245, 0
	v_cvt_pk_fp8_f32 v242, v226, v227
	v_cvt_pk_fp8_f32 v243, v230, v231
	v_cvt_pk_fp8_f32 v244, v234, v235
	v_cvt_pk_fp8_f32 v245, v238, v239
	v_cvt_pk_fp8_f32 v242, v228, v229 op_sel:[0,0,1]
	v_cvt_pk_fp8_f32 v243, v232, v233 op_sel:[0,0,1]
	v_cvt_pk_fp8_f32 v244, v236, v237 op_sel:[0,0,1]
	v_cvt_pk_fp8_f32 v245, v240, v241 op_sel:[0,0,1]
	s_nop 0
	global_store_dwordx4 v78, v[242:245], s[6:7]
	s_waitcnt vmcnt(12)
	v_mul_f32_e32 v144, v34, v144
	v_mul_f32_e32 v145, v34, v145
	v_mul_f32_e32 v146, v34, v146
	v_mul_f32_e32 v147, v34, v147
	ds_write_b128 v209, v[144:147]
	v_mul_f32_e32 v148, v35, v148
	v_mul_f32_e32 v149, v35, v149
	v_mul_f32_e32 v150, v35, v150
	v_mul_f32_e32 v151, v35, v151
	ds_write_b128 v209, v[148:151] offset:1024
	v_mul_f32_e32 v152, v36, v152
	v_mul_f32_e32 v153, v36, v153
	v_mul_f32_e32 v154, v36, v154
	v_mul_f32_e32 v155, v36, v155
	ds_write_b128 v209, v[152:155] offset:2048
	v_mul_f32_e32 v156, v37, v156
	v_mul_f32_e32 v157, v37, v157
	v_mul_f32_e32 v158, v37, v158
	v_mul_f32_e32 v159, v37, v159
	ds_write_b128 v209, v[156:159] offset:3072
	v_mul_f32_e32 v160, v38, v160
	v_mul_f32_e32 v161, v38, v161
	v_mul_f32_e32 v162, v38, v162
	v_mul_f32_e32 v163, v38, v163
	ds_write_b128 v209, v[160:163] offset:4096
	v_mul_f32_e32 v164, v39, v164
	v_mul_f32_e32 v165, v39, v165
	v_mul_f32_e32 v166, v39, v166
	v_mul_f32_e32 v167, v39, v167
	ds_write_b128 v209, v[164:167] offset:5120
	v_mul_f32_e32 v168, v40, v168
	v_mul_f32_e32 v169, v40, v169
	v_mul_f32_e32 v170, v40, v170
	v_mul_f32_e32 v171, v40, v171
	ds_write_b128 v209, v[168:171] offset:6144
	v_mul_f32_e32 v172, v41, v172
	v_mul_f32_e32 v173, v41, v173
	v_mul_f32_e32 v174, v41, v174
	v_mul_f32_e32 v175, v41, v175
	ds_write_b128 v209, v[172:175] offset:7168
	s_waitcnt lgkmcnt(0)
	s_barrier
; #define GAS __attribute__((address_space(1)))
; #define LAS __attribute__((address_space(3)))
; #define LDS_WAIT() asm volatile("s_waitcnt lgkmcnt(0)" ::: "memory")
;     const int pr = item >> 1, kb = 2 * (pr / nblk) + (item & 1), nb = pr % nblk, k0 = 64 * kb, n0 = 32 * nb;
;     const int nr = n0 + (lane & 31); const int sc = MAP == 1 ? src_col_in(nr) : nr;
;     float v[32];
; #pragma unroll
;     for (int i = 0; i < 32; ++i) v[i] = sc >= 0 ? W[(size_t)(k0 + 2 * i + (lane >> 5)) * Nsrc + sc] : 0.f;
; #pragma unroll
;     for (int i = 0; i < 32; ++i) { const int k = k0 + 2 * i + (lane >> 5); float x = v[i] * wscale; if (KS) x *= (k < ksplit ? ksA[k] : ksB[k - ksplit]); scr[(2 * i + (lane >> 5)) * 33 + (lane & 31)] = x; }
;     LDS_WAIT(); asm volatile("" ::: "memory");
;     const int c = lane & 7;
; #pragma unroll
;     for (int j = 0; j < 4; ++j) { const int n = (lane >> 3) + 8 * j; const LAS float* s = scr + (8 * c) * 33 + n;
;         const unsigned long long o = (unsigned long long)pg8::pk4_fp8(s[0 * 33], s[1 * 33], s[2 * 33], s[3 * 33]) | ((unsigned long long)pg8::pk4_fp8(s[4 * 33], s[5 * 33], s[6 * 33], s[7 * 33]) << 32);
;         *(GAS unsigned long long*)(WT + (size_t)(n0 + n) * K + k0 + 8 * c) = o; }
;     LDS_WAIT(); asm volatile("" ::: "memory");
; }
; __global__ void __launch_bounds__(NWAVES * 64, 2) hybrid_fwd(Args args) {
;     ...
;             if (r < I_UP) { p0_transpose_item_f8<true>(args.in[15] + (size_t)l * DM * FF, DM, FF, FF / 32, (unsigned char*)(ws + WS_WUP + l * SZ_WUP), WUP8_SCALE, args.in[14] + l * DM, args.in[14] + l * DM, DM, scr, r, lane); continue; } r -= I_UP;
	s_add_u32 s8, s34, 0x6000
	s_addc_u32 s9, s35, 0
	global_load_dwordx4 v[144:147], v74, s[8:9]
	s_add_u32 s8, s8, 0x20000
	s_addc_u32 s9, s9, 0
	global_load_dwordx4 v[148:151], v74, s[8:9]
	s_add_u32 s8, s8, 0x20000
	s_addc_u32 s9, s9, 0
	global_load_dwordx4 v[152:155], v74, s[8:9]
	s_add_u32 s8, s8, 0x20000
	s_addc_u32 s9, s9, 0
	global_load_dwordx4 v[156:159], v74, s[8:9]
	s_add_u32 s8, s8, 0x20000
	s_addc_u32 s9, s9, 0
	global_load_dwordx4 v[160:163], v74, s[8:9]
	s_add_u32 s8, s8, 0x20000
	s_addc_u32 s9, s9, 0
	global_load_dwordx4 v[164:167], v74, s[8:9]
	s_add_u32 s8, s8, 0x20000
	s_addc_u32 s9, s9, 0
	global_load_dwordx4 v[168:171], v74, s[8:9]
	s_add_u32 s8, s8, 0x20000
	s_addc_u32 s9, s9, 0
	global_load_dwordx4 v[172:175], v74, s[8:9]
	s_add_u32 s6, s36, 0x1000000
	s_addc_u32 s7, s37, 0
	ds_read_b32 v226, v211
	ds_read_b32 v227, v211 offset:512
	ds_read_b32 v228, v211 offset:1024
	ds_read_b32 v229, v211 offset:1536
	ds_read_b32 v230, v211 offset:2048
	ds_read_b32 v231, v211 offset:2560
	ds_read_b32 v232, v211 offset:3072
	ds_read_b32 v233, v211 offset:3584
	ds_read_b32 v234, v211 offset:4096
	ds_read_b32 v235, v211 offset:4608
	ds_read_b32 v236, v211 offset:5120
	ds_read_b32 v237, v211 offset:5632
	ds_read_b32 v238, v211 offset:6144
	ds_read_b32 v239, v211 offset:6656
	ds_read_b32 v240, v211 offset:7168
	ds_read_b32 v241, v211 offset:7680
	s_waitcnt lgkmcnt(0)
	v_max_f32_e32 v226, v226, v226
	v_max_f32_e32 v227, v227, v227
	v_max_f32_e32 v228, v228, v228
	v_max_f32_e32 v229, v229, v229
	v_max_f32_e32 v230, v230, v230
	v_max_f32_e32 v231, v231, v231
	v_max_f32_e32 v232, v232, v232
	v_max_f32_e32 v233, v233, v233
	v_max_f32_e32 v234, v234, v234
	v_max_f32_e32 v235, v235, v235
	v_max_f32_e32 v236, v236, v236
	v_max_f32_e32 v237, v237, v237
	v_max_f32_e32 v238, v238, v238
	v_max_f32_e32 v239, v239, v239
	v_max_f32_e32 v240, v240, v240
	v_max_f32_e32 v241, v241, v241
	v_med3_f32 v226, v226, s62, v95
	v_med3_f32 v227, v227, s62, v95
	v_med3_f32 v228, v228, s62, v95
	v_med3_f32 v229, v229, s62, v95
	v_med3_f32 v230, v230, s62, v95
	v_med3_f32 v231, v231, s62, v95
	v_med3_f32 v232, v232, s62, v95
	v_med3_f32 v233, v233, s62, v95
	v_med3_f32 v234, v234, s62, v95
	v_med3_f32 v235, v235, s62, v95
	v_med3_f32 v236, v236, s62, v95
	v_med3_f32 v237, v237, s62, v95
	v_med3_f32 v238, v238, s62, v95
	v_med3_f32 v239, v239, s62, v95
	v_med3_f32 v240, v240, s62, v95
	v_med3_f32 v241, v241, s62, v95
	v_mov_b32_e32 v242, 0
	v_mov_b32_e32 v243, 0
	v_mov_b32_e32 v244, 0
	v_mov_b32_e32 v245, 0
	v_cvt_pk_fp8_f32 v242, v226, v227
	v_cvt_pk_fp8_f32 v243, v230, v231
	v_cvt_pk_fp8_f32 v244, v234, v235
	v_cvt_pk_fp8_f32 v245, v238, v239
	v_cvt_pk_fp8_f32 v242, v228, v229 op_sel:[0,0,1]
	v_cvt_pk_fp8_f32 v243, v232, v233 op_sel:[0,0,1]
	v_cvt_pk_fp8_f32 v244, v236, v237 op_sel:[0,0,1]
	v_cvt_pk_fp8_f32 v245, v240, v241 op_sel:[0,0,1]
	s_nop 0
	global_store_dwordx4 v77, v[242:245], s[6:7]
	ds_read_b32 v226, v213
	ds_read_b32 v227, v213 offset:512
	ds_read_b32 v228, v213 offset:1024
	ds_read_b32 v229, v213 offset:1536
	ds_read_b32 v230, v213 offset:2048
	ds_read_b32 v231, v213 offset:2560
	ds_read_b32 v232, v213 offset:3072
	ds_read_b32 v233, v213 offset:3584
	ds_read_b32 v234, v213 offset:4096
	ds_read_b32 v235, v213 offset:4608
	ds_read_b32 v236, v213 offset:5120
	ds_read_b32 v237, v213 offset:5632
	ds_read_b32 v238, v213 offset:6144
	ds_read_b32 v239, v213 offset:6656
	ds_read_b32 v240, v213 offset:7168
	ds_read_b32 v241, v213 offset:7680
	s_waitcnt lgkmcnt(0)
	v_max_f32_e32 v226, v226, v226
	v_max_f32_e32 v227, v227, v227
	v_max_f32_e32 v228, v228, v228
	v_max_f32_e32 v229, v229, v229
	v_max_f32_e32 v230, v230, v230
	v_max_f32_e32 v231, v231, v231
	v_max_f32_e32 v232, v232, v232
	v_max_f32_e32 v233, v233, v233
	v_max_f32_e32 v234, v234, v234
	v_max_f32_e32 v235, v235, v235
	v_max_f32_e32 v236, v236, v236
	v_max_f32_e32 v237, v237, v237
	v_max_f32_e32 v238, v238, v238
	v_max_f32_e32 v239, v239, v239
	v_max_f32_e32 v240, v240, v240
	v_max_f32_e32 v241, v241, v241
	v_med3_f32 v226, v226, s62, v95
	v_med3_f32 v227, v227, s62, v95
	v_med3_f32 v228, v228, s62, v95
	v_med3_f32 v229, v229, s62, v95
	v_med3_f32 v230, v230, s62, v95
	v_med3_f32 v231, v231, s62, v95
	v_med3_f32 v232, v232, s62, v95
	v_med3_f32 v233, v233, s62, v95
	v_med3_f32 v234, v234, s62, v95
	v_med3_f32 v235, v235, s62, v95
	v_med3_f32 v236, v236, s62, v95
	v_med3_f32 v237, v237, s62, v95
	v_med3_f32 v238, v238, s62, v95
	v_med3_f32 v239, v239, s62, v95
	v_med3_f32 v240, v240, s62, v95
	v_med3_f32 v241, v241, s62, v95
	v_mov_b32_e32 v242, 0
	v_mov_b32_e32 v243, 0
	v_mov_b32_e32 v244, 0
	v_mov_b32_e32 v245, 0
	v_cvt_pk_fp8_f32 v242, v226, v227
	v_cvt_pk_fp8_f32 v243, v230, v231
	v_cvt_pk_fp8_f32 v244, v234, v235
	v_cvt_pk_fp8_f32 v245, v238, v239
	v_cvt_pk_fp8_f32 v242, v228, v229 op_sel:[0,0,1]
	v_cvt_pk_fp8_f32 v243, v232, v233 op_sel:[0,0,1]
	v_cvt_pk_fp8_f32 v244, v236, v237 op_sel:[0,0,1]
	v_cvt_pk_fp8_f32 v245, v240, v241 op_sel:[0,0,1]
	s_nop 0
	global_store_dwordx4 v78, v[242:245], s[6:7]
	s_waitcnt vmcnt(12)
	v_mul_f32_e32 v176, v34, v176
	v_mul_f32_e32 v177, v34, v177
	v_mul_f32_e32 v178, v34, v178
	v_mul_f32_e32 v179, v34, v179
	ds_write_b128 v210, v[176:179]
	v_mul_f32_e32 v180, v35, v180
	v_mul_f32_e32 v181, v35, v181
	v_mul_f32_e32 v182, v35, v182
	v_mul_f32_e32 v183, v35, v183
	ds_write_b128 v210, v[180:183] offset:1024
	v_mul_f32_e32 v184, v36, v184
	v_mul_f32_e32 v185, v36, v185
	v_mul_f32_e32 v186, v36, v186
	v_mul_f32_e32 v187, v36, v187
	ds_write_b128 v210, v[184:187] offset:2048
	v_mul_f32_e32 v188, v37, v188
	v_mul_f32_e32 v189, v37, v189
	v_mul_f32_e32 v190, v37, v190
	v_mul_f32_e32 v191, v37, v191
	ds_write_b128 v210, v[188:191] offset:3072
	v_mul_f32_e32 v192, v38, v192
	v_mul_f32_e32 v193, v38, v193
	v_mul_f32_e32 v194, v38, v194
	v_mul_f32_e32 v195, v38, v195
	ds_write_b128 v210, v[192:195] offset:4096
	v_mul_f32_e32 v196, v39, v196
	v_mul_f32_e32 v197, v39, v197
	v_mul_f32_e32 v198, v39, v198
	v_mul_f32_e32 v199, v39, v199
	ds_write_b128 v210, v[196:199] offset:5120
	v_mul_f32_e32 v200, v40, v200
	v_mul_f32_e32 v201, v40, v201
	v_mul_f32_e32 v202, v40, v202
	v_mul_f32_e32 v203, v40, v203
	ds_write_b128 v210, v[200:203] offset:6144
	v_mul_f32_e32 v204, v41, v204
	v_mul_f32_e32 v205, v41, v205
	v_mul_f32_e32 v206, v41, v206
	v_mul_f32_e32 v207, v41, v207
	ds_write_b128 v210, v[204:207] offset:7168
	s_waitcnt lgkmcnt(0)
	s_barrier
; #define GAS __attribute__((address_space(1)))
; #define LAS __attribute__((address_space(3)))
; #define LDS_WAIT() asm volatile("s_waitcnt lgkmcnt(0)" ::: "memory")
;     const int pr = item >> 1, kb = 2 * (pr / nblk) + (item & 1), nb = pr % nblk, k0 = 64 * kb, n0 = 32 * nb;
;     const int nr = n0 + (lane & 31); const int sc = MAP == 1 ? src_col_in(nr) : nr;
;     float v[32];
; #pragma unroll
;     for (int i = 0; i < 32; ++i) v[i] = sc >= 0 ? W[(size_t)(k0 + 2 * i + (lane >> 5)) * Nsrc + sc] : 0.f;
; #pragma unroll
;     for (int i = 0; i < 32; ++i) { const int k = k0 + 2 * i + (lane >> 5); float x = v[i] * wscale; if (KS) x *= (k < ksplit ? ksA[k] : ksB[k - ksplit]); scr[(2 * i + (lane >> 5)) * 33 + (lane & 31)] = x; }
;     LDS_WAIT(); asm volatile("" ::: "memory");
;     const int c = lane & 7;
; #pragma unroll
;     for (int j = 0; j < 4; ++j) { const int n = (lane >> 3) + 8 * j; const LAS float* s = scr + (8 * c) * 33 + n;
;         const unsigned long long o = (unsigned long long)pg8::pk4_fp8(s[0 * 33], s[1 * 33], s[2 * 33], s[3 * 33]) | ((unsigned long long)pg8::pk4_fp8(s[4 * 33], s[5 * 33], s[6 * 33], s[7 * 33]) << 32);
;         *(GAS unsigned long long*)(WT + (size_t)(n0 + n) * K + k0 + 8 * c) = o; }
;     LDS_WAIT(); asm volatile("" ::: "memory");
; }
; __global__ void __launch_bounds__(NWAVES * 64, 2) hybrid_fwd(Args args) {
;     ...
;             if (r < I_UP) { p0_transpose_item_f8<true>(args.in[15] + (size_t)l * DM * FF, DM, FF, FF / 32, (unsigned char*)(ws + WS_WUP + l * SZ_WUP), WUP8_SCALE, args.in[14] + l * DM, args.in[14] + l * DM, DM, scr, r, lane); continue; } r -= I_UP;
	s_add_u32 s8, s34, 0x7000
	s_addc_u32 s9, s35, 0
	global_load_dwordx4 v[176:179], v74, s[8:9]
	s_add_u32 s8, s8, 0x20000
	s_addc_u32 s9, s9, 0
	global_load_dwordx4 v[180:183], v74, s[8:9]
	s_add_u32 s8, s8, 0x20000
	s_addc_u32 s9, s9, 0
	global_load_dwordx4 v[184:187], v74, s[8:9]
	s_add_u32 s8, s8, 0x20000
	s_addc_u32 s9, s9, 0
	global_load_dwordx4 v[188:191], v74, s[8:9]
	s_add_u32 s8, s8, 0x20000
	s_addc_u32 s9, s9, 0
	global_load_dwordx4 v[192:195], v74, s[8:9]
	s_add_u32 s8, s8, 0x20000
	s_addc_u32 s9, s9, 0
	global_load_dwordx4 v[196:199], v74, s[8:9]
	s_add_u32 s8, s8, 0x20000
	s_addc_u32 s9, s9, 0
	global_load_dwordx4 v[200:203], v74, s[8:9]
	s_add_u32 s8, s8, 0x20000
	s_addc_u32 s9, s9, 0
	global_load_dwordx4 v[204:207], v74, s[8:9]
	s_add_u32 s6, s36, 0x1400000
	s_addc_u32 s7, s37, 0
	ds_read_b32 v226, v212
	ds_read_b32 v227, v212 offset:512
	ds_read_b32 v228, v212 offset:1024
	ds_read_b32 v229, v212 offset:1536
	ds_read_b32 v230, v212 offset:2048
	ds_read_b32 v231, v212 offset:2560
	ds_read_b32 v232, v212 offset:3072
	ds_read_b32 v233, v212 offset:3584
	ds_read_b32 v234, v212 offset:4096
	ds_read_b32 v235, v212 offset:4608
	ds_read_b32 v236, v212 offset:5120
	ds_read_b32 v237, v212 offset:5632
	ds_read_b32 v238, v212 offset:6144
	ds_read_b32 v239, v212 offset:6656
	ds_read_b32 v240, v212 offset:7168
	ds_read_b32 v241, v212 offset:7680
	s_waitcnt lgkmcnt(0)
	v_max_f32_e32 v226, v226, v226
	v_max_f32_e32 v227, v227, v227
	v_max_f32_e32 v228, v228, v228
	v_max_f32_e32 v229, v229, v229
	v_max_f32_e32 v230, v230, v230
	v_max_f32_e32 v231, v231, v231
	v_max_f32_e32 v232, v232, v232
	v_max_f32_e32 v233, v233, v233
	v_max_f32_e32 v234, v234, v234
	v_max_f32_e32 v235, v235, v235
	v_max_f32_e32 v236, v236, v236
	v_max_f32_e32 v237, v237, v237
	v_max_f32_e32 v238, v238, v238
	v_max_f32_e32 v239, v239, v239
	v_max_f32_e32 v240, v240, v240
	v_max_f32_e32 v241, v241, v241
	v_med3_f32 v226, v226, s62, v95
	v_med3_f32 v227, v227, s62, v95
	v_med3_f32 v228, v228, s62, v95
	v_med3_f32 v229, v229, s62, v95
	v_med3_f32 v230, v230, s62, v95
	v_med3_f32 v231, v231, s62, v95
	v_med3_f32 v232, v232, s62, v95
	v_med3_f32 v233, v233, s62, v95
	v_med3_f32 v234, v234, s62, v95
	v_med3_f32 v235, v235, s62, v95
	v_med3_f32 v236, v236, s62, v95
	v_med3_f32 v237, v237, s62, v95
	v_med3_f32 v238, v238, s62, v95
	v_med3_f32 v239, v239, s62, v95
	v_med3_f32 v240, v240, s62, v95
	v_med3_f32 v241, v241, s62, v95
	v_mov_b32_e32 v242, 0
	v_mov_b32_e32 v243, 0
	v_mov_b32_e32 v244, 0
	v_mov_b32_e32 v245, 0
	v_cvt_pk_fp8_f32 v242, v226, v227
	v_cvt_pk_fp8_f32 v243, v230, v231
	v_cvt_pk_fp8_f32 v244, v234, v235
	v_cvt_pk_fp8_f32 v245, v238, v239
	v_cvt_pk_fp8_f32 v242, v228, v229 op_sel:[0,0,1]
	v_cvt_pk_fp8_f32 v243, v232, v233 op_sel:[0,0,1]
	v_cvt_pk_fp8_f32 v244, v236, v237 op_sel:[0,0,1]
	v_cvt_pk_fp8_f32 v245, v240, v241 op_sel:[0,0,1]
	s_nop 0
	global_store_dwordx4 v77, v[242:245], s[6:7]
	ds_read_b32 v226, v214
	ds_read_b32 v227, v214 offset:512
	ds_read_b32 v228, v214 offset:1024
	ds_read_b32 v229, v214 offset:1536
	ds_read_b32 v230, v214 offset:2048
	ds_read_b32 v231, v214 offset:2560
	ds_read_b32 v232, v214 offset:3072
	ds_read_b32 v233, v214 offset:3584
	ds_read_b32 v234, v214 offset:4096
	ds_read_b32 v235, v214 offset:4608
	ds_read_b32 v236, v214 offset:5120
	ds_read_b32 v237, v214 offset:5632
	ds_read_b32 v238, v214 offset:6144
	ds_read_b32 v239, v214 offset:6656
	ds_read_b32 v240, v214 offset:7168
	ds_read_b32 v241, v214 offset:7680
	s_waitcnt lgkmcnt(0)
	v_max_f32_e32 v226, v226, v226
	v_max_f32_e32 v227, v227, v227
	v_max_f32_e32 v228, v228, v228
	v_max_f32_e32 v229, v229, v229
	v_max_f32_e32 v230, v230, v230
	v_max_f32_e32 v231, v231, v231
	v_max_f32_e32 v232, v232, v232
	v_max_f32_e32 v233, v233, v233
	v_max_f32_e32 v234, v234, v234
	v_max_f32_e32 v235, v235, v235
	v_max_f32_e32 v236, v236, v236
	v_max_f32_e32 v237, v237, v237
	v_max_f32_e32 v238, v238, v238
	v_max_f32_e32 v239, v239, v239
	v_max_f32_e32 v240, v240, v240
	v_max_f32_e32 v241, v241, v241
	v_med3_f32 v226, v226, s62, v95
	v_med3_f32 v227, v227, s62, v95
	v_med3_f32 v228, v228, s62, v95
	v_med3_f32 v229, v229, s62, v95
	v_med3_f32 v230, v230, s62, v95
	v_med3_f32 v231, v231, s62, v95
	v_med3_f32 v232, v232, s62, v95
	v_med3_f32 v233, v233, s62, v95
	v_med3_f32 v234, v234, s62, v95
	v_med3_f32 v235, v235, s62, v95
	v_med3_f32 v236, v236, s62, v95
	v_med3_f32 v237, v237, s62, v95
	v_med3_f32 v238, v238, s62, v95
	v_med3_f32 v239, v239, s62, v95
	v_med3_f32 v240, v240, s62, v95
	v_med3_f32 v241, v241, s62, v95
	v_mov_b32_e32 v242, 0
	v_mov_b32_e32 v243, 0
	v_mov_b32_e32 v244, 0
	v_mov_b32_e32 v245, 0
	v_cvt_pk_fp8_f32 v242, v226, v227
	v_cvt_pk_fp8_f32 v243, v230, v231
	v_cvt_pk_fp8_f32 v244, v234, v235
	v_cvt_pk_fp8_f32 v245, v238, v239
	v_cvt_pk_fp8_f32 v242, v228, v229 op_sel:[0,0,1]
	v_cvt_pk_fp8_f32 v243, v232, v233 op_sel:[0,0,1]
	v_cvt_pk_fp8_f32 v244, v236, v237 op_sel:[0,0,1]
	v_cvt_pk_fp8_f32 v245, v240, v241 op_sel:[0,0,1]
	s_nop 0
	global_store_dwordx4 v78, v[242:245], s[6:7]
	s_waitcnt vmcnt(12)
	v_mul_f32_e32 v144, v34, v144
	v_mul_f32_e32 v145, v34, v145
	v_mul_f32_e32 v146, v34, v146
	v_mul_f32_e32 v147, v34, v147
	ds_write_b128 v209, v[144:147]
	v_mul_f32_e32 v148, v35, v148
	v_mul_f32_e32 v149, v35, v149
	v_mul_f32_e32 v150, v35, v150
	v_mul_f32_e32 v151, v35, v151
	ds_write_b128 v209, v[148:151] offset:1024
	v_mul_f32_e32 v152, v36, v152
	v_mul_f32_e32 v153, v36, v153
	v_mul_f32_e32 v154, v36, v154
	v_mul_f32_e32 v155, v36, v155
	ds_write_b128 v209, v[152:155] offset:2048
	v_mul_f32_e32 v156, v37, v156
	v_mul_f32_e32 v157, v37, v157
	v_mul_f32_e32 v158, v37, v158
	v_mul_f32_e32 v159, v37, v159
	ds_write_b128 v209, v[156:159] offset:3072
	v_mul_f32_e32 v160, v38, v160
	v_mul_f32_e32 v161, v38, v161
	v_mul_f32_e32 v162, v38, v162
	v_mul_f32_e32 v163, v38, v163
	ds_write_b128 v209, v[160:163] offset:4096
	v_mul_f32_e32 v164, v39, v164
	v_mul_f32_e32 v165, v39, v165
	v_mul_f32_e32 v166, v39, v166
	v_mul_f32_e32 v167, v39, v167
	ds_write_b128 v209, v[164:167] offset:5120
	v_mul_f32_e32 v168, v40, v168
	v_mul_f32_e32 v169, v40, v169
	v_mul_f32_e32 v170, v40, v170
	v_mul_f32_e32 v171, v40, v171
	ds_write_b128 v209, v[168:171] offset:6144
	v_mul_f32_e32 v172, v41, v172
	v_mul_f32_e32 v173, v41, v173
	v_mul_f32_e32 v174, v41, v174
	v_mul_f32_e32 v175, v41, v175
	ds_write_b128 v209, v[172:175] offset:7168
	s_waitcnt lgkmcnt(0)
	s_barrier
; #define GAS __attribute__((address_space(1)))
; #define LAS __attribute__((address_space(3)))
; #define LDS_WAIT() asm volatile("s_waitcnt lgkmcnt(0)" ::: "memory")
;     const int pr = item >> 1, kb = 2 * (pr / nblk) + (item & 1), nb = pr % nblk, k0 = 64 * kb, n0 = 32 * nb;
;     const int nr = n0 + (lane & 31); const int sc = MAP == 1 ? src_col_in(nr) : nr;
;     float v[32];
; #pragma unroll
;     for (int i = 0; i < 32; ++i) v[i] = sc >= 0 ? W[(size_t)(k0 + 2 * i + (lane >> 5)) * Nsrc + sc] : 0.f;
; #pragma unroll
;     for (int i = 0; i < 32; ++i) { const int k = k0 + 2 * i + (lane >> 5); float x = v[i] * wscale; if (KS) x *= (k < ksplit ? ksA[k] : ksB[k - ksplit]); scr[(2 * i + (lane >> 5)) * 33 + (lane & 31)] = x; }
;     LDS_WAIT(); asm volatile("" ::: "memory");
;     const int c = lane & 7;
; #pragma unroll
;     for (int j = 0; j < 4; ++j) { const int n = (lane >> 3) + 8 * j; const LAS float* s = scr + (8 * c) * 33 + n;
;         const unsigned long long o = (unsigned long long)pg8::pk4_fp8(s[0 * 33], s[1 * 33], s[2 * 33], s[3 * 33]) | ((unsigned long long)pg8::pk4_fp8(s[4 * 33], s[5 * 33], s[6 * 33], s[7 * 33]) << 32);
;         *(GAS unsigned long long*)(WT + (size_t)(n0 + n) * K + k0 + 8 * c) = o; }
;     LDS_WAIT(); asm volatile("" ::: "memory");
; }
; __global__ void __launch_bounds__(NWAVES * 64, 2) hybrid_fwd(Args args) {
;     ...
;             if (r < I_UP) { p0_transpose_item_f8<true>(args.in[15] + (size_t)l * DM * FF, DM, FF, FF / 32, (unsigned char*)(ws + WS_WUP + l * SZ_WUP), WUP8_SCALE, args.in[14] + l * DM, args.in[14] + l * DM, DM, scr, r, lane); continue; } r -= I_UP;
	s_add_u32 s8, s34, 0x8000
	s_addc_u32 s9, s35, 0
	global_load_dwordx4 v[144:147], v74, s[8:9]
	s_add_u32 s8, s8, 0x20000
	s_addc_u32 s9, s9, 0
	global_load_dwordx4 v[148:151], v74, s[8:9]
	s_add_u32 s8, s8, 0x20000
	s_addc_u32 s9, s9, 0
	global_load_dwordx4 v[152:155], v74, s[8:9]
	s_add_u32 s8, s8, 0x20000
	s_addc_u32 s9, s9, 0
	global_load_dwordx4 v[156:159], v74, s[8:9]
	s_add_u32 s8, s8, 0x20000
	s_addc_u32 s9, s9, 0
	global_load_dwordx4 v[160:163], v74, s[8:9]
	s_add_u32 s8, s8, 0x20000
	s_addc_u32 s9, s9, 0
	global_load_dwordx4 v[164:167], v74, s[8:9]
	s_add_u32 s8, s8, 0x20000
	s_addc_u32 s9, s9, 0
	global_load_dwordx4 v[168:171], v74, s[8:9]
	s_add_u32 s8, s8, 0x20000
	s_addc_u32 s9, s9, 0
	global_load_dwordx4 v[172:175], v74, s[8:9]
	s_add_u32 s6, s36, 0x1800000
	s_addc_u32 s7, s37, 0
	ds_read_b32 v226, v211
	ds_read_b32 v227, v211 offset:512
	ds_read_b32 v228, v211 offset:1024
	ds_read_b32 v229, v211 offset:1536
	ds_read_b32 v230, v211 offset:2048
	ds_read_b32 v231, v211 offset:2560
	ds_read_b32 v232, v211 offset:3072
	ds_read_b32 v233, v211 offset:3584
	ds_read_b32 v234, v211 offset:4096
	ds_read_b32 v235, v211 offset:4608
	ds_read_b32 v236, v211 offset:5120
	ds_read_b32 v237, v211 offset:5632
	ds_read_b32 v238, v211 offset:6144
	ds_read_b32 v239, v211 offset:6656
	ds_read_b32 v240, v211 offset:7168
	ds_read_b32 v241, v211 offset:7680
	s_waitcnt lgkmcnt(0)
	v_max_f32_e32 v226, v226, v226
	v_max_f32_e32 v227, v227, v227
	v_max_f32_e32 v228, v228, v228
	v_max_f32_e32 v229, v229, v229
	v_max_f32_e32 v230, v230, v230
	v_max_f32_e32 v231, v231, v231
	v_max_f32_e32 v232, v232, v232
	v_max_f32_e32 v233, v233, v233
	v_max_f32_e32 v234, v234, v234
	v_max_f32_e32 v235, v235, v235
	v_max_f32_e32 v236, v236, v236
	v_max_f32_e32 v237, v237, v237
	v_max_f32_e32 v238, v238, v238
	v_max_f32_e32 v239, v239, v239
	v_max_f32_e32 v240, v240, v240
	v_max_f32_e32 v241, v241, v241
	v_med3_f32 v226, v226, s62, v95
	v_med3_f32 v227, v227, s62, v95
	v_med3_f32 v228, v228, s62, v95
	v_med3_f32 v229, v229, s62, v95
	v_med3_f32 v230, v230, s62, v95
	v_med3_f32 v231, v231, s62, v95
	v_med3_f32 v232, v232, s62, v95
	v_med3_f32 v233, v233, s62, v95
	v_med3_f32 v234, v234, s62, v95
	v_med3_f32 v235, v235, s62, v95
	v_med3_f32 v236, v236, s62, v95
	v_med3_f32 v237, v237, s62, v95
	v_med3_f32 v238, v238, s62, v95
	v_med3_f32 v239, v239, s62, v95
	v_med3_f32 v240, v240, s62, v95
	v_med3_f32 v241, v241, s62, v95
	v_mov_b32_e32 v242, 0
	v_mov_b32_e32 v243, 0
	v_mov_b32_e32 v244, 0
	v_mov_b32_e32 v245, 0
	v_cvt_pk_fp8_f32 v242, v226, v227
	v_cvt_pk_fp8_f32 v243, v230, v231
	v_cvt_pk_fp8_f32 v244, v234, v235
	v_cvt_pk_fp8_f32 v245, v238, v239
	v_cvt_pk_fp8_f32 v242, v228, v229 op_sel:[0,0,1]
	v_cvt_pk_fp8_f32 v243, v232, v233 op_sel:[0,0,1]
	v_cvt_pk_fp8_f32 v244, v236, v237 op_sel:[0,0,1]
	v_cvt_pk_fp8_f32 v245, v240, v241 op_sel:[0,0,1]
	s_nop 0
	global_store_dwordx4 v77, v[242:245], s[6:7]
	ds_read_b32 v226, v213
	ds_read_b32 v227, v213 offset:512
	ds_read_b32 v228, v213 offset:1024
	ds_read_b32 v229, v213 offset:1536
	ds_read_b32 v230, v213 offset:2048
	ds_read_b32 v231, v213 offset:2560
	ds_read_b32 v232, v213 offset:3072
	ds_read_b32 v233, v213 offset:3584
	ds_read_b32 v234, v213 offset:4096
	ds_read_b32 v235, v213 offset:4608
	ds_read_b32 v236, v213 offset:5120
	ds_read_b32 v237, v213 offset:5632
	ds_read_b32 v238, v213 offset:6144
	ds_read_b32 v239, v213 offset:6656
	ds_read_b32 v240, v213 offset:7168
	ds_read_b32 v241, v213 offset:7680
	s_waitcnt lgkmcnt(0)
	v_max_f32_e32 v226, v226, v226
	v_max_f32_e32 v227, v227, v227
	v_max_f32_e32 v228, v228, v228
	v_max_f32_e32 v229, v229, v229
	v_max_f32_e32 v230, v230, v230
	v_max_f32_e32 v231, v231, v231
	v_max_f32_e32 v232, v232, v232
	v_max_f32_e32 v233, v233, v233
	v_max_f32_e32 v234, v234, v234
	v_max_f32_e32 v235, v235, v235
	v_max_f32_e32 v236, v236, v236
	v_max_f32_e32 v237, v237, v237
	v_max_f32_e32 v238, v238, v238
	v_max_f32_e32 v239, v239, v239
	v_max_f32_e32 v240, v240, v240
	v_max_f32_e32 v241, v241, v241
	v_med3_f32 v226, v226, s62, v95
	v_med3_f32 v227, v227, s62, v95
	v_med3_f32 v228, v228, s62, v95
	v_med3_f32 v229, v229, s62, v95
	v_med3_f32 v230, v230, s62, v95
	v_med3_f32 v231, v231, s62, v95
	v_med3_f32 v232, v232, s62, v95
	v_med3_f32 v233, v233, s62, v95
	v_med3_f32 v234, v234, s62, v95
	v_med3_f32 v235, v235, s62, v95
	v_med3_f32 v236, v236, s62, v95
	v_med3_f32 v237, v237, s62, v95
	v_med3_f32 v238, v238, s62, v95
	v_med3_f32 v239, v239, s62, v95
	v_med3_f32 v240, v240, s62, v95
	v_med3_f32 v241, v241, s62, v95
	v_mov_b32_e32 v242, 0
	v_mov_b32_e32 v243, 0
	v_mov_b32_e32 v244, 0
	v_mov_b32_e32 v245, 0
	v_cvt_pk_fp8_f32 v242, v226, v227
	v_cvt_pk_fp8_f32 v243, v230, v231
	v_cvt_pk_fp8_f32 v244, v234, v235
	v_cvt_pk_fp8_f32 v245, v238, v239
	v_cvt_pk_fp8_f32 v242, v228, v229 op_sel:[0,0,1]
	v_cvt_pk_fp8_f32 v243, v232, v233 op_sel:[0,0,1]
	v_cvt_pk_fp8_f32 v244, v236, v237 op_sel:[0,0,1]
	v_cvt_pk_fp8_f32 v245, v240, v241 op_sel:[0,0,1]
	s_nop 0
	global_store_dwordx4 v78, v[242:245], s[6:7]
	s_waitcnt vmcnt(12)
	v_mul_f32_e32 v176, v34, v176
	v_mul_f32_e32 v177, v34, v177
	v_mul_f32_e32 v178, v34, v178
	v_mul_f32_e32 v179, v34, v179
	ds_write_b128 v210, v[176:179]
	v_mul_f32_e32 v180, v35, v180
	v_mul_f32_e32 v181, v35, v181
	v_mul_f32_e32 v182, v35, v182
	v_mul_f32_e32 v183, v35, v183
	ds_write_b128 v210, v[180:183] offset:1024
	v_mul_f32_e32 v184, v36, v184
	v_mul_f32_e32 v185, v36, v185
	v_mul_f32_e32 v186, v36, v186
	v_mul_f32_e32 v187, v36, v187
	ds_write_b128 v210, v[184:187] offset:2048
	v_mul_f32_e32 v188, v37, v188
	v_mul_f32_e32 v189, v37, v189
	v_mul_f32_e32 v190, v37, v190
	v_mul_f32_e32 v191, v37, v191
	ds_write_b128 v210, v[188:191] offset:3072
	v_mul_f32_e32 v192, v38, v192
	v_mul_f32_e32 v193, v38, v193
	v_mul_f32_e32 v194, v38, v194
	v_mul_f32_e32 v195, v38, v195
	ds_write_b128 v210, v[192:195] offset:4096
	v_mul_f32_e32 v196, v39, v196
	v_mul_f32_e32 v197, v39, v197
	v_mul_f32_e32 v198, v39, v198
	v_mul_f32_e32 v199, v39, v199
	ds_write_b128 v210, v[196:199] offset:5120
	v_mul_f32_e32 v200, v40, v200
	v_mul_f32_e32 v201, v40, v201
	v_mul_f32_e32 v202, v40, v202
	v_mul_f32_e32 v203, v40, v203
	ds_write_b128 v210, v[200:203] offset:6144
	v_mul_f32_e32 v204, v41, v204
	v_mul_f32_e32 v205, v41, v205
	v_mul_f32_e32 v206, v41, v206
	v_mul_f32_e32 v207, v41, v207
	ds_write_b128 v210, v[204:207] offset:7168
	s_waitcnt lgkmcnt(0)
	s_barrier
; #define GAS __attribute__((address_space(1)))
; #define LAS __attribute__((address_space(3)))
; #define LDS_WAIT() asm volatile("s_waitcnt lgkmcnt(0)" ::: "memory")
;     const int pr = item >> 1, kb = 2 * (pr / nblk) + (item & 1), nb = pr % nblk, k0 = 64 * kb, n0 = 32 * nb;
;     const int nr = n0 + (lane & 31); const int sc = MAP == 1 ? src_col_in(nr) : nr;
;     float v[32];
; #pragma unroll
;     for (int i = 0; i < 32; ++i) v[i] = sc >= 0 ? W[(size_t)(k0 + 2 * i + (lane >> 5)) * Nsrc + sc] : 0.f;
; #pragma unroll
;     for (int i = 0; i < 32; ++i) { const int k = k0 + 2 * i + (lane >> 5); float x = v[i] * wscale; if (KS) x *= (k < ksplit ? ksA[k] : ksB[k - ksplit]); scr[(2 * i + (lane >> 5)) * 33 + (lane & 31)] = x; }
;     LDS_WAIT(); asm volatile("" ::: "memory");
;     const int c = lane & 7;
; #pragma unroll
;     for (int j = 0; j < 4; ++j) { const int n = (lane >> 3) + 8 * j; const LAS float* s = scr + (8 * c) * 33 + n;
;         const unsigned long long o = (unsigned long long)pg8::pk4_fp8(s[0 * 33], s[1 * 33], s[2 * 33], s[3 * 33]) | ((unsigned long long)pg8::pk4_fp8(s[4 * 33], s[5 * 33], s[6 * 33], s[7 * 33]) << 32);
;         *(GAS unsigned long long*)(WT + (size_t)(n0 + n) * K + k0 + 8 * c) = o; }
;     LDS_WAIT(); asm volatile("" ::: "memory");
; }
; __global__ void __launch_bounds__(NWAVES * 64, 2) hybrid_fwd(Args args) {
;     ...
;             if (r < I_UP) { p0_transpose_item_f8<true>(args.in[15] + (size_t)l * DM * FF, DM, FF, FF / 32, (unsigned char*)(ws + WS_WUP + l * SZ_WUP), WUP8_SCALE, args.in[14] + l * DM, args.in[14] + l * DM, DM, scr, r, lane); continue; } r -= I_UP;
	s_add_u32 s8, s34, 0x9000
	s_addc_u32 s9, s35, 0
	global_load_dwordx4 v[176:179], v74, s[8:9]
	s_add_u32 s8, s8, 0x20000
	s_addc_u32 s9, s9, 0
	global_load_dwordx4 v[180:183], v74, s[8:9]
	s_add_u32 s8, s8, 0x20000
	s_addc_u32 s9, s9, 0
	global_load_dwordx4 v[184:187], v74, s[8:9]
	s_add_u32 s8, s8, 0x20000
	s_addc_u32 s9, s9, 0
	global_load_dwordx4 v[188:191], v74, s[8:9]
	s_add_u32 s8, s8, 0x20000
	s_addc_u32 s9, s9, 0
	global_load_dwordx4 v[192:195], v74, s[8:9]
	s_add_u32 s8, s8, 0x20000
	s_addc_u32 s9, s9, 0
	global_load_dwordx4 v[196:199], v74, s[8:9]
	s_add_u32 s8, s8, 0x20000
	s_addc_u32 s9, s9, 0
	global_load_dwordx4 v[200:203], v74, s[8:9]
	s_add_u32 s8, s8, 0x20000
	s_addc_u32 s9, s9, 0
	global_load_dwordx4 v[204:207], v74, s[8:9]
	s_add_u32 s6, s36, 0x1c00000
	s_addc_u32 s7, s37, 0
	ds_read_b32 v226, v212
	ds_read_b32 v227, v212 offset:512
	ds_read_b32 v228, v212 offset:1024
	ds_read_b32 v229, v212 offset:1536
	ds_read_b32 v230, v212 offset:2048
	ds_read_b32 v231, v212 offset:2560
	ds_read_b32 v232, v212 offset:3072
	ds_read_b32 v233, v212 offset:3584
	ds_read_b32 v234, v212 offset:4096
	ds_read_b32 v235, v212 offset:4608
	ds_read_b32 v236, v212 offset:5120
	ds_read_b32 v237, v212 offset:5632
	ds_read_b32 v238, v212 offset:6144
	ds_read_b32 v239, v212 offset:6656
	ds_read_b32 v240, v212 offset:7168
	ds_read_b32 v241, v212 offset:7680
	s_waitcnt lgkmcnt(0)
	v_max_f32_e32 v226, v226, v226
	v_max_f32_e32 v227, v227, v227
	v_max_f32_e32 v228, v228, v228
	v_max_f32_e32 v229, v229, v229
	v_max_f32_e32 v230, v230, v230
	v_max_f32_e32 v231, v231, v231
	v_max_f32_e32 v232, v232, v232
	v_max_f32_e32 v233, v233, v233
	v_max_f32_e32 v234, v234, v234
	v_max_f32_e32 v235, v235, v235
	v_max_f32_e32 v236, v236, v236
	v_max_f32_e32 v237, v237, v237
	v_max_f32_e32 v238, v238, v238
	v_max_f32_e32 v239, v239, v239
	v_max_f32_e32 v240, v240, v240
	v_max_f32_e32 v241, v241, v241
	v_med3_f32 v226, v226, s62, v95
	v_med3_f32 v227, v227, s62, v95
	v_med3_f32 v228, v228, s62, v95
	v_med3_f32 v229, v229, s62, v95
	v_med3_f32 v230, v230, s62, v95
	v_med3_f32 v231, v231, s62, v95
	v_med3_f32 v232, v232, s62, v95
	v_med3_f32 v233, v233, s62, v95
	v_med3_f32 v234, v234, s62, v95
	v_med3_f32 v235, v235, s62, v95
	v_med3_f32 v236, v236, s62, v95
	v_med3_f32 v237, v237, s62, v95
	v_med3_f32 v238, v238, s62, v95
	v_med3_f32 v239, v239, s62, v95
	v_med3_f32 v240, v240, s62, v95
	v_med3_f32 v241, v241, s62, v95
	v_mov_b32_e32 v242, 0
	v_mov_b32_e32 v243, 0
	v_mov_b32_e32 v244, 0
	v_mov_b32_e32 v245, 0
	v_cvt_pk_fp8_f32 v242, v226, v227
	v_cvt_pk_fp8_f32 v243, v230, v231
	v_cvt_pk_fp8_f32 v244, v234, v235
	v_cvt_pk_fp8_f32 v245, v238, v239
	v_cvt_pk_fp8_f32 v242, v228, v229 op_sel:[0,0,1]
	v_cvt_pk_fp8_f32 v243, v232, v233 op_sel:[0,0,1]
	v_cvt_pk_fp8_f32 v244, v236, v237 op_sel:[0,0,1]
	v_cvt_pk_fp8_f32 v245, v240, v241 op_sel:[0,0,1]
	s_nop 0
	global_store_dwordx4 v77, v[242:245], s[6:7]
	ds_read_b32 v226, v214
	ds_read_b32 v227, v214 offset:512
	ds_read_b32 v228, v214 offset:1024
	ds_read_b32 v229, v214 offset:1536
	ds_read_b32 v230, v214 offset:2048
	ds_read_b32 v231, v214 offset:2560
	ds_read_b32 v232, v214 offset:3072
	ds_read_b32 v233, v214 offset:3584
	ds_read_b32 v234, v214 offset:4096
	ds_read_b32 v235, v214 offset:4608
	ds_read_b32 v236, v214 offset:5120
	ds_read_b32 v237, v214 offset:5632
	ds_read_b32 v238, v214 offset:6144
	ds_read_b32 v239, v214 offset:6656
	ds_read_b32 v240, v214 offset:7168
	ds_read_b32 v241, v214 offset:7680
	s_waitcnt lgkmcnt(0)
	v_max_f32_e32 v226, v226, v226
	v_max_f32_e32 v227, v227, v227
	v_max_f32_e32 v228, v228, v228
	v_max_f32_e32 v229, v229, v229
	v_max_f32_e32 v230, v230, v230
	v_max_f32_e32 v231, v231, v231
	v_max_f32_e32 v232, v232, v232
	v_max_f32_e32 v233, v233, v233
	v_max_f32_e32 v234, v234, v234
	v_max_f32_e32 v235, v235, v235
	v_max_f32_e32 v236, v236, v236
	v_max_f32_e32 v237, v237, v237
	v_max_f32_e32 v238, v238, v238
	v_max_f32_e32 v239, v239, v239
	v_max_f32_e32 v240, v240, v240
	v_max_f32_e32 v241, v241, v241
	v_med3_f32 v226, v226, s62, v95
	v_med3_f32 v227, v227, s62, v95
	v_med3_f32 v228, v228, s62, v95
	v_med3_f32 v229, v229, s62, v95
	v_med3_f32 v230, v230, s62, v95
	v_med3_f32 v231, v231, s62, v95
	v_med3_f32 v232, v232, s62, v95
	v_med3_f32 v233, v233, s62, v95
	v_med3_f32 v234, v234, s62, v95
	v_med3_f32 v235, v235, s62, v95
	v_med3_f32 v236, v236, s62, v95
	v_med3_f32 v237, v237, s62, v95
	v_med3_f32 v238, v238, s62, v95
	v_med3_f32 v239, v239, s62, v95
	v_med3_f32 v240, v240, s62, v95
	v_med3_f32 v241, v241, s62, v95
	v_mov_b32_e32 v242, 0
	v_mov_b32_e32 v243, 0
	v_mov_b32_e32 v244, 0
	v_mov_b32_e32 v245, 0
	v_cvt_pk_fp8_f32 v242, v226, v227
	v_cvt_pk_fp8_f32 v243, v230, v231
	v_cvt_pk_fp8_f32 v244, v234, v235
	v_cvt_pk_fp8_f32 v245, v238, v239
	v_cvt_pk_fp8_f32 v242, v228, v229 op_sel:[0,0,1]
	v_cvt_pk_fp8_f32 v243, v232, v233 op_sel:[0,0,1]
	v_cvt_pk_fp8_f32 v244, v236, v237 op_sel:[0,0,1]
	v_cvt_pk_fp8_f32 v245, v240, v241 op_sel:[0,0,1]
	s_nop 0
	global_store_dwordx4 v78, v[242:245], s[6:7]
	s_waitcnt vmcnt(12)
	v_mul_f32_e32 v144, v34, v144
	v_mul_f32_e32 v145, v34, v145
	v_mul_f32_e32 v146, v34, v146
	v_mul_f32_e32 v147, v34, v147
	ds_write_b128 v209, v[144:147]
	v_mul_f32_e32 v148, v35, v148
	v_mul_f32_e32 v149, v35, v149
	v_mul_f32_e32 v150, v35, v150
	v_mul_f32_e32 v151, v35, v151
	ds_write_b128 v209, v[148:151] offset:1024
	v_mul_f32_e32 v152, v36, v152
	v_mul_f32_e32 v153, v36, v153
	v_mul_f32_e32 v154, v36, v154
	v_mul_f32_e32 v155, v36, v155
	ds_write_b128 v209, v[152:155] offset:2048
	v_mul_f32_e32 v156, v37, v156
	v_mul_f32_e32 v157, v37, v157
	v_mul_f32_e32 v158, v37, v158
	v_mul_f32_e32 v159, v37, v159
	ds_write_b128 v209, v[156:159] offset:3072
	v_mul_f32_e32 v160, v38, v160
	v_mul_f32_e32 v161, v38, v161
	v_mul_f32_e32 v162, v38, v162
	v_mul_f32_e32 v163, v38, v163
	ds_write_b128 v209, v[160:163] offset:4096
	v_mul_f32_e32 v164, v39, v164
	v_mul_f32_e32 v165, v39, v165
	v_mul_f32_e32 v166, v39, v166
	v_mul_f32_e32 v167, v39, v167
	ds_write_b128 v209, v[164:167] offset:5120
	v_mul_f32_e32 v168, v40, v168
	v_mul_f32_e32 v169, v40, v169
	v_mul_f32_e32 v170, v40, v170
	v_mul_f32_e32 v171, v40, v171
	ds_write_b128 v209, v[168:171] offset:6144
	v_mul_f32_e32 v172, v41, v172
	v_mul_f32_e32 v173, v41, v173
	v_mul_f32_e32 v174, v41, v174
	v_mul_f32_e32 v175, v41, v175
	ds_write_b128 v209, v[172:175] offset:7168
	s_waitcnt lgkmcnt(0)
	s_barrier
; #define GAS __attribute__((address_space(1)))
; #define LAS __attribute__((address_space(3)))
; #define LDS_WAIT() asm volatile("s_waitcnt lgkmcnt(0)" ::: "memory")
;     const int pr = item >> 1, kb = 2 * (pr / nblk) + (item & 1), nb = pr % nblk, k0 = 64 * kb, n0 = 32 * nb;
;     const int nr = n0 + (lane & 31); const int sc = MAP == 1 ? src_col_in(nr) : nr;
;     float v[32];
; #pragma unroll
;     for (int i = 0; i < 32; ++i) v[i] = sc >= 0 ? W[(size_t)(k0 + 2 * i + (lane >> 5)) * Nsrc + sc] : 0.f;
; #pragma unroll
;     for (int i = 0; i < 32; ++i) { const int k = k0 + 2 * i + (lane >> 5); float x = v[i] * wscale; if (KS) x *= (k < ksplit ? ksA[k] : ksB[k - ksplit]); scr[(2 * i + (lane >> 5)) * 33 + (lane & 31)] = x; }
;     LDS_WAIT(); asm volatile("" ::: "memory");
;     const int c = lane & 7;
; #pragma unroll
;     for (int j = 0; j < 4; ++j) { const int n = (lane >> 3) + 8 * j; const LAS float* s = scr + (8 * c) * 33 + n;
;         const unsigned long long o = (unsigned long long)pg8::pk4_fp8(s[0 * 33], s[1 * 33], s[2 * 33], s[3 * 33]) | ((unsigned long long)pg8::pk4_fp8(s[4 * 33], s[5 * 33], s[6 * 33], s[7 * 33]) << 32);
;         *(GAS unsigned long long*)(WT + (size_t)(n0 + n) * K + k0 + 8 * c) = o; }
;     LDS_WAIT(); asm volatile("" ::: "memory");
; }
; __global__ void __launch_bounds__(NWAVES * 64, 2) hybrid_fwd(Args args) {
;     ...
;             if (r < I_UP) { p0_transpose_item_f8<true>(args.in[15] + (size_t)l * DM * FF, DM, FF, FF / 32, (unsigned char*)(ws + WS_WUP + l * SZ_WUP), WUP8_SCALE, args.in[14] + l * DM, args.in[14] + l * DM, DM, scr, r, lane); continue; } r -= I_UP;
	s_add_u32 s8, s34, 0xa000
	s_addc_u32 s9, s35, 0
	global_load_dwordx4 v[144:147], v74, s[8:9]
	s_add_u32 s8, s8, 0x20000
	s_addc_u32 s9, s9, 0
	global_load_dwordx4 v[148:151], v74, s[8:9]
	s_add_u32 s8, s8, 0x20000
	s_addc_u32 s9, s9, 0
	global_load_dwordx4 v[152:155], v74, s[8:9]
	s_add_u32 s8, s8, 0x20000
	s_addc_u32 s9, s9, 0
	global_load_dwordx4 v[156:159], v74, s[8:9]
	s_add_u32 s8, s8, 0x20000
	s_addc_u32 s9, s9, 0
	global_load_dwordx4 v[160:163], v74, s[8:9]
	s_add_u32 s8, s8, 0x20000
	s_addc_u32 s9, s9, 0
	global_load_dwordx4 v[164:167], v74, s[8:9]
	s_add_u32 s8, s8, 0x20000
	s_addc_u32 s9, s9, 0
	global_load_dwordx4 v[168:171], v74, s[8:9]
	s_add_u32 s8, s8, 0x20000
	s_addc_u32 s9, s9, 0
	global_load_dwordx4 v[172:175], v74, s[8:9]
	s_add_u32 s6, s36, 0x2000000
	s_addc_u32 s7, s37, 0
	ds_read_b32 v226, v211
	ds_read_b32 v227, v211 offset:512
	ds_read_b32 v228, v211 offset:1024
	ds_read_b32 v229, v211 offset:1536
	ds_read_b32 v230, v211 offset:2048
	ds_read_b32 v231, v211 offset:2560
	ds_read_b32 v232, v211 offset:3072
	ds_read_b32 v233, v211 offset:3584
	ds_read_b32 v234, v211 offset:4096
	ds_read_b32 v235, v211 offset:4608
	ds_read_b32 v236, v211 offset:5120
	ds_read_b32 v237, v211 offset:5632
	ds_read_b32 v238, v211 offset:6144
	ds_read_b32 v239, v211 offset:6656
	ds_read_b32 v240, v211 offset:7168
	ds_read_b32 v241, v211 offset:7680
	s_waitcnt lgkmcnt(0)
	v_max_f32_e32 v226, v226, v226
	v_max_f32_e32 v227, v227, v227
	v_max_f32_e32 v228, v228, v228
	v_max_f32_e32 v229, v229, v229
	v_max_f32_e32 v230, v230, v230
	v_max_f32_e32 v231, v231, v231
	v_max_f32_e32 v232, v232, v232
	v_max_f32_e32 v233, v233, v233
	v_max_f32_e32 v234, v234, v234
	v_max_f32_e32 v235, v235, v235
	v_max_f32_e32 v236, v236, v236
	v_max_f32_e32 v237, v237, v237
	v_max_f32_e32 v238, v238, v238
	v_max_f32_e32 v239, v239, v239
	v_max_f32_e32 v240, v240, v240
	v_max_f32_e32 v241, v241, v241
	v_med3_f32 v226, v226, s62, v95
	v_med3_f32 v227, v227, s62, v95
	v_med3_f32 v228, v228, s62, v95
	v_med3_f32 v229, v229, s62, v95
	v_med3_f32 v230, v230, s62, v95
	v_med3_f32 v231, v231, s62, v95
	v_med3_f32 v232, v232, s62, v95
	v_med3_f32 v233, v233, s62, v95
	v_med3_f32 v234, v234, s62, v95
	v_med3_f32 v235, v235, s62, v95
	v_med3_f32 v236, v236, s62, v95
	v_med3_f32 v237, v237, s62, v95
	v_med3_f32 v238, v238, s62, v95
	v_med3_f32 v239, v239, s62, v95
	v_med3_f32 v240, v240, s62, v95
	v_med3_f32 v241, v241, s62, v95
	v_mov_b32_e32 v242, 0
	v_mov_b32_e32 v243, 0
	v_mov_b32_e32 v244, 0
	v_mov_b32_e32 v245, 0
	v_cvt_pk_fp8_f32 v242, v226, v227
	v_cvt_pk_fp8_f32 v243, v230, v231
	v_cvt_pk_fp8_f32 v244, v234, v235
	v_cvt_pk_fp8_f32 v245, v238, v239
	v_cvt_pk_fp8_f32 v242, v228, v229 op_sel:[0,0,1]
	v_cvt_pk_fp8_f32 v243, v232, v233 op_sel:[0,0,1]
	v_cvt_pk_fp8_f32 v244, v236, v237 op_sel:[0,0,1]
	v_cvt_pk_fp8_f32 v245, v240, v241 op_sel:[0,0,1]
	s_nop 0
	global_store_dwordx4 v77, v[242:245], s[6:7]
	ds_read_b32 v226, v213
	ds_read_b32 v227, v213 offset:512
	ds_read_b32 v228, v213 offset:1024
	ds_read_b32 v229, v213 offset:1536
	ds_read_b32 v230, v213 offset:2048
	ds_read_b32 v231, v213 offset:2560
	ds_read_b32 v232, v213 offset:3072
	ds_read_b32 v233, v213 offset:3584
	ds_read_b32 v234, v213 offset:4096
	ds_read_b32 v235, v213 offset:4608
	ds_read_b32 v236, v213 offset:5120
	ds_read_b32 v237, v213 offset:5632
	ds_read_b32 v238, v213 offset:6144
	ds_read_b32 v239, v213 offset:6656
	ds_read_b32 v240, v213 offset:7168
	ds_read_b32 v241, v213 offset:7680
	s_waitcnt lgkmcnt(0)
	v_max_f32_e32 v226, v226, v226
	v_max_f32_e32 v227, v227, v227
	v_max_f32_e32 v228, v228, v228
	v_max_f32_e32 v229, v229, v229
	v_max_f32_e32 v230, v230, v230
	v_max_f32_e32 v231, v231, v231
	v_max_f32_e32 v232, v232, v232
	v_max_f32_e32 v233, v233, v233
	v_max_f32_e32 v234, v234, v234
	v_max_f32_e32 v235, v235, v235
	v_max_f32_e32 v236, v236, v236
	v_max_f32_e32 v237, v237, v237
	v_max_f32_e32 v238, v238, v238
	v_max_f32_e32 v239, v239, v239
	v_max_f32_e32 v240, v240, v240
	v_max_f32_e32 v241, v241, v241
	v_med3_f32 v226, v226, s62, v95
	v_med3_f32 v227, v227, s62, v95
	v_med3_f32 v228, v228, s62, v95
	v_med3_f32 v229, v229, s62, v95
	v_med3_f32 v230, v230, s62, v95
	v_med3_f32 v231, v231, s62, v95
	v_med3_f32 v232, v232, s62, v95
	v_med3_f32 v233, v233, s62, v95
	v_med3_f32 v234, v234, s62, v95
	v_med3_f32 v235, v235, s62, v95
	v_med3_f32 v236, v236, s62, v95
	v_med3_f32 v237, v237, s62, v95
	v_med3_f32 v238, v238, s62, v95
	v_med3_f32 v239, v239, s62, v95
	v_med3_f32 v240, v240, s62, v95
	v_med3_f32 v241, v241, s62, v95
	v_mov_b32_e32 v242, 0
	v_mov_b32_e32 v243, 0
	v_mov_b32_e32 v244, 0
	v_mov_b32_e32 v245, 0
	v_cvt_pk_fp8_f32 v242, v226, v227
	v_cvt_pk_fp8_f32 v243, v230, v231
	v_cvt_pk_fp8_f32 v244, v234, v235
	v_cvt_pk_fp8_f32 v245, v238, v239
	v_cvt_pk_fp8_f32 v242, v228, v229 op_sel:[0,0,1]
	v_cvt_pk_fp8_f32 v243, v232, v233 op_sel:[0,0,1]
	v_cvt_pk_fp8_f32 v244, v236, v237 op_sel:[0,0,1]
	v_cvt_pk_fp8_f32 v245, v240, v241 op_sel:[0,0,1]
	s_nop 0
	global_store_dwordx4 v78, v[242:245], s[6:7]
	s_waitcnt vmcnt(12)
	v_mul_f32_e32 v176, v34, v176
	v_mul_f32_e32 v177, v34, v177
	v_mul_f32_e32 v178, v34, v178
	v_mul_f32_e32 v179, v34, v179
	ds_write_b128 v210, v[176:179]
	v_mul_f32_e32 v180, v35, v180
	v_mul_f32_e32 v181, v35, v181
	v_mul_f32_e32 v182, v35, v182
	v_mul_f32_e32 v183, v35, v183
	ds_write_b128 v210, v[180:183] offset:1024
	v_mul_f32_e32 v184, v36, v184
	v_mul_f32_e32 v185, v36, v185
	v_mul_f32_e32 v186, v36, v186
	v_mul_f32_e32 v187, v36, v187
	ds_write_b128 v210, v[184:187] offset:2048
	v_mul_f32_e32 v188, v37, v188
	v_mul_f32_e32 v189, v37, v189
	v_mul_f32_e32 v190, v37, v190
	v_mul_f32_e32 v191, v37, v191
	ds_write_b128 v210, v[188:191] offset:3072
	v_mul_f32_e32 v192, v38, v192
	v_mul_f32_e32 v193, v38, v193
	v_mul_f32_e32 v194, v38, v194
	v_mul_f32_e32 v195, v38, v195
	ds_write_b128 v210, v[192:195] offset:4096
	v_mul_f32_e32 v196, v39, v196
	v_mul_f32_e32 v197, v39, v197
	v_mul_f32_e32 v198, v39, v198
	v_mul_f32_e32 v199, v39, v199
	ds_write_b128 v210, v[196:199] offset:5120
	v_mul_f32_e32 v200, v40, v200
	v_mul_f32_e32 v201, v40, v201
	v_mul_f32_e32 v202, v40, v202
	v_mul_f32_e32 v203, v40, v203
	ds_write_b128 v210, v[200:203] offset:6144
	v_mul_f32_e32 v204, v41, v204
	v_mul_f32_e32 v205, v41, v205
	v_mul_f32_e32 v206, v41, v206
	v_mul_f32_e32 v207, v41, v207
	ds_write_b128 v210, v[204:207] offset:7168
	s_waitcnt lgkmcnt(0)
	s_barrier
; #define GAS __attribute__((address_space(1)))
; #define LAS __attribute__((address_space(3)))
; #define LDS_WAIT() asm volatile("s_waitcnt lgkmcnt(0)" ::: "memory")
;     const int pr = item >> 1, kb = 2 * (pr / nblk) + (item & 1), nb = pr % nblk, k0 = 64 * kb, n0 = 32 * nb;
;     const int nr = n0 + (lane & 31); const int sc = MAP == 1 ? src_col_in(nr) : nr;
;     float v[32];
; #pragma unroll
;     for (int i = 0; i < 32; ++i) v[i] = sc >= 0 ? W[(size_t)(k0 + 2 * i + (lane >> 5)) * Nsrc + sc] : 0.f;
; #pragma unroll
;     for (int i = 0; i < 32; ++i) { const int k = k0 + 2 * i + (lane >> 5); float x = v[i] * wscale; if (KS) x *= (k < ksplit ? ksA[k] : ksB[k - ksplit]); scr[(2 * i + (lane >> 5)) * 33 + (lane & 31)] = x; }
;     LDS_WAIT(); asm volatile("" ::: "memory");
;     const int c = lane & 7;
; #pragma unroll
;     for (int j = 0; j < 4; ++j) { const int n = (lane >> 3) + 8 * j; const LAS float* s = scr + (8 * c) * 33 + n;
;         const unsigned long long o = (unsigned long long)pg8::pk4_fp8(s[0 * 33], s[1 * 33], s[2 * 33], s[3 * 33]) | ((unsigned long long)pg8::pk4_fp8(s[4 * 33], s[5 * 33], s[6 * 33], s[7 * 33]) << 32);
;         *(GAS unsigned long long*)(WT + (size_t)(n0 + n) * K + k0 + 8 * c) = o; }
;     LDS_WAIT(); asm volatile("" ::: "memory");
; }
; __global__ void __launch_bounds__(NWAVES * 64, 2) hybrid_fwd(Args args) {
;     ...
;             if (r < I_UP) { p0_transpose_item_f8<true>(args.in[15] + (size_t)l * DM * FF, DM, FF, FF / 32, (unsigned char*)(ws + WS_WUP + l * SZ_WUP), WUP8_SCALE, args.in[14] + l * DM, args.in[14] + l * DM, DM, scr, r, lane); continue; } r -= I_UP;
	s_add_u32 s8, s34, 0xb000
	s_addc_u32 s9, s35, 0
	global_load_dwordx4 v[176:179], v74, s[8:9]
	s_add_u32 s8, s8, 0x20000
	s_addc_u32 s9, s9, 0
	global_load_dwordx4 v[180:183], v74, s[8:9]
	s_add_u32 s8, s8, 0x20000
	s_addc_u32 s9, s9, 0
	global_load_dwordx4 v[184:187], v74, s[8:9]
	s_add_u32 s8, s8, 0x20000
	s_addc_u32 s9, s9, 0
	global_load_dwordx4 v[188:191], v74, s[8:9]
	s_add_u32 s8, s8, 0x20000
	s_addc_u32 s9, s9, 0
	global_load_dwordx4 v[192:195], v74, s[8:9]
	s_add_u32 s8, s8, 0x20000
	s_addc_u32 s9, s9, 0
	global_load_dwordx4 v[196:199], v74, s[8:9]
	s_add_u32 s8, s8, 0x20000
	s_addc_u32 s9, s9, 0
	global_load_dwordx4 v[200:203], v74, s[8:9]
	s_add_u32 s8, s8, 0x20000
	s_addc_u32 s9, s9, 0
	global_load_dwordx4 v[204:207], v74, s[8:9]
	s_add_u32 s6, s36, 0x2400000
	s_addc_u32 s7, s37, 0
	ds_read_b32 v226, v212
	ds_read_b32 v227, v212 offset:512
	ds_read_b32 v228, v212 offset:1024
	ds_read_b32 v229, v212 offset:1536
	ds_read_b32 v230, v212 offset:2048
	ds_read_b32 v231, v212 offset:2560
	ds_read_b32 v232, v212 offset:3072
	ds_read_b32 v233, v212 offset:3584
	ds_read_b32 v234, v212 offset:4096
	ds_read_b32 v235, v212 offset:4608
	ds_read_b32 v236, v212 offset:5120
	ds_read_b32 v237, v212 offset:5632
	ds_read_b32 v238, v212 offset:6144
	ds_read_b32 v239, v212 offset:6656
	ds_read_b32 v240, v212 offset:7168
	ds_read_b32 v241, v212 offset:7680
	s_waitcnt lgkmcnt(0)
	v_max_f32_e32 v226, v226, v226
	v_max_f32_e32 v227, v227, v227
	v_max_f32_e32 v228, v228, v228
	v_max_f32_e32 v229, v229, v229
	v_max_f32_e32 v230, v230, v230
	v_max_f32_e32 v231, v231, v231
	v_max_f32_e32 v232, v232, v232
	v_max_f32_e32 v233, v233, v233
	v_max_f32_e32 v234, v234, v234
	v_max_f32_e32 v235, v235, v235
	v_max_f32_e32 v236, v236, v236
	v_max_f32_e32 v237, v237, v237
	v_max_f32_e32 v238, v238, v238
	v_max_f32_e32 v239, v239, v239
	v_max_f32_e32 v240, v240, v240
	v_max_f32_e32 v241, v241, v241
	v_med3_f32 v226, v226, s62, v95
	v_med3_f32 v227, v227, s62, v95
	v_med3_f32 v228, v228, s62, v95
	v_med3_f32 v229, v229, s62, v95
	v_med3_f32 v230, v230, s62, v95
	v_med3_f32 v231, v231, s62, v95
	v_med3_f32 v232, v232, s62, v95
	v_med3_f32 v233, v233, s62, v95
	v_med3_f32 v234, v234, s62, v95
	v_med3_f32 v235, v235, s62, v95
	v_med3_f32 v236, v236, s62, v95
	v_med3_f32 v237, v237, s62, v95
	v_med3_f32 v238, v238, s62, v95
	v_med3_f32 v239, v239, s62, v95
	v_med3_f32 v240, v240, s62, v95
	v_med3_f32 v241, v241, s62, v95
	v_mov_b32_e32 v242, 0
	v_mov_b32_e32 v243, 0
	v_mov_b32_e32 v244, 0
	v_mov_b32_e32 v245, 0
	v_cvt_pk_fp8_f32 v242, v226, v227
	v_cvt_pk_fp8_f32 v243, v230, v231
	v_cvt_pk_fp8_f32 v244, v234, v235
	v_cvt_pk_fp8_f32 v245, v238, v239
	v_cvt_pk_fp8_f32 v242, v228, v229 op_sel:[0,0,1]
	v_cvt_pk_fp8_f32 v243, v232, v233 op_sel:[0,0,1]
	v_cvt_pk_fp8_f32 v244, v236, v237 op_sel:[0,0,1]
	v_cvt_pk_fp8_f32 v245, v240, v241 op_sel:[0,0,1]
	s_nop 0
	global_store_dwordx4 v77, v[242:245], s[6:7]
	ds_read_b32 v226, v214
	ds_read_b32 v227, v214 offset:512
	ds_read_b32 v228, v214 offset:1024
	ds_read_b32 v229, v214 offset:1536
	ds_read_b32 v230, v214 offset:2048
	ds_read_b32 v231, v214 offset:2560
	ds_read_b32 v232, v214 offset:3072
	ds_read_b32 v233, v214 offset:3584
	ds_read_b32 v234, v214 offset:4096
	ds_read_b32 v235, v214 offset:4608
	ds_read_b32 v236, v214 offset:5120
	ds_read_b32 v237, v214 offset:5632
	ds_read_b32 v238, v214 offset:6144
	ds_read_b32 v239, v214 offset:6656
	ds_read_b32 v240, v214 offset:7168
	ds_read_b32 v241, v214 offset:7680
	s_waitcnt lgkmcnt(0)
	v_max_f32_e32 v226, v226, v226
	v_max_f32_e32 v227, v227, v227
	v_max_f32_e32 v228, v228, v228
	v_max_f32_e32 v229, v229, v229
	v_max_f32_e32 v230, v230, v230
	v_max_f32_e32 v231, v231, v231
	v_max_f32_e32 v232, v232, v232
	v_max_f32_e32 v233, v233, v233
	v_max_f32_e32 v234, v234, v234
	v_max_f32_e32 v235, v235, v235
	v_max_f32_e32 v236, v236, v236
	v_max_f32_e32 v237, v237, v237
	v_max_f32_e32 v238, v238, v238
	v_max_f32_e32 v239, v239, v239
	v_max_f32_e32 v240, v240, v240
	v_max_f32_e32 v241, v241, v241
	v_med3_f32 v226, v226, s62, v95
	v_med3_f32 v227, v227, s62, v95
	v_med3_f32 v228, v228, s62, v95
	v_med3_f32 v229, v229, s62, v95
	v_med3_f32 v230, v230, s62, v95
	v_med3_f32 v231, v231, s62, v95
	v_med3_f32 v232, v232, s62, v95
	v_med3_f32 v233, v233, s62, v95
	v_med3_f32 v234, v234, s62, v95
	v_med3_f32 v235, v235, s62, v95
	v_med3_f32 v236, v236, s62, v95
	v_med3_f32 v237, v237, s62, v95
	v_med3_f32 v238, v238, s62, v95
	v_med3_f32 v239, v239, s62, v95
	v_med3_f32 v240, v240, s62, v95
	v_med3_f32 v241, v241, s62, v95
	v_mov_b32_e32 v242, 0
	v_mov_b32_e32 v243, 0
	v_mov_b32_e32 v244, 0
	v_mov_b32_e32 v245, 0
	v_cvt_pk_fp8_f32 v242, v226, v227
	v_cvt_pk_fp8_f32 v243, v230, v231
	v_cvt_pk_fp8_f32 v244, v234, v235
	v_cvt_pk_fp8_f32 v245, v238, v239
	v_cvt_pk_fp8_f32 v242, v228, v229 op_sel:[0,0,1]
	v_cvt_pk_fp8_f32 v243, v232, v233 op_sel:[0,0,1]
	v_cvt_pk_fp8_f32 v244, v236, v237 op_sel:[0,0,1]
	v_cvt_pk_fp8_f32 v245, v240, v241 op_sel:[0,0,1]
	s_nop 0
	global_store_dwordx4 v78, v[242:245], s[6:7]
	s_waitcnt vmcnt(12)
	v_mul_f32_e32 v144, v34, v144
	v_mul_f32_e32 v145, v34, v145
	v_mul_f32_e32 v146, v34, v146
	v_mul_f32_e32 v147, v34, v147
	ds_write_b128 v209, v[144:147]
	v_mul_f32_e32 v148, v35, v148
	v_mul_f32_e32 v149, v35, v149
	v_mul_f32_e32 v150, v35, v150
	v_mul_f32_e32 v151, v35, v151
	ds_write_b128 v209, v[148:151] offset:1024
	v_mul_f32_e32 v152, v36, v152
	v_mul_f32_e32 v153, v36, v153
	v_mul_f32_e32 v154, v36, v154
	v_mul_f32_e32 v155, v36, v155
	ds_write_b128 v209, v[152:155] offset:2048
	v_mul_f32_e32 v156, v37, v156
	v_mul_f32_e32 v157, v37, v157
	v_mul_f32_e32 v158, v37, v158
	v_mul_f32_e32 v159, v37, v159
	ds_write_b128 v209, v[156:159] offset:3072
	v_mul_f32_e32 v160, v38, v160
	v_mul_f32_e32 v161, v38, v161
	v_mul_f32_e32 v162, v38, v162
	v_mul_f32_e32 v163, v38, v163
	ds_write_b128 v209, v[160:163] offset:4096
	v_mul_f32_e32 v164, v39, v164
	v_mul_f32_e32 v165, v39, v165
	v_mul_f32_e32 v166, v39, v166
	v_mul_f32_e32 v167, v39, v167
	ds_write_b128 v209, v[164:167] offset:5120
	v_mul_f32_e32 v168, v40, v168
	v_mul_f32_e32 v169, v40, v169
	v_mul_f32_e32 v170, v40, v170
	v_mul_f32_e32 v171, v40, v171
	ds_write_b128 v209, v[168:171] offset:6144
	v_mul_f32_e32 v172, v41, v172
	v_mul_f32_e32 v173, v41, v173
	v_mul_f32_e32 v174, v41, v174
	v_mul_f32_e32 v175, v41, v175
	ds_write_b128 v209, v[172:175] offset:7168
	s_waitcnt lgkmcnt(0)
	s_barrier
; #define GAS __attribute__((address_space(1)))
; #define LAS __attribute__((address_space(3)))
; #define LDS_WAIT() asm volatile("s_waitcnt lgkmcnt(0)" ::: "memory")
;     const int pr = item >> 1, kb = 2 * (pr / nblk) + (item & 1), nb = pr % nblk, k0 = 64 * kb, n0 = 32 * nb;
;     const int nr = n0 + (lane & 31); const int sc = MAP == 1 ? src_col_in(nr) : nr;
;     float v[32];
; #pragma unroll
;     for (int i = 0; i < 32; ++i) v[i] = sc >= 0 ? W[(size_t)(k0 + 2 * i + (lane >> 5)) * Nsrc + sc] : 0.f;
; #pragma unroll
;     for (int i = 0; i < 32; ++i) { const int k = k0 + 2 * i + (lane >> 5); float x = v[i] * wscale; if (KS) x *= (k < ksplit ? ksA[k] : ksB[k - ksplit]); scr[(2 * i + (lane >> 5)) * 33 + (lane & 31)] = x; }
;     LDS_WAIT(); asm volatile("" ::: "memory");
;     const int c = lane & 7;
; #pragma unroll
;     for (int j = 0; j < 4; ++j) { const int n = (lane >> 3) + 8 * j; const LAS float* s = scr + (8 * c) * 33 + n;
;         const unsigned long long o = (unsigned long long)pg8::pk4_fp8(s[0 * 33], s[1 * 33], s[2 * 33], s[3 * 33]) | ((unsigned long long)pg8::pk4_fp8(s[4 * 33], s[5 * 33], s[6 * 33], s[7 * 33]) << 32);
;         *(GAS unsigned long long*)(WT + (size_t)(n0 + n) * K + k0 + 8 * c) = o; }
;     LDS_WAIT(); asm volatile("" ::: "memory");
; }
; __global__ void __launch_bounds__(NWAVES * 64, 2) hybrid_fwd(Args args) {
;     ...
;             if (r < I_UP) { p0_transpose_item_f8<true>(args.in[15] + (size_t)l * DM * FF, DM, FF, FF / 32, (unsigned char*)(ws + WS_WUP + l * SZ_WUP), WUP8_SCALE, args.in[14] + l * DM, args.in[14] + l * DM, DM, scr, r, lane); continue; } r -= I_UP;
	s_add_u32 s8, s34, 0xc000
	s_addc_u32 s9, s35, 0
	global_load_dwordx4 v[144:147], v74, s[8:9]
	s_add_u32 s8, s8, 0x20000
	s_addc_u32 s9, s9, 0
	global_load_dwordx4 v[148:151], v74, s[8:9]
	s_add_u32 s8, s8, 0x20000
	s_addc_u32 s9, s9, 0
	global_load_dwordx4 v[152:155], v74, s[8:9]
	s_add_u32 s8, s8, 0x20000
	s_addc_u32 s9, s9, 0
	global_load_dwordx4 v[156:159], v74, s[8:9]
	s_add_u32 s8, s8, 0x20000
	s_addc_u32 s9, s9, 0
	global_load_dwordx4 v[160:163], v74, s[8:9]
	s_add_u32 s8, s8, 0x20000
	s_addc_u32 s9, s9, 0
	global_load_dwordx4 v[164:167], v74, s[8:9]
	s_add_u32 s8, s8, 0x20000
	s_addc_u32 s9, s9, 0
	global_load_dwordx4 v[168:171], v74, s[8:9]
	s_add_u32 s8, s8, 0x20000
	s_addc_u32 s9, s9, 0
	global_load_dwordx4 v[172:175], v74, s[8:9]
	s_add_u32 s6, s36, 0x2800000
	s_addc_u32 s7, s37, 0
	ds_read_b32 v226, v211
	ds_read_b32 v227, v211 offset:512
	ds_read_b32 v228, v211 offset:1024
	ds_read_b32 v229, v211 offset:1536
	ds_read_b32 v230, v211 offset:2048
	ds_read_b32 v231, v211 offset:2560
	ds_read_b32 v232, v211 offset:3072
	ds_read_b32 v233, v211 offset:3584
	ds_read_b32 v234, v211 offset:4096
	ds_read_b32 v235, v211 offset:4608
	ds_read_b32 v236, v211 offset:5120
	ds_read_b32 v237, v211 offset:5632
	ds_read_b32 v238, v211 offset:6144
	ds_read_b32 v239, v211 offset:6656
	ds_read_b32 v240, v211 offset:7168
	ds_read_b32 v241, v211 offset:7680
	s_waitcnt lgkmcnt(0)
	v_max_f32_e32 v226, v226, v226
	v_max_f32_e32 v227, v227, v227
	v_max_f32_e32 v228, v228, v228
	v_max_f32_e32 v229, v229, v229
	v_max_f32_e32 v230, v230, v230
	v_max_f32_e32 v231, v231, v231
	v_max_f32_e32 v232, v232, v232
	v_max_f32_e32 v233, v233, v233
	v_max_f32_e32 v234, v234, v234
	v_max_f32_e32 v235, v235, v235
	v_max_f32_e32 v236, v236, v236
	v_max_f32_e32 v237, v237, v237
	v_max_f32_e32 v238, v238, v238
	v_max_f32_e32 v239, v239, v239
	v_max_f32_e32 v240, v240, v240
	v_max_f32_e32 v241, v241, v241
	v_med3_f32 v226, v226, s62, v95
	v_med3_f32 v227, v227, s62, v95
	v_med3_f32 v228, v228, s62, v95
	v_med3_f32 v229, v229, s62, v95
	v_med3_f32 v230, v230, s62, v95
	v_med3_f32 v231, v231, s62, v95
	v_med3_f32 v232, v232, s62, v95
	v_med3_f32 v233, v233, s62, v95
	v_med3_f32 v234, v234, s62, v95
	v_med3_f32 v235, v235, s62, v95
	v_med3_f32 v236, v236, s62, v95
	v_med3_f32 v237, v237, s62, v95
	v_med3_f32 v238, v238, s62, v95
	v_med3_f32 v239, v239, s62, v95
	v_med3_f32 v240, v240, s62, v95
	v_med3_f32 v241, v241, s62, v95
	v_mov_b32_e32 v242, 0
	v_mov_b32_e32 v243, 0
	v_mov_b32_e32 v244, 0
	v_mov_b32_e32 v245, 0
	v_cvt_pk_fp8_f32 v242, v226, v227
	v_cvt_pk_fp8_f32 v243, v230, v231
	v_cvt_pk_fp8_f32 v244, v234, v235
	v_cvt_pk_fp8_f32 v245, v238, v239
	v_cvt_pk_fp8_f32 v242, v228, v229 op_sel:[0,0,1]
	v_cvt_pk_fp8_f32 v243, v232, v233 op_sel:[0,0,1]
	v_cvt_pk_fp8_f32 v244, v236, v237 op_sel:[0,0,1]
	v_cvt_pk_fp8_f32 v245, v240, v241 op_sel:[0,0,1]
	s_nop 0
	global_store_dwordx4 v77, v[242:245], s[6:7]
	ds_read_b32 v226, v213
	ds_read_b32 v227, v213 offset:512
	ds_read_b32 v228, v213 offset:1024
	ds_read_b32 v229, v213 offset:1536
	ds_read_b32 v230, v213 offset:2048
	ds_read_b32 v231, v213 offset:2560
	ds_read_b32 v232, v213 offset:3072
	ds_read_b32 v233, v213 offset:3584
	ds_read_b32 v234, v213 offset:4096
	ds_read_b32 v235, v213 offset:4608
	ds_read_b32 v236, v213 offset:5120
	ds_read_b32 v237, v213 offset:5632
	ds_read_b32 v238, v213 offset:6144
	ds_read_b32 v239, v213 offset:6656
	ds_read_b32 v240, v213 offset:7168
	ds_read_b32 v241, v213 offset:7680
	s_waitcnt lgkmcnt(0)
	v_max_f32_e32 v226, v226, v226
	v_max_f32_e32 v227, v227, v227
	v_max_f32_e32 v228, v228, v228
	v_max_f32_e32 v229, v229, v229
	v_max_f32_e32 v230, v230, v230
	v_max_f32_e32 v231, v231, v231
	v_max_f32_e32 v232, v232, v232
	v_max_f32_e32 v233, v233, v233
	v_max_f32_e32 v234, v234, v234
	v_max_f32_e32 v235, v235, v235
	v_max_f32_e32 v236, v236, v236
	v_max_f32_e32 v237, v237, v237
	v_max_f32_e32 v238, v238, v238
	v_max_f32_e32 v239, v239, v239
	v_max_f32_e32 v240, v240, v240
	v_max_f32_e32 v241, v241, v241
	v_med3_f32 v226, v226, s62, v95
	v_med3_f32 v227, v227, s62, v95
	v_med3_f32 v228, v228, s62, v95
	v_med3_f32 v229, v229, s62, v95
	v_med3_f32 v230, v230, s62, v95
	v_med3_f32 v231, v231, s62, v95
	v_med3_f32 v232, v232, s62, v95
	v_med3_f32 v233, v233, s62, v95
	v_med3_f32 v234, v234, s62, v95
	v_med3_f32 v235, v235, s62, v95
	v_med3_f32 v236, v236, s62, v95
	v_med3_f32 v237, v237, s62, v95
	v_med3_f32 v238, v238, s62, v95
	v_med3_f32 v239, v239, s62, v95
	v_med3_f32 v240, v240, s62, v95
	v_med3_f32 v241, v241, s62, v95
	v_mov_b32_e32 v242, 0
	v_mov_b32_e32 v243, 0
	v_mov_b32_e32 v244, 0
	v_mov_b32_e32 v245, 0
	v_cvt_pk_fp8_f32 v242, v226, v227
	v_cvt_pk_fp8_f32 v243, v230, v231
	v_cvt_pk_fp8_f32 v244, v234, v235
	v_cvt_pk_fp8_f32 v245, v238, v239
	v_cvt_pk_fp8_f32 v242, v228, v229 op_sel:[0,0,1]
	v_cvt_pk_fp8_f32 v243, v232, v233 op_sel:[0,0,1]
	v_cvt_pk_fp8_f32 v244, v236, v237 op_sel:[0,0,1]
	v_cvt_pk_fp8_f32 v245, v240, v241 op_sel:[0,0,1]
	s_nop 0
	global_store_dwordx4 v78, v[242:245], s[6:7]
	s_waitcnt vmcnt(12)
	v_mul_f32_e32 v176, v34, v176
	v_mul_f32_e32 v177, v34, v177
	v_mul_f32_e32 v178, v34, v178
	v_mul_f32_e32 v179, v34, v179
	ds_write_b128 v210, v[176:179]
	v_mul_f32_e32 v180, v35, v180
	v_mul_f32_e32 v181, v35, v181
	v_mul_f32_e32 v182, v35, v182
	v_mul_f32_e32 v183, v35, v183
	ds_write_b128 v210, v[180:183] offset:1024
	v_mul_f32_e32 v184, v36, v184
	v_mul_f32_e32 v185, v36, v185
	v_mul_f32_e32 v186, v36, v186
	v_mul_f32_e32 v187, v36, v187
	ds_write_b128 v210, v[184:187] offset:2048
	v_mul_f32_e32 v188, v37, v188
	v_mul_f32_e32 v189, v37, v189
	v_mul_f32_e32 v190, v37, v190
	v_mul_f32_e32 v191, v37, v191
	ds_write_b128 v210, v[188:191] offset:3072
	v_mul_f32_e32 v192, v38, v192
	v_mul_f32_e32 v193, v38, v193
	v_mul_f32_e32 v194, v38, v194
	v_mul_f32_e32 v195, v38, v195
	ds_write_b128 v210, v[192:195] offset:4096
	v_mul_f32_e32 v196, v39, v196
	v_mul_f32_e32 v197, v39, v197
	v_mul_f32_e32 v198, v39, v198
	v_mul_f32_e32 v199, v39, v199
	ds_write_b128 v210, v[196:199] offset:5120
	v_mul_f32_e32 v200, v40, v200
	v_mul_f32_e32 v201, v40, v201
	v_mul_f32_e32 v202, v40, v202
	v_mul_f32_e32 v203, v40, v203
	ds_write_b128 v210, v[200:203] offset:6144
	v_mul_f32_e32 v204, v41, v204
	v_mul_f32_e32 v205, v41, v205
	v_mul_f32_e32 v206, v41, v206
	v_mul_f32_e32 v207, v41, v207
	ds_write_b128 v210, v[204:207] offset:7168
	s_waitcnt lgkmcnt(0)
	s_barrier
; #define GAS __attribute__((address_space(1)))
; #define LAS __attribute__((address_space(3)))
; #define LDS_WAIT() asm volatile("s_waitcnt lgkmcnt(0)" ::: "memory")
;     const int pr = item >> 1, kb = 2 * (pr / nblk) + (item & 1), nb = pr % nblk, k0 = 64 * kb, n0 = 32 * nb;
;     const int nr = n0 + (lane & 31); const int sc = MAP == 1 ? src_col_in(nr) : nr;
;     float v[32];
; #pragma unroll
;     for (int i = 0; i < 32; ++i) v[i] = sc >= 0 ? W[(size_t)(k0 + 2 * i + (lane >> 5)) * Nsrc + sc] : 0.f;
; #pragma unroll
;     for (int i = 0; i < 32; ++i) { const int k = k0 + 2 * i + (lane >> 5); float x = v[i] * wscale; if (KS) x *= (k < ksplit ? ksA[k] : ksB[k - ksplit]); scr[(2 * i + (lane >> 5)) * 33 + (lane & 31)] = x; }
;     LDS_WAIT(); asm volatile("" ::: "memory");
;     const int c = lane & 7;
; #pragma unroll
;     for (int j = 0; j < 4; ++j) { const int n = (lane >> 3) + 8 * j; const LAS float* s = scr + (8 * c) * 33 + n;
;         const unsigned long long o = (unsigned long long)pg8::pk4_fp8(s[0 * 33], s[1 * 33], s[2 * 33], s[3 * 33]) | ((unsigned long long)pg8::pk4_fp8(s[4 * 33], s[5 * 33], s[6 * 33], s[7 * 33]) << 32);
;         *(GAS unsigned long long*)(WT + (size_t)(n0 + n) * K + k0 + 8 * c) = o; }
;     LDS_WAIT(); asm volatile("" ::: "memory");
; }
; __global__ void __launch_bounds__(NWAVES * 64, 2) hybrid_fwd(Args args) {
;     ...
;             if (r < I_UP) { p0_transpose_item_f8<true>(args.in[15] + (size_t)l * DM * FF, DM, FF, FF / 32, (unsigned char*)(ws + WS_WUP + l * SZ_WUP), WUP8_SCALE, args.in[14] + l * DM, args.in[14] + l * DM, DM, scr, r, lane); continue; } r -= I_UP;
	s_add_u32 s8, s34, 0xd000
	s_addc_u32 s9, s35, 0
	global_load_dwordx4 v[176:179], v74, s[8:9]
	s_add_u32 s8, s8, 0x20000
	s_addc_u32 s9, s9, 0
	global_load_dwordx4 v[180:183], v74, s[8:9]
	s_add_u32 s8, s8, 0x20000
	s_addc_u32 s9, s9, 0
	global_load_dwordx4 v[184:187], v74, s[8:9]
	s_add_u32 s8, s8, 0x20000
	s_addc_u32 s9, s9, 0
	global_load_dwordx4 v[188:191], v74, s[8:9]
	s_add_u32 s8, s8, 0x20000
	s_addc_u32 s9, s9, 0
	global_load_dwordx4 v[192:195], v74, s[8:9]
	s_add_u32 s8, s8, 0x20000
	s_addc_u32 s9, s9, 0
	global_load_dwordx4 v[196:199], v74, s[8:9]
	s_add_u32 s8, s8, 0x20000
	s_addc_u32 s9, s9, 0
	global_load_dwordx4 v[200:203], v74, s[8:9]
	s_add_u32 s8, s8, 0x20000
	s_addc_u32 s9, s9, 0
	global_load_dwordx4 v[204:207], v74, s[8:9]
	s_add_u32 s6, s36, 0x2c00000
	s_addc_u32 s7, s37, 0
	ds_read_b32 v226, v212
	ds_read_b32 v227, v212 offset:512
	ds_read_b32 v228, v212 offset:1024
	ds_read_b32 v229, v212 offset:1536
	ds_read_b32 v230, v212 offset:2048
	ds_read_b32 v231, v212 offset:2560
	ds_read_b32 v232, v212 offset:3072
	ds_read_b32 v233, v212 offset:3584
	ds_read_b32 v234, v212 offset:4096
	ds_read_b32 v235, v212 offset:4608
	ds_read_b32 v236, v212 offset:5120
	ds_read_b32 v237, v212 offset:5632
	ds_read_b32 v238, v212 offset:6144
	ds_read_b32 v239, v212 offset:6656
	ds_read_b32 v240, v212 offset:7168
	ds_read_b32 v241, v212 offset:7680
	s_waitcnt lgkmcnt(0)
	v_max_f32_e32 v226, v226, v226
	v_max_f32_e32 v227, v227, v227
	v_max_f32_e32 v228, v228, v228
	v_max_f32_e32 v229, v229, v229
	v_max_f32_e32 v230, v230, v230
	v_max_f32_e32 v231, v231, v231
	v_max_f32_e32 v232, v232, v232
	v_max_f32_e32 v233, v233, v233
	v_max_f32_e32 v234, v234, v234
	v_max_f32_e32 v235, v235, v235
	v_max_f32_e32 v236, v236, v236
	v_max_f32_e32 v237, v237, v237
	v_max_f32_e32 v238, v238, v238
	v_max_f32_e32 v239, v239, v239
	v_max_f32_e32 v240, v240, v240
	v_max_f32_e32 v241, v241, v241
	v_med3_f32 v226, v226, s62, v95
	v_med3_f32 v227, v227, s62, v95
	v_med3_f32 v228, v228, s62, v95
	v_med3_f32 v229, v229, s62, v95
	v_med3_f32 v230, v230, s62, v95
	v_med3_f32 v231, v231, s62, v95
	v_med3_f32 v232, v232, s62, v95
	v_med3_f32 v233, v233, s62, v95
	v_med3_f32 v234, v234, s62, v95
	v_med3_f32 v235, v235, s62, v95
	v_med3_f32 v236, v236, s62, v95
	v_med3_f32 v237, v237, s62, v95
	v_med3_f32 v238, v238, s62, v95
	v_med3_f32 v239, v239, s62, v95
	v_med3_f32 v240, v240, s62, v95
	v_med3_f32 v241, v241, s62, v95
	v_mov_b32_e32 v242, 0
	v_mov_b32_e32 v243, 0
	v_mov_b32_e32 v244, 0
	v_mov_b32_e32 v245, 0
	v_cvt_pk_fp8_f32 v242, v226, v227
	v_cvt_pk_fp8_f32 v243, v230, v231
	v_cvt_pk_fp8_f32 v244, v234, v235
	v_cvt_pk_fp8_f32 v245, v238, v239
	v_cvt_pk_fp8_f32 v242, v228, v229 op_sel:[0,0,1]
	v_cvt_pk_fp8_f32 v243, v232, v233 op_sel:[0,0,1]
	v_cvt_pk_fp8_f32 v244, v236, v237 op_sel:[0,0,1]
	v_cvt_pk_fp8_f32 v245, v240, v241 op_sel:[0,0,1]
	s_nop 0
	global_store_dwordx4 v77, v[242:245], s[6:7]
	ds_read_b32 v226, v214
	ds_read_b32 v227, v214 offset:512
	ds_read_b32 v228, v214 offset:1024
	ds_read_b32 v229, v214 offset:1536
	ds_read_b32 v230, v214 offset:2048
	ds_read_b32 v231, v214 offset:2560
	ds_read_b32 v232, v214 offset:3072
	ds_read_b32 v233, v214 offset:3584
	ds_read_b32 v234, v214 offset:4096
	ds_read_b32 v235, v214 offset:4608
	ds_read_b32 v236, v214 offset:5120
	ds_read_b32 v237, v214 offset:5632
	ds_read_b32 v238, v214 offset:6144
	ds_read_b32 v239, v214 offset:6656
	ds_read_b32 v240, v214 offset:7168
	ds_read_b32 v241, v214 offset:7680
	s_waitcnt lgkmcnt(0)
	v_max_f32_e32 v226, v226, v226
	v_max_f32_e32 v227, v227, v227
	v_max_f32_e32 v228, v228, v228
	v_max_f32_e32 v229, v229, v229
	v_max_f32_e32 v230, v230, v230
	v_max_f32_e32 v231, v231, v231
	v_max_f32_e32 v232, v232, v232
	v_max_f32_e32 v233, v233, v233
	v_max_f32_e32 v234, v234, v234
	v_max_f32_e32 v235, v235, v235
	v_max_f32_e32 v236, v236, v236
	v_max_f32_e32 v237, v237, v237
	v_max_f32_e32 v238, v238, v238
	v_max_f32_e32 v239, v239, v239
	v_max_f32_e32 v240, v240, v240
	v_max_f32_e32 v241, v241, v241
	v_med3_f32 v226, v226, s62, v95
	v_med3_f32 v227, v227, s62, v95
	v_med3_f32 v228, v228, s62, v95
	v_med3_f32 v229, v229, s62, v95
	v_med3_f32 v230, v230, s62, v95
	v_med3_f32 v231, v231, s62, v95
	v_med3_f32 v232, v232, s62, v95
	v_med3_f32 v233, v233, s62, v95
	v_med3_f32 v234, v234, s62, v95
	v_med3_f32 v235, v235, s62, v95
	v_med3_f32 v236, v236, s62, v95
	v_med3_f32 v237, v237, s62, v95
	v_med3_f32 v238, v238, s62, v95
	v_med3_f32 v239, v239, s62, v95
	v_med3_f32 v240, v240, s62, v95
	v_med3_f32 v241, v241, s62, v95
	v_mov_b32_e32 v242, 0
	v_mov_b32_e32 v243, 0
	v_mov_b32_e32 v244, 0
	v_mov_b32_e32 v245, 0
	v_cvt_pk_fp8_f32 v242, v226, v227
	v_cvt_pk_fp8_f32 v243, v230, v231
	v_cvt_pk_fp8_f32 v244, v234, v235
	v_cvt_pk_fp8_f32 v245, v238, v239
	v_cvt_pk_fp8_f32 v242, v228, v229 op_sel:[0,0,1]
	v_cvt_pk_fp8_f32 v243, v232, v233 op_sel:[0,0,1]
	v_cvt_pk_fp8_f32 v244, v236, v237 op_sel:[0,0,1]
	v_cvt_pk_fp8_f32 v245, v240, v241 op_sel:[0,0,1]
	s_nop 0
	global_store_dwordx4 v78, v[242:245], s[6:7]
	s_waitcnt vmcnt(12)
	v_mul_f32_e32 v144, v34, v144
	v_mul_f32_e32 v145, v34, v145
	v_mul_f32_e32 v146, v34, v146
	v_mul_f32_e32 v147, v34, v147
	ds_write_b128 v209, v[144:147]
	v_mul_f32_e32 v148, v35, v148
	v_mul_f32_e32 v149, v35, v149
	v_mul_f32_e32 v150, v35, v150
	v_mul_f32_e32 v151, v35, v151
	ds_write_b128 v209, v[148:151] offset:1024
	v_mul_f32_e32 v152, v36, v152
	v_mul_f32_e32 v153, v36, v153
	v_mul_f32_e32 v154, v36, v154
	v_mul_f32_e32 v155, v36, v155
	ds_write_b128 v209, v[152:155] offset:2048
	v_mul_f32_e32 v156, v37, v156
	v_mul_f32_e32 v157, v37, v157
	v_mul_f32_e32 v158, v37, v158
	v_mul_f32_e32 v159, v37, v159
	ds_write_b128 v209, v[156:159] offset:3072
	v_mul_f32_e32 v160, v38, v160
	v_mul_f32_e32 v161, v38, v161
	v_mul_f32_e32 v162, v38, v162
	v_mul_f32_e32 v163, v38, v163
	ds_write_b128 v209, v[160:163] offset:4096
	v_mul_f32_e32 v164, v39, v164
	v_mul_f32_e32 v165, v39, v165
	v_mul_f32_e32 v166, v39, v166
	v_mul_f32_e32 v167, v39, v167
	ds_write_b128 v209, v[164:167] offset:5120
	v_mul_f32_e32 v168, v40, v168
	v_mul_f32_e32 v169, v40, v169
	v_mul_f32_e32 v170, v40, v170
	v_mul_f32_e32 v171, v40, v171
	ds_write_b128 v209, v[168:171] offset:6144
	v_mul_f32_e32 v172, v41, v172
	v_mul_f32_e32 v173, v41, v173
	v_mul_f32_e32 v174, v41, v174
	v_mul_f32_e32 v175, v41, v175
	ds_write_b128 v209, v[172:175] offset:7168
	s_waitcnt lgkmcnt(0)
	s_barrier
; #define GAS __attribute__((address_space(1)))
; #define LAS __attribute__((address_space(3)))
; #define LDS_WAIT() asm volatile("s_waitcnt lgkmcnt(0)" ::: "memory")
;     const int pr = item >> 1, kb = 2 * (pr / nblk) + (item & 1), nb = pr % nblk, k0 = 64 * kb, n0 = 32 * nb;
;     const int nr = n0 + (lane & 31); const int sc = MAP == 1 ? src_col_in(nr) : nr;
;     float v[32];
; #pragma unroll
;     for (int i = 0; i < 32; ++i) v[i] = sc >= 0 ? W[(size_t)(k0 + 2 * i + (lane >> 5)) * Nsrc + sc] : 0.f;
; #pragma unroll
;     for (int i = 0; i < 32; ++i) { const int k = k0 + 2 * i + (lane >> 5); float x = v[i] * wscale; if (KS) x *= (k < ksplit ? ksA[k] : ksB[k - ksplit]); scr[(2 * i + (lane >> 5)) * 33 + (lane & 31)] = x; }
;     LDS_WAIT(); asm volatile("" ::: "memory");
;     const int c = lane & 7;
; #pragma unroll
;     for (int j = 0; j < 4; ++j) { const int n = (lane >> 3) + 8 * j; const LAS float* s = scr + (8 * c) * 33 + n;
;         const unsigned long long o = (unsigned long long)pg8::pk4_fp8(s[0 * 33], s[1 * 33], s[2 * 33], s[3 * 33]) | ((unsigned long long)pg8::pk4_fp8(s[4 * 33], s[5 * 33], s[6 * 33], s[7 * 33]) << 32);
;         *(GAS unsigned long long*)(WT + (size_t)(n0 + n) * K + k0 + 8 * c) = o; }
;     LDS_WAIT(); asm volatile("" ::: "memory");
; }
; __global__ void __launch_bounds__(NWAVES * 64, 2) hybrid_fwd(Args args) {
;     ...
;             if (r < I_UP) { p0_transpose_item_f8<true>(args.in[15] + (size_t)l * DM * FF, DM, FF, FF / 32, (unsigned char*)(ws + WS_WUP + l * SZ_WUP), WUP8_SCALE, args.in[14] + l * DM, args.in[14] + l * DM, DM, scr, r, lane); continue; } r -= I_UP;
	s_add_u32 s8, s34, 0xe000
	s_addc_u32 s9, s35, 0
	global_load_dwordx4 v[144:147], v74, s[8:9]
	s_add_u32 s8, s8, 0x20000
	s_addc_u32 s9, s9, 0
	global_load_dwordx4 v[148:151], v74, s[8:9]
	s_add_u32 s8, s8, 0x20000
	s_addc_u32 s9, s9, 0
	global_load_dwordx4 v[152:155], v74, s[8:9]
	s_add_u32 s8, s8, 0x20000
	s_addc_u32 s9, s9, 0
	global_load_dwordx4 v[156:159], v74, s[8:9]
	s_add_u32 s8, s8, 0x20000
	s_addc_u32 s9, s9, 0
	global_load_dwordx4 v[160:163], v74, s[8:9]
	s_add_u32 s8, s8, 0x20000
	s_addc_u32 s9, s9, 0
	global_load_dwordx4 v[164:167], v74, s[8:9]
	s_add_u32 s8, s8, 0x20000
	s_addc_u32 s9, s9, 0
	global_load_dwordx4 v[168:171], v74, s[8:9]
	s_add_u32 s8, s8, 0x20000
	s_addc_u32 s9, s9, 0
	global_load_dwordx4 v[172:175], v74, s[8:9]
	s_add_u32 s6, s36, 0x3000000
	s_addc_u32 s7, s37, 0
	ds_read_b32 v226, v211
	ds_read_b32 v227, v211 offset:512
	ds_read_b32 v228, v211 offset:1024
	ds_read_b32 v229, v211 offset:1536
	ds_read_b32 v230, v211 offset:2048
	ds_read_b32 v231, v211 offset:2560
	ds_read_b32 v232, v211 offset:3072
	ds_read_b32 v233, v211 offset:3584
	ds_read_b32 v234, v211 offset:4096
	ds_read_b32 v235, v211 offset:4608
	ds_read_b32 v236, v211 offset:5120
	ds_read_b32 v237, v211 offset:5632
	ds_read_b32 v238, v211 offset:6144
	ds_read_b32 v239, v211 offset:6656
	ds_read_b32 v240, v211 offset:7168
	ds_read_b32 v241, v211 offset:7680
	s_waitcnt lgkmcnt(0)
	v_max_f32_e32 v226, v226, v226
	v_max_f32_e32 v227, v227, v227
	v_max_f32_e32 v228, v228, v228
	v_max_f32_e32 v229, v229, v229
	v_max_f32_e32 v230, v230, v230
	v_max_f32_e32 v231, v231, v231
	v_max_f32_e32 v232, v232, v232
	v_max_f32_e32 v233, v233, v233
	v_max_f32_e32 v234, v234, v234
	v_max_f32_e32 v235, v235, v235
	v_max_f32_e32 v236, v236, v236
	v_max_f32_e32 v237, v237, v237
	v_max_f32_e32 v238, v238, v238
	v_max_f32_e32 v239, v239, v239
	v_max_f32_e32 v240, v240, v240
	v_max_f32_e32 v241, v241, v241
	v_med3_f32 v226, v226, s62, v95
	v_med3_f32 v227, v227, s62, v95
	v_med3_f32 v228, v228, s62, v95
	v_med3_f32 v229, v229, s62, v95
	v_med3_f32 v230, v230, s62, v95
	v_med3_f32 v231, v231, s62, v95
	v_med3_f32 v232, v232, s62, v95
	v_med3_f32 v233, v233, s62, v95
	v_med3_f32 v234, v234, s62, v95
	v_med3_f32 v235, v235, s62, v95
	v_med3_f32 v236, v236, s62, v95
	v_med3_f32 v237, v237, s62, v95
	v_med3_f32 v238, v238, s62, v95
	v_med3_f32 v239, v239, s62, v95
	v_med3_f32 v240, v240, s62, v95
	v_med3_f32 v241, v241, s62, v95
	v_mov_b32_e32 v242, 0
	v_mov_b32_e32 v243, 0
	v_mov_b32_e32 v244, 0
	v_mov_b32_e32 v245, 0
	v_cvt_pk_fp8_f32 v242, v226, v227
	v_cvt_pk_fp8_f32 v243, v230, v231
	v_cvt_pk_fp8_f32 v244, v234, v235
	v_cvt_pk_fp8_f32 v245, v238, v239
	v_cvt_pk_fp8_f32 v242, v228, v229 op_sel:[0,0,1]
	v_cvt_pk_fp8_f32 v243, v232, v233 op_sel:[0,0,1]
	v_cvt_pk_fp8_f32 v244, v236, v237 op_sel:[0,0,1]
	v_cvt_pk_fp8_f32 v245, v240, v241 op_sel:[0,0,1]
	s_nop 0
	global_store_dwordx4 v77, v[242:245], s[6:7]
	ds_read_b32 v226, v213
	ds_read_b32 v227, v213 offset:512
	ds_read_b32 v228, v213 offset:1024
	ds_read_b32 v229, v213 offset:1536
	ds_read_b32 v230, v213 offset:2048
	ds_read_b32 v231, v213 offset:2560
	ds_read_b32 v232, v213 offset:3072
	ds_read_b32 v233, v213 offset:3584
	ds_read_b32 v234, v213 offset:4096
	ds_read_b32 v235, v213 offset:4608
	ds_read_b32 v236, v213 offset:5120
	ds_read_b32 v237, v213 offset:5632
	ds_read_b32 v238, v213 offset:6144
	ds_read_b32 v239, v213 offset:6656
	ds_read_b32 v240, v213 offset:7168
	ds_read_b32 v241, v213 offset:7680
	s_waitcnt lgkmcnt(0)
	v_max_f32_e32 v226, v226, v226
	v_max_f32_e32 v227, v227, v227
	v_max_f32_e32 v228, v228, v228
	v_max_f32_e32 v229, v229, v229
	v_max_f32_e32 v230, v230, v230
	v_max_f32_e32 v231, v231, v231
	v_max_f32_e32 v232, v232, v232
	v_max_f32_e32 v233, v233, v233
	v_max_f32_e32 v234, v234, v234
	v_max_f32_e32 v235, v235, v235
	v_max_f32_e32 v236, v236, v236
	v_max_f32_e32 v237, v237, v237
	v_max_f32_e32 v238, v238, v238
	v_max_f32_e32 v239, v239, v239
	v_max_f32_e32 v240, v240, v240
	v_max_f32_e32 v241, v241, v241
	v_med3_f32 v226, v226, s62, v95
	v_med3_f32 v227, v227, s62, v95
	v_med3_f32 v228, v228, s62, v95
	v_med3_f32 v229, v229, s62, v95
	v_med3_f32 v230, v230, s62, v95
	v_med3_f32 v231, v231, s62, v95
	v_med3_f32 v232, v232, s62, v95
	v_med3_f32 v233, v233, s62, v95
	v_med3_f32 v234, v234, s62, v95
	v_med3_f32 v235, v235, s62, v95
	v_med3_f32 v236, v236, s62, v95
	v_med3_f32 v237, v237, s62, v95
	v_med3_f32 v238, v238, s62, v95
	v_med3_f32 v239, v239, s62, v95
	v_med3_f32 v240, v240, s62, v95
	v_med3_f32 v241, v241, s62, v95
	v_mov_b32_e32 v242, 0
	v_mov_b32_e32 v243, 0
	v_mov_b32_e32 v244, 0
	v_mov_b32_e32 v245, 0
	v_cvt_pk_fp8_f32 v242, v226, v227
	v_cvt_pk_fp8_f32 v243, v230, v231
	v_cvt_pk_fp8_f32 v244, v234, v235
	v_cvt_pk_fp8_f32 v245, v238, v239
	v_cvt_pk_fp8_f32 v242, v228, v229 op_sel:[0,0,1]
	v_cvt_pk_fp8_f32 v243, v232, v233 op_sel:[0,0,1]
	v_cvt_pk_fp8_f32 v244, v236, v237 op_sel:[0,0,1]
	v_cvt_pk_fp8_f32 v245, v240, v241 op_sel:[0,0,1]
	s_nop 0
	global_store_dwordx4 v78, v[242:245], s[6:7]
	s_waitcnt vmcnt(12)
	v_mul_f32_e32 v176, v34, v176
	v_mul_f32_e32 v177, v34, v177
	v_mul_f32_e32 v178, v34, v178
	v_mul_f32_e32 v179, v34, v179
	ds_write_b128 v210, v[176:179]
	v_mul_f32_e32 v180, v35, v180
	v_mul_f32_e32 v181, v35, v181
	v_mul_f32_e32 v182, v35, v182
	v_mul_f32_e32 v183, v35, v183
	ds_write_b128 v210, v[180:183] offset:1024
	v_mul_f32_e32 v184, v36, v184
	v_mul_f32_e32 v185, v36, v185
	v_mul_f32_e32 v186, v36, v186
	v_mul_f32_e32 v187, v36, v187
	ds_write_b128 v210, v[184:187] offset:2048
	v_mul_f32_e32 v188, v37, v188
	v_mul_f32_e32 v189, v37, v189
	v_mul_f32_e32 v190, v37, v190
	v_mul_f32_e32 v191, v37, v191
	ds_write_b128 v210, v[188:191] offset:3072
	v_mul_f32_e32 v192, v38, v192
	v_mul_f32_e32 v193, v38, v193
	v_mul_f32_e32 v194, v38, v194
	v_mul_f32_e32 v195, v38, v195
	ds_write_b128 v210, v[192:195] offset:4096
	v_mul_f32_e32 v196, v39, v196
	v_mul_f32_e32 v197, v39, v197
	v_mul_f32_e32 v198, v39, v198
	v_mul_f32_e32 v199, v39, v199
	ds_write_b128 v210, v[196:199] offset:5120
	v_mul_f32_e32 v200, v40, v200
	v_mul_f32_e32 v201, v40, v201
	v_mul_f32_e32 v202, v40, v202
	v_mul_f32_e32 v203, v40, v203
	ds_write_b128 v210, v[200:203] offset:6144
	v_mul_f32_e32 v204, v41, v204
	v_mul_f32_e32 v205, v41, v205
	v_mul_f32_e32 v206, v41, v206
	v_mul_f32_e32 v207, v41, v207
	ds_write_b128 v210, v[204:207] offset:7168
	s_waitcnt lgkmcnt(0)
	s_barrier
; #define GAS __attribute__((address_space(1)))
; #define LAS __attribute__((address_space(3)))
; #define LDS_WAIT() asm volatile("s_waitcnt lgkmcnt(0)" ::: "memory")
;     const int pr = item >> 1, kb = 2 * (pr / nblk) + (item & 1), nb = pr % nblk, k0 = 64 * kb, n0 = 32 * nb;
;     const int nr = n0 + (lane & 31); const int sc = MAP == 1 ? src_col_in(nr) : nr;
;     float v[32];
; #pragma unroll
;     for (int i = 0; i < 32; ++i) v[i] = sc >= 0 ? W[(size_t)(k0 + 2 * i + (lane >> 5)) * Nsrc + sc] : 0.f;
; #pragma unroll
;     for (int i = 0; i < 32; ++i) { const int k = k0 + 2 * i + (lane >> 5); float x = v[i] * wscale; if (KS) x *= (k < ksplit ? ksA[k] : ksB[k - ksplit]); scr[(2 * i + (lane >> 5)) * 33 + (lane & 31)] = x; }
;     LDS_WAIT(); asm volatile("" ::: "memory");
;     const int c = lane & 7;
; #pragma unroll
;     for (int j = 0; j < 4; ++j) { const int n = (lane >> 3) + 8 * j; const LAS float* s = scr + (8 * c) * 33 + n;
;         const unsigned long long o = (unsigned long long)pg8::pk4_fp8(s[0 * 33], s[1 * 33], s[2 * 33], s[3 * 33]) | ((unsigned long long)pg8::pk4_fp8(s[4 * 33], s[5 * 33], s[6 * 33], s[7 * 33]) << 32);
;         *(GAS unsigned long long*)(WT + (size_t)(n0 + n) * K + k0 + 8 * c) = o; }
;     LDS_WAIT(); asm volatile("" ::: "memory");
; }
; __global__ void __launch_bounds__(NWAVES * 64, 2) hybrid_fwd(Args args) {
;     ...
;             if (r < I_UP) { p0_transpose_item_f8<true>(args.in[15] + (size_t)l * DM * FF, DM, FF, FF / 32, (unsigned char*)(ws + WS_WUP + l * SZ_WUP), WUP8_SCALE, args.in[14] + l * DM, args.in[14] + l * DM, DM, scr, r, lane); continue; } r -= I_UP;
	s_add_u32 s8, s34, 0xf000
	s_addc_u32 s9, s35, 0
	global_load_dwordx4 v[176:179], v74, s[8:9]
	s_add_u32 s8, s8, 0x20000
	s_addc_u32 s9, s9, 0
	global_load_dwordx4 v[180:183], v74, s[8:9]
	s_add_u32 s8, s8, 0x20000
	s_addc_u32 s9, s9, 0
	global_load_dwordx4 v[184:187], v74, s[8:9]
	s_add_u32 s8, s8, 0x20000
	s_addc_u32 s9, s9, 0
	global_load_dwordx4 v[188:191], v74, s[8:9]
	s_add_u32 s8, s8, 0x20000
	s_addc_u32 s9, s9, 0
	global_load_dwordx4 v[192:195], v74, s[8:9]
	s_add_u32 s8, s8, 0x20000
	s_addc_u32 s9, s9, 0
	global_load_dwordx4 v[196:199], v74, s[8:9]
	s_add_u32 s8, s8, 0x20000
	s_addc_u32 s9, s9, 0
	global_load_dwordx4 v[200:203], v74, s[8:9]
	s_add_u32 s8, s8, 0x20000
	s_addc_u32 s9, s9, 0
	global_load_dwordx4 v[204:207], v74, s[8:9]
	s_add_u32 s6, s36, 0x3400000
	s_addc_u32 s7, s37, 0
	ds_read_b32 v226, v212
	ds_read_b32 v227, v212 offset:512
	ds_read_b32 v228, v212 offset:1024
	ds_read_b32 v229, v212 offset:1536
	ds_read_b32 v230, v212 offset:2048
	ds_read_b32 v231, v212 offset:2560
	ds_read_b32 v232, v212 offset:3072
	ds_read_b32 v233, v212 offset:3584
	ds_read_b32 v234, v212 offset:4096
	ds_read_b32 v235, v212 offset:4608
	ds_read_b32 v236, v212 offset:5120
	ds_read_b32 v237, v212 offset:5632
	ds_read_b32 v238, v212 offset:6144
	ds_read_b32 v239, v212 offset:6656
	ds_read_b32 v240, v212 offset:7168
	ds_read_b32 v241, v212 offset:7680
	s_waitcnt lgkmcnt(0)
	v_max_f32_e32 v226, v226, v226
	v_max_f32_e32 v227, v227, v227
	v_max_f32_e32 v228, v228, v228
	v_max_f32_e32 v229, v229, v229
	v_max_f32_e32 v230, v230, v230
	v_max_f32_e32 v231, v231, v231
	v_max_f32_e32 v232, v232, v232
	v_max_f32_e32 v233, v233, v233
	v_max_f32_e32 v234, v234, v234
	v_max_f32_e32 v235, v235, v235
	v_max_f32_e32 v236, v236, v236
	v_max_f32_e32 v237, v237, v237
	v_max_f32_e32 v238, v238, v238
	v_max_f32_e32 v239, v239, v239
	v_max_f32_e32 v240, v240, v240
	v_max_f32_e32 v241, v241, v241
	v_med3_f32 v226, v226, s62, v95
	v_med3_f32 v227, v227, s62, v95
	v_med3_f32 v228, v228, s62, v95
	v_med3_f32 v229, v229, s62, v95
	v_med3_f32 v230, v230, s62, v95
	v_med3_f32 v231, v231, s62, v95
	v_med3_f32 v232, v232, s62, v95
	v_med3_f32 v233, v233, s62, v95
	v_med3_f32 v234, v234, s62, v95
	v_med3_f32 v235, v235, s62, v95
	v_med3_f32 v236, v236, s62, v95
	v_med3_f32 v237, v237, s62, v95
	v_med3_f32 v238, v238, s62, v95
	v_med3_f32 v239, v239, s62, v95
	v_med3_f32 v240, v240, s62, v95
	v_med3_f32 v241, v241, s62, v95
	v_mov_b32_e32 v242, 0
	v_mov_b32_e32 v243, 0
	v_mov_b32_e32 v244, 0
	v_mov_b32_e32 v245, 0
	v_cvt_pk_fp8_f32 v242, v226, v227
	v_cvt_pk_fp8_f32 v243, v230, v231
	v_cvt_pk_fp8_f32 v244, v234, v235
	v_cvt_pk_fp8_f32 v245, v238, v239
	v_cvt_pk_fp8_f32 v242, v228, v229 op_sel:[0,0,1]
	v_cvt_pk_fp8_f32 v243, v232, v233 op_sel:[0,0,1]
	v_cvt_pk_fp8_f32 v244, v236, v237 op_sel:[0,0,1]
	v_cvt_pk_fp8_f32 v245, v240, v241 op_sel:[0,0,1]
	s_nop 0
	global_store_dwordx4 v77, v[242:245], s[6:7]
	ds_read_b32 v226, v214
	ds_read_b32 v227, v214 offset:512
	ds_read_b32 v228, v214 offset:1024
	ds_read_b32 v229, v214 offset:1536
	ds_read_b32 v230, v214 offset:2048
	ds_read_b32 v231, v214 offset:2560
	ds_read_b32 v232, v214 offset:3072
	ds_read_b32 v233, v214 offset:3584
	ds_read_b32 v234, v214 offset:4096
	ds_read_b32 v235, v214 offset:4608
	ds_read_b32 v236, v214 offset:5120
	ds_read_b32 v237, v214 offset:5632
	ds_read_b32 v238, v214 offset:6144
	ds_read_b32 v239, v214 offset:6656
	ds_read_b32 v240, v214 offset:7168
	ds_read_b32 v241, v214 offset:7680
	s_waitcnt lgkmcnt(0)
	v_max_f32_e32 v226, v226, v226
	v_max_f32_e32 v227, v227, v227
	v_max_f32_e32 v228, v228, v228
	v_max_f32_e32 v229, v229, v229
	v_max_f32_e32 v230, v230, v230
	v_max_f32_e32 v231, v231, v231
	v_max_f32_e32 v232, v232, v232
	v_max_f32_e32 v233, v233, v233
	v_max_f32_e32 v234, v234, v234
	v_max_f32_e32 v235, v235, v235
	v_max_f32_e32 v236, v236, v236
	v_max_f32_e32 v237, v237, v237
	v_max_f32_e32 v238, v238, v238
	v_max_f32_e32 v239, v239, v239
	v_max_f32_e32 v240, v240, v240
	v_max_f32_e32 v241, v241, v241
	v_med3_f32 v226, v226, s62, v95
	v_med3_f32 v227, v227, s62, v95
	v_med3_f32 v228, v228, s62, v95
	v_med3_f32 v229, v229, s62, v95
	v_med3_f32 v230, v230, s62, v95
	v_med3_f32 v231, v231, s62, v95
	v_med3_f32 v232, v232, s62, v95
	v_med3_f32 v233, v233, s62, v95
	v_med3_f32 v234, v234, s62, v95
	v_med3_f32 v235, v235, s62, v95
	v_med3_f32 v236, v236, s62, v95
	v_med3_f32 v237, v237, s62, v95
	v_med3_f32 v238, v238, s62, v95
	v_med3_f32 v239, v239, s62, v95
	v_med3_f32 v240, v240, s62, v95
	v_med3_f32 v241, v241, s62, v95
	v_mov_b32_e32 v242, 0
	v_mov_b32_e32 v243, 0
	v_mov_b32_e32 v244, 0
	v_mov_b32_e32 v245, 0
	v_cvt_pk_fp8_f32 v242, v226, v227
	v_cvt_pk_fp8_f32 v243, v230, v231
	v_cvt_pk_fp8_f32 v244, v234, v235
	v_cvt_pk_fp8_f32 v245, v238, v239
	v_cvt_pk_fp8_f32 v242, v228, v229 op_sel:[0,0,1]
	v_cvt_pk_fp8_f32 v243, v232, v233 op_sel:[0,0,1]
	v_cvt_pk_fp8_f32 v244, v236, v237 op_sel:[0,0,1]
	v_cvt_pk_fp8_f32 v245, v240, v241 op_sel:[0,0,1]
	s_nop 0
	global_store_dwordx4 v78, v[242:245], s[6:7]
	s_waitcnt vmcnt(12)
	v_mul_f32_e32 v144, v34, v144
	v_mul_f32_e32 v145, v34, v145
	v_mul_f32_e32 v146, v34, v146
	v_mul_f32_e32 v147, v34, v147
	ds_write_b128 v209, v[144:147]
	v_mul_f32_e32 v148, v35, v148
	v_mul_f32_e32 v149, v35, v149
	v_mul_f32_e32 v150, v35, v150
	v_mul_f32_e32 v151, v35, v151
	ds_write_b128 v209, v[148:151] offset:1024
	v_mul_f32_e32 v152, v36, v152
	v_mul_f32_e32 v153, v36, v153
	v_mul_f32_e32 v154, v36, v154
	v_mul_f32_e32 v155, v36, v155
	ds_write_b128 v209, v[152:155] offset:2048
	v_mul_f32_e32 v156, v37, v156
	v_mul_f32_e32 v157, v37, v157
	v_mul_f32_e32 v158, v37, v158
	v_mul_f32_e32 v159, v37, v159
	ds_write_b128 v209, v[156:159] offset:3072
	v_mul_f32_e32 v160, v38, v160
	v_mul_f32_e32 v161, v38, v161
	v_mul_f32_e32 v162, v38, v162
	v_mul_f32_e32 v163, v38, v163
	ds_write_b128 v209, v[160:163] offset:4096
	v_mul_f32_e32 v164, v39, v164
	v_mul_f32_e32 v165, v39, v165
	v_mul_f32_e32 v166, v39, v166
	v_mul_f32_e32 v167, v39, v167
	ds_write_b128 v209, v[164:167] offset:5120
	v_mul_f32_e32 v168, v40, v168
	v_mul_f32_e32 v169, v40, v169
	v_mul_f32_e32 v170, v40, v170
	v_mul_f32_e32 v171, v40, v171
	ds_write_b128 v209, v[168:171] offset:6144
	v_mul_f32_e32 v172, v41, v172
	v_mul_f32_e32 v173, v41, v173
	v_mul_f32_e32 v174, v41, v174
	v_mul_f32_e32 v175, v41, v175
	ds_write_b128 v209, v[172:175] offset:7168
	s_waitcnt lgkmcnt(0)
	s_barrier
; #define GAS __attribute__((address_space(1)))
; #define LAS __attribute__((address_space(3)))
; #define LDS_WAIT() asm volatile("s_waitcnt lgkmcnt(0)" ::: "memory")
;     const int pr = item >> 1, kb = 2 * (pr / nblk) + (item & 1), nb = pr % nblk, k0 = 64 * kb, n0 = 32 * nb;
;     const int nr = n0 + (lane & 31); const int sc = MAP == 1 ? src_col_in(nr) : nr;
;     float v[32];
; #pragma unroll
;     for (int i = 0; i < 32; ++i) v[i] = sc >= 0 ? W[(size_t)(k0 + 2 * i + (lane >> 5)) * Nsrc + sc] : 0.f;
; #pragma unroll
;     for (int i = 0; i < 32; ++i) { const int k = k0 + 2 * i + (lane >> 5); float x = v[i] * wscale; if (KS) x *= (k < ksplit ? ksA[k] : ksB[k - ksplit]); scr[(2 * i + (lane >> 5)) * 33 + (lane & 31)] = x; }
;     LDS_WAIT(); asm volatile("" ::: "memory");
;     const int c = lane & 7;
; #pragma unroll
;     for (int j = 0; j < 4; ++j) { const int n = (lane >> 3) + 8 * j; const LAS float* s = scr + (8 * c) * 33 + n;
;         const unsigned long long o = (unsigned long long)pg8::pk4_fp8(s[0 * 33], s[1 * 33], s[2 * 33], s[3 * 33]) | ((unsigned long long)pg8::pk4_fp8(s[4 * 33], s[5 * 33], s[6 * 33], s[7 * 33]) << 32);
;         *(GAS unsigned long long*)(WT + (size_t)(n0 + n) * K + k0 + 8 * c) = o; }
;     LDS_WAIT(); asm volatile("" ::: "memory");
; }
; __global__ void __launch_bounds__(NWAVES * 64, 2) hybrid_fwd(Args args) {
;     ...
;             p0_transpose_item_f8<false>(args.in[16] + (size_t)l * FF * DM, FF, DM, DM / 32, (unsigned char*)(ws + WS_WDN + l * SZ_WDN), 128.f, args.in[16], args.in[16], 0, scr, r, lane);
	s_mov_b64 s[8:9], s[38:39]
	global_load_dwordx4 v[144:147], v75, s[8:9]
	s_add_u32 s8, s8, 0x8000
	s_addc_u32 s9, s9, 0
	global_load_dwordx4 v[148:151], v75, s[8:9]
	s_add_u32 s8, s8, 0x8000
	s_addc_u32 s9, s9, 0
	global_load_dwordx4 v[152:155], v75, s[8:9]
	s_add_u32 s8, s8, 0x8000
	s_addc_u32 s9, s9, 0
	global_load_dwordx4 v[156:159], v75, s[8:9]
	s_add_u32 s8, s8, 0x8000
	s_addc_u32 s9, s9, 0
	global_load_dwordx4 v[160:163], v75, s[8:9]
	s_add_u32 s8, s8, 0x8000
	s_addc_u32 s9, s9, 0
	global_load_dwordx4 v[164:167], v75, s[8:9]
	s_add_u32 s8, s8, 0x8000
	s_addc_u32 s9, s9, 0
	global_load_dwordx4 v[168:171], v75, s[8:9]
	s_add_u32 s8, s8, 0x8000
	s_addc_u32 s9, s9, 0
	global_load_dwordx4 v[172:175], v75, s[8:9]
	s_add_u32 s6, s36, 0x3800000
	s_addc_u32 s7, s37, 0
	ds_read_b32 v226, v211
	ds_read_b32 v227, v211 offset:512
	ds_read_b32 v228, v211 offset:1024
	ds_read_b32 v229, v211 offset:1536
	ds_read_b32 v230, v211 offset:2048
	ds_read_b32 v231, v211 offset:2560
	ds_read_b32 v232, v211 offset:3072
	ds_read_b32 v233, v211 offset:3584
	ds_read_b32 v234, v211 offset:4096
	ds_read_b32 v235, v211 offset:4608
	ds_read_b32 v236, v211 offset:5120
	ds_read_b32 v237, v211 offset:5632
	ds_read_b32 v238, v211 offset:6144
	ds_read_b32 v239, v211 offset:6656
	ds_read_b32 v240, v211 offset:7168
	ds_read_b32 v241, v211 offset:7680
	s_waitcnt lgkmcnt(0)
	v_max_f32_e32 v226, v226, v226
	v_max_f32_e32 v227, v227, v227
	v_max_f32_e32 v228, v228, v228
	v_max_f32_e32 v229, v229, v229
	v_max_f32_e32 v230, v230, v230
	v_max_f32_e32 v231, v231, v231
	v_max_f32_e32 v232, v232, v232
	v_max_f32_e32 v233, v233, v233
	v_max_f32_e32 v234, v234, v234
	v_max_f32_e32 v235, v235, v235
	v_max_f32_e32 v236, v236, v236
	v_max_f32_e32 v237, v237, v237
	v_max_f32_e32 v238, v238, v238
	v_max_f32_e32 v239, v239, v239
	v_max_f32_e32 v240, v240, v240
	v_max_f32_e32 v241, v241, v241
	v_med3_f32 v226, v226, s62, v95
	v_med3_f32 v227, v227, s62, v95
	v_med3_f32 v228, v228, s62, v95
	v_med3_f32 v229, v229, s62, v95
	v_med3_f32 v230, v230, s62, v95
	v_med3_f32 v231, v231, s62, v95
	v_med3_f32 v232, v232, s62, v95
	v_med3_f32 v233, v233, s62, v95
	v_med3_f32 v234, v234, s62, v95
	v_med3_f32 v235, v235, s62, v95
	v_med3_f32 v236, v236, s62, v95
	v_med3_f32 v237, v237, s62, v95
	v_med3_f32 v238, v238, s62, v95
	v_med3_f32 v239, v239, s62, v95
	v_med3_f32 v240, v240, s62, v95
	v_med3_f32 v241, v241, s62, v95
	v_mov_b32_e32 v242, 0
	v_mov_b32_e32 v243, 0
	v_mov_b32_e32 v244, 0
	v_mov_b32_e32 v245, 0
	v_cvt_pk_fp8_f32 v242, v226, v227
	v_cvt_pk_fp8_f32 v243, v230, v231
	v_cvt_pk_fp8_f32 v244, v234, v235
	v_cvt_pk_fp8_f32 v245, v238, v239
	v_cvt_pk_fp8_f32 v242, v228, v229 op_sel:[0,0,1]
	v_cvt_pk_fp8_f32 v243, v232, v233 op_sel:[0,0,1]
	v_cvt_pk_fp8_f32 v244, v236, v237 op_sel:[0,0,1]
	v_cvt_pk_fp8_f32 v245, v240, v241 op_sel:[0,0,1]
	s_nop 0
	global_store_dwordx4 v77, v[242:245], s[6:7]
	ds_read_b32 v226, v213
	ds_read_b32 v227, v213 offset:512
	ds_read_b32 v228, v213 offset:1024
	ds_read_b32 v229, v213 offset:1536
	ds_read_b32 v230, v213 offset:2048
	ds_read_b32 v231, v213 offset:2560
	ds_read_b32 v232, v213 offset:3072
	ds_read_b32 v233, v213 offset:3584
	ds_read_b32 v234, v213 offset:4096
	ds_read_b32 v235, v213 offset:4608
	ds_read_b32 v236, v213 offset:5120
	ds_read_b32 v237, v213 offset:5632
	ds_read_b32 v238, v213 offset:6144
	ds_read_b32 v239, v213 offset:6656
	ds_read_b32 v240, v213 offset:7168
	ds_read_b32 v241, v213 offset:7680
	s_waitcnt lgkmcnt(0)
	v_max_f32_e32 v226, v226, v226
	v_max_f32_e32 v227, v227, v227
	v_max_f32_e32 v228, v228, v228
	v_max_f32_e32 v229, v229, v229
	v_max_f32_e32 v230, v230, v230
	v_max_f32_e32 v231, v231, v231
	v_max_f32_e32 v232, v232, v232
	v_max_f32_e32 v233, v233, v233
	v_max_f32_e32 v234, v234, v234
	v_max_f32_e32 v235, v235, v235
	v_max_f32_e32 v236, v236, v236
	v_max_f32_e32 v237, v237, v237
	v_max_f32_e32 v238, v238, v238
	v_max_f32_e32 v239, v239, v239
	v_max_f32_e32 v240, v240, v240
	v_max_f32_e32 v241, v241, v241
	v_med3_f32 v226, v226, s62, v95
	v_med3_f32 v227, v227, s62, v95
	v_med3_f32 v228, v228, s62, v95
	v_med3_f32 v229, v229, s62, v95
	v_med3_f32 v230, v230, s62, v95
	v_med3_f32 v231, v231, s62, v95
	v_med3_f32 v232, v232, s62, v95
	v_med3_f32 v233, v233, s62, v95
	v_med3_f32 v234, v234, s62, v95
	v_med3_f32 v235, v235, s62, v95
	v_med3_f32 v236, v236, s62, v95
	v_med3_f32 v237, v237, s62, v95
	v_med3_f32 v238, v238, s62, v95
	v_med3_f32 v239, v239, s62, v95
	v_med3_f32 v240, v240, s62, v95
	v_med3_f32 v241, v241, s62, v95
	v_mov_b32_e32 v242, 0
	v_mov_b32_e32 v243, 0
	v_mov_b32_e32 v244, 0
	v_mov_b32_e32 v245, 0
	v_cvt_pk_fp8_f32 v242, v226, v227
	v_cvt_pk_fp8_f32 v243, v230, v231
	v_cvt_pk_fp8_f32 v244, v234, v235
	v_cvt_pk_fp8_f32 v245, v238, v239
	v_cvt_pk_fp8_f32 v242, v228, v229 op_sel:[0,0,1]
	v_cvt_pk_fp8_f32 v243, v232, v233 op_sel:[0,0,1]
	v_cvt_pk_fp8_f32 v244, v236, v237 op_sel:[0,0,1]
	v_cvt_pk_fp8_f32 v245, v240, v241 op_sel:[0,0,1]
	s_nop 0
	global_store_dwordx4 v78, v[242:245], s[6:7]
	s_waitcnt vmcnt(12)
	v_mul_f32_e32 v176, v34, v176
	v_mul_f32_e32 v177, v34, v177
	v_mul_f32_e32 v178, v34, v178
	v_mul_f32_e32 v179, v34, v179
	ds_write_b128 v210, v[176:179]
	v_mul_f32_e32 v180, v35, v180
	v_mul_f32_e32 v181, v35, v181
	v_mul_f32_e32 v182, v35, v182
	v_mul_f32_e32 v183, v35, v183
	ds_write_b128 v210, v[180:183] offset:1024
	v_mul_f32_e32 v184, v36, v184
	v_mul_f32_e32 v185, v36, v185
	v_mul_f32_e32 v186, v36, v186
	v_mul_f32_e32 v187, v36, v187
	ds_write_b128 v210, v[184:187] offset:2048
	v_mul_f32_e32 v188, v37, v188
	v_mul_f32_e32 v189, v37, v189
	v_mul_f32_e32 v190, v37, v190
	v_mul_f32_e32 v191, v37, v191
	ds_write_b128 v210, v[188:191] offset:3072
	v_mul_f32_e32 v192, v38, v192
	v_mul_f32_e32 v193, v38, v193
	v_mul_f32_e32 v194, v38, v194
	v_mul_f32_e32 v195, v38, v195
	ds_write_b128 v210, v[192:195] offset:4096
	v_mul_f32_e32 v196, v39, v196
	v_mul_f32_e32 v197, v39, v197
	v_mul_f32_e32 v198, v39, v198
	v_mul_f32_e32 v199, v39, v199
	ds_write_b128 v210, v[196:199] offset:5120
	v_mul_f32_e32 v200, v40, v200
	v_mul_f32_e32 v201, v40, v201
	v_mul_f32_e32 v202, v40, v202
	v_mul_f32_e32 v203, v40, v203
	ds_write_b128 v210, v[200:203] offset:6144
	v_mul_f32_e32 v204, v41, v204
	v_mul_f32_e32 v205, v41, v205
	v_mul_f32_e32 v206, v41, v206
	v_mul_f32_e32 v207, v41, v207
	ds_write_b128 v210, v[204:207] offset:7168
	s_waitcnt lgkmcnt(0)
	s_barrier
; #define GAS __attribute__((address_space(1)))
; #define LAS __attribute__((address_space(3)))
; #define LDS_WAIT() asm volatile("s_waitcnt lgkmcnt(0)" ::: "memory")
;     const int pr = item >> 1, kb = 2 * (pr / nblk) + (item & 1), nb = pr % nblk, k0 = 64 * kb, n0 = 32 * nb;
;     const int nr = n0 + (lane & 31); const int sc = MAP == 1 ? src_col_in(nr) : nr;
;     float v[32];
; #pragma unroll
;     for (int i = 0; i < 32; ++i) v[i] = sc >= 0 ? W[(size_t)(k0 + 2 * i + (lane >> 5)) * Nsrc + sc] : 0.f;
; #pragma unroll
;     for (int i = 0; i < 32; ++i) { const int k = k0 + 2 * i + (lane >> 5); float x = v[i] * wscale; if (KS) x *= (k < ksplit ? ksA[k] : ksB[k - ksplit]); scr[(2 * i + (lane >> 5)) * 33 + (lane & 31)] = x; }
;     LDS_WAIT(); asm volatile("" ::: "memory");
;     const int c = lane & 7;
; #pragma unroll
;     for (int j = 0; j < 4; ++j) { const int n = (lane >> 3) + 8 * j; const LAS float* s = scr + (8 * c) * 33 + n;
;         const unsigned long long o = (unsigned long long)pg8::pk4_fp8(s[0 * 33], s[1 * 33], s[2 * 33], s[3 * 33]) | ((unsigned long long)pg8::pk4_fp8(s[4 * 33], s[5 * 33], s[6 * 33], s[7 * 33]) << 32);
;         *(GAS unsigned long long*)(WT + (size_t)(n0 + n) * K + k0 + 8 * c) = o; }
;     LDS_WAIT(); asm volatile("" ::: "memory");
; }
; __global__ void __launch_bounds__(NWAVES * 64, 2) hybrid_fwd(Args args) {
;     ...
;             p0_transpose_item_f8<false>(args.in[16] + (size_t)l * FF * DM, FF, DM, DM / 32, (unsigned char*)(ws + WS_WDN + l * SZ_WDN), 128.f, args.in[16], args.in[16], 0, scr, r, lane);
	s_add_u32 s8, s38, 0x1000
	s_addc_u32 s9, s39, 0
	global_load_dwordx4 v[176:179], v75, s[8:9]
	s_add_u32 s8, s8, 0x8000
	s_addc_u32 s9, s9, 0
	global_load_dwordx4 v[180:183], v75, s[8:9]
	s_add_u32 s8, s8, 0x8000
	s_addc_u32 s9, s9, 0
	global_load_dwordx4 v[184:187], v75, s[8:9]
	s_add_u32 s8, s8, 0x8000
	s_addc_u32 s9, s9, 0
	global_load_dwordx4 v[188:191], v75, s[8:9]
	s_add_u32 s8, s8, 0x8000
	s_addc_u32 s9, s9, 0
	global_load_dwordx4 v[192:195], v75, s[8:9]
	s_add_u32 s8, s8, 0x8000
	s_addc_u32 s9, s9, 0
	global_load_dwordx4 v[196:199], v75, s[8:9]
	s_add_u32 s8, s8, 0x8000
	s_addc_u32 s9, s9, 0
	global_load_dwordx4 v[200:203], v75, s[8:9]
	s_add_u32 s8, s8, 0x8000
	s_addc_u32 s9, s9, 0
	global_load_dwordx4 v[204:207], v75, s[8:9]
	s_add_u32 s6, s36, 0x3c00000
	s_addc_u32 s7, s37, 0
	ds_read_b32 v226, v212
	ds_read_b32 v227, v212 offset:512
	ds_read_b32 v228, v212 offset:1024
	ds_read_b32 v229, v212 offset:1536
	ds_read_b32 v230, v212 offset:2048
	ds_read_b32 v231, v212 offset:2560
	ds_read_b32 v232, v212 offset:3072
	ds_read_b32 v233, v212 offset:3584
	ds_read_b32 v234, v212 offset:4096
	ds_read_b32 v235, v212 offset:4608
	ds_read_b32 v236, v212 offset:5120
	ds_read_b32 v237, v212 offset:5632
	ds_read_b32 v238, v212 offset:6144
	ds_read_b32 v239, v212 offset:6656
	ds_read_b32 v240, v212 offset:7168
	ds_read_b32 v241, v212 offset:7680
	s_waitcnt lgkmcnt(0)
	v_max_f32_e32 v226, v226, v226
	v_max_f32_e32 v227, v227, v227
	v_max_f32_e32 v228, v228, v228
	v_max_f32_e32 v229, v229, v229
	v_max_f32_e32 v230, v230, v230
	v_max_f32_e32 v231, v231, v231
	v_max_f32_e32 v232, v232, v232
	v_max_f32_e32 v233, v233, v233
	v_max_f32_e32 v234, v234, v234
	v_max_f32_e32 v235, v235, v235
	v_max_f32_e32 v236, v236, v236
	v_max_f32_e32 v237, v237, v237
	v_max_f32_e32 v238, v238, v238
	v_max_f32_e32 v239, v239, v239
	v_max_f32_e32 v240, v240, v240
	v_max_f32_e32 v241, v241, v241
	v_med3_f32 v226, v226, s62, v95
	v_med3_f32 v227, v227, s62, v95
	v_med3_f32 v228, v228, s62, v95
	v_med3_f32 v229, v229, s62, v95
	v_med3_f32 v230, v230, s62, v95
	v_med3_f32 v231, v231, s62, v95
	v_med3_f32 v232, v232, s62, v95
	v_med3_f32 v233, v233, s62, v95
	v_med3_f32 v234, v234, s62, v95
	v_med3_f32 v235, v235, s62, v95
	v_med3_f32 v236, v236, s62, v95
	v_med3_f32 v237, v237, s62, v95
	v_med3_f32 v238, v238, s62, v95
	v_med3_f32 v239, v239, s62, v95
	v_med3_f32 v240, v240, s62, v95
	v_med3_f32 v241, v241, s62, v95
	v_mov_b32_e32 v242, 0
	v_mov_b32_e32 v243, 0
	v_mov_b32_e32 v244, 0
	v_mov_b32_e32 v245, 0
	v_cvt_pk_fp8_f32 v242, v226, v227
	v_cvt_pk_fp8_f32 v243, v230, v231
	v_cvt_pk_fp8_f32 v244, v234, v235
	v_cvt_pk_fp8_f32 v245, v238, v239
	v_cvt_pk_fp8_f32 v242, v228, v229 op_sel:[0,0,1]
	v_cvt_pk_fp8_f32 v243, v232, v233 op_sel:[0,0,1]
	v_cvt_pk_fp8_f32 v244, v236, v237 op_sel:[0,0,1]
	v_cvt_pk_fp8_f32 v245, v240, v241 op_sel:[0,0,1]
	s_nop 0
	global_store_dwordx4 v77, v[242:245], s[6:7]
	ds_read_b32 v226, v214
	ds_read_b32 v227, v214 offset:512
	ds_read_b32 v228, v214 offset:1024
	ds_read_b32 v229, v214 offset:1536
	ds_read_b32 v230, v214 offset:2048
	ds_read_b32 v231, v214 offset:2560
	ds_read_b32 v232, v214 offset:3072
	ds_read_b32 v233, v214 offset:3584
	ds_read_b32 v234, v214 offset:4096
	ds_read_b32 v235, v214 offset:4608
	ds_read_b32 v236, v214 offset:5120
	ds_read_b32 v237, v214 offset:5632
	ds_read_b32 v238, v214 offset:6144
	ds_read_b32 v239, v214 offset:6656
	ds_read_b32 v240, v214 offset:7168
	ds_read_b32 v241, v214 offset:7680
	s_waitcnt lgkmcnt(0)
	v_max_f32_e32 v226, v226, v226
	v_max_f32_e32 v227, v227, v227
	v_max_f32_e32 v228, v228, v228
	v_max_f32_e32 v229, v229, v229
	v_max_f32_e32 v230, v230, v230
	v_max_f32_e32 v231, v231, v231
	v_max_f32_e32 v232, v232, v232
	v_max_f32_e32 v233, v233, v233
	v_max_f32_e32 v234, v234, v234
	v_max_f32_e32 v235, v235, v235
	v_max_f32_e32 v236, v236, v236
	v_max_f32_e32 v237, v237, v237
	v_max_f32_e32 v238, v238, v238
	v_max_f32_e32 v239, v239, v239
	v_max_f32_e32 v240, v240, v240
	v_max_f32_e32 v241, v241, v241
	v_med3_f32 v226, v226, s62, v95
	v_med3_f32 v227, v227, s62, v95
	v_med3_f32 v228, v228, s62, v95
	v_med3_f32 v229, v229, s62, v95
	v_med3_f32 v230, v230, s62, v95
	v_med3_f32 v231, v231, s62, v95
	v_med3_f32 v232, v232, s62, v95
	v_med3_f32 v233, v233, s62, v95
	v_med3_f32 v234, v234, s62, v95
	v_med3_f32 v235, v235, s62, v95
	v_med3_f32 v236, v236, s62, v95
	v_med3_f32 v237, v237, s62, v95
	v_med3_f32 v238, v238, s62, v95
	v_med3_f32 v239, v239, s62, v95
	v_med3_f32 v240, v240, s62, v95
	v_med3_f32 v241, v241, s62, v95
	v_mov_b32_e32 v242, 0
	v_mov_b32_e32 v243, 0
	v_mov_b32_e32 v244, 0
	v_mov_b32_e32 v245, 0
	v_cvt_pk_fp8_f32 v242, v226, v227
	v_cvt_pk_fp8_f32 v243, v230, v231
	v_cvt_pk_fp8_f32 v244, v234, v235
	v_cvt_pk_fp8_f32 v245, v238, v239
	v_cvt_pk_fp8_f32 v242, v228, v229 op_sel:[0,0,1]
	v_cvt_pk_fp8_f32 v243, v232, v233 op_sel:[0,0,1]
	v_cvt_pk_fp8_f32 v244, v236, v237 op_sel:[0,0,1]
	v_cvt_pk_fp8_f32 v245, v240, v241 op_sel:[0,0,1]
	s_nop 0
	global_store_dwordx4 v78, v[242:245], s[6:7]
	s_waitcnt vmcnt(12)
	v_mul_f32_e32 v144, 0x43000000, v144
	v_mul_f32_e32 v145, 0x43000000, v145
	v_mul_f32_e32 v146, 0x43000000, v146
	v_mul_f32_e32 v147, 0x43000000, v147
	ds_write_b128 v209, v[144:147]
	v_mul_f32_e32 v148, 0x43000000, v148
	v_mul_f32_e32 v149, 0x43000000, v149
	v_mul_f32_e32 v150, 0x43000000, v150
	v_mul_f32_e32 v151, 0x43000000, v151
	ds_write_b128 v209, v[148:151] offset:1024
	v_mul_f32_e32 v152, 0x43000000, v152
	v_mul_f32_e32 v153, 0x43000000, v153
	v_mul_f32_e32 v154, 0x43000000, v154
	v_mul_f32_e32 v155, 0x43000000, v155
	ds_write_b128 v209, v[152:155] offset:2048
	v_mul_f32_e32 v156, 0x43000000, v156
	v_mul_f32_e32 v157, 0x43000000, v157
	v_mul_f32_e32 v158, 0x43000000, v158
	v_mul_f32_e32 v159, 0x43000000, v159
	ds_write_b128 v209, v[156:159] offset:3072
	v_mul_f32_e32 v160, 0x43000000, v160
	v_mul_f32_e32 v161, 0x43000000, v161
	v_mul_f32_e32 v162, 0x43000000, v162
	v_mul_f32_e32 v163, 0x43000000, v163
	ds_write_b128 v209, v[160:163] offset:4096
	v_mul_f32_e32 v164, 0x43000000, v164
	v_mul_f32_e32 v165, 0x43000000, v165
	v_mul_f32_e32 v166, 0x43000000, v166
	v_mul_f32_e32 v167, 0x43000000, v167
	ds_write_b128 v209, v[164:167] offset:5120
	v_mul_f32_e32 v168, 0x43000000, v168
	v_mul_f32_e32 v169, 0x43000000, v169
	v_mul_f32_e32 v170, 0x43000000, v170
	v_mul_f32_e32 v171, 0x43000000, v171
	ds_write_b128 v209, v[168:171] offset:6144
	v_mul_f32_e32 v172, 0x43000000, v172
	v_mul_f32_e32 v173, 0x43000000, v173
	v_mul_f32_e32 v174, 0x43000000, v174
	v_mul_f32_e32 v175, 0x43000000, v175
	ds_write_b128 v209, v[172:175] offset:7168
	s_waitcnt lgkmcnt(0)
	s_barrier
; #define GAS __attribute__((address_space(1)))
; #define LAS __attribute__((address_space(3)))
; #define LDS_WAIT() asm volatile("s_waitcnt lgkmcnt(0)" ::: "memory")
;     const int pr = item >> 1, kb = 2 * (pr / nblk) + (item & 1), nb = pr % nblk, k0 = 64 * kb, n0 = 32 * nb;
;     const int nr = n0 + (lane & 31); const int sc = MAP == 1 ? src_col_in(nr) : nr;
;     float v[32];
; #pragma unroll
;     for (int i = 0; i < 32; ++i) v[i] = sc >= 0 ? W[(size_t)(k0 + 2 * i + (lane >> 5)) * Nsrc + sc] : 0.f;
; #pragma unroll
;     for (int i = 0; i < 32; ++i) { const int k = k0 + 2 * i + (lane >> 5); float x = v[i] * wscale; if (KS) x *= (k < ksplit ? ksA[k] : ksB[k - ksplit]); scr[(2 * i + (lane >> 5)) * 33 + (lane & 31)] = x; }
;     LDS_WAIT(); asm volatile("" ::: "memory");
;     const int c = lane & 7;
; #pragma unroll
;     for (int j = 0; j < 4; ++j) { const int n = (lane >> 3) + 8 * j; const LAS float* s = scr + (8 * c) * 33 + n;
;         const unsigned long long o = (unsigned long long)pg8::pk4_fp8(s[0 * 33], s[1 * 33], s[2 * 33], s[3 * 33]) | ((unsigned long long)pg8::pk4_fp8(s[4 * 33], s[5 * 33], s[6 * 33], s[7 * 33]) << 32);
;         *(GAS unsigned long long*)(WT + (size_t)(n0 + n) * K + k0 + 8 * c) = o; }
;     LDS_WAIT(); asm volatile("" ::: "memory");
; }
	s_add_u32 s8, s38, 0x2000
	s_addc_u32 s9, s39, 0
	global_load_dwordx4 v[144:147], v75, s[8:9]
	s_add_u32 s8, s8, 0x8000
	s_addc_u32 s9, s9, 0
	global_load_dwordx4 v[148:151], v75, s[8:9]
	s_add_u32 s8, s8, 0x8000
	s_addc_u32 s9, s9, 0
	global_load_dwordx4 v[152:155], v75, s[8:9]
	s_add_u32 s8, s8, 0x8000
	s_addc_u32 s9, s9, 0
	global_load_dwordx4 v[156:159], v75, s[8:9]
	s_add_u32 s8, s8, 0x8000
	s_addc_u32 s9, s9, 0
	global_load_dwordx4 v[160:163], v75, s[8:9]
	s_add_u32 s8, s8, 0x8000
	s_addc_u32 s9, s9, 0
	global_load_dwordx4 v[164:167], v75, s[8:9]
	s_add_u32 s8, s8, 0x8000
	s_addc_u32 s9, s9, 0
	global_load_dwordx4 v[168:171], v75, s[8:9]
	s_add_u32 s8, s8, 0x8000
	s_addc_u32 s9, s9, 0
	global_load_dwordx4 v[172:175], v75, s[8:9]
	s_mov_b64 s[6:7], s[40:41]
	ds_read_b32 v226, v211
	ds_read_b32 v227, v211 offset:512
	ds_read_b32 v228, v211 offset:1024
	ds_read_b32 v229, v211 offset:1536
	ds_read_b32 v230, v211 offset:2048
	ds_read_b32 v231, v211 offset:2560
	ds_read_b32 v232, v211 offset:3072
	ds_read_b32 v233, v211 offset:3584
	ds_read_b32 v234, v211 offset:4096
	ds_read_b32 v235, v211 offset:4608
	ds_read_b32 v236, v211 offset:5120
	ds_read_b32 v237, v211 offset:5632
	ds_read_b32 v238, v211 offset:6144
	ds_read_b32 v239, v211 offset:6656
	ds_read_b32 v240, v211 offset:7168
	ds_read_b32 v241, v211 offset:7680
	s_waitcnt lgkmcnt(0)
	v_max_f32_e32 v226, v226, v226
	v_max_f32_e32 v227, v227, v227
	v_max_f32_e32 v228, v228, v228
	v_max_f32_e32 v229, v229, v229
	v_max_f32_e32 v230, v230, v230
	v_max_f32_e32 v231, v231, v231
	v_max_f32_e32 v232, v232, v232
	v_max_f32_e32 v233, v233, v233
	v_max_f32_e32 v234, v234, v234
	v_max_f32_e32 v235, v235, v235
	v_max_f32_e32 v236, v236, v236
	v_max_f32_e32 v237, v237, v237
	v_max_f32_e32 v238, v238, v238
	v_max_f32_e32 v239, v239, v239
	v_max_f32_e32 v240, v240, v240
	v_max_f32_e32 v241, v241, v241
	v_med3_f32 v226, v226, s62, v95
	v_med3_f32 v227, v227, s62, v95
	v_med3_f32 v228, v228, s62, v95
	v_med3_f32 v229, v229, s62, v95
	v_med3_f32 v230, v230, s62, v95
	v_med3_f32 v231, v231, s62, v95
	v_med3_f32 v232, v232, s62, v95
	v_med3_f32 v233, v233, s62, v95
	v_med3_f32 v234, v234, s62, v95
	v_med3_f32 v235, v235, s62, v95
	v_med3_f32 v236, v236, s62, v95
	v_med3_f32 v237, v237, s62, v95
	v_med3_f32 v238, v238, s62, v95
	v_med3_f32 v239, v239, s62, v95
	v_med3_f32 v240, v240, s62, v95
	v_med3_f32 v241, v241, s62, v95
	v_mov_b32_e32 v242, 0
	v_mov_b32_e32 v243, 0
	v_mov_b32_e32 v244, 0
	v_mov_b32_e32 v245, 0
	v_cvt_pk_fp8_f32 v242, v226, v227
	v_cvt_pk_fp8_f32 v243, v230, v231
	v_cvt_pk_fp8_f32 v244, v234, v235
	v_cvt_pk_fp8_f32 v245, v238, v239
	v_cvt_pk_fp8_f32 v242, v228, v229 op_sel:[0,0,1]
	v_cvt_pk_fp8_f32 v243, v232, v233 op_sel:[0,0,1]
	v_cvt_pk_fp8_f32 v244, v236, v237 op_sel:[0,0,1]
	v_cvt_pk_fp8_f32 v245, v240, v241 op_sel:[0,0,1]
	s_nop 0
	global_store_dwordx4 v79, v[242:245], s[6:7]
	ds_read_b32 v226, v213
	ds_read_b32 v227, v213 offset:512
	ds_read_b32 v228, v213 offset:1024
	ds_read_b32 v229, v213 offset:1536
	ds_read_b32 v230, v213 offset:2048
	ds_read_b32 v231, v213 offset:2560
	ds_read_b32 v232, v213 offset:3072
	ds_read_b32 v233, v213 offset:3584
	ds_read_b32 v234, v213 offset:4096
	ds_read_b32 v235, v213 offset:4608
	ds_read_b32 v236, v213 offset:5120
	ds_read_b32 v237, v213 offset:5632
	ds_read_b32 v238, v213 offset:6144
	ds_read_b32 v239, v213 offset:6656
	ds_read_b32 v240, v213 offset:7168
	ds_read_b32 v241, v213 offset:7680
	s_waitcnt lgkmcnt(0)
	v_max_f32_e32 v226, v226, v226
	v_max_f32_e32 v227, v227, v227
	v_max_f32_e32 v228, v228, v228
	v_max_f32_e32 v229, v229, v229
	v_max_f32_e32 v230, v230, v230
	v_max_f32_e32 v231, v231, v231
	v_max_f32_e32 v232, v232, v232
	v_max_f32_e32 v233, v233, v233
	v_max_f32_e32 v234, v234, v234
	v_max_f32_e32 v235, v235, v235
	v_max_f32_e32 v236, v236, v236
	v_max_f32_e32 v237, v237, v237
	v_max_f32_e32 v238, v238, v238
	v_max_f32_e32 v239, v239, v239
	v_max_f32_e32 v240, v240, v240
	v_max_f32_e32 v241, v241, v241
	v_med3_f32 v226, v226, s62, v95
	v_med3_f32 v227, v227, s62, v95
	v_med3_f32 v228, v228, s62, v95
	v_med3_f32 v229, v229, s62, v95
	v_med3_f32 v230, v230, s62, v95
	v_med3_f32 v231, v231, s62, v95
	v_med3_f32 v232, v232, s62, v95
	v_med3_f32 v233, v233, s62, v95
	v_med3_f32 v234, v234, s62, v95
	v_med3_f32 v235, v235, s62, v95
	v_med3_f32 v236, v236, s62, v95
	v_med3_f32 v237, v237, s62, v95
	v_med3_f32 v238, v238, s62, v95
	v_med3_f32 v239, v239, s62, v95
	v_med3_f32 v240, v240, s62, v95
	v_med3_f32 v241, v241, s62, v95
	v_mov_b32_e32 v242, 0
	v_mov_b32_e32 v243, 0
	v_mov_b32_e32 v244, 0
	v_mov_b32_e32 v245, 0
	v_cvt_pk_fp8_f32 v242, v226, v227
	v_cvt_pk_fp8_f32 v243, v230, v231
	v_cvt_pk_fp8_f32 v244, v234, v235
	v_cvt_pk_fp8_f32 v245, v238, v239
	v_cvt_pk_fp8_f32 v242, v228, v229 op_sel:[0,0,1]
	v_cvt_pk_fp8_f32 v243, v232, v233 op_sel:[0,0,1]
	v_cvt_pk_fp8_f32 v244, v236, v237 op_sel:[0,0,1]
	v_cvt_pk_fp8_f32 v245, v240, v241 op_sel:[0,0,1]
	s_nop 0
	global_store_dwordx4 v80, v[242:245], s[6:7]
	s_waitcnt vmcnt(12)
	v_mul_f32_e32 v176, 0x43000000, v176
	v_mul_f32_e32 v177, 0x43000000, v177
	v_mul_f32_e32 v178, 0x43000000, v178
	v_mul_f32_e32 v179, 0x43000000, v179
	ds_write_b128 v210, v[176:179]
	v_mul_f32_e32 v180, 0x43000000, v180
	v_mul_f32_e32 v181, 0x43000000, v181
	v_mul_f32_e32 v182, 0x43000000, v182
	v_mul_f32_e32 v183, 0x43000000, v183
	ds_write_b128 v210, v[180:183] offset:1024
	v_mul_f32_e32 v184, 0x43000000, v184
	v_mul_f32_e32 v185, 0x43000000, v185
	v_mul_f32_e32 v186, 0x43000000, v186
	v_mul_f32_e32 v187, 0x43000000, v187
	ds_write_b128 v210, v[184:187] offset:2048
	v_mul_f32_e32 v188, 0x43000000, v188
	v_mul_f32_e32 v189, 0x43000000, v189
	v_mul_f32_e32 v190, 0x43000000, v190
	v_mul_f32_e32 v191, 0x43000000, v191
	ds_write_b128 v210, v[188:191] offset:3072
	v_mul_f32_e32 v192, 0x43000000, v192
	v_mul_f32_e32 v193, 0x43000000, v193
	v_mul_f32_e32 v194, 0x43000000, v194
	v_mul_f32_e32 v195, 0x43000000, v195
	ds_write_b128 v210, v[192:195] offset:4096
	v_mul_f32_e32 v196, 0x43000000, v196
	v_mul_f32_e32 v197, 0x43000000, v197
	v_mul_f32_e32 v198, 0x43000000, v198
	v_mul_f32_e32 v199, 0x43000000, v199
	ds_write_b128 v210, v[196:199] offset:5120
	v_mul_f32_e32 v200, 0x43000000, v200
	v_mul_f32_e32 v201, 0x43000000, v201
	v_mul_f32_e32 v202, 0x43000000, v202
	v_mul_f32_e32 v203, 0x43000000, v203
	ds_write_b128 v210, v[200:203] offset:6144
	v_mul_f32_e32 v204, 0x43000000, v204
	v_mul_f32_e32 v205, 0x43000000, v205
	v_mul_f32_e32 v206, 0x43000000, v206
	v_mul_f32_e32 v207, 0x43000000, v207
	ds_write_b128 v210, v[204:207] offset:7168
	s_waitcnt lgkmcnt(0)
	s_barrier
; #define GAS __attribute__((address_space(1)))
; #define LAS __attribute__((address_space(3)))
; #define LDS_WAIT() asm volatile("s_waitcnt lgkmcnt(0)" ::: "memory")
;     const int pr = item >> 1, kb = 2 * (pr / nblk) + (item & 1), nb = pr % nblk, k0 = 64 * kb, n0 = 32 * nb;
;     const int nr = n0 + (lane & 31); const int sc = MAP == 1 ? src_col_in(nr) : nr;
;     float v[32];
; #pragma unroll
;     for (int i = 0; i < 32; ++i) v[i] = sc >= 0 ? W[(size_t)(k0 + 2 * i + (lane >> 5)) * Nsrc + sc] : 0.f;
; #pragma unroll
;     for (int i = 0; i < 32; ++i) { const int k = k0 + 2 * i + (lane >> 5); float x = v[i] * wscale; if (KS) x *= (k < ksplit ? ksA[k] : ksB[k - ksplit]); scr[(2 * i + (lane >> 5)) * 33 + (lane & 31)] = x; }
;     LDS_WAIT(); asm volatile("" ::: "memory");
;     const int c = lane & 7;
; #pragma unroll
;     for (int j = 0; j < 4; ++j) { const int n = (lane >> 3) + 8 * j; const LAS float* s = scr + (8 * c) * 33 + n;
;         const unsigned long long o = (unsigned long long)pg8::pk4_fp8(s[0 * 33], s[1 * 33], s[2 * 33], s[3 * 33]) | ((unsigned long long)pg8::pk4_fp8(s[4 * 33], s[5 * 33], s[6 * 33], s[7 * 33]) << 32);
;         *(GAS unsigned long long*)(WT + (size_t)(n0 + n) * K + k0 + 8 * c) = o; }
;     LDS_WAIT(); asm volatile("" ::: "memory");
; }
	s_add_u32 s8, s38, 0x3000
	s_addc_u32 s9, s39, 0
	global_load_dwordx4 v[176:179], v75, s[8:9]
	s_add_u32 s8, s8, 0x8000
	s_addc_u32 s9, s9, 0
	global_load_dwordx4 v[180:183], v75, s[8:9]
	s_add_u32 s8, s8, 0x8000
	s_addc_u32 s9, s9, 0
	global_load_dwordx4 v[184:187], v75, s[8:9]
	s_add_u32 s8, s8, 0x8000
	s_addc_u32 s9, s9, 0
	global_load_dwordx4 v[188:191], v75, s[8:9]
	s_add_u32 s8, s8, 0x8000
	s_addc_u32 s9, s9, 0
	global_load_dwordx4 v[192:195], v75, s[8:9]
	s_add_u32 s8, s8, 0x8000
	s_addc_u32 s9, s9, 0
	global_load_dwordx4 v[196:199], v75, s[8:9]
	s_add_u32 s8, s8, 0x8000
	s_addc_u32 s9, s9, 0
	global_load_dwordx4 v[200:203], v75, s[8:9]
	s_add_u32 s8, s8, 0x8000
	s_addc_u32 s9, s9, 0
	global_load_dwordx4 v[204:207], v75, s[8:9]
	s_add_u32 s6, s40, 0x1000000
	s_addc_u32 s7, s41, 0
	ds_read_b32 v226, v212
	ds_read_b32 v227, v212 offset:512
	ds_read_b32 v228, v212 offset:1024
	ds_read_b32 v229, v212 offset:1536
	ds_read_b32 v230, v212 offset:2048
	ds_read_b32 v231, v212 offset:2560
	ds_read_b32 v232, v212 offset:3072
	ds_read_b32 v233, v212 offset:3584
	ds_read_b32 v234, v212 offset:4096
	ds_read_b32 v235, v212 offset:4608
	ds_read_b32 v236, v212 offset:5120
	ds_read_b32 v237, v212 offset:5632
	ds_read_b32 v238, v212 offset:6144
	ds_read_b32 v239, v212 offset:6656
	ds_read_b32 v240, v212 offset:7168
	ds_read_b32 v241, v212 offset:7680
	s_waitcnt lgkmcnt(0)
	v_max_f32_e32 v226, v226, v226
	v_max_f32_e32 v227, v227, v227
	v_max_f32_e32 v228, v228, v228
	v_max_f32_e32 v229, v229, v229
	v_max_f32_e32 v230, v230, v230
	v_max_f32_e32 v231, v231, v231
	v_max_f32_e32 v232, v232, v232
	v_max_f32_e32 v233, v233, v233
	v_max_f32_e32 v234, v234, v234
	v_max_f32_e32 v235, v235, v235
	v_max_f32_e32 v236, v236, v236
	v_max_f32_e32 v237, v237, v237
	v_max_f32_e32 v238, v238, v238
	v_max_f32_e32 v239, v239, v239
	v_max_f32_e32 v240, v240, v240
	v_max_f32_e32 v241, v241, v241
	v_med3_f32 v226, v226, s62, v95
	v_med3_f32 v227, v227, s62, v95
	v_med3_f32 v228, v228, s62, v95
	v_med3_f32 v229, v229, s62, v95
	v_med3_f32 v230, v230, s62, v95
	v_med3_f32 v231, v231, s62, v95
	v_med3_f32 v232, v232, s62, v95
	v_med3_f32 v233, v233, s62, v95
	v_med3_f32 v234, v234, s62, v95
	v_med3_f32 v235, v235, s62, v95
	v_med3_f32 v236, v236, s62, v95
	v_med3_f32 v237, v237, s62, v95
	v_med3_f32 v238, v238, s62, v95
	v_med3_f32 v239, v239, s62, v95
	v_med3_f32 v240, v240, s62, v95
	v_med3_f32 v241, v241, s62, v95
	v_mov_b32_e32 v242, 0
	v_mov_b32_e32 v243, 0
	v_mov_b32_e32 v244, 0
	v_mov_b32_e32 v245, 0
	v_cvt_pk_fp8_f32 v242, v226, v227
	v_cvt_pk_fp8_f32 v243, v230, v231
	v_cvt_pk_fp8_f32 v244, v234, v235
	v_cvt_pk_fp8_f32 v245, v238, v239
	v_cvt_pk_fp8_f32 v242, v228, v229 op_sel:[0,0,1]
	v_cvt_pk_fp8_f32 v243, v232, v233 op_sel:[0,0,1]
	v_cvt_pk_fp8_f32 v244, v236, v237 op_sel:[0,0,1]
	v_cvt_pk_fp8_f32 v245, v240, v241 op_sel:[0,0,1]
	s_nop 0
	global_store_dwordx4 v79, v[242:245], s[6:7]
	ds_read_b32 v226, v214
	ds_read_b32 v227, v214 offset:512
	ds_read_b32 v228, v214 offset:1024
	ds_read_b32 v229, v214 offset:1536
	ds_read_b32 v230, v214 offset:2048
	ds_read_b32 v231, v214 offset:2560
	ds_read_b32 v232, v214 offset:3072
	ds_read_b32 v233, v214 offset:3584
	ds_read_b32 v234, v214 offset:4096
	ds_read_b32 v235, v214 offset:4608
	ds_read_b32 v236, v214 offset:5120
	ds_read_b32 v237, v214 offset:5632
	ds_read_b32 v238, v214 offset:6144
	ds_read_b32 v239, v214 offset:6656
	ds_read_b32 v240, v214 offset:7168
	ds_read_b32 v241, v214 offset:7680
	s_waitcnt lgkmcnt(0)
	v_max_f32_e32 v226, v226, v226
	v_max_f32_e32 v227, v227, v227
	v_max_f32_e32 v228, v228, v228
	v_max_f32_e32 v229, v229, v229
	v_max_f32_e32 v230, v230, v230
	v_max_f32_e32 v231, v231, v231
	v_max_f32_e32 v232, v232, v232
	v_max_f32_e32 v233, v233, v233
	v_max_f32_e32 v234, v234, v234
	v_max_f32_e32 v235, v235, v235
	v_max_f32_e32 v236, v236, v236
	v_max_f32_e32 v237, v237, v237
	v_max_f32_e32 v238, v238, v238
	v_max_f32_e32 v239, v239, v239
	v_max_f32_e32 v240, v240, v240
	v_max_f32_e32 v241, v241, v241
	v_med3_f32 v226, v226, s62, v95
	v_med3_f32 v227, v227, s62, v95
	v_med3_f32 v228, v228, s62, v95
	v_med3_f32 v229, v229, s62, v95
	v_med3_f32 v230, v230, s62, v95
	v_med3_f32 v231, v231, s62, v95
	v_med3_f32 v232, v232, s62, v95
	v_med3_f32 v233, v233, s62, v95
	v_med3_f32 v234, v234, s62, v95
	v_med3_f32 v235, v235, s62, v95
	v_med3_f32 v236, v236, s62, v95
	v_med3_f32 v237, v237, s62, v95
	v_med3_f32 v238, v238, s62, v95
	v_med3_f32 v239, v239, s62, v95
	v_med3_f32 v240, v240, s62, v95
	v_med3_f32 v241, v241, s62, v95
	v_mov_b32_e32 v242, 0
	v_mov_b32_e32 v243, 0
	v_mov_b32_e32 v244, 0
	v_mov_b32_e32 v245, 0
	v_cvt_pk_fp8_f32 v242, v226, v227
	v_cvt_pk_fp8_f32 v243, v230, v231
	v_cvt_pk_fp8_f32 v244, v234, v235
	v_cvt_pk_fp8_f32 v245, v238, v239
	v_cvt_pk_fp8_f32 v242, v228, v229 op_sel:[0,0,1]
	v_cvt_pk_fp8_f32 v243, v232, v233 op_sel:[0,0,1]
	v_cvt_pk_fp8_f32 v244, v236, v237 op_sel:[0,0,1]
	v_cvt_pk_fp8_f32 v245, v240, v241 op_sel:[0,0,1]
	s_nop 0
	global_store_dwordx4 v80, v[242:245], s[6:7]
	s_waitcnt vmcnt(12)
	v_mul_f32_e32 v144, 0x43000000, v144
	v_mul_f32_e32 v145, 0x43000000, v145
	v_mul_f32_e32 v146, 0x43000000, v146
	v_mul_f32_e32 v147, 0x43000000, v147
	ds_write_b128 v209, v[144:147]
	v_mul_f32_e32 v148, 0x43000000, v148
	v_mul_f32_e32 v149, 0x43000000, v149
	v_mul_f32_e32 v150, 0x43000000, v150
	v_mul_f32_e32 v151, 0x43000000, v151
	ds_write_b128 v209, v[148:151] offset:1024
	v_mul_f32_e32 v152, 0x43000000, v152
	v_mul_f32_e32 v153, 0x43000000, v153
	v_mul_f32_e32 v154, 0x43000000, v154
	v_mul_f32_e32 v155, 0x43000000, v155
	ds_write_b128 v209, v[152:155] offset:2048
	v_mul_f32_e32 v156, 0x43000000, v156
	v_mul_f32_e32 v157, 0x43000000, v157
	v_mul_f32_e32 v158, 0x43000000, v158
	v_mul_f32_e32 v159, 0x43000000, v159
	ds_write_b128 v209, v[156:159] offset:3072
	v_mul_f32_e32 v160, 0x43000000, v160
	v_mul_f32_e32 v161, 0x43000000, v161
	v_mul_f32_e32 v162, 0x43000000, v162
	v_mul_f32_e32 v163, 0x43000000, v163
	ds_write_b128 v209, v[160:163] offset:4096
	v_mul_f32_e32 v164, 0x43000000, v164
	v_mul_f32_e32 v165, 0x43000000, v165
	v_mul_f32_e32 v166, 0x43000000, v166
	v_mul_f32_e32 v167, 0x43000000, v167
	ds_write_b128 v209, v[164:167] offset:5120
	v_mul_f32_e32 v168, 0x43000000, v168
	v_mul_f32_e32 v169, 0x43000000, v169
	v_mul_f32_e32 v170, 0x43000000, v170
	v_mul_f32_e32 v171, 0x43000000, v171
	ds_write_b128 v209, v[168:171] offset:6144
	v_mul_f32_e32 v172, 0x43000000, v172
	v_mul_f32_e32 v173, 0x43000000, v173
	v_mul_f32_e32 v174, 0x43000000, v174
	v_mul_f32_e32 v175, 0x43000000, v175
	ds_write_b128 v209, v[172:175] offset:7168
	s_waitcnt lgkmcnt(0)
	s_barrier
; #define GAS __attribute__((address_space(1)))
; #define LAS __attribute__((address_space(3)))
; #define LDS_WAIT() asm volatile("s_waitcnt lgkmcnt(0)" ::: "memory")
;     const int pr = item >> 1, kb = 2 * (pr / nblk) + (item & 1), nb = pr % nblk, k0 = 64 * kb, n0 = 32 * nb;
;     const int nr = n0 + (lane & 31); const int sc = MAP == 1 ? src_col_in(nr) : nr;
;     float v[32];
; #pragma unroll
;     for (int i = 0; i < 32; ++i) v[i] = sc >= 0 ? W[(size_t)(k0 + 2 * i + (lane >> 5)) * Nsrc + sc] : 0.f;
; #pragma unroll
;     for (int i = 0; i < 32; ++i) { const int k = k0 + 2 * i + (lane >> 5); float x = v[i] * wscale; if (KS) x *= (k < ksplit ? ksA[k] : ksB[k - ksplit]); scr[(2 * i + (lane >> 5)) * 33 + (lane & 31)] = x; }
;     LDS_WAIT(); asm volatile("" ::: "memory");
;     const int c = lane & 7;
; #pragma unroll
;     for (int j = 0; j < 4; ++j) { const int n = (lane >> 3) + 8 * j; const LAS float* s = scr + (8 * c) * 33 + n;
;         const unsigned long long o = (unsigned long long)pg8::pk4_fp8(s[0 * 33], s[1 * 33], s[2 * 33], s[3 * 33]) | ((unsigned long long)pg8::pk4_fp8(s[4 * 33], s[5 * 33], s[6 * 33], s[7 * 33]) << 32);
;         *(GAS unsigned long long*)(WT + (size_t)(n0 + n) * K + k0 + 8 * c) = o; }
;     LDS_WAIT(); asm volatile("" ::: "memory");
; }
	s_add_u32 s8, s38, 0x4000000
	s_addc_u32 s9, s39, 0
	global_load_dwordx4 v[144:147], v75, s[8:9]
	s_add_u32 s8, s8, 0x8000
	s_addc_u32 s9, s9, 0
	global_load_dwordx4 v[148:151], v75, s[8:9]
	s_add_u32 s8, s8, 0x8000
	s_addc_u32 s9, s9, 0
	global_load_dwordx4 v[152:155], v75, s[8:9]
	s_add_u32 s8, s8, 0x8000
	s_addc_u32 s9, s9, 0
	global_load_dwordx4 v[156:159], v75, s[8:9]
	s_add_u32 s8, s8, 0x8000
	s_addc_u32 s9, s9, 0
	global_load_dwordx4 v[160:163], v75, s[8:9]
	s_add_u32 s8, s8, 0x8000
	s_addc_u32 s9, s9, 0
	global_load_dwordx4 v[164:167], v75, s[8:9]
	s_add_u32 s8, s8, 0x8000
	s_addc_u32 s9, s9, 0
	global_load_dwordx4 v[168:171], v75, s[8:9]
	s_add_u32 s8, s8, 0x8000
	s_addc_u32 s9, s9, 0
	global_load_dwordx4 v[172:175], v75, s[8:9]
	s_add_u32 s6, s40, 0x2000000
	s_addc_u32 s7, s41, 0
	ds_read_b32 v226, v211
	ds_read_b32 v227, v211 offset:512
	ds_read_b32 v228, v211 offset:1024
	ds_read_b32 v229, v211 offset:1536
	ds_read_b32 v230, v211 offset:2048
	ds_read_b32 v231, v211 offset:2560
	ds_read_b32 v232, v211 offset:3072
	ds_read_b32 v233, v211 offset:3584
	ds_read_b32 v234, v211 offset:4096
	ds_read_b32 v235, v211 offset:4608
	ds_read_b32 v236, v211 offset:5120
	ds_read_b32 v237, v211 offset:5632
	ds_read_b32 v238, v211 offset:6144
	ds_read_b32 v239, v211 offset:6656
	ds_read_b32 v240, v211 offset:7168
	ds_read_b32 v241, v211 offset:7680
	s_waitcnt lgkmcnt(0)
	v_max_f32_e32 v226, v226, v226
	v_max_f32_e32 v227, v227, v227
	v_max_f32_e32 v228, v228, v228
	v_max_f32_e32 v229, v229, v229
	v_max_f32_e32 v230, v230, v230
	v_max_f32_e32 v231, v231, v231
	v_max_f32_e32 v232, v232, v232
	v_max_f32_e32 v233, v233, v233
	v_max_f32_e32 v234, v234, v234
	v_max_f32_e32 v235, v235, v235
	v_max_f32_e32 v236, v236, v236
	v_max_f32_e32 v237, v237, v237
	v_max_f32_e32 v238, v238, v238
	v_max_f32_e32 v239, v239, v239
	v_max_f32_e32 v240, v240, v240
	v_max_f32_e32 v241, v241, v241
	v_med3_f32 v226, v226, s62, v95
	v_med3_f32 v227, v227, s62, v95
	v_med3_f32 v228, v228, s62, v95
	v_med3_f32 v229, v229, s62, v95
	v_med3_f32 v230, v230, s62, v95
	v_med3_f32 v231, v231, s62, v95
	v_med3_f32 v232, v232, s62, v95
	v_med3_f32 v233, v233, s62, v95
	v_med3_f32 v234, v234, s62, v95
	v_med3_f32 v235, v235, s62, v95
	v_med3_f32 v236, v236, s62, v95
	v_med3_f32 v237, v237, s62, v95
	v_med3_f32 v238, v238, s62, v95
	v_med3_f32 v239, v239, s62, v95
	v_med3_f32 v240, v240, s62, v95
	v_med3_f32 v241, v241, s62, v95
	v_mov_b32_e32 v242, 0
	v_mov_b32_e32 v243, 0
	v_mov_b32_e32 v244, 0
	v_mov_b32_e32 v245, 0
	v_cvt_pk_fp8_f32 v242, v226, v227
	v_cvt_pk_fp8_f32 v243, v230, v231
	v_cvt_pk_fp8_f32 v244, v234, v235
	v_cvt_pk_fp8_f32 v245, v238, v239
	v_cvt_pk_fp8_f32 v242, v228, v229 op_sel:[0,0,1]
	v_cvt_pk_fp8_f32 v243, v232, v233 op_sel:[0,0,1]
	v_cvt_pk_fp8_f32 v244, v236, v237 op_sel:[0,0,1]
	v_cvt_pk_fp8_f32 v245, v240, v241 op_sel:[0,0,1]
	s_nop 0
	global_store_dwordx4 v79, v[242:245], s[6:7]
	ds_read_b32 v226, v213
	ds_read_b32 v227, v213 offset:512
	ds_read_b32 v228, v213 offset:1024
	ds_read_b32 v229, v213 offset:1536
	ds_read_b32 v230, v213 offset:2048
	ds_read_b32 v231, v213 offset:2560
	ds_read_b32 v232, v213 offset:3072
	ds_read_b32 v233, v213 offset:3584
	ds_read_b32 v234, v213 offset:4096
	ds_read_b32 v235, v213 offset:4608
	ds_read_b32 v236, v213 offset:5120
	ds_read_b32 v237, v213 offset:5632
	ds_read_b32 v238, v213 offset:6144
	ds_read_b32 v239, v213 offset:6656
	ds_read_b32 v240, v213 offset:7168
	ds_read_b32 v241, v213 offset:7680
	s_waitcnt lgkmcnt(0)
	v_max_f32_e32 v226, v226, v226
	v_max_f32_e32 v227, v227, v227
	v_max_f32_e32 v228, v228, v228
	v_max_f32_e32 v229, v229, v229
	v_max_f32_e32 v230, v230, v230
	v_max_f32_e32 v231, v231, v231
	v_max_f32_e32 v232, v232, v232
	v_max_f32_e32 v233, v233, v233
	v_max_f32_e32 v234, v234, v234
	v_max_f32_e32 v235, v235, v235
	v_max_f32_e32 v236, v236, v236
	v_max_f32_e32 v237, v237, v237
	v_max_f32_e32 v238, v238, v238
	v_max_f32_e32 v239, v239, v239
	v_max_f32_e32 v240, v240, v240
	v_max_f32_e32 v241, v241, v241
	v_med3_f32 v226, v226, s62, v95
	v_med3_f32 v227, v227, s62, v95
	v_med3_f32 v228, v228, s62, v95
	v_med3_f32 v229, v229, s62, v95
	v_med3_f32 v230, v230, s62, v95
	v_med3_f32 v231, v231, s62, v95
	v_med3_f32 v232, v232, s62, v95
	v_med3_f32 v233, v233, s62, v95
	v_med3_f32 v234, v234, s62, v95
	v_med3_f32 v235, v235, s62, v95
	v_med3_f32 v236, v236, s62, v95
	v_med3_f32 v237, v237, s62, v95
	v_med3_f32 v238, v238, s62, v95
	v_med3_f32 v239, v239, s62, v95
	v_med3_f32 v240, v240, s62, v95
	v_med3_f32 v241, v241, s62, v95
	v_mov_b32_e32 v242, 0
	v_mov_b32_e32 v243, 0
	v_mov_b32_e32 v244, 0
	v_mov_b32_e32 v245, 0
	v_cvt_pk_fp8_f32 v242, v226, v227
	v_cvt_pk_fp8_f32 v243, v230, v231
	v_cvt_pk_fp8_f32 v244, v234, v235
	v_cvt_pk_fp8_f32 v245, v238, v239
	v_cvt_pk_fp8_f32 v242, v228, v229 op_sel:[0,0,1]
	v_cvt_pk_fp8_f32 v243, v232, v233 op_sel:[0,0,1]
	v_cvt_pk_fp8_f32 v244, v236, v237 op_sel:[0,0,1]
	v_cvt_pk_fp8_f32 v245, v240, v241 op_sel:[0,0,1]
	s_nop 0
	global_store_dwordx4 v80, v[242:245], s[6:7]
	s_waitcnt vmcnt(12)
	v_mul_f32_e32 v176, 0x43000000, v176
	v_mul_f32_e32 v177, 0x43000000, v177
	v_mul_f32_e32 v178, 0x43000000, v178
	v_mul_f32_e32 v179, 0x43000000, v179
	ds_write_b128 v210, v[176:179]
	v_mul_f32_e32 v180, 0x43000000, v180
	v_mul_f32_e32 v181, 0x43000000, v181
	v_mul_f32_e32 v182, 0x43000000, v182
	v_mul_f32_e32 v183, 0x43000000, v183
	ds_write_b128 v210, v[180:183] offset:1024
	v_mul_f32_e32 v184, 0x43000000, v184
	v_mul_f32_e32 v185, 0x43000000, v185
	v_mul_f32_e32 v186, 0x43000000, v186
	v_mul_f32_e32 v187, 0x43000000, v187
	ds_write_b128 v210, v[184:187] offset:2048
	v_mul_f32_e32 v188, 0x43000000, v188
	v_mul_f32_e32 v189, 0x43000000, v189
	v_mul_f32_e32 v190, 0x43000000, v190
	v_mul_f32_e32 v191, 0x43000000, v191
	ds_write_b128 v210, v[188:191] offset:3072
	v_mul_f32_e32 v192, 0x43000000, v192
	v_mul_f32_e32 v193, 0x43000000, v193
	v_mul_f32_e32 v194, 0x43000000, v194
	v_mul_f32_e32 v195, 0x43000000, v195
	ds_write_b128 v210, v[192:195] offset:4096
	v_mul_f32_e32 v196, 0x43000000, v196
	v_mul_f32_e32 v197, 0x43000000, v197
	v_mul_f32_e32 v198, 0x43000000, v198
	v_mul_f32_e32 v199, 0x43000000, v199
	ds_write_b128 v210, v[196:199] offset:5120
	v_mul_f32_e32 v200, 0x43000000, v200
	v_mul_f32_e32 v201, 0x43000000, v201
	v_mul_f32_e32 v202, 0x43000000, v202
	v_mul_f32_e32 v203, 0x43000000, v203
	ds_write_b128 v210, v[200:203] offset:6144
	v_mul_f32_e32 v204, 0x43000000, v204
	v_mul_f32_e32 v205, 0x43000000, v205
	v_mul_f32_e32 v206, 0x43000000, v206
	v_mul_f32_e32 v207, 0x43000000, v207
	ds_write_b128 v210, v[204:207] offset:7168
	s_waitcnt lgkmcnt(0)
	s_barrier
; #define GAS __attribute__((address_space(1)))
; #define LAS __attribute__((address_space(3)))
; #define LDS_WAIT() asm volatile("s_waitcnt lgkmcnt(0)" ::: "memory")
;     const int pr = item >> 1, kb = 2 * (pr / nblk) + (item & 1), nb = pr % nblk, k0 = 64 * kb, n0 = 32 * nb;
;     const int nr = n0 + (lane & 31); const int sc = MAP == 1 ? src_col_in(nr) : nr;
;     float v[32];
; #pragma unroll
;     for (int i = 0; i < 32; ++i) v[i] = sc >= 0 ? W[(size_t)(k0 + 2 * i + (lane >> 5)) * Nsrc + sc] : 0.f;
; #pragma unroll
;     for (int i = 0; i < 32; ++i) { const int k = k0 + 2 * i + (lane >> 5); float x = v[i] * wscale; if (KS) x *= (k < ksplit ? ksA[k] : ksB[k - ksplit]); scr[(2 * i + (lane >> 5)) * 33 + (lane & 31)] = x; }
;     LDS_WAIT(); asm volatile("" ::: "memory");
;     const int c = lane & 7;
; #pragma unroll
;     for (int j = 0; j < 4; ++j) { const int n = (lane >> 3) + 8 * j; const LAS float* s = scr + (8 * c) * 33 + n;
;         const unsigned long long o = (unsigned long long)pg8::pk4_fp8(s[0 * 33], s[1 * 33], s[2 * 33], s[3 * 33]) | ((unsigned long long)pg8::pk4_fp8(s[4 * 33], s[5 * 33], s[6 * 33], s[7 * 33]) << 32);
;         *(GAS unsigned long long*)(WT + (size_t)(n0 + n) * K + k0 + 8 * c) = o; }
;     LDS_WAIT(); asm volatile("" ::: "memory");
; }
	s_add_u32 s8, s38, 0x4001000
	s_addc_u32 s9, s39, 0
	global_load_dwordx4 v[176:179], v75, s[8:9]
	s_add_u32 s8, s8, 0x8000
	s_addc_u32 s9, s9, 0
	global_load_dwordx4 v[180:183], v75, s[8:9]
	s_add_u32 s8, s8, 0x8000
	s_addc_u32 s9, s9, 0
	global_load_dwordx4 v[184:187], v75, s[8:9]
	s_add_u32 s8, s8, 0x8000
	s_addc_u32 s9, s9, 0
	global_load_dwordx4 v[188:191], v75, s[8:9]
	s_add_u32 s8, s8, 0x8000
	s_addc_u32 s9, s9, 0
	global_load_dwordx4 v[192:195], v75, s[8:9]
	s_add_u32 s8, s8, 0x8000
	s_addc_u32 s9, s9, 0
	global_load_dwordx4 v[196:199], v75, s[8:9]
	s_add_u32 s8, s8, 0x8000
	s_addc_u32 s9, s9, 0
	global_load_dwordx4 v[200:203], v75, s[8:9]
	s_add_u32 s8, s8, 0x8000
	s_addc_u32 s9, s9, 0
	global_load_dwordx4 v[204:207], v75, s[8:9]
	s_add_u32 s6, s40, 0x3000000
	s_addc_u32 s7, s41, 0
	ds_read_b32 v226, v212
	ds_read_b32 v227, v212 offset:512
	ds_read_b32 v228, v212 offset:1024
	ds_read_b32 v229, v212 offset:1536
	ds_read_b32 v230, v212 offset:2048
	ds_read_b32 v231, v212 offset:2560
	ds_read_b32 v232, v212 offset:3072
	ds_read_b32 v233, v212 offset:3584
	ds_read_b32 v234, v212 offset:4096
	ds_read_b32 v235, v212 offset:4608
	ds_read_b32 v236, v212 offset:5120
	ds_read_b32 v237, v212 offset:5632
	ds_read_b32 v238, v212 offset:6144
	ds_read_b32 v239, v212 offset:6656
	ds_read_b32 v240, v212 offset:7168
	ds_read_b32 v241, v212 offset:7680
	s_waitcnt lgkmcnt(0)
	v_max_f32_e32 v226, v226, v226
	v_max_f32_e32 v227, v227, v227
	v_max_f32_e32 v228, v228, v228
	v_max_f32_e32 v229, v229, v229
	v_max_f32_e32 v230, v230, v230
	v_max_f32_e32 v231, v231, v231
	v_max_f32_e32 v232, v232, v232
	v_max_f32_e32 v233, v233, v233
	v_max_f32_e32 v234, v234, v234
	v_max_f32_e32 v235, v235, v235
	v_max_f32_e32 v236, v236, v236
	v_max_f32_e32 v237, v237, v237
	v_max_f32_e32 v238, v238, v238
	v_max_f32_e32 v239, v239, v239
	v_max_f32_e32 v240, v240, v240
	v_max_f32_e32 v241, v241, v241
	v_med3_f32 v226, v226, s62, v95
	v_med3_f32 v227, v227, s62, v95
	v_med3_f32 v228, v228, s62, v95
	v_med3_f32 v229, v229, s62, v95
	v_med3_f32 v230, v230, s62, v95
	v_med3_f32 v231, v231, s62, v95
	v_med3_f32 v232, v232, s62, v95
	v_med3_f32 v233, v233, s62, v95
	v_med3_f32 v234, v234, s62, v95
	v_med3_f32 v235, v235, s62, v95
	v_med3_f32 v236, v236, s62, v95
	v_med3_f32 v237, v237, s62, v95
	v_med3_f32 v238, v238, s62, v95
	v_med3_f32 v239, v239, s62, v95
	v_med3_f32 v240, v240, s62, v95
	v_med3_f32 v241, v241, s62, v95
	v_mov_b32_e32 v242, 0
	v_mov_b32_e32 v243, 0
	v_mov_b32_e32 v244, 0
	v_mov_b32_e32 v245, 0
	v_cvt_pk_fp8_f32 v242, v226, v227
	v_cvt_pk_fp8_f32 v243, v230, v231
	v_cvt_pk_fp8_f32 v244, v234, v235
	v_cvt_pk_fp8_f32 v245, v238, v239
	v_cvt_pk_fp8_f32 v242, v228, v229 op_sel:[0,0,1]
	v_cvt_pk_fp8_f32 v243, v232, v233 op_sel:[0,0,1]
	v_cvt_pk_fp8_f32 v244, v236, v237 op_sel:[0,0,1]
	v_cvt_pk_fp8_f32 v245, v240, v241 op_sel:[0,0,1]
	s_nop 0
	global_store_dwordx4 v79, v[242:245], s[6:7]
	ds_read_b32 v226, v214
	ds_read_b32 v227, v214 offset:512
	ds_read_b32 v228, v214 offset:1024
	ds_read_b32 v229, v214 offset:1536
	ds_read_b32 v230, v214 offset:2048
	ds_read_b32 v231, v214 offset:2560
	ds_read_b32 v232, v214 offset:3072
	ds_read_b32 v233, v214 offset:3584
	ds_read_b32 v234, v214 offset:4096
	ds_read_b32 v235, v214 offset:4608
	ds_read_b32 v236, v214 offset:5120
	ds_read_b32 v237, v214 offset:5632
	ds_read_b32 v238, v214 offset:6144
	ds_read_b32 v239, v214 offset:6656
	ds_read_b32 v240, v214 offset:7168
	ds_read_b32 v241, v214 offset:7680
	s_waitcnt lgkmcnt(0)
	v_max_f32_e32 v226, v226, v226
	v_max_f32_e32 v227, v227, v227
	v_max_f32_e32 v228, v228, v228
	v_max_f32_e32 v229, v229, v229
	v_max_f32_e32 v230, v230, v230
	v_max_f32_e32 v231, v231, v231
	v_max_f32_e32 v232, v232, v232
	v_max_f32_e32 v233, v233, v233
	v_max_f32_e32 v234, v234, v234
	v_max_f32_e32 v235, v235, v235
	v_max_f32_e32 v236, v236, v236
	v_max_f32_e32 v237, v237, v237
	v_max_f32_e32 v238, v238, v238
	v_max_f32_e32 v239, v239, v239
	v_max_f32_e32 v240, v240, v240
	v_max_f32_e32 v241, v241, v241
	v_med3_f32 v226, v226, s62, v95
	v_med3_f32 v227, v227, s62, v95
	v_med3_f32 v228, v228, s62, v95
	v_med3_f32 v229, v229, s62, v95
	v_med3_f32 v230, v230, s62, v95
	v_med3_f32 v231, v231, s62, v95
	v_med3_f32 v232, v232, s62, v95
	v_med3_f32 v233, v233, s62, v95
	v_med3_f32 v234, v234, s62, v95
	v_med3_f32 v235, v235, s62, v95
	v_med3_f32 v236, v236, s62, v95
	v_med3_f32 v237, v237, s62, v95
	v_med3_f32 v238, v238, s62, v95
	v_med3_f32 v239, v239, s62, v95
	v_med3_f32 v240, v240, s62, v95
	v_med3_f32 v241, v241, s62, v95
	v_mov_b32_e32 v242, 0
	v_mov_b32_e32 v243, 0
	v_mov_b32_e32 v244, 0
	v_mov_b32_e32 v245, 0
	v_cvt_pk_fp8_f32 v242, v226, v227
	v_cvt_pk_fp8_f32 v243, v230, v231
	v_cvt_pk_fp8_f32 v244, v234, v235
	v_cvt_pk_fp8_f32 v245, v238, v239
	v_cvt_pk_fp8_f32 v242, v228, v229 op_sel:[0,0,1]
	v_cvt_pk_fp8_f32 v243, v232, v233 op_sel:[0,0,1]
	v_cvt_pk_fp8_f32 v244, v236, v237 op_sel:[0,0,1]
	v_cvt_pk_fp8_f32 v245, v240, v241 op_sel:[0,0,1]
	s_nop 0
	global_store_dwordx4 v80, v[242:245], s[6:7]
	s_waitcnt vmcnt(12)
	v_mul_f32_e32 v144, 0x43000000, v144
	v_mul_f32_e32 v145, 0x43000000, v145
	v_mul_f32_e32 v146, 0x43000000, v146
	v_mul_f32_e32 v147, 0x43000000, v147
	ds_write_b128 v209, v[144:147]
	v_mul_f32_e32 v148, 0x43000000, v148
	v_mul_f32_e32 v149, 0x43000000, v149
	v_mul_f32_e32 v150, 0x43000000, v150
	v_mul_f32_e32 v151, 0x43000000, v151
	ds_write_b128 v209, v[148:151] offset:1024
	v_mul_f32_e32 v152, 0x43000000, v152
	v_mul_f32_e32 v153, 0x43000000, v153
	v_mul_f32_e32 v154, 0x43000000, v154
	v_mul_f32_e32 v155, 0x43000000, v155
	ds_write_b128 v209, v[152:155] offset:2048
	v_mul_f32_e32 v156, 0x43000000, v156
	v_mul_f32_e32 v157, 0x43000000, v157
	v_mul_f32_e32 v158, 0x43000000, v158
	v_mul_f32_e32 v159, 0x43000000, v159
	ds_write_b128 v209, v[156:159] offset:3072
	v_mul_f32_e32 v160, 0x43000000, v160
	v_mul_f32_e32 v161, 0x43000000, v161
	v_mul_f32_e32 v162, 0x43000000, v162
	v_mul_f32_e32 v163, 0x43000000, v163
	ds_write_b128 v209, v[160:163] offset:4096
	v_mul_f32_e32 v164, 0x43000000, v164
	v_mul_f32_e32 v165, 0x43000000, v165
	v_mul_f32_e32 v166, 0x43000000, v166
	v_mul_f32_e32 v167, 0x43000000, v167
	ds_write_b128 v209, v[164:167] offset:5120
	v_mul_f32_e32 v168, 0x43000000, v168
	v_mul_f32_e32 v169, 0x43000000, v169
	v_mul_f32_e32 v170, 0x43000000, v170
	v_mul_f32_e32 v171, 0x43000000, v171
	ds_write_b128 v209, v[168:171] offset:6144
	v_mul_f32_e32 v172, 0x43000000, v172
	v_mul_f32_e32 v173, 0x43000000, v173
	v_mul_f32_e32 v174, 0x43000000, v174
	v_mul_f32_e32 v175, 0x43000000, v175
	ds_write_b128 v209, v[172:175] offset:7168
	s_waitcnt lgkmcnt(0)
	s_barrier
; #define GAS __attribute__((address_space(1)))
; #define LAS __attribute__((address_space(3)))
; #define LDS_WAIT() asm volatile("s_waitcnt lgkmcnt(0)" ::: "memory")
;     const int pr = item >> 1, kb = 2 * (pr / nblk) + (item & 1), nb = pr % nblk, k0 = 64 * kb, n0 = 32 * nb;
;     const int nr = n0 + (lane & 31); const int sc = MAP == 1 ? src_col_in(nr) : nr;
;     float v[32];
; #pragma unroll
;     for (int i = 0; i < 32; ++i) v[i] = sc >= 0 ? W[(size_t)(k0 + 2 * i + (lane >> 5)) * Nsrc + sc] : 0.f;
; #pragma unroll
;     for (int i = 0; i < 32; ++i) { const int k = k0 + 2 * i + (lane >> 5); float x = v[i] * wscale; if (KS) x *= (k < ksplit ? ksA[k] : ksB[k - ksplit]); scr[(2 * i + (lane >> 5)) * 33 + (lane & 31)] = x; }
;     LDS_WAIT(); asm volatile("" ::: "memory");
;     const int c = lane & 7;
; #pragma unroll
;     for (int j = 0; j < 4; ++j) { const int n = (lane >> 3) + 8 * j; const LAS float* s = scr + (8 * c) * 33 + n;
;         const unsigned long long o = (unsigned long long)pg8::pk4_fp8(s[0 * 33], s[1 * 33], s[2 * 33], s[3 * 33]) | ((unsigned long long)pg8::pk4_fp8(s[4 * 33], s[5 * 33], s[6 * 33], s[7 * 33]) << 32);
;         *(GAS unsigned long long*)(WT + (size_t)(n0 + n) * K + k0 + 8 * c) = o; }
;     LDS_WAIT(); asm volatile("" ::: "memory");
; }
	s_add_u32 s8, s38, 0x4002000
	s_addc_u32 s9, s39, 0
	global_load_dwordx4 v[144:147], v75, s[8:9]
	s_add_u32 s8, s8, 0x8000
	s_addc_u32 s9, s9, 0
	global_load_dwordx4 v[148:151], v75, s[8:9]
	s_add_u32 s8, s8, 0x8000
	s_addc_u32 s9, s9, 0
	global_load_dwordx4 v[152:155], v75, s[8:9]
	s_add_u32 s8, s8, 0x8000
	s_addc_u32 s9, s9, 0
	global_load_dwordx4 v[156:159], v75, s[8:9]
	s_add_u32 s8, s8, 0x8000
	s_addc_u32 s9, s9, 0
	global_load_dwordx4 v[160:163], v75, s[8:9]
	s_add_u32 s8, s8, 0x8000
	s_addc_u32 s9, s9, 0
	global_load_dwordx4 v[164:167], v75, s[8:9]
	s_add_u32 s8, s8, 0x8000
	s_addc_u32 s9, s9, 0
	global_load_dwordx4 v[168:171], v75, s[8:9]
	s_add_u32 s8, s8, 0x8000
	s_addc_u32 s9, s9, 0
	global_load_dwordx4 v[172:175], v75, s[8:9]
	s_add_u32 s6, s40, 0x1000
	s_addc_u32 s7, s41, 0
	ds_read_b32 v226, v211
	ds_read_b32 v227, v211 offset:512
	ds_read_b32 v228, v211 offset:1024
	ds_read_b32 v229, v211 offset:1536
	ds_read_b32 v230, v211 offset:2048
	ds_read_b32 v231, v211 offset:2560
	ds_read_b32 v232, v211 offset:3072
	ds_read_b32 v233, v211 offset:3584
	ds_read_b32 v234, v211 offset:4096
	ds_read_b32 v235, v211 offset:4608
	ds_read_b32 v236, v211 offset:5120
	ds_read_b32 v237, v211 offset:5632
	ds_read_b32 v238, v211 offset:6144
	ds_read_b32 v239, v211 offset:6656
	ds_read_b32 v240, v211 offset:7168
	ds_read_b32 v241, v211 offset:7680
	s_waitcnt lgkmcnt(0)
	v_max_f32_e32 v226, v226, v226
	v_max_f32_e32 v227, v227, v227
	v_max_f32_e32 v228, v228, v228
	v_max_f32_e32 v229, v229, v229
	v_max_f32_e32 v230, v230, v230
	v_max_f32_e32 v231, v231, v231
	v_max_f32_e32 v232, v232, v232
	v_max_f32_e32 v233, v233, v233
	v_max_f32_e32 v234, v234, v234
	v_max_f32_e32 v235, v235, v235
	v_max_f32_e32 v236, v236, v236
	v_max_f32_e32 v237, v237, v237
	v_max_f32_e32 v238, v238, v238
	v_max_f32_e32 v239, v239, v239
	v_max_f32_e32 v240, v240, v240
	v_max_f32_e32 v241, v241, v241
	v_med3_f32 v226, v226, s62, v95
	v_med3_f32 v227, v227, s62, v95
	v_med3_f32 v228, v228, s62, v95
	v_med3_f32 v229, v229, s62, v95
	v_med3_f32 v230, v230, s62, v95
	v_med3_f32 v231, v231, s62, v95
	v_med3_f32 v232, v232, s62, v95
	v_med3_f32 v233, v233, s62, v95
	v_med3_f32 v234, v234, s62, v95
	v_med3_f32 v235, v235, s62, v95
	v_med3_f32 v236, v236, s62, v95
	v_med3_f32 v237, v237, s62, v95
	v_med3_f32 v238, v238, s62, v95
	v_med3_f32 v239, v239, s62, v95
	v_med3_f32 v240, v240, s62, v95
	v_med3_f32 v241, v241, s62, v95
	v_mov_b32_e32 v242, 0
	v_mov_b32_e32 v243, 0
	v_mov_b32_e32 v244, 0
	v_mov_b32_e32 v245, 0
	v_cvt_pk_fp8_f32 v242, v226, v227
	v_cvt_pk_fp8_f32 v243, v230, v231
	v_cvt_pk_fp8_f32 v244, v234, v235
	v_cvt_pk_fp8_f32 v245, v238, v239
	v_cvt_pk_fp8_f32 v242, v228, v229 op_sel:[0,0,1]
	v_cvt_pk_fp8_f32 v243, v232, v233 op_sel:[0,0,1]
	v_cvt_pk_fp8_f32 v244, v236, v237 op_sel:[0,0,1]
	v_cvt_pk_fp8_f32 v245, v240, v241 op_sel:[0,0,1]
	s_nop 0
	global_store_dwordx4 v79, v[242:245], s[6:7]
	ds_read_b32 v226, v213
	ds_read_b32 v227, v213 offset:512
	ds_read_b32 v228, v213 offset:1024
	ds_read_b32 v229, v213 offset:1536
	ds_read_b32 v230, v213 offset:2048
	ds_read_b32 v231, v213 offset:2560
	ds_read_b32 v232, v213 offset:3072
	ds_read_b32 v233, v213 offset:3584
	ds_read_b32 v234, v213 offset:4096
	ds_read_b32 v235, v213 offset:4608
	ds_read_b32 v236, v213 offset:5120
	ds_read_b32 v237, v213 offset:5632
	ds_read_b32 v238, v213 offset:6144
	ds_read_b32 v239, v213 offset:6656
	ds_read_b32 v240, v213 offset:7168
	ds_read_b32 v241, v213 offset:7680
	s_waitcnt lgkmcnt(0)
	v_max_f32_e32 v226, v226, v226
	v_max_f32_e32 v227, v227, v227
	v_max_f32_e32 v228, v228, v228
	v_max_f32_e32 v229, v229, v229
	v_max_f32_e32 v230, v230, v230
	v_max_f32_e32 v231, v231, v231
	v_max_f32_e32 v232, v232, v232
	v_max_f32_e32 v233, v233, v233
	v_max_f32_e32 v234, v234, v234
	v_max_f32_e32 v235, v235, v235
	v_max_f32_e32 v236, v236, v236
	v_max_f32_e32 v237, v237, v237
	v_max_f32_e32 v238, v238, v238
	v_max_f32_e32 v239, v239, v239
	v_max_f32_e32 v240, v240, v240
	v_max_f32_e32 v241, v241, v241
	v_med3_f32 v226, v226, s62, v95
	v_med3_f32 v227, v227, s62, v95
	v_med3_f32 v228, v228, s62, v95
	v_med3_f32 v229, v229, s62, v95
	v_med3_f32 v230, v230, s62, v95
	v_med3_f32 v231, v231, s62, v95
	v_med3_f32 v232, v232, s62, v95
	v_med3_f32 v233, v233, s62, v95
	v_med3_f32 v234, v234, s62, v95
	v_med3_f32 v235, v235, s62, v95
	v_med3_f32 v236, v236, s62, v95
	v_med3_f32 v237, v237, s62, v95
	v_med3_f32 v238, v238, s62, v95
	v_med3_f32 v239, v239, s62, v95
	v_med3_f32 v240, v240, s62, v95
	v_med3_f32 v241, v241, s62, v95
	v_mov_b32_e32 v242, 0
	v_mov_b32_e32 v243, 0
	v_mov_b32_e32 v244, 0
	v_mov_b32_e32 v245, 0
	v_cvt_pk_fp8_f32 v242, v226, v227
	v_cvt_pk_fp8_f32 v243, v230, v231
	v_cvt_pk_fp8_f32 v244, v234, v235
	v_cvt_pk_fp8_f32 v245, v238, v239
	v_cvt_pk_fp8_f32 v242, v228, v229 op_sel:[0,0,1]
	v_cvt_pk_fp8_f32 v243, v232, v233 op_sel:[0,0,1]
	v_cvt_pk_fp8_f32 v244, v236, v237 op_sel:[0,0,1]
	v_cvt_pk_fp8_f32 v245, v240, v241 op_sel:[0,0,1]
	s_nop 0
	global_store_dwordx4 v80, v[242:245], s[6:7]
	s_waitcnt vmcnt(12)
	v_mul_f32_e32 v176, 0x43000000, v176
	v_mul_f32_e32 v177, 0x43000000, v177
	v_mul_f32_e32 v178, 0x43000000, v178
	v_mul_f32_e32 v179, 0x43000000, v179
	ds_write_b128 v210, v[176:179]
	v_mul_f32_e32 v180, 0x43000000, v180
	v_mul_f32_e32 v181, 0x43000000, v181
	v_mul_f32_e32 v182, 0x43000000, v182
	v_mul_f32_e32 v183, 0x43000000, v183
	ds_write_b128 v210, v[180:183] offset:1024
	v_mul_f32_e32 v184, 0x43000000, v184
	v_mul_f32_e32 v185, 0x43000000, v185
	v_mul_f32_e32 v186, 0x43000000, v186
	v_mul_f32_e32 v187, 0x43000000, v187
	ds_write_b128 v210, v[184:187] offset:2048
	v_mul_f32_e32 v188, 0x43000000, v188
	v_mul_f32_e32 v189, 0x43000000, v189
	v_mul_f32_e32 v190, 0x43000000, v190
	v_mul_f32_e32 v191, 0x43000000, v191
	ds_write_b128 v210, v[188:191] offset:3072
	v_mul_f32_e32 v192, 0x43000000, v192
	v_mul_f32_e32 v193, 0x43000000, v193
	v_mul_f32_e32 v194, 0x43000000, v194
	v_mul_f32_e32 v195, 0x43000000, v195
	ds_write_b128 v210, v[192:195] offset:4096
	v_mul_f32_e32 v196, 0x43000000, v196
	v_mul_f32_e32 v197, 0x43000000, v197
	v_mul_f32_e32 v198, 0x43000000, v198
	v_mul_f32_e32 v199, 0x43000000, v199
	ds_write_b128 v210, v[196:199] offset:5120
	v_mul_f32_e32 v200, 0x43000000, v200
	v_mul_f32_e32 v201, 0x43000000, v201
	v_mul_f32_e32 v202, 0x43000000, v202
	v_mul_f32_e32 v203, 0x43000000, v203
	ds_write_b128 v210, v[200:203] offset:6144
	v_mul_f32_e32 v204, 0x43000000, v204
	v_mul_f32_e32 v205, 0x43000000, v205
	v_mul_f32_e32 v206, 0x43000000, v206
	v_mul_f32_e32 v207, 0x43000000, v207
	ds_write_b128 v210, v[204:207] offset:7168
	s_waitcnt lgkmcnt(0)
	s_barrier
; #define GAS __attribute__((address_space(1)))
; #define LAS __attribute__((address_space(3)))
; #define LDS_WAIT() asm volatile("s_waitcnt lgkmcnt(0)" ::: "memory")
;     const int pr = item >> 1, kb = 2 * (pr / nblk) + (item & 1), nb = pr % nblk, k0 = 64 * kb, n0 = 32 * nb;
;     const int nr = n0 + (lane & 31); const int sc = MAP == 1 ? src_col_in(nr) : nr;
;     float v[32];
; #pragma unroll
;     for (int i = 0; i < 32; ++i) v[i] = sc >= 0 ? W[(size_t)(k0 + 2 * i + (lane >> 5)) * Nsrc + sc] : 0.f;
; #pragma unroll
;     for (int i = 0; i < 32; ++i) { const int k = k0 + 2 * i + (lane >> 5); float x = v[i] * wscale; if (KS) x *= (k < ksplit ? ksA[k] : ksB[k - ksplit]); scr[(2 * i + (lane >> 5)) * 33 + (lane & 31)] = x; }
;     LDS_WAIT(); asm volatile("" ::: "memory");
;     const int c = lane & 7;
; #pragma unroll
;     for (int j = 0; j < 4; ++j) { const int n = (lane >> 3) + 8 * j; const LAS float* s = scr + (8 * c) * 33 + n;
;         const unsigned long long o = (unsigned long long)pg8::pk4_fp8(s[0 * 33], s[1 * 33], s[2 * 33], s[3 * 33]) | ((unsigned long long)pg8::pk4_fp8(s[4 * 33], s[5 * 33], s[6 * 33], s[7 * 33]) << 32);
;         *(GAS unsigned long long*)(WT + (size_t)(n0 + n) * K + k0 + 8 * c) = o; }
;     LDS_WAIT(); asm volatile("" ::: "memory");
; }
	s_add_u32 s8, s38, 0x4003000
	s_addc_u32 s9, s39, 0
	global_load_dwordx4 v[176:179], v75, s[8:9]
	s_add_u32 s8, s8, 0x8000
	s_addc_u32 s9, s9, 0
	global_load_dwordx4 v[180:183], v75, s[8:9]
	s_add_u32 s8, s8, 0x8000
	s_addc_u32 s9, s9, 0
	global_load_dwordx4 v[184:187], v75, s[8:9]
	s_add_u32 s8, s8, 0x8000
	s_addc_u32 s9, s9, 0
	global_load_dwordx4 v[188:191], v75, s[8:9]
	s_add_u32 s8, s8, 0x8000
	s_addc_u32 s9, s9, 0
	global_load_dwordx4 v[192:195], v75, s[8:9]
	s_add_u32 s8, s8, 0x8000
	s_addc_u32 s9, s9, 0
	global_load_dwordx4 v[196:199], v75, s[8:9]
	s_add_u32 s8, s8, 0x8000
	s_addc_u32 s9, s9, 0
	global_load_dwordx4 v[200:203], v75, s[8:9]
	s_add_u32 s8, s8, 0x8000
	s_addc_u32 s9, s9, 0
	global_load_dwordx4 v[204:207], v75, s[8:9]
	s_add_u32 s6, s40, 0x1001000
	s_addc_u32 s7, s41, 0
	ds_read_b32 v226, v212
	ds_read_b32 v227, v212 offset:512
	ds_read_b32 v228, v212 offset:1024
	ds_read_b32 v229, v212 offset:1536
	ds_read_b32 v230, v212 offset:2048
	ds_read_b32 v231, v212 offset:2560
	ds_read_b32 v232, v212 offset:3072
	ds_read_b32 v233, v212 offset:3584
	ds_read_b32 v234, v212 offset:4096
	ds_read_b32 v235, v212 offset:4608
	ds_read_b32 v236, v212 offset:5120
	ds_read_b32 v237, v212 offset:5632
	ds_read_b32 v238, v212 offset:6144
	ds_read_b32 v239, v212 offset:6656
	ds_read_b32 v240, v212 offset:7168
	ds_read_b32 v241, v212 offset:7680
	s_waitcnt lgkmcnt(0)
	v_max_f32_e32 v226, v226, v226
	v_max_f32_e32 v227, v227, v227
	v_max_f32_e32 v228, v228, v228
	v_max_f32_e32 v229, v229, v229
	v_max_f32_e32 v230, v230, v230
	v_max_f32_e32 v231, v231, v231
	v_max_f32_e32 v232, v232, v232
	v_max_f32_e32 v233, v233, v233
	v_max_f32_e32 v234, v234, v234
	v_max_f32_e32 v235, v235, v235
	v_max_f32_e32 v236, v236, v236
	v_max_f32_e32 v237, v237, v237
	v_max_f32_e32 v238, v238, v238
	v_max_f32_e32 v239, v239, v239
	v_max_f32_e32 v240, v240, v240
	v_max_f32_e32 v241, v241, v241
	v_med3_f32 v226, v226, s62, v95
	v_med3_f32 v227, v227, s62, v95
	v_med3_f32 v228, v228, s62, v95
	v_med3_f32 v229, v229, s62, v95
	v_med3_f32 v230, v230, s62, v95
	v_med3_f32 v231, v231, s62, v95
	v_med3_f32 v232, v232, s62, v95
	v_med3_f32 v233, v233, s62, v95
	v_med3_f32 v234, v234, s62, v95
	v_med3_f32 v235, v235, s62, v95
	v_med3_f32 v236, v236, s62, v95
	v_med3_f32 v237, v237, s62, v95
	v_med3_f32 v238, v238, s62, v95
	v_med3_f32 v239, v239, s62, v95
	v_med3_f32 v240, v240, s62, v95
	v_med3_f32 v241, v241, s62, v95
	v_mov_b32_e32 v242, 0
	v_mov_b32_e32 v243, 0
	v_mov_b32_e32 v244, 0
	v_mov_b32_e32 v245, 0
	v_cvt_pk_fp8_f32 v242, v226, v227
	v_cvt_pk_fp8_f32 v243, v230, v231
	v_cvt_pk_fp8_f32 v244, v234, v235
	v_cvt_pk_fp8_f32 v245, v238, v239
	v_cvt_pk_fp8_f32 v242, v228, v229 op_sel:[0,0,1]
	v_cvt_pk_fp8_f32 v243, v232, v233 op_sel:[0,0,1]
	v_cvt_pk_fp8_f32 v244, v236, v237 op_sel:[0,0,1]
	v_cvt_pk_fp8_f32 v245, v240, v241 op_sel:[0,0,1]
	s_nop 0
	global_store_dwordx4 v79, v[242:245], s[6:7]
	ds_read_b32 v226, v214
	ds_read_b32 v227, v214 offset:512
	ds_read_b32 v228, v214 offset:1024
	ds_read_b32 v229, v214 offset:1536
	ds_read_b32 v230, v214 offset:2048
	ds_read_b32 v231, v214 offset:2560
	ds_read_b32 v232, v214 offset:3072
	ds_read_b32 v233, v214 offset:3584
	ds_read_b32 v234, v214 offset:4096
	ds_read_b32 v235, v214 offset:4608
	ds_read_b32 v236, v214 offset:5120
	ds_read_b32 v237, v214 offset:5632
	ds_read_b32 v238, v214 offset:6144
	ds_read_b32 v239, v214 offset:6656
	ds_read_b32 v240, v214 offset:7168
	ds_read_b32 v241, v214 offset:7680
	s_waitcnt lgkmcnt(0)
	v_max_f32_e32 v226, v226, v226
	v_max_f32_e32 v227, v227, v227
	v_max_f32_e32 v228, v228, v228
	v_max_f32_e32 v229, v229, v229
	v_max_f32_e32 v230, v230, v230
	v_max_f32_e32 v231, v231, v231
	v_max_f32_e32 v232, v232, v232
	v_max_f32_e32 v233, v233, v233
	v_max_f32_e32 v234, v234, v234
	v_max_f32_e32 v235, v235, v235
	v_max_f32_e32 v236, v236, v236
	v_max_f32_e32 v237, v237, v237
	v_max_f32_e32 v238, v238, v238
	v_max_f32_e32 v239, v239, v239
	v_max_f32_e32 v240, v240, v240
	v_max_f32_e32 v241, v241, v241
	v_med3_f32 v226, v226, s62, v95
	v_med3_f32 v227, v227, s62, v95
	v_med3_f32 v228, v228, s62, v95
	v_med3_f32 v229, v229, s62, v95
	v_med3_f32 v230, v230, s62, v95
	v_med3_f32 v231, v231, s62, v95
	v_med3_f32 v232, v232, s62, v95
	v_med3_f32 v233, v233, s62, v95
	v_med3_f32 v234, v234, s62, v95
	v_med3_f32 v235, v235, s62, v95
	v_med3_f32 v236, v236, s62, v95
	v_med3_f32 v237, v237, s62, v95
	v_med3_f32 v238, v238, s62, v95
	v_med3_f32 v239, v239, s62, v95
	v_med3_f32 v240, v240, s62, v95
	v_med3_f32 v241, v241, s62, v95
	v_mov_b32_e32 v242, 0
	v_mov_b32_e32 v243, 0
	v_mov_b32_e32 v244, 0
	v_mov_b32_e32 v245, 0
	v_cvt_pk_fp8_f32 v242, v226, v227
	v_cvt_pk_fp8_f32 v243, v230, v231
	v_cvt_pk_fp8_f32 v244, v234, v235
	v_cvt_pk_fp8_f32 v245, v238, v239
	v_cvt_pk_fp8_f32 v242, v228, v229 op_sel:[0,0,1]
	v_cvt_pk_fp8_f32 v243, v232, v233 op_sel:[0,0,1]
	v_cvt_pk_fp8_f32 v244, v236, v237 op_sel:[0,0,1]
	v_cvt_pk_fp8_f32 v245, v240, v241 op_sel:[0,0,1]
	s_nop 0
	global_store_dwordx4 v80, v[242:245], s[6:7]
	s_waitcnt vmcnt(12)
	v_mul_f32_e32 v144, 0x43000000, v144
	v_mul_f32_e32 v145, 0x43000000, v145
	v_mul_f32_e32 v146, 0x43000000, v146
	v_mul_f32_e32 v147, 0x43000000, v147
	ds_write_b128 v209, v[144:147]
	v_mul_f32_e32 v148, 0x43000000, v148
	v_mul_f32_e32 v149, 0x43000000, v149
	v_mul_f32_e32 v150, 0x43000000, v150
	v_mul_f32_e32 v151, 0x43000000, v151
	ds_write_b128 v209, v[148:151] offset:1024
	v_mul_f32_e32 v152, 0x43000000, v152
	v_mul_f32_e32 v153, 0x43000000, v153
	v_mul_f32_e32 v154, 0x43000000, v154
	v_mul_f32_e32 v155, 0x43000000, v155
	ds_write_b128 v209, v[152:155] offset:2048
	v_mul_f32_e32 v156, 0x43000000, v156
	v_mul_f32_e32 v157, 0x43000000, v157
	v_mul_f32_e32 v158, 0x43000000, v158
	v_mul_f32_e32 v159, 0x43000000, v159
	ds_write_b128 v209, v[156:159] offset:3072
	v_mul_f32_e32 v160, 0x43000000, v160
	v_mul_f32_e32 v161, 0x43000000, v161
	v_mul_f32_e32 v162, 0x43000000, v162
	v_mul_f32_e32 v163, 0x43000000, v163
	ds_write_b128 v209, v[160:163] offset:4096
	v_mul_f32_e32 v164, 0x43000000, v164
	v_mul_f32_e32 v165, 0x43000000, v165
	v_mul_f32_e32 v166, 0x43000000, v166
	v_mul_f32_e32 v167, 0x43000000, v167
	ds_write_b128 v209, v[164:167] offset:5120
	v_mul_f32_e32 v168, 0x43000000, v168
	v_mul_f32_e32 v169, 0x43000000, v169
	v_mul_f32_e32 v170, 0x43000000, v170
	v_mul_f32_e32 v171, 0x43000000, v171
	ds_write_b128 v209, v[168:171] offset:6144
	v_mul_f32_e32 v172, 0x43000000, v172
	v_mul_f32_e32 v173, 0x43000000, v173
	v_mul_f32_e32 v174, 0x43000000, v174
	v_mul_f32_e32 v175, 0x43000000, v175
	ds_write_b128 v209, v[172:175] offset:7168
	s_waitcnt lgkmcnt(0)
	s_barrier
; #define GAS __attribute__((address_space(1)))
; #define LAS __attribute__((address_space(3)))
; #define LDS_WAIT() asm volatile("s_waitcnt lgkmcnt(0)" ::: "memory")
;     const int pr = item >> 1, kb = 2 * (pr / nblk) + (item & 1), nb = pr % nblk, k0 = 64 * kb, n0 = 32 * nb;
;     const int nr = n0 + (lane & 31); const int sc = MAP == 1 ? src_col_in(nr) : nr;
;     float v[32];
; #pragma unroll
;     for (int i = 0; i < 32; ++i) v[i] = sc >= 0 ? W[(size_t)(k0 + 2 * i + (lane >> 5)) * Nsrc + sc] : 0.f;
; #pragma unroll
;     for (int i = 0; i < 32; ++i) { const int k = k0 + 2 * i + (lane >> 5); float x = v[i] * wscale; if (KS) x *= (k < ksplit ? ksA[k] : ksB[k - ksplit]); scr[(2 * i + (lane >> 5)) * 33 + (lane & 31)] = x; }
;     LDS_WAIT(); asm volatile("" ::: "memory");
;     const int c = lane & 7;
; #pragma unroll
;     for (int j = 0; j < 4; ++j) { const int n = (lane >> 3) + 8 * j; const LAS float* s = scr + (8 * c) * 33 + n;
;         const unsigned long long o = (unsigned long long)pg8::pk4_fp8(s[0 * 33], s[1 * 33], s[2 * 33], s[3 * 33]) | ((unsigned long long)pg8::pk4_fp8(s[4 * 33], s[5 * 33], s[6 * 33], s[7 * 33]) << 32);
;         *(GAS unsigned long long*)(WT + (size_t)(n0 + n) * K + k0 + 8 * c) = o; }
;     LDS_WAIT(); asm volatile("" ::: "memory");
; }
	s_add_u32 s8, s38, 0x8000000
	s_addc_u32 s9, s39, 0
	global_load_dwordx4 v[144:147], v75, s[8:9]
	s_add_u32 s8, s8, 0x8000
	s_addc_u32 s9, s9, 0
	global_load_dwordx4 v[148:151], v75, s[8:9]
	s_add_u32 s8, s8, 0x8000
	s_addc_u32 s9, s9, 0
	global_load_dwordx4 v[152:155], v75, s[8:9]
	s_add_u32 s8, s8, 0x8000
	s_addc_u32 s9, s9, 0
	global_load_dwordx4 v[156:159], v75, s[8:9]
	s_add_u32 s8, s8, 0x8000
	s_addc_u32 s9, s9, 0
	global_load_dwordx4 v[160:163], v75, s[8:9]
	s_add_u32 s8, s8, 0x8000
	s_addc_u32 s9, s9, 0
	global_load_dwordx4 v[164:167], v75, s[8:9]
	s_add_u32 s8, s8, 0x8000
	s_addc_u32 s9, s9, 0
	global_load_dwordx4 v[168:171], v75, s[8:9]
	s_add_u32 s8, s8, 0x8000
	s_addc_u32 s9, s9, 0
	global_load_dwordx4 v[172:175], v75, s[8:9]
	s_add_u32 s6, s40, 0x2001000
	s_addc_u32 s7, s41, 0
	ds_read_b32 v226, v211
	ds_read_b32 v227, v211 offset:512
	ds_read_b32 v228, v211 offset:1024
	ds_read_b32 v229, v211 offset:1536
	ds_read_b32 v230, v211 offset:2048
	ds_read_b32 v231, v211 offset:2560
	ds_read_b32 v232, v211 offset:3072
	ds_read_b32 v233, v211 offset:3584
	ds_read_b32 v234, v211 offset:4096
	ds_read_b32 v235, v211 offset:4608
	ds_read_b32 v236, v211 offset:5120
	ds_read_b32 v237, v211 offset:5632
	ds_read_b32 v238, v211 offset:6144
	ds_read_b32 v239, v211 offset:6656
	ds_read_b32 v240, v211 offset:7168
	ds_read_b32 v241, v211 offset:7680
	s_waitcnt lgkmcnt(0)
	v_max_f32_e32 v226, v226, v226
	v_max_f32_e32 v227, v227, v227
	v_max_f32_e32 v228, v228, v228
	v_max_f32_e32 v229, v229, v229
	v_max_f32_e32 v230, v230, v230
	v_max_f32_e32 v231, v231, v231
	v_max_f32_e32 v232, v232, v232
	v_max_f32_e32 v233, v233, v233
	v_max_f32_e32 v234, v234, v234
	v_max_f32_e32 v235, v235, v235
	v_max_f32_e32 v236, v236, v236
	v_max_f32_e32 v237, v237, v237
	v_max_f32_e32 v238, v238, v238
	v_max_f32_e32 v239, v239, v239
	v_max_f32_e32 v240, v240, v240
	v_max_f32_e32 v241, v241, v241
	v_med3_f32 v226, v226, s62, v95
	v_med3_f32 v227, v227, s62, v95
	v_med3_f32 v228, v228, s62, v95
	v_med3_f32 v229, v229, s62, v95
	v_med3_f32 v230, v230, s62, v95
	v_med3_f32 v231, v231, s62, v95
	v_med3_f32 v232, v232, s62, v95
	v_med3_f32 v233, v233, s62, v95
	v_med3_f32 v234, v234, s62, v95
	v_med3_f32 v235, v235, s62, v95
	v_med3_f32 v236, v236, s62, v95
	v_med3_f32 v237, v237, s62, v95
	v_med3_f32 v238, v238, s62, v95
	v_med3_f32 v239, v239, s62, v95
	v_med3_f32 v240, v240, s62, v95
	v_med3_f32 v241, v241, s62, v95
	v_mov_b32_e32 v242, 0
	v_mov_b32_e32 v243, 0
	v_mov_b32_e32 v244, 0
	v_mov_b32_e32 v245, 0
	v_cvt_pk_fp8_f32 v242, v226, v227
	v_cvt_pk_fp8_f32 v243, v230, v231
	v_cvt_pk_fp8_f32 v244, v234, v235
	v_cvt_pk_fp8_f32 v245, v238, v239
	v_cvt_pk_fp8_f32 v242, v228, v229 op_sel:[0,0,1]
	v_cvt_pk_fp8_f32 v243, v232, v233 op_sel:[0,0,1]
	v_cvt_pk_fp8_f32 v244, v236, v237 op_sel:[0,0,1]
	v_cvt_pk_fp8_f32 v245, v240, v241 op_sel:[0,0,1]
	s_nop 0
	global_store_dwordx4 v79, v[242:245], s[6:7]
	ds_read_b32 v226, v213
	ds_read_b32 v227, v213 offset:512
	ds_read_b32 v228, v213 offset:1024
	ds_read_b32 v229, v213 offset:1536
	ds_read_b32 v230, v213 offset:2048
	ds_read_b32 v231, v213 offset:2560
	ds_read_b32 v232, v213 offset:3072
	ds_read_b32 v233, v213 offset:3584
	ds_read_b32 v234, v213 offset:4096
	ds_read_b32 v235, v213 offset:4608
	ds_read_b32 v236, v213 offset:5120
	ds_read_b32 v237, v213 offset:5632
	ds_read_b32 v238, v213 offset:6144
	ds_read_b32 v239, v213 offset:6656
	ds_read_b32 v240, v213 offset:7168
	ds_read_b32 v241, v213 offset:7680
	s_waitcnt lgkmcnt(0)
	v_max_f32_e32 v226, v226, v226
	v_max_f32_e32 v227, v227, v227
	v_max_f32_e32 v228, v228, v228
	v_max_f32_e32 v229, v229, v229
	v_max_f32_e32 v230, v230, v230
	v_max_f32_e32 v231, v231, v231
	v_max_f32_e32 v232, v232, v232
	v_max_f32_e32 v233, v233, v233
	v_max_f32_e32 v234, v234, v234
	v_max_f32_e32 v235, v235, v235
	v_max_f32_e32 v236, v236, v236
	v_max_f32_e32 v237, v237, v237
	v_max_f32_e32 v238, v238, v238
	v_max_f32_e32 v239, v239, v239
	v_max_f32_e32 v240, v240, v240
	v_max_f32_e32 v241, v241, v241
	v_med3_f32 v226, v226, s62, v95
	v_med3_f32 v227, v227, s62, v95
	v_med3_f32 v228, v228, s62, v95
	v_med3_f32 v229, v229, s62, v95
	v_med3_f32 v230, v230, s62, v95
	v_med3_f32 v231, v231, s62, v95
	v_med3_f32 v232, v232, s62, v95
	v_med3_f32 v233, v233, s62, v95
	v_med3_f32 v234, v234, s62, v95
	v_med3_f32 v235, v235, s62, v95
	v_med3_f32 v236, v236, s62, v95
	v_med3_f32 v237, v237, s62, v95
	v_med3_f32 v238, v238, s62, v95
	v_med3_f32 v239, v239, s62, v95
	v_med3_f32 v240, v240, s62, v95
	v_med3_f32 v241, v241, s62, v95
	v_mov_b32_e32 v242, 0
	v_mov_b32_e32 v243, 0
	v_mov_b32_e32 v244, 0
	v_mov_b32_e32 v245, 0
	v_cvt_pk_fp8_f32 v242, v226, v227
	v_cvt_pk_fp8_f32 v243, v230, v231
	v_cvt_pk_fp8_f32 v244, v234, v235
	v_cvt_pk_fp8_f32 v245, v238, v239
	v_cvt_pk_fp8_f32 v242, v228, v229 op_sel:[0,0,1]
	v_cvt_pk_fp8_f32 v243, v232, v233 op_sel:[0,0,1]
	v_cvt_pk_fp8_f32 v244, v236, v237 op_sel:[0,0,1]
	v_cvt_pk_fp8_f32 v245, v240, v241 op_sel:[0,0,1]
	s_nop 0
	global_store_dwordx4 v80, v[242:245], s[6:7]
	s_branch .Lco3_hop_skip

; #define GAS __attribute__((address_space(1)))
; #define LAS __attribute__((address_space(3)))
; #define LDS_WAIT() asm volatile("s_waitcnt lgkmcnt(0)" ::: "memory")
;     const int pr = item >> 1, kb = 2 * (pr / nblk) + (item & 1), nb = pr % nblk, k0 = 64 * kb, n0 = 32 * nb;
;     const int nr = n0 + (lane & 31); const int sc = MAP == 1 ? src_col_in(nr) : nr;
;     float v[32];
; #pragma unroll
;     for (int i = 0; i < 32; ++i) v[i] = sc >= 0 ? W[(size_t)(k0 + 2 * i + (lane >> 5)) * Nsrc + sc] : 0.f;
; #pragma unroll
;     for (int i = 0; i < 32; ++i) { const int k = k0 + 2 * i + (lane >> 5); float x = v[i] * wscale; if (KS) x *= (k < ksplit ? ksA[k] : ksB[k - ksplit]); scr[(2 * i + (lane >> 5)) * 33 + (lane & 31)] = x; }
;     LDS_WAIT(); asm volatile("" ::: "memory");
;     const int c = lane & 7;
; #pragma unroll
;     for (int j = 0; j < 4; ++j) { const int n = (lane >> 3) + 8 * j; const LAS float* s = scr + (8 * c) * 33 + n;
;         const unsigned long long o = (unsigned long long)pg8::pk4_fp8(s[0 * 33], s[1 * 33], s[2 * 33], s[3 * 33]) | ((unsigned long long)pg8::pk4_fp8(s[4 * 33], s[5 * 33], s[6 * 33], s[7 * 33]) << 32);
;         *(GAS unsigned long long*)(WT + (size_t)(n0 + n) * K + k0 + 8 * c) = o; }
;     LDS_WAIT(); asm volatile("" ::: "memory");
; }
.Lco3_hop_skip:
	s_waitcnt vmcnt(12)
	v_mul_f32_e32 v176, 0x43000000, v176
	v_mul_f32_e32 v177, 0x43000000, v177
	v_mul_f32_e32 v178, 0x43000000, v178
	v_mul_f32_e32 v179, 0x43000000, v179
	ds_write_b128 v210, v[176:179]
	v_mul_f32_e32 v180, 0x43000000, v180
	v_mul_f32_e32 v181, 0x43000000, v181
	v_mul_f32_e32 v182, 0x43000000, v182
	v_mul_f32_e32 v183, 0x43000000, v183
	ds_write_b128 v210, v[180:183] offset:1024
	v_mul_f32_e32 v184, 0x43000000, v184
	v_mul_f32_e32 v185, 0x43000000, v185
	v_mul_f32_e32 v186, 0x43000000, v186
	v_mul_f32_e32 v187, 0x43000000, v187
	ds_write_b128 v210, v[184:187] offset:2048
	v_mul_f32_e32 v188, 0x43000000, v188
	v_mul_f32_e32 v189, 0x43000000, v189
	v_mul_f32_e32 v190, 0x43000000, v190
	v_mul_f32_e32 v191, 0x43000000, v191
	ds_write_b128 v210, v[188:191] offset:3072
	v_mul_f32_e32 v192, 0x43000000, v192
	v_mul_f32_e32 v193, 0x43000000, v193
	v_mul_f32_e32 v194, 0x43000000, v194
	v_mul_f32_e32 v195, 0x43000000, v195
	ds_write_b128 v210, v[192:195] offset:4096
	v_mul_f32_e32 v196, 0x43000000, v196
	v_mul_f32_e32 v197, 0x43000000, v197
	v_mul_f32_e32 v198, 0x43000000, v198
	v_mul_f32_e32 v199, 0x43000000, v199
	ds_write_b128 v210, v[196:199] offset:5120
	v_mul_f32_e32 v200, 0x43000000, v200
	v_mul_f32_e32 v201, 0x43000000, v201
	v_mul_f32_e32 v202, 0x43000000, v202
	v_mul_f32_e32 v203, 0x43000000, v203
	ds_write_b128 v210, v[200:203] offset:6144
	v_mul_f32_e32 v204, 0x43000000, v204
	v_mul_f32_e32 v205, 0x43000000, v205
	v_mul_f32_e32 v206, 0x43000000, v206
	v_mul_f32_e32 v207, 0x43000000, v207
	ds_write_b128 v210, v[204:207] offset:7168
	s_waitcnt lgkmcnt(0)
	s_barrier
	s_add_u32 s8, s38, 0x8001000
	s_addc_u32 s9, s39, 0
	global_load_dwordx4 v[176:179], v75, s[8:9]
	s_add_u32 s8, s8, 0x8000
	s_addc_u32 s9, s9, 0
	global_load_dwordx4 v[180:183], v75, s[8:9]
	s_add_u32 s8, s8, 0x8000
	s_addc_u32 s9, s9, 0
	global_load_dwordx4 v[184:187], v75, s[8:9]
	s_add_u32 s8, s8, 0x8000
	s_addc_u32 s9, s9, 0
	global_load_dwordx4 v[188:191], v75, s[8:9]
	s_add_u32 s8, s8, 0x8000
	s_addc_u32 s9, s9, 0
	global_load_dwordx4 v[192:195], v75, s[8:9]
	s_add_u32 s8, s8, 0x8000
	s_addc_u32 s9, s9, 0
	global_load_dwordx4 v[196:199], v75, s[8:9]
	s_add_u32 s8, s8, 0x8000
	s_addc_u32 s9, s9, 0
	global_load_dwordx4 v[200:203], v75, s[8:9]
	s_add_u32 s8, s8, 0x8000
	s_addc_u32 s9, s9, 0
	global_load_dwordx4 v[204:207], v75, s[8:9]
	s_add_u32 s6, s40, 0x3001000
	s_addc_u32 s7, s41, 0
	ds_read_b32 v226, v212
	ds_read_b32 v227, v212 offset:512
	ds_read_b32 v228, v212 offset:1024
	ds_read_b32 v229, v212 offset:1536
	ds_read_b32 v230, v212 offset:2048
	ds_read_b32 v231, v212 offset:2560
	ds_read_b32 v232, v212 offset:3072
	ds_read_b32 v233, v212 offset:3584
	ds_read_b32 v234, v212 offset:4096
	ds_read_b32 v235, v212 offset:4608
	ds_read_b32 v236, v212 offset:5120
	ds_read_b32 v237, v212 offset:5632
	ds_read_b32 v238, v212 offset:6144
	ds_read_b32 v239, v212 offset:6656
	ds_read_b32 v240, v212 offset:7168
	ds_read_b32 v241, v212 offset:7680
	s_waitcnt lgkmcnt(0)
	v_max_f32_e32 v226, v226, v226
	v_max_f32_e32 v227, v227, v227
	v_max_f32_e32 v228, v228, v228
	v_max_f32_e32 v229, v229, v229
	v_max_f32_e32 v230, v230, v230
	v_max_f32_e32 v231, v231, v231
	v_max_f32_e32 v232, v232, v232
	v_max_f32_e32 v233, v233, v233
	v_max_f32_e32 v234, v234, v234
	v_max_f32_e32 v235, v235, v235
	v_max_f32_e32 v236, v236, v236
	v_max_f32_e32 v237, v237, v237
	v_max_f32_e32 v238, v238, v238
	v_max_f32_e32 v239, v239, v239
	v_max_f32_e32 v240, v240, v240
	v_max_f32_e32 v241, v241, v241
	v_med3_f32 v226, v226, s62, v95
	v_med3_f32 v227, v227, s62, v95
	v_med3_f32 v228, v228, s62, v95
	v_med3_f32 v229, v229, s62, v95
	v_med3_f32 v230, v230, s62, v95
	v_med3_f32 v231, v231, s62, v95
	v_med3_f32 v232, v232, s62, v95
	v_med3_f32 v233, v233, s62, v95
	v_med3_f32 v234, v234, s62, v95
	v_med3_f32 v235, v235, s62, v95
	v_med3_f32 v236, v236, s62, v95
	v_med3_f32 v237, v237, s62, v95
	v_med3_f32 v238, v238, s62, v95
	v_med3_f32 v239, v239, s62, v95
	v_med3_f32 v240, v240, s62, v95
	v_med3_f32 v241, v241, s62, v95
	v_mov_b32_e32 v242, 0
	v_mov_b32_e32 v243, 0
	v_mov_b32_e32 v244, 0
	v_mov_b32_e32 v245, 0
	v_cvt_pk_fp8_f32 v242, v226, v227
	v_cvt_pk_fp8_f32 v243, v230, v231
	v_cvt_pk_fp8_f32 v244, v234, v235
	v_cvt_pk_fp8_f32 v245, v238, v239
	v_cvt_pk_fp8_f32 v242, v228, v229 op_sel:[0,0,1]
	v_cvt_pk_fp8_f32 v243, v232, v233 op_sel:[0,0,1]
	v_cvt_pk_fp8_f32 v244, v236, v237 op_sel:[0,0,1]
	v_cvt_pk_fp8_f32 v245, v240, v241 op_sel:[0,0,1]
	s_nop 0
	global_store_dwordx4 v79, v[242:245], s[6:7]
	ds_read_b32 v226, v214
	ds_read_b32 v227, v214 offset:512
	ds_read_b32 v228, v214 offset:1024
	ds_read_b32 v229, v214 offset:1536
	ds_read_b32 v230, v214 offset:2048
	ds_read_b32 v231, v214 offset:2560
	ds_read_b32 v232, v214 offset:3072
	ds_read_b32 v233, v214 offset:3584
	ds_read_b32 v234, v214 offset:4096
	ds_read_b32 v235, v214 offset:4608
	ds_read_b32 v236, v214 offset:5120
	ds_read_b32 v237, v214 offset:5632
	ds_read_b32 v238, v214 offset:6144
	ds_read_b32 v239, v214 offset:6656
	ds_read_b32 v240, v214 offset:7168
	ds_read_b32 v241, v214 offset:7680
	s_waitcnt lgkmcnt(0)
; #define GAS __attribute__((address_space(1)))
; #define LAS __attribute__((address_space(3)))
; #define LDS_WAIT() asm volatile("s_waitcnt lgkmcnt(0)" ::: "memory")
;     const int pr = item >> 1, kb = 2 * (pr / nblk) + (item & 1), nb = pr % nblk, k0 = 64 * kb, n0 = 32 * nb;
;     const int nr = n0 + (lane & 31); const int sc = MAP == 1 ? src_col_in(nr) : nr;
;     float v[32];
; #pragma unroll
;     for (int i = 0; i < 32; ++i) v[i] = sc >= 0 ? W[(size_t)(k0 + 2 * i + (lane >> 5)) * Nsrc + sc] : 0.f;
; #pragma unroll
;     for (int i = 0; i < 32; ++i) { const int k = k0 + 2 * i + (lane >> 5); float x = v[i] * wscale; if (KS) x *= (k < ksplit ? ksA[k] : ksB[k - ksplit]); scr[(2 * i + (lane >> 5)) * 33 + (lane & 31)] = x; }
;     LDS_WAIT(); asm volatile("" ::: "memory");
;     const int c = lane & 7;
; #pragma unroll
;     for (int j = 0; j < 4; ++j) { const int n = (lane >> 3) + 8 * j; const LAS float* s = scr + (8 * c) * 33 + n;
;         const unsigned long long o = (unsigned long long)pg8::pk4_fp8(s[0 * 33], s[1 * 33], s[2 * 33], s[3 * 33]) | ((unsigned long long)pg8::pk4_fp8(s[4 * 33], s[5 * 33], s[6 * 33], s[7 * 33]) << 32);
;         *(GAS unsigned long long*)(WT + (size_t)(n0 + n) * K + k0 + 8 * c) = o; }
;     LDS_WAIT(); asm volatile("" ::: "memory");
; }
	v_max_f32_e32 v226, v226, v226
	v_max_f32_e32 v227, v227, v227
	v_max_f32_e32 v228, v228, v228
	v_max_f32_e32 v229, v229, v229
	v_max_f32_e32 v230, v230, v230
	v_max_f32_e32 v231, v231, v231
	v_max_f32_e32 v232, v232, v232
	v_max_f32_e32 v233, v233, v233
	v_max_f32_e32 v234, v234, v234
	v_max_f32_e32 v235, v235, v235
	v_max_f32_e32 v236, v236, v236
	v_max_f32_e32 v237, v237, v237
	v_max_f32_e32 v238, v238, v238
	v_max_f32_e32 v239, v239, v239
	v_max_f32_e32 v240, v240, v240
	v_max_f32_e32 v241, v241, v241
	v_med3_f32 v226, v226, s62, v95
	v_med3_f32 v227, v227, s62, v95
	v_med3_f32 v228, v228, s62, v95
	v_med3_f32 v229, v229, s62, v95
	v_med3_f32 v230, v230, s62, v95
	v_med3_f32 v231, v231, s62, v95
	v_med3_f32 v232, v232, s62, v95
	v_med3_f32 v233, v233, s62, v95
	v_med3_f32 v234, v234, s62, v95
	v_med3_f32 v235, v235, s62, v95
	v_med3_f32 v236, v236, s62, v95
	v_med3_f32 v237, v237, s62, v95
	v_med3_f32 v238, v238, s62, v95
	v_med3_f32 v239, v239, s62, v95
	v_med3_f32 v240, v240, s62, v95
	v_med3_f32 v241, v241, s62, v95
	v_mov_b32_e32 v242, 0
	v_mov_b32_e32 v243, 0
	v_mov_b32_e32 v244, 0
	v_mov_b32_e32 v245, 0
	v_cvt_pk_fp8_f32 v242, v226, v227
	v_cvt_pk_fp8_f32 v243, v230, v231
	v_cvt_pk_fp8_f32 v244, v234, v235
	v_cvt_pk_fp8_f32 v245, v238, v239
	v_cvt_pk_fp8_f32 v242, v228, v229 op_sel:[0,0,1]
	v_cvt_pk_fp8_f32 v243, v232, v233 op_sel:[0,0,1]
	v_cvt_pk_fp8_f32 v244, v236, v237 op_sel:[0,0,1]
	v_cvt_pk_fp8_f32 v245, v240, v241 op_sel:[0,0,1]
	s_nop 0
	global_store_dwordx4 v80, v[242:245], s[6:7]
	s_waitcnt vmcnt(12)
	v_mul_f32_e32 v144, 0x43000000, v144
	v_mul_f32_e32 v145, 0x43000000, v145
	v_mul_f32_e32 v146, 0x43000000, v146
	v_mul_f32_e32 v147, 0x43000000, v147
	ds_write_b128 v209, v[144:147]
	v_mul_f32_e32 v148, 0x43000000, v148
	v_mul_f32_e32 v149, 0x43000000, v149
	v_mul_f32_e32 v150, 0x43000000, v150
	v_mul_f32_e32 v151, 0x43000000, v151
	ds_write_b128 v209, v[148:151] offset:1024
	v_mul_f32_e32 v152, 0x43000000, v152
	v_mul_f32_e32 v153, 0x43000000, v153
	v_mul_f32_e32 v154, 0x43000000, v154
	v_mul_f32_e32 v155, 0x43000000, v155
	ds_write_b128 v209, v[152:155] offset:2048
	v_mul_f32_e32 v156, 0x43000000, v156
	v_mul_f32_e32 v157, 0x43000000, v157
	v_mul_f32_e32 v158, 0x43000000, v158
	v_mul_f32_e32 v159, 0x43000000, v159
	ds_write_b128 v209, v[156:159] offset:3072
	v_mul_f32_e32 v160, 0x43000000, v160
	v_mul_f32_e32 v161, 0x43000000, v161
	v_mul_f32_e32 v162, 0x43000000, v162
	v_mul_f32_e32 v163, 0x43000000, v163
	ds_write_b128 v209, v[160:163] offset:4096
	v_mul_f32_e32 v164, 0x43000000, v164
	v_mul_f32_e32 v165, 0x43000000, v165
	v_mul_f32_e32 v166, 0x43000000, v166
	v_mul_f32_e32 v167, 0x43000000, v167
	ds_write_b128 v209, v[164:167] offset:5120
	v_mul_f32_e32 v168, 0x43000000, v168
	v_mul_f32_e32 v169, 0x43000000, v169
	v_mul_f32_e32 v170, 0x43000000, v170
	v_mul_f32_e32 v171, 0x43000000, v171
	ds_write_b128 v209, v[168:171] offset:6144
	v_mul_f32_e32 v172, 0x43000000, v172
	v_mul_f32_e32 v173, 0x43000000, v173
	v_mul_f32_e32 v174, 0x43000000, v174
	v_mul_f32_e32 v175, 0x43000000, v175
	ds_write_b128 v209, v[172:175] offset:7168
	s_waitcnt lgkmcnt(0)
	s_barrier
	s_add_u32 s8, s38, 0x8002000
	s_addc_u32 s9, s39, 0
	global_load_dwordx4 v[144:147], v75, s[8:9]
	s_add_u32 s8, s8, 0x8000
	s_addc_u32 s9, s9, 0
	global_load_dwordx4 v[148:151], v75, s[8:9]
	s_add_u32 s8, s8, 0x8000
	s_addc_u32 s9, s9, 0
	global_load_dwordx4 v[152:155], v75, s[8:9]
	s_add_u32 s8, s8, 0x8000
	s_addc_u32 s9, s9, 0
	global_load_dwordx4 v[156:159], v75, s[8:9]
	s_add_u32 s8, s8, 0x8000
	s_addc_u32 s9, s9, 0
	global_load_dwordx4 v[160:163], v75, s[8:9]
	s_add_u32 s8, s8, 0x8000
	s_addc_u32 s9, s9, 0
	global_load_dwordx4 v[164:167], v75, s[8:9]
	s_add_u32 s8, s8, 0x8000
	s_addc_u32 s9, s9, 0
	global_load_dwordx4 v[168:171], v75, s[8:9]
	s_add_u32 s8, s8, 0x8000
	s_addc_u32 s9, s9, 0
	global_load_dwordx4 v[172:175], v75, s[8:9]
	s_add_u32 s6, s40, 0x2000
	s_addc_u32 s7, s41, 0
	ds_read_b32 v226, v211
	ds_read_b32 v227, v211 offset:512
	ds_read_b32 v228, v211 offset:1024
	ds_read_b32 v229, v211 offset:1536
	ds_read_b32 v230, v211 offset:2048
	ds_read_b32 v231, v211 offset:2560
	ds_read_b32 v232, v211 offset:3072
	ds_read_b32 v233, v211 offset:3584
	ds_read_b32 v234, v211 offset:4096
	ds_read_b32 v235, v211 offset:4608
	ds_read_b32 v236, v211 offset:5120
	ds_read_b32 v237, v211 offset:5632
	ds_read_b32 v238, v211 offset:6144
	ds_read_b32 v239, v211 offset:6656
	ds_read_b32 v240, v211 offset:7168
	ds_read_b32 v241, v211 offset:7680
	s_waitcnt lgkmcnt(0)
	v_max_f32_e32 v226, v226, v226
	v_max_f32_e32 v227, v227, v227
	v_max_f32_e32 v228, v228, v228
	v_max_f32_e32 v229, v229, v229
	v_max_f32_e32 v230, v230, v230
	v_max_f32_e32 v231, v231, v231
	v_max_f32_e32 v232, v232, v232
	v_max_f32_e32 v233, v233, v233
	v_max_f32_e32 v234, v234, v234
	v_max_f32_e32 v235, v235, v235
	v_max_f32_e32 v236, v236, v236
	v_max_f32_e32 v237, v237, v237
	v_max_f32_e32 v238, v238, v238
	v_max_f32_e32 v239, v239, v239
	v_max_f32_e32 v240, v240, v240
	v_max_f32_e32 v241, v241, v241
	v_med3_f32 v226, v226, s62, v95
	v_med3_f32 v227, v227, s62, v95
	v_med3_f32 v228, v228, s62, v95
	v_med3_f32 v229, v229, s62, v95
	v_med3_f32 v230, v230, s62, v95
	v_med3_f32 v231, v231, s62, v95
	v_med3_f32 v232, v232, s62, v95
	v_med3_f32 v233, v233, s62, v95
	v_med3_f32 v234, v234, s62, v95
	v_med3_f32 v235, v235, s62, v95
	v_med3_f32 v236, v236, s62, v95
	v_med3_f32 v237, v237, s62, v95
	v_med3_f32 v238, v238, s62, v95
	v_med3_f32 v239, v239, s62, v95
	v_med3_f32 v240, v240, s62, v95
	v_med3_f32 v241, v241, s62, v95
	v_mov_b32_e32 v242, 0
	v_mov_b32_e32 v243, 0
	v_mov_b32_e32 v244, 0
	v_mov_b32_e32 v245, 0
	v_cvt_pk_fp8_f32 v242, v226, v227
	v_cvt_pk_fp8_f32 v243, v230, v231
	v_cvt_pk_fp8_f32 v244, v234, v235
	v_cvt_pk_fp8_f32 v245, v238, v239
	v_cvt_pk_fp8_f32 v242, v228, v229 op_sel:[0,0,1]
	v_cvt_pk_fp8_f32 v243, v232, v233 op_sel:[0,0,1]
	v_cvt_pk_fp8_f32 v244, v236, v237 op_sel:[0,0,1]
	v_cvt_pk_fp8_f32 v245, v240, v241 op_sel:[0,0,1]
	s_nop 0
	global_store_dwordx4 v79, v[242:245], s[6:7]
	ds_read_b32 v226, v213
	ds_read_b32 v227, v213 offset:512
	ds_read_b32 v228, v213 offset:1024
	ds_read_b32 v229, v213 offset:1536
	ds_read_b32 v230, v213 offset:2048
	ds_read_b32 v231, v213 offset:2560
	ds_read_b32 v232, v213 offset:3072
	ds_read_b32 v233, v213 offset:3584
	ds_read_b32 v234, v213 offset:4096
	ds_read_b32 v235, v213 offset:4608
	ds_read_b32 v236, v213 offset:5120
	ds_read_b32 v237, v213 offset:5632
	ds_read_b32 v238, v213 offset:6144
	ds_read_b32 v239, v213 offset:6656
	ds_read_b32 v240, v213 offset:7168
	ds_read_b32 v241, v213 offset:7680
	s_waitcnt lgkmcnt(0)
; #define GAS __attribute__((address_space(1)))
; #define LAS __attribute__((address_space(3)))
; #define LDS_WAIT() asm volatile("s_waitcnt lgkmcnt(0)" ::: "memory")
;     const int pr = item >> 1, kb = 2 * (pr / nblk) + (item & 1), nb = pr % nblk, k0 = 64 * kb, n0 = 32 * nb;
;     const int nr = n0 + (lane & 31); const int sc = MAP == 1 ? src_col_in(nr) : nr;
;     float v[32];
; #pragma unroll
;     for (int i = 0; i < 32; ++i) v[i] = sc >= 0 ? W[(size_t)(k0 + 2 * i + (lane >> 5)) * Nsrc + sc] : 0.f;
; #pragma unroll
;     for (int i = 0; i < 32; ++i) { const int k = k0 + 2 * i + (lane >> 5); float x = v[i] * wscale; if (KS) x *= (k < ksplit ? ksA[k] : ksB[k - ksplit]); scr[(2 * i + (lane >> 5)) * 33 + (lane & 31)] = x; }
;     LDS_WAIT(); asm volatile("" ::: "memory");
;     const int c = lane & 7;
; #pragma unroll
;     for (int j = 0; j < 4; ++j) { const int n = (lane >> 3) + 8 * j; const LAS float* s = scr + (8 * c) * 33 + n;
;         const unsigned long long o = (unsigned long long)pg8::pk4_fp8(s[0 * 33], s[1 * 33], s[2 * 33], s[3 * 33]) | ((unsigned long long)pg8::pk4_fp8(s[4 * 33], s[5 * 33], s[6 * 33], s[7 * 33]) << 32);
;         *(GAS unsigned long long*)(WT + (size_t)(n0 + n) * K + k0 + 8 * c) = o; }
;     LDS_WAIT(); asm volatile("" ::: "memory");
; }
	v_max_f32_e32 v226, v226, v226
	v_max_f32_e32 v227, v227, v227
	v_max_f32_e32 v228, v228, v228
	v_max_f32_e32 v229, v229, v229
	v_max_f32_e32 v230, v230, v230
	v_max_f32_e32 v231, v231, v231
	v_max_f32_e32 v232, v232, v232
	v_max_f32_e32 v233, v233, v233
	v_max_f32_e32 v234, v234, v234
	v_max_f32_e32 v235, v235, v235
	v_max_f32_e32 v236, v236, v236
	v_max_f32_e32 v237, v237, v237
	v_max_f32_e32 v238, v238, v238
	v_max_f32_e32 v239, v239, v239
	v_max_f32_e32 v240, v240, v240
	v_max_f32_e32 v241, v241, v241
	v_med3_f32 v226, v226, s62, v95
	v_med3_f32 v227, v227, s62, v95
	v_med3_f32 v228, v228, s62, v95
	v_med3_f32 v229, v229, s62, v95
	v_med3_f32 v230, v230, s62, v95
	v_med3_f32 v231, v231, s62, v95
	v_med3_f32 v232, v232, s62, v95
	v_med3_f32 v233, v233, s62, v95
	v_med3_f32 v234, v234, s62, v95
	v_med3_f32 v235, v235, s62, v95
	v_med3_f32 v236, v236, s62, v95
	v_med3_f32 v237, v237, s62, v95
	v_med3_f32 v238, v238, s62, v95
	v_med3_f32 v239, v239, s62, v95
	v_med3_f32 v240, v240, s62, v95
	v_med3_f32 v241, v241, s62, v95
	v_mov_b32_e32 v242, 0
	v_mov_b32_e32 v243, 0
	v_mov_b32_e32 v244, 0
	v_mov_b32_e32 v245, 0
	v_cvt_pk_fp8_f32 v242, v226, v227
	v_cvt_pk_fp8_f32 v243, v230, v231
	v_cvt_pk_fp8_f32 v244, v234, v235
	v_cvt_pk_fp8_f32 v245, v238, v239
	v_cvt_pk_fp8_f32 v242, v228, v229 op_sel:[0,0,1]
	v_cvt_pk_fp8_f32 v243, v232, v233 op_sel:[0,0,1]
	v_cvt_pk_fp8_f32 v244, v236, v237 op_sel:[0,0,1]
	v_cvt_pk_fp8_f32 v245, v240, v241 op_sel:[0,0,1]
	s_nop 0
	global_store_dwordx4 v80, v[242:245], s[6:7]
	s_waitcnt vmcnt(12)
	v_mul_f32_e32 v176, 0x43000000, v176
	v_mul_f32_e32 v177, 0x43000000, v177
	v_mul_f32_e32 v178, 0x43000000, v178
	v_mul_f32_e32 v179, 0x43000000, v179
	ds_write_b128 v210, v[176:179]
	v_mul_f32_e32 v180, 0x43000000, v180
	v_mul_f32_e32 v181, 0x43000000, v181
	v_mul_f32_e32 v182, 0x43000000, v182
	v_mul_f32_e32 v183, 0x43000000, v183
	ds_write_b128 v210, v[180:183] offset:1024
	v_mul_f32_e32 v184, 0x43000000, v184
	v_mul_f32_e32 v185, 0x43000000, v185
	v_mul_f32_e32 v186, 0x43000000, v186
	v_mul_f32_e32 v187, 0x43000000, v187
	ds_write_b128 v210, v[184:187] offset:2048
	v_mul_f32_e32 v188, 0x43000000, v188
	v_mul_f32_e32 v189, 0x43000000, v189
	v_mul_f32_e32 v190, 0x43000000, v190
	v_mul_f32_e32 v191, 0x43000000, v191
	ds_write_b128 v210, v[188:191] offset:3072
	v_mul_f32_e32 v192, 0x43000000, v192
	v_mul_f32_e32 v193, 0x43000000, v193
	v_mul_f32_e32 v194, 0x43000000, v194
	v_mul_f32_e32 v195, 0x43000000, v195
	ds_write_b128 v210, v[192:195] offset:4096
	v_mul_f32_e32 v196, 0x43000000, v196
	v_mul_f32_e32 v197, 0x43000000, v197
	v_mul_f32_e32 v198, 0x43000000, v198
	v_mul_f32_e32 v199, 0x43000000, v199
	ds_write_b128 v210, v[196:199] offset:5120
	v_mul_f32_e32 v200, 0x43000000, v200
	v_mul_f32_e32 v201, 0x43000000, v201
	v_mul_f32_e32 v202, 0x43000000, v202
	v_mul_f32_e32 v203, 0x43000000, v203
	ds_write_b128 v210, v[200:203] offset:6144
	v_mul_f32_e32 v204, 0x43000000, v204
	v_mul_f32_e32 v205, 0x43000000, v205
	v_mul_f32_e32 v206, 0x43000000, v206
	v_mul_f32_e32 v207, 0x43000000, v207
	ds_write_b128 v210, v[204:207] offset:7168
	s_waitcnt lgkmcnt(0)
	s_barrier
	s_add_u32 s8, s38, 0x8003000
	s_addc_u32 s9, s39, 0
	global_load_dwordx4 v[176:179], v75, s[8:9]
	s_add_u32 s8, s8, 0x8000
	s_addc_u32 s9, s9, 0
	global_load_dwordx4 v[180:183], v75, s[8:9]
	s_add_u32 s8, s8, 0x8000
	s_addc_u32 s9, s9, 0
	global_load_dwordx4 v[184:187], v75, s[8:9]
	s_add_u32 s8, s8, 0x8000
	s_addc_u32 s9, s9, 0
	global_load_dwordx4 v[188:191], v75, s[8:9]
	s_add_u32 s8, s8, 0x8000
	s_addc_u32 s9, s9, 0
	global_load_dwordx4 v[192:195], v75, s[8:9]
	s_add_u32 s8, s8, 0x8000
	s_addc_u32 s9, s9, 0
	global_load_dwordx4 v[196:199], v75, s[8:9]
	s_add_u32 s8, s8, 0x8000
	s_addc_u32 s9, s9, 0
	global_load_dwordx4 v[200:203], v75, s[8:9]
	s_add_u32 s8, s8, 0x8000
	s_addc_u32 s9, s9, 0
	global_load_dwordx4 v[204:207], v75, s[8:9]
	s_add_u32 s6, s40, 0x1002000
	s_addc_u32 s7, s41, 0
	ds_read_b32 v226, v212
	ds_read_b32 v227, v212 offset:512
	ds_read_b32 v228, v212 offset:1024
	ds_read_b32 v229, v212 offset:1536
	ds_read_b32 v230, v212 offset:2048
	ds_read_b32 v231, v212 offset:2560
	ds_read_b32 v232, v212 offset:3072
	ds_read_b32 v233, v212 offset:3584
	ds_read_b32 v234, v212 offset:4096
	ds_read_b32 v235, v212 offset:4608
	ds_read_b32 v236, v212 offset:5120
	ds_read_b32 v237, v212 offset:5632
	ds_read_b32 v238, v212 offset:6144
	ds_read_b32 v239, v212 offset:6656
	ds_read_b32 v240, v212 offset:7168
	ds_read_b32 v241, v212 offset:7680
	s_waitcnt lgkmcnt(0)
	v_max_f32_e32 v226, v226, v226
	v_max_f32_e32 v227, v227, v227
	v_max_f32_e32 v228, v228, v228
	v_max_f32_e32 v229, v229, v229
	v_max_f32_e32 v230, v230, v230
	v_max_f32_e32 v231, v231, v231
	v_max_f32_e32 v232, v232, v232
	v_max_f32_e32 v233, v233, v233
	v_max_f32_e32 v234, v234, v234
	v_max_f32_e32 v235, v235, v235
	v_max_f32_e32 v236, v236, v236
	v_max_f32_e32 v237, v237, v237
	v_max_f32_e32 v238, v238, v238
	v_max_f32_e32 v239, v239, v239
	v_max_f32_e32 v240, v240, v240
	v_max_f32_e32 v241, v241, v241
	v_med3_f32 v226, v226, s62, v95
	v_med3_f32 v227, v227, s62, v95
	v_med3_f32 v228, v228, s62, v95
	v_med3_f32 v229, v229, s62, v95
	v_med3_f32 v230, v230, s62, v95
	v_med3_f32 v231, v231, s62, v95
	v_med3_f32 v232, v232, s62, v95
	v_med3_f32 v233, v233, s62, v95
	v_med3_f32 v234, v234, s62, v95
	v_med3_f32 v235, v235, s62, v95
	v_med3_f32 v236, v236, s62, v95
	v_med3_f32 v237, v237, s62, v95
	v_med3_f32 v238, v238, s62, v95
	v_med3_f32 v239, v239, s62, v95
	v_med3_f32 v240, v240, s62, v95
	v_med3_f32 v241, v241, s62, v95
	v_mov_b32_e32 v242, 0
	v_mov_b32_e32 v243, 0
	v_mov_b32_e32 v244, 0
	v_mov_b32_e32 v245, 0
	v_cvt_pk_fp8_f32 v242, v226, v227
	v_cvt_pk_fp8_f32 v243, v230, v231
	v_cvt_pk_fp8_f32 v244, v234, v235
	v_cvt_pk_fp8_f32 v245, v238, v239
	v_cvt_pk_fp8_f32 v242, v228, v229 op_sel:[0,0,1]
	v_cvt_pk_fp8_f32 v243, v232, v233 op_sel:[0,0,1]
	v_cvt_pk_fp8_f32 v244, v236, v237 op_sel:[0,0,1]
	v_cvt_pk_fp8_f32 v245, v240, v241 op_sel:[0,0,1]
	s_nop 0
	global_store_dwordx4 v79, v[242:245], s[6:7]
	ds_read_b32 v226, v214
	ds_read_b32 v227, v214 offset:512
	ds_read_b32 v228, v214 offset:1024
	ds_read_b32 v229, v214 offset:1536
	ds_read_b32 v230, v214 offset:2048
	ds_read_b32 v231, v214 offset:2560
	ds_read_b32 v232, v214 offset:3072
	ds_read_b32 v233, v214 offset:3584
	ds_read_b32 v234, v214 offset:4096
	ds_read_b32 v235, v214 offset:4608
	ds_read_b32 v236, v214 offset:5120
	ds_read_b32 v237, v214 offset:5632
	ds_read_b32 v238, v214 offset:6144
	ds_read_b32 v239, v214 offset:6656
	ds_read_b32 v240, v214 offset:7168
	ds_read_b32 v241, v214 offset:7680
	s_waitcnt lgkmcnt(0)
; #define GAS __attribute__((address_space(1)))
; #define LAS __attribute__((address_space(3)))
; #define LDS_WAIT() asm volatile("s_waitcnt lgkmcnt(0)" ::: "memory")
;     const int pr = item >> 1, kb = 2 * (pr / nblk) + (item & 1), nb = pr % nblk, k0 = 64 * kb, n0 = 32 * nb;
;     const int nr = n0 + (lane & 31); const int sc = MAP == 1 ? src_col_in(nr) : nr;
;     float v[32];
; #pragma unroll
;     for (int i = 0; i < 32; ++i) v[i] = sc >= 0 ? W[(size_t)(k0 + 2 * i + (lane >> 5)) * Nsrc + sc] : 0.f;
; #pragma unroll
;     for (int i = 0; i < 32; ++i) { const int k = k0 + 2 * i + (lane >> 5); float x = v[i] * wscale; if (KS) x *= (k < ksplit ? ksA[k] : ksB[k - ksplit]); scr[(2 * i + (lane >> 5)) * 33 + (lane & 31)] = x; }
;     LDS_WAIT(); asm volatile("" ::: "memory");
;     const int c = lane & 7;
; #pragma unroll
;     for (int j = 0; j < 4; ++j) { const int n = (lane >> 3) + 8 * j; const LAS float* s = scr + (8 * c) * 33 + n;
;         const unsigned long long o = (unsigned long long)pg8::pk4_fp8(s[0 * 33], s[1 * 33], s[2 * 33], s[3 * 33]) | ((unsigned long long)pg8::pk4_fp8(s[4 * 33], s[5 * 33], s[6 * 33], s[7 * 33]) << 32);
;         *(GAS unsigned long long*)(WT + (size_t)(n0 + n) * K + k0 + 8 * c) = o; }
;     LDS_WAIT(); asm volatile("" ::: "memory");
; }
	v_max_f32_e32 v226, v226, v226
	v_max_f32_e32 v227, v227, v227
	v_max_f32_e32 v228, v228, v228
	v_max_f32_e32 v229, v229, v229
	v_max_f32_e32 v230, v230, v230
	v_max_f32_e32 v231, v231, v231
	v_max_f32_e32 v232, v232, v232
	v_max_f32_e32 v233, v233, v233
	v_max_f32_e32 v234, v234, v234
	v_max_f32_e32 v235, v235, v235
	v_max_f32_e32 v236, v236, v236
	v_max_f32_e32 v237, v237, v237
	v_max_f32_e32 v238, v238, v238
	v_max_f32_e32 v239, v239, v239
	v_max_f32_e32 v240, v240, v240
	v_max_f32_e32 v241, v241, v241
	v_med3_f32 v226, v226, s62, v95
	v_med3_f32 v227, v227, s62, v95
	v_med3_f32 v228, v228, s62, v95
	v_med3_f32 v229, v229, s62, v95
	v_med3_f32 v230, v230, s62, v95
	v_med3_f32 v231, v231, s62, v95
	v_med3_f32 v232, v232, s62, v95
	v_med3_f32 v233, v233, s62, v95
	v_med3_f32 v234, v234, s62, v95
	v_med3_f32 v235, v235, s62, v95
	v_med3_f32 v236, v236, s62, v95
	v_med3_f32 v237, v237, s62, v95
	v_med3_f32 v238, v238, s62, v95
	v_med3_f32 v239, v239, s62, v95
	v_med3_f32 v240, v240, s62, v95
	v_med3_f32 v241, v241, s62, v95
	v_mov_b32_e32 v242, 0
	v_mov_b32_e32 v243, 0
	v_mov_b32_e32 v244, 0
	v_mov_b32_e32 v245, 0
	v_cvt_pk_fp8_f32 v242, v226, v227
	v_cvt_pk_fp8_f32 v243, v230, v231
	v_cvt_pk_fp8_f32 v244, v234, v235
	v_cvt_pk_fp8_f32 v245, v238, v239
	v_cvt_pk_fp8_f32 v242, v228, v229 op_sel:[0,0,1]
	v_cvt_pk_fp8_f32 v243, v232, v233 op_sel:[0,0,1]
	v_cvt_pk_fp8_f32 v244, v236, v237 op_sel:[0,0,1]
	v_cvt_pk_fp8_f32 v245, v240, v241 op_sel:[0,0,1]
	s_nop 0
	global_store_dwordx4 v80, v[242:245], s[6:7]
	s_waitcnt vmcnt(12)
	v_mul_f32_e32 v144, 0x43000000, v144
	v_mul_f32_e32 v145, 0x43000000, v145
	v_mul_f32_e32 v146, 0x43000000, v146
	v_mul_f32_e32 v147, 0x43000000, v147
	ds_write_b128 v209, v[144:147]
	v_mul_f32_e32 v148, 0x43000000, v148
	v_mul_f32_e32 v149, 0x43000000, v149
	v_mul_f32_e32 v150, 0x43000000, v150
	v_mul_f32_e32 v151, 0x43000000, v151
	ds_write_b128 v209, v[148:151] offset:1024
	v_mul_f32_e32 v152, 0x43000000, v152
	v_mul_f32_e32 v153, 0x43000000, v153
	v_mul_f32_e32 v154, 0x43000000, v154
	v_mul_f32_e32 v155, 0x43000000, v155
	ds_write_b128 v209, v[152:155] offset:2048
	v_mul_f32_e32 v156, 0x43000000, v156
	v_mul_f32_e32 v157, 0x43000000, v157
	v_mul_f32_e32 v158, 0x43000000, v158
	v_mul_f32_e32 v159, 0x43000000, v159
	ds_write_b128 v209, v[156:159] offset:3072
	v_mul_f32_e32 v160, 0x43000000, v160
	v_mul_f32_e32 v161, 0x43000000, v161
	v_mul_f32_e32 v162, 0x43000000, v162
	v_mul_f32_e32 v163, 0x43000000, v163
	ds_write_b128 v209, v[160:163] offset:4096
	v_mul_f32_e32 v164, 0x43000000, v164
	v_mul_f32_e32 v165, 0x43000000, v165
	v_mul_f32_e32 v166, 0x43000000, v166
	v_mul_f32_e32 v167, 0x43000000, v167
	ds_write_b128 v209, v[164:167] offset:5120
	v_mul_f32_e32 v168, 0x43000000, v168
	v_mul_f32_e32 v169, 0x43000000, v169
	v_mul_f32_e32 v170, 0x43000000, v170
	v_mul_f32_e32 v171, 0x43000000, v171
	ds_write_b128 v209, v[168:171] offset:6144
	v_mul_f32_e32 v172, 0x43000000, v172
	v_mul_f32_e32 v173, 0x43000000, v173
	v_mul_f32_e32 v174, 0x43000000, v174
	v_mul_f32_e32 v175, 0x43000000, v175
	ds_write_b128 v209, v[172:175] offset:7168
	s_waitcnt lgkmcnt(0)
	s_barrier
	s_add_u32 s8, s38, 0xc000000
	s_addc_u32 s9, s39, 0
	global_load_dwordx4 v[144:147], v75, s[8:9]
	s_add_u32 s8, s8, 0x8000
	s_addc_u32 s9, s9, 0
	global_load_dwordx4 v[148:151], v75, s[8:9]
	s_add_u32 s8, s8, 0x8000
	s_addc_u32 s9, s9, 0
	global_load_dwordx4 v[152:155], v75, s[8:9]
	s_add_u32 s8, s8, 0x8000
	s_addc_u32 s9, s9, 0
	global_load_dwordx4 v[156:159], v75, s[8:9]
	s_add_u32 s8, s8, 0x8000
	s_addc_u32 s9, s9, 0
	global_load_dwordx4 v[160:163], v75, s[8:9]
	s_add_u32 s8, s8, 0x8000
	s_addc_u32 s9, s9, 0
	global_load_dwordx4 v[164:167], v75, s[8:9]
	s_add_u32 s8, s8, 0x8000
	s_addc_u32 s9, s9, 0
	global_load_dwordx4 v[168:171], v75, s[8:9]
	s_add_u32 s8, s8, 0x8000
	s_addc_u32 s9, s9, 0
	global_load_dwordx4 v[172:175], v75, s[8:9]
	s_add_u32 s6, s40, 0x2002000
	s_addc_u32 s7, s41, 0
	ds_read_b32 v226, v211
	ds_read_b32 v227, v211 offset:512
	ds_read_b32 v228, v211 offset:1024
	ds_read_b32 v229, v211 offset:1536
	ds_read_b32 v230, v211 offset:2048
	ds_read_b32 v231, v211 offset:2560
	ds_read_b32 v232, v211 offset:3072
	ds_read_b32 v233, v211 offset:3584
	ds_read_b32 v234, v211 offset:4096
	ds_read_b32 v235, v211 offset:4608
	ds_read_b32 v236, v211 offset:5120
	ds_read_b32 v237, v211 offset:5632
	ds_read_b32 v238, v211 offset:6144
	ds_read_b32 v239, v211 offset:6656
	ds_read_b32 v240, v211 offset:7168
	ds_read_b32 v241, v211 offset:7680
	s_waitcnt lgkmcnt(0)
	v_max_f32_e32 v226, v226, v226
	v_max_f32_e32 v227, v227, v227
	v_max_f32_e32 v228, v228, v228
	v_max_f32_e32 v229, v229, v229
	v_max_f32_e32 v230, v230, v230
	v_max_f32_e32 v231, v231, v231
	v_max_f32_e32 v232, v232, v232
	v_max_f32_e32 v233, v233, v233
	v_max_f32_e32 v234, v234, v234
	v_max_f32_e32 v235, v235, v235
	v_max_f32_e32 v236, v236, v236
	v_max_f32_e32 v237, v237, v237
	v_max_f32_e32 v238, v238, v238
	v_max_f32_e32 v239, v239, v239
	v_max_f32_e32 v240, v240, v240
	v_max_f32_e32 v241, v241, v241
	v_med3_f32 v226, v226, s62, v95
	v_med3_f32 v227, v227, s62, v95
	v_med3_f32 v228, v228, s62, v95
	v_med3_f32 v229, v229, s62, v95
	v_med3_f32 v230, v230, s62, v95
	v_med3_f32 v231, v231, s62, v95
	v_med3_f32 v232, v232, s62, v95
	v_med3_f32 v233, v233, s62, v95
	v_med3_f32 v234, v234, s62, v95
	v_med3_f32 v235, v235, s62, v95
	v_med3_f32 v236, v236, s62, v95
	v_med3_f32 v237, v237, s62, v95
	v_med3_f32 v238, v238, s62, v95
	v_med3_f32 v239, v239, s62, v95
	v_med3_f32 v240, v240, s62, v95
	v_med3_f32 v241, v241, s62, v95
	v_mov_b32_e32 v242, 0
	v_mov_b32_e32 v243, 0
	v_mov_b32_e32 v244, 0
	v_mov_b32_e32 v245, 0
	v_cvt_pk_fp8_f32 v242, v226, v227
	v_cvt_pk_fp8_f32 v243, v230, v231
	v_cvt_pk_fp8_f32 v244, v234, v235
	v_cvt_pk_fp8_f32 v245, v238, v239
	v_cvt_pk_fp8_f32 v242, v228, v229 op_sel:[0,0,1]
	v_cvt_pk_fp8_f32 v243, v232, v233 op_sel:[0,0,1]
	v_cvt_pk_fp8_f32 v244, v236, v237 op_sel:[0,0,1]
	v_cvt_pk_fp8_f32 v245, v240, v241 op_sel:[0,0,1]
	s_nop 0
	global_store_dwordx4 v79, v[242:245], s[6:7]
	ds_read_b32 v226, v213
	ds_read_b32 v227, v213 offset:512
	ds_read_b32 v228, v213 offset:1024
	ds_read_b32 v229, v213 offset:1536
	ds_read_b32 v230, v213 offset:2048
	ds_read_b32 v231, v213 offset:2560
	ds_read_b32 v232, v213 offset:3072
	ds_read_b32 v233, v213 offset:3584
	ds_read_b32 v234, v213 offset:4096
	ds_read_b32 v235, v213 offset:4608
	ds_read_b32 v236, v213 offset:5120
	ds_read_b32 v237, v213 offset:5632
	ds_read_b32 v238, v213 offset:6144
	ds_read_b32 v239, v213 offset:6656
	ds_read_b32 v240, v213 offset:7168
	ds_read_b32 v241, v213 offset:7680
	s_waitcnt lgkmcnt(0)
; #define GAS __attribute__((address_space(1)))
; #define LAS __attribute__((address_space(3)))
; #define LDS_WAIT() asm volatile("s_waitcnt lgkmcnt(0)" ::: "memory")
;     const int pr = item >> 1, kb = 2 * (pr / nblk) + (item & 1), nb = pr % nblk, k0 = 64 * kb, n0 = 32 * nb;
;     const int nr = n0 + (lane & 31); const int sc = MAP == 1 ? src_col_in(nr) : nr;
;     float v[32];
; #pragma unroll
;     for (int i = 0; i < 32; ++i) v[i] = sc >= 0 ? W[(size_t)(k0 + 2 * i + (lane >> 5)) * Nsrc + sc] : 0.f;
; #pragma unroll
;     for (int i = 0; i < 32; ++i) { const int k = k0 + 2 * i + (lane >> 5); float x = v[i] * wscale; if (KS) x *= (k < ksplit ? ksA[k] : ksB[k - ksplit]); scr[(2 * i + (lane >> 5)) * 33 + (lane & 31)] = x; }
;     LDS_WAIT(); asm volatile("" ::: "memory");
;     const int c = lane & 7;
; #pragma unroll
;     for (int j = 0; j < 4; ++j) { const int n = (lane >> 3) + 8 * j; const LAS float* s = scr + (8 * c) * 33 + n;
;         const unsigned long long o = (unsigned long long)pg8::pk4_fp8(s[0 * 33], s[1 * 33], s[2 * 33], s[3 * 33]) | ((unsigned long long)pg8::pk4_fp8(s[4 * 33], s[5 * 33], s[6 * 33], s[7 * 33]) << 32);
;         *(GAS unsigned long long*)(WT + (size_t)(n0 + n) * K + k0 + 8 * c) = o; }
;     LDS_WAIT(); asm volatile("" ::: "memory");
; }
	v_max_f32_e32 v226, v226, v226
	v_max_f32_e32 v227, v227, v227
	v_max_f32_e32 v228, v228, v228
	v_max_f32_e32 v229, v229, v229
	v_max_f32_e32 v230, v230, v230
	v_max_f32_e32 v231, v231, v231
	v_max_f32_e32 v232, v232, v232
	v_max_f32_e32 v233, v233, v233
	v_max_f32_e32 v234, v234, v234
	v_max_f32_e32 v235, v235, v235
	v_max_f32_e32 v236, v236, v236
	v_max_f32_e32 v237, v237, v237
	v_max_f32_e32 v238, v238, v238
	v_max_f32_e32 v239, v239, v239
	v_max_f32_e32 v240, v240, v240
	v_max_f32_e32 v241, v241, v241
	v_med3_f32 v226, v226, s62, v95
	v_med3_f32 v227, v227, s62, v95
	v_med3_f32 v228, v228, s62, v95
	v_med3_f32 v229, v229, s62, v95
	v_med3_f32 v230, v230, s62, v95
	v_med3_f32 v231, v231, s62, v95
	v_med3_f32 v232, v232, s62, v95
	v_med3_f32 v233, v233, s62, v95
	v_med3_f32 v234, v234, s62, v95
	v_med3_f32 v235, v235, s62, v95
	v_med3_f32 v236, v236, s62, v95
	v_med3_f32 v237, v237, s62, v95
	v_med3_f32 v238, v238, s62, v95
	v_med3_f32 v239, v239, s62, v95
	v_med3_f32 v240, v240, s62, v95
	v_med3_f32 v241, v241, s62, v95
	v_mov_b32_e32 v242, 0
	v_mov_b32_e32 v243, 0
	v_mov_b32_e32 v244, 0
	v_mov_b32_e32 v245, 0
	v_cvt_pk_fp8_f32 v242, v226, v227
	v_cvt_pk_fp8_f32 v243, v230, v231
	v_cvt_pk_fp8_f32 v244, v234, v235
	v_cvt_pk_fp8_f32 v245, v238, v239
	v_cvt_pk_fp8_f32 v242, v228, v229 op_sel:[0,0,1]
	v_cvt_pk_fp8_f32 v243, v232, v233 op_sel:[0,0,1]
	v_cvt_pk_fp8_f32 v244, v236, v237 op_sel:[0,0,1]
	v_cvt_pk_fp8_f32 v245, v240, v241 op_sel:[0,0,1]
	s_nop 0
	global_store_dwordx4 v80, v[242:245], s[6:7]
	s_waitcnt vmcnt(12)
	v_mul_f32_e32 v176, 0x43000000, v176
	v_mul_f32_e32 v177, 0x43000000, v177
	v_mul_f32_e32 v178, 0x43000000, v178
	v_mul_f32_e32 v179, 0x43000000, v179
	ds_write_b128 v210, v[176:179]
	v_mul_f32_e32 v180, 0x43000000, v180
	v_mul_f32_e32 v181, 0x43000000, v181
	v_mul_f32_e32 v182, 0x43000000, v182
	v_mul_f32_e32 v183, 0x43000000, v183
	ds_write_b128 v210, v[180:183] offset:1024
	v_mul_f32_e32 v184, 0x43000000, v184
	v_mul_f32_e32 v185, 0x43000000, v185
	v_mul_f32_e32 v186, 0x43000000, v186
	v_mul_f32_e32 v187, 0x43000000, v187
	ds_write_b128 v210, v[184:187] offset:2048
	v_mul_f32_e32 v188, 0x43000000, v188
	v_mul_f32_e32 v189, 0x43000000, v189
	v_mul_f32_e32 v190, 0x43000000, v190
	v_mul_f32_e32 v191, 0x43000000, v191
	ds_write_b128 v210, v[188:191] offset:3072
	v_mul_f32_e32 v192, 0x43000000, v192
	v_mul_f32_e32 v193, 0x43000000, v193
	v_mul_f32_e32 v194, 0x43000000, v194
	v_mul_f32_e32 v195, 0x43000000, v195
	ds_write_b128 v210, v[192:195] offset:4096
	v_mul_f32_e32 v196, 0x43000000, v196
	v_mul_f32_e32 v197, 0x43000000, v197
	v_mul_f32_e32 v198, 0x43000000, v198
	v_mul_f32_e32 v199, 0x43000000, v199
	ds_write_b128 v210, v[196:199] offset:5120
	v_mul_f32_e32 v200, 0x43000000, v200
	v_mul_f32_e32 v201, 0x43000000, v201
	v_mul_f32_e32 v202, 0x43000000, v202
	v_mul_f32_e32 v203, 0x43000000, v203
	ds_write_b128 v210, v[200:203] offset:6144
	v_mul_f32_e32 v204, 0x43000000, v204
	v_mul_f32_e32 v205, 0x43000000, v205
	v_mul_f32_e32 v206, 0x43000000, v206
	v_mul_f32_e32 v207, 0x43000000, v207
	ds_write_b128 v210, v[204:207] offset:7168
	s_waitcnt lgkmcnt(0)
	s_barrier
	s_add_u32 s8, s38, 0xc001000
	s_addc_u32 s9, s39, 0
	global_load_dwordx4 v[176:179], v75, s[8:9]
	s_add_u32 s8, s8, 0x8000
	s_addc_u32 s9, s9, 0
	global_load_dwordx4 v[180:183], v75, s[8:9]
	s_add_u32 s8, s8, 0x8000
	s_addc_u32 s9, s9, 0
	global_load_dwordx4 v[184:187], v75, s[8:9]
	s_add_u32 s8, s8, 0x8000
	s_addc_u32 s9, s9, 0
	global_load_dwordx4 v[188:191], v75, s[8:9]
	s_add_u32 s8, s8, 0x8000
	s_addc_u32 s9, s9, 0
	global_load_dwordx4 v[192:195], v75, s[8:9]
	s_add_u32 s8, s8, 0x8000
	s_addc_u32 s9, s9, 0
	global_load_dwordx4 v[196:199], v75, s[8:9]
	s_add_u32 s8, s8, 0x8000
	s_addc_u32 s9, s9, 0
	global_load_dwordx4 v[200:203], v75, s[8:9]
	s_add_u32 s8, s8, 0x8000
	s_addc_u32 s9, s9, 0
	global_load_dwordx4 v[204:207], v75, s[8:9]
	s_add_u32 s6, s40, 0x3002000
	s_addc_u32 s7, s41, 0
	ds_read_b32 v226, v212
	ds_read_b32 v227, v212 offset:512
	ds_read_b32 v228, v212 offset:1024
	ds_read_b32 v229, v212 offset:1536
	ds_read_b32 v230, v212 offset:2048
	ds_read_b32 v231, v212 offset:2560
	ds_read_b32 v232, v212 offset:3072
	ds_read_b32 v233, v212 offset:3584
	ds_read_b32 v234, v212 offset:4096
	ds_read_b32 v235, v212 offset:4608
	ds_read_b32 v236, v212 offset:5120
	ds_read_b32 v237, v212 offset:5632
	ds_read_b32 v238, v212 offset:6144
	ds_read_b32 v239, v212 offset:6656
	ds_read_b32 v240, v212 offset:7168
	ds_read_b32 v241, v212 offset:7680
	s_waitcnt lgkmcnt(0)
	v_max_f32_e32 v226, v226, v226
	v_max_f32_e32 v227, v227, v227
	v_max_f32_e32 v228, v228, v228
	v_max_f32_e32 v229, v229, v229
	v_max_f32_e32 v230, v230, v230
	v_max_f32_e32 v231, v231, v231
	v_max_f32_e32 v232, v232, v232
	v_max_f32_e32 v233, v233, v233
	v_max_f32_e32 v234, v234, v234
	v_max_f32_e32 v235, v235, v235
	v_max_f32_e32 v236, v236, v236
	v_max_f32_e32 v237, v237, v237
	v_max_f32_e32 v238, v238, v238
	v_max_f32_e32 v239, v239, v239
	v_max_f32_e32 v240, v240, v240
	v_max_f32_e32 v241, v241, v241
	v_med3_f32 v226, v226, s62, v95
	v_med3_f32 v227, v227, s62, v95
	v_med3_f32 v228, v228, s62, v95
	v_med3_f32 v229, v229, s62, v95
	v_med3_f32 v230, v230, s62, v95
	v_med3_f32 v231, v231, s62, v95
	v_med3_f32 v232, v232, s62, v95
	v_med3_f32 v233, v233, s62, v95
	v_med3_f32 v234, v234, s62, v95
	v_med3_f32 v235, v235, s62, v95
	v_med3_f32 v236, v236, s62, v95
	v_med3_f32 v237, v237, s62, v95
	v_med3_f32 v238, v238, s62, v95
	v_med3_f32 v239, v239, s62, v95
	v_med3_f32 v240, v240, s62, v95
	v_med3_f32 v241, v241, s62, v95
	v_mov_b32_e32 v242, 0
	v_mov_b32_e32 v243, 0
	v_mov_b32_e32 v244, 0
	v_mov_b32_e32 v245, 0
	v_cvt_pk_fp8_f32 v242, v226, v227
	v_cvt_pk_fp8_f32 v243, v230, v231
	v_cvt_pk_fp8_f32 v244, v234, v235
	v_cvt_pk_fp8_f32 v245, v238, v239
	v_cvt_pk_fp8_f32 v242, v228, v229 op_sel:[0,0,1]
	v_cvt_pk_fp8_f32 v243, v232, v233 op_sel:[0,0,1]
	v_cvt_pk_fp8_f32 v244, v236, v237 op_sel:[0,0,1]
	v_cvt_pk_fp8_f32 v245, v240, v241 op_sel:[0,0,1]
	s_nop 0
	global_store_dwordx4 v79, v[242:245], s[6:7]
	ds_read_b32 v226, v214
	ds_read_b32 v227, v214 offset:512
	ds_read_b32 v228, v214 offset:1024
	ds_read_b32 v229, v214 offset:1536
	ds_read_b32 v230, v214 offset:2048
	ds_read_b32 v231, v214 offset:2560
	ds_read_b32 v232, v214 offset:3072
	ds_read_b32 v233, v214 offset:3584
	ds_read_b32 v234, v214 offset:4096
	ds_read_b32 v235, v214 offset:4608
	ds_read_b32 v236, v214 offset:5120
	ds_read_b32 v237, v214 offset:5632
	ds_read_b32 v238, v214 offset:6144
	ds_read_b32 v239, v214 offset:6656
	ds_read_b32 v240, v214 offset:7168
	ds_read_b32 v241, v214 offset:7680
	s_waitcnt lgkmcnt(0)
; #define GAS __attribute__((address_space(1)))
; #define LAS __attribute__((address_space(3)))
; #define LDS_WAIT() asm volatile("s_waitcnt lgkmcnt(0)" ::: "memory")
;     const int pr = item >> 1, kb = 2 * (pr / nblk) + (item & 1), nb = pr % nblk, k0 = 64 * kb, n0 = 32 * nb;
;     const int nr = n0 + (lane & 31); const int sc = MAP == 1 ? src_col_in(nr) : nr;
;     float v[32];
; #pragma unroll
;     for (int i = 0; i < 32; ++i) v[i] = sc >= 0 ? W[(size_t)(k0 + 2 * i + (lane >> 5)) * Nsrc + sc] : 0.f;
; #pragma unroll
;     for (int i = 0; i < 32; ++i) { const int k = k0 + 2 * i + (lane >> 5); float x = v[i] * wscale; if (KS) x *= (k < ksplit ? ksA[k] : ksB[k - ksplit]); scr[(2 * i + (lane >> 5)) * 33 + (lane & 31)] = x; }
;     LDS_WAIT(); asm volatile("" ::: "memory");
;     const int c = lane & 7;
; #pragma unroll
;     for (int j = 0; j < 4; ++j) { const int n = (lane >> 3) + 8 * j; const LAS float* s = scr + (8 * c) * 33 + n;
;         const unsigned long long o = (unsigned long long)pg8::pk4_fp8(s[0 * 33], s[1 * 33], s[2 * 33], s[3 * 33]) | ((unsigned long long)pg8::pk4_fp8(s[4 * 33], s[5 * 33], s[6 * 33], s[7 * 33]) << 32);
;         *(GAS unsigned long long*)(WT + (size_t)(n0 + n) * K + k0 + 8 * c) = o; }
;     LDS_WAIT(); asm volatile("" ::: "memory");
; }
	v_max_f32_e32 v226, v226, v226
	v_max_f32_e32 v227, v227, v227
	v_max_f32_e32 v228, v228, v228
	v_max_f32_e32 v229, v229, v229
	v_max_f32_e32 v230, v230, v230
	v_max_f32_e32 v231, v231, v231
	v_max_f32_e32 v232, v232, v232
	v_max_f32_e32 v233, v233, v233
	v_max_f32_e32 v234, v234, v234
	v_max_f32_e32 v235, v235, v235
	v_max_f32_e32 v236, v236, v236
	v_max_f32_e32 v237, v237, v237
	v_max_f32_e32 v238, v238, v238
	v_max_f32_e32 v239, v239, v239
	v_max_f32_e32 v240, v240, v240
	v_max_f32_e32 v241, v241, v241
	v_med3_f32 v226, v226, s62, v95
	v_med3_f32 v227, v227, s62, v95
	v_med3_f32 v228, v228, s62, v95
	v_med3_f32 v229, v229, s62, v95
	v_med3_f32 v230, v230, s62, v95
	v_med3_f32 v231, v231, s62, v95
	v_med3_f32 v232, v232, s62, v95
	v_med3_f32 v233, v233, s62, v95
	v_med3_f32 v234, v234, s62, v95
	v_med3_f32 v235, v235, s62, v95
	v_med3_f32 v236, v236, s62, v95
	v_med3_f32 v237, v237, s62, v95
	v_med3_f32 v238, v238, s62, v95
	v_med3_f32 v239, v239, s62, v95
	v_med3_f32 v240, v240, s62, v95
	v_med3_f32 v241, v241, s62, v95
	v_mov_b32_e32 v242, 0
	v_mov_b32_e32 v243, 0
	v_mov_b32_e32 v244, 0
	v_mov_b32_e32 v245, 0
	v_cvt_pk_fp8_f32 v242, v226, v227
	v_cvt_pk_fp8_f32 v243, v230, v231
	v_cvt_pk_fp8_f32 v244, v234, v235
	v_cvt_pk_fp8_f32 v245, v238, v239
	v_cvt_pk_fp8_f32 v242, v228, v229 op_sel:[0,0,1]
	v_cvt_pk_fp8_f32 v243, v232, v233 op_sel:[0,0,1]
	v_cvt_pk_fp8_f32 v244, v236, v237 op_sel:[0,0,1]
	v_cvt_pk_fp8_f32 v245, v240, v241 op_sel:[0,0,1]
	s_nop 0
	global_store_dwordx4 v80, v[242:245], s[6:7]
	s_waitcnt vmcnt(12)
	v_mul_f32_e32 v144, 0x43000000, v144
	v_mul_f32_e32 v145, 0x43000000, v145
	v_mul_f32_e32 v146, 0x43000000, v146
	v_mul_f32_e32 v147, 0x43000000, v147
	ds_write_b128 v209, v[144:147]
	v_mul_f32_e32 v148, 0x43000000, v148
	v_mul_f32_e32 v149, 0x43000000, v149
	v_mul_f32_e32 v150, 0x43000000, v150
	v_mul_f32_e32 v151, 0x43000000, v151
	ds_write_b128 v209, v[148:151] offset:1024
	v_mul_f32_e32 v152, 0x43000000, v152
	v_mul_f32_e32 v153, 0x43000000, v153
	v_mul_f32_e32 v154, 0x43000000, v154
	v_mul_f32_e32 v155, 0x43000000, v155
	ds_write_b128 v209, v[152:155] offset:2048
	v_mul_f32_e32 v156, 0x43000000, v156
	v_mul_f32_e32 v157, 0x43000000, v157
	v_mul_f32_e32 v158, 0x43000000, v158
	v_mul_f32_e32 v159, 0x43000000, v159
	ds_write_b128 v209, v[156:159] offset:3072
	v_mul_f32_e32 v160, 0x43000000, v160
	v_mul_f32_e32 v161, 0x43000000, v161
	v_mul_f32_e32 v162, 0x43000000, v162
	v_mul_f32_e32 v163, 0x43000000, v163
	ds_write_b128 v209, v[160:163] offset:4096
	v_mul_f32_e32 v164, 0x43000000, v164
	v_mul_f32_e32 v165, 0x43000000, v165
	v_mul_f32_e32 v166, 0x43000000, v166
	v_mul_f32_e32 v167, 0x43000000, v167
	ds_write_b128 v209, v[164:167] offset:5120
	v_mul_f32_e32 v168, 0x43000000, v168
	v_mul_f32_e32 v169, 0x43000000, v169
	v_mul_f32_e32 v170, 0x43000000, v170
	v_mul_f32_e32 v171, 0x43000000, v171
	ds_write_b128 v209, v[168:171] offset:6144
	v_mul_f32_e32 v172, 0x43000000, v172
	v_mul_f32_e32 v173, 0x43000000, v173
	v_mul_f32_e32 v174, 0x43000000, v174
	v_mul_f32_e32 v175, 0x43000000, v175
	ds_write_b128 v209, v[172:175] offset:7168
	s_waitcnt lgkmcnt(0)
	s_barrier
	s_add_u32 s8, s38, 0xc002000
	s_addc_u32 s9, s39, 0
	global_load_dwordx4 v[144:147], v75, s[8:9]
	s_add_u32 s8, s8, 0x8000
	s_addc_u32 s9, s9, 0
	global_load_dwordx4 v[148:151], v75, s[8:9]
	s_add_u32 s8, s8, 0x8000
	s_addc_u32 s9, s9, 0
	global_load_dwordx4 v[152:155], v75, s[8:9]
	s_add_u32 s8, s8, 0x8000
	s_addc_u32 s9, s9, 0
	global_load_dwordx4 v[156:159], v75, s[8:9]
	s_add_u32 s8, s8, 0x8000
	s_addc_u32 s9, s9, 0
	global_load_dwordx4 v[160:163], v75, s[8:9]
	s_add_u32 s8, s8, 0x8000
	s_addc_u32 s9, s9, 0
	global_load_dwordx4 v[164:167], v75, s[8:9]
	s_add_u32 s8, s8, 0x8000
	s_addc_u32 s9, s9, 0
	global_load_dwordx4 v[168:171], v75, s[8:9]
	s_add_u32 s8, s8, 0x8000
	s_addc_u32 s9, s9, 0
	global_load_dwordx4 v[172:175], v75, s[8:9]
	s_add_u32 s6, s40, 0x3000
	s_addc_u32 s7, s41, 0
	ds_read_b32 v226, v211
	ds_read_b32 v227, v211 offset:512
	ds_read_b32 v228, v211 offset:1024
	ds_read_b32 v229, v211 offset:1536
	ds_read_b32 v230, v211 offset:2048
	ds_read_b32 v231, v211 offset:2560
	ds_read_b32 v232, v211 offset:3072
	ds_read_b32 v233, v211 offset:3584
	ds_read_b32 v234, v211 offset:4096
	ds_read_b32 v235, v211 offset:4608
	ds_read_b32 v236, v211 offset:5120
	ds_read_b32 v237, v211 offset:5632
	ds_read_b32 v238, v211 offset:6144
	ds_read_b32 v239, v211 offset:6656
	ds_read_b32 v240, v211 offset:7168
	ds_read_b32 v241, v211 offset:7680
	s_waitcnt lgkmcnt(0)
	v_max_f32_e32 v226, v226, v226
	v_max_f32_e32 v227, v227, v227
	v_max_f32_e32 v228, v228, v228
	v_max_f32_e32 v229, v229, v229
	v_max_f32_e32 v230, v230, v230
	v_max_f32_e32 v231, v231, v231
	v_max_f32_e32 v232, v232, v232
	v_max_f32_e32 v233, v233, v233
	v_max_f32_e32 v234, v234, v234
	v_max_f32_e32 v235, v235, v235
	v_max_f32_e32 v236, v236, v236
	v_max_f32_e32 v237, v237, v237
	v_max_f32_e32 v238, v238, v238
	v_max_f32_e32 v239, v239, v239
	v_max_f32_e32 v240, v240, v240
	v_max_f32_e32 v241, v241, v241
	v_med3_f32 v226, v226, s62, v95
	v_med3_f32 v227, v227, s62, v95
	v_med3_f32 v228, v228, s62, v95
	v_med3_f32 v229, v229, s62, v95
	v_med3_f32 v230, v230, s62, v95
	v_med3_f32 v231, v231, s62, v95
	v_med3_f32 v232, v232, s62, v95
	v_med3_f32 v233, v233, s62, v95
	v_med3_f32 v234, v234, s62, v95
	v_med3_f32 v235, v235, s62, v95
	v_med3_f32 v236, v236, s62, v95
	v_med3_f32 v237, v237, s62, v95
	v_med3_f32 v238, v238, s62, v95
	v_med3_f32 v239, v239, s62, v95
	v_med3_f32 v240, v240, s62, v95
	v_med3_f32 v241, v241, s62, v95
	v_mov_b32_e32 v242, 0
	v_mov_b32_e32 v243, 0
	v_mov_b32_e32 v244, 0
	v_mov_b32_e32 v245, 0
	v_cvt_pk_fp8_f32 v242, v226, v227
	v_cvt_pk_fp8_f32 v243, v230, v231
	v_cvt_pk_fp8_f32 v244, v234, v235
	v_cvt_pk_fp8_f32 v245, v238, v239
	v_cvt_pk_fp8_f32 v242, v228, v229 op_sel:[0,0,1]
	v_cvt_pk_fp8_f32 v243, v232, v233 op_sel:[0,0,1]
	v_cvt_pk_fp8_f32 v244, v236, v237 op_sel:[0,0,1]
	v_cvt_pk_fp8_f32 v245, v240, v241 op_sel:[0,0,1]
	s_nop 0
	global_store_dwordx4 v79, v[242:245], s[6:7]
	ds_read_b32 v226, v213
	ds_read_b32 v227, v213 offset:512
	ds_read_b32 v228, v213 offset:1024
	ds_read_b32 v229, v213 offset:1536
	ds_read_b32 v230, v213 offset:2048
	ds_read_b32 v231, v213 offset:2560
	ds_read_b32 v232, v213 offset:3072
	ds_read_b32 v233, v213 offset:3584
	ds_read_b32 v234, v213 offset:4096
	ds_read_b32 v235, v213 offset:4608
	ds_read_b32 v236, v213 offset:5120
	ds_read_b32 v237, v213 offset:5632
	ds_read_b32 v238, v213 offset:6144
	ds_read_b32 v239, v213 offset:6656
	ds_read_b32 v240, v213 offset:7168
	ds_read_b32 v241, v213 offset:7680
	s_waitcnt lgkmcnt(0)
; #define GAS __attribute__((address_space(1)))
; #define LAS __attribute__((address_space(3)))
; #define LDS_WAIT() asm volatile("s_waitcnt lgkmcnt(0)" ::: "memory")
;     const int pr = item >> 1, kb = 2 * (pr / nblk) + (item & 1), nb = pr % nblk, k0 = 64 * kb, n0 = 32 * nb;
;     const int nr = n0 + (lane & 31); const int sc = MAP == 1 ? src_col_in(nr) : nr;
;     float v[32];
; #pragma unroll
;     for (int i = 0; i < 32; ++i) v[i] = sc >= 0 ? W[(size_t)(k0 + 2 * i + (lane >> 5)) * Nsrc + sc] : 0.f;
; #pragma unroll
;     for (int i = 0; i < 32; ++i) { const int k = k0 + 2 * i + (lane >> 5); float x = v[i] * wscale; if (KS) x *= (k < ksplit ? ksA[k] : ksB[k - ksplit]); scr[(2 * i + (lane >> 5)) * 33 + (lane & 31)] = x; }
;     LDS_WAIT(); asm volatile("" ::: "memory");
;     const int c = lane & 7;
; #pragma unroll
;     for (int j = 0; j < 4; ++j) { const int n = (lane >> 3) + 8 * j; const LAS float* s = scr + (8 * c) * 33 + n;
;         const unsigned long long o = (unsigned long long)pg8::pk4_fp8(s[0 * 33], s[1 * 33], s[2 * 33], s[3 * 33]) | ((unsigned long long)pg8::pk4_fp8(s[4 * 33], s[5 * 33], s[6 * 33], s[7 * 33]) << 32);
;         *(GAS unsigned long long*)(WT + (size_t)(n0 + n) * K + k0 + 8 * c) = o; }
;     LDS_WAIT(); asm volatile("" ::: "memory");
; }
	v_max_f32_e32 v226, v226, v226
	v_max_f32_e32 v227, v227, v227
	v_max_f32_e32 v228, v228, v228
	v_max_f32_e32 v229, v229, v229
	v_max_f32_e32 v230, v230, v230
	v_max_f32_e32 v231, v231, v231
	v_max_f32_e32 v232, v232, v232
	v_max_f32_e32 v233, v233, v233
	v_max_f32_e32 v234, v234, v234
	v_max_f32_e32 v235, v235, v235
	v_max_f32_e32 v236, v236, v236
	v_max_f32_e32 v237, v237, v237
	v_max_f32_e32 v238, v238, v238
	v_max_f32_e32 v239, v239, v239
	v_max_f32_e32 v240, v240, v240
	v_max_f32_e32 v241, v241, v241
	v_med3_f32 v226, v226, s62, v95
	v_med3_f32 v227, v227, s62, v95
	v_med3_f32 v228, v228, s62, v95
	v_med3_f32 v229, v229, s62, v95
	v_med3_f32 v230, v230, s62, v95
	v_med3_f32 v231, v231, s62, v95
	v_med3_f32 v232, v232, s62, v95
	v_med3_f32 v233, v233, s62, v95
	v_med3_f32 v234, v234, s62, v95
	v_med3_f32 v235, v235, s62, v95
	v_med3_f32 v236, v236, s62, v95
	v_med3_f32 v237, v237, s62, v95
	v_med3_f32 v238, v238, s62, v95
	v_med3_f32 v239, v239, s62, v95
	v_med3_f32 v240, v240, s62, v95
	v_med3_f32 v241, v241, s62, v95
	v_mov_b32_e32 v242, 0
	v_mov_b32_e32 v243, 0
	v_mov_b32_e32 v244, 0
	v_mov_b32_e32 v245, 0
	v_cvt_pk_fp8_f32 v242, v226, v227
	v_cvt_pk_fp8_f32 v243, v230, v231
	v_cvt_pk_fp8_f32 v244, v234, v235
	v_cvt_pk_fp8_f32 v245, v238, v239
	v_cvt_pk_fp8_f32 v242, v228, v229 op_sel:[0,0,1]
	v_cvt_pk_fp8_f32 v243, v232, v233 op_sel:[0,0,1]
	v_cvt_pk_fp8_f32 v244, v236, v237 op_sel:[0,0,1]
	v_cvt_pk_fp8_f32 v245, v240, v241 op_sel:[0,0,1]
	s_nop 0
	global_store_dwordx4 v80, v[242:245], s[6:7]
	s_waitcnt vmcnt(12)
	v_mul_f32_e32 v176, 0x43000000, v176
	v_mul_f32_e32 v177, 0x43000000, v177
	v_mul_f32_e32 v178, 0x43000000, v178
	v_mul_f32_e32 v179, 0x43000000, v179
	ds_write_b128 v210, v[176:179]
	v_mul_f32_e32 v180, 0x43000000, v180
	v_mul_f32_e32 v181, 0x43000000, v181
	v_mul_f32_e32 v182, 0x43000000, v182
	v_mul_f32_e32 v183, 0x43000000, v183
	ds_write_b128 v210, v[180:183] offset:1024
	v_mul_f32_e32 v184, 0x43000000, v184
	v_mul_f32_e32 v185, 0x43000000, v185
	v_mul_f32_e32 v186, 0x43000000, v186
	v_mul_f32_e32 v187, 0x43000000, v187
	ds_write_b128 v210, v[184:187] offset:2048
	v_mul_f32_e32 v188, 0x43000000, v188
	v_mul_f32_e32 v189, 0x43000000, v189
	v_mul_f32_e32 v190, 0x43000000, v190
	v_mul_f32_e32 v191, 0x43000000, v191
	ds_write_b128 v210, v[188:191] offset:3072
	v_mul_f32_e32 v192, 0x43000000, v192
	v_mul_f32_e32 v193, 0x43000000, v193
	v_mul_f32_e32 v194, 0x43000000, v194
	v_mul_f32_e32 v195, 0x43000000, v195
	ds_write_b128 v210, v[192:195] offset:4096
	v_mul_f32_e32 v196, 0x43000000, v196
	v_mul_f32_e32 v197, 0x43000000, v197
	v_mul_f32_e32 v198, 0x43000000, v198
	v_mul_f32_e32 v199, 0x43000000, v199
	ds_write_b128 v210, v[196:199] offset:5120
	v_mul_f32_e32 v200, 0x43000000, v200
	v_mul_f32_e32 v201, 0x43000000, v201
	v_mul_f32_e32 v202, 0x43000000, v202
	v_mul_f32_e32 v203, 0x43000000, v203
	ds_write_b128 v210, v[200:203] offset:6144
	v_mul_f32_e32 v204, 0x43000000, v204
	v_mul_f32_e32 v205, 0x43000000, v205
	v_mul_f32_e32 v206, 0x43000000, v206
	v_mul_f32_e32 v207, 0x43000000, v207
	ds_write_b128 v210, v[204:207] offset:7168
	s_waitcnt lgkmcnt(0)
	s_barrier
	s_add_u32 s8, s38, 0xc003000
	s_addc_u32 s9, s39, 0
	global_load_dwordx4 v[176:179], v75, s[8:9]
	s_add_u32 s8, s8, 0x8000
	s_addc_u32 s9, s9, 0
	global_load_dwordx4 v[180:183], v75, s[8:9]
	s_add_u32 s8, s8, 0x8000
	s_addc_u32 s9, s9, 0
	global_load_dwordx4 v[184:187], v75, s[8:9]
	s_add_u32 s8, s8, 0x8000
	s_addc_u32 s9, s9, 0
	global_load_dwordx4 v[188:191], v75, s[8:9]
	s_add_u32 s8, s8, 0x8000
	s_addc_u32 s9, s9, 0
	global_load_dwordx4 v[192:195], v75, s[8:9]
	s_add_u32 s8, s8, 0x8000
	s_addc_u32 s9, s9, 0
	global_load_dwordx4 v[196:199], v75, s[8:9]
	s_add_u32 s8, s8, 0x8000
	s_addc_u32 s9, s9, 0
	global_load_dwordx4 v[200:203], v75, s[8:9]
	s_add_u32 s8, s8, 0x8000
	s_addc_u32 s9, s9, 0
	global_load_dwordx4 v[204:207], v75, s[8:9]
	s_add_u32 s6, s40, 0x1003000
	s_addc_u32 s7, s41, 0
	ds_read_b32 v226, v212
	ds_read_b32 v227, v212 offset:512
	ds_read_b32 v228, v212 offset:1024
	ds_read_b32 v229, v212 offset:1536
	ds_read_b32 v230, v212 offset:2048
	ds_read_b32 v231, v212 offset:2560
	ds_read_b32 v232, v212 offset:3072
	ds_read_b32 v233, v212 offset:3584
	ds_read_b32 v234, v212 offset:4096
	ds_read_b32 v235, v212 offset:4608
	ds_read_b32 v236, v212 offset:5120
	ds_read_b32 v237, v212 offset:5632
	ds_read_b32 v238, v212 offset:6144
	ds_read_b32 v239, v212 offset:6656
	ds_read_b32 v240, v212 offset:7168
	ds_read_b32 v241, v212 offset:7680
	s_waitcnt lgkmcnt(0)
	v_max_f32_e32 v226, v226, v226
	v_max_f32_e32 v227, v227, v227
	v_max_f32_e32 v228, v228, v228
	v_max_f32_e32 v229, v229, v229
	v_max_f32_e32 v230, v230, v230
	v_max_f32_e32 v231, v231, v231
	v_max_f32_e32 v232, v232, v232
	v_max_f32_e32 v233, v233, v233
	v_max_f32_e32 v234, v234, v234
	v_max_f32_e32 v235, v235, v235
	v_max_f32_e32 v236, v236, v236
	v_max_f32_e32 v237, v237, v237
	v_max_f32_e32 v238, v238, v238
	v_max_f32_e32 v239, v239, v239
	v_max_f32_e32 v240, v240, v240
	v_max_f32_e32 v241, v241, v241
	v_med3_f32 v226, v226, s62, v95
	v_med3_f32 v227, v227, s62, v95
	v_med3_f32 v228, v228, s62, v95
	v_med3_f32 v229, v229, s62, v95
	v_med3_f32 v230, v230, s62, v95
	v_med3_f32 v231, v231, s62, v95
	v_med3_f32 v232, v232, s62, v95
	v_med3_f32 v233, v233, s62, v95
	v_med3_f32 v234, v234, s62, v95
	v_med3_f32 v235, v235, s62, v95
	v_med3_f32 v236, v236, s62, v95
	v_med3_f32 v237, v237, s62, v95
	v_med3_f32 v238, v238, s62, v95
	v_med3_f32 v239, v239, s62, v95
	v_med3_f32 v240, v240, s62, v95
	v_med3_f32 v241, v241, s62, v95
	v_mov_b32_e32 v242, 0
	v_mov_b32_e32 v243, 0
	v_mov_b32_e32 v244, 0
	v_mov_b32_e32 v245, 0
	v_cvt_pk_fp8_f32 v242, v226, v227
	v_cvt_pk_fp8_f32 v243, v230, v231
	v_cvt_pk_fp8_f32 v244, v234, v235
	v_cvt_pk_fp8_f32 v245, v238, v239
	v_cvt_pk_fp8_f32 v242, v228, v229 op_sel:[0,0,1]
	v_cvt_pk_fp8_f32 v243, v232, v233 op_sel:[0,0,1]
	v_cvt_pk_fp8_f32 v244, v236, v237 op_sel:[0,0,1]
	v_cvt_pk_fp8_f32 v245, v240, v241 op_sel:[0,0,1]
	s_nop 0
	global_store_dwordx4 v79, v[242:245], s[6:7]
	ds_read_b32 v226, v214
	ds_read_b32 v227, v214 offset:512
	ds_read_b32 v228, v214 offset:1024
	ds_read_b32 v229, v214 offset:1536
	ds_read_b32 v230, v214 offset:2048
	ds_read_b32 v231, v214 offset:2560
	ds_read_b32 v232, v214 offset:3072
	ds_read_b32 v233, v214 offset:3584
	ds_read_b32 v234, v214 offset:4096
	ds_read_b32 v235, v214 offset:4608
	ds_read_b32 v236, v214 offset:5120
	ds_read_b32 v237, v214 offset:5632
	ds_read_b32 v238, v214 offset:6144
	ds_read_b32 v239, v214 offset:6656
	ds_read_b32 v240, v214 offset:7168
	ds_read_b32 v241, v214 offset:7680
	s_waitcnt lgkmcnt(0)
; #define GAS __attribute__((address_space(1)))
; #define LAS __attribute__((address_space(3)))
; #define LDS_WAIT() asm volatile("s_waitcnt lgkmcnt(0)" ::: "memory")
; __device__ __forceinline__ int nat_dim(int p) { return (p >> 1) + 64 * (p & 1); }
; template <int MAP, bool KS, bool KPERM = false>
; __device__ __forceinline__ void p0_transpose_item(const float* W, int K, int Nsrc, int nblk, bf16* WT, const float* ksA, const float* ksB, int ksplit, LAS float* scr, int item, int lane) {
;     const int kb = item / nblk, nb = item % nblk, k0 = 64 * kb, n0 = 32 * nb;
;     const int nr = n0 + (lane & 31); const int sc = MAP == 1 ? src_col_in(nr) : (MAP == 2 ? nat_dim(nr) : nr);
;     float v[32];
; #pragma unroll
;     for (int i = 0; i < 32; ++i) { const int k = k0 + 2 * i + (lane >> 5); const int ksrc = KPERM ? ((k & ~127) + nat_dim(k & 127)) : k;
;         v[i] = sc >= 0 ? W[(size_t)ksrc * Nsrc + sc] : 0.f; }
;     const int pr = item >> 1, kb = 2 * (pr / nblk) + (item & 1), nb = pr % nblk, k0 = 64 * kb, n0 = 32 * nb;
;     const int nr = n0 + (lane & 31); const int sc = MAP == 1 ? src_col_in(nr) : nr;
;     float v[32];
; #pragma unroll
;     for (int i = 0; i < 32; ++i) v[i] = sc >= 0 ? W[(size_t)(k0 + 2 * i + (lane >> 5)) * Nsrc + sc] : 0.f;
; #pragma unroll
;     for (int i = 0; i < 32; ++i) { const int k = k0 + 2 * i + (lane >> 5); float x = v[i] * wscale; if (KS) x *= (k < ksplit ? ksA[k] : ksB[k - ksplit]); scr[(2 * i + (lane >> 5)) * 33 + (lane & 31)] = x; }
;     LDS_WAIT(); asm volatile("" ::: "memory");
;     const int c = lane & 7;
; #pragma unroll
;     for (int j = 0; j < 4; ++j) { const int n = (lane >> 3) + 8 * j; const LAS float* s = scr + (8 * c) * 33 + n;
;         const unsigned long long o = (unsigned long long)pg8::pk4_fp8(s[0 * 33], s[1 * 33], s[2 * 33], s[3 * 33]) | ((unsigned long long)pg8::pk4_fp8(s[4 * 33], s[5 * 33], s[6 * 33], s[7 * 33]) << 32);
;         *(GAS unsigned long long*)(WT + (size_t)(n0 + n) * K + k0 + 8 * c) = o; }
;     LDS_WAIT(); asm volatile("" ::: "memory");
; }
	v_max_f32_e32 v226, v226, v226
	v_max_f32_e32 v227, v227, v227
	v_max_f32_e32 v228, v228, v228
	v_max_f32_e32 v229, v229, v229
	v_max_f32_e32 v230, v230, v230
	v_max_f32_e32 v231, v231, v231
	v_max_f32_e32 v232, v232, v232
	v_max_f32_e32 v233, v233, v233
	v_max_f32_e32 v234, v234, v234
	v_max_f32_e32 v235, v235, v235
	v_max_f32_e32 v236, v236, v236
	v_max_f32_e32 v237, v237, v237
	v_max_f32_e32 v238, v238, v238
	v_max_f32_e32 v239, v239, v239
	v_max_f32_e32 v240, v240, v240
	v_max_f32_e32 v241, v241, v241
	v_med3_f32 v226, v226, s62, v95
	v_med3_f32 v227, v227, s62, v95
	v_med3_f32 v228, v228, s62, v95
	v_med3_f32 v229, v229, s62, v95
	v_med3_f32 v230, v230, s62, v95
	v_med3_f32 v231, v231, s62, v95
	v_med3_f32 v232, v232, s62, v95
	v_med3_f32 v233, v233, s62, v95
	v_med3_f32 v234, v234, s62, v95
	v_med3_f32 v235, v235, s62, v95
	v_med3_f32 v236, v236, s62, v95
	v_med3_f32 v237, v237, s62, v95
	v_med3_f32 v238, v238, s62, v95
	v_med3_f32 v239, v239, s62, v95
	v_med3_f32 v240, v240, s62, v95
	v_med3_f32 v241, v241, s62, v95
	v_mov_b32_e32 v242, 0
	v_mov_b32_e32 v243, 0
	v_mov_b32_e32 v244, 0
	v_mov_b32_e32 v245, 0
	v_cvt_pk_fp8_f32 v242, v226, v227
	v_cvt_pk_fp8_f32 v243, v230, v231
	v_cvt_pk_fp8_f32 v244, v234, v235
	v_cvt_pk_fp8_f32 v245, v238, v239
	v_cvt_pk_fp8_f32 v242, v228, v229 op_sel:[0,0,1]
	v_cvt_pk_fp8_f32 v243, v232, v233 op_sel:[0,0,1]
	v_cvt_pk_fp8_f32 v244, v236, v237 op_sel:[0,0,1]
	v_cvt_pk_fp8_f32 v245, v240, v241 op_sel:[0,0,1]
	s_nop 0
	global_store_dwordx4 v80, v[242:245], s[6:7]
	s_waitcnt vmcnt(12)
	v_mul_f32_e32 v144, 0x43000000, v144
	v_mul_f32_e32 v145, 0x43000000, v145
	v_mul_f32_e32 v146, 0x43000000, v146
	v_mul_f32_e32 v147, 0x43000000, v147
	ds_write_b128 v209, v[144:147]
	v_mul_f32_e32 v148, 0x43000000, v148
	v_mul_f32_e32 v149, 0x43000000, v149
	v_mul_f32_e32 v150, 0x43000000, v150
	v_mul_f32_e32 v151, 0x43000000, v151
	ds_write_b128 v209, v[148:151] offset:1024
	v_mul_f32_e32 v152, 0x43000000, v152
	v_mul_f32_e32 v153, 0x43000000, v153
	v_mul_f32_e32 v154, 0x43000000, v154
	v_mul_f32_e32 v155, 0x43000000, v155
	ds_write_b128 v209, v[152:155] offset:2048
	v_mul_f32_e32 v156, 0x43000000, v156
	v_mul_f32_e32 v157, 0x43000000, v157
	v_mul_f32_e32 v158, 0x43000000, v158
	v_mul_f32_e32 v159, 0x43000000, v159
	ds_write_b128 v209, v[156:159] offset:3072
	v_mul_f32_e32 v160, 0x43000000, v160
	v_mul_f32_e32 v161, 0x43000000, v161
	v_mul_f32_e32 v162, 0x43000000, v162
	v_mul_f32_e32 v163, 0x43000000, v163
	ds_write_b128 v209, v[160:163] offset:4096
	v_mul_f32_e32 v164, 0x43000000, v164
	v_mul_f32_e32 v165, 0x43000000, v165
	v_mul_f32_e32 v166, 0x43000000, v166
	v_mul_f32_e32 v167, 0x43000000, v167
	ds_write_b128 v209, v[164:167] offset:5120
	v_mul_f32_e32 v168, 0x43000000, v168
	v_mul_f32_e32 v169, 0x43000000, v169
	v_mul_f32_e32 v170, 0x43000000, v170
	v_mul_f32_e32 v171, 0x43000000, v171
	ds_write_b128 v209, v[168:171] offset:6144
	v_mul_f32_e32 v172, 0x43000000, v172
	v_mul_f32_e32 v173, 0x43000000, v173
	v_mul_f32_e32 v174, 0x43000000, v174
	v_mul_f32_e32 v175, 0x43000000, v175
	ds_write_b128 v209, v[172:175] offset:7168
	s_waitcnt lgkmcnt(0)
	s_barrier
	s_add_i32 s24, s23, 0
	s_lshl_b32 s20, s24, 7
	s_cmp_lt_u32 s24, 40
	s_cselect_b32 s21, 0, 0x830
	s_cmp_lt_u32 s24, 72
	s_cselect_b32 s21, s21, 0xfffff030
	s_add_i32 s20, s20, s21
	s_lshl_b32 s20, s20, 2
	s_add_u32 s8, s46, s20
	s_addc_u32 s9, s47, 0
	global_load_dwordx4 v[144:147], v76, s[8:9]
	s_add_u32 s8, s8, 0x16280
	s_addc_u32 s9, s9, 0
	global_load_dwordx4 v[148:151], v76, s[8:9]
	s_add_u32 s8, s8, 0x16280
	s_addc_u32 s9, s9, 0
	global_load_dwordx4 v[152:155], v76, s[8:9]
	s_add_u32 s8, s8, 0x16280
	s_addc_u32 s9, s9, 0
	global_load_dwordx4 v[156:159], v76, s[8:9]
	s_add_u32 s8, s8, 0x16280
	s_addc_u32 s9, s9, 0
	global_load_dwordx4 v[160:163], v76, s[8:9]
	s_add_u32 s8, s8, 0x16280
	s_addc_u32 s9, s9, 0
	global_load_dwordx4 v[164:167], v76, s[8:9]
	s_add_u32 s8, s8, 0x16280
	s_addc_u32 s9, s9, 0
	global_load_dwordx4 v[168:171], v76, s[8:9]
	s_add_u32 s8, s8, 0x16280
	s_addc_u32 s9, s9, 0
	global_load_dwordx4 v[172:175], v76, s[8:9]
	s_add_u32 s6, s40, 0x2003000
	s_addc_u32 s7, s41, 0
	ds_read_b32 v226, v211
	ds_read_b32 v227, v211 offset:512
	ds_read_b32 v228, v211 offset:1024
	ds_read_b32 v229, v211 offset:1536
	ds_read_b32 v230, v211 offset:2048
	ds_read_b32 v231, v211 offset:2560
	ds_read_b32 v232, v211 offset:3072
	ds_read_b32 v233, v211 offset:3584
	ds_read_b32 v234, v211 offset:4096
	ds_read_b32 v235, v211 offset:4608
	ds_read_b32 v236, v211 offset:5120
	ds_read_b32 v237, v211 offset:5632
	ds_read_b32 v238, v211 offset:6144
	ds_read_b32 v239, v211 offset:6656
	ds_read_b32 v240, v211 offset:7168
	ds_read_b32 v241, v211 offset:7680
	s_waitcnt lgkmcnt(0)
; #define GAS __attribute__((address_space(1)))
; #define LAS __attribute__((address_space(3)))
; #define LDS_WAIT() asm volatile("s_waitcnt lgkmcnt(0)" ::: "memory")
;     const int pr = item >> 1, kb = 2 * (pr / nblk) + (item & 1), nb = pr % nblk, k0 = 64 * kb, n0 = 32 * nb;
;     const int nr = n0 + (lane & 31); const int sc = MAP == 1 ? src_col_in(nr) : nr;
;     float v[32];
; #pragma unroll
;     for (int i = 0; i < 32; ++i) v[i] = sc >= 0 ? W[(size_t)(k0 + 2 * i + (lane >> 5)) * Nsrc + sc] : 0.f;
; #pragma unroll
;     for (int i = 0; i < 32; ++i) { const int k = k0 + 2 * i + (lane >> 5); float x = v[i] * wscale; if (KS) x *= (k < ksplit ? ksA[k] : ksB[k - ksplit]); scr[(2 * i + (lane >> 5)) * 33 + (lane & 31)] = x; }
;     LDS_WAIT(); asm volatile("" ::: "memory");
;     const int c = lane & 7;
; #pragma unroll
;     for (int j = 0; j < 4; ++j) { const int n = (lane >> 3) + 8 * j; const LAS float* s = scr + (8 * c) * 33 + n;
;         const unsigned long long o = (unsigned long long)pg8::pk4_fp8(s[0 * 33], s[1 * 33], s[2 * 33], s[3 * 33]) | ((unsigned long long)pg8::pk4_fp8(s[4 * 33], s[5 * 33], s[6 * 33], s[7 * 33]) << 32);
;         *(GAS unsigned long long*)(WT + (size_t)(n0 + n) * K + k0 + 8 * c) = o; }
;     LDS_WAIT(); asm volatile("" ::: "memory");
; }
	v_max_f32_e32 v226, v226, v226
	v_max_f32_e32 v227, v227, v227
	v_max_f32_e32 v228, v228, v228
	v_max_f32_e32 v229, v229, v229
	v_max_f32_e32 v230, v230, v230
	v_max_f32_e32 v231, v231, v231
	v_max_f32_e32 v232, v232, v232
	v_max_f32_e32 v233, v233, v233
	v_max_f32_e32 v234, v234, v234
	v_max_f32_e32 v235, v235, v235
	v_max_f32_e32 v236, v236, v236
	v_max_f32_e32 v237, v237, v237
	v_max_f32_e32 v238, v238, v238
	v_max_f32_e32 v239, v239, v239
	v_max_f32_e32 v240, v240, v240
	v_max_f32_e32 v241, v241, v241
	v_med3_f32 v226, v226, s62, v95
	v_med3_f32 v227, v227, s62, v95
	v_med3_f32 v228, v228, s62, v95
	v_med3_f32 v229, v229, s62, v95
	v_med3_f32 v230, v230, s62, v95
	v_med3_f32 v231, v231, s62, v95
	v_med3_f32 v232, v232, s62, v95
	v_med3_f32 v233, v233, s62, v95
	v_med3_f32 v234, v234, s62, v95
	v_med3_f32 v235, v235, s62, v95
	v_med3_f32 v236, v236, s62, v95
	v_med3_f32 v237, v237, s62, v95
	v_med3_f32 v238, v238, s62, v95
	v_med3_f32 v239, v239, s62, v95
	v_med3_f32 v240, v240, s62, v95
	v_med3_f32 v241, v241, s62, v95
	v_mov_b32_e32 v242, 0
	v_mov_b32_e32 v243, 0
	v_mov_b32_e32 v244, 0
	v_mov_b32_e32 v245, 0
	v_cvt_pk_fp8_f32 v242, v226, v227
	v_cvt_pk_fp8_f32 v243, v230, v231
	v_cvt_pk_fp8_f32 v244, v234, v235
	v_cvt_pk_fp8_f32 v245, v238, v239
	v_cvt_pk_fp8_f32 v242, v228, v229 op_sel:[0,0,1]
	v_cvt_pk_fp8_f32 v243, v232, v233 op_sel:[0,0,1]
	v_cvt_pk_fp8_f32 v244, v236, v237 op_sel:[0,0,1]
	v_cvt_pk_fp8_f32 v245, v240, v241 op_sel:[0,0,1]
	s_nop 0
	global_store_dwordx4 v79, v[242:245], s[6:7]
	ds_read_b32 v226, v213
	ds_read_b32 v227, v213 offset:512
	ds_read_b32 v228, v213 offset:1024
	ds_read_b32 v229, v213 offset:1536
	ds_read_b32 v230, v213 offset:2048
	ds_read_b32 v231, v213 offset:2560
	ds_read_b32 v232, v213 offset:3072
	ds_read_b32 v233, v213 offset:3584
	ds_read_b32 v234, v213 offset:4096
	ds_read_b32 v235, v213 offset:4608
	ds_read_b32 v236, v213 offset:5120
	ds_read_b32 v237, v213 offset:5632
	ds_read_b32 v238, v213 offset:6144
	ds_read_b32 v239, v213 offset:6656
	ds_read_b32 v240, v213 offset:7168
	ds_read_b32 v241, v213 offset:7680
	s_waitcnt lgkmcnt(0)
	v_max_f32_e32 v226, v226, v226
	v_max_f32_e32 v227, v227, v227
	v_max_f32_e32 v228, v228, v228
	v_max_f32_e32 v229, v229, v229
	v_max_f32_e32 v230, v230, v230
	v_max_f32_e32 v231, v231, v231
	v_max_f32_e32 v232, v232, v232
	v_max_f32_e32 v233, v233, v233
	v_max_f32_e32 v234, v234, v234
	v_max_f32_e32 v235, v235, v235
	v_max_f32_e32 v236, v236, v236
	v_max_f32_e32 v237, v237, v237
	v_max_f32_e32 v238, v238, v238
	v_max_f32_e32 v239, v239, v239
	v_max_f32_e32 v240, v240, v240
	v_max_f32_e32 v241, v241, v241
	v_med3_f32 v226, v226, s62, v95
	v_med3_f32 v227, v227, s62, v95
	v_med3_f32 v228, v228, s62, v95
	v_med3_f32 v229, v229, s62, v95
	v_med3_f32 v230, v230, s62, v95
	v_med3_f32 v231, v231, s62, v95
	v_med3_f32 v232, v232, s62, v95
	v_med3_f32 v233, v233, s62, v95
	v_med3_f32 v234, v234, s62, v95
	v_med3_f32 v235, v235, s62, v95
	v_med3_f32 v236, v236, s62, v95
	v_med3_f32 v237, v237, s62, v95
	v_med3_f32 v238, v238, s62, v95
	v_med3_f32 v239, v239, s62, v95
	v_med3_f32 v240, v240, s62, v95
	v_med3_f32 v241, v241, s62, v95
	v_mov_b32_e32 v242, 0
	v_mov_b32_e32 v243, 0
	v_mov_b32_e32 v244, 0
	v_mov_b32_e32 v245, 0
	v_cvt_pk_fp8_f32 v242, v226, v227
	v_cvt_pk_fp8_f32 v243, v230, v231
	v_cvt_pk_fp8_f32 v244, v234, v235
	v_cvt_pk_fp8_f32 v245, v238, v239
	v_cvt_pk_fp8_f32 v242, v228, v229 op_sel:[0,0,1]
	v_cvt_pk_fp8_f32 v243, v232, v233 op_sel:[0,0,1]
	v_cvt_pk_fp8_f32 v244, v236, v237 op_sel:[0,0,1]
	v_cvt_pk_fp8_f32 v245, v240, v241 op_sel:[0,0,1]
	s_nop 0
	global_store_dwordx4 v80, v[242:245], s[6:7]
	s_waitcnt vmcnt(12)
	v_mul_f32_e32 v176, 0x43000000, v176
	v_mul_f32_e32 v177, 0x43000000, v177
	v_mul_f32_e32 v178, 0x43000000, v178
	v_mul_f32_e32 v179, 0x43000000, v179
	ds_write_b128 v210, v[176:179]
	v_mul_f32_e32 v180, 0x43000000, v180
	v_mul_f32_e32 v181, 0x43000000, v181
	v_mul_f32_e32 v182, 0x43000000, v182
	v_mul_f32_e32 v183, 0x43000000, v183
	ds_write_b128 v210, v[180:183] offset:1024
	v_mul_f32_e32 v184, 0x43000000, v184
	v_mul_f32_e32 v185, 0x43000000, v185
	v_mul_f32_e32 v186, 0x43000000, v186
	v_mul_f32_e32 v187, 0x43000000, v187
	ds_write_b128 v210, v[184:187] offset:2048
	v_mul_f32_e32 v188, 0x43000000, v188
	v_mul_f32_e32 v189, 0x43000000, v189
	v_mul_f32_e32 v190, 0x43000000, v190
	v_mul_f32_e32 v191, 0x43000000, v191
	ds_write_b128 v210, v[188:191] offset:3072
	v_mul_f32_e32 v192, 0x43000000, v192
	v_mul_f32_e32 v193, 0x43000000, v193
	v_mul_f32_e32 v194, 0x43000000, v194
	v_mul_f32_e32 v195, 0x43000000, v195
	ds_write_b128 v210, v[192:195] offset:4096
	v_mul_f32_e32 v196, 0x43000000, v196
	v_mul_f32_e32 v197, 0x43000000, v197
	v_mul_f32_e32 v198, 0x43000000, v198
	v_mul_f32_e32 v199, 0x43000000, v199
	ds_write_b128 v210, v[196:199] offset:5120
	v_mul_f32_e32 v200, 0x43000000, v200
	v_mul_f32_e32 v201, 0x43000000, v201
	v_mul_f32_e32 v202, 0x43000000, v202
	v_mul_f32_e32 v203, 0x43000000, v203
	ds_write_b128 v210, v[200:203] offset:6144
	v_mul_f32_e32 v204, 0x43000000, v204
	v_mul_f32_e32 v205, 0x43000000, v205
	v_mul_f32_e32 v206, 0x43000000, v206
	v_mul_f32_e32 v207, 0x43000000, v207
	ds_write_b128 v210, v[204:207] offset:7168
	s_waitcnt lgkmcnt(0)
	s_barrier
; #define LAS __attribute__((address_space(3)))
; __device__ __forceinline__ int nat_dim(int p) { return (p >> 1) + 64 * (p & 1); }
; __device__ __forceinline__ int src_col_in(int c) {
;     if (c < 5120) { const int blk = c >> 7, p = c & 127; const bool rope = blk < 16 || ((((blk - 16) >> 2) & 1) == 0); const int d = rope ? (p >> 1) + 64 * (p & 1) : p; return blk * 128 + d; }
;     if (c < OFF_Z) return c + 2096;
;     if (c < OFF_G) return c - 4048;
;     if (c < OFF_DT) return 5120 + (c - OFF_G);
;     if (c < NSRC) return c;
;     return -1;
; }
; template <int MAP, bool KS, bool KPERM = false>
; __device__ __forceinline__ void p0_transpose_item(const float* W, int K, int Nsrc, int nblk, bf16* WT, const float* ksA, const float* ksB, int ksplit, LAS float* scr, int item, int lane) {
;     const int kb = item / nblk, nb = item % nblk, k0 = 64 * kb, n0 = 32 * nb;
;     const int nr = n0 + (lane & 31); const int sc = MAP == 1 ? src_col_in(nr) : (MAP == 2 ? nat_dim(nr) : nr);
;     float v[32];
; #pragma unroll
;     for (int i = 0; i < 32; ++i) { const int k = k0 + 2 * i + (lane >> 5); const int ksrc = KPERM ? ((k & ~127) + nat_dim(k & 127)) : k;
;         v[i] = sc >= 0 ? W[(size_t)ksrc * Nsrc + sc] : 0.f; }
; #pragma unroll
;     for (int i = 0; i < 32; ++i) { const int kk = 2 * i + (lane >> 5); const int k = k0 + kk;
;         if (KS) v[i] *= (k < ksplit ? ksA[k] : ksB[k - ksplit]);
;         scr[kk * 33 + (lane & 31)] = v[i]; }
	s_add_i32 s24, s23, 8
	s_lshl_b32 s20, s24, 7
	s_cmp_lt_u32 s24, 40
	s_cselect_b32 s21, 0, 0x830
	s_cmp_lt_u32 s24, 72
	s_cselect_b32 s21, s21, 0xfffff030
	s_add_i32 s20, s20, s21
	s_lshl_b32 s20, s20, 2
	s_add_u32 s8, s46, s20
	s_addc_u32 s9, s47, 0
	global_load_dwordx4 v[176:179], v76, s[8:9]
	s_add_u32 s8, s8, 0x16280
	s_addc_u32 s9, s9, 0
	global_load_dwordx4 v[180:183], v76, s[8:9]
	s_add_u32 s8, s8, 0x16280
	s_addc_u32 s9, s9, 0
	global_load_dwordx4 v[184:187], v76, s[8:9]
	s_add_u32 s8, s8, 0x16280
	s_addc_u32 s9, s9, 0
	global_load_dwordx4 v[188:191], v76, s[8:9]
	s_add_u32 s8, s8, 0x16280
	s_addc_u32 s9, s9, 0
	global_load_dwordx4 v[192:195], v76, s[8:9]
	s_add_u32 s8, s8, 0x16280
	s_addc_u32 s9, s9, 0
	global_load_dwordx4 v[196:199], v76, s[8:9]
	s_add_u32 s8, s8, 0x16280
	s_addc_u32 s9, s9, 0
	global_load_dwordx4 v[200:203], v76, s[8:9]
	s_add_u32 s8, s8, 0x16280
	s_addc_u32 s9, s9, 0
	global_load_dwordx4 v[204:207], v76, s[8:9]
	s_add_u32 s6, s40, 0x3003000
	s_addc_u32 s7, s41, 0
	ds_read_b32 v226, v212
	ds_read_b32 v227, v212 offset:512
	ds_read_b32 v228, v212 offset:1024
	ds_read_b32 v229, v212 offset:1536
	ds_read_b32 v230, v212 offset:2048
	ds_read_b32 v231, v212 offset:2560
	ds_read_b32 v232, v212 offset:3072
	ds_read_b32 v233, v212 offset:3584
	ds_read_b32 v234, v212 offset:4096
	ds_read_b32 v235, v212 offset:4608
	ds_read_b32 v236, v212 offset:5120
	ds_read_b32 v237, v212 offset:5632
	ds_read_b32 v238, v212 offset:6144
	ds_read_b32 v239, v212 offset:6656
	ds_read_b32 v240, v212 offset:7168
	ds_read_b32 v241, v212 offset:7680
	s_waitcnt lgkmcnt(0)
	v_max_f32_e32 v226, v226, v226
	v_max_f32_e32 v227, v227, v227
	v_max_f32_e32 v228, v228, v228
	v_max_f32_e32 v229, v229, v229
	v_max_f32_e32 v230, v230, v230
	v_max_f32_e32 v231, v231, v231
	v_max_f32_e32 v232, v232, v232
	v_max_f32_e32 v233, v233, v233
	v_max_f32_e32 v234, v234, v234
	v_max_f32_e32 v235, v235, v235
	v_max_f32_e32 v236, v236, v236
	v_max_f32_e32 v237, v237, v237
	v_max_f32_e32 v238, v238, v238
	v_max_f32_e32 v239, v239, v239
	v_max_f32_e32 v240, v240, v240
	v_max_f32_e32 v241, v241, v241
	v_med3_f32 v226, v226, s62, v95
	v_med3_f32 v227, v227, s62, v95
	v_med3_f32 v228, v228, s62, v95
	v_med3_f32 v229, v229, s62, v95
	v_med3_f32 v230, v230, s62, v95
	v_med3_f32 v231, v231, s62, v95
	v_med3_f32 v232, v232, s62, v95
	v_med3_f32 v233, v233, s62, v95
	v_med3_f32 v234, v234, s62, v95
	v_med3_f32 v235, v235, s62, v95
	v_med3_f32 v236, v236, s62, v95
	v_med3_f32 v237, v237, s62, v95
	v_med3_f32 v238, v238, s62, v95
	v_med3_f32 v239, v239, s62, v95
	v_med3_f32 v240, v240, s62, v95
	v_med3_f32 v241, v241, s62, v95
	v_mov_b32_e32 v242, 0
	v_mov_b32_e32 v243, 0
	v_mov_b32_e32 v244, 0
	v_mov_b32_e32 v245, 0
	v_cvt_pk_fp8_f32 v242, v226, v227
	v_cvt_pk_fp8_f32 v243, v230, v231
	v_cvt_pk_fp8_f32 v244, v234, v235
	v_cvt_pk_fp8_f32 v245, v238, v239
	v_cvt_pk_fp8_f32 v242, v228, v229 op_sel:[0,0,1]
	v_cvt_pk_fp8_f32 v243, v232, v233 op_sel:[0,0,1]
	v_cvt_pk_fp8_f32 v244, v236, v237 op_sel:[0,0,1]
	v_cvt_pk_fp8_f32 v245, v240, v241 op_sel:[0,0,1]
	s_nop 0
	global_store_dwordx4 v79, v[242:245], s[6:7]
	ds_read_b32 v226, v214
	ds_read_b32 v227, v214 offset:512
	ds_read_b32 v228, v214 offset:1024
	ds_read_b32 v229, v214 offset:1536
	ds_read_b32 v230, v214 offset:2048
	ds_read_b32 v231, v214 offset:2560
	ds_read_b32 v232, v214 offset:3072
	ds_read_b32 v233, v214 offset:3584
	ds_read_b32 v234, v214 offset:4096
	ds_read_b32 v235, v214 offset:4608
	ds_read_b32 v236, v214 offset:5120
	ds_read_b32 v237, v214 offset:5632
	ds_read_b32 v238, v214 offset:6144
	ds_read_b32 v239, v214 offset:6656
	ds_read_b32 v240, v214 offset:7168
	ds_read_b32 v241, v214 offset:7680
	s_waitcnt lgkmcnt(0)
	v_max_f32_e32 v226, v226, v226
	v_max_f32_e32 v227, v227, v227
	v_max_f32_e32 v228, v228, v228
	v_max_f32_e32 v229, v229, v229
	v_max_f32_e32 v230, v230, v230
	v_max_f32_e32 v231, v231, v231
	v_max_f32_e32 v232, v232, v232
	v_max_f32_e32 v233, v233, v233
	v_max_f32_e32 v234, v234, v234
	v_max_f32_e32 v235, v235, v235
	v_max_f32_e32 v236, v236, v236
	v_max_f32_e32 v237, v237, v237
	v_max_f32_e32 v238, v238, v238
	v_max_f32_e32 v239, v239, v239
	v_max_f32_e32 v240, v240, v240
	v_max_f32_e32 v241, v241, v241
	v_med3_f32 v226, v226, s62, v95
	v_med3_f32 v227, v227, s62, v95
	v_med3_f32 v228, v228, s62, v95
	v_med3_f32 v229, v229, s62, v95
	v_med3_f32 v230, v230, s62, v95
	v_med3_f32 v231, v231, s62, v95
	v_med3_f32 v232, v232, s62, v95
	v_med3_f32 v233, v233, s62, v95
	v_med3_f32 v234, v234, s62, v95
	v_med3_f32 v235, v235, s62, v95
	v_med3_f32 v236, v236, s62, v95
	v_med3_f32 v237, v237, s62, v95
	v_med3_f32 v238, v238, s62, v95
	v_med3_f32 v239, v239, s62, v95
	v_med3_f32 v240, v240, s62, v95
	v_med3_f32 v241, v241, s62, v95
	v_mov_b32_e32 v242, 0
	v_mov_b32_e32 v243, 0
	v_mov_b32_e32 v244, 0
	v_mov_b32_e32 v245, 0
	v_cvt_pk_fp8_f32 v242, v226, v227
	v_cvt_pk_fp8_f32 v243, v230, v231
	v_cvt_pk_fp8_f32 v244, v234, v235
	v_cvt_pk_fp8_f32 v245, v238, v239
	v_cvt_pk_fp8_f32 v242, v228, v229 op_sel:[0,0,1]
	v_cvt_pk_fp8_f32 v243, v232, v233 op_sel:[0,0,1]
	v_cvt_pk_fp8_f32 v244, v236, v237 op_sel:[0,0,1]
	v_cvt_pk_fp8_f32 v245, v240, v241 op_sel:[0,0,1]
	s_nop 0
	global_store_dwordx4 v80, v[242:245], s[6:7]
	s_waitcnt vmcnt(12)
	v_mul_f32_e32 v144, v42, v144
	v_mul_f32_e32 v145, v42, v145
	v_mul_f32_e32 v146, v42, v146
	v_mul_f32_e32 v147, v42, v147
	ds_write_b128 v209, v[144:147]
	v_mul_f32_e32 v148, v43, v148
	v_mul_f32_e32 v149, v43, v149
	v_mul_f32_e32 v150, v43, v150
	v_mul_f32_e32 v151, v43, v151
	ds_write_b128 v209, v[148:151] offset:1024
	v_mul_f32_e32 v152, v44, v152
	v_mul_f32_e32 v153, v44, v153
	v_mul_f32_e32 v154, v44, v154
	v_mul_f32_e32 v155, v44, v155
	ds_write_b128 v209, v[152:155] offset:2048
	v_mul_f32_e32 v156, v45, v156
	v_mul_f32_e32 v157, v45, v157
	v_mul_f32_e32 v158, v45, v158
	v_mul_f32_e32 v159, v45, v159
	ds_write_b128 v209, v[156:159] offset:3072
	v_mul_f32_e32 v160, v46, v160
	v_mul_f32_e32 v161, v46, v161
	v_mul_f32_e32 v162, v46, v162
	v_mul_f32_e32 v163, v46, v163
	ds_write_b128 v209, v[160:163] offset:4096
	v_mul_f32_e32 v164, v47, v164
	v_mul_f32_e32 v165, v47, v165
	v_mul_f32_e32 v166, v47, v166
	v_mul_f32_e32 v167, v47, v167
	ds_write_b128 v209, v[164:167] offset:5120
	v_mul_f32_e32 v168, v48, v168
	v_mul_f32_e32 v169, v48, v169
	v_mul_f32_e32 v170, v48, v170
	v_mul_f32_e32 v171, v48, v171
	ds_write_b128 v209, v[168:171] offset:6144
	v_mul_f32_e32 v172, v49, v172
	v_mul_f32_e32 v173, v49, v173
	v_mul_f32_e32 v174, v49, v174
	v_mul_f32_e32 v175, v49, v175
	ds_write_b128 v209, v[172:175] offset:7168
	s_waitcnt lgkmcnt(0)
	s_barrier
; #define GAS __attribute__((address_space(1)))
; #define LAS __attribute__((address_space(3)))
; #define LDS_WAIT() asm volatile("s_waitcnt lgkmcnt(0)" ::: "memory")
; __device__ __forceinline__ unsigned pk2(float lo, float hi) { return f2bf(lo) | (f2bf(hi) << 16); }
; __device__ __forceinline__ int nat_dim(int p) { return (p >> 1) + 64 * (p & 1); }
; __device__ __forceinline__ int src_col_in(int c) {
;     if (c < 5120) { const int blk = c >> 7, p = c & 127; const bool rope = blk < 16 || ((((blk - 16) >> 2) & 1) == 0); const int d = rope ? (p >> 1) + 64 * (p & 1) : p; return blk * 128 + d; }
;     if (c < OFF_Z) return c + 2096;
;     if (c < OFF_G) return c - 4048;
;     if (c < OFF_DT) return 5120 + (c - OFF_G);
;     if (c < NSRC) return c;
;     return -1;
; }
; template <int MAP, bool KS, bool KPERM = false>
; __device__ __forceinline__ void p0_transpose_item(const float* W, int K, int Nsrc, int nblk, bf16* WT, const float* ksA, const float* ksB, int ksplit, LAS float* scr, int item, int lane) {
;     const int kb = item / nblk, nb = item % nblk, k0 = 64 * kb, n0 = 32 * nb;
;     const int nr = n0 + (lane & 31); const int sc = MAP == 1 ? src_col_in(nr) : (MAP == 2 ? nat_dim(nr) : nr);
;     float v[32];
; #pragma unroll
;     for (int i = 0; i < 32; ++i) { const int k = k0 + 2 * i + (lane >> 5); const int ksrc = KPERM ? ((k & ~127) + nat_dim(k & 127)) : k;
;         v[i] = sc >= 0 ? W[(size_t)ksrc * Nsrc + sc] : 0.f; }
; #pragma unroll
;     for (int i = 0; i < 32; ++i) { const int kk = 2 * i + (lane >> 5); const int k = k0 + kk;
;         if (KS) v[i] *= (k < ksplit ? ksA[k] : ksB[k - ksplit]);
;         scr[kk * 33 + (lane & 31)] = v[i]; }
;     LDS_WAIT(); asm volatile("" ::: "memory");
;     const int c = lane & 7;
; #pragma unroll
;     for (int j = 0; j < 4; ++j) { const int n = (lane >> 3) + 8 * j; const LAS float* s = scr + (8 * c) * 33 + n;
;         v4u o; o.x = pk2(s[0 * 33], s[1 * 33]); o.y = pk2(s[2 * 33], s[3 * 33]); o.z = pk2(s[4 * 33], s[5 * 33]); o.w = pk2(s[6 * 33], s[7 * 33]);
;         *(GAS v4u*)(WT + (size_t)(n0 + n) * K + k0 + 8 * c) = o; }
;     LDS_WAIT(); asm volatile("" ::: "memory");
	s_add_i32 s24, s23, 16
	s_lshl_b32 s20, s24, 7
	s_cmp_lt_u32 s24, 40
	s_cselect_b32 s21, 0, 0x830
	s_cmp_lt_u32 s24, 72
	s_cselect_b32 s21, s21, 0xfffff030
	s_add_i32 s20, s20, s21
	s_lshl_b32 s20, s20, 2
	s_add_u32 s8, s46, s20
	s_addc_u32 s9, s47, 0
	global_load_dwordx4 v[144:147], v76, s[8:9]
	s_add_u32 s8, s8, 0x16280
	s_addc_u32 s9, s9, 0
	global_load_dwordx4 v[148:151], v76, s[8:9]
	s_add_u32 s8, s8, 0x16280
	s_addc_u32 s9, s9, 0
	global_load_dwordx4 v[152:155], v76, s[8:9]
	s_add_u32 s8, s8, 0x16280
	s_addc_u32 s9, s9, 0
	global_load_dwordx4 v[156:159], v76, s[8:9]
	s_add_u32 s8, s8, 0x16280
	s_addc_u32 s9, s9, 0
	global_load_dwordx4 v[160:163], v76, s[8:9]
	s_add_u32 s8, s8, 0x16280
	s_addc_u32 s9, s9, 0
	global_load_dwordx4 v[164:167], v76, s[8:9]
	s_add_u32 s8, s8, 0x16280
	s_addc_u32 s9, s9, 0
	global_load_dwordx4 v[168:171], v76, s[8:9]
	s_add_u32 s8, s8, 0x16280
	s_addc_u32 s9, s9, 0
	global_load_dwordx4 v[172:175], v76, s[8:9]
	s_add_i32 s24, s23, 0
	s_mul_i32 s20, s24, 0x100000
	s_add_u32 s6, s48, s20
	s_addc_u32 s7, s49, 0
	s_cmp_lt_u32 s24, 16
	s_cselect_b32 s20, 1, 0
	s_sub_i32 s21, s24, 16
	s_bitcmp0_b32 s21, 2
	s_cselect_b32 s21, 1, 0
	s_cmp_lt_u32 s24, 40
	s_cselect_b32 s21, s21, 0
	s_or_b32 s20, s20, s21
	s_cmp_lg_u32 s20, 0
	s_cselect_b64 s[20:21], -1, 0
	v_cndmask_b32_e64 v91, v83, v87, s[20:21]
	v_cndmask_b32_e64 v92, v84, v88, s[20:21]
	v_cndmask_b32_e64 v93, v85, v89, s[20:21]
	v_cndmask_b32_e64 v94, v86, v90, s[20:21]
	ds_read_b32 v226, v112
	ds_read_b32 v227, v112 offset:512
	ds_read_b32 v228, v112 offset:1024
	ds_read_b32 v229, v112 offset:1536
	ds_read_b32 v230, v112 offset:2048
	ds_read_b32 v231, v112 offset:2560
	ds_read_b32 v232, v112 offset:3072
	ds_read_b32 v233, v112 offset:3584
	s_waitcnt lgkmcnt(0)
	v_bfe_u32 v120, v226, 16, 1
	v_bfe_u32 v121, v227, 16, 1
	v_bfe_u32 v122, v228, 16, 1
	v_bfe_u32 v123, v229, 16, 1
	v_bfe_u32 v124, v230, 16, 1
	v_bfe_u32 v125, v231, 16, 1
	v_bfe_u32 v126, v232, 16, 1
	v_bfe_u32 v127, v233, 16, 1
	v_add3_u32 v226, v226, v120, s63
	v_add3_u32 v227, v227, v121, s63
	v_add3_u32 v228, v228, v122, s63
	v_add3_u32 v229, v229, v123, s63
	v_add3_u32 v230, v230, v124, s63
	v_add3_u32 v231, v231, v125, s63
	v_add3_u32 v232, v232, v126, s63
	v_add3_u32 v233, v233, v127, s63
	v_perm_b32 v242, v227, v226, s64
	v_perm_b32 v243, v229, v228, s64
	v_perm_b32 v244, v231, v230, s64
	v_perm_b32 v245, v233, v232, s64
	s_nop 0
	global_store_dwordx4 v91, v[242:245], s[6:7]
	ds_read_b32 v226, v114
	ds_read_b32 v227, v114 offset:512
	ds_read_b32 v228, v114 offset:1024
	ds_read_b32 v229, v114 offset:1536
	ds_read_b32 v230, v114 offset:2048
	ds_read_b32 v231, v114 offset:2560
	ds_read_b32 v232, v114 offset:3072
	ds_read_b32 v233, v114 offset:3584
	s_waitcnt lgkmcnt(0)
	v_bfe_u32 v120, v226, 16, 1
	v_bfe_u32 v121, v227, 16, 1
	v_bfe_u32 v122, v228, 16, 1
	v_bfe_u32 v123, v229, 16, 1
	v_bfe_u32 v124, v230, 16, 1
	v_bfe_u32 v125, v231, 16, 1
	v_bfe_u32 v126, v232, 16, 1
	v_bfe_u32 v127, v233, 16, 1
	v_add3_u32 v226, v226, v120, s63
	v_add3_u32 v227, v227, v121, s63
	v_add3_u32 v228, v228, v122, s63
	v_add3_u32 v229, v229, v123, s63
	v_add3_u32 v230, v230, v124, s63
	v_add3_u32 v231, v231, v125, s63
	v_add3_u32 v232, v232, v126, s63
	v_add3_u32 v233, v233, v127, s63
	v_perm_b32 v242, v227, v226, s64
	v_perm_b32 v243, v229, v228, s64
	v_perm_b32 v244, v231, v230, s64
	v_perm_b32 v245, v233, v232, s64
	s_nop 0
	global_store_dwordx4 v92, v[242:245], s[6:7]
	ds_read_b32 v226, v116
	ds_read_b32 v227, v116 offset:512
	ds_read_b32 v228, v116 offset:1024
	ds_read_b32 v229, v116 offset:1536
	ds_read_b32 v230, v116 offset:2048
	ds_read_b32 v231, v116 offset:2560
	ds_read_b32 v232, v116 offset:3072
	ds_read_b32 v233, v116 offset:3584
	s_waitcnt lgkmcnt(0)
	v_bfe_u32 v120, v226, 16, 1
	v_bfe_u32 v121, v227, 16, 1
	v_bfe_u32 v122, v228, 16, 1
	v_bfe_u32 v123, v229, 16, 1
	v_bfe_u32 v124, v230, 16, 1
	v_bfe_u32 v125, v231, 16, 1
	v_bfe_u32 v126, v232, 16, 1
	v_bfe_u32 v127, v233, 16, 1
	v_add3_u32 v226, v226, v120, s63
	v_add3_u32 v227, v227, v121, s63
	v_add3_u32 v228, v228, v122, s63
	v_add3_u32 v229, v229, v123, s63
	v_add3_u32 v230, v230, v124, s63
	v_add3_u32 v231, v231, v125, s63
	v_add3_u32 v232, v232, v126, s63
	v_add3_u32 v233, v233, v127, s63
	v_perm_b32 v242, v227, v226, s64
	v_perm_b32 v243, v229, v228, s64
	v_perm_b32 v244, v231, v230, s64
	v_perm_b32 v245, v233, v232, s64
	s_nop 0
	global_store_dwordx4 v93, v[242:245], s[6:7]
	ds_read_b32 v226, v118
	ds_read_b32 v227, v118 offset:512
	ds_read_b32 v228, v118 offset:1024
	ds_read_b32 v229, v118 offset:1536
	ds_read_b32 v230, v118 offset:2048
	ds_read_b32 v231, v118 offset:2560
	ds_read_b32 v232, v118 offset:3072
	ds_read_b32 v233, v118 offset:3584
	s_waitcnt lgkmcnt(0)
	v_bfe_u32 v120, v226, 16, 1
	v_bfe_u32 v121, v227, 16, 1
	v_bfe_u32 v122, v228, 16, 1
	v_bfe_u32 v123, v229, 16, 1
	v_bfe_u32 v124, v230, 16, 1
	v_bfe_u32 v125, v231, 16, 1
	v_bfe_u32 v126, v232, 16, 1
	v_bfe_u32 v127, v233, 16, 1
	v_add3_u32 v226, v226, v120, s63
	v_add3_u32 v227, v227, v121, s63
	v_add3_u32 v228, v228, v122, s63
	v_add3_u32 v229, v229, v123, s63
	v_add3_u32 v230, v230, v124, s63
	v_add3_u32 v231, v231, v125, s63
	v_add3_u32 v232, v232, v126, s63
	v_add3_u32 v233, v233, v127, s63
	v_perm_b32 v242, v227, v226, s64
	v_perm_b32 v243, v229, v228, s64
	v_perm_b32 v244, v231, v230, s64
	v_perm_b32 v245, v233, v232, s64
	s_nop 0
	global_store_dwordx4 v94, v[242:245], s[6:7]
	s_waitcnt vmcnt(14)
	v_mul_f32_e32 v176, v42, v176
	v_mul_f32_e32 v177, v42, v177
	v_mul_f32_e32 v178, v42, v178
	v_mul_f32_e32 v179, v42, v179
	ds_write_b128 v210, v[176:179]
	v_mul_f32_e32 v180, v43, v180
	v_mul_f32_e32 v181, v43, v181
	v_mul_f32_e32 v182, v43, v182
	v_mul_f32_e32 v183, v43, v183
	ds_write_b128 v210, v[180:183] offset:1024
	v_mul_f32_e32 v184, v44, v184
	v_mul_f32_e32 v185, v44, v185
	v_mul_f32_e32 v186, v44, v186
	v_mul_f32_e32 v187, v44, v187
	ds_write_b128 v210, v[184:187] offset:2048
	v_mul_f32_e32 v188, v45, v188
	v_mul_f32_e32 v189, v45, v189
	v_mul_f32_e32 v190, v45, v190
	v_mul_f32_e32 v191, v45, v191
	ds_write_b128 v210, v[188:191] offset:3072
	v_mul_f32_e32 v192, v46, v192
	v_mul_f32_e32 v193, v46, v193
	v_mul_f32_e32 v194, v46, v194
	v_mul_f32_e32 v195, v46, v195
	ds_write_b128 v210, v[192:195] offset:4096
	v_mul_f32_e32 v196, v47, v196
	v_mul_f32_e32 v197, v47, v197
	v_mul_f32_e32 v198, v47, v198
	v_mul_f32_e32 v199, v47, v199
	ds_write_b128 v210, v[196:199] offset:5120
	v_mul_f32_e32 v200, v48, v200
	v_mul_f32_e32 v201, v48, v201
	v_mul_f32_e32 v202, v48, v202
	v_mul_f32_e32 v203, v48, v203
	ds_write_b128 v210, v[200:203] offset:6144
	v_mul_f32_e32 v204, v49, v204
	v_mul_f32_e32 v205, v49, v205
	v_mul_f32_e32 v206, v49, v206
	v_mul_f32_e32 v207, v49, v207
	ds_write_b128 v210, v[204:207] offset:7168
	s_waitcnt lgkmcnt(0)
	s_barrier
; #define GAS __attribute__((address_space(1)))
; #define LAS __attribute__((address_space(3)))
; #define LDS_WAIT() asm volatile("s_waitcnt lgkmcnt(0)" ::: "memory")
; __device__ __forceinline__ unsigned pk2(float lo, float hi) { return f2bf(lo) | (f2bf(hi) << 16); }
; __device__ __forceinline__ int nat_dim(int p) { return (p >> 1) + 64 * (p & 1); }
; __device__ __forceinline__ int src_col_in(int c) {
;     if (c < 5120) { const int blk = c >> 7, p = c & 127; const bool rope = blk < 16 || ((((blk - 16) >> 2) & 1) == 0); const int d = rope ? (p >> 1) + 64 * (p & 1) : p; return blk * 128 + d; }
;     if (c < OFF_Z) return c + 2096;
;     if (c < OFF_G) return c - 4048;
;     if (c < OFF_DT) return 5120 + (c - OFF_G);
;     if (c < NSRC) return c;
;     return -1;
; }
; template <int MAP, bool KS, bool KPERM = false>
; __device__ __forceinline__ void p0_transpose_item(const float* W, int K, int Nsrc, int nblk, bf16* WT, const float* ksA, const float* ksB, int ksplit, LAS float* scr, int item, int lane) {
;     const int kb = item / nblk, nb = item % nblk, k0 = 64 * kb, n0 = 32 * nb;
;     const int nr = n0 + (lane & 31); const int sc = MAP == 1 ? src_col_in(nr) : (MAP == 2 ? nat_dim(nr) : nr);
;     float v[32];
; #pragma unroll
;     for (int i = 0; i < 32; ++i) { const int k = k0 + 2 * i + (lane >> 5); const int ksrc = KPERM ? ((k & ~127) + nat_dim(k & 127)) : k;
;         v[i] = sc >= 0 ? W[(size_t)ksrc * Nsrc + sc] : 0.f; }
; #pragma unroll
;     for (int i = 0; i < 32; ++i) { const int kk = 2 * i + (lane >> 5); const int k = k0 + kk;
;         if (KS) v[i] *= (k < ksplit ? ksA[k] : ksB[k - ksplit]);
;         scr[kk * 33 + (lane & 31)] = v[i]; }
;     LDS_WAIT(); asm volatile("" ::: "memory");
;     const int c = lane & 7;
; #pragma unroll
;     for (int j = 0; j < 4; ++j) { const int n = (lane >> 3) + 8 * j; const LAS float* s = scr + (8 * c) * 33 + n;
;         v4u o; o.x = pk2(s[0 * 33], s[1 * 33]); o.y = pk2(s[2 * 33], s[3 * 33]); o.z = pk2(s[4 * 33], s[5 * 33]); o.w = pk2(s[6 * 33], s[7 * 33]);
;         *(GAS v4u*)(WT + (size_t)(n0 + n) * K + k0 + 8 * c) = o; }
;     LDS_WAIT(); asm volatile("" ::: "memory");
	s_add_i32 s24, s23, 24
	s_lshl_b32 s20, s24, 7
	s_cmp_lt_u32 s24, 40
	s_cselect_b32 s21, 0, 0x830
	s_cmp_lt_u32 s24, 72
	s_cselect_b32 s21, s21, 0xfffff030
	s_add_i32 s20, s20, s21
	s_lshl_b32 s20, s20, 2
	s_add_u32 s8, s46, s20
	s_addc_u32 s9, s47, 0
	global_load_dwordx4 v[176:179], v76, s[8:9]
	s_add_u32 s8, s8, 0x16280
	s_addc_u32 s9, s9, 0
	global_load_dwordx4 v[180:183], v76, s[8:9]
	s_add_u32 s8, s8, 0x16280
	s_addc_u32 s9, s9, 0
	global_load_dwordx4 v[184:187], v76, s[8:9]
	s_add_u32 s8, s8, 0x16280
	s_addc_u32 s9, s9, 0
	global_load_dwordx4 v[188:191], v76, s[8:9]
	s_add_u32 s8, s8, 0x16280
	s_addc_u32 s9, s9, 0
	global_load_dwordx4 v[192:195], v76, s[8:9]
	s_add_u32 s8, s8, 0x16280
	s_addc_u32 s9, s9, 0
	global_load_dwordx4 v[196:199], v76, s[8:9]
	s_add_u32 s8, s8, 0x16280
	s_addc_u32 s9, s9, 0
	global_load_dwordx4 v[200:203], v76, s[8:9]
	s_add_u32 s8, s8, 0x16280
	s_addc_u32 s9, s9, 0
	global_load_dwordx4 v[204:207], v76, s[8:9]
	s_add_i32 s24, s23, 8
	s_mul_i32 s20, s24, 0x100000
	s_add_u32 s6, s48, s20
	s_addc_u32 s7, s49, 0
	s_cmp_lt_u32 s24, 16
	s_cselect_b32 s20, 1, 0
	s_sub_i32 s21, s24, 16
	s_bitcmp0_b32 s21, 2
	s_cselect_b32 s21, 1, 0
	s_cmp_lt_u32 s24, 40
	s_cselect_b32 s21, s21, 0
	s_or_b32 s20, s20, s21
	s_cmp_lg_u32 s20, 0
	s_cselect_b64 s[20:21], -1, 0
	v_cndmask_b32_e64 v91, v83, v87, s[20:21]
	v_cndmask_b32_e64 v92, v84, v88, s[20:21]
	v_cndmask_b32_e64 v93, v85, v89, s[20:21]
	v_cndmask_b32_e64 v94, v86, v90, s[20:21]
	ds_read_b32 v226, v113
	ds_read_b32 v227, v113 offset:512
	ds_read_b32 v228, v113 offset:1024
	ds_read_b32 v229, v113 offset:1536
	ds_read_b32 v230, v113 offset:2048
	ds_read_b32 v231, v113 offset:2560
	ds_read_b32 v232, v113 offset:3072
	ds_read_b32 v233, v113 offset:3584
	s_waitcnt lgkmcnt(0)
	v_bfe_u32 v120, v226, 16, 1
	v_bfe_u32 v121, v227, 16, 1
	v_bfe_u32 v122, v228, 16, 1
	v_bfe_u32 v123, v229, 16, 1
	v_bfe_u32 v124, v230, 16, 1
	v_bfe_u32 v125, v231, 16, 1
	v_bfe_u32 v126, v232, 16, 1
	v_bfe_u32 v127, v233, 16, 1
	v_add3_u32 v226, v226, v120, s63
	v_add3_u32 v227, v227, v121, s63
	v_add3_u32 v228, v228, v122, s63
	v_add3_u32 v229, v229, v123, s63
	v_add3_u32 v230, v230, v124, s63
	v_add3_u32 v231, v231, v125, s63
	v_add3_u32 v232, v232, v126, s63
	v_add3_u32 v233, v233, v127, s63
	v_perm_b32 v242, v227, v226, s64
	v_perm_b32 v243, v229, v228, s64
	v_perm_b32 v244, v231, v230, s64
	v_perm_b32 v245, v233, v232, s64
	s_nop 0
	global_store_dwordx4 v91, v[242:245], s[6:7]
	ds_read_b32 v226, v115
	ds_read_b32 v227, v115 offset:512
	ds_read_b32 v228, v115 offset:1024
	ds_read_b32 v229, v115 offset:1536
	ds_read_b32 v230, v115 offset:2048
	ds_read_b32 v231, v115 offset:2560
	ds_read_b32 v232, v115 offset:3072
	ds_read_b32 v233, v115 offset:3584
	s_waitcnt lgkmcnt(0)
	v_bfe_u32 v120, v226, 16, 1
	v_bfe_u32 v121, v227, 16, 1
	v_bfe_u32 v122, v228, 16, 1
	v_bfe_u32 v123, v229, 16, 1
	v_bfe_u32 v124, v230, 16, 1
	v_bfe_u32 v125, v231, 16, 1
	v_bfe_u32 v126, v232, 16, 1
	v_bfe_u32 v127, v233, 16, 1
	v_add3_u32 v226, v226, v120, s63
	v_add3_u32 v227, v227, v121, s63
	v_add3_u32 v228, v228, v122, s63
	v_add3_u32 v229, v229, v123, s63
	v_add3_u32 v230, v230, v124, s63
	v_add3_u32 v231, v231, v125, s63
	v_add3_u32 v232, v232, v126, s63
	v_add3_u32 v233, v233, v127, s63
	v_perm_b32 v242, v227, v226, s64
	v_perm_b32 v243, v229, v228, s64
	v_perm_b32 v244, v231, v230, s64
	v_perm_b32 v245, v233, v232, s64
	s_nop 0
	global_store_dwordx4 v92, v[242:245], s[6:7]
	ds_read_b32 v226, v117
	ds_read_b32 v227, v117 offset:512
	ds_read_b32 v228, v117 offset:1024
	ds_read_b32 v229, v117 offset:1536
	ds_read_b32 v230, v117 offset:2048
	ds_read_b32 v231, v117 offset:2560
	ds_read_b32 v232, v117 offset:3072
	ds_read_b32 v233, v117 offset:3584
	s_waitcnt lgkmcnt(0)
	v_bfe_u32 v120, v226, 16, 1
	v_bfe_u32 v121, v227, 16, 1
	v_bfe_u32 v122, v228, 16, 1
	v_bfe_u32 v123, v229, 16, 1
	v_bfe_u32 v124, v230, 16, 1
	v_bfe_u32 v125, v231, 16, 1
	v_bfe_u32 v126, v232, 16, 1
	v_bfe_u32 v127, v233, 16, 1
	v_add3_u32 v226, v226, v120, s63
	v_add3_u32 v227, v227, v121, s63
	v_add3_u32 v228, v228, v122, s63
	v_add3_u32 v229, v229, v123, s63
	v_add3_u32 v230, v230, v124, s63
	v_add3_u32 v231, v231, v125, s63
	v_add3_u32 v232, v232, v126, s63
	v_add3_u32 v233, v233, v127, s63
	v_perm_b32 v242, v227, v226, s64
	v_perm_b32 v243, v229, v228, s64
	v_perm_b32 v244, v231, v230, s64
	v_perm_b32 v245, v233, v232, s64
	s_nop 0
	global_store_dwordx4 v93, v[242:245], s[6:7]
	ds_read_b32 v226, v119
	ds_read_b32 v227, v119 offset:512
	ds_read_b32 v228, v119 offset:1024
	ds_read_b32 v229, v119 offset:1536
	ds_read_b32 v230, v119 offset:2048
	ds_read_b32 v231, v119 offset:2560
	ds_read_b32 v232, v119 offset:3072
	ds_read_b32 v233, v119 offset:3584
	s_waitcnt lgkmcnt(0)
	v_bfe_u32 v120, v226, 16, 1
	v_bfe_u32 v121, v227, 16, 1
	v_bfe_u32 v122, v228, 16, 1
	v_bfe_u32 v123, v229, 16, 1
	v_bfe_u32 v124, v230, 16, 1
	v_bfe_u32 v125, v231, 16, 1
	v_bfe_u32 v126, v232, 16, 1
	v_bfe_u32 v127, v233, 16, 1
	v_add3_u32 v226, v226, v120, s63
	v_add3_u32 v227, v227, v121, s63
	v_add3_u32 v228, v228, v122, s63
	v_add3_u32 v229, v229, v123, s63
	v_add3_u32 v230, v230, v124, s63
	v_add3_u32 v231, v231, v125, s63
	v_add3_u32 v232, v232, v126, s63
	v_add3_u32 v233, v233, v127, s63
	v_perm_b32 v242, v227, v226, s64
	v_perm_b32 v243, v229, v228, s64
	v_perm_b32 v244, v231, v230, s64
	v_perm_b32 v245, v233, v232, s64
	s_nop 0
	global_store_dwordx4 v94, v[242:245], s[6:7]
	s_waitcnt vmcnt(16)
	v_mul_f32_e32 v144, v42, v144
	v_mul_f32_e32 v145, v42, v145
	v_mul_f32_e32 v146, v42, v146
	v_mul_f32_e32 v147, v42, v147
	ds_write_b128 v209, v[144:147]
	v_mul_f32_e32 v148, v43, v148
	v_mul_f32_e32 v149, v43, v149
	v_mul_f32_e32 v150, v43, v150
	v_mul_f32_e32 v151, v43, v151
	ds_write_b128 v209, v[148:151] offset:1024
	v_mul_f32_e32 v152, v44, v152
	v_mul_f32_e32 v153, v44, v153
	v_mul_f32_e32 v154, v44, v154
	v_mul_f32_e32 v155, v44, v155
	ds_write_b128 v209, v[152:155] offset:2048
	v_mul_f32_e32 v156, v45, v156
	v_mul_f32_e32 v157, v45, v157
	v_mul_f32_e32 v158, v45, v158
	v_mul_f32_e32 v159, v45, v159
	ds_write_b128 v209, v[156:159] offset:3072
	v_mul_f32_e32 v160, v46, v160
	v_mul_f32_e32 v161, v46, v161
	v_mul_f32_e32 v162, v46, v162
	v_mul_f32_e32 v163, v46, v163
	ds_write_b128 v209, v[160:163] offset:4096
	v_mul_f32_e32 v164, v47, v164
	v_mul_f32_e32 v165, v47, v165
	v_mul_f32_e32 v166, v47, v166
	v_mul_f32_e32 v167, v47, v167
	ds_write_b128 v209, v[164:167] offset:5120
	v_mul_f32_e32 v168, v48, v168
	v_mul_f32_e32 v169, v48, v169
	v_mul_f32_e32 v170, v48, v170
	v_mul_f32_e32 v171, v48, v171
	ds_write_b128 v209, v[168:171] offset:6144
	v_mul_f32_e32 v172, v49, v172
	v_mul_f32_e32 v173, v49, v173
	v_mul_f32_e32 v174, v49, v174
	v_mul_f32_e32 v175, v49, v175
	ds_write_b128 v209, v[172:175] offset:7168
	s_waitcnt lgkmcnt(0)
	s_barrier
; #define GAS __attribute__((address_space(1)))
; #define LAS __attribute__((address_space(3)))
; #define LDS_WAIT() asm volatile("s_waitcnt lgkmcnt(0)" ::: "memory")
; __device__ __forceinline__ unsigned pk2(float lo, float hi) { return f2bf(lo) | (f2bf(hi) << 16); }
; __device__ __forceinline__ int src_col_in(int c) {
;     if (c < 5120) { const int blk = c >> 7, p = c & 127; const bool rope = blk < 16 || ((((blk - 16) >> 2) & 1) == 0); const int d = rope ? (p >> 1) + 64 * (p & 1) : p; return blk * 128 + d; }
;     if (c < OFF_Z) return c + 2096;
;     if (c < OFF_G) return c - 4048;
;     if (c < OFF_DT) return 5120 + (c - OFF_G);
;     if (c < NSRC) return c;
;     return -1;
; }
; __device__ __forceinline__ int nat_dim(int p) { return (p >> 1) + 64 * (p & 1); }
; template <int MAP, bool KS, bool KPERM = false>
; __device__ __forceinline__ void p0_transpose_item(const float* W, int K, int Nsrc, int nblk, bf16* WT, const float* ksA, const float* ksB, int ksplit, LAS float* scr, int item, int lane) {
;     const int kb = item / nblk, nb = item % nblk, k0 = 64 * kb, n0 = 32 * nb;
;     const int nr = n0 + (lane & 31); const int sc = MAP == 1 ? src_col_in(nr) : (MAP == 2 ? nat_dim(nr) : nr);
;     float v[32];
; #pragma unroll
;     for (int i = 0; i < 32; ++i) { const int k = k0 + 2 * i + (lane >> 5); const int ksrc = KPERM ? ((k & ~127) + nat_dim(k & 127)) : k;
;         v[i] = sc >= 0 ? W[(size_t)ksrc * Nsrc + sc] : 0.f; }
; #pragma unroll
;     for (int i = 0; i < 32; ++i) { const int kk = 2 * i + (lane >> 5); const int k = k0 + kk;
;         if (KS) v[i] *= (k < ksplit ? ksA[k] : ksB[k - ksplit]);
;         scr[kk * 33 + (lane & 31)] = v[i]; }
;     LDS_WAIT(); asm volatile("" ::: "memory");
;     const int c = lane & 7;
; #pragma unroll
;     for (int j = 0; j < 4; ++j) { const int n = (lane >> 3) + 8 * j; const LAS float* s = scr + (8 * c) * 33 + n;
;         v4u o; o.x = pk2(s[0 * 33], s[1 * 33]); o.y = pk2(s[2 * 33], s[3 * 33]); o.z = pk2(s[4 * 33], s[5 * 33]); o.w = pk2(s[6 * 33], s[7 * 33]);
;         *(GAS v4u*)(WT + (size_t)(n0 + n) * K + k0 + 8 * c) = o; }
;     LDS_WAIT(); asm volatile("" ::: "memory");
; }
	s_add_i32 s24, s23, 32
	s_lshl_b32 s20, s24, 7
	s_cmp_lt_u32 s24, 40
	s_cselect_b32 s21, 0, 0x830
	s_cmp_lt_u32 s24, 72
	s_cselect_b32 s21, s21, 0xfffff030
	s_add_i32 s20, s20, s21
	s_lshl_b32 s20, s20, 2
	s_add_u32 s8, s46, s20
	s_addc_u32 s9, s47, 0
	global_load_dwordx4 v[144:147], v76, s[8:9]
	s_add_u32 s8, s8, 0x16280
	s_addc_u32 s9, s9, 0
	global_load_dwordx4 v[148:151], v76, s[8:9]
	s_add_u32 s8, s8, 0x16280
	s_addc_u32 s9, s9, 0
	global_load_dwordx4 v[152:155], v76, s[8:9]
	s_add_u32 s8, s8, 0x16280
	s_addc_u32 s9, s9, 0
	global_load_dwordx4 v[156:159], v76, s[8:9]
	s_add_u32 s8, s8, 0x16280
	s_addc_u32 s9, s9, 0
	global_load_dwordx4 v[160:163], v76, s[8:9]
	s_add_u32 s8, s8, 0x16280
	s_addc_u32 s9, s9, 0
	global_load_dwordx4 v[164:167], v76, s[8:9]
	s_add_u32 s8, s8, 0x16280
	s_addc_u32 s9, s9, 0
	global_load_dwordx4 v[168:171], v76, s[8:9]
	s_add_u32 s8, s8, 0x16280
	s_addc_u32 s9, s9, 0
	global_load_dwordx4 v[172:175], v76, s[8:9]
	s_add_i32 s24, s23, 16
	s_mul_i32 s20, s24, 0x100000
	s_add_u32 s6, s48, s20
	s_addc_u32 s7, s49, 0
	s_cmp_lt_u32 s24, 16
	s_cselect_b32 s20, 1, 0
	s_sub_i32 s21, s24, 16
	s_bitcmp0_b32 s21, 2
	s_cselect_b32 s21, 1, 0
	s_cmp_lt_u32 s24, 40
	s_cselect_b32 s21, s21, 0
	s_or_b32 s20, s20, s21
	s_cmp_lg_u32 s20, 0
	s_cselect_b64 s[20:21], -1, 0
	v_cndmask_b32_e64 v91, v83, v87, s[20:21]
	v_cndmask_b32_e64 v92, v84, v88, s[20:21]
	v_cndmask_b32_e64 v93, v85, v89, s[20:21]
	v_cndmask_b32_e64 v94, v86, v90, s[20:21]
	ds_read_b32 v226, v112
	ds_read_b32 v227, v112 offset:512
	ds_read_b32 v228, v112 offset:1024
	ds_read_b32 v229, v112 offset:1536
	ds_read_b32 v230, v112 offset:2048
	ds_read_b32 v231, v112 offset:2560
	ds_read_b32 v232, v112 offset:3072
	ds_read_b32 v233, v112 offset:3584
	s_waitcnt lgkmcnt(0)
	v_bfe_u32 v120, v226, 16, 1
	v_bfe_u32 v121, v227, 16, 1
	v_bfe_u32 v122, v228, 16, 1
	v_bfe_u32 v123, v229, 16, 1
	v_bfe_u32 v124, v230, 16, 1
	v_bfe_u32 v125, v231, 16, 1
	v_bfe_u32 v126, v232, 16, 1
	v_bfe_u32 v127, v233, 16, 1
	v_add3_u32 v226, v226, v120, s63
	v_add3_u32 v227, v227, v121, s63
	v_add3_u32 v228, v228, v122, s63
	v_add3_u32 v229, v229, v123, s63
	v_add3_u32 v230, v230, v124, s63
	v_add3_u32 v231, v231, v125, s63
	v_add3_u32 v232, v232, v126, s63
	v_add3_u32 v233, v233, v127, s63
	v_perm_b32 v242, v227, v226, s64
	v_perm_b32 v243, v229, v228, s64
	v_perm_b32 v244, v231, v230, s64
	v_perm_b32 v245, v233, v232, s64
	s_nop 0
	global_store_dwordx4 v91, v[242:245], s[6:7]
	ds_read_b32 v226, v114
	ds_read_b32 v227, v114 offset:512
	ds_read_b32 v228, v114 offset:1024
	ds_read_b32 v229, v114 offset:1536
	ds_read_b32 v230, v114 offset:2048
	ds_read_b32 v231, v114 offset:2560
	ds_read_b32 v232, v114 offset:3072
	ds_read_b32 v233, v114 offset:3584
	s_waitcnt lgkmcnt(0)
	v_bfe_u32 v120, v226, 16, 1
	v_bfe_u32 v121, v227, 16, 1
	v_bfe_u32 v122, v228, 16, 1
	v_bfe_u32 v123, v229, 16, 1
	v_bfe_u32 v124, v230, 16, 1
	v_bfe_u32 v125, v231, 16, 1
	v_bfe_u32 v126, v232, 16, 1
	v_bfe_u32 v127, v233, 16, 1
	v_add3_u32 v226, v226, v120, s63
	v_add3_u32 v227, v227, v121, s63
	v_add3_u32 v228, v228, v122, s63
	v_add3_u32 v229, v229, v123, s63
	v_add3_u32 v230, v230, v124, s63
	v_add3_u32 v231, v231, v125, s63
	v_add3_u32 v232, v232, v126, s63
	v_add3_u32 v233, v233, v127, s63
	v_perm_b32 v242, v227, v226, s64
	v_perm_b32 v243, v229, v228, s64
	v_perm_b32 v244, v231, v230, s64
	v_perm_b32 v245, v233, v232, s64
	s_nop 0
	global_store_dwordx4 v92, v[242:245], s[6:7]
	ds_read_b32 v226, v116
	ds_read_b32 v227, v116 offset:512
	ds_read_b32 v228, v116 offset:1024
	ds_read_b32 v229, v116 offset:1536
	ds_read_b32 v230, v116 offset:2048
	ds_read_b32 v231, v116 offset:2560
	ds_read_b32 v232, v116 offset:3072
	ds_read_b32 v233, v116 offset:3584
	s_waitcnt lgkmcnt(0)
	v_bfe_u32 v120, v226, 16, 1
	v_bfe_u32 v121, v227, 16, 1
	v_bfe_u32 v122, v228, 16, 1
	v_bfe_u32 v123, v229, 16, 1
	v_bfe_u32 v124, v230, 16, 1
	v_bfe_u32 v125, v231, 16, 1
	v_bfe_u32 v126, v232, 16, 1
	v_bfe_u32 v127, v233, 16, 1
	v_add3_u32 v226, v226, v120, s63
	v_add3_u32 v227, v227, v121, s63
	v_add3_u32 v228, v228, v122, s63
	v_add3_u32 v229, v229, v123, s63
	v_add3_u32 v230, v230, v124, s63
	v_add3_u32 v231, v231, v125, s63
	v_add3_u32 v232, v232, v126, s63
	v_add3_u32 v233, v233, v127, s63
	v_perm_b32 v242, v227, v226, s64
	v_perm_b32 v243, v229, v228, s64
	v_perm_b32 v244, v231, v230, s64
	v_perm_b32 v245, v233, v232, s64
	s_nop 0
	global_store_dwordx4 v93, v[242:245], s[6:7]
	ds_read_b32 v226, v118
	ds_read_b32 v227, v118 offset:512
	ds_read_b32 v228, v118 offset:1024
	ds_read_b32 v229, v118 offset:1536
	ds_read_b32 v230, v118 offset:2048
	ds_read_b32 v231, v118 offset:2560
	ds_read_b32 v232, v118 offset:3072
	ds_read_b32 v233, v118 offset:3584
	s_waitcnt lgkmcnt(0)
	v_bfe_u32 v120, v226, 16, 1
	v_bfe_u32 v121, v227, 16, 1
	v_bfe_u32 v122, v228, 16, 1
	v_bfe_u32 v123, v229, 16, 1
	v_bfe_u32 v124, v230, 16, 1
	v_bfe_u32 v125, v231, 16, 1
	v_bfe_u32 v126, v232, 16, 1
	v_bfe_u32 v127, v233, 16, 1
	v_add3_u32 v226, v226, v120, s63
	v_add3_u32 v227, v227, v121, s63
	v_add3_u32 v228, v228, v122, s63
	v_add3_u32 v229, v229, v123, s63
	v_add3_u32 v230, v230, v124, s63
	v_add3_u32 v231, v231, v125, s63
	v_add3_u32 v232, v232, v126, s63
	v_add3_u32 v233, v233, v127, s63
	v_perm_b32 v242, v227, v226, s64
	v_perm_b32 v243, v229, v228, s64
	v_perm_b32 v244, v231, v230, s64
	v_perm_b32 v245, v233, v232, s64
	s_nop 0
	global_store_dwordx4 v94, v[242:245], s[6:7]
	s_waitcnt vmcnt(16)
	v_mul_f32_e32 v176, v42, v176
	v_mul_f32_e32 v177, v42, v177
	v_mul_f32_e32 v178, v42, v178
	v_mul_f32_e32 v179, v42, v179
	ds_write_b128 v210, v[176:179]
	v_mul_f32_e32 v180, v43, v180
	v_mul_f32_e32 v181, v43, v181
	v_mul_f32_e32 v182, v43, v182
	v_mul_f32_e32 v183, v43, v183
	ds_write_b128 v210, v[180:183] offset:1024
	v_mul_f32_e32 v184, v44, v184
	v_mul_f32_e32 v185, v44, v185
	v_mul_f32_e32 v186, v44, v186
	v_mul_f32_e32 v187, v44, v187
	ds_write_b128 v210, v[184:187] offset:2048
	v_mul_f32_e32 v188, v45, v188
	v_mul_f32_e32 v189, v45, v189
	v_mul_f32_e32 v190, v45, v190
	v_mul_f32_e32 v191, v45, v191
	ds_write_b128 v210, v[188:191] offset:3072
	v_mul_f32_e32 v192, v46, v192
	v_mul_f32_e32 v193, v46, v193
	v_mul_f32_e32 v194, v46, v194
	v_mul_f32_e32 v195, v46, v195
	ds_write_b128 v210, v[192:195] offset:4096
	v_mul_f32_e32 v196, v47, v196
	v_mul_f32_e32 v197, v47, v197
	v_mul_f32_e32 v198, v47, v198
	v_mul_f32_e32 v199, v47, v199
	ds_write_b128 v210, v[196:199] offset:5120
	v_mul_f32_e32 v200, v48, v200
	v_mul_f32_e32 v201, v48, v201
	v_mul_f32_e32 v202, v48, v202
	v_mul_f32_e32 v203, v48, v203
	ds_write_b128 v210, v[200:203] offset:6144
	v_mul_f32_e32 v204, v49, v204
	v_mul_f32_e32 v205, v49, v205
	v_mul_f32_e32 v206, v49, v206
	v_mul_f32_e32 v207, v49, v207
	ds_write_b128 v210, v[204:207] offset:7168
	s_waitcnt lgkmcnt(0)
	s_barrier
; #define GAS __attribute__((address_space(1)))
; #define LAS __attribute__((address_space(3)))
; #define LDS_WAIT() asm volatile("s_waitcnt lgkmcnt(0)" ::: "memory")
; __device__ __forceinline__ unsigned pk2(float lo, float hi) { return f2bf(lo) | (f2bf(hi) << 16); }
; __device__ __forceinline__ int src_col_in(int c) {
;     if (c < 5120) { const int blk = c >> 7, p = c & 127; const bool rope = blk < 16 || ((((blk - 16) >> 2) & 1) == 0); const int d = rope ? (p >> 1) + 64 * (p & 1) : p; return blk * 128 + d; }
;     if (c < OFF_Z) return c + 2096;
;     if (c < OFF_G) return c - 4048;
;     if (c < OFF_DT) return 5120 + (c - OFF_G);
;     if (c < NSRC) return c;
;     return -1;
; }
; __device__ __forceinline__ int nat_dim(int p) { return (p >> 1) + 64 * (p & 1); }
; template <int MAP, bool KS, bool KPERM = false>
; __device__ __forceinline__ void p0_transpose_item(const float* W, int K, int Nsrc, int nblk, bf16* WT, const float* ksA, const float* ksB, int ksplit, LAS float* scr, int item, int lane) {
;     const int kb = item / nblk, nb = item % nblk, k0 = 64 * kb, n0 = 32 * nb;
;     const int nr = n0 + (lane & 31); const int sc = MAP == 1 ? src_col_in(nr) : (MAP == 2 ? nat_dim(nr) : nr);
;     float v[32];
; #pragma unroll
;     for (int i = 0; i < 32; ++i) { const int k = k0 + 2 * i + (lane >> 5); const int ksrc = KPERM ? ((k & ~127) + nat_dim(k & 127)) : k;
;         v[i] = sc >= 0 ? W[(size_t)ksrc * Nsrc + sc] : 0.f; }
; #pragma unroll
;     for (int i = 0; i < 32; ++i) { const int kk = 2 * i + (lane >> 5); const int k = k0 + kk;
;         if (KS) v[i] *= (k < ksplit ? ksA[k] : ksB[k - ksplit]);
;         scr[kk * 33 + (lane & 31)] = v[i]; }
;     LDS_WAIT(); asm volatile("" ::: "memory");
;     const int c = lane & 7;
; #pragma unroll
;     for (int j = 0; j < 4; ++j) { const int n = (lane >> 3) + 8 * j; const LAS float* s = scr + (8 * c) * 33 + n;
;         v4u o; o.x = pk2(s[0 * 33], s[1 * 33]); o.y = pk2(s[2 * 33], s[3 * 33]); o.z = pk2(s[4 * 33], s[5 * 33]); o.w = pk2(s[6 * 33], s[7 * 33]);
;         *(GAS v4u*)(WT + (size_t)(n0 + n) * K + k0 + 8 * c) = o; }
;     LDS_WAIT(); asm volatile("" ::: "memory");
; }
	s_add_i32 s24, s23, 40
	s_lshl_b32 s20, s24, 7
	s_cmp_lt_u32 s24, 40
	s_cselect_b32 s21, 0, 0x830
	s_cmp_lt_u32 s24, 72
	s_cselect_b32 s21, s21, 0xfffff030
	s_add_i32 s20, s20, s21
	s_lshl_b32 s20, s20, 2
	s_add_u32 s8, s46, s20
	s_addc_u32 s9, s47, 0
	global_load_dwordx4 v[176:179], v76, s[8:9]
	s_add_u32 s8, s8, 0x16280
	s_addc_u32 s9, s9, 0
	global_load_dwordx4 v[180:183], v76, s[8:9]
	s_add_u32 s8, s8, 0x16280
	s_addc_u32 s9, s9, 0
	global_load_dwordx4 v[184:187], v76, s[8:9]
	s_add_u32 s8, s8, 0x16280
	s_addc_u32 s9, s9, 0
	global_load_dwordx4 v[188:191], v76, s[8:9]
	s_add_u32 s8, s8, 0x16280
	s_addc_u32 s9, s9, 0
	global_load_dwordx4 v[192:195], v76, s[8:9]
	s_add_u32 s8, s8, 0x16280
	s_addc_u32 s9, s9, 0
	global_load_dwordx4 v[196:199], v76, s[8:9]
	s_add_u32 s8, s8, 0x16280
	s_addc_u32 s9, s9, 0
	global_load_dwordx4 v[200:203], v76, s[8:9]
	s_add_u32 s8, s8, 0x16280
	s_addc_u32 s9, s9, 0
	global_load_dwordx4 v[204:207], v76, s[8:9]
	s_add_i32 s24, s23, 24
	s_mul_i32 s20, s24, 0x100000
	s_add_u32 s6, s48, s20
	s_addc_u32 s7, s49, 0
	s_cmp_lt_u32 s24, 16
	s_cselect_b32 s20, 1, 0
	s_sub_i32 s21, s24, 16
	s_bitcmp0_b32 s21, 2
	s_cselect_b32 s21, 1, 0
	s_cmp_lt_u32 s24, 40
	s_cselect_b32 s21, s21, 0
	s_or_b32 s20, s20, s21
	s_cmp_lg_u32 s20, 0
	s_cselect_b64 s[20:21], -1, 0
	v_cndmask_b32_e64 v91, v83, v87, s[20:21]
	v_cndmask_b32_e64 v92, v84, v88, s[20:21]
	v_cndmask_b32_e64 v93, v85, v89, s[20:21]
	v_cndmask_b32_e64 v94, v86, v90, s[20:21]
	ds_read_b32 v226, v113
	ds_read_b32 v227, v113 offset:512
	ds_read_b32 v228, v113 offset:1024
	ds_read_b32 v229, v113 offset:1536
	ds_read_b32 v230, v113 offset:2048
	ds_read_b32 v231, v113 offset:2560
	ds_read_b32 v232, v113 offset:3072
	ds_read_b32 v233, v113 offset:3584
	s_waitcnt lgkmcnt(0)
	v_bfe_u32 v120, v226, 16, 1
	v_bfe_u32 v121, v227, 16, 1
	v_bfe_u32 v122, v228, 16, 1
	v_bfe_u32 v123, v229, 16, 1
	v_bfe_u32 v124, v230, 16, 1
	v_bfe_u32 v125, v231, 16, 1
	v_bfe_u32 v126, v232, 16, 1
	v_bfe_u32 v127, v233, 16, 1
	v_add3_u32 v226, v226, v120, s63
	v_add3_u32 v227, v227, v121, s63
	v_add3_u32 v228, v228, v122, s63
	v_add3_u32 v229, v229, v123, s63
	v_add3_u32 v230, v230, v124, s63
	v_add3_u32 v231, v231, v125, s63
	v_add3_u32 v232, v232, v126, s63
	v_add3_u32 v233, v233, v127, s63
	v_perm_b32 v242, v227, v226, s64
	v_perm_b32 v243, v229, v228, s64
	v_perm_b32 v244, v231, v230, s64
	v_perm_b32 v245, v233, v232, s64
	s_nop 0
	global_store_dwordx4 v91, v[242:245], s[6:7]
	ds_read_b32 v226, v115
	ds_read_b32 v227, v115 offset:512
	ds_read_b32 v228, v115 offset:1024
	ds_read_b32 v229, v115 offset:1536
	ds_read_b32 v230, v115 offset:2048
	ds_read_b32 v231, v115 offset:2560
	ds_read_b32 v232, v115 offset:3072
	ds_read_b32 v233, v115 offset:3584
	s_waitcnt lgkmcnt(0)
	v_bfe_u32 v120, v226, 16, 1
	v_bfe_u32 v121, v227, 16, 1
	v_bfe_u32 v122, v228, 16, 1
	v_bfe_u32 v123, v229, 16, 1
	v_bfe_u32 v124, v230, 16, 1
	v_bfe_u32 v125, v231, 16, 1
	v_bfe_u32 v126, v232, 16, 1
	v_bfe_u32 v127, v233, 16, 1
	v_add3_u32 v226, v226, v120, s63
	v_add3_u32 v227, v227, v121, s63
	v_add3_u32 v228, v228, v122, s63
	v_add3_u32 v229, v229, v123, s63
	v_add3_u32 v230, v230, v124, s63
	v_add3_u32 v231, v231, v125, s63
	v_add3_u32 v232, v232, v126, s63
	v_add3_u32 v233, v233, v127, s63
	v_perm_b32 v242, v227, v226, s64
	v_perm_b32 v243, v229, v228, s64
	v_perm_b32 v244, v231, v230, s64
	v_perm_b32 v245, v233, v232, s64
	s_nop 0
	global_store_dwordx4 v92, v[242:245], s[6:7]
	ds_read_b32 v226, v117
	ds_read_b32 v227, v117 offset:512
	ds_read_b32 v228, v117 offset:1024
	ds_read_b32 v229, v117 offset:1536
	ds_read_b32 v230, v117 offset:2048
	ds_read_b32 v231, v117 offset:2560
	ds_read_b32 v232, v117 offset:3072
	ds_read_b32 v233, v117 offset:3584
	s_waitcnt lgkmcnt(0)
	v_bfe_u32 v120, v226, 16, 1
	v_bfe_u32 v121, v227, 16, 1
	v_bfe_u32 v122, v228, 16, 1
	v_bfe_u32 v123, v229, 16, 1
	v_bfe_u32 v124, v230, 16, 1
	v_bfe_u32 v125, v231, 16, 1
	v_bfe_u32 v126, v232, 16, 1
	v_bfe_u32 v127, v233, 16, 1
	v_add3_u32 v226, v226, v120, s63
	v_add3_u32 v227, v227, v121, s63
	v_add3_u32 v228, v228, v122, s63
	v_add3_u32 v229, v229, v123, s63
	v_add3_u32 v230, v230, v124, s63
	v_add3_u32 v231, v231, v125, s63
	v_add3_u32 v232, v232, v126, s63
	v_add3_u32 v233, v233, v127, s63
	v_perm_b32 v242, v227, v226, s64
	v_perm_b32 v243, v229, v228, s64
	v_perm_b32 v244, v231, v230, s64
	v_perm_b32 v245, v233, v232, s64
	s_nop 0
	global_store_dwordx4 v93, v[242:245], s[6:7]
	ds_read_b32 v226, v119
	ds_read_b32 v227, v119 offset:512
	ds_read_b32 v228, v119 offset:1024
	ds_read_b32 v229, v119 offset:1536
	ds_read_b32 v230, v119 offset:2048
	ds_read_b32 v231, v119 offset:2560
	ds_read_b32 v232, v119 offset:3072
	ds_read_b32 v233, v119 offset:3584
	s_waitcnt lgkmcnt(0)
	v_bfe_u32 v120, v226, 16, 1
	v_bfe_u32 v121, v227, 16, 1
	v_bfe_u32 v122, v228, 16, 1
	v_bfe_u32 v123, v229, 16, 1
	v_bfe_u32 v124, v230, 16, 1
	v_bfe_u32 v125, v231, 16, 1
	v_bfe_u32 v126, v232, 16, 1
	v_bfe_u32 v127, v233, 16, 1
	v_add3_u32 v226, v226, v120, s63
	v_add3_u32 v227, v227, v121, s63
	v_add3_u32 v228, v228, v122, s63
	v_add3_u32 v229, v229, v123, s63
	v_add3_u32 v230, v230, v124, s63
	v_add3_u32 v231, v231, v125, s63
	v_add3_u32 v232, v232, v126, s63
	v_add3_u32 v233, v233, v127, s63
	v_perm_b32 v242, v227, v226, s64
	v_perm_b32 v243, v229, v228, s64
	v_perm_b32 v244, v231, v230, s64
	v_perm_b32 v245, v233, v232, s64
	s_nop 0
	global_store_dwordx4 v94, v[242:245], s[6:7]
	s_waitcnt vmcnt(16)
	v_mul_f32_e32 v144, v42, v144
	v_mul_f32_e32 v145, v42, v145
	v_mul_f32_e32 v146, v42, v146
	v_mul_f32_e32 v147, v42, v147
	ds_write_b128 v209, v[144:147]
	v_mul_f32_e32 v148, v43, v148
	v_mul_f32_e32 v149, v43, v149
	v_mul_f32_e32 v150, v43, v150
	v_mul_f32_e32 v151, v43, v151
	ds_write_b128 v209, v[148:151] offset:1024
	v_mul_f32_e32 v152, v44, v152
	v_mul_f32_e32 v153, v44, v153
	v_mul_f32_e32 v154, v44, v154
	v_mul_f32_e32 v155, v44, v155
	ds_write_b128 v209, v[152:155] offset:2048
	v_mul_f32_e32 v156, v45, v156
	v_mul_f32_e32 v157, v45, v157
	v_mul_f32_e32 v158, v45, v158
	v_mul_f32_e32 v159, v45, v159
	ds_write_b128 v209, v[156:159] offset:3072
	v_mul_f32_e32 v160, v46, v160
	v_mul_f32_e32 v161, v46, v161
	v_mul_f32_e32 v162, v46, v162
	v_mul_f32_e32 v163, v46, v163
	ds_write_b128 v209, v[160:163] offset:4096
	v_mul_f32_e32 v164, v47, v164
	v_mul_f32_e32 v165, v47, v165
	v_mul_f32_e32 v166, v47, v166
	v_mul_f32_e32 v167, v47, v167
	ds_write_b128 v209, v[164:167] offset:5120
	v_mul_f32_e32 v168, v48, v168
	v_mul_f32_e32 v169, v48, v169
	v_mul_f32_e32 v170, v48, v170
	v_mul_f32_e32 v171, v48, v171
	ds_write_b128 v209, v[168:171] offset:6144
	v_mul_f32_e32 v172, v49, v172
	v_mul_f32_e32 v173, v49, v173
	v_mul_f32_e32 v174, v49, v174
	v_mul_f32_e32 v175, v49, v175
	ds_write_b128 v209, v[172:175] offset:7168
	s_waitcnt lgkmcnt(0)
	s_barrier
; #define GAS __attribute__((address_space(1)))
; #define LAS __attribute__((address_space(3)))
; #define LDS_WAIT() asm volatile("s_waitcnt lgkmcnt(0)" ::: "memory")
; __device__ __forceinline__ unsigned pk2(float lo, float hi) { return f2bf(lo) | (f2bf(hi) << 16); }
; __device__ __forceinline__ int src_col_in(int c) {
;     if (c < 5120) { const int blk = c >> 7, p = c & 127; const bool rope = blk < 16 || ((((blk - 16) >> 2) & 1) == 0); const int d = rope ? (p >> 1) + 64 * (p & 1) : p; return blk * 128 + d; }
;     if (c < OFF_Z) return c + 2096;
;     if (c < OFF_G) return c - 4048;
;     if (c < OFF_DT) return 5120 + (c - OFF_G);
;     if (c < NSRC) return c;
;     return -1;
; }
; __device__ __forceinline__ int nat_dim(int p) { return (p >> 1) + 64 * (p & 1); }
; template <int MAP, bool KS, bool KPERM = false>
; __device__ __forceinline__ void p0_transpose_item(const float* W, int K, int Nsrc, int nblk, bf16* WT, const float* ksA, const float* ksB, int ksplit, LAS float* scr, int item, int lane) {
;     const int kb = item / nblk, nb = item % nblk, k0 = 64 * kb, n0 = 32 * nb;
;     const int nr = n0 + (lane & 31); const int sc = MAP == 1 ? src_col_in(nr) : (MAP == 2 ? nat_dim(nr) : nr);
;     float v[32];
; #pragma unroll
;     for (int i = 0; i < 32; ++i) { const int k = k0 + 2 * i + (lane >> 5); const int ksrc = KPERM ? ((k & ~127) + nat_dim(k & 127)) : k;
;         v[i] = sc >= 0 ? W[(size_t)ksrc * Nsrc + sc] : 0.f; }
; #pragma unroll
;     for (int i = 0; i < 32; ++i) { const int kk = 2 * i + (lane >> 5); const int k = k0 + kk;
;         if (KS) v[i] *= (k < ksplit ? ksA[k] : ksB[k - ksplit]);
;         scr[kk * 33 + (lane & 31)] = v[i]; }
;     LDS_WAIT(); asm volatile("" ::: "memory");
;     const int c = lane & 7;
; #pragma unroll
;     for (int j = 0; j < 4; ++j) { const int n = (lane >> 3) + 8 * j; const LAS float* s = scr + (8 * c) * 33 + n;
;         v4u o; o.x = pk2(s[0 * 33], s[1 * 33]); o.y = pk2(s[2 * 33], s[3 * 33]); o.z = pk2(s[4 * 33], s[5 * 33]); o.w = pk2(s[6 * 33], s[7 * 33]);
;         *(GAS v4u*)(WT + (size_t)(n0 + n) * K + k0 + 8 * c) = o; }
;     LDS_WAIT(); asm volatile("" ::: "memory");
; }
	s_add_i32 s24, s23, 48
	s_lshl_b32 s20, s24, 7
	s_cmp_lt_u32 s24, 40
	s_cselect_b32 s21, 0, 0x830
	s_cmp_lt_u32 s24, 72
	s_cselect_b32 s21, s21, 0xfffff030
	s_add_i32 s20, s20, s21
	s_lshl_b32 s20, s20, 2
	s_add_u32 s8, s46, s20
	s_addc_u32 s9, s47, 0
	global_load_dwordx4 v[144:147], v76, s[8:9]
	s_add_u32 s8, s8, 0x16280
	s_addc_u32 s9, s9, 0
	global_load_dwordx4 v[148:151], v76, s[8:9]
	s_add_u32 s8, s8, 0x16280
	s_addc_u32 s9, s9, 0
	global_load_dwordx4 v[152:155], v76, s[8:9]
	s_add_u32 s8, s8, 0x16280
	s_addc_u32 s9, s9, 0
	global_load_dwordx4 v[156:159], v76, s[8:9]
	s_add_u32 s8, s8, 0x16280
	s_addc_u32 s9, s9, 0
	global_load_dwordx4 v[160:163], v76, s[8:9]
	s_add_u32 s8, s8, 0x16280
	s_addc_u32 s9, s9, 0
	global_load_dwordx4 v[164:167], v76, s[8:9]
	s_add_u32 s8, s8, 0x16280
	s_addc_u32 s9, s9, 0
	global_load_dwordx4 v[168:171], v76, s[8:9]
	s_add_u32 s8, s8, 0x16280
	s_addc_u32 s9, s9, 0
	global_load_dwordx4 v[172:175], v76, s[8:9]
	s_add_i32 s24, s23, 32
	s_mul_i32 s20, s24, 0x100000
	s_add_u32 s6, s48, s20
	s_addc_u32 s7, s49, 0
	s_cmp_lt_u32 s24, 16
	s_cselect_b32 s20, 1, 0
	s_sub_i32 s21, s24, 16
	s_bitcmp0_b32 s21, 2
	s_cselect_b32 s21, 1, 0
	s_cmp_lt_u32 s24, 40
	s_cselect_b32 s21, s21, 0
	s_or_b32 s20, s20, s21
	s_cmp_lg_u32 s20, 0
	s_cselect_b64 s[20:21], -1, 0
	v_cndmask_b32_e64 v91, v83, v87, s[20:21]
	v_cndmask_b32_e64 v92, v84, v88, s[20:21]
	v_cndmask_b32_e64 v93, v85, v89, s[20:21]
	v_cndmask_b32_e64 v94, v86, v90, s[20:21]
	ds_read_b32 v226, v112
	ds_read_b32 v227, v112 offset:512
	ds_read_b32 v228, v112 offset:1024
	ds_read_b32 v229, v112 offset:1536
	ds_read_b32 v230, v112 offset:2048
	ds_read_b32 v231, v112 offset:2560
	ds_read_b32 v232, v112 offset:3072
	ds_read_b32 v233, v112 offset:3584
	s_waitcnt lgkmcnt(0)
	v_bfe_u32 v120, v226, 16, 1
	v_bfe_u32 v121, v227, 16, 1
	v_bfe_u32 v122, v228, 16, 1
	v_bfe_u32 v123, v229, 16, 1
	v_bfe_u32 v124, v230, 16, 1
	v_bfe_u32 v125, v231, 16, 1
	v_bfe_u32 v126, v232, 16, 1
	v_bfe_u32 v127, v233, 16, 1
	v_add3_u32 v226, v226, v120, s63
	v_add3_u32 v227, v227, v121, s63
	v_add3_u32 v228, v228, v122, s63
	v_add3_u32 v229, v229, v123, s63
	v_add3_u32 v230, v230, v124, s63
	v_add3_u32 v231, v231, v125, s63
	v_add3_u32 v232, v232, v126, s63
	v_add3_u32 v233, v233, v127, s63
	v_perm_b32 v242, v227, v226, s64
	v_perm_b32 v243, v229, v228, s64
	v_perm_b32 v244, v231, v230, s64
	v_perm_b32 v245, v233, v232, s64
	s_nop 0
	global_store_dwordx4 v91, v[242:245], s[6:7]
	ds_read_b32 v226, v114
	ds_read_b32 v227, v114 offset:512
	ds_read_b32 v228, v114 offset:1024
	ds_read_b32 v229, v114 offset:1536
	ds_read_b32 v230, v114 offset:2048
	ds_read_b32 v231, v114 offset:2560
	ds_read_b32 v232, v114 offset:3072
	ds_read_b32 v233, v114 offset:3584
	s_waitcnt lgkmcnt(0)
	v_bfe_u32 v120, v226, 16, 1
	v_bfe_u32 v121, v227, 16, 1
	v_bfe_u32 v122, v228, 16, 1
	v_bfe_u32 v123, v229, 16, 1
	v_bfe_u32 v124, v230, 16, 1
	v_bfe_u32 v125, v231, 16, 1
	v_bfe_u32 v126, v232, 16, 1
	v_bfe_u32 v127, v233, 16, 1
	v_add3_u32 v226, v226, v120, s63
	v_add3_u32 v227, v227, v121, s63
	v_add3_u32 v228, v228, v122, s63
	v_add3_u32 v229, v229, v123, s63
	v_add3_u32 v230, v230, v124, s63
	v_add3_u32 v231, v231, v125, s63
	v_add3_u32 v232, v232, v126, s63
	v_add3_u32 v233, v233, v127, s63
	v_perm_b32 v242, v227, v226, s64
	v_perm_b32 v243, v229, v228, s64
	v_perm_b32 v244, v231, v230, s64
	v_perm_b32 v245, v233, v232, s64
	s_nop 0
	global_store_dwordx4 v92, v[242:245], s[6:7]
	ds_read_b32 v226, v116
	ds_read_b32 v227, v116 offset:512
	ds_read_b32 v228, v116 offset:1024
	ds_read_b32 v229, v116 offset:1536
	ds_read_b32 v230, v116 offset:2048
	ds_read_b32 v231, v116 offset:2560
	ds_read_b32 v232, v116 offset:3072
	ds_read_b32 v233, v116 offset:3584
	s_waitcnt lgkmcnt(0)
	v_bfe_u32 v120, v226, 16, 1
	v_bfe_u32 v121, v227, 16, 1
	v_bfe_u32 v122, v228, 16, 1
	v_bfe_u32 v123, v229, 16, 1
	v_bfe_u32 v124, v230, 16, 1
	v_bfe_u32 v125, v231, 16, 1
	v_bfe_u32 v126, v232, 16, 1
	v_bfe_u32 v127, v233, 16, 1
	v_add3_u32 v226, v226, v120, s63
	v_add3_u32 v227, v227, v121, s63
	v_add3_u32 v228, v228, v122, s63
	v_add3_u32 v229, v229, v123, s63
	v_add3_u32 v230, v230, v124, s63
	v_add3_u32 v231, v231, v125, s63
	v_add3_u32 v232, v232, v126, s63
	v_add3_u32 v233, v233, v127, s63
	v_perm_b32 v242, v227, v226, s64
	v_perm_b32 v243, v229, v228, s64
	v_perm_b32 v244, v231, v230, s64
	v_perm_b32 v245, v233, v232, s64
	s_nop 0
	global_store_dwordx4 v93, v[242:245], s[6:7]
	ds_read_b32 v226, v118
	ds_read_b32 v227, v118 offset:512
	ds_read_b32 v228, v118 offset:1024
	ds_read_b32 v229, v118 offset:1536
	ds_read_b32 v230, v118 offset:2048
	ds_read_b32 v231, v118 offset:2560
	ds_read_b32 v232, v118 offset:3072
	ds_read_b32 v233, v118 offset:3584
	s_waitcnt lgkmcnt(0)
	v_bfe_u32 v120, v226, 16, 1
	v_bfe_u32 v121, v227, 16, 1
	v_bfe_u32 v122, v228, 16, 1
	v_bfe_u32 v123, v229, 16, 1
	v_bfe_u32 v124, v230, 16, 1
	v_bfe_u32 v125, v231, 16, 1
	v_bfe_u32 v126, v232, 16, 1
	v_bfe_u32 v127, v233, 16, 1
	v_add3_u32 v226, v226, v120, s63
	v_add3_u32 v227, v227, v121, s63
	v_add3_u32 v228, v228, v122, s63
	v_add3_u32 v229, v229, v123, s63
	v_add3_u32 v230, v230, v124, s63
	v_add3_u32 v231, v231, v125, s63
	v_add3_u32 v232, v232, v126, s63
	v_add3_u32 v233, v233, v127, s63
	v_perm_b32 v242, v227, v226, s64
	v_perm_b32 v243, v229, v228, s64
	v_perm_b32 v244, v231, v230, s64
	v_perm_b32 v245, v233, v232, s64
	s_nop 0
	global_store_dwordx4 v94, v[242:245], s[6:7]
	s_waitcnt vmcnt(16)
	v_mul_f32_e32 v176, v42, v176
	v_mul_f32_e32 v177, v42, v177
	v_mul_f32_e32 v178, v42, v178
	v_mul_f32_e32 v179, v42, v179
	ds_write_b128 v210, v[176:179]
	v_mul_f32_e32 v180, v43, v180
	v_mul_f32_e32 v181, v43, v181
	v_mul_f32_e32 v182, v43, v182
	v_mul_f32_e32 v183, v43, v183
	ds_write_b128 v210, v[180:183] offset:1024
	v_mul_f32_e32 v184, v44, v184
	v_mul_f32_e32 v185, v44, v185
	v_mul_f32_e32 v186, v44, v186
	v_mul_f32_e32 v187, v44, v187
	ds_write_b128 v210, v[184:187] offset:2048
	v_mul_f32_e32 v188, v45, v188
	v_mul_f32_e32 v189, v45, v189
	v_mul_f32_e32 v190, v45, v190
	v_mul_f32_e32 v191, v45, v191
	ds_write_b128 v210, v[188:191] offset:3072
	v_mul_f32_e32 v192, v46, v192
	v_mul_f32_e32 v193, v46, v193
	v_mul_f32_e32 v194, v46, v194
	v_mul_f32_e32 v195, v46, v195
	ds_write_b128 v210, v[192:195] offset:4096
	v_mul_f32_e32 v196, v47, v196
	v_mul_f32_e32 v197, v47, v197
	v_mul_f32_e32 v198, v47, v198
	v_mul_f32_e32 v199, v47, v199
	ds_write_b128 v210, v[196:199] offset:5120
	v_mul_f32_e32 v200, v48, v200
	v_mul_f32_e32 v201, v48, v201
	v_mul_f32_e32 v202, v48, v202
	v_mul_f32_e32 v203, v48, v203
	ds_write_b128 v210, v[200:203] offset:6144
	v_mul_f32_e32 v204, v49, v204
	v_mul_f32_e32 v205, v49, v205
	v_mul_f32_e32 v206, v49, v206
	v_mul_f32_e32 v207, v49, v207
	ds_write_b128 v210, v[204:207] offset:7168
	s_waitcnt lgkmcnt(0)
	s_barrier
; #define GAS __attribute__((address_space(1)))
; #define LAS __attribute__((address_space(3)))
; #define LDS_WAIT() asm volatile("s_waitcnt lgkmcnt(0)" ::: "memory")
; __device__ __forceinline__ unsigned pk2(float lo, float hi) { return f2bf(lo) | (f2bf(hi) << 16); }
; __device__ __forceinline__ int src_col_in(int c) {
;     if (c < 5120) { const int blk = c >> 7, p = c & 127; const bool rope = blk < 16 || ((((blk - 16) >> 2) & 1) == 0); const int d = rope ? (p >> 1) + 64 * (p & 1) : p; return blk * 128 + d; }
;     if (c < OFF_Z) return c + 2096;
;     if (c < OFF_G) return c - 4048;
;     if (c < OFF_DT) return 5120 + (c - OFF_G);
;     if (c < NSRC) return c;
;     return -1;
; }
; __device__ __forceinline__ int nat_dim(int p) { return (p >> 1) + 64 * (p & 1); }
; template <int MAP, bool KS, bool KPERM = false>
; __device__ __forceinline__ void p0_transpose_item(const float* W, int K, int Nsrc, int nblk, bf16* WT, const float* ksA, const float* ksB, int ksplit, LAS float* scr, int item, int lane) {
;     const int kb = item / nblk, nb = item % nblk, k0 = 64 * kb, n0 = 32 * nb;
;     const int nr = n0 + (lane & 31); const int sc = MAP == 1 ? src_col_in(nr) : (MAP == 2 ? nat_dim(nr) : nr);
;     float v[32];
; #pragma unroll
;     for (int i = 0; i < 32; ++i) { const int k = k0 + 2 * i + (lane >> 5); const int ksrc = KPERM ? ((k & ~127) + nat_dim(k & 127)) : k;
;         v[i] = sc >= 0 ? W[(size_t)ksrc * Nsrc + sc] : 0.f; }
; #pragma unroll
;     for (int i = 0; i < 32; ++i) { const int kk = 2 * i + (lane >> 5); const int k = k0 + kk;
;         if (KS) v[i] *= (k < ksplit ? ksA[k] : ksB[k - ksplit]);
;         scr[kk * 33 + (lane & 31)] = v[i]; }
;     LDS_WAIT(); asm volatile("" ::: "memory");
;     const int c = lane & 7;
; #pragma unroll
;     for (int j = 0; j < 4; ++j) { const int n = (lane >> 3) + 8 * j; const LAS float* s = scr + (8 * c) * 33 + n;
;         v4u o; o.x = pk2(s[0 * 33], s[1 * 33]); o.y = pk2(s[2 * 33], s[3 * 33]); o.z = pk2(s[4 * 33], s[5 * 33]); o.w = pk2(s[6 * 33], s[7 * 33]);
;         *(GAS v4u*)(WT + (size_t)(n0 + n) * K + k0 + 8 * c) = o; }
;     LDS_WAIT(); asm volatile("" ::: "memory");
; }
	s_add_i32 s24, s23, 56
	s_lshl_b32 s20, s24, 7
	s_cmp_lt_u32 s24, 40
	s_cselect_b32 s21, 0, 0x830
	s_cmp_lt_u32 s24, 72
	s_cselect_b32 s21, s21, 0xfffff030
	s_add_i32 s20, s20, s21
	s_lshl_b32 s20, s20, 2
	s_add_u32 s8, s46, s20
	s_addc_u32 s9, s47, 0
	global_load_dwordx4 v[176:179], v76, s[8:9]
	s_add_u32 s8, s8, 0x16280
	s_addc_u32 s9, s9, 0
	global_load_dwordx4 v[180:183], v76, s[8:9]
	s_add_u32 s8, s8, 0x16280
	s_addc_u32 s9, s9, 0
	global_load_dwordx4 v[184:187], v76, s[8:9]
	s_add_u32 s8, s8, 0x16280
	s_addc_u32 s9, s9, 0
	global_load_dwordx4 v[188:191], v76, s[8:9]
	s_add_u32 s8, s8, 0x16280
	s_addc_u32 s9, s9, 0
	global_load_dwordx4 v[192:195], v76, s[8:9]
	s_add_u32 s8, s8, 0x16280
	s_addc_u32 s9, s9, 0
	global_load_dwordx4 v[196:199], v76, s[8:9]
	s_add_u32 s8, s8, 0x16280
	s_addc_u32 s9, s9, 0
	global_load_dwordx4 v[200:203], v76, s[8:9]
	s_add_u32 s8, s8, 0x16280
	s_addc_u32 s9, s9, 0
	global_load_dwordx4 v[204:207], v76, s[8:9]
	s_add_i32 s24, s23, 40
	s_mul_i32 s20, s24, 0x100000
	s_add_u32 s6, s48, s20
	s_addc_u32 s7, s49, 0
	s_cmp_lt_u32 s24, 16
	s_cselect_b32 s20, 1, 0
	s_sub_i32 s21, s24, 16
	s_bitcmp0_b32 s21, 2
	s_cselect_b32 s21, 1, 0
	s_cmp_lt_u32 s24, 40
	s_cselect_b32 s21, s21, 0
	s_or_b32 s20, s20, s21
	s_cmp_lg_u32 s20, 0
	s_cselect_b64 s[20:21], -1, 0
	v_cndmask_b32_e64 v91, v83, v87, s[20:21]
	v_cndmask_b32_e64 v92, v84, v88, s[20:21]
	v_cndmask_b32_e64 v93, v85, v89, s[20:21]
	v_cndmask_b32_e64 v94, v86, v90, s[20:21]
	ds_read_b32 v226, v113
	ds_read_b32 v227, v113 offset:512
	ds_read_b32 v228, v113 offset:1024
	ds_read_b32 v229, v113 offset:1536
	ds_read_b32 v230, v113 offset:2048
	ds_read_b32 v231, v113 offset:2560
	ds_read_b32 v232, v113 offset:3072
	ds_read_b32 v233, v113 offset:3584
	s_waitcnt lgkmcnt(0)
	v_bfe_u32 v120, v226, 16, 1
	v_bfe_u32 v121, v227, 16, 1
	v_bfe_u32 v122, v228, 16, 1
	v_bfe_u32 v123, v229, 16, 1
	v_bfe_u32 v124, v230, 16, 1
	v_bfe_u32 v125, v231, 16, 1
	v_bfe_u32 v126, v232, 16, 1
	v_bfe_u32 v127, v233, 16, 1
	v_add3_u32 v226, v226, v120, s63
	v_add3_u32 v227, v227, v121, s63
	v_add3_u32 v228, v228, v122, s63
	v_add3_u32 v229, v229, v123, s63
	v_add3_u32 v230, v230, v124, s63
	v_add3_u32 v231, v231, v125, s63
	v_add3_u32 v232, v232, v126, s63
	v_add3_u32 v233, v233, v127, s63
	v_perm_b32 v242, v227, v226, s64
	v_perm_b32 v243, v229, v228, s64
	v_perm_b32 v244, v231, v230, s64
	v_perm_b32 v245, v233, v232, s64
	s_nop 0
	global_store_dwordx4 v91, v[242:245], s[6:7]
	ds_read_b32 v226, v115
	ds_read_b32 v227, v115 offset:512
	ds_read_b32 v228, v115 offset:1024
	ds_read_b32 v229, v115 offset:1536
	ds_read_b32 v230, v115 offset:2048
	ds_read_b32 v231, v115 offset:2560
	ds_read_b32 v232, v115 offset:3072
	ds_read_b32 v233, v115 offset:3584
	s_waitcnt lgkmcnt(0)
	v_bfe_u32 v120, v226, 16, 1
	v_bfe_u32 v121, v227, 16, 1
	v_bfe_u32 v122, v228, 16, 1
	v_bfe_u32 v123, v229, 16, 1
	v_bfe_u32 v124, v230, 16, 1
	v_bfe_u32 v125, v231, 16, 1
	v_bfe_u32 v126, v232, 16, 1
	v_bfe_u32 v127, v233, 16, 1
	v_add3_u32 v226, v226, v120, s63
	v_add3_u32 v227, v227, v121, s63
	v_add3_u32 v228, v228, v122, s63
	v_add3_u32 v229, v229, v123, s63
	v_add3_u32 v230, v230, v124, s63
	v_add3_u32 v231, v231, v125, s63
	v_add3_u32 v232, v232, v126, s63
	v_add3_u32 v233, v233, v127, s63
	v_perm_b32 v242, v227, v226, s64
	v_perm_b32 v243, v229, v228, s64
	v_perm_b32 v244, v231, v230, s64
	v_perm_b32 v245, v233, v232, s64
	s_nop 0
	global_store_dwordx4 v92, v[242:245], s[6:7]
	ds_read_b32 v226, v117
	ds_read_b32 v227, v117 offset:512
	ds_read_b32 v228, v117 offset:1024
	ds_read_b32 v229, v117 offset:1536
	ds_read_b32 v230, v117 offset:2048
	ds_read_b32 v231, v117 offset:2560
	ds_read_b32 v232, v117 offset:3072
	ds_read_b32 v233, v117 offset:3584
	s_waitcnt lgkmcnt(0)
	v_bfe_u32 v120, v226, 16, 1
	v_bfe_u32 v121, v227, 16, 1
	v_bfe_u32 v122, v228, 16, 1
	v_bfe_u32 v123, v229, 16, 1
	v_bfe_u32 v124, v230, 16, 1
	v_bfe_u32 v125, v231, 16, 1
	v_bfe_u32 v126, v232, 16, 1
	v_bfe_u32 v127, v233, 16, 1
	v_add3_u32 v226, v226, v120, s63
	v_add3_u32 v227, v227, v121, s63
	v_add3_u32 v228, v228, v122, s63
	v_add3_u32 v229, v229, v123, s63
	v_add3_u32 v230, v230, v124, s63
	v_add3_u32 v231, v231, v125, s63
	v_add3_u32 v232, v232, v126, s63
	v_add3_u32 v233, v233, v127, s63
	v_perm_b32 v242, v227, v226, s64
	v_perm_b32 v243, v229, v228, s64
	v_perm_b32 v244, v231, v230, s64
	v_perm_b32 v245, v233, v232, s64
	s_nop 0
	global_store_dwordx4 v93, v[242:245], s[6:7]
	ds_read_b32 v226, v119
	ds_read_b32 v227, v119 offset:512
	ds_read_b32 v228, v119 offset:1024
	ds_read_b32 v229, v119 offset:1536
	ds_read_b32 v230, v119 offset:2048
	ds_read_b32 v231, v119 offset:2560
	ds_read_b32 v232, v119 offset:3072
	ds_read_b32 v233, v119 offset:3584
	s_waitcnt lgkmcnt(0)
	v_bfe_u32 v120, v226, 16, 1
	v_bfe_u32 v121, v227, 16, 1
	v_bfe_u32 v122, v228, 16, 1
	v_bfe_u32 v123, v229, 16, 1
	v_bfe_u32 v124, v230, 16, 1
	v_bfe_u32 v125, v231, 16, 1
	v_bfe_u32 v126, v232, 16, 1
	v_bfe_u32 v127, v233, 16, 1
	v_add3_u32 v226, v226, v120, s63
	v_add3_u32 v227, v227, v121, s63
	v_add3_u32 v228, v228, v122, s63
	v_add3_u32 v229, v229, v123, s63
	v_add3_u32 v230, v230, v124, s63
	v_add3_u32 v231, v231, v125, s63
	v_add3_u32 v232, v232, v126, s63
	v_add3_u32 v233, v233, v127, s63
	v_perm_b32 v242, v227, v226, s64
	v_perm_b32 v243, v229, v228, s64
	v_perm_b32 v244, v231, v230, s64
	v_perm_b32 v245, v233, v232, s64
	s_nop 0
	global_store_dwordx4 v94, v[242:245], s[6:7]
	s_waitcnt vmcnt(16)
	v_mul_f32_e32 v144, v42, v144
	v_mul_f32_e32 v145, v42, v145
	v_mul_f32_e32 v146, v42, v146
	v_mul_f32_e32 v147, v42, v147
	ds_write_b128 v209, v[144:147]
	v_mul_f32_e32 v148, v43, v148
	v_mul_f32_e32 v149, v43, v149
	v_mul_f32_e32 v150, v43, v150
	v_mul_f32_e32 v151, v43, v151
	ds_write_b128 v209, v[148:151] offset:1024
	v_mul_f32_e32 v152, v44, v152
	v_mul_f32_e32 v153, v44, v153
	v_mul_f32_e32 v154, v44, v154
	v_mul_f32_e32 v155, v44, v155
	ds_write_b128 v209, v[152:155] offset:2048
	v_mul_f32_e32 v156, v45, v156
	v_mul_f32_e32 v157, v45, v157
	v_mul_f32_e32 v158, v45, v158
	v_mul_f32_e32 v159, v45, v159
	ds_write_b128 v209, v[156:159] offset:3072
	v_mul_f32_e32 v160, v46, v160
	v_mul_f32_e32 v161, v46, v161
	v_mul_f32_e32 v162, v46, v162
	v_mul_f32_e32 v163, v46, v163
	ds_write_b128 v209, v[160:163] offset:4096
	v_mul_f32_e32 v164, v47, v164
	v_mul_f32_e32 v165, v47, v165
	v_mul_f32_e32 v166, v47, v166
	v_mul_f32_e32 v167, v47, v167
	ds_write_b128 v209, v[164:167] offset:5120
	v_mul_f32_e32 v168, v48, v168
	v_mul_f32_e32 v169, v48, v169
	v_mul_f32_e32 v170, v48, v170
	v_mul_f32_e32 v171, v48, v171
	ds_write_b128 v209, v[168:171] offset:6144
	v_mul_f32_e32 v172, v49, v172
	v_mul_f32_e32 v173, v49, v173
	v_mul_f32_e32 v174, v49, v174
	v_mul_f32_e32 v175, v49, v175
	ds_write_b128 v209, v[172:175] offset:7168
	s_waitcnt lgkmcnt(0)
	s_barrier
; #define GAS __attribute__((address_space(1)))
; #define LAS __attribute__((address_space(3)))
; #define LDS_WAIT() asm volatile("s_waitcnt lgkmcnt(0)" ::: "memory")
; __device__ __forceinline__ unsigned pk2(float lo, float hi) { return f2bf(lo) | (f2bf(hi) << 16); }
; __device__ __forceinline__ int src_col_in(int c) {
;     if (c < 5120) { const int blk = c >> 7, p = c & 127; const bool rope = blk < 16 || ((((blk - 16) >> 2) & 1) == 0); const int d = rope ? (p >> 1) + 64 * (p & 1) : p; return blk * 128 + d; }
;     if (c < OFF_Z) return c + 2096;
;     if (c < OFF_G) return c - 4048;
;     if (c < OFF_DT) return 5120 + (c - OFF_G);
;     if (c < NSRC) return c;
;     return -1;
; }
; __device__ __forceinline__ int nat_dim(int p) { return (p >> 1) + 64 * (p & 1); }
; template <int MAP, bool KS, bool KPERM = false>
; __device__ __forceinline__ void p0_transpose_item(const float* W, int K, int Nsrc, int nblk, bf16* WT, const float* ksA, const float* ksB, int ksplit, LAS float* scr, int item, int lane) {
;     const int kb = item / nblk, nb = item % nblk, k0 = 64 * kb, n0 = 32 * nb;
;     const int nr = n0 + (lane & 31); const int sc = MAP == 1 ? src_col_in(nr) : (MAP == 2 ? nat_dim(nr) : nr);
;     float v[32];
; #pragma unroll
;     for (int i = 0; i < 32; ++i) { const int k = k0 + 2 * i + (lane >> 5); const int ksrc = KPERM ? ((k & ~127) + nat_dim(k & 127)) : k;
;         v[i] = sc >= 0 ? W[(size_t)ksrc * Nsrc + sc] : 0.f; }
; #pragma unroll
;     for (int i = 0; i < 32; ++i) { const int kk = 2 * i + (lane >> 5); const int k = k0 + kk;
;         if (KS) v[i] *= (k < ksplit ? ksA[k] : ksB[k - ksplit]);
;         scr[kk * 33 + (lane & 31)] = v[i]; }
;     LDS_WAIT(); asm volatile("" ::: "memory");
;     const int c = lane & 7;
; #pragma unroll
;     for (int j = 0; j < 4; ++j) { const int n = (lane >> 3) + 8 * j; const LAS float* s = scr + (8 * c) * 33 + n;
;         v4u o; o.x = pk2(s[0 * 33], s[1 * 33]); o.y = pk2(s[2 * 33], s[3 * 33]); o.z = pk2(s[4 * 33], s[5 * 33]); o.w = pk2(s[6 * 33], s[7 * 33]);
;         *(GAS v4u*)(WT + (size_t)(n0 + n) * K + k0 + 8 * c) = o; }
;     LDS_WAIT(); asm volatile("" ::: "memory");
; }
	s_add_i32 s24, s23, 64
	s_lshl_b32 s20, s24, 7
	s_cmp_lt_u32 s24, 40
	s_cselect_b32 s21, 0, 0x830
	s_cmp_lt_u32 s24, 72
	s_cselect_b32 s21, s21, 0xfffff030
	s_add_i32 s20, s20, s21
	s_lshl_b32 s20, s20, 2
	s_add_u32 s8, s46, s20
	s_addc_u32 s9, s47, 0
	global_load_dwordx4 v[144:147], v76, s[8:9]
	s_add_u32 s8, s8, 0x16280
	s_addc_u32 s9, s9, 0
	global_load_dwordx4 v[148:151], v76, s[8:9]
	s_add_u32 s8, s8, 0x16280
	s_addc_u32 s9, s9, 0
	global_load_dwordx4 v[152:155], v76, s[8:9]
	s_add_u32 s8, s8, 0x16280
	s_addc_u32 s9, s9, 0
	global_load_dwordx4 v[156:159], v76, s[8:9]
	s_add_u32 s8, s8, 0x16280
	s_addc_u32 s9, s9, 0
	global_load_dwordx4 v[160:163], v76, s[8:9]
	s_add_u32 s8, s8, 0x16280
	s_addc_u32 s9, s9, 0
	global_load_dwordx4 v[164:167], v76, s[8:9]
	s_add_u32 s8, s8, 0x16280
	s_addc_u32 s9, s9, 0
	global_load_dwordx4 v[168:171], v76, s[8:9]
	s_add_u32 s8, s8, 0x16280
	s_addc_u32 s9, s9, 0
	global_load_dwordx4 v[172:175], v76, s[8:9]
	s_add_i32 s24, s23, 48
	s_mul_i32 s20, s24, 0x100000
	s_add_u32 s6, s48, s20
	s_addc_u32 s7, s49, 0
	s_cmp_lt_u32 s24, 16
	s_cselect_b32 s20, 1, 0
	s_sub_i32 s21, s24, 16
	s_bitcmp0_b32 s21, 2
	s_cselect_b32 s21, 1, 0
	s_cmp_lt_u32 s24, 40
	s_cselect_b32 s21, s21, 0
	s_or_b32 s20, s20, s21
	s_cmp_lg_u32 s20, 0
	s_cselect_b64 s[20:21], -1, 0
	v_cndmask_b32_e64 v91, v83, v87, s[20:21]
	v_cndmask_b32_e64 v92, v84, v88, s[20:21]
	v_cndmask_b32_e64 v93, v85, v89, s[20:21]
	v_cndmask_b32_e64 v94, v86, v90, s[20:21]
	ds_read_b32 v226, v112
	ds_read_b32 v227, v112 offset:512
	ds_read_b32 v228, v112 offset:1024
	ds_read_b32 v229, v112 offset:1536
	ds_read_b32 v230, v112 offset:2048
	ds_read_b32 v231, v112 offset:2560
	ds_read_b32 v232, v112 offset:3072
	ds_read_b32 v233, v112 offset:3584
	s_waitcnt lgkmcnt(0)
	v_bfe_u32 v120, v226, 16, 1
	v_bfe_u32 v121, v227, 16, 1
	v_bfe_u32 v122, v228, 16, 1
	v_bfe_u32 v123, v229, 16, 1
	v_bfe_u32 v124, v230, 16, 1
	v_bfe_u32 v125, v231, 16, 1
	v_bfe_u32 v126, v232, 16, 1
	v_bfe_u32 v127, v233, 16, 1
	v_add3_u32 v226, v226, v120, s63
	v_add3_u32 v227, v227, v121, s63
	v_add3_u32 v228, v228, v122, s63
	v_add3_u32 v229, v229, v123, s63
	v_add3_u32 v230, v230, v124, s63
	v_add3_u32 v231, v231, v125, s63
	v_add3_u32 v232, v232, v126, s63
	v_add3_u32 v233, v233, v127, s63
	v_perm_b32 v242, v227, v226, s64
	v_perm_b32 v243, v229, v228, s64
	v_perm_b32 v244, v231, v230, s64
	v_perm_b32 v245, v233, v232, s64
	s_nop 0
	global_store_dwordx4 v91, v[242:245], s[6:7]
	ds_read_b32 v226, v114
	ds_read_b32 v227, v114 offset:512
	ds_read_b32 v228, v114 offset:1024
	ds_read_b32 v229, v114 offset:1536
	ds_read_b32 v230, v114 offset:2048
	ds_read_b32 v231, v114 offset:2560
	ds_read_b32 v232, v114 offset:3072
	ds_read_b32 v233, v114 offset:3584
	s_waitcnt lgkmcnt(0)
	v_bfe_u32 v120, v226, 16, 1
	v_bfe_u32 v121, v227, 16, 1
	v_bfe_u32 v122, v228, 16, 1
	v_bfe_u32 v123, v229, 16, 1
	v_bfe_u32 v124, v230, 16, 1
	v_bfe_u32 v125, v231, 16, 1
	v_bfe_u32 v126, v232, 16, 1
	v_bfe_u32 v127, v233, 16, 1
	v_add3_u32 v226, v226, v120, s63
	v_add3_u32 v227, v227, v121, s63
	v_add3_u32 v228, v228, v122, s63
	v_add3_u32 v229, v229, v123, s63
	v_add3_u32 v230, v230, v124, s63
	v_add3_u32 v231, v231, v125, s63
	v_add3_u32 v232, v232, v126, s63
	v_add3_u32 v233, v233, v127, s63
	v_perm_b32 v242, v227, v226, s64
	v_perm_b32 v243, v229, v228, s64
	v_perm_b32 v244, v231, v230, s64
	v_perm_b32 v245, v233, v232, s64
	s_nop 0
	global_store_dwordx4 v92, v[242:245], s[6:7]
	ds_read_b32 v226, v116
	ds_read_b32 v227, v116 offset:512
	ds_read_b32 v228, v116 offset:1024
	ds_read_b32 v229, v116 offset:1536
	ds_read_b32 v230, v116 offset:2048
	ds_read_b32 v231, v116 offset:2560
	ds_read_b32 v232, v116 offset:3072
	ds_read_b32 v233, v116 offset:3584
	s_waitcnt lgkmcnt(0)
	v_bfe_u32 v120, v226, 16, 1
	v_bfe_u32 v121, v227, 16, 1
	v_bfe_u32 v122, v228, 16, 1
	v_bfe_u32 v123, v229, 16, 1
	v_bfe_u32 v124, v230, 16, 1
	v_bfe_u32 v125, v231, 16, 1
	v_bfe_u32 v126, v232, 16, 1
	v_bfe_u32 v127, v233, 16, 1
	v_add3_u32 v226, v226, v120, s63
	v_add3_u32 v227, v227, v121, s63
	v_add3_u32 v228, v228, v122, s63
	v_add3_u32 v229, v229, v123, s63
	v_add3_u32 v230, v230, v124, s63
	v_add3_u32 v231, v231, v125, s63
	v_add3_u32 v232, v232, v126, s63
	v_add3_u32 v233, v233, v127, s63
	v_perm_b32 v242, v227, v226, s64
	v_perm_b32 v243, v229, v228, s64
	v_perm_b32 v244, v231, v230, s64
	v_perm_b32 v245, v233, v232, s64
	s_nop 0
	global_store_dwordx4 v93, v[242:245], s[6:7]
	ds_read_b32 v226, v118
	ds_read_b32 v227, v118 offset:512
	ds_read_b32 v228, v118 offset:1024
	ds_read_b32 v229, v118 offset:1536
	ds_read_b32 v230, v118 offset:2048
	ds_read_b32 v231, v118 offset:2560
	ds_read_b32 v232, v118 offset:3072
	ds_read_b32 v233, v118 offset:3584
	s_waitcnt lgkmcnt(0)
	v_bfe_u32 v120, v226, 16, 1
	v_bfe_u32 v121, v227, 16, 1
	v_bfe_u32 v122, v228, 16, 1
	v_bfe_u32 v123, v229, 16, 1
	v_bfe_u32 v124, v230, 16, 1
	v_bfe_u32 v125, v231, 16, 1
	v_bfe_u32 v126, v232, 16, 1
	v_bfe_u32 v127, v233, 16, 1
	v_add3_u32 v226, v226, v120, s63
	v_add3_u32 v227, v227, v121, s63
	v_add3_u32 v228, v228, v122, s63
	v_add3_u32 v229, v229, v123, s63
	v_add3_u32 v230, v230, v124, s63
	v_add3_u32 v231, v231, v125, s63
	v_add3_u32 v232, v232, v126, s63
	v_add3_u32 v233, v233, v127, s63
	v_perm_b32 v242, v227, v226, s64
	v_perm_b32 v243, v229, v228, s64
	v_perm_b32 v244, v231, v230, s64
	v_perm_b32 v245, v233, v232, s64
	s_nop 0
	global_store_dwordx4 v94, v[242:245], s[6:7]
	s_waitcnt vmcnt(16)
	v_mul_f32_e32 v176, v42, v176
	v_mul_f32_e32 v177, v42, v177
	v_mul_f32_e32 v178, v42, v178
	v_mul_f32_e32 v179, v42, v179
	ds_write_b128 v210, v[176:179]
	v_mul_f32_e32 v180, v43, v180
	v_mul_f32_e32 v181, v43, v181
	v_mul_f32_e32 v182, v43, v182
	v_mul_f32_e32 v183, v43, v183
	ds_write_b128 v210, v[180:183] offset:1024
	v_mul_f32_e32 v184, v44, v184
	v_mul_f32_e32 v185, v44, v185
	v_mul_f32_e32 v186, v44, v186
	v_mul_f32_e32 v187, v44, v187
	ds_write_b128 v210, v[184:187] offset:2048
	v_mul_f32_e32 v188, v45, v188
	v_mul_f32_e32 v189, v45, v189
	v_mul_f32_e32 v190, v45, v190
	v_mul_f32_e32 v191, v45, v191
	ds_write_b128 v210, v[188:191] offset:3072
	v_mul_f32_e32 v192, v46, v192
	v_mul_f32_e32 v193, v46, v193
	v_mul_f32_e32 v194, v46, v194
	v_mul_f32_e32 v195, v46, v195
	ds_write_b128 v210, v[192:195] offset:4096
	v_mul_f32_e32 v196, v47, v196
	v_mul_f32_e32 v197, v47, v197
	v_mul_f32_e32 v198, v47, v198
	v_mul_f32_e32 v199, v47, v199
	ds_write_b128 v210, v[196:199] offset:5120
	v_mul_f32_e32 v200, v48, v200
	v_mul_f32_e32 v201, v48, v201
	v_mul_f32_e32 v202, v48, v202
	v_mul_f32_e32 v203, v48, v203
	ds_write_b128 v210, v[200:203] offset:6144
	v_mul_f32_e32 v204, v49, v204
	v_mul_f32_e32 v205, v49, v205
	v_mul_f32_e32 v206, v49, v206
	v_mul_f32_e32 v207, v49, v207
	ds_write_b128 v210, v[204:207] offset:7168
	s_waitcnt lgkmcnt(0)
	s_barrier
; #define GAS __attribute__((address_space(1)))
; #define LAS __attribute__((address_space(3)))
; #define LDS_WAIT() asm volatile("s_waitcnt lgkmcnt(0)" ::: "memory")
; __device__ __forceinline__ unsigned pk2(float lo, float hi) { return f2bf(lo) | (f2bf(hi) << 16); }
; __device__ __forceinline__ int src_col_in(int c) {
;     if (c < 5120) { const int blk = c >> 7, p = c & 127; const bool rope = blk < 16 || ((((blk - 16) >> 2) & 1) == 0); const int d = rope ? (p >> 1) + 64 * (p & 1) : p; return blk * 128 + d; }
;     if (c < OFF_Z) return c + 2096;
;     if (c < OFF_G) return c - 4048;
;     if (c < OFF_DT) return 5120 + (c - OFF_G);
;     if (c < NSRC) return c;
;     return -1;
; }
; __device__ __forceinline__ int nat_dim(int p) { return (p >> 1) + 64 * (p & 1); }
; template <int MAP, bool KS, bool KPERM = false>
; __device__ __forceinline__ void p0_transpose_item(const float* W, int K, int Nsrc, int nblk, bf16* WT, const float* ksA, const float* ksB, int ksplit, LAS float* scr, int item, int lane) {
;     const int kb = item / nblk, nb = item % nblk, k0 = 64 * kb, n0 = 32 * nb;
;     const int nr = n0 + (lane & 31); const int sc = MAP == 1 ? src_col_in(nr) : (MAP == 2 ? nat_dim(nr) : nr);
;     float v[32];
; #pragma unroll
;     for (int i = 0; i < 32; ++i) { const int k = k0 + 2 * i + (lane >> 5); const int ksrc = KPERM ? ((k & ~127) + nat_dim(k & 127)) : k;
;         v[i] = sc >= 0 ? W[(size_t)ksrc * Nsrc + sc] : 0.f; }
; #pragma unroll
;     for (int i = 0; i < 32; ++i) { const int kk = 2 * i + (lane >> 5); const int k = k0 + kk;
;         if (KS) v[i] *= (k < ksplit ? ksA[k] : ksB[k - ksplit]);
;         scr[kk * 33 + (lane & 31)] = v[i]; }
;     LDS_WAIT(); asm volatile("" ::: "memory");
;     const int c = lane & 7;
; #pragma unroll
;     for (int j = 0; j < 4; ++j) { const int n = (lane >> 3) + 8 * j; const LAS float* s = scr + (8 * c) * 33 + n;
;         v4u o; o.x = pk2(s[0 * 33], s[1 * 33]); o.y = pk2(s[2 * 33], s[3 * 33]); o.z = pk2(s[4 * 33], s[5 * 33]); o.w = pk2(s[6 * 33], s[7 * 33]);
;         *(GAS v4u*)(WT + (size_t)(n0 + n) * K + k0 + 8 * c) = o; }
;     LDS_WAIT(); asm volatile("" ::: "memory");
; }
	s_add_i32 s24, s23, 72
	s_lshl_b32 s20, s24, 7
	s_cmp_lt_u32 s24, 40
	s_cselect_b32 s21, 0, 0x830
	s_cmp_lt_u32 s24, 72
	s_cselect_b32 s21, s21, 0xfffff030
	s_add_i32 s20, s20, s21
	s_lshl_b32 s20, s20, 2
	s_add_u32 s8, s46, s20
	s_addc_u32 s9, s47, 0
	global_load_dwordx4 v[176:179], v76, s[8:9]
	s_add_u32 s8, s8, 0x16280
	s_addc_u32 s9, s9, 0
	global_load_dwordx4 v[180:183], v76, s[8:9]
	s_add_u32 s8, s8, 0x16280
	s_addc_u32 s9, s9, 0
	global_load_dwordx4 v[184:187], v76, s[8:9]
	s_add_u32 s8, s8, 0x16280
	s_addc_u32 s9, s9, 0
	global_load_dwordx4 v[188:191], v76, s[8:9]
	s_add_u32 s8, s8, 0x16280
	s_addc_u32 s9, s9, 0
	global_load_dwordx4 v[192:195], v76, s[8:9]
	s_add_u32 s8, s8, 0x16280
	s_addc_u32 s9, s9, 0
	global_load_dwordx4 v[196:199], v76, s[8:9]
	s_add_u32 s8, s8, 0x16280
	s_addc_u32 s9, s9, 0
	global_load_dwordx4 v[200:203], v76, s[8:9]
	s_add_u32 s8, s8, 0x16280
	s_addc_u32 s9, s9, 0
	global_load_dwordx4 v[204:207], v76, s[8:9]
	s_add_i32 s24, s23, 56
	s_mul_i32 s20, s24, 0x100000
	s_add_u32 s6, s48, s20
	s_addc_u32 s7, s49, 0
	s_cmp_lt_u32 s24, 16
	s_cselect_b32 s20, 1, 0
	s_sub_i32 s21, s24, 16
	s_bitcmp0_b32 s21, 2
	s_cselect_b32 s21, 1, 0
	s_cmp_lt_u32 s24, 40
	s_cselect_b32 s21, s21, 0
	s_or_b32 s20, s20, s21
	s_cmp_lg_u32 s20, 0
	s_cselect_b64 s[20:21], -1, 0
	v_cndmask_b32_e64 v91, v83, v87, s[20:21]
	v_cndmask_b32_e64 v92, v84, v88, s[20:21]
	v_cndmask_b32_e64 v93, v85, v89, s[20:21]
	v_cndmask_b32_e64 v94, v86, v90, s[20:21]
	ds_read_b32 v226, v113
	ds_read_b32 v227, v113 offset:512
	ds_read_b32 v228, v113 offset:1024
	ds_read_b32 v229, v113 offset:1536
	ds_read_b32 v230, v113 offset:2048
	ds_read_b32 v231, v113 offset:2560
	ds_read_b32 v232, v113 offset:3072
	ds_read_b32 v233, v113 offset:3584
	s_waitcnt lgkmcnt(0)
	v_bfe_u32 v120, v226, 16, 1
	v_bfe_u32 v121, v227, 16, 1
	v_bfe_u32 v122, v228, 16, 1
	v_bfe_u32 v123, v229, 16, 1
	v_bfe_u32 v124, v230, 16, 1
	v_bfe_u32 v125, v231, 16, 1
	v_bfe_u32 v126, v232, 16, 1
	v_bfe_u32 v127, v233, 16, 1
	v_add3_u32 v226, v226, v120, s63
	v_add3_u32 v227, v227, v121, s63
	v_add3_u32 v228, v228, v122, s63
	v_add3_u32 v229, v229, v123, s63
	v_add3_u32 v230, v230, v124, s63
	v_add3_u32 v231, v231, v125, s63
	v_add3_u32 v232, v232, v126, s63
	v_add3_u32 v233, v233, v127, s63
	v_perm_b32 v242, v227, v226, s64
	v_perm_b32 v243, v229, v228, s64
	v_perm_b32 v244, v231, v230, s64
	v_perm_b32 v245, v233, v232, s64
	s_nop 0
	global_store_dwordx4 v91, v[242:245], s[6:7]
	ds_read_b32 v226, v115
	ds_read_b32 v227, v115 offset:512
	ds_read_b32 v228, v115 offset:1024
	ds_read_b32 v229, v115 offset:1536
	ds_read_b32 v230, v115 offset:2048
	ds_read_b32 v231, v115 offset:2560
	ds_read_b32 v232, v115 offset:3072
	ds_read_b32 v233, v115 offset:3584
	s_waitcnt lgkmcnt(0)
	v_bfe_u32 v120, v226, 16, 1
	v_bfe_u32 v121, v227, 16, 1
	v_bfe_u32 v122, v228, 16, 1
	v_bfe_u32 v123, v229, 16, 1
	v_bfe_u32 v124, v230, 16, 1
	v_bfe_u32 v125, v231, 16, 1
	v_bfe_u32 v126, v232, 16, 1
	v_bfe_u32 v127, v233, 16, 1
	v_add3_u32 v226, v226, v120, s63
	v_add3_u32 v227, v227, v121, s63
	v_add3_u32 v228, v228, v122, s63
	v_add3_u32 v229, v229, v123, s63
	v_add3_u32 v230, v230, v124, s63
	v_add3_u32 v231, v231, v125, s63
	v_add3_u32 v232, v232, v126, s63
	v_add3_u32 v233, v233, v127, s63
	v_perm_b32 v242, v227, v226, s64
	v_perm_b32 v243, v229, v228, s64
	v_perm_b32 v244, v231, v230, s64
	v_perm_b32 v245, v233, v232, s64
	s_nop 0
	global_store_dwordx4 v92, v[242:245], s[6:7]
	ds_read_b32 v226, v117
	ds_read_b32 v227, v117 offset:512
	ds_read_b32 v228, v117 offset:1024
	ds_read_b32 v229, v117 offset:1536
	ds_read_b32 v230, v117 offset:2048
	ds_read_b32 v231, v117 offset:2560
	ds_read_b32 v232, v117 offset:3072
	ds_read_b32 v233, v117 offset:3584
	s_waitcnt lgkmcnt(0)
	v_bfe_u32 v120, v226, 16, 1
	v_bfe_u32 v121, v227, 16, 1
	v_bfe_u32 v122, v228, 16, 1
	v_bfe_u32 v123, v229, 16, 1
	v_bfe_u32 v124, v230, 16, 1
	v_bfe_u32 v125, v231, 16, 1
	v_bfe_u32 v126, v232, 16, 1
	v_bfe_u32 v127, v233, 16, 1
	v_add3_u32 v226, v226, v120, s63
	v_add3_u32 v227, v227, v121, s63
	v_add3_u32 v228, v228, v122, s63
	v_add3_u32 v229, v229, v123, s63
	v_add3_u32 v230, v230, v124, s63
	v_add3_u32 v231, v231, v125, s63
	v_add3_u32 v232, v232, v126, s63
	v_add3_u32 v233, v233, v127, s63
	v_perm_b32 v242, v227, v226, s64
	v_perm_b32 v243, v229, v228, s64
	v_perm_b32 v244, v231, v230, s64
	v_perm_b32 v245, v233, v232, s64
	s_nop 0
	global_store_dwordx4 v93, v[242:245], s[6:7]
	ds_read_b32 v226, v119
	ds_read_b32 v227, v119 offset:512
	ds_read_b32 v228, v119 offset:1024
	ds_read_b32 v229, v119 offset:1536
	ds_read_b32 v230, v119 offset:2048
	ds_read_b32 v231, v119 offset:2560
	ds_read_b32 v232, v119 offset:3072
	ds_read_b32 v233, v119 offset:3584
	s_waitcnt lgkmcnt(0)
	v_bfe_u32 v120, v226, 16, 1
	v_bfe_u32 v121, v227, 16, 1
	v_bfe_u32 v122, v228, 16, 1
	v_bfe_u32 v123, v229, 16, 1
	v_bfe_u32 v124, v230, 16, 1
	v_bfe_u32 v125, v231, 16, 1
	v_bfe_u32 v126, v232, 16, 1
	v_bfe_u32 v127, v233, 16, 1
	v_add3_u32 v226, v226, v120, s63
	v_add3_u32 v227, v227, v121, s63
	v_add3_u32 v228, v228, v122, s63
	v_add3_u32 v229, v229, v123, s63
	v_add3_u32 v230, v230, v124, s63
	v_add3_u32 v231, v231, v125, s63
	v_add3_u32 v232, v232, v126, s63
	v_add3_u32 v233, v233, v127, s63
	v_perm_b32 v242, v227, v226, s64
	v_perm_b32 v243, v229, v228, s64
	v_perm_b32 v244, v231, v230, s64
	v_perm_b32 v245, v233, v232, s64
	s_nop 0
	global_store_dwordx4 v94, v[242:245], s[6:7]
	s_waitcnt vmcnt(16)
	v_mul_f32_e32 v144, v42, v144
	v_mul_f32_e32 v145, v42, v145
	v_mul_f32_e32 v146, v42, v146
	v_mul_f32_e32 v147, v42, v147
	ds_write_b128 v209, v[144:147]
	v_mul_f32_e32 v148, v43, v148
	v_mul_f32_e32 v149, v43, v149
	v_mul_f32_e32 v150, v43, v150
	v_mul_f32_e32 v151, v43, v151
	ds_write_b128 v209, v[148:151] offset:1024
	v_mul_f32_e32 v152, v44, v152
	v_mul_f32_e32 v153, v44, v153
	v_mul_f32_e32 v154, v44, v154
	v_mul_f32_e32 v155, v44, v155
	ds_write_b128 v209, v[152:155] offset:2048
	v_mul_f32_e32 v156, v45, v156
	v_mul_f32_e32 v157, v45, v157
	v_mul_f32_e32 v158, v45, v158
	v_mul_f32_e32 v159, v45, v159
	ds_write_b128 v209, v[156:159] offset:3072
	v_mul_f32_e32 v160, v46, v160
	v_mul_f32_e32 v161, v46, v161
	v_mul_f32_e32 v162, v46, v162
	v_mul_f32_e32 v163, v46, v163
	ds_write_b128 v209, v[160:163] offset:4096
	v_mul_f32_e32 v164, v47, v164
	v_mul_f32_e32 v165, v47, v165
	v_mul_f32_e32 v166, v47, v166
	v_mul_f32_e32 v167, v47, v167
	ds_write_b128 v209, v[164:167] offset:5120
	v_mul_f32_e32 v168, v48, v168
	v_mul_f32_e32 v169, v48, v169
	v_mul_f32_e32 v170, v48, v170
	v_mul_f32_e32 v171, v48, v171
	ds_write_b128 v209, v[168:171] offset:6144
	v_mul_f32_e32 v172, v49, v172
	v_mul_f32_e32 v173, v49, v173
	v_mul_f32_e32 v174, v49, v174
	v_mul_f32_e32 v175, v49, v175
	ds_write_b128 v209, v[172:175] offset:7168
	s_waitcnt lgkmcnt(0)
	s_barrier
; #define GAS __attribute__((address_space(1)))
; #define LAS __attribute__((address_space(3)))
; #define LDS_WAIT() asm volatile("s_waitcnt lgkmcnt(0)" ::: "memory")
; __device__ __forceinline__ unsigned pk2(float lo, float hi) { return f2bf(lo) | (f2bf(hi) << 16); }
; __device__ __forceinline__ int src_col_in(int c) {
;     if (c < 5120) { const int blk = c >> 7, p = c & 127; const bool rope = blk < 16 || ((((blk - 16) >> 2) & 1) == 0); const int d = rope ? (p >> 1) + 64 * (p & 1) : p; return blk * 128 + d; }
;     if (c < OFF_Z) return c + 2096;
;     if (c < OFF_G) return c - 4048;
;     if (c < OFF_DT) return 5120 + (c - OFF_G);
;     if (c < NSRC) return c;
;     return -1;
; }
; __device__ __forceinline__ int nat_dim(int p) { return (p >> 1) + 64 * (p & 1); }
; template <int MAP, bool KS, bool KPERM = false>
; __device__ __forceinline__ void p0_transpose_item(const float* W, int K, int Nsrc, int nblk, bf16* WT, const float* ksA, const float* ksB, int ksplit, LAS float* scr, int item, int lane) {
;     const int kb = item / nblk, nb = item % nblk, k0 = 64 * kb, n0 = 32 * nb;
;     const int nr = n0 + (lane & 31); const int sc = MAP == 1 ? src_col_in(nr) : (MAP == 2 ? nat_dim(nr) : nr);
;     float v[32];
; #pragma unroll
;     for (int i = 0; i < 32; ++i) { const int k = k0 + 2 * i + (lane >> 5); const int ksrc = KPERM ? ((k & ~127) + nat_dim(k & 127)) : k;
;         v[i] = sc >= 0 ? W[(size_t)ksrc * Nsrc + sc] : 0.f; }
; #pragma unroll
;     for (int i = 0; i < 32; ++i) { const int kk = 2 * i + (lane >> 5); const int k = k0 + kk;
;         if (KS) v[i] *= (k < ksplit ? ksA[k] : ksB[k - ksplit]);
;         scr[kk * 33 + (lane & 31)] = v[i]; }
;     LDS_WAIT(); asm volatile("" ::: "memory");
;     const int c = lane & 7;
; #pragma unroll
;     for (int j = 0; j < 4; ++j) { const int n = (lane >> 3) + 8 * j; const LAS float* s = scr + (8 * c) * 33 + n;
;         v4u o; o.x = pk2(s[0 * 33], s[1 * 33]); o.y = pk2(s[2 * 33], s[3 * 33]); o.z = pk2(s[4 * 33], s[5 * 33]); o.w = pk2(s[6 * 33], s[7 * 33]);
;         *(GAS v4u*)(WT + (size_t)(n0 + n) * K + k0 + 8 * c) = o; }
;     LDS_WAIT(); asm volatile("" ::: "memory");
; }
	s_add_i32 s24, s23, 80
	s_lshl_b32 s20, s24, 7
	s_cmp_lt_u32 s24, 40
	s_cselect_b32 s21, 0, 0x830
	s_cmp_lt_u32 s24, 72
	s_cselect_b32 s21, s21, 0xfffff030
	s_add_i32 s20, s20, s21
	s_lshl_b32 s20, s20, 2
	s_add_u32 s8, s46, s20
	s_addc_u32 s9, s47, 0
	global_load_dwordx4 v[144:147], v76, s[8:9]
	s_add_u32 s8, s8, 0x16280
	s_addc_u32 s9, s9, 0
	global_load_dwordx4 v[148:151], v76, s[8:9]
	s_add_u32 s8, s8, 0x16280
	s_addc_u32 s9, s9, 0
	global_load_dwordx4 v[152:155], v76, s[8:9]
	s_add_u32 s8, s8, 0x16280
	s_addc_u32 s9, s9, 0
	global_load_dwordx4 v[156:159], v76, s[8:9]
	s_add_u32 s8, s8, 0x16280
	s_addc_u32 s9, s9, 0
	global_load_dwordx4 v[160:163], v76, s[8:9]
	s_add_u32 s8, s8, 0x16280
	s_addc_u32 s9, s9, 0
	global_load_dwordx4 v[164:167], v76, s[8:9]
	s_add_u32 s8, s8, 0x16280
	s_addc_u32 s9, s9, 0
	global_load_dwordx4 v[168:171], v76, s[8:9]
	s_add_u32 s8, s8, 0x16280
	s_addc_u32 s9, s9, 0
	global_load_dwordx4 v[172:175], v76, s[8:9]
	s_add_i32 s24, s23, 64
	s_mul_i32 s20, s24, 0x100000
	s_add_u32 s6, s48, s20
	s_addc_u32 s7, s49, 0
	s_cmp_lt_u32 s24, 16
	s_cselect_b32 s20, 1, 0
	s_sub_i32 s21, s24, 16
	s_bitcmp0_b32 s21, 2
	s_cselect_b32 s21, 1, 0
	s_cmp_lt_u32 s24, 40
	s_cselect_b32 s21, s21, 0
	s_or_b32 s20, s20, s21
	s_cmp_lg_u32 s20, 0
	s_cselect_b64 s[20:21], -1, 0
	v_cndmask_b32_e64 v91, v83, v87, s[20:21]
	v_cndmask_b32_e64 v92, v84, v88, s[20:21]
	v_cndmask_b32_e64 v93, v85, v89, s[20:21]
	v_cndmask_b32_e64 v94, v86, v90, s[20:21]
	ds_read_b32 v226, v112
	ds_read_b32 v227, v112 offset:512
	ds_read_b32 v228, v112 offset:1024
	ds_read_b32 v229, v112 offset:1536
	ds_read_b32 v230, v112 offset:2048
	ds_read_b32 v231, v112 offset:2560
	ds_read_b32 v232, v112 offset:3072
	ds_read_b32 v233, v112 offset:3584
	s_waitcnt lgkmcnt(0)
	v_bfe_u32 v120, v226, 16, 1
	v_bfe_u32 v121, v227, 16, 1
	v_bfe_u32 v122, v228, 16, 1
	v_bfe_u32 v123, v229, 16, 1
	v_bfe_u32 v124, v230, 16, 1
	v_bfe_u32 v125, v231, 16, 1
	v_bfe_u32 v126, v232, 16, 1
	v_bfe_u32 v127, v233, 16, 1
	v_add3_u32 v226, v226, v120, s63
	v_add3_u32 v227, v227, v121, s63
	v_add3_u32 v228, v228, v122, s63
	v_add3_u32 v229, v229, v123, s63
	v_add3_u32 v230, v230, v124, s63
	v_add3_u32 v231, v231, v125, s63
	v_add3_u32 v232, v232, v126, s63
	v_add3_u32 v233, v233, v127, s63
	v_perm_b32 v242, v227, v226, s64
	v_perm_b32 v243, v229, v228, s64
	v_perm_b32 v244, v231, v230, s64
	v_perm_b32 v245, v233, v232, s64
	s_nop 0
	global_store_dwordx4 v91, v[242:245], s[6:7]
	ds_read_b32 v226, v114
	ds_read_b32 v227, v114 offset:512
	ds_read_b32 v228, v114 offset:1024
	ds_read_b32 v229, v114 offset:1536
	ds_read_b32 v230, v114 offset:2048
	ds_read_b32 v231, v114 offset:2560
	ds_read_b32 v232, v114 offset:3072
	ds_read_b32 v233, v114 offset:3584
	s_waitcnt lgkmcnt(0)
	v_bfe_u32 v120, v226, 16, 1
	v_bfe_u32 v121, v227, 16, 1
	v_bfe_u32 v122, v228, 16, 1
	v_bfe_u32 v123, v229, 16, 1
	v_bfe_u32 v124, v230, 16, 1
	v_bfe_u32 v125, v231, 16, 1
	v_bfe_u32 v126, v232, 16, 1
	v_bfe_u32 v127, v233, 16, 1
	v_add3_u32 v226, v226, v120, s63
	v_add3_u32 v227, v227, v121, s63
	v_add3_u32 v228, v228, v122, s63
	v_add3_u32 v229, v229, v123, s63
	v_add3_u32 v230, v230, v124, s63
	v_add3_u32 v231, v231, v125, s63
	v_add3_u32 v232, v232, v126, s63
	v_add3_u32 v233, v233, v127, s63
	v_perm_b32 v242, v227, v226, s64
	v_perm_b32 v243, v229, v228, s64
	v_perm_b32 v244, v231, v230, s64
	v_perm_b32 v245, v233, v232, s64
	s_nop 0
	global_store_dwordx4 v92, v[242:245], s[6:7]
	ds_read_b32 v226, v116
	ds_read_b32 v227, v116 offset:512
	ds_read_b32 v228, v116 offset:1024
	ds_read_b32 v229, v116 offset:1536
	ds_read_b32 v230, v116 offset:2048
	ds_read_b32 v231, v116 offset:2560
	ds_read_b32 v232, v116 offset:3072
	ds_read_b32 v233, v116 offset:3584
	s_waitcnt lgkmcnt(0)
	v_bfe_u32 v120, v226, 16, 1
	v_bfe_u32 v121, v227, 16, 1
	v_bfe_u32 v122, v228, 16, 1
	v_bfe_u32 v123, v229, 16, 1
	v_bfe_u32 v124, v230, 16, 1
	v_bfe_u32 v125, v231, 16, 1
	v_bfe_u32 v126, v232, 16, 1
	v_bfe_u32 v127, v233, 16, 1
	v_add3_u32 v226, v226, v120, s63
	v_add3_u32 v227, v227, v121, s63
	v_add3_u32 v228, v228, v122, s63
	v_add3_u32 v229, v229, v123, s63
	v_add3_u32 v230, v230, v124, s63
	v_add3_u32 v231, v231, v125, s63
	v_add3_u32 v232, v232, v126, s63
	v_add3_u32 v233, v233, v127, s63
	v_perm_b32 v242, v227, v226, s64
	v_perm_b32 v243, v229, v228, s64
	v_perm_b32 v244, v231, v230, s64
	v_perm_b32 v245, v233, v232, s64
	s_nop 0
	global_store_dwordx4 v93, v[242:245], s[6:7]
	ds_read_b32 v226, v118
	ds_read_b32 v227, v118 offset:512
	ds_read_b32 v228, v118 offset:1024
	ds_read_b32 v229, v118 offset:1536
	ds_read_b32 v230, v118 offset:2048
	ds_read_b32 v231, v118 offset:2560
	ds_read_b32 v232, v118 offset:3072
	ds_read_b32 v233, v118 offset:3584
	s_waitcnt lgkmcnt(0)
	v_bfe_u32 v120, v226, 16, 1
	v_bfe_u32 v121, v227, 16, 1
	v_bfe_u32 v122, v228, 16, 1
	v_bfe_u32 v123, v229, 16, 1
	v_bfe_u32 v124, v230, 16, 1
	v_bfe_u32 v125, v231, 16, 1
	v_bfe_u32 v126, v232, 16, 1
	v_bfe_u32 v127, v233, 16, 1
	v_add3_u32 v226, v226, v120, s63
	v_add3_u32 v227, v227, v121, s63
	v_add3_u32 v228, v228, v122, s63
	v_add3_u32 v229, v229, v123, s63
	v_add3_u32 v230, v230, v124, s63
	v_add3_u32 v231, v231, v125, s63
	v_add3_u32 v232, v232, v126, s63
	v_add3_u32 v233, v233, v127, s63
	v_perm_b32 v242, v227, v226, s64
	v_perm_b32 v243, v229, v228, s64
	v_perm_b32 v244, v231, v230, s64
	v_perm_b32 v245, v233, v232, s64
	s_nop 0
	global_store_dwordx4 v94, v[242:245], s[6:7]
	s_waitcnt vmcnt(16)
	v_mul_f32_e32 v176, v42, v176
	v_mul_f32_e32 v177, v42, v177
	v_mul_f32_e32 v178, v42, v178
	v_mul_f32_e32 v179, v42, v179
	ds_write_b128 v210, v[176:179]
	v_mul_f32_e32 v180, v43, v180
	v_mul_f32_e32 v181, v43, v181
	v_mul_f32_e32 v182, v43, v182
	v_mul_f32_e32 v183, v43, v183
	ds_write_b128 v210, v[180:183] offset:1024
	v_mul_f32_e32 v184, v44, v184
	v_mul_f32_e32 v185, v44, v185
	v_mul_f32_e32 v186, v44, v186
	v_mul_f32_e32 v187, v44, v187
	ds_write_b128 v210, v[184:187] offset:2048
	v_mul_f32_e32 v188, v45, v188
	v_mul_f32_e32 v189, v45, v189
	v_mul_f32_e32 v190, v45, v190
	v_mul_f32_e32 v191, v45, v191
	ds_write_b128 v210, v[188:191] offset:3072
	v_mul_f32_e32 v192, v46, v192
	v_mul_f32_e32 v193, v46, v193
	v_mul_f32_e32 v194, v46, v194
	v_mul_f32_e32 v195, v46, v195
	ds_write_b128 v210, v[192:195] offset:4096
	v_mul_f32_e32 v196, v47, v196
	v_mul_f32_e32 v197, v47, v197
	v_mul_f32_e32 v198, v47, v198
	v_mul_f32_e32 v199, v47, v199
	ds_write_b128 v210, v[196:199] offset:5120
	v_mul_f32_e32 v200, v48, v200
	v_mul_f32_e32 v201, v48, v201
	v_mul_f32_e32 v202, v48, v202
	v_mul_f32_e32 v203, v48, v203
	ds_write_b128 v210, v[200:203] offset:6144
	v_mul_f32_e32 v204, v49, v204
	v_mul_f32_e32 v205, v49, v205
	v_mul_f32_e32 v206, v49, v206
	v_mul_f32_e32 v207, v49, v207
	ds_write_b128 v210, v[204:207] offset:7168
	s_waitcnt lgkmcnt(0)
	s_barrier
; #define GAS __attribute__((address_space(1)))
; #define LAS __attribute__((address_space(3)))
; #define LDS_WAIT() asm volatile("s_waitcnt lgkmcnt(0)" ::: "memory")
; __device__ __forceinline__ unsigned pk2(float lo, float hi) { return f2bf(lo) | (f2bf(hi) << 16); }
; __device__ __forceinline__ int src_col_in(int c) {
;     if (c < 5120) { const int blk = c >> 7, p = c & 127; const bool rope = blk < 16 || ((((blk - 16) >> 2) & 1) == 0); const int d = rope ? (p >> 1) + 64 * (p & 1) : p; return blk * 128 + d; }
;     if (c < OFF_Z) return c + 2096;
;     if (c < OFF_G) return c - 4048;
;     if (c < OFF_DT) return 5120 + (c - OFF_G);
;     if (c < NSRC) return c;
;     return -1;
; }
; __device__ __forceinline__ int nat_dim(int p) { return (p >> 1) + 64 * (p & 1); }
; template <int MAP, bool KS, bool KPERM = false>
; __device__ __forceinline__ void p0_transpose_item(const float* W, int K, int Nsrc, int nblk, bf16* WT, const float* ksA, const float* ksB, int ksplit, LAS float* scr, int item, int lane) {
;     const int kb = item / nblk, nb = item % nblk, k0 = 64 * kb, n0 = 32 * nb;
;     const int nr = n0 + (lane & 31); const int sc = MAP == 1 ? src_col_in(nr) : (MAP == 2 ? nat_dim(nr) : nr);
;     float v[32];
; #pragma unroll
;     for (int i = 0; i < 32; ++i) { const int k = k0 + 2 * i + (lane >> 5); const int ksrc = KPERM ? ((k & ~127) + nat_dim(k & 127)) : k;
;         v[i] = sc >= 0 ? W[(size_t)ksrc * Nsrc + sc] : 0.f; }
; #pragma unroll
;     for (int i = 0; i < 32; ++i) { const int kk = 2 * i + (lane >> 5); const int k = k0 + kk;
;         if (KS) v[i] *= (k < ksplit ? ksA[k] : ksB[k - ksplit]);
;         scr[kk * 33 + (lane & 31)] = v[i]; }
;     LDS_WAIT(); asm volatile("" ::: "memory");
;     const int c = lane & 7;
; #pragma unroll
;     for (int j = 0; j < 4; ++j) { const int n = (lane >> 3) + 8 * j; const LAS float* s = scr + (8 * c) * 33 + n;
;         v4u o; o.x = pk2(s[0 * 33], s[1 * 33]); o.y = pk2(s[2 * 33], s[3 * 33]); o.z = pk2(s[4 * 33], s[5 * 33]); o.w = pk2(s[6 * 33], s[7 * 33]);
;         *(GAS v4u*)(WT + (size_t)(n0 + n) * K + k0 + 8 * c) = o; }
;     LDS_WAIT(); asm volatile("" ::: "memory");
; }
	s_add_i32 s24, s23, 0
	s_lshl_b32 s20, s24, 7
	s_cmp_lt_u32 s24, 40
	s_cselect_b32 s21, 0, 0x830
	s_cmp_lt_u32 s24, 72
	s_cselect_b32 s21, s21, 0xfffff030
	s_add_i32 s20, s20, s21
	s_lshl_b32 s20, s20, 2
	s_add_u32 s8, s50, s20
	s_addc_u32 s9, s51, 0
	global_load_dwordx4 v[176:179], v76, s[8:9]
	s_add_u32 s8, s8, 0x16280
	s_addc_u32 s9, s9, 0
	global_load_dwordx4 v[180:183], v76, s[8:9]
	s_add_u32 s8, s8, 0x16280
	s_addc_u32 s9, s9, 0
	global_load_dwordx4 v[184:187], v76, s[8:9]
	s_add_u32 s8, s8, 0x16280
	s_addc_u32 s9, s9, 0
	global_load_dwordx4 v[188:191], v76, s[8:9]
	s_add_u32 s8, s8, 0x16280
	s_addc_u32 s9, s9, 0
	global_load_dwordx4 v[192:195], v76, s[8:9]
	s_add_u32 s8, s8, 0x16280
	s_addc_u32 s9, s9, 0
	global_load_dwordx4 v[196:199], v76, s[8:9]
	s_add_u32 s8, s8, 0x16280
	s_addc_u32 s9, s9, 0
	global_load_dwordx4 v[200:203], v76, s[8:9]
	s_add_u32 s8, s8, 0x16280
	s_addc_u32 s9, s9, 0
	global_load_dwordx4 v[204:207], v76, s[8:9]
	s_add_i32 s24, s23, 72
	s_mul_i32 s20, s24, 0x100000
	s_add_u32 s6, s48, s20
	s_addc_u32 s7, s49, 0
	s_cmp_lt_u32 s24, 16
	s_cselect_b32 s20, 1, 0
	s_sub_i32 s21, s24, 16
	s_bitcmp0_b32 s21, 2
	s_cselect_b32 s21, 1, 0
	s_cmp_lt_u32 s24, 40
	s_cselect_b32 s21, s21, 0
	s_or_b32 s20, s20, s21
	s_cmp_lg_u32 s20, 0
	s_cselect_b64 s[20:21], -1, 0
	v_cndmask_b32_e64 v91, v83, v87, s[20:21]
	v_cndmask_b32_e64 v92, v84, v88, s[20:21]
	v_cndmask_b32_e64 v93, v85, v89, s[20:21]
	v_cndmask_b32_e64 v94, v86, v90, s[20:21]
	ds_read_b32 v226, v113
	ds_read_b32 v227, v113 offset:512
	ds_read_b32 v228, v113 offset:1024
	ds_read_b32 v229, v113 offset:1536
	ds_read_b32 v230, v113 offset:2048
	ds_read_b32 v231, v113 offset:2560
	ds_read_b32 v232, v113 offset:3072
	ds_read_b32 v233, v113 offset:3584
	s_waitcnt lgkmcnt(0)
	v_bfe_u32 v120, v226, 16, 1
	v_bfe_u32 v121, v227, 16, 1
	v_bfe_u32 v122, v228, 16, 1
	v_bfe_u32 v123, v229, 16, 1
	v_bfe_u32 v124, v230, 16, 1
	v_bfe_u32 v125, v231, 16, 1
	v_bfe_u32 v126, v232, 16, 1
	v_bfe_u32 v127, v233, 16, 1
	v_add3_u32 v226, v226, v120, s63
	v_add3_u32 v227, v227, v121, s63
	v_add3_u32 v228, v228, v122, s63
	v_add3_u32 v229, v229, v123, s63
	v_add3_u32 v230, v230, v124, s63
	v_add3_u32 v231, v231, v125, s63
	v_add3_u32 v232, v232, v126, s63
	v_add3_u32 v233, v233, v127, s63
	v_perm_b32 v242, v227, v226, s64
	v_perm_b32 v243, v229, v228, s64
	v_perm_b32 v244, v231, v230, s64
	v_perm_b32 v245, v233, v232, s64
	s_nop 0
	global_store_dwordx4 v91, v[242:245], s[6:7]
	ds_read_b32 v226, v115
	ds_read_b32 v227, v115 offset:512
	ds_read_b32 v228, v115 offset:1024
	ds_read_b32 v229, v115 offset:1536
	ds_read_b32 v230, v115 offset:2048
	ds_read_b32 v231, v115 offset:2560
	ds_read_b32 v232, v115 offset:3072
	ds_read_b32 v233, v115 offset:3584
	s_waitcnt lgkmcnt(0)
	v_bfe_u32 v120, v226, 16, 1
	v_bfe_u32 v121, v227, 16, 1
	v_bfe_u32 v122, v228, 16, 1
	v_bfe_u32 v123, v229, 16, 1
	v_bfe_u32 v124, v230, 16, 1
	v_bfe_u32 v125, v231, 16, 1
	v_bfe_u32 v126, v232, 16, 1
	v_bfe_u32 v127, v233, 16, 1
	v_add3_u32 v226, v226, v120, s63
	v_add3_u32 v227, v227, v121, s63
	v_add3_u32 v228, v228, v122, s63
	v_add3_u32 v229, v229, v123, s63
	v_add3_u32 v230, v230, v124, s63
	v_add3_u32 v231, v231, v125, s63
	v_add3_u32 v232, v232, v126, s63
	v_add3_u32 v233, v233, v127, s63
	v_perm_b32 v242, v227, v226, s64
	v_perm_b32 v243, v229, v228, s64
	v_perm_b32 v244, v231, v230, s64
	v_perm_b32 v245, v233, v232, s64
	s_nop 0
	global_store_dwordx4 v92, v[242:245], s[6:7]
	ds_read_b32 v226, v117
	ds_read_b32 v227, v117 offset:512
	ds_read_b32 v228, v117 offset:1024
	ds_read_b32 v229, v117 offset:1536
	ds_read_b32 v230, v117 offset:2048
	ds_read_b32 v231, v117 offset:2560
	ds_read_b32 v232, v117 offset:3072
	ds_read_b32 v233, v117 offset:3584
	s_waitcnt lgkmcnt(0)
	v_bfe_u32 v120, v226, 16, 1
	v_bfe_u32 v121, v227, 16, 1
	v_bfe_u32 v122, v228, 16, 1
	v_bfe_u32 v123, v229, 16, 1
	v_bfe_u32 v124, v230, 16, 1
	v_bfe_u32 v125, v231, 16, 1
	v_bfe_u32 v126, v232, 16, 1
	v_bfe_u32 v127, v233, 16, 1
	v_add3_u32 v226, v226, v120, s63
	v_add3_u32 v227, v227, v121, s63
	v_add3_u32 v228, v228, v122, s63
	v_add3_u32 v229, v229, v123, s63
	v_add3_u32 v230, v230, v124, s63
	v_add3_u32 v231, v231, v125, s63
	v_add3_u32 v232, v232, v126, s63
	v_add3_u32 v233, v233, v127, s63
	v_perm_b32 v242, v227, v226, s64
	v_perm_b32 v243, v229, v228, s64
	v_perm_b32 v244, v231, v230, s64
	v_perm_b32 v245, v233, v232, s64
	s_nop 0
	global_store_dwordx4 v93, v[242:245], s[6:7]
	ds_read_b32 v226, v119
	ds_read_b32 v227, v119 offset:512
	ds_read_b32 v228, v119 offset:1024
	ds_read_b32 v229, v119 offset:1536
	ds_read_b32 v230, v119 offset:2048
	ds_read_b32 v231, v119 offset:2560
	ds_read_b32 v232, v119 offset:3072
	ds_read_b32 v233, v119 offset:3584
	s_waitcnt lgkmcnt(0)
	v_bfe_u32 v120, v226, 16, 1
	v_bfe_u32 v121, v227, 16, 1
	v_bfe_u32 v122, v228, 16, 1
	v_bfe_u32 v123, v229, 16, 1
	v_bfe_u32 v124, v230, 16, 1
	v_bfe_u32 v125, v231, 16, 1
	v_bfe_u32 v126, v232, 16, 1
	v_bfe_u32 v127, v233, 16, 1
	v_add3_u32 v226, v226, v120, s63
	v_add3_u32 v227, v227, v121, s63
	v_add3_u32 v228, v228, v122, s63
	v_add3_u32 v229, v229, v123, s63
	v_add3_u32 v230, v230, v124, s63
	v_add3_u32 v231, v231, v125, s63
	v_add3_u32 v232, v232, v126, s63
	v_add3_u32 v233, v233, v127, s63
	v_perm_b32 v242, v227, v226, s64
	v_perm_b32 v243, v229, v228, s64
	v_perm_b32 v244, v231, v230, s64
	v_perm_b32 v245, v233, v232, s64
	s_nop 0
	global_store_dwordx4 v94, v[242:245], s[6:7]
	s_waitcnt vmcnt(16)
	v_mul_f32_e32 v144, v42, v144
	v_mul_f32_e32 v145, v42, v145
	v_mul_f32_e32 v146, v42, v146
	v_mul_f32_e32 v147, v42, v147
	ds_write_b128 v209, v[144:147]
	v_mul_f32_e32 v148, v43, v148
	v_mul_f32_e32 v149, v43, v149
	v_mul_f32_e32 v150, v43, v150
	v_mul_f32_e32 v151, v43, v151
	ds_write_b128 v209, v[148:151] offset:1024
	v_mul_f32_e32 v152, v44, v152
	v_mul_f32_e32 v153, v44, v153
	v_mul_f32_e32 v154, v44, v154
	v_mul_f32_e32 v155, v44, v155
	ds_write_b128 v209, v[152:155] offset:2048
	v_mul_f32_e32 v156, v45, v156
	v_mul_f32_e32 v157, v45, v157
	v_mul_f32_e32 v158, v45, v158
	v_mul_f32_e32 v159, v45, v159
	ds_write_b128 v209, v[156:159] offset:3072
	v_mul_f32_e32 v160, v46, v160
	v_mul_f32_e32 v161, v46, v161
	v_mul_f32_e32 v162, v46, v162
	v_mul_f32_e32 v163, v46, v163
	ds_write_b128 v209, v[160:163] offset:4096
	v_mul_f32_e32 v164, v47, v164
	v_mul_f32_e32 v165, v47, v165
	v_mul_f32_e32 v166, v47, v166
	v_mul_f32_e32 v167, v47, v167
	ds_write_b128 v209, v[164:167] offset:5120
	v_mul_f32_e32 v168, v48, v168
	v_mul_f32_e32 v169, v48, v169
	v_mul_f32_e32 v170, v48, v170
	v_mul_f32_e32 v171, v48, v171
	ds_write_b128 v209, v[168:171] offset:6144
	v_mul_f32_e32 v172, v49, v172
	v_mul_f32_e32 v173, v49, v173
	v_mul_f32_e32 v174, v49, v174
	v_mul_f32_e32 v175, v49, v175
	ds_write_b128 v209, v[172:175] offset:7168
	s_waitcnt lgkmcnt(0)
	s_barrier
; #define GAS __attribute__((address_space(1)))
; #define LAS __attribute__((address_space(3)))
; #define LDS_WAIT() asm volatile("s_waitcnt lgkmcnt(0)" ::: "memory")
; __device__ __forceinline__ unsigned pk2(float lo, float hi) { return f2bf(lo) | (f2bf(hi) << 16); }
; __device__ __forceinline__ int src_col_in(int c) {
;     if (c < 5120) { const int blk = c >> 7, p = c & 127; const bool rope = blk < 16 || ((((blk - 16) >> 2) & 1) == 0); const int d = rope ? (p >> 1) + 64 * (p & 1) : p; return blk * 128 + d; }
;     if (c < OFF_Z) return c + 2096;
;     if (c < OFF_G) return c - 4048;
;     if (c < OFF_DT) return 5120 + (c - OFF_G);
;     if (c < NSRC) return c;
;     return -1;
; }
; __device__ __forceinline__ int nat_dim(int p) { return (p >> 1) + 64 * (p & 1); }
; template <int MAP, bool KS, bool KPERM = false>
; __device__ __forceinline__ void p0_transpose_item(const float* W, int K, int Nsrc, int nblk, bf16* WT, const float* ksA, const float* ksB, int ksplit, LAS float* scr, int item, int lane) {
;     const int kb = item / nblk, nb = item % nblk, k0 = 64 * kb, n0 = 32 * nb;
;     const int nr = n0 + (lane & 31); const int sc = MAP == 1 ? src_col_in(nr) : (MAP == 2 ? nat_dim(nr) : nr);
;     float v[32];
; #pragma unroll
;     for (int i = 0; i < 32; ++i) { const int k = k0 + 2 * i + (lane >> 5); const int ksrc = KPERM ? ((k & ~127) + nat_dim(k & 127)) : k;
;         v[i] = sc >= 0 ? W[(size_t)ksrc * Nsrc + sc] : 0.f; }
; #pragma unroll
;     for (int i = 0; i < 32; ++i) { const int kk = 2 * i + (lane >> 5); const int k = k0 + kk;
;         if (KS) v[i] *= (k < ksplit ? ksA[k] : ksB[k - ksplit]);
;         scr[kk * 33 + (lane & 31)] = v[i]; }
;     LDS_WAIT(); asm volatile("" ::: "memory");
;     const int c = lane & 7;
; #pragma unroll
;     for (int j = 0; j < 4; ++j) { const int n = (lane >> 3) + 8 * j; const LAS float* s = scr + (8 * c) * 33 + n;
;         v4u o; o.x = pk2(s[0 * 33], s[1 * 33]); o.y = pk2(s[2 * 33], s[3 * 33]); o.z = pk2(s[4 * 33], s[5 * 33]); o.w = pk2(s[6 * 33], s[7 * 33]);
;         *(GAS v4u*)(WT + (size_t)(n0 + n) * K + k0 + 8 * c) = o; }
;     LDS_WAIT(); asm volatile("" ::: "memory");
; }
	s_add_i32 s24, s23, 8
	s_lshl_b32 s20, s24, 7
	s_cmp_lt_u32 s24, 40
	s_cselect_b32 s21, 0, 0x830
	s_cmp_lt_u32 s24, 72
	s_cselect_b32 s21, s21, 0xfffff030
	s_add_i32 s20, s20, s21
	s_lshl_b32 s20, s20, 2
	s_add_u32 s8, s50, s20
	s_addc_u32 s9, s51, 0
	global_load_dwordx4 v[144:147], v76, s[8:9]
	s_add_u32 s8, s8, 0x16280
	s_addc_u32 s9, s9, 0
	global_load_dwordx4 v[148:151], v76, s[8:9]
	s_add_u32 s8, s8, 0x16280
	s_addc_u32 s9, s9, 0
	global_load_dwordx4 v[152:155], v76, s[8:9]
	s_add_u32 s8, s8, 0x16280
	s_addc_u32 s9, s9, 0
	global_load_dwordx4 v[156:159], v76, s[8:9]
	s_add_u32 s8, s8, 0x16280
	s_addc_u32 s9, s9, 0
	global_load_dwordx4 v[160:163], v76, s[8:9]
	s_add_u32 s8, s8, 0x16280
	s_addc_u32 s9, s9, 0
	global_load_dwordx4 v[164:167], v76, s[8:9]
	s_add_u32 s8, s8, 0x16280
	s_addc_u32 s9, s9, 0
	global_load_dwordx4 v[168:171], v76, s[8:9]
	s_add_u32 s8, s8, 0x16280
	s_addc_u32 s9, s9, 0
	global_load_dwordx4 v[172:175], v76, s[8:9]
	s_add_i32 s24, s23, 80
	s_mul_i32 s20, s24, 0x100000
	s_add_u32 s6, s48, s20
	s_addc_u32 s7, s49, 0
	s_cmp_lt_u32 s24, 16
	s_cselect_b32 s20, 1, 0
	s_sub_i32 s21, s24, 16
	s_bitcmp0_b32 s21, 2
	s_cselect_b32 s21, 1, 0
	s_cmp_lt_u32 s24, 40
	s_cselect_b32 s21, s21, 0
	s_or_b32 s20, s20, s21
	s_cmp_lg_u32 s20, 0
	s_cselect_b64 s[20:21], -1, 0
	v_cndmask_b32_e64 v91, v83, v87, s[20:21]
	v_cndmask_b32_e64 v92, v84, v88, s[20:21]
	v_cndmask_b32_e64 v93, v85, v89, s[20:21]
	v_cndmask_b32_e64 v94, v86, v90, s[20:21]
	ds_read_b32 v226, v112
	ds_read_b32 v227, v112 offset:512
	ds_read_b32 v228, v112 offset:1024
	ds_read_b32 v229, v112 offset:1536
	ds_read_b32 v230, v112 offset:2048
	ds_read_b32 v231, v112 offset:2560
	ds_read_b32 v232, v112 offset:3072
	ds_read_b32 v233, v112 offset:3584
	s_waitcnt lgkmcnt(0)
	v_bfe_u32 v120, v226, 16, 1
	v_bfe_u32 v121, v227, 16, 1
	v_bfe_u32 v122, v228, 16, 1
	v_bfe_u32 v123, v229, 16, 1
	v_bfe_u32 v124, v230, 16, 1
	v_bfe_u32 v125, v231, 16, 1
	v_bfe_u32 v126, v232, 16, 1
	v_bfe_u32 v127, v233, 16, 1
	v_add3_u32 v226, v226, v120, s63
	v_add3_u32 v227, v227, v121, s63
	v_add3_u32 v228, v228, v122, s63
	v_add3_u32 v229, v229, v123, s63
	v_add3_u32 v230, v230, v124, s63
	v_add3_u32 v231, v231, v125, s63
	v_add3_u32 v232, v232, v126, s63
	v_add3_u32 v233, v233, v127, s63
	v_perm_b32 v242, v227, v226, s64
	v_perm_b32 v243, v229, v228, s64
	v_perm_b32 v244, v231, v230, s64
	v_perm_b32 v245, v233, v232, s64
	s_nop 0
	global_store_dwordx4 v91, v[242:245], s[6:7]
	ds_read_b32 v226, v114
	ds_read_b32 v227, v114 offset:512
	ds_read_b32 v228, v114 offset:1024
	ds_read_b32 v229, v114 offset:1536
	ds_read_b32 v230, v114 offset:2048
	ds_read_b32 v231, v114 offset:2560
	ds_read_b32 v232, v114 offset:3072
	ds_read_b32 v233, v114 offset:3584
	s_waitcnt lgkmcnt(0)
	v_bfe_u32 v120, v226, 16, 1
	v_bfe_u32 v121, v227, 16, 1
	v_bfe_u32 v122, v228, 16, 1
	v_bfe_u32 v123, v229, 16, 1
	v_bfe_u32 v124, v230, 16, 1
	v_bfe_u32 v125, v231, 16, 1
	v_bfe_u32 v126, v232, 16, 1
	v_bfe_u32 v127, v233, 16, 1
	v_add3_u32 v226, v226, v120, s63
	v_add3_u32 v227, v227, v121, s63
	v_add3_u32 v228, v228, v122, s63
	v_add3_u32 v229, v229, v123, s63
	v_add3_u32 v230, v230, v124, s63
	v_add3_u32 v231, v231, v125, s63
	v_add3_u32 v232, v232, v126, s63
	v_add3_u32 v233, v233, v127, s63
	v_perm_b32 v242, v227, v226, s64
	v_perm_b32 v243, v229, v228, s64
	v_perm_b32 v244, v231, v230, s64
	v_perm_b32 v245, v233, v232, s64
	s_nop 0
	global_store_dwordx4 v92, v[242:245], s[6:7]
	ds_read_b32 v226, v116
	ds_read_b32 v227, v116 offset:512
	ds_read_b32 v228, v116 offset:1024
	ds_read_b32 v229, v116 offset:1536
	ds_read_b32 v230, v116 offset:2048
	ds_read_b32 v231, v116 offset:2560
	ds_read_b32 v232, v116 offset:3072
	ds_read_b32 v233, v116 offset:3584
	s_waitcnt lgkmcnt(0)
	v_bfe_u32 v120, v226, 16, 1
	v_bfe_u32 v121, v227, 16, 1
	v_bfe_u32 v122, v228, 16, 1
	v_bfe_u32 v123, v229, 16, 1
	v_bfe_u32 v124, v230, 16, 1
	v_bfe_u32 v125, v231, 16, 1
	v_bfe_u32 v126, v232, 16, 1
	v_bfe_u32 v127, v233, 16, 1
	v_add3_u32 v226, v226, v120, s63
	v_add3_u32 v227, v227, v121, s63
	v_add3_u32 v228, v228, v122, s63
	v_add3_u32 v229, v229, v123, s63
	v_add3_u32 v230, v230, v124, s63
	v_add3_u32 v231, v231, v125, s63
	v_add3_u32 v232, v232, v126, s63
	v_add3_u32 v233, v233, v127, s63
	v_perm_b32 v242, v227, v226, s64
	v_perm_b32 v243, v229, v228, s64
	v_perm_b32 v244, v231, v230, s64
	v_perm_b32 v245, v233, v232, s64
	s_nop 0
	global_store_dwordx4 v93, v[242:245], s[6:7]
	ds_read_b32 v226, v118
	ds_read_b32 v227, v118 offset:512
	ds_read_b32 v228, v118 offset:1024
	ds_read_b32 v229, v118 offset:1536
	ds_read_b32 v230, v118 offset:2048
	ds_read_b32 v231, v118 offset:2560
	ds_read_b32 v232, v118 offset:3072
	ds_read_b32 v233, v118 offset:3584
	s_waitcnt lgkmcnt(0)
	v_bfe_u32 v120, v226, 16, 1
	v_bfe_u32 v121, v227, 16, 1
	v_bfe_u32 v122, v228, 16, 1
	v_bfe_u32 v123, v229, 16, 1
	v_bfe_u32 v124, v230, 16, 1
	v_bfe_u32 v125, v231, 16, 1
	v_bfe_u32 v126, v232, 16, 1
	v_bfe_u32 v127, v233, 16, 1
	v_add3_u32 v226, v226, v120, s63
	v_add3_u32 v227, v227, v121, s63
	v_add3_u32 v228, v228, v122, s63
	v_add3_u32 v229, v229, v123, s63
	v_add3_u32 v230, v230, v124, s63
	v_add3_u32 v231, v231, v125, s63
	v_add3_u32 v232, v232, v126, s63
	v_add3_u32 v233, v233, v127, s63
	v_perm_b32 v242, v227, v226, s64
	v_perm_b32 v243, v229, v228, s64
	v_perm_b32 v244, v231, v230, s64
	v_perm_b32 v245, v233, v232, s64
	s_nop 0
	global_store_dwordx4 v94, v[242:245], s[6:7]
	s_waitcnt vmcnt(16)
	v_mul_f32_e32 v176, v50, v176
	v_mul_f32_e32 v177, v50, v177
	v_mul_f32_e32 v178, v50, v178
	v_mul_f32_e32 v179, v50, v179
	ds_write_b128 v210, v[176:179]
	v_mul_f32_e32 v180, v51, v180
	v_mul_f32_e32 v181, v51, v181
	v_mul_f32_e32 v182, v51, v182
	v_mul_f32_e32 v183, v51, v183
	ds_write_b128 v210, v[180:183] offset:1024
	v_mul_f32_e32 v184, v52, v184
	v_mul_f32_e32 v185, v52, v185
	v_mul_f32_e32 v186, v52, v186
	v_mul_f32_e32 v187, v52, v187
	ds_write_b128 v210, v[184:187] offset:2048
	v_mul_f32_e32 v188, v53, v188
	v_mul_f32_e32 v189, v53, v189
	v_mul_f32_e32 v190, v53, v190
	v_mul_f32_e32 v191, v53, v191
	ds_write_b128 v210, v[188:191] offset:3072
	v_mul_f32_e32 v192, v54, v192
	v_mul_f32_e32 v193, v54, v193
	v_mul_f32_e32 v194, v54, v194
	v_mul_f32_e32 v195, v54, v195
	ds_write_b128 v210, v[192:195] offset:4096
	v_mul_f32_e32 v196, v55, v196
	v_mul_f32_e32 v197, v55, v197
	v_mul_f32_e32 v198, v55, v198
	v_mul_f32_e32 v199, v55, v199
	ds_write_b128 v210, v[196:199] offset:5120
	v_mul_f32_e32 v200, v56, v200
	v_mul_f32_e32 v201, v56, v201
	v_mul_f32_e32 v202, v56, v202
	v_mul_f32_e32 v203, v56, v203
	ds_write_b128 v210, v[200:203] offset:6144
	v_mul_f32_e32 v204, v57, v204
	v_mul_f32_e32 v205, v57, v205
	v_mul_f32_e32 v206, v57, v206
	v_mul_f32_e32 v207, v57, v207
	ds_write_b128 v210, v[204:207] offset:7168
	s_waitcnt lgkmcnt(0)
	s_barrier
; #define GAS __attribute__((address_space(1)))
; #define LAS __attribute__((address_space(3)))
; #define LDS_WAIT() asm volatile("s_waitcnt lgkmcnt(0)" ::: "memory")
; __device__ __forceinline__ unsigned pk4_fp8(float a, float b, float c, float d) {
;     a = fminf(fmaxf(a, -448.f), 448.f); b = fminf(fmaxf(b, -448.f), 448.f); c = fminf(fmaxf(c, -448.f), 448.f); d = fminf(fmaxf(d, -448.f), 448.f);
;     int w = __builtin_amdgcn_cvt_pk_fp8_f32(a, b, 0, false); w = __builtin_amdgcn_cvt_pk_fp8_f32(c, d, w, true); return (unsigned)w; }
;     const int pr = item >> 1, kb = 2 * (pr / nblk) + (item & 1), nb = pr % nblk, k0 = 64 * kb, n0 = 32 * nb;
;     const int nr = n0 + (lane & 31); const int sc = MAP == 1 ? src_col_in(nr) : nr;
;     float v[32];
; #pragma unroll
;     for (int i = 0; i < 32; ++i) v[i] = sc >= 0 ? W[(size_t)(k0 + 2 * i + (lane >> 5)) * Nsrc + sc] : 0.f;
; #pragma unroll
;     for (int i = 0; i < 32; ++i) { const int k = k0 + 2 * i + (lane >> 5); float x = v[i] * wscale; if (KS) x *= (k < ksplit ? ksA[k] : ksB[k - ksplit]); scr[(2 * i + (lane >> 5)) * 33 + (lane & 31)] = x; }
;     LDS_WAIT(); asm volatile("" ::: "memory");
;     const int c = lane & 7;
; #pragma unroll
;     for (int j = 0; j < 4; ++j) { const int n = (lane >> 3) + 8 * j; const LAS float* s = scr + (8 * c) * 33 + n;
;         const unsigned long long o = (unsigned long long)pg8::pk4_fp8(s[0 * 33], s[1 * 33], s[2 * 33], s[3 * 33]) | ((unsigned long long)pg8::pk4_fp8(s[4 * 33], s[5 * 33], s[6 * 33], s[7 * 33]) << 32);
;         *(GAS unsigned long long*)(WT + (size_t)(n0 + n) * K + k0 + 8 * c) = o; }
;     LDS_WAIT(); asm volatile("" ::: "memory");
; }
	s_add_i32 s24, s23, 16
	s_lshl_b32 s20, s24, 7
	s_cmp_lt_u32 s24, 40
	s_cselect_b32 s21, 0, 0x830
	s_cmp_lt_u32 s24, 72
	s_cselect_b32 s21, s21, 0xfffff030
	s_add_i32 s20, s20, s21
	s_lshl_b32 s20, s20, 2
	s_add_u32 s8, s50, s20
	s_addc_u32 s9, s51, 0
	global_load_dwordx4 v[176:179], v76, s[8:9]
	s_add_u32 s8, s8, 0x16280
	s_addc_u32 s9, s9, 0
	global_load_dwordx4 v[180:183], v76, s[8:9]
	s_add_u32 s8, s8, 0x16280
	s_addc_u32 s9, s9, 0
	global_load_dwordx4 v[184:187], v76, s[8:9]
	s_add_u32 s8, s8, 0x16280
	s_addc_u32 s9, s9, 0
	global_load_dwordx4 v[188:191], v76, s[8:9]
	s_add_u32 s8, s8, 0x16280
	s_addc_u32 s9, s9, 0
	global_load_dwordx4 v[192:195], v76, s[8:9]
	s_add_u32 s8, s8, 0x16280
	s_addc_u32 s9, s9, 0
	global_load_dwordx4 v[196:199], v76, s[8:9]
	s_add_u32 s8, s8, 0x16280
	s_addc_u32 s9, s9, 0
	global_load_dwordx4 v[200:203], v76, s[8:9]
	s_add_u32 s8, s8, 0x16280
	s_addc_u32 s9, s9, 0
	global_load_dwordx4 v[204:207], v76, s[8:9]
	s_add_i32 s24, s23, 0
	s_mul_i32 s20, s24, 0x80000
	s_add_u32 s6, s52, s20
	s_addc_u32 s7, s53, 0
	s_cmp_lt_u32 s24, 16
	s_cselect_b32 s20, 1, 0
	s_sub_i32 s21, s24, 16
	s_bitcmp0_b32 s21, 2
	s_cselect_b32 s21, 1, 0
	s_cmp_lt_u32 s24, 40
	s_cselect_b32 s21, s21, 0
	s_or_b32 s20, s20, s21
	s_cmp_lg_u32 s20, 0
	s_cselect_b64 s[20:21], -1, 0
	v_cndmask_b32_e64 v91, v77, v81, s[20:21]
	v_cndmask_b32_e64 v92, v78, v82, s[20:21]
	ds_read_b32 v226, v212
	ds_read_b32 v227, v212 offset:512
	ds_read_b32 v228, v212 offset:1024
	ds_read_b32 v229, v212 offset:1536
	ds_read_b32 v230, v212 offset:2048
	ds_read_b32 v231, v212 offset:2560
	ds_read_b32 v232, v212 offset:3072
	ds_read_b32 v233, v212 offset:3584
	ds_read_b32 v234, v212 offset:4096
	ds_read_b32 v235, v212 offset:4608
	ds_read_b32 v236, v212 offset:5120
	ds_read_b32 v237, v212 offset:5632
	ds_read_b32 v238, v212 offset:6144
	ds_read_b32 v239, v212 offset:6656
	ds_read_b32 v240, v212 offset:7168
	ds_read_b32 v241, v212 offset:7680
	s_waitcnt lgkmcnt(0)
	v_max_f32_e32 v226, v226, v226
	v_max_f32_e32 v227, v227, v227
	v_max_f32_e32 v228, v228, v228
	v_max_f32_e32 v229, v229, v229
	v_max_f32_e32 v230, v230, v230
	v_max_f32_e32 v231, v231, v231
	v_max_f32_e32 v232, v232, v232
	v_max_f32_e32 v233, v233, v233
	v_max_f32_e32 v234, v234, v234
	v_max_f32_e32 v235, v235, v235
	v_max_f32_e32 v236, v236, v236
	v_max_f32_e32 v237, v237, v237
	v_max_f32_e32 v238, v238, v238
	v_max_f32_e32 v239, v239, v239
	v_max_f32_e32 v240, v240, v240
	v_max_f32_e32 v241, v241, v241
	v_med3_f32 v226, v226, s62, v95
	v_med3_f32 v227, v227, s62, v95
	v_med3_f32 v228, v228, s62, v95
	v_med3_f32 v229, v229, s62, v95
	v_med3_f32 v230, v230, s62, v95
	v_med3_f32 v231, v231, s62, v95
	v_med3_f32 v232, v232, s62, v95
	v_med3_f32 v233, v233, s62, v95
	v_med3_f32 v234, v234, s62, v95
	v_med3_f32 v235, v235, s62, v95
	v_med3_f32 v236, v236, s62, v95
	v_med3_f32 v237, v237, s62, v95
	v_med3_f32 v238, v238, s62, v95
	v_med3_f32 v239, v239, s62, v95
	v_med3_f32 v240, v240, s62, v95
	v_med3_f32 v241, v241, s62, v95
	v_mov_b32_e32 v242, 0
	v_mov_b32_e32 v243, 0
	v_mov_b32_e32 v244, 0
	v_mov_b32_e32 v245, 0
	v_cvt_pk_fp8_f32 v242, v226, v227
	v_cvt_pk_fp8_f32 v243, v230, v231
	v_cvt_pk_fp8_f32 v244, v234, v235
	v_cvt_pk_fp8_f32 v245, v238, v239
	v_cvt_pk_fp8_f32 v242, v228, v229 op_sel:[0,0,1]
	v_cvt_pk_fp8_f32 v243, v232, v233 op_sel:[0,0,1]
	v_cvt_pk_fp8_f32 v244, v236, v237 op_sel:[0,0,1]
	v_cvt_pk_fp8_f32 v245, v240, v241 op_sel:[0,0,1]
	s_nop 0
	global_store_dwordx4 v91, v[242:245], s[6:7]
	ds_read_b32 v226, v214
	ds_read_b32 v227, v214 offset:512
	ds_read_b32 v228, v214 offset:1024
	ds_read_b32 v229, v214 offset:1536
	ds_read_b32 v230, v214 offset:2048
	ds_read_b32 v231, v214 offset:2560
	ds_read_b32 v232, v214 offset:3072
	ds_read_b32 v233, v214 offset:3584
	ds_read_b32 v234, v214 offset:4096
	ds_read_b32 v235, v214 offset:4608
	ds_read_b32 v236, v214 offset:5120
	ds_read_b32 v237, v214 offset:5632
	ds_read_b32 v238, v214 offset:6144
	ds_read_b32 v239, v214 offset:6656
	ds_read_b32 v240, v214 offset:7168
	ds_read_b32 v241, v214 offset:7680
	s_waitcnt lgkmcnt(0)
	v_max_f32_e32 v226, v226, v226
	v_max_f32_e32 v227, v227, v227
	v_max_f32_e32 v228, v228, v228
	v_max_f32_e32 v229, v229, v229
	v_max_f32_e32 v230, v230, v230
	v_max_f32_e32 v231, v231, v231
	v_max_f32_e32 v232, v232, v232
	v_max_f32_e32 v233, v233, v233
	v_max_f32_e32 v234, v234, v234
	v_max_f32_e32 v235, v235, v235
	v_max_f32_e32 v236, v236, v236
	v_max_f32_e32 v237, v237, v237
	v_max_f32_e32 v238, v238, v238
	v_max_f32_e32 v239, v239, v239
	v_max_f32_e32 v240, v240, v240
	v_max_f32_e32 v241, v241, v241
	v_med3_f32 v226, v226, s62, v95
	v_med3_f32 v227, v227, s62, v95
	v_med3_f32 v228, v228, s62, v95
	v_med3_f32 v229, v229, s62, v95
	v_med3_f32 v230, v230, s62, v95
	v_med3_f32 v231, v231, s62, v95
	v_med3_f32 v232, v232, s62, v95
	v_med3_f32 v233, v233, s62, v95
	v_med3_f32 v234, v234, s62, v95
	v_med3_f32 v235, v235, s62, v95
	v_med3_f32 v236, v236, s62, v95
	v_med3_f32 v237, v237, s62, v95
	v_med3_f32 v238, v238, s62, v95
	v_med3_f32 v239, v239, s62, v95
	v_med3_f32 v240, v240, s62, v95
	v_med3_f32 v241, v241, s62, v95
	v_mov_b32_e32 v242, 0
	v_mov_b32_e32 v243, 0
	v_mov_b32_e32 v244, 0
	v_mov_b32_e32 v245, 0
	v_cvt_pk_fp8_f32 v242, v226, v227
	v_cvt_pk_fp8_f32 v243, v230, v231
	v_cvt_pk_fp8_f32 v244, v234, v235
	v_cvt_pk_fp8_f32 v245, v238, v239
	v_cvt_pk_fp8_f32 v242, v228, v229 op_sel:[0,0,1]
	v_cvt_pk_fp8_f32 v243, v232, v233 op_sel:[0,0,1]
	v_cvt_pk_fp8_f32 v244, v236, v237 op_sel:[0,0,1]
	v_cvt_pk_fp8_f32 v245, v240, v241 op_sel:[0,0,1]
	s_nop 0
	global_store_dwordx4 v92, v[242:245], s[6:7]
	s_waitcnt vmcnt(14)
	v_mul_f32_e32 v144, v50, v144
	v_mul_f32_e32 v145, v50, v145
	v_mul_f32_e32 v146, v50, v146
	v_mul_f32_e32 v147, v50, v147
	ds_write_b128 v209, v[144:147]
	v_mul_f32_e32 v148, v51, v148
	v_mul_f32_e32 v149, v51, v149
	v_mul_f32_e32 v150, v51, v150
	v_mul_f32_e32 v151, v51, v151
	ds_write_b128 v209, v[148:151] offset:1024
	v_mul_f32_e32 v152, v52, v152
	v_mul_f32_e32 v153, v52, v153
	v_mul_f32_e32 v154, v52, v154
	v_mul_f32_e32 v155, v52, v155
	ds_write_b128 v209, v[152:155] offset:2048
	v_mul_f32_e32 v156, v53, v156
	v_mul_f32_e32 v157, v53, v157
	v_mul_f32_e32 v158, v53, v158
	v_mul_f32_e32 v159, v53, v159
	ds_write_b128 v209, v[156:159] offset:3072
	v_mul_f32_e32 v160, v54, v160
	v_mul_f32_e32 v161, v54, v161
	v_mul_f32_e32 v162, v54, v162
	v_mul_f32_e32 v163, v54, v163
	ds_write_b128 v209, v[160:163] offset:4096
	v_mul_f32_e32 v164, v55, v164
	v_mul_f32_e32 v165, v55, v165
	v_mul_f32_e32 v166, v55, v166
	v_mul_f32_e32 v167, v55, v167
	ds_write_b128 v209, v[164:167] offset:5120
	v_mul_f32_e32 v168, v56, v168
	v_mul_f32_e32 v169, v56, v169
	v_mul_f32_e32 v170, v56, v170
	v_mul_f32_e32 v171, v56, v171
	ds_write_b128 v209, v[168:171] offset:6144
	v_mul_f32_e32 v172, v57, v172
	v_mul_f32_e32 v173, v57, v173
	v_mul_f32_e32 v174, v57, v174
	v_mul_f32_e32 v175, v57, v175
	ds_write_b128 v209, v[172:175] offset:7168
	s_waitcnt lgkmcnt(0)
	s_barrier
; #define GAS __attribute__((address_space(1)))
; #define LAS __attribute__((address_space(3)))
; #define LDS_WAIT() asm volatile("s_waitcnt lgkmcnt(0)" ::: "memory")
; __device__ __forceinline__ unsigned pk4_fp8(float a, float b, float c, float d) {
;     a = fminf(fmaxf(a, -448.f), 448.f); b = fminf(fmaxf(b, -448.f), 448.f); c = fminf(fmaxf(c, -448.f), 448.f); d = fminf(fmaxf(d, -448.f), 448.f);
;     int w = __builtin_amdgcn_cvt_pk_fp8_f32(a, b, 0, false); w = __builtin_amdgcn_cvt_pk_fp8_f32(c, d, w, true); return (unsigned)w; }
;     const int pr = item >> 1, kb = 2 * (pr / nblk) + (item & 1), nb = pr % nblk, k0 = 64 * kb, n0 = 32 * nb;
;     const int nr = n0 + (lane & 31); const int sc = MAP == 1 ? src_col_in(nr) : nr;
;     float v[32];
; #pragma unroll
;     for (int i = 0; i < 32; ++i) v[i] = sc >= 0 ? W[(size_t)(k0 + 2 * i + (lane >> 5)) * Nsrc + sc] : 0.f;
; #pragma unroll
;     for (int i = 0; i < 32; ++i) { const int k = k0 + 2 * i + (lane >> 5); float x = v[i] * wscale; if (KS) x *= (k < ksplit ? ksA[k] : ksB[k - ksplit]); scr[(2 * i + (lane >> 5)) * 33 + (lane & 31)] = x; }
;     LDS_WAIT(); asm volatile("" ::: "memory");
;     const int c = lane & 7;
; #pragma unroll
;     for (int j = 0; j < 4; ++j) { const int n = (lane >> 3) + 8 * j; const LAS float* s = scr + (8 * c) * 33 + n;
;         const unsigned long long o = (unsigned long long)pg8::pk4_fp8(s[0 * 33], s[1 * 33], s[2 * 33], s[3 * 33]) | ((unsigned long long)pg8::pk4_fp8(s[4 * 33], s[5 * 33], s[6 * 33], s[7 * 33]) << 32);
;         *(GAS unsigned long long*)(WT + (size_t)(n0 + n) * K + k0 + 8 * c) = o; }
;     LDS_WAIT(); asm volatile("" ::: "memory");
; }
	s_add_i32 s24, s23, 24
	s_lshl_b32 s20, s24, 7
	s_cmp_lt_u32 s24, 40
	s_cselect_b32 s21, 0, 0x830
	s_cmp_lt_u32 s24, 72
	s_cselect_b32 s21, s21, 0xfffff030
	s_add_i32 s20, s20, s21
	s_lshl_b32 s20, s20, 2
	s_add_u32 s8, s50, s20
	s_addc_u32 s9, s51, 0
	global_load_dwordx4 v[144:147], v76, s[8:9]
	s_add_u32 s8, s8, 0x16280
	s_addc_u32 s9, s9, 0
	global_load_dwordx4 v[148:151], v76, s[8:9]
	s_add_u32 s8, s8, 0x16280
	s_addc_u32 s9, s9, 0
	global_load_dwordx4 v[152:155], v76, s[8:9]
	s_add_u32 s8, s8, 0x16280
	s_addc_u32 s9, s9, 0
	global_load_dwordx4 v[156:159], v76, s[8:9]
	s_add_u32 s8, s8, 0x16280
	s_addc_u32 s9, s9, 0
	global_load_dwordx4 v[160:163], v76, s[8:9]
	s_add_u32 s8, s8, 0x16280
	s_addc_u32 s9, s9, 0
	global_load_dwordx4 v[164:167], v76, s[8:9]
	s_add_u32 s8, s8, 0x16280
	s_addc_u32 s9, s9, 0
	global_load_dwordx4 v[168:171], v76, s[8:9]
	s_add_u32 s8, s8, 0x16280
	s_addc_u32 s9, s9, 0
	global_load_dwordx4 v[172:175], v76, s[8:9]
	s_add_i32 s24, s23, 8
	s_mul_i32 s20, s24, 0x80000
	s_add_u32 s6, s52, s20
	s_addc_u32 s7, s53, 0
	s_cmp_lt_u32 s24, 16
	s_cselect_b32 s20, 1, 0
	s_sub_i32 s21, s24, 16
	s_bitcmp0_b32 s21, 2
	s_cselect_b32 s21, 1, 0
	s_cmp_lt_u32 s24, 40
	s_cselect_b32 s21, s21, 0
	s_or_b32 s20, s20, s21
	s_cmp_lg_u32 s20, 0
	s_cselect_b64 s[20:21], -1, 0
	v_cndmask_b32_e64 v91, v77, v81, s[20:21]
	v_cndmask_b32_e64 v92, v78, v82, s[20:21]
	ds_read_b32 v226, v211
	ds_read_b32 v227, v211 offset:512
	ds_read_b32 v228, v211 offset:1024
	ds_read_b32 v229, v211 offset:1536
	ds_read_b32 v230, v211 offset:2048
	ds_read_b32 v231, v211 offset:2560
	ds_read_b32 v232, v211 offset:3072
	ds_read_b32 v233, v211 offset:3584
	ds_read_b32 v234, v211 offset:4096
	ds_read_b32 v235, v211 offset:4608
	ds_read_b32 v236, v211 offset:5120
	ds_read_b32 v237, v211 offset:5632
	ds_read_b32 v238, v211 offset:6144
	ds_read_b32 v239, v211 offset:6656
	ds_read_b32 v240, v211 offset:7168
	ds_read_b32 v241, v211 offset:7680
	s_waitcnt lgkmcnt(0)
	v_max_f32_e32 v226, v226, v226
	v_max_f32_e32 v227, v227, v227
	v_max_f32_e32 v228, v228, v228
	v_max_f32_e32 v229, v229, v229
	v_max_f32_e32 v230, v230, v230
	v_max_f32_e32 v231, v231, v231
	v_max_f32_e32 v232, v232, v232
	v_max_f32_e32 v233, v233, v233
	v_max_f32_e32 v234, v234, v234
	v_max_f32_e32 v235, v235, v235
	v_max_f32_e32 v236, v236, v236
	v_max_f32_e32 v237, v237, v237
	v_max_f32_e32 v238, v238, v238
	v_max_f32_e32 v239, v239, v239
	v_max_f32_e32 v240, v240, v240
	v_max_f32_e32 v241, v241, v241
	v_med3_f32 v226, v226, s62, v95
	v_med3_f32 v227, v227, s62, v95
	v_med3_f32 v228, v228, s62, v95
	v_med3_f32 v229, v229, s62, v95
	v_med3_f32 v230, v230, s62, v95
	v_med3_f32 v231, v231, s62, v95
	v_med3_f32 v232, v232, s62, v95
	v_med3_f32 v233, v233, s62, v95
	v_med3_f32 v234, v234, s62, v95
	v_med3_f32 v235, v235, s62, v95
	v_med3_f32 v236, v236, s62, v95
	v_med3_f32 v237, v237, s62, v95
	v_med3_f32 v238, v238, s62, v95
	v_med3_f32 v239, v239, s62, v95
	v_med3_f32 v240, v240, s62, v95
	v_med3_f32 v241, v241, s62, v95
	v_mov_b32_e32 v242, 0
	v_mov_b32_e32 v243, 0
	v_mov_b32_e32 v244, 0
	v_mov_b32_e32 v245, 0
	v_cvt_pk_fp8_f32 v242, v226, v227
	v_cvt_pk_fp8_f32 v243, v230, v231
	v_cvt_pk_fp8_f32 v244, v234, v235
	v_cvt_pk_fp8_f32 v245, v238, v239
	v_cvt_pk_fp8_f32 v242, v228, v229 op_sel:[0,0,1]
	v_cvt_pk_fp8_f32 v243, v232, v233 op_sel:[0,0,1]
	v_cvt_pk_fp8_f32 v244, v236, v237 op_sel:[0,0,1]
	v_cvt_pk_fp8_f32 v245, v240, v241 op_sel:[0,0,1]
	s_nop 0
	global_store_dwordx4 v91, v[242:245], s[6:7]
	ds_read_b32 v226, v213
	ds_read_b32 v227, v213 offset:512
	ds_read_b32 v228, v213 offset:1024
	ds_read_b32 v229, v213 offset:1536
	ds_read_b32 v230, v213 offset:2048
	ds_read_b32 v231, v213 offset:2560
	ds_read_b32 v232, v213 offset:3072
	ds_read_b32 v233, v213 offset:3584
	ds_read_b32 v234, v213 offset:4096
	ds_read_b32 v235, v213 offset:4608
	ds_read_b32 v236, v213 offset:5120
	ds_read_b32 v237, v213 offset:5632
	ds_read_b32 v238, v213 offset:6144
	ds_read_b32 v239, v213 offset:6656
	ds_read_b32 v240, v213 offset:7168
	ds_read_b32 v241, v213 offset:7680
	s_waitcnt lgkmcnt(0)
	v_max_f32_e32 v226, v226, v226
	v_max_f32_e32 v227, v227, v227
	v_max_f32_e32 v228, v228, v228
	v_max_f32_e32 v229, v229, v229
	v_max_f32_e32 v230, v230, v230
	v_max_f32_e32 v231, v231, v231
	v_max_f32_e32 v232, v232, v232
	v_max_f32_e32 v233, v233, v233
	v_max_f32_e32 v234, v234, v234
	v_max_f32_e32 v235, v235, v235
	v_max_f32_e32 v236, v236, v236
	v_max_f32_e32 v237, v237, v237
	v_max_f32_e32 v238, v238, v238
	v_max_f32_e32 v239, v239, v239
	v_max_f32_e32 v240, v240, v240
	v_max_f32_e32 v241, v241, v241
	v_med3_f32 v226, v226, s62, v95
	v_med3_f32 v227, v227, s62, v95
	v_med3_f32 v228, v228, s62, v95
	v_med3_f32 v229, v229, s62, v95
	v_med3_f32 v230, v230, s62, v95
	v_med3_f32 v231, v231, s62, v95
	v_med3_f32 v232, v232, s62, v95
	v_med3_f32 v233, v233, s62, v95
	v_med3_f32 v234, v234, s62, v95
	v_med3_f32 v235, v235, s62, v95
	v_med3_f32 v236, v236, s62, v95
	v_med3_f32 v237, v237, s62, v95
	v_med3_f32 v238, v238, s62, v95
	v_med3_f32 v239, v239, s62, v95
	v_med3_f32 v240, v240, s62, v95
	v_med3_f32 v241, v241, s62, v95
	v_mov_b32_e32 v242, 0
	v_mov_b32_e32 v243, 0
	v_mov_b32_e32 v244, 0
	v_mov_b32_e32 v245, 0
	v_cvt_pk_fp8_f32 v242, v226, v227
	v_cvt_pk_fp8_f32 v243, v230, v231
	v_cvt_pk_fp8_f32 v244, v234, v235
	v_cvt_pk_fp8_f32 v245, v238, v239
	v_cvt_pk_fp8_f32 v242, v228, v229 op_sel:[0,0,1]
	v_cvt_pk_fp8_f32 v243, v232, v233 op_sel:[0,0,1]
	v_cvt_pk_fp8_f32 v244, v236, v237 op_sel:[0,0,1]
	v_cvt_pk_fp8_f32 v245, v240, v241 op_sel:[0,0,1]
	s_nop 0
	global_store_dwordx4 v92, v[242:245], s[6:7]
	s_waitcnt vmcnt(12)
	v_mul_f32_e32 v176, v50, v176
	v_mul_f32_e32 v177, v50, v177
	v_mul_f32_e32 v178, v50, v178
	v_mul_f32_e32 v179, v50, v179
	ds_write_b128 v210, v[176:179]
	v_mul_f32_e32 v180, v51, v180
	v_mul_f32_e32 v181, v51, v181
	v_mul_f32_e32 v182, v51, v182
	v_mul_f32_e32 v183, v51, v183
	ds_write_b128 v210, v[180:183] offset:1024
	v_mul_f32_e32 v184, v52, v184
	v_mul_f32_e32 v185, v52, v185
	v_mul_f32_e32 v186, v52, v186
	v_mul_f32_e32 v187, v52, v187
	ds_write_b128 v210, v[184:187] offset:2048
	v_mul_f32_e32 v188, v53, v188
	v_mul_f32_e32 v189, v53, v189
	v_mul_f32_e32 v190, v53, v190
	v_mul_f32_e32 v191, v53, v191
	ds_write_b128 v210, v[188:191] offset:3072
	v_mul_f32_e32 v192, v54, v192
	v_mul_f32_e32 v193, v54, v193
	v_mul_f32_e32 v194, v54, v194
	v_mul_f32_e32 v195, v54, v195
	ds_write_b128 v210, v[192:195] offset:4096
	v_mul_f32_e32 v196, v55, v196
	v_mul_f32_e32 v197, v55, v197
	v_mul_f32_e32 v198, v55, v198
	v_mul_f32_e32 v199, v55, v199
	ds_write_b128 v210, v[196:199] offset:5120
	v_mul_f32_e32 v200, v56, v200
	v_mul_f32_e32 v201, v56, v201
	v_mul_f32_e32 v202, v56, v202
	v_mul_f32_e32 v203, v56, v203
	ds_write_b128 v210, v[200:203] offset:6144
	v_mul_f32_e32 v204, v57, v204
	v_mul_f32_e32 v205, v57, v205
	v_mul_f32_e32 v206, v57, v206
	v_mul_f32_e32 v207, v57, v207
	ds_write_b128 v210, v[204:207] offset:7168
	s_waitcnt lgkmcnt(0)
	s_barrier
; #define GAS __attribute__((address_space(1)))
; #define LAS __attribute__((address_space(3)))
; #define LDS_WAIT() asm volatile("s_waitcnt lgkmcnt(0)" ::: "memory")
; __device__ __forceinline__ unsigned pk4_fp8(float a, float b, float c, float d) {
;     a = fminf(fmaxf(a, -448.f), 448.f); b = fminf(fmaxf(b, -448.f), 448.f); c = fminf(fmaxf(c, -448.f), 448.f); d = fminf(fmaxf(d, -448.f), 448.f);
;     int w = __builtin_amdgcn_cvt_pk_fp8_f32(a, b, 0, false); w = __builtin_amdgcn_cvt_pk_fp8_f32(c, d, w, true); return (unsigned)w; }
;     const int pr = item >> 1, kb = 2 * (pr / nblk) + (item & 1), nb = pr % nblk, k0 = 64 * kb, n0 = 32 * nb;
;     const int nr = n0 + (lane & 31); const int sc = MAP == 1 ? src_col_in(nr) : nr;
;     float v[32];
; #pragma unroll
;     for (int i = 0; i < 32; ++i) v[i] = sc >= 0 ? W[(size_t)(k0 + 2 * i + (lane >> 5)) * Nsrc + sc] : 0.f;
; #pragma unroll
;     for (int i = 0; i < 32; ++i) { const int k = k0 + 2 * i + (lane >> 5); float x = v[i] * wscale; if (KS) x *= (k < ksplit ? ksA[k] : ksB[k - ksplit]); scr[(2 * i + (lane >> 5)) * 33 + (lane & 31)] = x; }
;     LDS_WAIT(); asm volatile("" ::: "memory");
;     const int c = lane & 7;
; #pragma unroll
;     for (int j = 0; j < 4; ++j) { const int n = (lane >> 3) + 8 * j; const LAS float* s = scr + (8 * c) * 33 + n;
;         const unsigned long long o = (unsigned long long)pg8::pk4_fp8(s[0 * 33], s[1 * 33], s[2 * 33], s[3 * 33]) | ((unsigned long long)pg8::pk4_fp8(s[4 * 33], s[5 * 33], s[6 * 33], s[7 * 33]) << 32);
;         *(GAS unsigned long long*)(WT + (size_t)(n0 + n) * K + k0 + 8 * c) = o; }
;     LDS_WAIT(); asm volatile("" ::: "memory");
; }
	s_add_i32 s24, s23, 32
	s_lshl_b32 s20, s24, 7
	s_cmp_lt_u32 s24, 40
	s_cselect_b32 s21, 0, 0x830
	s_cmp_lt_u32 s24, 72
	s_cselect_b32 s21, s21, 0xfffff030
	s_add_i32 s20, s20, s21
	s_lshl_b32 s20, s20, 2
	s_add_u32 s8, s50, s20
	s_addc_u32 s9, s51, 0
	global_load_dwordx4 v[176:179], v76, s[8:9]
	s_add_u32 s8, s8, 0x16280
	s_addc_u32 s9, s9, 0
	global_load_dwordx4 v[180:183], v76, s[8:9]
	s_add_u32 s8, s8, 0x16280
	s_addc_u32 s9, s9, 0
	global_load_dwordx4 v[184:187], v76, s[8:9]
	s_add_u32 s8, s8, 0x16280
	s_addc_u32 s9, s9, 0
	global_load_dwordx4 v[188:191], v76, s[8:9]
	s_add_u32 s8, s8, 0x16280
	s_addc_u32 s9, s9, 0
	global_load_dwordx4 v[192:195], v76, s[8:9]
	s_add_u32 s8, s8, 0x16280
	s_addc_u32 s9, s9, 0
	global_load_dwordx4 v[196:199], v76, s[8:9]
	s_add_u32 s8, s8, 0x16280
	s_addc_u32 s9, s9, 0
	global_load_dwordx4 v[200:203], v76, s[8:9]
	s_add_u32 s8, s8, 0x16280
	s_addc_u32 s9, s9, 0
	global_load_dwordx4 v[204:207], v76, s[8:9]
	s_add_i32 s24, s23, 16
	s_mul_i32 s20, s24, 0x80000
	s_add_u32 s6, s52, s20
	s_addc_u32 s7, s53, 0
	s_cmp_lt_u32 s24, 16
	s_cselect_b32 s20, 1, 0
	s_sub_i32 s21, s24, 16
	s_bitcmp0_b32 s21, 2
	s_cselect_b32 s21, 1, 0
	s_cmp_lt_u32 s24, 40
	s_cselect_b32 s21, s21, 0
	s_or_b32 s20, s20, s21
	s_cmp_lg_u32 s20, 0
	s_cselect_b64 s[20:21], -1, 0
	v_cndmask_b32_e64 v91, v77, v81, s[20:21]
	v_cndmask_b32_e64 v92, v78, v82, s[20:21]
	ds_read_b32 v226, v212
	ds_read_b32 v227, v212 offset:512
	ds_read_b32 v228, v212 offset:1024
	ds_read_b32 v229, v212 offset:1536
	ds_read_b32 v230, v212 offset:2048
	ds_read_b32 v231, v212 offset:2560
	ds_read_b32 v232, v212 offset:3072
	ds_read_b32 v233, v212 offset:3584
	ds_read_b32 v234, v212 offset:4096
	ds_read_b32 v235, v212 offset:4608
	ds_read_b32 v236, v212 offset:5120
	ds_read_b32 v237, v212 offset:5632
	ds_read_b32 v238, v212 offset:6144
	ds_read_b32 v239, v212 offset:6656
	ds_read_b32 v240, v212 offset:7168
	ds_read_b32 v241, v212 offset:7680
	s_waitcnt lgkmcnt(0)
	v_max_f32_e32 v226, v226, v226
	v_max_f32_e32 v227, v227, v227
	v_max_f32_e32 v228, v228, v228
	v_max_f32_e32 v229, v229, v229
	v_max_f32_e32 v230, v230, v230
	v_max_f32_e32 v231, v231, v231
	v_max_f32_e32 v232, v232, v232
	v_max_f32_e32 v233, v233, v233
	v_max_f32_e32 v234, v234, v234
	v_max_f32_e32 v235, v235, v235
	v_max_f32_e32 v236, v236, v236
	v_max_f32_e32 v237, v237, v237
	v_max_f32_e32 v238, v238, v238
	v_max_f32_e32 v239, v239, v239
	v_max_f32_e32 v240, v240, v240
	v_max_f32_e32 v241, v241, v241
	v_med3_f32 v226, v226, s62, v95
	v_med3_f32 v227, v227, s62, v95
	v_med3_f32 v228, v228, s62, v95
	v_med3_f32 v229, v229, s62, v95
	v_med3_f32 v230, v230, s62, v95
	v_med3_f32 v231, v231, s62, v95
	v_med3_f32 v232, v232, s62, v95
	v_med3_f32 v233, v233, s62, v95
	v_med3_f32 v234, v234, s62, v95
	v_med3_f32 v235, v235, s62, v95
	v_med3_f32 v236, v236, s62, v95
	v_med3_f32 v237, v237, s62, v95
	v_med3_f32 v238, v238, s62, v95
	v_med3_f32 v239, v239, s62, v95
	v_med3_f32 v240, v240, s62, v95
	v_med3_f32 v241, v241, s62, v95
	v_mov_b32_e32 v242, 0
	v_mov_b32_e32 v243, 0
	v_mov_b32_e32 v244, 0
	v_mov_b32_e32 v245, 0
	v_cvt_pk_fp8_f32 v242, v226, v227
	v_cvt_pk_fp8_f32 v243, v230, v231
	v_cvt_pk_fp8_f32 v244, v234, v235
	v_cvt_pk_fp8_f32 v245, v238, v239
	v_cvt_pk_fp8_f32 v242, v228, v229 op_sel:[0,0,1]
	v_cvt_pk_fp8_f32 v243, v232, v233 op_sel:[0,0,1]
	v_cvt_pk_fp8_f32 v244, v236, v237 op_sel:[0,0,1]
	v_cvt_pk_fp8_f32 v245, v240, v241 op_sel:[0,0,1]
	s_nop 0
	global_store_dwordx4 v91, v[242:245], s[6:7]
	ds_read_b32 v226, v214
	ds_read_b32 v227, v214 offset:512
	ds_read_b32 v228, v214 offset:1024
	ds_read_b32 v229, v214 offset:1536
	ds_read_b32 v230, v214 offset:2048
	ds_read_b32 v231, v214 offset:2560
	ds_read_b32 v232, v214 offset:3072
	ds_read_b32 v233, v214 offset:3584
	ds_read_b32 v234, v214 offset:4096
	ds_read_b32 v235, v214 offset:4608
	ds_read_b32 v236, v214 offset:5120
	ds_read_b32 v237, v214 offset:5632
	ds_read_b32 v238, v214 offset:6144
	ds_read_b32 v239, v214 offset:6656
	ds_read_b32 v240, v214 offset:7168
	ds_read_b32 v241, v214 offset:7680
	s_waitcnt lgkmcnt(0)
	v_max_f32_e32 v226, v226, v226
	v_max_f32_e32 v227, v227, v227
	v_max_f32_e32 v228, v228, v228
	v_max_f32_e32 v229, v229, v229
	v_max_f32_e32 v230, v230, v230
	v_max_f32_e32 v231, v231, v231
	v_max_f32_e32 v232, v232, v232
	v_max_f32_e32 v233, v233, v233
	v_max_f32_e32 v234, v234, v234
	v_max_f32_e32 v235, v235, v235
	v_max_f32_e32 v236, v236, v236
	v_max_f32_e32 v237, v237, v237
	v_max_f32_e32 v238, v238, v238
	v_max_f32_e32 v239, v239, v239
	v_max_f32_e32 v240, v240, v240
	v_max_f32_e32 v241, v241, v241
	v_med3_f32 v226, v226, s62, v95
	v_med3_f32 v227, v227, s62, v95
	v_med3_f32 v228, v228, s62, v95
	v_med3_f32 v229, v229, s62, v95
	v_med3_f32 v230, v230, s62, v95
	v_med3_f32 v231, v231, s62, v95
	v_med3_f32 v232, v232, s62, v95
	v_med3_f32 v233, v233, s62, v95
	v_med3_f32 v234, v234, s62, v95
	v_med3_f32 v235, v235, s62, v95
	v_med3_f32 v236, v236, s62, v95
	v_med3_f32 v237, v237, s62, v95
	v_med3_f32 v238, v238, s62, v95
	v_med3_f32 v239, v239, s62, v95
	v_med3_f32 v240, v240, s62, v95
	v_med3_f32 v241, v241, s62, v95
	v_mov_b32_e32 v242, 0
	v_mov_b32_e32 v243, 0
	v_mov_b32_e32 v244, 0
	v_mov_b32_e32 v245, 0
	v_cvt_pk_fp8_f32 v242, v226, v227
	v_cvt_pk_fp8_f32 v243, v230, v231
	v_cvt_pk_fp8_f32 v244, v234, v235
	v_cvt_pk_fp8_f32 v245, v238, v239
	v_cvt_pk_fp8_f32 v242, v228, v229 op_sel:[0,0,1]
	v_cvt_pk_fp8_f32 v243, v232, v233 op_sel:[0,0,1]
	v_cvt_pk_fp8_f32 v244, v236, v237 op_sel:[0,0,1]
	v_cvt_pk_fp8_f32 v245, v240, v241 op_sel:[0,0,1]
	s_nop 0
	global_store_dwordx4 v92, v[242:245], s[6:7]
	s_waitcnt vmcnt(12)
	v_mul_f32_e32 v144, v50, v144
	v_mul_f32_e32 v145, v50, v145
	v_mul_f32_e32 v146, v50, v146
	v_mul_f32_e32 v147, v50, v147
	ds_write_b128 v209, v[144:147]
	v_mul_f32_e32 v148, v51, v148
	v_mul_f32_e32 v149, v51, v149
	v_mul_f32_e32 v150, v51, v150
	v_mul_f32_e32 v151, v51, v151
	ds_write_b128 v209, v[148:151] offset:1024
	v_mul_f32_e32 v152, v52, v152
	v_mul_f32_e32 v153, v52, v153
	v_mul_f32_e32 v154, v52, v154
	v_mul_f32_e32 v155, v52, v155
	ds_write_b128 v209, v[152:155] offset:2048
	v_mul_f32_e32 v156, v53, v156
	v_mul_f32_e32 v157, v53, v157
	v_mul_f32_e32 v158, v53, v158
	v_mul_f32_e32 v159, v53, v159
	ds_write_b128 v209, v[156:159] offset:3072
	v_mul_f32_e32 v160, v54, v160
	v_mul_f32_e32 v161, v54, v161
	v_mul_f32_e32 v162, v54, v162
	v_mul_f32_e32 v163, v54, v163
	ds_write_b128 v209, v[160:163] offset:4096
	v_mul_f32_e32 v164, v55, v164
	v_mul_f32_e32 v165, v55, v165
	v_mul_f32_e32 v166, v55, v166
	v_mul_f32_e32 v167, v55, v167
	ds_write_b128 v209, v[164:167] offset:5120
	v_mul_f32_e32 v168, v56, v168
	v_mul_f32_e32 v169, v56, v169
	v_mul_f32_e32 v170, v56, v170
	v_mul_f32_e32 v171, v56, v171
	ds_write_b128 v209, v[168:171] offset:6144
	v_mul_f32_e32 v172, v57, v172
	v_mul_f32_e32 v173, v57, v173
	v_mul_f32_e32 v174, v57, v174
	v_mul_f32_e32 v175, v57, v175
	ds_write_b128 v209, v[172:175] offset:7168
	s_waitcnt lgkmcnt(0)
	s_barrier
; #define GAS __attribute__((address_space(1)))
; #define LAS __attribute__((address_space(3)))
; #define LDS_WAIT() asm volatile("s_waitcnt lgkmcnt(0)" ::: "memory")
; __device__ __forceinline__ unsigned pk4_fp8(float a, float b, float c, float d) {
;     a = fminf(fmaxf(a, -448.f), 448.f); b = fminf(fmaxf(b, -448.f), 448.f); c = fminf(fmaxf(c, -448.f), 448.f); d = fminf(fmaxf(d, -448.f), 448.f);
;     int w = __builtin_amdgcn_cvt_pk_fp8_f32(a, b, 0, false); w = __builtin_amdgcn_cvt_pk_fp8_f32(c, d, w, true); return (unsigned)w; }
;     const int pr = item >> 1, kb = 2 * (pr / nblk) + (item & 1), nb = pr % nblk, k0 = 64 * kb, n0 = 32 * nb;
;     const int nr = n0 + (lane & 31); const int sc = MAP == 1 ? src_col_in(nr) : nr;
;     float v[32];
; #pragma unroll
;     for (int i = 0; i < 32; ++i) v[i] = sc >= 0 ? W[(size_t)(k0 + 2 * i + (lane >> 5)) * Nsrc + sc] : 0.f;
; #pragma unroll
;     for (int i = 0; i < 32; ++i) { const int k = k0 + 2 * i + (lane >> 5); float x = v[i] * wscale; if (KS) x *= (k < ksplit ? ksA[k] : ksB[k - ksplit]); scr[(2 * i + (lane >> 5)) * 33 + (lane & 31)] = x; }
;     LDS_WAIT(); asm volatile("" ::: "memory");
;     const int c = lane & 7;
; #pragma unroll
;     for (int j = 0; j < 4; ++j) { const int n = (lane >> 3) + 8 * j; const LAS float* s = scr + (8 * c) * 33 + n;
;         const unsigned long long o = (unsigned long long)pg8::pk4_fp8(s[0 * 33], s[1 * 33], s[2 * 33], s[3 * 33]) | ((unsigned long long)pg8::pk4_fp8(s[4 * 33], s[5 * 33], s[6 * 33], s[7 * 33]) << 32);
;         *(GAS unsigned long long*)(WT + (size_t)(n0 + n) * K + k0 + 8 * c) = o; }
;     LDS_WAIT(); asm volatile("" ::: "memory");
; }
	s_add_i32 s24, s23, 40
	s_lshl_b32 s20, s24, 7
	s_cmp_lt_u32 s24, 40
	s_cselect_b32 s21, 0, 0x830
	s_cmp_lt_u32 s24, 72
	s_cselect_b32 s21, s21, 0xfffff030
	s_add_i32 s20, s20, s21
	s_lshl_b32 s20, s20, 2
	s_add_u32 s8, s50, s20
	s_addc_u32 s9, s51, 0
	global_load_dwordx4 v[144:147], v76, s[8:9]
	s_add_u32 s8, s8, 0x16280
	s_addc_u32 s9, s9, 0
	global_load_dwordx4 v[148:151], v76, s[8:9]
	s_add_u32 s8, s8, 0x16280
	s_addc_u32 s9, s9, 0
	global_load_dwordx4 v[152:155], v76, s[8:9]
	s_add_u32 s8, s8, 0x16280
	s_addc_u32 s9, s9, 0
	global_load_dwordx4 v[156:159], v76, s[8:9]
	s_add_u32 s8, s8, 0x16280
	s_addc_u32 s9, s9, 0
	global_load_dwordx4 v[160:163], v76, s[8:9]
	s_add_u32 s8, s8, 0x16280
	s_addc_u32 s9, s9, 0
	global_load_dwordx4 v[164:167], v76, s[8:9]
	s_add_u32 s8, s8, 0x16280
	s_addc_u32 s9, s9, 0
	global_load_dwordx4 v[168:171], v76, s[8:9]
	s_add_u32 s8, s8, 0x16280
	s_addc_u32 s9, s9, 0
	global_load_dwordx4 v[172:175], v76, s[8:9]
	s_add_i32 s24, s23, 24
	s_mul_i32 s20, s24, 0x80000
	s_add_u32 s6, s52, s20
	s_addc_u32 s7, s53, 0
	s_cmp_lt_u32 s24, 16
	s_cselect_b32 s20, 1, 0
	s_sub_i32 s21, s24, 16
	s_bitcmp0_b32 s21, 2
	s_cselect_b32 s21, 1, 0
	s_cmp_lt_u32 s24, 40
	s_cselect_b32 s21, s21, 0
	s_or_b32 s20, s20, s21
	s_cmp_lg_u32 s20, 0
	s_cselect_b64 s[20:21], -1, 0
	v_cndmask_b32_e64 v91, v77, v81, s[20:21]
	v_cndmask_b32_e64 v92, v78, v82, s[20:21]
	ds_read_b32 v226, v211
	ds_read_b32 v227, v211 offset:512
	ds_read_b32 v228, v211 offset:1024
	ds_read_b32 v229, v211 offset:1536
	ds_read_b32 v230, v211 offset:2048
	ds_read_b32 v231, v211 offset:2560
	ds_read_b32 v232, v211 offset:3072
	ds_read_b32 v233, v211 offset:3584
	ds_read_b32 v234, v211 offset:4096
	ds_read_b32 v235, v211 offset:4608
	ds_read_b32 v236, v211 offset:5120
	ds_read_b32 v237, v211 offset:5632
	ds_read_b32 v238, v211 offset:6144
	ds_read_b32 v239, v211 offset:6656
	ds_read_b32 v240, v211 offset:7168
	ds_read_b32 v241, v211 offset:7680
	s_waitcnt lgkmcnt(0)
	v_max_f32_e32 v226, v226, v226
	v_max_f32_e32 v227, v227, v227
	v_max_f32_e32 v228, v228, v228
	v_max_f32_e32 v229, v229, v229
	v_max_f32_e32 v230, v230, v230
	v_max_f32_e32 v231, v231, v231
	v_max_f32_e32 v232, v232, v232
	v_max_f32_e32 v233, v233, v233
	v_max_f32_e32 v234, v234, v234
	v_max_f32_e32 v235, v235, v235
	v_max_f32_e32 v236, v236, v236
	v_max_f32_e32 v237, v237, v237
	v_max_f32_e32 v238, v238, v238
	v_max_f32_e32 v239, v239, v239
	v_max_f32_e32 v240, v240, v240
	v_max_f32_e32 v241, v241, v241
	v_med3_f32 v226, v226, s62, v95
	v_med3_f32 v227, v227, s62, v95
	v_med3_f32 v228, v228, s62, v95
	v_med3_f32 v229, v229, s62, v95
	v_med3_f32 v230, v230, s62, v95
	v_med3_f32 v231, v231, s62, v95
	v_med3_f32 v232, v232, s62, v95
	v_med3_f32 v233, v233, s62, v95
	v_med3_f32 v234, v234, s62, v95
	v_med3_f32 v235, v235, s62, v95
	v_med3_f32 v236, v236, s62, v95
	v_med3_f32 v237, v237, s62, v95
	v_med3_f32 v238, v238, s62, v95
	v_med3_f32 v239, v239, s62, v95
	v_med3_f32 v240, v240, s62, v95
	v_med3_f32 v241, v241, s62, v95
	v_mov_b32_e32 v242, 0
	v_mov_b32_e32 v243, 0
	v_mov_b32_e32 v244, 0
	v_mov_b32_e32 v245, 0
	v_cvt_pk_fp8_f32 v242, v226, v227
	v_cvt_pk_fp8_f32 v243, v230, v231
	v_cvt_pk_fp8_f32 v244, v234, v235
	v_cvt_pk_fp8_f32 v245, v238, v239
	v_cvt_pk_fp8_f32 v242, v228, v229 op_sel:[0,0,1]
	v_cvt_pk_fp8_f32 v243, v232, v233 op_sel:[0,0,1]
	v_cvt_pk_fp8_f32 v244, v236, v237 op_sel:[0,0,1]
	v_cvt_pk_fp8_f32 v245, v240, v241 op_sel:[0,0,1]
	s_nop 0
	global_store_dwordx4 v91, v[242:245], s[6:7]
	ds_read_b32 v226, v213
	ds_read_b32 v227, v213 offset:512
	ds_read_b32 v228, v213 offset:1024
	ds_read_b32 v229, v213 offset:1536
	ds_read_b32 v230, v213 offset:2048
	ds_read_b32 v231, v213 offset:2560
	ds_read_b32 v232, v213 offset:3072
	ds_read_b32 v233, v213 offset:3584
	ds_read_b32 v234, v213 offset:4096
	ds_read_b32 v235, v213 offset:4608
	ds_read_b32 v236, v213 offset:5120
	ds_read_b32 v237, v213 offset:5632
	ds_read_b32 v238, v213 offset:6144
	ds_read_b32 v239, v213 offset:6656
	ds_read_b32 v240, v213 offset:7168
	ds_read_b32 v241, v213 offset:7680
	s_waitcnt lgkmcnt(0)
	v_max_f32_e32 v226, v226, v226
	v_max_f32_e32 v227, v227, v227
	v_max_f32_e32 v228, v228, v228
	v_max_f32_e32 v229, v229, v229
	v_max_f32_e32 v230, v230, v230
	v_max_f32_e32 v231, v231, v231
	v_max_f32_e32 v232, v232, v232
	v_max_f32_e32 v233, v233, v233
	v_max_f32_e32 v234, v234, v234
	v_max_f32_e32 v235, v235, v235
	v_max_f32_e32 v236, v236, v236
	v_max_f32_e32 v237, v237, v237
	v_max_f32_e32 v238, v238, v238
	v_max_f32_e32 v239, v239, v239
	v_max_f32_e32 v240, v240, v240
	v_max_f32_e32 v241, v241, v241
	v_med3_f32 v226, v226, s62, v95
	v_med3_f32 v227, v227, s62, v95
	v_med3_f32 v228, v228, s62, v95
	v_med3_f32 v229, v229, s62, v95
	v_med3_f32 v230, v230, s62, v95
	v_med3_f32 v231, v231, s62, v95
	v_med3_f32 v232, v232, s62, v95
	v_med3_f32 v233, v233, s62, v95
	v_med3_f32 v234, v234, s62, v95
	v_med3_f32 v235, v235, s62, v95
	v_med3_f32 v236, v236, s62, v95
	v_med3_f32 v237, v237, s62, v95
	v_med3_f32 v238, v238, s62, v95
	v_med3_f32 v239, v239, s62, v95
	v_med3_f32 v240, v240, s62, v95
	v_med3_f32 v241, v241, s62, v95
	v_mov_b32_e32 v242, 0
	v_mov_b32_e32 v243, 0
	v_mov_b32_e32 v244, 0
	v_mov_b32_e32 v245, 0
	v_cvt_pk_fp8_f32 v242, v226, v227
	v_cvt_pk_fp8_f32 v243, v230, v231
	v_cvt_pk_fp8_f32 v244, v234, v235
	v_cvt_pk_fp8_f32 v245, v238, v239
	v_cvt_pk_fp8_f32 v242, v228, v229 op_sel:[0,0,1]
	v_cvt_pk_fp8_f32 v243, v232, v233 op_sel:[0,0,1]
	v_cvt_pk_fp8_f32 v244, v236, v237 op_sel:[0,0,1]
	v_cvt_pk_fp8_f32 v245, v240, v241 op_sel:[0,0,1]
	s_nop 0
	global_store_dwordx4 v92, v[242:245], s[6:7]
	s_waitcnt vmcnt(12)
	v_mul_f32_e32 v176, v50, v176
	v_mul_f32_e32 v177, v50, v177
	v_mul_f32_e32 v178, v50, v178
	v_mul_f32_e32 v179, v50, v179
	ds_write_b128 v210, v[176:179]
	v_mul_f32_e32 v180, v51, v180
	v_mul_f32_e32 v181, v51, v181
	v_mul_f32_e32 v182, v51, v182
	v_mul_f32_e32 v183, v51, v183
	ds_write_b128 v210, v[180:183] offset:1024
	v_mul_f32_e32 v184, v52, v184
	v_mul_f32_e32 v185, v52, v185
	v_mul_f32_e32 v186, v52, v186
	v_mul_f32_e32 v187, v52, v187
	ds_write_b128 v210, v[184:187] offset:2048
	v_mul_f32_e32 v188, v53, v188
	v_mul_f32_e32 v189, v53, v189
	v_mul_f32_e32 v190, v53, v190
	v_mul_f32_e32 v191, v53, v191
	ds_write_b128 v210, v[188:191] offset:3072
	v_mul_f32_e32 v192, v54, v192
	v_mul_f32_e32 v193, v54, v193
	v_mul_f32_e32 v194, v54, v194
	v_mul_f32_e32 v195, v54, v195
	ds_write_b128 v210, v[192:195] offset:4096
	v_mul_f32_e32 v196, v55, v196
	v_mul_f32_e32 v197, v55, v197
	v_mul_f32_e32 v198, v55, v198
	v_mul_f32_e32 v199, v55, v199
	ds_write_b128 v210, v[196:199] offset:5120
	v_mul_f32_e32 v200, v56, v200
	v_mul_f32_e32 v201, v56, v201
	v_mul_f32_e32 v202, v56, v202
	v_mul_f32_e32 v203, v56, v203
	ds_write_b128 v210, v[200:203] offset:6144
	v_mul_f32_e32 v204, v57, v204
	v_mul_f32_e32 v205, v57, v205
	v_mul_f32_e32 v206, v57, v206
	v_mul_f32_e32 v207, v57, v207
	ds_write_b128 v210, v[204:207] offset:7168
	s_waitcnt lgkmcnt(0)
	s_barrier
; #define GAS __attribute__((address_space(1)))
; #define LAS __attribute__((address_space(3)))
; #define LDS_WAIT() asm volatile("s_waitcnt lgkmcnt(0)" ::: "memory")
; __device__ __forceinline__ unsigned pk4_fp8(float a, float b, float c, float d) {
;     a = fminf(fmaxf(a, -448.f), 448.f); b = fminf(fmaxf(b, -448.f), 448.f); c = fminf(fmaxf(c, -448.f), 448.f); d = fminf(fmaxf(d, -448.f), 448.f);
;     int w = __builtin_amdgcn_cvt_pk_fp8_f32(a, b, 0, false); w = __builtin_amdgcn_cvt_pk_fp8_f32(c, d, w, true); return (unsigned)w; }
;     const int pr = item >> 1, kb = 2 * (pr / nblk) + (item & 1), nb = pr % nblk, k0 = 64 * kb, n0 = 32 * nb;
;     const int nr = n0 + (lane & 31); const int sc = MAP == 1 ? src_col_in(nr) : nr;
;     float v[32];
; #pragma unroll
;     for (int i = 0; i < 32; ++i) v[i] = sc >= 0 ? W[(size_t)(k0 + 2 * i + (lane >> 5)) * Nsrc + sc] : 0.f;
; #pragma unroll
;     for (int i = 0; i < 32; ++i) { const int k = k0 + 2 * i + (lane >> 5); float x = v[i] * wscale; if (KS) x *= (k < ksplit ? ksA[k] : ksB[k - ksplit]); scr[(2 * i + (lane >> 5)) * 33 + (lane & 31)] = x; }
;     LDS_WAIT(); asm volatile("" ::: "memory");
;     const int c = lane & 7;
; #pragma unroll
;     for (int j = 0; j < 4; ++j) { const int n = (lane >> 3) + 8 * j; const LAS float* s = scr + (8 * c) * 33 + n;
;         const unsigned long long o = (unsigned long long)pg8::pk4_fp8(s[0 * 33], s[1 * 33], s[2 * 33], s[3 * 33]) | ((unsigned long long)pg8::pk4_fp8(s[4 * 33], s[5 * 33], s[6 * 33], s[7 * 33]) << 32);
;         *(GAS unsigned long long*)(WT + (size_t)(n0 + n) * K + k0 + 8 * c) = o; }
;     LDS_WAIT(); asm volatile("" ::: "memory");
; }
	s_add_i32 s24, s23, 48
	s_lshl_b32 s20, s24, 7
	s_cmp_lt_u32 s24, 40
	s_cselect_b32 s21, 0, 0x830
	s_cmp_lt_u32 s24, 72
	s_cselect_b32 s21, s21, 0xfffff030
	s_add_i32 s20, s20, s21
	s_lshl_b32 s20, s20, 2
	s_add_u32 s8, s50, s20
	s_addc_u32 s9, s51, 0
	global_load_dwordx4 v[176:179], v76, s[8:9]
	s_add_u32 s8, s8, 0x16280
	s_addc_u32 s9, s9, 0
	global_load_dwordx4 v[180:183], v76, s[8:9]
	s_add_u32 s8, s8, 0x16280
	s_addc_u32 s9, s9, 0
	global_load_dwordx4 v[184:187], v76, s[8:9]
	s_add_u32 s8, s8, 0x16280
	s_addc_u32 s9, s9, 0
	global_load_dwordx4 v[188:191], v76, s[8:9]
	s_add_u32 s8, s8, 0x16280
	s_addc_u32 s9, s9, 0
	global_load_dwordx4 v[192:195], v76, s[8:9]
	s_add_u32 s8, s8, 0x16280
	s_addc_u32 s9, s9, 0
	global_load_dwordx4 v[196:199], v76, s[8:9]
	s_add_u32 s8, s8, 0x16280
	s_addc_u32 s9, s9, 0
	global_load_dwordx4 v[200:203], v76, s[8:9]
	s_add_u32 s8, s8, 0x16280
	s_addc_u32 s9, s9, 0
	global_load_dwordx4 v[204:207], v76, s[8:9]
	s_add_i32 s24, s23, 32
	s_mul_i32 s20, s24, 0x80000
	s_add_u32 s6, s52, s20
	s_addc_u32 s7, s53, 0
	s_cmp_lt_u32 s24, 16
	s_cselect_b32 s20, 1, 0
	s_sub_i32 s21, s24, 16
	s_bitcmp0_b32 s21, 2
	s_cselect_b32 s21, 1, 0
	s_cmp_lt_u32 s24, 40
	s_cselect_b32 s21, s21, 0
	s_or_b32 s20, s20, s21
	s_cmp_lg_u32 s20, 0
	s_cselect_b64 s[20:21], -1, 0
	v_cndmask_b32_e64 v91, v77, v81, s[20:21]
	v_cndmask_b32_e64 v92, v78, v82, s[20:21]
	ds_read_b32 v226, v212
	ds_read_b32 v227, v212 offset:512
	ds_read_b32 v228, v212 offset:1024
	ds_read_b32 v229, v212 offset:1536
	ds_read_b32 v230, v212 offset:2048
	ds_read_b32 v231, v212 offset:2560
	ds_read_b32 v232, v212 offset:3072
	ds_read_b32 v233, v212 offset:3584
	ds_read_b32 v234, v212 offset:4096
	ds_read_b32 v235, v212 offset:4608
	ds_read_b32 v236, v212 offset:5120
	ds_read_b32 v237, v212 offset:5632
	ds_read_b32 v238, v212 offset:6144
	ds_read_b32 v239, v212 offset:6656
	ds_read_b32 v240, v212 offset:7168
	ds_read_b32 v241, v212 offset:7680
	s_waitcnt lgkmcnt(0)
	v_max_f32_e32 v226, v226, v226
	v_max_f32_e32 v227, v227, v227
	v_max_f32_e32 v228, v228, v228
	v_max_f32_e32 v229, v229, v229
	v_max_f32_e32 v230, v230, v230
	v_max_f32_e32 v231, v231, v231
	v_max_f32_e32 v232, v232, v232
	v_max_f32_e32 v233, v233, v233
	v_max_f32_e32 v234, v234, v234
	v_max_f32_e32 v235, v235, v235
	v_max_f32_e32 v236, v236, v236
	v_max_f32_e32 v237, v237, v237
	v_max_f32_e32 v238, v238, v238
	v_max_f32_e32 v239, v239, v239
	v_max_f32_e32 v240, v240, v240
	v_max_f32_e32 v241, v241, v241
	v_med3_f32 v226, v226, s62, v95
	v_med3_f32 v227, v227, s62, v95
	v_med3_f32 v228, v228, s62, v95
	v_med3_f32 v229, v229, s62, v95
	v_med3_f32 v230, v230, s62, v95
	v_med3_f32 v231, v231, s62, v95
	v_med3_f32 v232, v232, s62, v95
	v_med3_f32 v233, v233, s62, v95
	v_med3_f32 v234, v234, s62, v95
	v_med3_f32 v235, v235, s62, v95
	v_med3_f32 v236, v236, s62, v95
	v_med3_f32 v237, v237, s62, v95
	v_med3_f32 v238, v238, s62, v95
	v_med3_f32 v239, v239, s62, v95
	v_med3_f32 v240, v240, s62, v95
	v_med3_f32 v241, v241, s62, v95
	v_mov_b32_e32 v242, 0
	v_mov_b32_e32 v243, 0
	v_mov_b32_e32 v244, 0
	v_mov_b32_e32 v245, 0
	v_cvt_pk_fp8_f32 v242, v226, v227
	v_cvt_pk_fp8_f32 v243, v230, v231
	v_cvt_pk_fp8_f32 v244, v234, v235
	v_cvt_pk_fp8_f32 v245, v238, v239
	v_cvt_pk_fp8_f32 v242, v228, v229 op_sel:[0,0,1]
	v_cvt_pk_fp8_f32 v243, v232, v233 op_sel:[0,0,1]
	v_cvt_pk_fp8_f32 v244, v236, v237 op_sel:[0,0,1]
	v_cvt_pk_fp8_f32 v245, v240, v241 op_sel:[0,0,1]
	s_nop 0
	global_store_dwordx4 v91, v[242:245], s[6:7]
	ds_read_b32 v226, v214
	ds_read_b32 v227, v214 offset:512
	ds_read_b32 v228, v214 offset:1024
	ds_read_b32 v229, v214 offset:1536
	ds_read_b32 v230, v214 offset:2048
	ds_read_b32 v231, v214 offset:2560
	ds_read_b32 v232, v214 offset:3072
	ds_read_b32 v233, v214 offset:3584
	ds_read_b32 v234, v214 offset:4096
	ds_read_b32 v235, v214 offset:4608
	ds_read_b32 v236, v214 offset:5120
	ds_read_b32 v237, v214 offset:5632
	ds_read_b32 v238, v214 offset:6144
	ds_read_b32 v239, v214 offset:6656
	ds_read_b32 v240, v214 offset:7168
	ds_read_b32 v241, v214 offset:7680
	s_waitcnt lgkmcnt(0)
	v_max_f32_e32 v226, v226, v226
	v_max_f32_e32 v227, v227, v227
	v_max_f32_e32 v228, v228, v228
	v_max_f32_e32 v229, v229, v229
	v_max_f32_e32 v230, v230, v230
	v_max_f32_e32 v231, v231, v231
	v_max_f32_e32 v232, v232, v232
	v_max_f32_e32 v233, v233, v233
	v_max_f32_e32 v234, v234, v234
	v_max_f32_e32 v235, v235, v235
	v_max_f32_e32 v236, v236, v236
	v_max_f32_e32 v237, v237, v237
	v_max_f32_e32 v238, v238, v238
	v_max_f32_e32 v239, v239, v239
	v_max_f32_e32 v240, v240, v240
	v_max_f32_e32 v241, v241, v241
	v_med3_f32 v226, v226, s62, v95
	v_med3_f32 v227, v227, s62, v95
	v_med3_f32 v228, v228, s62, v95
	v_med3_f32 v229, v229, s62, v95
	v_med3_f32 v230, v230, s62, v95
	v_med3_f32 v231, v231, s62, v95
	v_med3_f32 v232, v232, s62, v95
	v_med3_f32 v233, v233, s62, v95
	v_med3_f32 v234, v234, s62, v95
	v_med3_f32 v235, v235, s62, v95
	v_med3_f32 v236, v236, s62, v95
	v_med3_f32 v237, v237, s62, v95
	v_med3_f32 v238, v238, s62, v95
	v_med3_f32 v239, v239, s62, v95
	v_med3_f32 v240, v240, s62, v95
	v_med3_f32 v241, v241, s62, v95
	v_mov_b32_e32 v242, 0
	v_mov_b32_e32 v243, 0
	v_mov_b32_e32 v244, 0
	v_mov_b32_e32 v245, 0
	v_cvt_pk_fp8_f32 v242, v226, v227
	v_cvt_pk_fp8_f32 v243, v230, v231
	v_cvt_pk_fp8_f32 v244, v234, v235
	v_cvt_pk_fp8_f32 v245, v238, v239
	v_cvt_pk_fp8_f32 v242, v228, v229 op_sel:[0,0,1]
	v_cvt_pk_fp8_f32 v243, v232, v233 op_sel:[0,0,1]
	v_cvt_pk_fp8_f32 v244, v236, v237 op_sel:[0,0,1]
	v_cvt_pk_fp8_f32 v245, v240, v241 op_sel:[0,0,1]
	s_nop 0
	global_store_dwordx4 v92, v[242:245], s[6:7]
	s_waitcnt vmcnt(12)
	v_mul_f32_e32 v144, v50, v144
	v_mul_f32_e32 v145, v50, v145
	v_mul_f32_e32 v146, v50, v146
	v_mul_f32_e32 v147, v50, v147
	ds_write_b128 v209, v[144:147]
	v_mul_f32_e32 v148, v51, v148
	v_mul_f32_e32 v149, v51, v149
	v_mul_f32_e32 v150, v51, v150
	v_mul_f32_e32 v151, v51, v151
	ds_write_b128 v209, v[148:151] offset:1024
	v_mul_f32_e32 v152, v52, v152
	v_mul_f32_e32 v153, v52, v153
	v_mul_f32_e32 v154, v52, v154
	v_mul_f32_e32 v155, v52, v155
	ds_write_b128 v209, v[152:155] offset:2048
	v_mul_f32_e32 v156, v53, v156
	v_mul_f32_e32 v157, v53, v157
	v_mul_f32_e32 v158, v53, v158
	v_mul_f32_e32 v159, v53, v159
	ds_write_b128 v209, v[156:159] offset:3072
	v_mul_f32_e32 v160, v54, v160
	v_mul_f32_e32 v161, v54, v161
	v_mul_f32_e32 v162, v54, v162
	v_mul_f32_e32 v163, v54, v163
	ds_write_b128 v209, v[160:163] offset:4096
	v_mul_f32_e32 v164, v55, v164
	v_mul_f32_e32 v165, v55, v165
	v_mul_f32_e32 v166, v55, v166
	v_mul_f32_e32 v167, v55, v167
	ds_write_b128 v209, v[164:167] offset:5120
	v_mul_f32_e32 v168, v56, v168
	v_mul_f32_e32 v169, v56, v169
	v_mul_f32_e32 v170, v56, v170
	v_mul_f32_e32 v171, v56, v171
	ds_write_b128 v209, v[168:171] offset:6144
	v_mul_f32_e32 v172, v57, v172
	v_mul_f32_e32 v173, v57, v173
	v_mul_f32_e32 v174, v57, v174
	v_mul_f32_e32 v175, v57, v175
	ds_write_b128 v209, v[172:175] offset:7168
	s_waitcnt lgkmcnt(0)
	s_barrier
; #define GAS __attribute__((address_space(1)))
; #define LAS __attribute__((address_space(3)))
; #define LDS_WAIT() asm volatile("s_waitcnt lgkmcnt(0)" ::: "memory")
; __device__ __forceinline__ unsigned pk4_fp8(float a, float b, float c, float d) {
;     a = fminf(fmaxf(a, -448.f), 448.f); b = fminf(fmaxf(b, -448.f), 448.f); c = fminf(fmaxf(c, -448.f), 448.f); d = fminf(fmaxf(d, -448.f), 448.f);
;     int w = __builtin_amdgcn_cvt_pk_fp8_f32(a, b, 0, false); w = __builtin_amdgcn_cvt_pk_fp8_f32(c, d, w, true); return (unsigned)w; }
;     const int pr = item >> 1, kb = 2 * (pr / nblk) + (item & 1), nb = pr % nblk, k0 = 64 * kb, n0 = 32 * nb;
;     const int nr = n0 + (lane & 31); const int sc = MAP == 1 ? src_col_in(nr) : nr;
;     float v[32];
; #pragma unroll
;     for (int i = 0; i < 32; ++i) v[i] = sc >= 0 ? W[(size_t)(k0 + 2 * i + (lane >> 5)) * Nsrc + sc] : 0.f;
; #pragma unroll
;     for (int i = 0; i < 32; ++i) { const int k = k0 + 2 * i + (lane >> 5); float x = v[i] * wscale; if (KS) x *= (k < ksplit ? ksA[k] : ksB[k - ksplit]); scr[(2 * i + (lane >> 5)) * 33 + (lane & 31)] = x; }
;     LDS_WAIT(); asm volatile("" ::: "memory");
;     const int c = lane & 7;
; #pragma unroll
;     for (int j = 0; j < 4; ++j) { const int n = (lane >> 3) + 8 * j; const LAS float* s = scr + (8 * c) * 33 + n;
;         const unsigned long long o = (unsigned long long)pg8::pk4_fp8(s[0 * 33], s[1 * 33], s[2 * 33], s[3 * 33]) | ((unsigned long long)pg8::pk4_fp8(s[4 * 33], s[5 * 33], s[6 * 33], s[7 * 33]) << 32);
;         *(GAS unsigned long long*)(WT + (size_t)(n0 + n) * K + k0 + 8 * c) = o; }
;     LDS_WAIT(); asm volatile("" ::: "memory");
; }
	s_add_i32 s24, s23, 56
	s_lshl_b32 s20, s24, 7
	s_cmp_lt_u32 s24, 40
	s_cselect_b32 s21, 0, 0x830
	s_cmp_lt_u32 s24, 72
	s_cselect_b32 s21, s21, 0xfffff030
	s_add_i32 s20, s20, s21
	s_lshl_b32 s20, s20, 2
	s_add_u32 s8, s50, s20
	s_addc_u32 s9, s51, 0
	global_load_dwordx4 v[144:147], v76, s[8:9]
	s_add_u32 s8, s8, 0x16280
	s_addc_u32 s9, s9, 0
	global_load_dwordx4 v[148:151], v76, s[8:9]
	s_add_u32 s8, s8, 0x16280
	s_addc_u32 s9, s9, 0
	global_load_dwordx4 v[152:155], v76, s[8:9]
	s_add_u32 s8, s8, 0x16280
	s_addc_u32 s9, s9, 0
	global_load_dwordx4 v[156:159], v76, s[8:9]
	s_add_u32 s8, s8, 0x16280
	s_addc_u32 s9, s9, 0
	global_load_dwordx4 v[160:163], v76, s[8:9]
	s_add_u32 s8, s8, 0x16280
	s_addc_u32 s9, s9, 0
	global_load_dwordx4 v[164:167], v76, s[8:9]
	s_add_u32 s8, s8, 0x16280
	s_addc_u32 s9, s9, 0
	global_load_dwordx4 v[168:171], v76, s[8:9]
	s_add_u32 s8, s8, 0x16280
	s_addc_u32 s9, s9, 0
	global_load_dwordx4 v[172:175], v76, s[8:9]
	s_add_i32 s24, s23, 40
	s_mul_i32 s20, s24, 0x80000
	s_add_u32 s6, s52, s20
	s_addc_u32 s7, s53, 0
	s_cmp_lt_u32 s24, 16
	s_cselect_b32 s20, 1, 0
	s_sub_i32 s21, s24, 16
	s_bitcmp0_b32 s21, 2
	s_cselect_b32 s21, 1, 0
	s_cmp_lt_u32 s24, 40
	s_cselect_b32 s21, s21, 0
	s_or_b32 s20, s20, s21
	s_cmp_lg_u32 s20, 0
	s_cselect_b64 s[20:21], -1, 0
	v_cndmask_b32_e64 v91, v77, v81, s[20:21]
	v_cndmask_b32_e64 v92, v78, v82, s[20:21]
	ds_read_b32 v226, v211
	ds_read_b32 v227, v211 offset:512
	ds_read_b32 v228, v211 offset:1024
	ds_read_b32 v229, v211 offset:1536
	ds_read_b32 v230, v211 offset:2048
	ds_read_b32 v231, v211 offset:2560
	ds_read_b32 v232, v211 offset:3072
	ds_read_b32 v233, v211 offset:3584
	ds_read_b32 v234, v211 offset:4096
	ds_read_b32 v235, v211 offset:4608
	ds_read_b32 v236, v211 offset:5120
	ds_read_b32 v237, v211 offset:5632
	ds_read_b32 v238, v211 offset:6144
	ds_read_b32 v239, v211 offset:6656
	ds_read_b32 v240, v211 offset:7168
	ds_read_b32 v241, v211 offset:7680
	s_waitcnt lgkmcnt(0)
	v_max_f32_e32 v226, v226, v226
	v_max_f32_e32 v227, v227, v227
	v_max_f32_e32 v228, v228, v228
	v_max_f32_e32 v229, v229, v229
	v_max_f32_e32 v230, v230, v230
	v_max_f32_e32 v231, v231, v231
	v_max_f32_e32 v232, v232, v232
	v_max_f32_e32 v233, v233, v233
	v_max_f32_e32 v234, v234, v234
	v_max_f32_e32 v235, v235, v235
	v_max_f32_e32 v236, v236, v236
	v_max_f32_e32 v237, v237, v237
	v_max_f32_e32 v238, v238, v238
	v_max_f32_e32 v239, v239, v239
	v_max_f32_e32 v240, v240, v240
	v_max_f32_e32 v241, v241, v241
	v_med3_f32 v226, v226, s62, v95
	v_med3_f32 v227, v227, s62, v95
	v_med3_f32 v228, v228, s62, v95
	v_med3_f32 v229, v229, s62, v95
	v_med3_f32 v230, v230, s62, v95
	v_med3_f32 v231, v231, s62, v95
	v_med3_f32 v232, v232, s62, v95
	v_med3_f32 v233, v233, s62, v95
	v_med3_f32 v234, v234, s62, v95
	v_med3_f32 v235, v235, s62, v95
	v_med3_f32 v236, v236, s62, v95
	v_med3_f32 v237, v237, s62, v95
	v_med3_f32 v238, v238, s62, v95
	v_med3_f32 v239, v239, s62, v95
	v_med3_f32 v240, v240, s62, v95
	v_med3_f32 v241, v241, s62, v95
	v_mov_b32_e32 v242, 0
	v_mov_b32_e32 v243, 0
	v_mov_b32_e32 v244, 0
	v_mov_b32_e32 v245, 0
	v_cvt_pk_fp8_f32 v242, v226, v227
	v_cvt_pk_fp8_f32 v243, v230, v231
	v_cvt_pk_fp8_f32 v244, v234, v235
	v_cvt_pk_fp8_f32 v245, v238, v239
	v_cvt_pk_fp8_f32 v242, v228, v229 op_sel:[0,0,1]
	v_cvt_pk_fp8_f32 v243, v232, v233 op_sel:[0,0,1]
	v_cvt_pk_fp8_f32 v244, v236, v237 op_sel:[0,0,1]
	v_cvt_pk_fp8_f32 v245, v240, v241 op_sel:[0,0,1]
	s_nop 0
	global_store_dwordx4 v91, v[242:245], s[6:7]
	ds_read_b32 v226, v213
	ds_read_b32 v227, v213 offset:512
	ds_read_b32 v228, v213 offset:1024
	ds_read_b32 v229, v213 offset:1536
	ds_read_b32 v230, v213 offset:2048
	ds_read_b32 v231, v213 offset:2560
	ds_read_b32 v232, v213 offset:3072
	ds_read_b32 v233, v213 offset:3584
	ds_read_b32 v234, v213 offset:4096
	ds_read_b32 v235, v213 offset:4608
	ds_read_b32 v236, v213 offset:5120
	ds_read_b32 v237, v213 offset:5632
	ds_read_b32 v238, v213 offset:6144
	ds_read_b32 v239, v213 offset:6656
	ds_read_b32 v240, v213 offset:7168
	ds_read_b32 v241, v213 offset:7680
	s_waitcnt lgkmcnt(0)
	v_max_f32_e32 v226, v226, v226
	v_max_f32_e32 v227, v227, v227
	v_max_f32_e32 v228, v228, v228
	v_max_f32_e32 v229, v229, v229
	v_max_f32_e32 v230, v230, v230
	v_max_f32_e32 v231, v231, v231
	v_max_f32_e32 v232, v232, v232
	v_max_f32_e32 v233, v233, v233
	v_max_f32_e32 v234, v234, v234
	v_max_f32_e32 v235, v235, v235
	v_max_f32_e32 v236, v236, v236
	v_max_f32_e32 v237, v237, v237
	v_max_f32_e32 v238, v238, v238
	v_max_f32_e32 v239, v239, v239
	v_max_f32_e32 v240, v240, v240
	v_max_f32_e32 v241, v241, v241
	v_med3_f32 v226, v226, s62, v95
	v_med3_f32 v227, v227, s62, v95
	v_med3_f32 v228, v228, s62, v95
	v_med3_f32 v229, v229, s62, v95
	v_med3_f32 v230, v230, s62, v95
	v_med3_f32 v231, v231, s62, v95
	v_med3_f32 v232, v232, s62, v95
	v_med3_f32 v233, v233, s62, v95
	v_med3_f32 v234, v234, s62, v95
	v_med3_f32 v235, v235, s62, v95
	v_med3_f32 v236, v236, s62, v95
	v_med3_f32 v237, v237, s62, v95
	v_med3_f32 v238, v238, s62, v95
	v_med3_f32 v239, v239, s62, v95
	v_med3_f32 v240, v240, s62, v95
	v_med3_f32 v241, v241, s62, v95
	v_mov_b32_e32 v242, 0
	v_mov_b32_e32 v243, 0
	v_mov_b32_e32 v244, 0
	v_mov_b32_e32 v245, 0
	v_cvt_pk_fp8_f32 v242, v226, v227
	v_cvt_pk_fp8_f32 v243, v230, v231
	v_cvt_pk_fp8_f32 v244, v234, v235
	v_cvt_pk_fp8_f32 v245, v238, v239
	v_cvt_pk_fp8_f32 v242, v228, v229 op_sel:[0,0,1]
	v_cvt_pk_fp8_f32 v243, v232, v233 op_sel:[0,0,1]
	v_cvt_pk_fp8_f32 v244, v236, v237 op_sel:[0,0,1]
	v_cvt_pk_fp8_f32 v245, v240, v241 op_sel:[0,0,1]
	s_nop 0
	global_store_dwordx4 v92, v[242:245], s[6:7]
	s_waitcnt vmcnt(12)
	v_mul_f32_e32 v176, v50, v176
	v_mul_f32_e32 v177, v50, v177
	v_mul_f32_e32 v178, v50, v178
	v_mul_f32_e32 v179, v50, v179
	ds_write_b128 v210, v[176:179]
	v_mul_f32_e32 v180, v51, v180
	v_mul_f32_e32 v181, v51, v181
	v_mul_f32_e32 v182, v51, v182
	v_mul_f32_e32 v183, v51, v183
	ds_write_b128 v210, v[180:183] offset:1024
	v_mul_f32_e32 v184, v52, v184
	v_mul_f32_e32 v185, v52, v185
	v_mul_f32_e32 v186, v52, v186
	v_mul_f32_e32 v187, v52, v187
	ds_write_b128 v210, v[184:187] offset:2048
	v_mul_f32_e32 v188, v53, v188
	v_mul_f32_e32 v189, v53, v189
	v_mul_f32_e32 v190, v53, v190
	v_mul_f32_e32 v191, v53, v191
	ds_write_b128 v210, v[188:191] offset:3072
	v_mul_f32_e32 v192, v54, v192
	v_mul_f32_e32 v193, v54, v193
	v_mul_f32_e32 v194, v54, v194
	v_mul_f32_e32 v195, v54, v195
	ds_write_b128 v210, v[192:195] offset:4096
	v_mul_f32_e32 v196, v55, v196
	v_mul_f32_e32 v197, v55, v197
	v_mul_f32_e32 v198, v55, v198
	v_mul_f32_e32 v199, v55, v199
	ds_write_b128 v210, v[196:199] offset:5120
	v_mul_f32_e32 v200, v56, v200
	v_mul_f32_e32 v201, v56, v201
	v_mul_f32_e32 v202, v56, v202
	v_mul_f32_e32 v203, v56, v203
	ds_write_b128 v210, v[200:203] offset:6144
	v_mul_f32_e32 v204, v57, v204
	v_mul_f32_e32 v205, v57, v205
	v_mul_f32_e32 v206, v57, v206
	v_mul_f32_e32 v207, v57, v207
	ds_write_b128 v210, v[204:207] offset:7168
	s_waitcnt lgkmcnt(0)
	s_barrier
; #define GAS __attribute__((address_space(1)))
; #define LAS __attribute__((address_space(3)))
; #define LDS_WAIT() asm volatile("s_waitcnt lgkmcnt(0)" ::: "memory")
; __device__ __forceinline__ unsigned pk4_fp8(float a, float b, float c, float d) {
;     a = fminf(fmaxf(a, -448.f), 448.f); b = fminf(fmaxf(b, -448.f), 448.f); c = fminf(fmaxf(c, -448.f), 448.f); d = fminf(fmaxf(d, -448.f), 448.f);
;     int w = __builtin_amdgcn_cvt_pk_fp8_f32(a, b, 0, false); w = __builtin_amdgcn_cvt_pk_fp8_f32(c, d, w, true); return (unsigned)w; }
;     const int pr = item >> 1, kb = 2 * (pr / nblk) + (item & 1), nb = pr % nblk, k0 = 64 * kb, n0 = 32 * nb;
;     const int nr = n0 + (lane & 31); const int sc = MAP == 1 ? src_col_in(nr) : nr;
;     float v[32];
; #pragma unroll
;     for (int i = 0; i < 32; ++i) v[i] = sc >= 0 ? W[(size_t)(k0 + 2 * i + (lane >> 5)) * Nsrc + sc] : 0.f;
; #pragma unroll
;     for (int i = 0; i < 32; ++i) { const int k = k0 + 2 * i + (lane >> 5); float x = v[i] * wscale; if (KS) x *= (k < ksplit ? ksA[k] : ksB[k - ksplit]); scr[(2 * i + (lane >> 5)) * 33 + (lane & 31)] = x; }
;     LDS_WAIT(); asm volatile("" ::: "memory");
;     const int c = lane & 7;
; #pragma unroll
;     for (int j = 0; j < 4; ++j) { const int n = (lane >> 3) + 8 * j; const LAS float* s = scr + (8 * c) * 33 + n;
;         const unsigned long long o = (unsigned long long)pg8::pk4_fp8(s[0 * 33], s[1 * 33], s[2 * 33], s[3 * 33]) | ((unsigned long long)pg8::pk4_fp8(s[4 * 33], s[5 * 33], s[6 * 33], s[7 * 33]) << 32);
;         *(GAS unsigned long long*)(WT + (size_t)(n0 + n) * K + k0 + 8 * c) = o; }
;     LDS_WAIT(); asm volatile("" ::: "memory");
; }
	s_add_i32 s24, s23, 64
	s_lshl_b32 s20, s24, 7
	s_cmp_lt_u32 s24, 40
	s_cselect_b32 s21, 0, 0x830
	s_cmp_lt_u32 s24, 72
	s_cselect_b32 s21, s21, 0xfffff030
	s_add_i32 s20, s20, s21
	s_lshl_b32 s20, s20, 2
	s_add_u32 s8, s50, s20
	s_addc_u32 s9, s51, 0
	global_load_dwordx4 v[176:179], v76, s[8:9]
	s_add_u32 s8, s8, 0x16280
	s_addc_u32 s9, s9, 0
	global_load_dwordx4 v[180:183], v76, s[8:9]
	s_add_u32 s8, s8, 0x16280
	s_addc_u32 s9, s9, 0
	global_load_dwordx4 v[184:187], v76, s[8:9]
	s_add_u32 s8, s8, 0x16280
	s_addc_u32 s9, s9, 0
	global_load_dwordx4 v[188:191], v76, s[8:9]
	s_add_u32 s8, s8, 0x16280
	s_addc_u32 s9, s9, 0
	global_load_dwordx4 v[192:195], v76, s[8:9]
	s_add_u32 s8, s8, 0x16280
	s_addc_u32 s9, s9, 0
	global_load_dwordx4 v[196:199], v76, s[8:9]
	s_add_u32 s8, s8, 0x16280
	s_addc_u32 s9, s9, 0
	global_load_dwordx4 v[200:203], v76, s[8:9]
	s_add_u32 s8, s8, 0x16280
	s_addc_u32 s9, s9, 0
	global_load_dwordx4 v[204:207], v76, s[8:9]
	s_add_i32 s24, s23, 48
	s_mul_i32 s20, s24, 0x80000
	s_add_u32 s6, s52, s20
	s_addc_u32 s7, s53, 0
	s_cmp_lt_u32 s24, 16
	s_cselect_b32 s20, 1, 0
	s_sub_i32 s21, s24, 16
	s_bitcmp0_b32 s21, 2
	s_cselect_b32 s21, 1, 0
	s_cmp_lt_u32 s24, 40
	s_cselect_b32 s21, s21, 0
	s_or_b32 s20, s20, s21
	s_cmp_lg_u32 s20, 0
	s_cselect_b64 s[20:21], -1, 0
	v_cndmask_b32_e64 v91, v77, v81, s[20:21]
	v_cndmask_b32_e64 v92, v78, v82, s[20:21]
	ds_read_b32 v226, v212
	ds_read_b32 v227, v212 offset:512
	ds_read_b32 v228, v212 offset:1024
	ds_read_b32 v229, v212 offset:1536
	ds_read_b32 v230, v212 offset:2048
	ds_read_b32 v231, v212 offset:2560
	ds_read_b32 v232, v212 offset:3072
	ds_read_b32 v233, v212 offset:3584
	ds_read_b32 v234, v212 offset:4096
	ds_read_b32 v235, v212 offset:4608
	ds_read_b32 v236, v212 offset:5120
	ds_read_b32 v237, v212 offset:5632
	ds_read_b32 v238, v212 offset:6144
	ds_read_b32 v239, v212 offset:6656
	ds_read_b32 v240, v212 offset:7168
	ds_read_b32 v241, v212 offset:7680
	s_waitcnt lgkmcnt(0)
	v_max_f32_e32 v226, v226, v226
	v_max_f32_e32 v227, v227, v227
	v_max_f32_e32 v228, v228, v228
	v_max_f32_e32 v229, v229, v229
	v_max_f32_e32 v230, v230, v230
	v_max_f32_e32 v231, v231, v231
	v_max_f32_e32 v232, v232, v232
	v_max_f32_e32 v233, v233, v233
	v_max_f32_e32 v234, v234, v234
	v_max_f32_e32 v235, v235, v235
	v_max_f32_e32 v236, v236, v236
	v_max_f32_e32 v237, v237, v237
	v_max_f32_e32 v238, v238, v238
	v_max_f32_e32 v239, v239, v239
	v_max_f32_e32 v240, v240, v240
	v_max_f32_e32 v241, v241, v241
	v_med3_f32 v226, v226, s62, v95
	v_med3_f32 v227, v227, s62, v95
	v_med3_f32 v228, v228, s62, v95
	v_med3_f32 v229, v229, s62, v95
	v_med3_f32 v230, v230, s62, v95
	v_med3_f32 v231, v231, s62, v95
	v_med3_f32 v232, v232, s62, v95
	v_med3_f32 v233, v233, s62, v95
	v_med3_f32 v234, v234, s62, v95
	v_med3_f32 v235, v235, s62, v95
	v_med3_f32 v236, v236, s62, v95
	v_med3_f32 v237, v237, s62, v95
	v_med3_f32 v238, v238, s62, v95
	v_med3_f32 v239, v239, s62, v95
	v_med3_f32 v240, v240, s62, v95
	v_med3_f32 v241, v241, s62, v95
	v_mov_b32_e32 v242, 0
	v_mov_b32_e32 v243, 0
	v_mov_b32_e32 v244, 0
	v_mov_b32_e32 v245, 0
	v_cvt_pk_fp8_f32 v242, v226, v227
	v_cvt_pk_fp8_f32 v243, v230, v231
	v_cvt_pk_fp8_f32 v244, v234, v235
	v_cvt_pk_fp8_f32 v245, v238, v239
	v_cvt_pk_fp8_f32 v242, v228, v229 op_sel:[0,0,1]
	v_cvt_pk_fp8_f32 v243, v232, v233 op_sel:[0,0,1]
	v_cvt_pk_fp8_f32 v244, v236, v237 op_sel:[0,0,1]
	v_cvt_pk_fp8_f32 v245, v240, v241 op_sel:[0,0,1]
	s_nop 0
	global_store_dwordx4 v91, v[242:245], s[6:7]
	ds_read_b32 v226, v214
	ds_read_b32 v227, v214 offset:512
	ds_read_b32 v228, v214 offset:1024
	ds_read_b32 v229, v214 offset:1536
	ds_read_b32 v230, v214 offset:2048
	ds_read_b32 v231, v214 offset:2560
	ds_read_b32 v232, v214 offset:3072
	ds_read_b32 v233, v214 offset:3584
	ds_read_b32 v234, v214 offset:4096
	ds_read_b32 v235, v214 offset:4608
	ds_read_b32 v236, v214 offset:5120
	ds_read_b32 v237, v214 offset:5632
	ds_read_b32 v238, v214 offset:6144
	ds_read_b32 v239, v214 offset:6656
	ds_read_b32 v240, v214 offset:7168
	ds_read_b32 v241, v214 offset:7680
	s_waitcnt lgkmcnt(0)
	v_max_f32_e32 v226, v226, v226
	v_max_f32_e32 v227, v227, v227
	v_max_f32_e32 v228, v228, v228
	v_max_f32_e32 v229, v229, v229
	v_max_f32_e32 v230, v230, v230
	v_max_f32_e32 v231, v231, v231
	v_max_f32_e32 v232, v232, v232
	v_max_f32_e32 v233, v233, v233
	v_max_f32_e32 v234, v234, v234
	v_max_f32_e32 v235, v235, v235
	v_max_f32_e32 v236, v236, v236
	v_max_f32_e32 v237, v237, v237
	v_max_f32_e32 v238, v238, v238
	v_max_f32_e32 v239, v239, v239
	v_max_f32_e32 v240, v240, v240
	v_max_f32_e32 v241, v241, v241
	v_med3_f32 v226, v226, s62, v95
	v_med3_f32 v227, v227, s62, v95
	v_med3_f32 v228, v228, s62, v95
	v_med3_f32 v229, v229, s62, v95
	v_med3_f32 v230, v230, s62, v95
	v_med3_f32 v231, v231, s62, v95
	v_med3_f32 v232, v232, s62, v95
	v_med3_f32 v233, v233, s62, v95
	v_med3_f32 v234, v234, s62, v95
	v_med3_f32 v235, v235, s62, v95
	v_med3_f32 v236, v236, s62, v95
	v_med3_f32 v237, v237, s62, v95
	v_med3_f32 v238, v238, s62, v95
	v_med3_f32 v239, v239, s62, v95
	v_med3_f32 v240, v240, s62, v95
	v_med3_f32 v241, v241, s62, v95
	v_mov_b32_e32 v242, 0
	v_mov_b32_e32 v243, 0
	v_mov_b32_e32 v244, 0
	v_mov_b32_e32 v245, 0
	v_cvt_pk_fp8_f32 v242, v226, v227
	v_cvt_pk_fp8_f32 v243, v230, v231
	v_cvt_pk_fp8_f32 v244, v234, v235
	v_cvt_pk_fp8_f32 v245, v238, v239
	v_cvt_pk_fp8_f32 v242, v228, v229 op_sel:[0,0,1]
	v_cvt_pk_fp8_f32 v243, v232, v233 op_sel:[0,0,1]
	v_cvt_pk_fp8_f32 v244, v236, v237 op_sel:[0,0,1]
	v_cvt_pk_fp8_f32 v245, v240, v241 op_sel:[0,0,1]
	s_nop 0
	global_store_dwordx4 v92, v[242:245], s[6:7]
	s_waitcnt vmcnt(12)
	v_mul_f32_e32 v144, v50, v144
	v_mul_f32_e32 v145, v50, v145
	v_mul_f32_e32 v146, v50, v146
	v_mul_f32_e32 v147, v50, v147
	ds_write_b128 v209, v[144:147]
	v_mul_f32_e32 v148, v51, v148
	v_mul_f32_e32 v149, v51, v149
	v_mul_f32_e32 v150, v51, v150
	v_mul_f32_e32 v151, v51, v151
	ds_write_b128 v209, v[148:151] offset:1024
	v_mul_f32_e32 v152, v52, v152
	v_mul_f32_e32 v153, v52, v153
	v_mul_f32_e32 v154, v52, v154
	v_mul_f32_e32 v155, v52, v155
	ds_write_b128 v209, v[152:155] offset:2048
	v_mul_f32_e32 v156, v53, v156
	v_mul_f32_e32 v157, v53, v157
	v_mul_f32_e32 v158, v53, v158
	v_mul_f32_e32 v159, v53, v159
	ds_write_b128 v209, v[156:159] offset:3072
	v_mul_f32_e32 v160, v54, v160
	v_mul_f32_e32 v161, v54, v161
	v_mul_f32_e32 v162, v54, v162
	v_mul_f32_e32 v163, v54, v163
	ds_write_b128 v209, v[160:163] offset:4096
	v_mul_f32_e32 v164, v55, v164
	v_mul_f32_e32 v165, v55, v165
	v_mul_f32_e32 v166, v55, v166
	v_mul_f32_e32 v167, v55, v167
	ds_write_b128 v209, v[164:167] offset:5120
	v_mul_f32_e32 v168, v56, v168
	v_mul_f32_e32 v169, v56, v169
	v_mul_f32_e32 v170, v56, v170
	v_mul_f32_e32 v171, v56, v171
	ds_write_b128 v209, v[168:171] offset:6144
	v_mul_f32_e32 v172, v57, v172
	v_mul_f32_e32 v173, v57, v173
	v_mul_f32_e32 v174, v57, v174
	v_mul_f32_e32 v175, v57, v175
	ds_write_b128 v209, v[172:175] offset:7168
	s_waitcnt lgkmcnt(0)
	s_barrier
; #define GAS __attribute__((address_space(1)))
; #define LAS __attribute__((address_space(3)))
; #define LDS_WAIT() asm volatile("s_waitcnt lgkmcnt(0)" ::: "memory")
; __device__ __forceinline__ unsigned pk4_fp8(float a, float b, float c, float d) {
;     a = fminf(fmaxf(a, -448.f), 448.f); b = fminf(fmaxf(b, -448.f), 448.f); c = fminf(fmaxf(c, -448.f), 448.f); d = fminf(fmaxf(d, -448.f), 448.f);
;     int w = __builtin_amdgcn_cvt_pk_fp8_f32(a, b, 0, false); w = __builtin_amdgcn_cvt_pk_fp8_f32(c, d, w, true); return (unsigned)w; }
;     const int pr = item >> 1, kb = 2 * (pr / nblk) + (item & 1), nb = pr % nblk, k0 = 64 * kb, n0 = 32 * nb;
;     const int nr = n0 + (lane & 31); const int sc = MAP == 1 ? src_col_in(nr) : nr;
;     float v[32];
; #pragma unroll
;     for (int i = 0; i < 32; ++i) v[i] = sc >= 0 ? W[(size_t)(k0 + 2 * i + (lane >> 5)) * Nsrc + sc] : 0.f;
; #pragma unroll
;     for (int i = 0; i < 32; ++i) { const int k = k0 + 2 * i + (lane >> 5); float x = v[i] * wscale; if (KS) x *= (k < ksplit ? ksA[k] : ksB[k - ksplit]); scr[(2 * i + (lane >> 5)) * 33 + (lane & 31)] = x; }
;     LDS_WAIT(); asm volatile("" ::: "memory");
;     const int c = lane & 7;
; #pragma unroll
;     for (int j = 0; j < 4; ++j) { const int n = (lane >> 3) + 8 * j; const LAS float* s = scr + (8 * c) * 33 + n;
;         const unsigned long long o = (unsigned long long)pg8::pk4_fp8(s[0 * 33], s[1 * 33], s[2 * 33], s[3 * 33]) | ((unsigned long long)pg8::pk4_fp8(s[4 * 33], s[5 * 33], s[6 * 33], s[7 * 33]) << 32);
;         *(GAS unsigned long long*)(WT + (size_t)(n0 + n) * K + k0 + 8 * c) = o; }
;     LDS_WAIT(); asm volatile("" ::: "memory");
; }
	s_add_i32 s24, s23, 72
	s_lshl_b32 s20, s24, 7
	s_cmp_lt_u32 s24, 40
	s_cselect_b32 s21, 0, 0x830
	s_cmp_lt_u32 s24, 72
	s_cselect_b32 s21, s21, 0xfffff030
	s_add_i32 s20, s20, s21
	s_lshl_b32 s20, s20, 2
	s_add_u32 s8, s50, s20
	s_addc_u32 s9, s51, 0
	global_load_dwordx4 v[144:147], v76, s[8:9]
	s_add_u32 s8, s8, 0x16280
	s_addc_u32 s9, s9, 0
	global_load_dwordx4 v[148:151], v76, s[8:9]
	s_add_u32 s8, s8, 0x16280
	s_addc_u32 s9, s9, 0
	global_load_dwordx4 v[152:155], v76, s[8:9]
	s_add_u32 s8, s8, 0x16280
	s_addc_u32 s9, s9, 0
	global_load_dwordx4 v[156:159], v76, s[8:9]
	s_add_u32 s8, s8, 0x16280
	s_addc_u32 s9, s9, 0
	global_load_dwordx4 v[160:163], v76, s[8:9]
	s_add_u32 s8, s8, 0x16280
	s_addc_u32 s9, s9, 0
	global_load_dwordx4 v[164:167], v76, s[8:9]
	s_add_u32 s8, s8, 0x16280
	s_addc_u32 s9, s9, 0
	global_load_dwordx4 v[168:171], v76, s[8:9]
	s_add_u32 s8, s8, 0x16280
	s_addc_u32 s9, s9, 0
	global_load_dwordx4 v[172:175], v76, s[8:9]
	s_add_i32 s24, s23, 56
	s_mul_i32 s20, s24, 0x80000
	s_add_u32 s6, s52, s20
	s_addc_u32 s7, s53, 0
	s_cmp_lt_u32 s24, 16
	s_cselect_b32 s20, 1, 0
	s_sub_i32 s21, s24, 16
	s_bitcmp0_b32 s21, 2
	s_cselect_b32 s21, 1, 0
	s_cmp_lt_u32 s24, 40
	s_cselect_b32 s21, s21, 0
	s_or_b32 s20, s20, s21
	s_cmp_lg_u32 s20, 0
	s_cselect_b64 s[20:21], -1, 0
	v_cndmask_b32_e64 v91, v77, v81, s[20:21]
	v_cndmask_b32_e64 v92, v78, v82, s[20:21]
	ds_read_b32 v226, v211
	ds_read_b32 v227, v211 offset:512
	ds_read_b32 v228, v211 offset:1024
	ds_read_b32 v229, v211 offset:1536
	ds_read_b32 v230, v211 offset:2048
	ds_read_b32 v231, v211 offset:2560
	ds_read_b32 v232, v211 offset:3072
	ds_read_b32 v233, v211 offset:3584
	ds_read_b32 v234, v211 offset:4096
	ds_read_b32 v235, v211 offset:4608
	ds_read_b32 v236, v211 offset:5120
	ds_read_b32 v237, v211 offset:5632
	ds_read_b32 v238, v211 offset:6144
	ds_read_b32 v239, v211 offset:6656
	ds_read_b32 v240, v211 offset:7168
	ds_read_b32 v241, v211 offset:7680
	s_waitcnt lgkmcnt(0)
	v_max_f32_e32 v226, v226, v226
	v_max_f32_e32 v227, v227, v227
	v_max_f32_e32 v228, v228, v228
	v_max_f32_e32 v229, v229, v229
	v_max_f32_e32 v230, v230, v230
	v_max_f32_e32 v231, v231, v231
	v_max_f32_e32 v232, v232, v232
	v_max_f32_e32 v233, v233, v233
	v_max_f32_e32 v234, v234, v234
	v_max_f32_e32 v235, v235, v235
	v_max_f32_e32 v236, v236, v236
	v_max_f32_e32 v237, v237, v237
	v_max_f32_e32 v238, v238, v238
	v_max_f32_e32 v239, v239, v239
	v_max_f32_e32 v240, v240, v240
	v_max_f32_e32 v241, v241, v241
	v_med3_f32 v226, v226, s62, v95
	v_med3_f32 v227, v227, s62, v95
	v_med3_f32 v228, v228, s62, v95
	v_med3_f32 v229, v229, s62, v95
	v_med3_f32 v230, v230, s62, v95
	v_med3_f32 v231, v231, s62, v95
	v_med3_f32 v232, v232, s62, v95
	v_med3_f32 v233, v233, s62, v95
	v_med3_f32 v234, v234, s62, v95
	v_med3_f32 v235, v235, s62, v95
	v_med3_f32 v236, v236, s62, v95
	v_med3_f32 v237, v237, s62, v95
	v_med3_f32 v238, v238, s62, v95
	v_med3_f32 v239, v239, s62, v95
	v_med3_f32 v240, v240, s62, v95
	v_med3_f32 v241, v241, s62, v95
	v_mov_b32_e32 v242, 0
	v_mov_b32_e32 v243, 0
	v_mov_b32_e32 v244, 0
	v_mov_b32_e32 v245, 0
	v_cvt_pk_fp8_f32 v242, v226, v227
	v_cvt_pk_fp8_f32 v243, v230, v231
	v_cvt_pk_fp8_f32 v244, v234, v235
	v_cvt_pk_fp8_f32 v245, v238, v239
	v_cvt_pk_fp8_f32 v242, v228, v229 op_sel:[0,0,1]
	v_cvt_pk_fp8_f32 v243, v232, v233 op_sel:[0,0,1]
	v_cvt_pk_fp8_f32 v244, v236, v237 op_sel:[0,0,1]
	v_cvt_pk_fp8_f32 v245, v240, v241 op_sel:[0,0,1]
	s_nop 0
	global_store_dwordx4 v91, v[242:245], s[6:7]
	ds_read_b32 v226, v213
	ds_read_b32 v227, v213 offset:512
	ds_read_b32 v228, v213 offset:1024
	ds_read_b32 v229, v213 offset:1536
	ds_read_b32 v230, v213 offset:2048
	ds_read_b32 v231, v213 offset:2560
	ds_read_b32 v232, v213 offset:3072
	ds_read_b32 v233, v213 offset:3584
	ds_read_b32 v234, v213 offset:4096
	ds_read_b32 v235, v213 offset:4608
	ds_read_b32 v236, v213 offset:5120
	ds_read_b32 v237, v213 offset:5632
	ds_read_b32 v238, v213 offset:6144
	ds_read_b32 v239, v213 offset:6656
	ds_read_b32 v240, v213 offset:7168
	ds_read_b32 v241, v213 offset:7680
	s_waitcnt lgkmcnt(0)
	v_max_f32_e32 v226, v226, v226
	v_max_f32_e32 v227, v227, v227
	v_max_f32_e32 v228, v228, v228
	v_max_f32_e32 v229, v229, v229
	v_max_f32_e32 v230, v230, v230
	v_max_f32_e32 v231, v231, v231
	v_max_f32_e32 v232, v232, v232
	v_max_f32_e32 v233, v233, v233
	v_max_f32_e32 v234, v234, v234
	v_max_f32_e32 v235, v235, v235
	v_max_f32_e32 v236, v236, v236
	v_max_f32_e32 v237, v237, v237
	v_max_f32_e32 v238, v238, v238
	v_max_f32_e32 v239, v239, v239
	v_max_f32_e32 v240, v240, v240
	v_max_f32_e32 v241, v241, v241
	v_med3_f32 v226, v226, s62, v95
	v_med3_f32 v227, v227, s62, v95
	v_med3_f32 v228, v228, s62, v95
	v_med3_f32 v229, v229, s62, v95
	v_med3_f32 v230, v230, s62, v95
	v_med3_f32 v231, v231, s62, v95
	v_med3_f32 v232, v232, s62, v95
	v_med3_f32 v233, v233, s62, v95
	v_med3_f32 v234, v234, s62, v95
	v_med3_f32 v235, v235, s62, v95
	v_med3_f32 v236, v236, s62, v95
	v_med3_f32 v237, v237, s62, v95
	v_med3_f32 v238, v238, s62, v95
	v_med3_f32 v239, v239, s62, v95
	v_med3_f32 v240, v240, s62, v95
	v_med3_f32 v241, v241, s62, v95
	v_mov_b32_e32 v242, 0
	v_mov_b32_e32 v243, 0
	v_mov_b32_e32 v244, 0
	v_mov_b32_e32 v245, 0
	v_cvt_pk_fp8_f32 v242, v226, v227
	v_cvt_pk_fp8_f32 v243, v230, v231
	v_cvt_pk_fp8_f32 v244, v234, v235
	v_cvt_pk_fp8_f32 v245, v238, v239
	v_cvt_pk_fp8_f32 v242, v228, v229 op_sel:[0,0,1]
	v_cvt_pk_fp8_f32 v243, v232, v233 op_sel:[0,0,1]
	v_cvt_pk_fp8_f32 v244, v236, v237 op_sel:[0,0,1]
	v_cvt_pk_fp8_f32 v245, v240, v241 op_sel:[0,0,1]
	s_nop 0
	global_store_dwordx4 v92, v[242:245], s[6:7]
	s_waitcnt vmcnt(12)
	v_mul_f32_e32 v176, v50, v176
	v_mul_f32_e32 v177, v50, v177
	v_mul_f32_e32 v178, v50, v178
	v_mul_f32_e32 v179, v50, v179
	ds_write_b128 v210, v[176:179]
	v_mul_f32_e32 v180, v51, v180
	v_mul_f32_e32 v181, v51, v181
	v_mul_f32_e32 v182, v51, v182
	v_mul_f32_e32 v183, v51, v183
	ds_write_b128 v210, v[180:183] offset:1024
	v_mul_f32_e32 v184, v52, v184
	v_mul_f32_e32 v185, v52, v185
	v_mul_f32_e32 v186, v52, v186
	v_mul_f32_e32 v187, v52, v187
	ds_write_b128 v210, v[184:187] offset:2048
	v_mul_f32_e32 v188, v53, v188
	v_mul_f32_e32 v189, v53, v189
	v_mul_f32_e32 v190, v53, v190
	v_mul_f32_e32 v191, v53, v191
	ds_write_b128 v210, v[188:191] offset:3072
	v_mul_f32_e32 v192, v54, v192
	v_mul_f32_e32 v193, v54, v193
	v_mul_f32_e32 v194, v54, v194
	v_mul_f32_e32 v195, v54, v195
	ds_write_b128 v210, v[192:195] offset:4096
	v_mul_f32_e32 v196, v55, v196
	v_mul_f32_e32 v197, v55, v197
	v_mul_f32_e32 v198, v55, v198
	v_mul_f32_e32 v199, v55, v199
	ds_write_b128 v210, v[196:199] offset:5120
	v_mul_f32_e32 v200, v56, v200
	v_mul_f32_e32 v201, v56, v201
	v_mul_f32_e32 v202, v56, v202
	v_mul_f32_e32 v203, v56, v203
	ds_write_b128 v210, v[200:203] offset:6144
	v_mul_f32_e32 v204, v57, v204
	v_mul_f32_e32 v205, v57, v205
	v_mul_f32_e32 v206, v57, v206
	v_mul_f32_e32 v207, v57, v207
	ds_write_b128 v210, v[204:207] offset:7168
	s_waitcnt lgkmcnt(0)
	s_barrier
; #define GAS __attribute__((address_space(1)))
; #define LAS __attribute__((address_space(3)))
; #define LDS_WAIT() asm volatile("s_waitcnt lgkmcnt(0)" ::: "memory")
; __device__ __forceinline__ int src_col_in(int c) {
;     if (c < 5120) { const int blk = c >> 7, p = c & 127; const bool rope = blk < 16 || ((((blk - 16) >> 2) & 1) == 0); const int d = rope ? (p >> 1) + 64 * (p & 1) : p; return blk * 128 + d; }
;     if (c < OFF_Z) return c + 2096;
;     if (c < OFF_G) return c - 4048;
;     if (c < OFF_DT) return 5120 + (c - OFF_G);
;     if (c < NSRC) return c;
;     return -1;
; }
;     const int pr = item >> 1, kb = 2 * (pr / nblk) + (item & 1), nb = pr % nblk, k0 = 64 * kb, n0 = 32 * nb;
;     const int nr = n0 + (lane & 31); const int sc = MAP == 1 ? src_col_in(nr) : nr;
;     float v[32];
; #pragma unroll
;     for (int i = 0; i < 32; ++i) v[i] = sc >= 0 ? W[(size_t)(k0 + 2 * i + (lane >> 5)) * Nsrc + sc] : 0.f;
; #pragma unroll
;     for (int i = 0; i < 32; ++i) { const int k = k0 + 2 * i + (lane >> 5); float x = v[i] * wscale; if (KS) x *= (k < ksplit ? ksA[k] : ksB[k - ksplit]); scr[(2 * i + (lane >> 5)) * 33 + (lane & 31)] = x; }
;     LDS_WAIT(); asm volatile("" ::: "memory");
;     const int c = lane & 7;
; #pragma unroll
;     for (int j = 0; j < 4; ++j) { const int n = (lane >> 3) + 8 * j; const LAS float* s = scr + (8 * c) * 33 + n;
;         const unsigned long long o = (unsigned long long)pg8::pk4_fp8(s[0 * 33], s[1 * 33], s[2 * 33], s[3 * 33]) | ((unsigned long long)pg8::pk4_fp8(s[4 * 33], s[5 * 33], s[6 * 33], s[7 * 33]) << 32);
;         *(GAS unsigned long long*)(WT + (size_t)(n0 + n) * K + k0 + 8 * c) = o; }
;     LDS_WAIT(); asm volatile("" ::: "memory");
; }
	s_add_i32 s24, s23, 80
	s_lshl_b32 s20, s24, 7
	s_cmp_lt_u32 s24, 40
	s_cselect_b32 s21, 0, 0x830
	s_cmp_lt_u32 s24, 72
	s_cselect_b32 s21, s21, 0xfffff030
	s_add_i32 s20, s20, s21
	s_lshl_b32 s20, s20, 2
	s_add_u32 s8, s50, s20
	s_addc_u32 s9, s51, 0
	global_load_dwordx4 v[176:179], v76, s[8:9]
	s_add_u32 s8, s8, 0x16280
	s_addc_u32 s9, s9, 0
	global_load_dwordx4 v[180:183], v76, s[8:9]
	s_add_u32 s8, s8, 0x16280
	s_addc_u32 s9, s9, 0
	global_load_dwordx4 v[184:187], v76, s[8:9]
	s_add_u32 s8, s8, 0x16280
	s_addc_u32 s9, s9, 0
	global_load_dwordx4 v[188:191], v76, s[8:9]
	s_add_u32 s8, s8, 0x16280
	s_addc_u32 s9, s9, 0
	global_load_dwordx4 v[192:195], v76, s[8:9]
	s_add_u32 s8, s8, 0x16280
	s_addc_u32 s9, s9, 0
	global_load_dwordx4 v[196:199], v76, s[8:9]
	s_add_u32 s8, s8, 0x16280
	s_addc_u32 s9, s9, 0
	global_load_dwordx4 v[200:203], v76, s[8:9]
	s_add_u32 s8, s8, 0x16280
	s_addc_u32 s9, s9, 0
	global_load_dwordx4 v[204:207], v76, s[8:9]
	s_add_i32 s24, s23, 64
	s_mul_i32 s20, s24, 0x80000
	s_add_u32 s6, s52, s20
	s_addc_u32 s7, s53, 0
	s_cmp_lt_u32 s24, 16
	s_cselect_b32 s20, 1, 0
	s_sub_i32 s21, s24, 16
	s_bitcmp0_b32 s21, 2
	s_cselect_b32 s21, 1, 0
	s_cmp_lt_u32 s24, 40
	s_cselect_b32 s21, s21, 0
	s_or_b32 s20, s20, s21
	s_cmp_lg_u32 s20, 0
	s_cselect_b64 s[20:21], -1, 0
	v_cndmask_b32_e64 v91, v77, v81, s[20:21]
	v_cndmask_b32_e64 v92, v78, v82, s[20:21]
	ds_read_b32 v226, v212
	ds_read_b32 v227, v212 offset:512
	ds_read_b32 v228, v212 offset:1024
	ds_read_b32 v229, v212 offset:1536
	ds_read_b32 v230, v212 offset:2048
	ds_read_b32 v231, v212 offset:2560
	ds_read_b32 v232, v212 offset:3072
	ds_read_b32 v233, v212 offset:3584
	ds_read_b32 v234, v212 offset:4096
	ds_read_b32 v235, v212 offset:4608
	ds_read_b32 v236, v212 offset:5120
	ds_read_b32 v237, v212 offset:5632
	ds_read_b32 v238, v212 offset:6144
	ds_read_b32 v239, v212 offset:6656
	ds_read_b32 v240, v212 offset:7168
	ds_read_b32 v241, v212 offset:7680
	s_waitcnt lgkmcnt(0)
	v_max_f32_e32 v226, v226, v226
	v_max_f32_e32 v227, v227, v227
	v_max_f32_e32 v228, v228, v228
	v_max_f32_e32 v229, v229, v229
	v_max_f32_e32 v230, v230, v230
	v_max_f32_e32 v231, v231, v231
	v_max_f32_e32 v232, v232, v232
	v_max_f32_e32 v233, v233, v233
	v_max_f32_e32 v234, v234, v234
	v_max_f32_e32 v235, v235, v235
	v_max_f32_e32 v236, v236, v236
	v_max_f32_e32 v237, v237, v237
	v_max_f32_e32 v238, v238, v238
	v_max_f32_e32 v239, v239, v239
	v_max_f32_e32 v240, v240, v240
	v_max_f32_e32 v241, v241, v241
	v_med3_f32 v226, v226, s62, v95
	v_med3_f32 v227, v227, s62, v95
	v_med3_f32 v228, v228, s62, v95
	v_med3_f32 v229, v229, s62, v95
	v_med3_f32 v230, v230, s62, v95
	v_med3_f32 v231, v231, s62, v95
	v_med3_f32 v232, v232, s62, v95
	v_med3_f32 v233, v233, s62, v95
	v_med3_f32 v234, v234, s62, v95
	v_med3_f32 v235, v235, s62, v95
	v_med3_f32 v236, v236, s62, v95
	v_med3_f32 v237, v237, s62, v95
	v_med3_f32 v238, v238, s62, v95
	v_med3_f32 v239, v239, s62, v95
	v_med3_f32 v240, v240, s62, v95
	v_med3_f32 v241, v241, s62, v95
	v_mov_b32_e32 v242, 0
	v_mov_b32_e32 v243, 0
	v_mov_b32_e32 v244, 0
	v_mov_b32_e32 v245, 0
	v_cvt_pk_fp8_f32 v242, v226, v227
	v_cvt_pk_fp8_f32 v243, v230, v231
	v_cvt_pk_fp8_f32 v244, v234, v235
	v_cvt_pk_fp8_f32 v245, v238, v239
	v_cvt_pk_fp8_f32 v242, v228, v229 op_sel:[0,0,1]
	v_cvt_pk_fp8_f32 v243, v232, v233 op_sel:[0,0,1]
	v_cvt_pk_fp8_f32 v244, v236, v237 op_sel:[0,0,1]
	v_cvt_pk_fp8_f32 v245, v240, v241 op_sel:[0,0,1]
	s_nop 0
	global_store_dwordx4 v91, v[242:245], s[6:7]
	ds_read_b32 v226, v214
	ds_read_b32 v227, v214 offset:512
	ds_read_b32 v228, v214 offset:1024
	ds_read_b32 v229, v214 offset:1536
	ds_read_b32 v230, v214 offset:2048
	ds_read_b32 v231, v214 offset:2560
	ds_read_b32 v232, v214 offset:3072
	ds_read_b32 v233, v214 offset:3584
	ds_read_b32 v234, v214 offset:4096
	ds_read_b32 v235, v214 offset:4608
	ds_read_b32 v236, v214 offset:5120
	ds_read_b32 v237, v214 offset:5632
	ds_read_b32 v238, v214 offset:6144
	ds_read_b32 v239, v214 offset:6656
	ds_read_b32 v240, v214 offset:7168
	ds_read_b32 v241, v214 offset:7680
	s_waitcnt lgkmcnt(0)
	v_max_f32_e32 v226, v226, v226
	v_max_f32_e32 v227, v227, v227
	v_max_f32_e32 v228, v228, v228
	v_max_f32_e32 v229, v229, v229
	v_max_f32_e32 v230, v230, v230
	v_max_f32_e32 v231, v231, v231
	v_max_f32_e32 v232, v232, v232
	v_max_f32_e32 v233, v233, v233
	v_max_f32_e32 v234, v234, v234
	v_max_f32_e32 v235, v235, v235
	v_max_f32_e32 v236, v236, v236
	v_max_f32_e32 v237, v237, v237
	v_max_f32_e32 v238, v238, v238
	v_max_f32_e32 v239, v239, v239
	v_max_f32_e32 v240, v240, v240
	v_max_f32_e32 v241, v241, v241
	v_med3_f32 v226, v226, s62, v95
	v_med3_f32 v227, v227, s62, v95
	v_med3_f32 v228, v228, s62, v95
	v_med3_f32 v229, v229, s62, v95
	v_med3_f32 v230, v230, s62, v95
	v_med3_f32 v231, v231, s62, v95
	v_med3_f32 v232, v232, s62, v95
	v_med3_f32 v233, v233, s62, v95
	v_med3_f32 v234, v234, s62, v95
	v_med3_f32 v235, v235, s62, v95
	v_med3_f32 v236, v236, s62, v95
	v_med3_f32 v237, v237, s62, v95
	v_med3_f32 v238, v238, s62, v95
	v_med3_f32 v239, v239, s62, v95
	v_med3_f32 v240, v240, s62, v95
	v_med3_f32 v241, v241, s62, v95
	v_mov_b32_e32 v242, 0
	v_mov_b32_e32 v243, 0
	v_mov_b32_e32 v244, 0
	v_mov_b32_e32 v245, 0
	v_cvt_pk_fp8_f32 v242, v226, v227
	v_cvt_pk_fp8_f32 v243, v230, v231
	v_cvt_pk_fp8_f32 v244, v234, v235
	v_cvt_pk_fp8_f32 v245, v238, v239
	v_cvt_pk_fp8_f32 v242, v228, v229 op_sel:[0,0,1]
	v_cvt_pk_fp8_f32 v243, v232, v233 op_sel:[0,0,1]
	v_cvt_pk_fp8_f32 v244, v236, v237 op_sel:[0,0,1]
	v_cvt_pk_fp8_f32 v245, v240, v241 op_sel:[0,0,1]
	s_nop 0
	global_store_dwordx4 v92, v[242:245], s[6:7]
	s_waitcnt vmcnt(12)
	v_mul_f32_e32 v144, v50, v144
	v_mul_f32_e32 v145, v50, v145
	v_mul_f32_e32 v146, v50, v146
	v_mul_f32_e32 v147, v50, v147
	ds_write_b128 v209, v[144:147]
	v_mul_f32_e32 v148, v51, v148
	v_mul_f32_e32 v149, v51, v149
	v_mul_f32_e32 v150, v51, v150
	v_mul_f32_e32 v151, v51, v151
	ds_write_b128 v209, v[148:151] offset:1024
	v_mul_f32_e32 v152, v52, v152
	v_mul_f32_e32 v153, v52, v153
	v_mul_f32_e32 v154, v52, v154
	v_mul_f32_e32 v155, v52, v155
	ds_write_b128 v209, v[152:155] offset:2048
	v_mul_f32_e32 v156, v53, v156
	v_mul_f32_e32 v157, v53, v157
	v_mul_f32_e32 v158, v53, v158
	v_mul_f32_e32 v159, v53, v159
	ds_write_b128 v209, v[156:159] offset:3072
	v_mul_f32_e32 v160, v54, v160
	v_mul_f32_e32 v161, v54, v161
	v_mul_f32_e32 v162, v54, v162
	v_mul_f32_e32 v163, v54, v163
	ds_write_b128 v209, v[160:163] offset:4096
	v_mul_f32_e32 v164, v55, v164
	v_mul_f32_e32 v165, v55, v165
	v_mul_f32_e32 v166, v55, v166
	v_mul_f32_e32 v167, v55, v167
	ds_write_b128 v209, v[164:167] offset:5120
	v_mul_f32_e32 v168, v56, v168
	v_mul_f32_e32 v169, v56, v169
	v_mul_f32_e32 v170, v56, v170
	v_mul_f32_e32 v171, v56, v171
	ds_write_b128 v209, v[168:171] offset:6144
	v_mul_f32_e32 v172, v57, v172
	v_mul_f32_e32 v173, v57, v173
	v_mul_f32_e32 v174, v57, v174
	v_mul_f32_e32 v175, v57, v175
	ds_write_b128 v209, v[172:175] offset:7168
	s_waitcnt lgkmcnt(0)
	s_barrier
; template <int MAP, bool KS, bool KPERM = false>
; __device__ __forceinline__ void p0_transpose_item(const float* W, int K, int Nsrc, int nblk, bf16* WT, const float* ksA, const float* ksB, int ksplit, LAS float* scr, int item, int lane) {
;     const int kb = item / nblk, nb = item % nblk, k0 = 64 * kb, n0 = 32 * nb;
;     const int nr = n0 + (lane & 31); const int sc = MAP == 1 ? src_col_in(nr) : (MAP == 2 ? nat_dim(nr) : nr);
;     float v[32];
; #pragma unroll
;     for (int i = 0; i < 32; ++i) { const int k = k0 + 2 * i + (lane >> 5); const int ksrc = KPERM ? ((k & ~127) + nat_dim(k & 127)) : k;
;         v[i] = sc >= 0 ? W[(size_t)ksrc * Nsrc + sc] : 0.f; }
; #pragma unroll
;     for (int i = 0; i < 32; ++i) { const int kk = 2 * i + (lane >> 5); const int k = k0 + kk;
;         if (KS) v[i] *= (k < ksplit ? ksA[k] : ksB[k - ksplit]);
;         scr[kk * 33 + (lane & 31)] = v[i]; }
;     LDS_WAIT(); asm volatile("" ::: "memory");
;     const int c = lane & 7;
; #pragma unroll
;     for (int j = 0; j < 4; ++j) { const int n = (lane >> 3) + 8 * j; const LAS float* s = scr + (8 * c) * 33 + n;
;         v4u o; o.x = pk2(s[0 * 33], s[1 * 33]); o.y = pk2(s[2 * 33], s[3 * 33]); o.z = pk2(s[4 * 33], s[5 * 33]); o.w = pk2(s[6 * 33], s[7 * 33]);
;         *(GAS v4u*)(WT + (size_t)(n0 + n) * K + k0 + 8 * c) = o; }
;     LDS_WAIT(); asm volatile("" ::: "memory");
; }
;     const int pr = item >> 1, kb = 2 * (pr / nblk) + (item & 1), nb = pr % nblk, k0 = 64 * kb, n0 = 32 * nb;
;     const int nr = n0 + (lane & 31); const int sc = MAP == 1 ? src_col_in(nr) : nr;
;     float v[32];
; #pragma unroll
;     for (int i = 0; i < 32; ++i) v[i] = sc >= 0 ? W[(size_t)(k0 + 2 * i + (lane >> 5)) * Nsrc + sc] : 0.f;
; #pragma unroll
;     for (int i = 0; i < 32; ++i) { const int k = k0 + 2 * i + (lane >> 5); float x = v[i] * wscale; if (KS) x *= (k < ksplit ? ksA[k] : ksB[k - ksplit]); scr[(2 * i + (lane >> 5)) * 33 + (lane & 31)] = x; }
;     LDS_WAIT(); asm volatile("" ::: "memory");
;     const int c = lane & 7;
; #pragma unroll
;     for (int j = 0; j < 4; ++j) { const int n = (lane >> 3) + 8 * j; const LAS float* s = scr + (8 * c) * 33 + n;
;         const unsigned long long o = (unsigned long long)pg8::pk4_fp8(s[0 * 33], s[1 * 33], s[2 * 33], s[3 * 33]) | ((unsigned long long)pg8::pk4_fp8(s[4 * 33], s[5 * 33], s[6 * 33], s[7 * 33]) << 32);
	s_mov_b64 s[8:9], s[54:55]
	global_load_dwordx4 v[144:147], v75, s[8:9]
	s_add_u32 s8, s8, 0x8000
	s_addc_u32 s9, s9, 0
	global_load_dwordx4 v[148:151], v75, s[8:9]
	s_add_u32 s8, s8, 0x8000
	s_addc_u32 s9, s9, 0
	global_load_dwordx4 v[152:155], v75, s[8:9]
	s_add_u32 s8, s8, 0x8000
	s_addc_u32 s9, s9, 0
	global_load_dwordx4 v[156:159], v75, s[8:9]
	s_add_u32 s8, s8, 0x8000
	s_addc_u32 s9, s9, 0
	global_load_dwordx4 v[160:163], v75, s[8:9]
	s_add_u32 s8, s8, 0x8000
	s_addc_u32 s9, s9, 0
	global_load_dwordx4 v[164:167], v75, s[8:9]
	s_add_u32 s8, s8, 0x8000
	s_addc_u32 s9, s9, 0
	global_load_dwordx4 v[168:171], v75, s[8:9]
	s_add_u32 s8, s8, 0x8000
	s_addc_u32 s9, s9, 0
	global_load_dwordx4 v[172:175], v75, s[8:9]
	s_add_i32 s24, s23, 72
	s_mul_i32 s20, s24, 0x80000
	s_add_u32 s6, s52, s20
	s_addc_u32 s7, s53, 0
	s_cmp_lt_u32 s24, 16
	s_cselect_b32 s20, 1, 0
	s_sub_i32 s21, s24, 16
	s_bitcmp0_b32 s21, 2
	s_cselect_b32 s21, 1, 0
	s_cmp_lt_u32 s24, 40
	s_cselect_b32 s21, s21, 0
	s_or_b32 s20, s20, s21
	s_cmp_lg_u32 s20, 0
	s_cselect_b64 s[20:21], -1, 0
	v_cndmask_b32_e64 v91, v77, v81, s[20:21]
	v_cndmask_b32_e64 v92, v78, v82, s[20:21]
	ds_read_b32 v226, v211
	ds_read_b32 v227, v211 offset:512
	ds_read_b32 v228, v211 offset:1024
	ds_read_b32 v229, v211 offset:1536
	ds_read_b32 v230, v211 offset:2048
	ds_read_b32 v231, v211 offset:2560
	ds_read_b32 v232, v211 offset:3072
	ds_read_b32 v233, v211 offset:3584
	ds_read_b32 v234, v211 offset:4096
	ds_read_b32 v235, v211 offset:4608
	ds_read_b32 v236, v211 offset:5120
	ds_read_b32 v237, v211 offset:5632
	ds_read_b32 v238, v211 offset:6144
	ds_read_b32 v239, v211 offset:6656
	ds_read_b32 v240, v211 offset:7168
	ds_read_b32 v241, v211 offset:7680
	s_waitcnt lgkmcnt(0)
	v_max_f32_e32 v226, v226, v226
	v_max_f32_e32 v227, v227, v227
	v_max_f32_e32 v228, v228, v228
	v_max_f32_e32 v229, v229, v229
	v_max_f32_e32 v230, v230, v230
	v_max_f32_e32 v231, v231, v231
	v_max_f32_e32 v232, v232, v232
	v_max_f32_e32 v233, v233, v233
	v_max_f32_e32 v234, v234, v234
	v_max_f32_e32 v235, v235, v235
	v_max_f32_e32 v236, v236, v236
	v_max_f32_e32 v237, v237, v237
	v_max_f32_e32 v238, v238, v238
	v_max_f32_e32 v239, v239, v239
	v_max_f32_e32 v240, v240, v240
	v_max_f32_e32 v241, v241, v241
	v_med3_f32 v226, v226, s62, v95
	v_med3_f32 v227, v227, s62, v95
	v_med3_f32 v228, v228, s62, v95
	v_med3_f32 v229, v229, s62, v95
	v_med3_f32 v230, v230, s62, v95
	v_med3_f32 v231, v231, s62, v95
	v_med3_f32 v232, v232, s62, v95
	v_med3_f32 v233, v233, s62, v95
	v_med3_f32 v234, v234, s62, v95
	v_med3_f32 v235, v235, s62, v95
	v_med3_f32 v236, v236, s62, v95
	v_med3_f32 v237, v237, s62, v95
	v_med3_f32 v238, v238, s62, v95
	v_med3_f32 v239, v239, s62, v95
	v_med3_f32 v240, v240, s62, v95
	v_med3_f32 v241, v241, s62, v95
	v_mov_b32_e32 v242, 0
	v_mov_b32_e32 v243, 0
	v_mov_b32_e32 v244, 0
	v_mov_b32_e32 v245, 0
	v_cvt_pk_fp8_f32 v242, v226, v227
	v_cvt_pk_fp8_f32 v243, v230, v231
	v_cvt_pk_fp8_f32 v244, v234, v235
	v_cvt_pk_fp8_f32 v245, v238, v239
	v_cvt_pk_fp8_f32 v242, v228, v229 op_sel:[0,0,1]
	v_cvt_pk_fp8_f32 v243, v232, v233 op_sel:[0,0,1]
	v_cvt_pk_fp8_f32 v244, v236, v237 op_sel:[0,0,1]
	v_cvt_pk_fp8_f32 v245, v240, v241 op_sel:[0,0,1]
	s_nop 0
	global_store_dwordx4 v91, v[242:245], s[6:7]
	ds_read_b32 v226, v213
	ds_read_b32 v227, v213 offset:512
	ds_read_b32 v228, v213 offset:1024
	ds_read_b32 v229, v213 offset:1536
	ds_read_b32 v230, v213 offset:2048
	ds_read_b32 v231, v213 offset:2560
	ds_read_b32 v232, v213 offset:3072
	ds_read_b32 v233, v213 offset:3584
	ds_read_b32 v234, v213 offset:4096
	ds_read_b32 v235, v213 offset:4608
	ds_read_b32 v236, v213 offset:5120
	ds_read_b32 v237, v213 offset:5632
	ds_read_b32 v238, v213 offset:6144
	ds_read_b32 v239, v213 offset:6656
	ds_read_b32 v240, v213 offset:7168
	ds_read_b32 v241, v213 offset:7680
	s_waitcnt lgkmcnt(0)
	v_max_f32_e32 v226, v226, v226
	v_max_f32_e32 v227, v227, v227
	v_max_f32_e32 v228, v228, v228
	v_max_f32_e32 v229, v229, v229
	v_max_f32_e32 v230, v230, v230
	v_max_f32_e32 v231, v231, v231
	v_max_f32_e32 v232, v232, v232
	v_max_f32_e32 v233, v233, v233
	v_max_f32_e32 v234, v234, v234
	v_max_f32_e32 v235, v235, v235
	v_max_f32_e32 v236, v236, v236
	v_max_f32_e32 v237, v237, v237
	v_max_f32_e32 v238, v238, v238
	v_max_f32_e32 v239, v239, v239
	v_max_f32_e32 v240, v240, v240
	v_max_f32_e32 v241, v241, v241
	v_med3_f32 v226, v226, s62, v95
	v_med3_f32 v227, v227, s62, v95
	v_med3_f32 v228, v228, s62, v95
	v_med3_f32 v229, v229, s62, v95
	v_med3_f32 v230, v230, s62, v95
	v_med3_f32 v231, v231, s62, v95
	v_med3_f32 v232, v232, s62, v95
	v_med3_f32 v233, v233, s62, v95
	v_med3_f32 v234, v234, s62, v95
	v_med3_f32 v235, v235, s62, v95
	v_med3_f32 v236, v236, s62, v95
	v_med3_f32 v237, v237, s62, v95
	v_med3_f32 v238, v238, s62, v95
	v_med3_f32 v239, v239, s62, v95
	v_med3_f32 v240, v240, s62, v95
	v_med3_f32 v241, v241, s62, v95
	v_mov_b32_e32 v242, 0
	v_mov_b32_e32 v243, 0
	v_mov_b32_e32 v244, 0
	v_mov_b32_e32 v245, 0
	v_cvt_pk_fp8_f32 v242, v226, v227
	v_cvt_pk_fp8_f32 v243, v230, v231
	v_cvt_pk_fp8_f32 v244, v234, v235
	v_cvt_pk_fp8_f32 v245, v238, v239
	v_cvt_pk_fp8_f32 v242, v228, v229 op_sel:[0,0,1]
	v_cvt_pk_fp8_f32 v243, v232, v233 op_sel:[0,0,1]
	v_cvt_pk_fp8_f32 v244, v236, v237 op_sel:[0,0,1]
	v_cvt_pk_fp8_f32 v245, v240, v241 op_sel:[0,0,1]
	s_nop 0
	global_store_dwordx4 v92, v[242:245], s[6:7]
	s_waitcnt vmcnt(12)
	v_mul_f32_e32 v176, v50, v176
	v_mul_f32_e32 v177, v50, v177
	v_mul_f32_e32 v178, v50, v178
	v_mul_f32_e32 v179, v50, v179
	ds_write_b128 v210, v[176:179]
	v_mul_f32_e32 v180, v51, v180
	v_mul_f32_e32 v181, v51, v181
	v_mul_f32_e32 v182, v51, v182
	v_mul_f32_e32 v183, v51, v183
	ds_write_b128 v210, v[180:183] offset:1024
	v_mul_f32_e32 v184, v52, v184
	v_mul_f32_e32 v185, v52, v185
	v_mul_f32_e32 v186, v52, v186
	v_mul_f32_e32 v187, v52, v187
	ds_write_b128 v210, v[184:187] offset:2048
	v_mul_f32_e32 v188, v53, v188
	v_mul_f32_e32 v189, v53, v189
	v_mul_f32_e32 v190, v53, v190
	v_mul_f32_e32 v191, v53, v191
	ds_write_b128 v210, v[188:191] offset:3072
	v_mul_f32_e32 v192, v54, v192
	v_mul_f32_e32 v193, v54, v193
	v_mul_f32_e32 v194, v54, v194
	v_mul_f32_e32 v195, v54, v195
	ds_write_b128 v210, v[192:195] offset:4096
	v_mul_f32_e32 v196, v55, v196
	v_mul_f32_e32 v197, v55, v197
	v_mul_f32_e32 v198, v55, v198
	v_mul_f32_e32 v199, v55, v199
	ds_write_b128 v210, v[196:199] offset:5120
	v_mul_f32_e32 v200, v56, v200
	v_mul_f32_e32 v201, v56, v201
	v_mul_f32_e32 v202, v56, v202
	v_mul_f32_e32 v203, v56, v203
	ds_write_b128 v210, v[200:203] offset:6144
	v_mul_f32_e32 v204, v57, v204
	v_mul_f32_e32 v205, v57, v205
	v_mul_f32_e32 v206, v57, v206
	v_mul_f32_e32 v207, v57, v207
	ds_write_b128 v210, v[204:207] offset:7168
	s_waitcnt lgkmcnt(0)
	s_barrier
; template <int MAP, bool KS, bool KPERM = false>
; __device__ __forceinline__ void p0_transpose_item(const float* W, int K, int Nsrc, int nblk, bf16* WT, const float* ksA, const float* ksB, int ksplit, LAS float* scr, int item, int lane) {
;     const int kb = item / nblk, nb = item % nblk, k0 = 64 * kb, n0 = 32 * nb;
;     const int nr = n0 + (lane & 31); const int sc = MAP == 1 ? src_col_in(nr) : (MAP == 2 ? nat_dim(nr) : nr);
;     float v[32];
; #pragma unroll
;     for (int i = 0; i < 32; ++i) { const int k = k0 + 2 * i + (lane >> 5); const int ksrc = KPERM ? ((k & ~127) + nat_dim(k & 127)) : k;
;         v[i] = sc >= 0 ? W[(size_t)ksrc * Nsrc + sc] : 0.f; }
; #pragma unroll
;     for (int i = 0; i < 32; ++i) { const int kk = 2 * i + (lane >> 5); const int k = k0 + kk;
;         if (KS) v[i] *= (k < ksplit ? ksA[k] : ksB[k - ksplit]);
;         scr[kk * 33 + (lane & 31)] = v[i]; }
;     LDS_WAIT(); asm volatile("" ::: "memory");
;     const int c = lane & 7;
; #pragma unroll
;     for (int j = 0; j < 4; ++j) { const int n = (lane >> 3) + 8 * j; const LAS float* s = scr + (8 * c) * 33 + n;
;         v4u o; o.x = pk2(s[0 * 33], s[1 * 33]); o.y = pk2(s[2 * 33], s[3 * 33]); o.z = pk2(s[4 * 33], s[5 * 33]); o.w = pk2(s[6 * 33], s[7 * 33]);
;         *(GAS v4u*)(WT + (size_t)(n0 + n) * K + k0 + 8 * c) = o; }
;     LDS_WAIT(); asm volatile("" ::: "memory");
; }
;     const int pr = item >> 1, kb = 2 * (pr / nblk) + (item & 1), nb = pr % nblk, k0 = 64 * kb, n0 = 32 * nb;
;     const int nr = n0 + (lane & 31); const int sc = MAP == 1 ? src_col_in(nr) : nr;
;     float v[32];
; #pragma unroll
;     for (int i = 0; i < 32; ++i) v[i] = sc >= 0 ? W[(size_t)(k0 + 2 * i + (lane >> 5)) * Nsrc + sc] : 0.f;
; #pragma unroll
;     for (int i = 0; i < 32; ++i) { const int k = k0 + 2 * i + (lane >> 5); float x = v[i] * wscale; if (KS) x *= (k < ksplit ? ksA[k] : ksB[k - ksplit]); scr[(2 * i + (lane >> 5)) * 33 + (lane & 31)] = x; }
;     LDS_WAIT(); asm volatile("" ::: "memory");
;     const int c = lane & 7;
; #pragma unroll
;     for (int j = 0; j < 4; ++j) { const int n = (lane >> 3) + 8 * j; const LAS float* s = scr + (8 * c) * 33 + n;
;         const unsigned long long o = (unsigned long long)pg8::pk4_fp8(s[0 * 33], s[1 * 33], s[2 * 33], s[3 * 33]) | ((unsigned long long)pg8::pk4_fp8(s[4 * 33], s[5 * 33], s[6 * 33], s[7 * 33]) << 32);
	s_add_u32 s8, s54, 0x1000
	s_addc_u32 s9, s55, 0
	global_load_dwordx4 v[176:179], v75, s[8:9]
	s_add_u32 s8, s8, 0x8000
	s_addc_u32 s9, s9, 0
	global_load_dwordx4 v[180:183], v75, s[8:9]
	s_add_u32 s8, s8, 0x8000
	s_addc_u32 s9, s9, 0
	global_load_dwordx4 v[184:187], v75, s[8:9]
	s_add_u32 s8, s8, 0x8000
	s_addc_u32 s9, s9, 0
	global_load_dwordx4 v[188:191], v75, s[8:9]
	s_add_u32 s8, s8, 0x8000
	s_addc_u32 s9, s9, 0
	global_load_dwordx4 v[192:195], v75, s[8:9]
	s_add_u32 s8, s8, 0x8000
	s_addc_u32 s9, s9, 0
	global_load_dwordx4 v[196:199], v75, s[8:9]
	s_add_u32 s8, s8, 0x8000
	s_addc_u32 s9, s9, 0
	global_load_dwordx4 v[200:203], v75, s[8:9]
	s_add_u32 s8, s8, 0x8000
	s_addc_u32 s9, s9, 0
	global_load_dwordx4 v[204:207], v75, s[8:9]
	s_add_i32 s24, s23, 80
	s_mul_i32 s20, s24, 0x80000
	s_add_u32 s6, s52, s20
	s_addc_u32 s7, s53, 0
	s_cmp_lt_u32 s24, 16
	s_cselect_b32 s20, 1, 0
	s_sub_i32 s21, s24, 16
	s_bitcmp0_b32 s21, 2
	s_cselect_b32 s21, 1, 0
	s_cmp_lt_u32 s24, 40
	s_cselect_b32 s21, s21, 0
	s_or_b32 s20, s20, s21
	s_cmp_lg_u32 s20, 0
	s_cselect_b64 s[20:21], -1, 0
	v_cndmask_b32_e64 v91, v77, v81, s[20:21]
	v_cndmask_b32_e64 v92, v78, v82, s[20:21]
	ds_read_b32 v226, v212
	ds_read_b32 v227, v212 offset:512
	ds_read_b32 v228, v212 offset:1024
	ds_read_b32 v229, v212 offset:1536
	ds_read_b32 v230, v212 offset:2048
	ds_read_b32 v231, v212 offset:2560
	ds_read_b32 v232, v212 offset:3072
	ds_read_b32 v233, v212 offset:3584
	ds_read_b32 v234, v212 offset:4096
	ds_read_b32 v235, v212 offset:4608
	ds_read_b32 v236, v212 offset:5120
	ds_read_b32 v237, v212 offset:5632
	ds_read_b32 v238, v212 offset:6144
	ds_read_b32 v239, v212 offset:6656
	ds_read_b32 v240, v212 offset:7168
	ds_read_b32 v241, v212 offset:7680
	s_waitcnt lgkmcnt(0)
	v_max_f32_e32 v226, v226, v226
	v_max_f32_e32 v227, v227, v227
	v_max_f32_e32 v228, v228, v228
	v_max_f32_e32 v229, v229, v229
	v_max_f32_e32 v230, v230, v230
	v_max_f32_e32 v231, v231, v231
	v_max_f32_e32 v232, v232, v232
	v_max_f32_e32 v233, v233, v233
	v_max_f32_e32 v234, v234, v234
	v_max_f32_e32 v235, v235, v235
	v_max_f32_e32 v236, v236, v236
	v_max_f32_e32 v237, v237, v237
	v_max_f32_e32 v238, v238, v238
	v_max_f32_e32 v239, v239, v239
	v_max_f32_e32 v240, v240, v240
	v_max_f32_e32 v241, v241, v241
	v_med3_f32 v226, v226, s62, v95
	v_med3_f32 v227, v227, s62, v95
	v_med3_f32 v228, v228, s62, v95
	v_med3_f32 v229, v229, s62, v95
	v_med3_f32 v230, v230, s62, v95
	v_med3_f32 v231, v231, s62, v95
	v_med3_f32 v232, v232, s62, v95
	v_med3_f32 v233, v233, s62, v95
	v_med3_f32 v234, v234, s62, v95
	v_med3_f32 v235, v235, s62, v95
	v_med3_f32 v236, v236, s62, v95
	v_med3_f32 v237, v237, s62, v95
	v_med3_f32 v238, v238, s62, v95
	v_med3_f32 v239, v239, s62, v95
	v_med3_f32 v240, v240, s62, v95
	v_med3_f32 v241, v241, s62, v95
	v_mov_b32_e32 v242, 0
	v_mov_b32_e32 v243, 0
	v_mov_b32_e32 v244, 0
	v_mov_b32_e32 v245, 0
	v_cvt_pk_fp8_f32 v242, v226, v227
	v_cvt_pk_fp8_f32 v243, v230, v231
	v_cvt_pk_fp8_f32 v244, v234, v235
	v_cvt_pk_fp8_f32 v245, v238, v239
	v_cvt_pk_fp8_f32 v242, v228, v229 op_sel:[0,0,1]
	v_cvt_pk_fp8_f32 v243, v232, v233 op_sel:[0,0,1]
	v_cvt_pk_fp8_f32 v244, v236, v237 op_sel:[0,0,1]
	v_cvt_pk_fp8_f32 v245, v240, v241 op_sel:[0,0,1]
	s_nop 0
	global_store_dwordx4 v91, v[242:245], s[6:7]
	ds_read_b32 v226, v214
	ds_read_b32 v227, v214 offset:512
	ds_read_b32 v228, v214 offset:1024
	ds_read_b32 v229, v214 offset:1536
	ds_read_b32 v230, v214 offset:2048
	ds_read_b32 v231, v214 offset:2560
	ds_read_b32 v232, v214 offset:3072
	ds_read_b32 v233, v214 offset:3584
	ds_read_b32 v234, v214 offset:4096
	ds_read_b32 v235, v214 offset:4608
	ds_read_b32 v236, v214 offset:5120
	ds_read_b32 v237, v214 offset:5632
	ds_read_b32 v238, v214 offset:6144
	ds_read_b32 v239, v214 offset:6656
	ds_read_b32 v240, v214 offset:7168
	ds_read_b32 v241, v214 offset:7680
	s_waitcnt lgkmcnt(0)
	v_max_f32_e32 v226, v226, v226
	v_max_f32_e32 v227, v227, v227
	v_max_f32_e32 v228, v228, v228
	v_max_f32_e32 v229, v229, v229
	v_max_f32_e32 v230, v230, v230
	v_max_f32_e32 v231, v231, v231
	v_max_f32_e32 v232, v232, v232
	v_max_f32_e32 v233, v233, v233
	v_max_f32_e32 v234, v234, v234
	v_max_f32_e32 v235, v235, v235
	v_max_f32_e32 v236, v236, v236
	v_max_f32_e32 v237, v237, v237
	v_max_f32_e32 v238, v238, v238
	v_max_f32_e32 v239, v239, v239
	v_max_f32_e32 v240, v240, v240
	v_max_f32_e32 v241, v241, v241
	v_med3_f32 v226, v226, s62, v95
	v_med3_f32 v227, v227, s62, v95
	v_med3_f32 v228, v228, s62, v95
	v_med3_f32 v229, v229, s62, v95
	v_med3_f32 v230, v230, s62, v95
	v_med3_f32 v231, v231, s62, v95
	v_med3_f32 v232, v232, s62, v95
	v_med3_f32 v233, v233, s62, v95
	v_med3_f32 v234, v234, s62, v95
	v_med3_f32 v235, v235, s62, v95
	v_med3_f32 v236, v236, s62, v95
	v_med3_f32 v237, v237, s62, v95
	v_med3_f32 v238, v238, s62, v95
	v_med3_f32 v239, v239, s62, v95
	v_med3_f32 v240, v240, s62, v95
	v_med3_f32 v241, v241, s62, v95
	v_mov_b32_e32 v242, 0
	v_mov_b32_e32 v243, 0
	v_mov_b32_e32 v244, 0
	v_mov_b32_e32 v245, 0
	v_cvt_pk_fp8_f32 v242, v226, v227
	v_cvt_pk_fp8_f32 v243, v230, v231
	v_cvt_pk_fp8_f32 v244, v234, v235
	v_cvt_pk_fp8_f32 v245, v238, v239
	v_cvt_pk_fp8_f32 v242, v228, v229 op_sel:[0,0,1]
	v_cvt_pk_fp8_f32 v243, v232, v233 op_sel:[0,0,1]
	v_cvt_pk_fp8_f32 v244, v236, v237 op_sel:[0,0,1]
	v_cvt_pk_fp8_f32 v245, v240, v241 op_sel:[0,0,1]
	s_nop 0
	global_store_dwordx4 v92, v[242:245], s[6:7]
	s_waitcnt vmcnt(12)
	v_mul_f32_e32 v144, v58, v144
	v_mul_f32_e32 v145, v58, v145
	v_mul_f32_e32 v146, v58, v146
	v_mul_f32_e32 v147, v58, v147
	ds_write_b128 v209, v[144:147]
	v_mul_f32_e32 v148, v59, v148
	v_mul_f32_e32 v149, v59, v149
	v_mul_f32_e32 v150, v59, v150
	v_mul_f32_e32 v151, v59, v151
	ds_write_b128 v209, v[148:151] offset:1024
	v_mul_f32_e32 v152, v60, v152
	v_mul_f32_e32 v153, v60, v153
	v_mul_f32_e32 v154, v60, v154
	v_mul_f32_e32 v155, v60, v155
	ds_write_b128 v209, v[152:155] offset:2048
	v_mul_f32_e32 v156, v61, v156
	v_mul_f32_e32 v157, v61, v157
	v_mul_f32_e32 v158, v61, v158
	v_mul_f32_e32 v159, v61, v159
	ds_write_b128 v209, v[156:159] offset:3072
	v_mul_f32_e32 v160, v62, v160
	v_mul_f32_e32 v161, v62, v161
	v_mul_f32_e32 v162, v62, v162
	v_mul_f32_e32 v163, v62, v163
	ds_write_b128 v209, v[160:163] offset:4096
	v_mul_f32_e32 v164, v63, v164
	v_mul_f32_e32 v165, v63, v165
	v_mul_f32_e32 v166, v63, v166
	v_mul_f32_e32 v167, v63, v167
	ds_write_b128 v209, v[164:167] offset:5120
	v_mul_f32_e32 v168, v64, v168
	v_mul_f32_e32 v169, v64, v169
	v_mul_f32_e32 v170, v64, v170
	v_mul_f32_e32 v171, v64, v171
	ds_write_b128 v209, v[168:171] offset:6144
	v_mul_f32_e32 v172, v65, v172
	v_mul_f32_e32 v173, v65, v173
	v_mul_f32_e32 v174, v65, v174
	v_mul_f32_e32 v175, v65, v175
	ds_write_b128 v209, v[172:175] offset:7168
	s_waitcnt lgkmcnt(0)
	s_barrier
; #define GAS __attribute__((address_space(1)))
; #define LAS __attribute__((address_space(3)))
; #define LDS_WAIT() asm volatile("s_waitcnt lgkmcnt(0)" ::: "memory")
; __device__ __forceinline__ unsigned pk2(float lo, float hi) { return f2bf(lo) | (f2bf(hi) << 16); }
; __device__ __forceinline__ int nat_dim(int p) { return (p >> 1) + 64 * (p & 1); }
; template <int MAP, bool KS, bool KPERM = false>
; __device__ __forceinline__ void p0_transpose_item(const float* W, int K, int Nsrc, int nblk, bf16* WT, const float* ksA, const float* ksB, int ksplit, LAS float* scr, int item, int lane) {
;     const int kb = item / nblk, nb = item % nblk, k0 = 64 * kb, n0 = 32 * nb;
;     const int nr = n0 + (lane & 31); const int sc = MAP == 1 ? src_col_in(nr) : (MAP == 2 ? nat_dim(nr) : nr);
;     float v[32];
; #pragma unroll
;     for (int i = 0; i < 32; ++i) { const int k = k0 + 2 * i + (lane >> 5); const int ksrc = KPERM ? ((k & ~127) + nat_dim(k & 127)) : k;
;         v[i] = sc >= 0 ? W[(size_t)ksrc * Nsrc + sc] : 0.f; }
; #pragma unroll
;     for (int i = 0; i < 32; ++i) { const int kk = 2 * i + (lane >> 5); const int k = k0 + kk;
;         if (KS) v[i] *= (k < ksplit ? ksA[k] : ksB[k - ksplit]);
;         scr[kk * 33 + (lane & 31)] = v[i]; }
;     LDS_WAIT(); asm volatile("" ::: "memory");
;     const int c = lane & 7;
; #pragma unroll
;     for (int j = 0; j < 4; ++j) { const int n = (lane >> 3) + 8 * j; const LAS float* s = scr + (8 * c) * 33 + n;
;         v4u o; o.x = pk2(s[0 * 33], s[1 * 33]); o.y = pk2(s[2 * 33], s[3 * 33]); o.z = pk2(s[4 * 33], s[5 * 33]); o.w = pk2(s[6 * 33], s[7 * 33]);
;         *(GAS v4u*)(WT + (size_t)(n0 + n) * K + k0 + 8 * c) = o; }
;     LDS_WAIT(); asm volatile("" ::: "memory");
; }
	s_add_u32 s8, s54, 0x2000
	s_addc_u32 s9, s55, 0
	global_load_dwordx4 v[144:147], v75, s[8:9]
	s_add_u32 s8, s8, 0x8000
	s_addc_u32 s9, s9, 0
	global_load_dwordx4 v[148:151], v75, s[8:9]
	s_add_u32 s8, s8, 0x8000
	s_addc_u32 s9, s9, 0
	global_load_dwordx4 v[152:155], v75, s[8:9]
	s_add_u32 s8, s8, 0x8000
	s_addc_u32 s9, s9, 0
	global_load_dwordx4 v[156:159], v75, s[8:9]
	s_add_u32 s8, s8, 0x8000
	s_addc_u32 s9, s9, 0
	global_load_dwordx4 v[160:163], v75, s[8:9]
	s_add_u32 s8, s8, 0x8000
	s_addc_u32 s9, s9, 0
	global_load_dwordx4 v[164:167], v75, s[8:9]
	s_add_u32 s8, s8, 0x8000
	s_addc_u32 s9, s9, 0
	global_load_dwordx4 v[168:171], v75, s[8:9]
	s_add_u32 s8, s8, 0x8000
	s_addc_u32 s9, s9, 0
	global_load_dwordx4 v[172:175], v75, s[8:9]
	s_mov_b64 s[6:7], s[56:57]
	ds_read_b32 v226, v112
	ds_read_b32 v227, v112 offset:512
	ds_read_b32 v228, v112 offset:1024
	ds_read_b32 v229, v112 offset:1536
	ds_read_b32 v230, v112 offset:2048
	ds_read_b32 v231, v112 offset:2560
	ds_read_b32 v232, v112 offset:3072
	ds_read_b32 v233, v112 offset:3584
	s_waitcnt lgkmcnt(0)
	v_bfe_u32 v120, v226, 16, 1
	v_bfe_u32 v121, v227, 16, 1
	v_bfe_u32 v122, v228, 16, 1
	v_bfe_u32 v123, v229, 16, 1
	v_bfe_u32 v124, v230, 16, 1
	v_bfe_u32 v125, v231, 16, 1
	v_bfe_u32 v126, v232, 16, 1
	v_bfe_u32 v127, v233, 16, 1
	v_add3_u32 v226, v226, v120, s63
	v_add3_u32 v227, v227, v121, s63
	v_add3_u32 v228, v228, v122, s63
	v_add3_u32 v229, v229, v123, s63
	v_add3_u32 v230, v230, v124, s63
	v_add3_u32 v231, v231, v125, s63
	v_add3_u32 v232, v232, v126, s63
	v_add3_u32 v233, v233, v127, s63
	v_perm_b32 v242, v227, v226, s64
	v_perm_b32 v243, v229, v228, s64
	v_perm_b32 v244, v231, v230, s64
	v_perm_b32 v245, v233, v232, s64
	s_nop 0
	global_store_dwordx4 v83, v[242:245], s[6:7]
	ds_read_b32 v226, v114
	ds_read_b32 v227, v114 offset:512
	ds_read_b32 v228, v114 offset:1024
	ds_read_b32 v229, v114 offset:1536
	ds_read_b32 v230, v114 offset:2048
	ds_read_b32 v231, v114 offset:2560
	ds_read_b32 v232, v114 offset:3072
	ds_read_b32 v233, v114 offset:3584
	s_waitcnt lgkmcnt(0)
	v_bfe_u32 v120, v226, 16, 1
	v_bfe_u32 v121, v227, 16, 1
	v_bfe_u32 v122, v228, 16, 1
	v_bfe_u32 v123, v229, 16, 1
	v_bfe_u32 v124, v230, 16, 1
	v_bfe_u32 v125, v231, 16, 1
	v_bfe_u32 v126, v232, 16, 1
	v_bfe_u32 v127, v233, 16, 1
	v_add3_u32 v226, v226, v120, s63
	v_add3_u32 v227, v227, v121, s63
	v_add3_u32 v228, v228, v122, s63
	v_add3_u32 v229, v229, v123, s63
	v_add3_u32 v230, v230, v124, s63
	v_add3_u32 v231, v231, v125, s63
	v_add3_u32 v232, v232, v126, s63
	v_add3_u32 v233, v233, v127, s63
	v_perm_b32 v242, v227, v226, s64
	v_perm_b32 v243, v229, v228, s64
	v_perm_b32 v244, v231, v230, s64
	v_perm_b32 v245, v233, v232, s64
	s_nop 0
	global_store_dwordx4 v84, v[242:245], s[6:7]
	ds_read_b32 v226, v116
	ds_read_b32 v227, v116 offset:512
	ds_read_b32 v228, v116 offset:1024
	ds_read_b32 v229, v116 offset:1536
	ds_read_b32 v230, v116 offset:2048
	ds_read_b32 v231, v116 offset:2560
	ds_read_b32 v232, v116 offset:3072
	ds_read_b32 v233, v116 offset:3584
	s_waitcnt lgkmcnt(0)
	v_bfe_u32 v120, v226, 16, 1
	v_bfe_u32 v121, v227, 16, 1
	v_bfe_u32 v122, v228, 16, 1
	v_bfe_u32 v123, v229, 16, 1
	v_bfe_u32 v124, v230, 16, 1
	v_bfe_u32 v125, v231, 16, 1
	v_bfe_u32 v126, v232, 16, 1
	v_bfe_u32 v127, v233, 16, 1
	v_add3_u32 v226, v226, v120, s63
	v_add3_u32 v227, v227, v121, s63
	v_add3_u32 v228, v228, v122, s63
	v_add3_u32 v229, v229, v123, s63
	v_add3_u32 v230, v230, v124, s63
	v_add3_u32 v231, v231, v125, s63
	v_add3_u32 v232, v232, v126, s63
	v_add3_u32 v233, v233, v127, s63
	v_perm_b32 v242, v227, v226, s64
	v_perm_b32 v243, v229, v228, s64
	v_perm_b32 v244, v231, v230, s64
	v_perm_b32 v245, v233, v232, s64
	s_nop 0
	global_store_dwordx4 v85, v[242:245], s[6:7]
	ds_read_b32 v226, v118
	ds_read_b32 v227, v118 offset:512
	ds_read_b32 v228, v118 offset:1024
	ds_read_b32 v229, v118 offset:1536
	ds_read_b32 v230, v118 offset:2048
	ds_read_b32 v231, v118 offset:2560
	ds_read_b32 v232, v118 offset:3072
	ds_read_b32 v233, v118 offset:3584
	s_waitcnt lgkmcnt(0)
	v_bfe_u32 v120, v226, 16, 1
	v_bfe_u32 v121, v227, 16, 1
	v_bfe_u32 v122, v228, 16, 1
	v_bfe_u32 v123, v229, 16, 1
	v_bfe_u32 v124, v230, 16, 1
	v_bfe_u32 v125, v231, 16, 1
	v_bfe_u32 v126, v232, 16, 1
	v_bfe_u32 v127, v233, 16, 1
	v_add3_u32 v226, v226, v120, s63
	v_add3_u32 v227, v227, v121, s63
	v_add3_u32 v228, v228, v122, s63
	v_add3_u32 v229, v229, v123, s63
	v_add3_u32 v230, v230, v124, s63
	v_add3_u32 v231, v231, v125, s63
	v_add3_u32 v232, v232, v126, s63
	v_add3_u32 v233, v233, v127, s63
	v_perm_b32 v242, v227, v226, s64
	v_perm_b32 v243, v229, v228, s64
	v_perm_b32 v244, v231, v230, s64
	v_perm_b32 v245, v233, v232, s64
	s_nop 0
	global_store_dwordx4 v86, v[242:245], s[6:7]
	s_waitcnt vmcnt(14)
	v_mul_f32_e32 v176, v58, v176
	v_mul_f32_e32 v177, v58, v177
	v_mul_f32_e32 v178, v58, v178
	v_mul_f32_e32 v179, v58, v179
	ds_write_b128 v210, v[176:179]
	v_mul_f32_e32 v180, v59, v180
	v_mul_f32_e32 v181, v59, v181
	v_mul_f32_e32 v182, v59, v182
	v_mul_f32_e32 v183, v59, v183
	ds_write_b128 v210, v[180:183] offset:1024
	v_mul_f32_e32 v184, v60, v184
	v_mul_f32_e32 v185, v60, v185
	v_mul_f32_e32 v186, v60, v186
	v_mul_f32_e32 v187, v60, v187
	ds_write_b128 v210, v[184:187] offset:2048
	v_mul_f32_e32 v188, v61, v188
	v_mul_f32_e32 v189, v61, v189
	v_mul_f32_e32 v190, v61, v190
	v_mul_f32_e32 v191, v61, v191
	ds_write_b128 v210, v[188:191] offset:3072
	v_mul_f32_e32 v192, v62, v192
	v_mul_f32_e32 v193, v62, v193
	v_mul_f32_e32 v194, v62, v194
	v_mul_f32_e32 v195, v62, v195
	ds_write_b128 v210, v[192:195] offset:4096
	v_mul_f32_e32 v196, v63, v196
	v_mul_f32_e32 v197, v63, v197
	v_mul_f32_e32 v198, v63, v198
	v_mul_f32_e32 v199, v63, v199
	ds_write_b128 v210, v[196:199] offset:5120
	v_mul_f32_e32 v200, v64, v200
	v_mul_f32_e32 v201, v64, v201
	v_mul_f32_e32 v202, v64, v202
	v_mul_f32_e32 v203, v64, v203
	ds_write_b128 v210, v[200:203] offset:6144
	v_mul_f32_e32 v204, v65, v204
	v_mul_f32_e32 v205, v65, v205
	v_mul_f32_e32 v206, v65, v206
	v_mul_f32_e32 v207, v65, v207
	ds_write_b128 v210, v[204:207] offset:7168
	s_waitcnt lgkmcnt(0)
	s_barrier
; #define GAS __attribute__((address_space(1)))
; #define LAS __attribute__((address_space(3)))
; #define LDS_WAIT() asm volatile("s_waitcnt lgkmcnt(0)" ::: "memory")
; __device__ __forceinline__ unsigned pk2(float lo, float hi) { return f2bf(lo) | (f2bf(hi) << 16); }
; __device__ __forceinline__ int nat_dim(int p) { return (p >> 1) + 64 * (p & 1); }
; template <int MAP, bool KS, bool KPERM = false>
; __device__ __forceinline__ void p0_transpose_item(const float* W, int K, int Nsrc, int nblk, bf16* WT, const float* ksA, const float* ksB, int ksplit, LAS float* scr, int item, int lane) {
;     const int kb = item / nblk, nb = item % nblk, k0 = 64 * kb, n0 = 32 * nb;
;     const int nr = n0 + (lane & 31); const int sc = MAP == 1 ? src_col_in(nr) : (MAP == 2 ? nat_dim(nr) : nr);
;     float v[32];
; #pragma unroll
;     for (int i = 0; i < 32; ++i) { const int k = k0 + 2 * i + (lane >> 5); const int ksrc = KPERM ? ((k & ~127) + nat_dim(k & 127)) : k;
;         v[i] = sc >= 0 ? W[(size_t)ksrc * Nsrc + sc] : 0.f; }
; #pragma unroll
;     for (int i = 0; i < 32; ++i) { const int kk = 2 * i + (lane >> 5); const int k = k0 + kk;
;         if (KS) v[i] *= (k < ksplit ? ksA[k] : ksB[k - ksplit]);
;         scr[kk * 33 + (lane & 31)] = v[i]; }
;     LDS_WAIT(); asm volatile("" ::: "memory");
;     const int c = lane & 7;
; #pragma unroll
;     for (int j = 0; j < 4; ++j) { const int n = (lane >> 3) + 8 * j; const LAS float* s = scr + (8 * c) * 33 + n;
;         v4u o; o.x = pk2(s[0 * 33], s[1 * 33]); o.y = pk2(s[2 * 33], s[3 * 33]); o.z = pk2(s[4 * 33], s[5 * 33]); o.w = pk2(s[6 * 33], s[7 * 33]);
;         *(GAS v4u*)(WT + (size_t)(n0 + n) * K + k0 + 8 * c) = o; }
;     LDS_WAIT(); asm volatile("" ::: "memory");
; }
	s_add_u32 s8, s54, 0x3000
	s_addc_u32 s9, s55, 0
	global_load_dwordx4 v[176:179], v75, s[8:9]
	s_add_u32 s8, s8, 0x8000
	s_addc_u32 s9, s9, 0
	global_load_dwordx4 v[180:183], v75, s[8:9]
	s_add_u32 s8, s8, 0x8000
	s_addc_u32 s9, s9, 0
	global_load_dwordx4 v[184:187], v75, s[8:9]
	s_add_u32 s8, s8, 0x8000
	s_addc_u32 s9, s9, 0
	global_load_dwordx4 v[188:191], v75, s[8:9]
	s_add_u32 s8, s8, 0x8000
	s_addc_u32 s9, s9, 0
	global_load_dwordx4 v[192:195], v75, s[8:9]
	s_add_u32 s8, s8, 0x8000
	s_addc_u32 s9, s9, 0
	global_load_dwordx4 v[196:199], v75, s[8:9]
	s_add_u32 s8, s8, 0x8000
	s_addc_u32 s9, s9, 0
	global_load_dwordx4 v[200:203], v75, s[8:9]
	s_add_u32 s8, s8, 0x8000
	s_addc_u32 s9, s9, 0
	global_load_dwordx4 v[204:207], v75, s[8:9]
	s_add_u32 s6, s56, 0x800000
	s_addc_u32 s7, s57, 0
	ds_read_b32 v226, v113
	ds_read_b32 v227, v113 offset:512
	ds_read_b32 v228, v113 offset:1024
	ds_read_b32 v229, v113 offset:1536
	ds_read_b32 v230, v113 offset:2048
	ds_read_b32 v231, v113 offset:2560
	ds_read_b32 v232, v113 offset:3072
	ds_read_b32 v233, v113 offset:3584
	s_waitcnt lgkmcnt(0)
	v_bfe_u32 v120, v226, 16, 1
	v_bfe_u32 v121, v227, 16, 1
	v_bfe_u32 v122, v228, 16, 1
	v_bfe_u32 v123, v229, 16, 1
	v_bfe_u32 v124, v230, 16, 1
	v_bfe_u32 v125, v231, 16, 1
	v_bfe_u32 v126, v232, 16, 1
	v_bfe_u32 v127, v233, 16, 1
	v_add3_u32 v226, v226, v120, s63
	v_add3_u32 v227, v227, v121, s63
	v_add3_u32 v228, v228, v122, s63
	v_add3_u32 v229, v229, v123, s63
	v_add3_u32 v230, v230, v124, s63
	v_add3_u32 v231, v231, v125, s63
	v_add3_u32 v232, v232, v126, s63
	v_add3_u32 v233, v233, v127, s63
	v_perm_b32 v242, v227, v226, s64
	v_perm_b32 v243, v229, v228, s64
	v_perm_b32 v244, v231, v230, s64
	v_perm_b32 v245, v233, v232, s64
	s_nop 0
	global_store_dwordx4 v83, v[242:245], s[6:7]
	ds_read_b32 v226, v115
	ds_read_b32 v227, v115 offset:512
	ds_read_b32 v228, v115 offset:1024
	ds_read_b32 v229, v115 offset:1536
	ds_read_b32 v230, v115 offset:2048
	ds_read_b32 v231, v115 offset:2560
	ds_read_b32 v232, v115 offset:3072
	ds_read_b32 v233, v115 offset:3584
	s_waitcnt lgkmcnt(0)
	v_bfe_u32 v120, v226, 16, 1
	v_bfe_u32 v121, v227, 16, 1
	v_bfe_u32 v122, v228, 16, 1
	v_bfe_u32 v123, v229, 16, 1
	v_bfe_u32 v124, v230, 16, 1
	v_bfe_u32 v125, v231, 16, 1
	v_bfe_u32 v126, v232, 16, 1
	v_bfe_u32 v127, v233, 16, 1
	v_add3_u32 v226, v226, v120, s63
	v_add3_u32 v227, v227, v121, s63
	v_add3_u32 v228, v228, v122, s63
	v_add3_u32 v229, v229, v123, s63
	v_add3_u32 v230, v230, v124, s63
	v_add3_u32 v231, v231, v125, s63
	v_add3_u32 v232, v232, v126, s63
	v_add3_u32 v233, v233, v127, s63
	v_perm_b32 v242, v227, v226, s64
	v_perm_b32 v243, v229, v228, s64
	v_perm_b32 v244, v231, v230, s64
	v_perm_b32 v245, v233, v232, s64
	s_nop 0
	global_store_dwordx4 v84, v[242:245], s[6:7]
	ds_read_b32 v226, v117
	ds_read_b32 v227, v117 offset:512
	ds_read_b32 v228, v117 offset:1024
	ds_read_b32 v229, v117 offset:1536
	ds_read_b32 v230, v117 offset:2048
	ds_read_b32 v231, v117 offset:2560
	ds_read_b32 v232, v117 offset:3072
	ds_read_b32 v233, v117 offset:3584
	s_waitcnt lgkmcnt(0)
	v_bfe_u32 v120, v226, 16, 1
	v_bfe_u32 v121, v227, 16, 1
	v_bfe_u32 v122, v228, 16, 1
	v_bfe_u32 v123, v229, 16, 1
	v_bfe_u32 v124, v230, 16, 1
	v_bfe_u32 v125, v231, 16, 1
	v_bfe_u32 v126, v232, 16, 1
	v_bfe_u32 v127, v233, 16, 1
	v_add3_u32 v226, v226, v120, s63
	v_add3_u32 v227, v227, v121, s63
	v_add3_u32 v228, v228, v122, s63
	v_add3_u32 v229, v229, v123, s63
	v_add3_u32 v230, v230, v124, s63
	v_add3_u32 v231, v231, v125, s63
	v_add3_u32 v232, v232, v126, s63
	v_add3_u32 v233, v233, v127, s63
	v_perm_b32 v242, v227, v226, s64
	v_perm_b32 v243, v229, v228, s64
	v_perm_b32 v244, v231, v230, s64
	v_perm_b32 v245, v233, v232, s64
	s_nop 0
	global_store_dwordx4 v85, v[242:245], s[6:7]
	ds_read_b32 v226, v119
	ds_read_b32 v227, v119 offset:512
	ds_read_b32 v228, v119 offset:1024
	ds_read_b32 v229, v119 offset:1536
	ds_read_b32 v230, v119 offset:2048
	ds_read_b32 v231, v119 offset:2560
	ds_read_b32 v232, v119 offset:3072
	ds_read_b32 v233, v119 offset:3584
	s_waitcnt lgkmcnt(0)
	v_bfe_u32 v120, v226, 16, 1
	v_bfe_u32 v121, v227, 16, 1
	v_bfe_u32 v122, v228, 16, 1
	v_bfe_u32 v123, v229, 16, 1
	v_bfe_u32 v124, v230, 16, 1
	v_bfe_u32 v125, v231, 16, 1
	v_bfe_u32 v126, v232, 16, 1
	v_bfe_u32 v127, v233, 16, 1
	v_add3_u32 v226, v226, v120, s63
	v_add3_u32 v227, v227, v121, s63
	v_add3_u32 v228, v228, v122, s63
	v_add3_u32 v229, v229, v123, s63
	v_add3_u32 v230, v230, v124, s63
	v_add3_u32 v231, v231, v125, s63
	v_add3_u32 v232, v232, v126, s63
	v_add3_u32 v233, v233, v127, s63
	v_perm_b32 v242, v227, v226, s64
	v_perm_b32 v243, v229, v228, s64
	v_perm_b32 v244, v231, v230, s64
	v_perm_b32 v245, v233, v232, s64
	s_nop 0
	global_store_dwordx4 v86, v[242:245], s[6:7]
	s_waitcnt vmcnt(16)
	v_mul_f32_e32 v144, v58, v144
	v_mul_f32_e32 v145, v58, v145
	v_mul_f32_e32 v146, v58, v146
	v_mul_f32_e32 v147, v58, v147
	ds_write_b128 v209, v[144:147]
	v_mul_f32_e32 v148, v59, v148
	v_mul_f32_e32 v149, v59, v149
	v_mul_f32_e32 v150, v59, v150
	v_mul_f32_e32 v151, v59, v151
	ds_write_b128 v209, v[148:151] offset:1024
	v_mul_f32_e32 v152, v60, v152
	v_mul_f32_e32 v153, v60, v153
	v_mul_f32_e32 v154, v60, v154
	v_mul_f32_e32 v155, v60, v155
	ds_write_b128 v209, v[152:155] offset:2048
	v_mul_f32_e32 v156, v61, v156
	v_mul_f32_e32 v157, v61, v157
	v_mul_f32_e32 v158, v61, v158
	v_mul_f32_e32 v159, v61, v159
	ds_write_b128 v209, v[156:159] offset:3072
	v_mul_f32_e32 v160, v62, v160
	v_mul_f32_e32 v161, v62, v161
	v_mul_f32_e32 v162, v62, v162
	v_mul_f32_e32 v163, v62, v163
	ds_write_b128 v209, v[160:163] offset:4096
	v_mul_f32_e32 v164, v63, v164
	v_mul_f32_e32 v165, v63, v165
	v_mul_f32_e32 v166, v63, v166
	v_mul_f32_e32 v167, v63, v167
	ds_write_b128 v209, v[164:167] offset:5120
	v_mul_f32_e32 v168, v64, v168
	v_mul_f32_e32 v169, v64, v169
	v_mul_f32_e32 v170, v64, v170
	v_mul_f32_e32 v171, v64, v171
	ds_write_b128 v209, v[168:171] offset:6144
	v_mul_f32_e32 v172, v65, v172
	v_mul_f32_e32 v173, v65, v173
	v_mul_f32_e32 v174, v65, v174
	v_mul_f32_e32 v175, v65, v175
	ds_write_b128 v209, v[172:175] offset:7168
	s_waitcnt lgkmcnt(0)
	s_barrier
; template <int MAP, bool KS, bool KPERM = false>
; __device__ __forceinline__ void p0_transpose_item(const float* W, int K, int Nsrc, int nblk, bf16* WT, const float* ksA, const float* ksB, int ksplit, LAS float* scr, int item, int lane) {
;     const int kb = item / nblk, nb = item % nblk, k0 = 64 * kb, n0 = 32 * nb;
;     const int nr = n0 + (lane & 31); const int sc = MAP == 1 ? src_col_in(nr) : (MAP == 2 ? nat_dim(nr) : nr);
;     float v[32];
; #pragma unroll
;     for (int i = 0; i < 32; ++i) { const int k = k0 + 2 * i + (lane >> 5); const int ksrc = KPERM ? ((k & ~127) + nat_dim(k & 127)) : k;
;         v[i] = sc >= 0 ? W[(size_t)ksrc * Nsrc + sc] : 0.f; }
; #pragma unroll
;     for (int i = 0; i < 32; ++i) { const int kk = 2 * i + (lane >> 5); const int k = k0 + kk;
;         if (KS) v[i] *= (k < ksplit ? ksA[k] : ksB[k - ksplit]);
;         scr[kk * 33 + (lane & 31)] = v[i]; }
;     LDS_WAIT(); asm volatile("" ::: "memory");
;     const int c = lane & 7;
; #pragma unroll
;     for (int j = 0; j < 4; ++j) { const int n = (lane >> 3) + 8 * j; const LAS float* s = scr + (8 * c) * 33 + n;
;         v4u o; o.x = pk2(s[0 * 33], s[1 * 33]); o.y = pk2(s[2 * 33], s[3 * 33]); o.z = pk2(s[4 * 33], s[5 * 33]); o.w = pk2(s[6 * 33], s[7 * 33]);
;         *(GAS v4u*)(WT + (size_t)(n0 + n) * K + k0 + 8 * c) = o; }
;     LDS_WAIT(); asm volatile("" ::: "memory");
; }
;     const int pr = item >> 1, kb = 2 * (pr / nblk) + (item & 1), nb = pr % nblk, k0 = 64 * kb, n0 = 32 * nb;
;     const int nr = n0 + (lane & 31); const int sc = MAP == 1 ? src_col_in(nr) : nr;
;     float v[32];
; #pragma unroll
;     for (int i = 0; i < 32; ++i) v[i] = sc >= 0 ? W[(size_t)(k0 + 2 * i + (lane >> 5)) * Nsrc + sc] : 0.f;
; #pragma unroll
;     for (int i = 0; i < 32; ++i) { const int k = k0 + 2 * i + (lane >> 5); float x = v[i] * wscale; if (KS) x *= (k < ksplit ? ksA[k] : ksB[k - ksplit]); scr[(2 * i + (lane >> 5)) * 33 + (lane & 31)] = x; }
;     LDS_WAIT(); asm volatile("" ::: "memory");
;     const int c = lane & 7;
; #pragma unroll
;     for (int j = 0; j < 4; ++j) { const int n = (lane >> 3) + 8 * j; const LAS float* s = scr + (8 * c) * 33 + n;
;         const unsigned long long o = (unsigned long long)pg8::pk4_fp8(s[0 * 33], s[1 * 33], s[2 * 33], s[3 * 33]) | ((unsigned long long)pg8::pk4_fp8(s[4 * 33], s[5 * 33], s[6 * 33], s[7 * 33]) << 32);
	s_mov_b64 s[8:9], s[58:59]
	global_load_dwordx4 v[144:147], v75, s[8:9]
	s_add_u32 s8, s8, 0x8000
	s_addc_u32 s9, s9, 0
	global_load_dwordx4 v[148:151], v75, s[8:9]
	s_add_u32 s8, s8, 0x8000
	s_addc_u32 s9, s9, 0
	global_load_dwordx4 v[152:155], v75, s[8:9]
	s_add_u32 s8, s8, 0x8000
	s_addc_u32 s9, s9, 0
	global_load_dwordx4 v[156:159], v75, s[8:9]
	s_add_u32 s8, s8, 0x8000
	s_addc_u32 s9, s9, 0
	global_load_dwordx4 v[160:163], v75, s[8:9]
	s_add_u32 s8, s8, 0x8000
	s_addc_u32 s9, s9, 0
	global_load_dwordx4 v[164:167], v75, s[8:9]
	s_add_u32 s8, s8, 0x8000
	s_addc_u32 s9, s9, 0
	global_load_dwordx4 v[168:171], v75, s[8:9]
	s_add_u32 s8, s8, 0x8000
	s_addc_u32 s9, s9, 0
	global_load_dwordx4 v[172:175], v75, s[8:9]
	s_add_u32 s6, s56, 0x1000000
	s_addc_u32 s7, s57, 0
	ds_read_b32 v226, v112
	ds_read_b32 v227, v112 offset:512
	ds_read_b32 v228, v112 offset:1024
	ds_read_b32 v229, v112 offset:1536
	ds_read_b32 v230, v112 offset:2048
	ds_read_b32 v231, v112 offset:2560
	ds_read_b32 v232, v112 offset:3072
	ds_read_b32 v233, v112 offset:3584
	s_waitcnt lgkmcnt(0)
	v_bfe_u32 v120, v226, 16, 1
	v_bfe_u32 v121, v227, 16, 1
	v_bfe_u32 v122, v228, 16, 1
	v_bfe_u32 v123, v229, 16, 1
	v_bfe_u32 v124, v230, 16, 1
	v_bfe_u32 v125, v231, 16, 1
	v_bfe_u32 v126, v232, 16, 1
	v_bfe_u32 v127, v233, 16, 1
	v_add3_u32 v226, v226, v120, s63
	v_add3_u32 v227, v227, v121, s63
	v_add3_u32 v228, v228, v122, s63
	v_add3_u32 v229, v229, v123, s63
	v_add3_u32 v230, v230, v124, s63
	v_add3_u32 v231, v231, v125, s63
	v_add3_u32 v232, v232, v126, s63
	v_add3_u32 v233, v233, v127, s63
	v_perm_b32 v242, v227, v226, s64
	v_perm_b32 v243, v229, v228, s64
	v_perm_b32 v244, v231, v230, s64
	v_perm_b32 v245, v233, v232, s64
	s_nop 0
	global_store_dwordx4 v83, v[242:245], s[6:7]
	ds_read_b32 v226, v114
	ds_read_b32 v227, v114 offset:512
	ds_read_b32 v228, v114 offset:1024
	ds_read_b32 v229, v114 offset:1536
	ds_read_b32 v230, v114 offset:2048
	ds_read_b32 v231, v114 offset:2560
	ds_read_b32 v232, v114 offset:3072
	ds_read_b32 v233, v114 offset:3584
	s_waitcnt lgkmcnt(0)
	v_bfe_u32 v120, v226, 16, 1
	v_bfe_u32 v121, v227, 16, 1
	v_bfe_u32 v122, v228, 16, 1
	v_bfe_u32 v123, v229, 16, 1
	v_bfe_u32 v124, v230, 16, 1
	v_bfe_u32 v125, v231, 16, 1
	v_bfe_u32 v126, v232, 16, 1
	v_bfe_u32 v127, v233, 16, 1
	v_add3_u32 v226, v226, v120, s63
	v_add3_u32 v227, v227, v121, s63
	v_add3_u32 v228, v228, v122, s63
	v_add3_u32 v229, v229, v123, s63
	v_add3_u32 v230, v230, v124, s63
	v_add3_u32 v231, v231, v125, s63
	v_add3_u32 v232, v232, v126, s63
	v_add3_u32 v233, v233, v127, s63
	v_perm_b32 v242, v227, v226, s64
	v_perm_b32 v243, v229, v228, s64
	v_perm_b32 v244, v231, v230, s64
	v_perm_b32 v245, v233, v232, s64
	s_nop 0
	global_store_dwordx4 v84, v[242:245], s[6:7]
	ds_read_b32 v226, v116
	ds_read_b32 v227, v116 offset:512
	ds_read_b32 v228, v116 offset:1024
	ds_read_b32 v229, v116 offset:1536
	ds_read_b32 v230, v116 offset:2048
	ds_read_b32 v231, v116 offset:2560
	ds_read_b32 v232, v116 offset:3072
	ds_read_b32 v233, v116 offset:3584
	s_waitcnt lgkmcnt(0)
	v_bfe_u32 v120, v226, 16, 1
	v_bfe_u32 v121, v227, 16, 1
	v_bfe_u32 v122, v228, 16, 1
	v_bfe_u32 v123, v229, 16, 1
	v_bfe_u32 v124, v230, 16, 1
	v_bfe_u32 v125, v231, 16, 1
	v_bfe_u32 v126, v232, 16, 1
	v_bfe_u32 v127, v233, 16, 1
	v_add3_u32 v226, v226, v120, s63
	v_add3_u32 v227, v227, v121, s63
	v_add3_u32 v228, v228, v122, s63
	v_add3_u32 v229, v229, v123, s63
	v_add3_u32 v230, v230, v124, s63
	v_add3_u32 v231, v231, v125, s63
	v_add3_u32 v232, v232, v126, s63
	v_add3_u32 v233, v233, v127, s63
	v_perm_b32 v242, v227, v226, s64
	v_perm_b32 v243, v229, v228, s64
	v_perm_b32 v244, v231, v230, s64
	v_perm_b32 v245, v233, v232, s64
	s_nop 0
	global_store_dwordx4 v85, v[242:245], s[6:7]
	ds_read_b32 v226, v118
	ds_read_b32 v227, v118 offset:512
	ds_read_b32 v228, v118 offset:1024
	ds_read_b32 v229, v118 offset:1536
	ds_read_b32 v230, v118 offset:2048
	ds_read_b32 v231, v118 offset:2560
	ds_read_b32 v232, v118 offset:3072
	ds_read_b32 v233, v118 offset:3584
	s_waitcnt lgkmcnt(0)
	v_bfe_u32 v120, v226, 16, 1
	v_bfe_u32 v121, v227, 16, 1
	v_bfe_u32 v122, v228, 16, 1
	v_bfe_u32 v123, v229, 16, 1
	v_bfe_u32 v124, v230, 16, 1
	v_bfe_u32 v125, v231, 16, 1
	v_bfe_u32 v126, v232, 16, 1
	v_bfe_u32 v127, v233, 16, 1
	v_add3_u32 v226, v226, v120, s63
	v_add3_u32 v227, v227, v121, s63
	v_add3_u32 v228, v228, v122, s63
	v_add3_u32 v229, v229, v123, s63
	v_add3_u32 v230, v230, v124, s63
	v_add3_u32 v231, v231, v125, s63
	v_add3_u32 v232, v232, v126, s63
	v_add3_u32 v233, v233, v127, s63
	v_perm_b32 v242, v227, v226, s64
	v_perm_b32 v243, v229, v228, s64
	v_perm_b32 v244, v231, v230, s64
	v_perm_b32 v245, v233, v232, s64
	s_nop 0
	global_store_dwordx4 v86, v[242:245], s[6:7]
	s_waitcnt vmcnt(16)
	v_mul_f32_e32 v176, v58, v176
	v_mul_f32_e32 v177, v58, v177
	v_mul_f32_e32 v178, v58, v178
	v_mul_f32_e32 v179, v58, v179
	ds_write_b128 v210, v[176:179]
	v_mul_f32_e32 v180, v59, v180
	v_mul_f32_e32 v181, v59, v181
	v_mul_f32_e32 v182, v59, v182
	v_mul_f32_e32 v183, v59, v183
	ds_write_b128 v210, v[180:183] offset:1024
	v_mul_f32_e32 v184, v60, v184
	v_mul_f32_e32 v185, v60, v185
	v_mul_f32_e32 v186, v60, v186
	v_mul_f32_e32 v187, v60, v187
	ds_write_b128 v210, v[184:187] offset:2048
	v_mul_f32_e32 v188, v61, v188
	v_mul_f32_e32 v189, v61, v189
	v_mul_f32_e32 v190, v61, v190
	v_mul_f32_e32 v191, v61, v191
	ds_write_b128 v210, v[188:191] offset:3072
	v_mul_f32_e32 v192, v62, v192
	v_mul_f32_e32 v193, v62, v193
	v_mul_f32_e32 v194, v62, v194
	v_mul_f32_e32 v195, v62, v195
	ds_write_b128 v210, v[192:195] offset:4096
	v_mul_f32_e32 v196, v63, v196
	v_mul_f32_e32 v197, v63, v197
	v_mul_f32_e32 v198, v63, v198
	v_mul_f32_e32 v199, v63, v199
	ds_write_b128 v210, v[196:199] offset:5120
	v_mul_f32_e32 v200, v64, v200
	v_mul_f32_e32 v201, v64, v201
	v_mul_f32_e32 v202, v64, v202
	v_mul_f32_e32 v203, v64, v203
	ds_write_b128 v210, v[200:203] offset:6144
	v_mul_f32_e32 v204, v65, v204
	v_mul_f32_e32 v205, v65, v205
	v_mul_f32_e32 v206, v65, v206
	v_mul_f32_e32 v207, v65, v207
	ds_write_b128 v210, v[204:207] offset:7168
	s_waitcnt lgkmcnt(0)
	s_barrier
; template <int MAP, bool KS, bool KPERM = false>
; __device__ __forceinline__ void p0_transpose_item(const float* W, int K, int Nsrc, int nblk, bf16* WT, const float* ksA, const float* ksB, int ksplit, LAS float* scr, int item, int lane) {
;     const int kb = item / nblk, nb = item % nblk, k0 = 64 * kb, n0 = 32 * nb;
;     const int nr = n0 + (lane & 31); const int sc = MAP == 1 ? src_col_in(nr) : (MAP == 2 ? nat_dim(nr) : nr);
;     float v[32];
; #pragma unroll
;     for (int i = 0; i < 32; ++i) { const int k = k0 + 2 * i + (lane >> 5); const int ksrc = KPERM ? ((k & ~127) + nat_dim(k & 127)) : k;
;         v[i] = sc >= 0 ? W[(size_t)ksrc * Nsrc + sc] : 0.f; }
; #pragma unroll
;     for (int i = 0; i < 32; ++i) { const int kk = 2 * i + (lane >> 5); const int k = k0 + kk;
;         if (KS) v[i] *= (k < ksplit ? ksA[k] : ksB[k - ksplit]);
;         scr[kk * 33 + (lane & 31)] = v[i]; }
;     LDS_WAIT(); asm volatile("" ::: "memory");
;     const int c = lane & 7;
; #pragma unroll
;     for (int j = 0; j < 4; ++j) { const int n = (lane >> 3) + 8 * j; const LAS float* s = scr + (8 * c) * 33 + n;
;         v4u o; o.x = pk2(s[0 * 33], s[1 * 33]); o.y = pk2(s[2 * 33], s[3 * 33]); o.z = pk2(s[4 * 33], s[5 * 33]); o.w = pk2(s[6 * 33], s[7 * 33]);
;         *(GAS v4u*)(WT + (size_t)(n0 + n) * K + k0 + 8 * c) = o; }
;     LDS_WAIT(); asm volatile("" ::: "memory");
; }
;     const int pr = item >> 1, kb = 2 * (pr / nblk) + (item & 1), nb = pr % nblk, k0 = 64 * kb, n0 = 32 * nb;
;     const int nr = n0 + (lane & 31); const int sc = MAP == 1 ? src_col_in(nr) : nr;
;     float v[32];
; #pragma unroll
;     for (int i = 0; i < 32; ++i) v[i] = sc >= 0 ? W[(size_t)(k0 + 2 * i + (lane >> 5)) * Nsrc + sc] : 0.f;
; #pragma unroll
;     for (int i = 0; i < 32; ++i) { const int k = k0 + 2 * i + (lane >> 5); float x = v[i] * wscale; if (KS) x *= (k < ksplit ? ksA[k] : ksB[k - ksplit]); scr[(2 * i + (lane >> 5)) * 33 + (lane & 31)] = x; }
;     LDS_WAIT(); asm volatile("" ::: "memory");
;     const int c = lane & 7;
; #pragma unroll
;     for (int j = 0; j < 4; ++j) { const int n = (lane >> 3) + 8 * j; const LAS float* s = scr + (8 * c) * 33 + n;
;         const unsigned long long o = (unsigned long long)pg8::pk4_fp8(s[0 * 33], s[1 * 33], s[2 * 33], s[3 * 33]) | ((unsigned long long)pg8::pk4_fp8(s[4 * 33], s[5 * 33], s[6 * 33], s[7 * 33]) << 32);
	s_add_u32 s8, s58, 0x1000
	s_addc_u32 s9, s59, 0
	global_load_dwordx4 v[176:179], v75, s[8:9]
	s_add_u32 s8, s8, 0x8000
	s_addc_u32 s9, s9, 0
	global_load_dwordx4 v[180:183], v75, s[8:9]
	s_add_u32 s8, s8, 0x8000
	s_addc_u32 s9, s9, 0
	global_load_dwordx4 v[184:187], v75, s[8:9]
	s_add_u32 s8, s8, 0x8000
	s_addc_u32 s9, s9, 0
	global_load_dwordx4 v[188:191], v75, s[8:9]
	s_add_u32 s8, s8, 0x8000
	s_addc_u32 s9, s9, 0
	global_load_dwordx4 v[192:195], v75, s[8:9]
	s_add_u32 s8, s8, 0x8000
	s_addc_u32 s9, s9, 0
	global_load_dwordx4 v[196:199], v75, s[8:9]
	s_add_u32 s8, s8, 0x8000
	s_addc_u32 s9, s9, 0
	global_load_dwordx4 v[200:203], v75, s[8:9]
	s_add_u32 s8, s8, 0x8000
	s_addc_u32 s9, s9, 0
	global_load_dwordx4 v[204:207], v75, s[8:9]
	s_add_u32 s6, s56, 0x1800000
	s_addc_u32 s7, s57, 0
	ds_read_b32 v226, v113
	ds_read_b32 v227, v113 offset:512
	ds_read_b32 v228, v113 offset:1024
	ds_read_b32 v229, v113 offset:1536
	ds_read_b32 v230, v113 offset:2048
	ds_read_b32 v231, v113 offset:2560
	ds_read_b32 v232, v113 offset:3072
	ds_read_b32 v233, v113 offset:3584
	s_waitcnt lgkmcnt(0)
	v_bfe_u32 v120, v226, 16, 1
	v_bfe_u32 v121, v227, 16, 1
	v_bfe_u32 v122, v228, 16, 1
	v_bfe_u32 v123, v229, 16, 1
	v_bfe_u32 v124, v230, 16, 1
	v_bfe_u32 v125, v231, 16, 1
	v_bfe_u32 v126, v232, 16, 1
	v_bfe_u32 v127, v233, 16, 1
	v_add3_u32 v226, v226, v120, s63
	v_add3_u32 v227, v227, v121, s63
	v_add3_u32 v228, v228, v122, s63
	v_add3_u32 v229, v229, v123, s63
	v_add3_u32 v230, v230, v124, s63
	v_add3_u32 v231, v231, v125, s63
	v_add3_u32 v232, v232, v126, s63
	v_add3_u32 v233, v233, v127, s63
	v_perm_b32 v242, v227, v226, s64
	v_perm_b32 v243, v229, v228, s64
	v_perm_b32 v244, v231, v230, s64
	v_perm_b32 v245, v233, v232, s64
	s_nop 0
	global_store_dwordx4 v83, v[242:245], s[6:7]
	ds_read_b32 v226, v115
	ds_read_b32 v227, v115 offset:512
	ds_read_b32 v228, v115 offset:1024
	ds_read_b32 v229, v115 offset:1536
	ds_read_b32 v230, v115 offset:2048
	ds_read_b32 v231, v115 offset:2560
	ds_read_b32 v232, v115 offset:3072
	ds_read_b32 v233, v115 offset:3584
	s_waitcnt lgkmcnt(0)
	v_bfe_u32 v120, v226, 16, 1
	v_bfe_u32 v121, v227, 16, 1
	v_bfe_u32 v122, v228, 16, 1
	v_bfe_u32 v123, v229, 16, 1
	v_bfe_u32 v124, v230, 16, 1
	v_bfe_u32 v125, v231, 16, 1
	v_bfe_u32 v126, v232, 16, 1
	v_bfe_u32 v127, v233, 16, 1
	v_add3_u32 v226, v226, v120, s63
	v_add3_u32 v227, v227, v121, s63
	v_add3_u32 v228, v228, v122, s63
	v_add3_u32 v229, v229, v123, s63
	v_add3_u32 v230, v230, v124, s63
	v_add3_u32 v231, v231, v125, s63
	v_add3_u32 v232, v232, v126, s63
	v_add3_u32 v233, v233, v127, s63
	v_perm_b32 v242, v227, v226, s64
	v_perm_b32 v243, v229, v228, s64
	v_perm_b32 v244, v231, v230, s64
	v_perm_b32 v245, v233, v232, s64
	s_nop 0
	global_store_dwordx4 v84, v[242:245], s[6:7]
	ds_read_b32 v226, v117
	ds_read_b32 v227, v117 offset:512
	ds_read_b32 v228, v117 offset:1024
	ds_read_b32 v229, v117 offset:1536
	ds_read_b32 v230, v117 offset:2048
	ds_read_b32 v231, v117 offset:2560
	ds_read_b32 v232, v117 offset:3072
	ds_read_b32 v233, v117 offset:3584
	s_waitcnt lgkmcnt(0)
	v_bfe_u32 v120, v226, 16, 1
	v_bfe_u32 v121, v227, 16, 1
	v_bfe_u32 v122, v228, 16, 1
	v_bfe_u32 v123, v229, 16, 1
	v_bfe_u32 v124, v230, 16, 1
	v_bfe_u32 v125, v231, 16, 1
	v_bfe_u32 v126, v232, 16, 1
	v_bfe_u32 v127, v233, 16, 1
	v_add3_u32 v226, v226, v120, s63
	v_add3_u32 v227, v227, v121, s63
	v_add3_u32 v228, v228, v122, s63
	v_add3_u32 v229, v229, v123, s63
	v_add3_u32 v230, v230, v124, s63
	v_add3_u32 v231, v231, v125, s63
	v_add3_u32 v232, v232, v126, s63
	v_add3_u32 v233, v233, v127, s63
	v_perm_b32 v242, v227, v226, s64
	v_perm_b32 v243, v229, v228, s64
	v_perm_b32 v244, v231, v230, s64
	v_perm_b32 v245, v233, v232, s64
	s_nop 0
	global_store_dwordx4 v85, v[242:245], s[6:7]
	ds_read_b32 v226, v119
	ds_read_b32 v227, v119 offset:512
	ds_read_b32 v228, v119 offset:1024
	ds_read_b32 v229, v119 offset:1536
	ds_read_b32 v230, v119 offset:2048
	ds_read_b32 v231, v119 offset:2560
	ds_read_b32 v232, v119 offset:3072
	ds_read_b32 v233, v119 offset:3584
	s_waitcnt lgkmcnt(0)
	v_bfe_u32 v120, v226, 16, 1
	v_bfe_u32 v121, v227, 16, 1
	v_bfe_u32 v122, v228, 16, 1
	v_bfe_u32 v123, v229, 16, 1
	v_bfe_u32 v124, v230, 16, 1
	v_bfe_u32 v125, v231, 16, 1
	v_bfe_u32 v126, v232, 16, 1
	v_bfe_u32 v127, v233, 16, 1
	v_add3_u32 v226, v226, v120, s63
	v_add3_u32 v227, v227, v121, s63
	v_add3_u32 v228, v228, v122, s63
	v_add3_u32 v229, v229, v123, s63
	v_add3_u32 v230, v230, v124, s63
	v_add3_u32 v231, v231, v125, s63
	v_add3_u32 v232, v232, v126, s63
	v_add3_u32 v233, v233, v127, s63
	v_perm_b32 v242, v227, v226, s64
	v_perm_b32 v243, v229, v228, s64
	v_perm_b32 v244, v231, v230, s64
	v_perm_b32 v245, v233, v232, s64
	s_nop 0
	global_store_dwordx4 v86, v[242:245], s[6:7]
	s_waitcnt vmcnt(16)
	v_mul_f32_e32 v144, v66, v144
	v_mul_f32_e32 v145, v66, v145
	v_mul_f32_e32 v146, v66, v146
	v_mul_f32_e32 v147, v66, v147
	ds_write_b128 v209, v[144:147]
	v_mul_f32_e32 v148, v67, v148
	v_mul_f32_e32 v149, v67, v149
	v_mul_f32_e32 v150, v67, v150
	v_mul_f32_e32 v151, v67, v151
	ds_write_b128 v209, v[148:151] offset:1024
	v_mul_f32_e32 v152, v68, v152
	v_mul_f32_e32 v153, v68, v153
	v_mul_f32_e32 v154, v68, v154
	v_mul_f32_e32 v155, v68, v155
	ds_write_b128 v209, v[152:155] offset:2048
	v_mul_f32_e32 v156, v69, v156
	v_mul_f32_e32 v157, v69, v157
	v_mul_f32_e32 v158, v69, v158
	v_mul_f32_e32 v159, v69, v159
	ds_write_b128 v209, v[156:159] offset:3072
	v_mul_f32_e32 v160, v70, v160
	v_mul_f32_e32 v161, v70, v161
	v_mul_f32_e32 v162, v70, v162
	v_mul_f32_e32 v163, v70, v163
	ds_write_b128 v209, v[160:163] offset:4096
	v_mul_f32_e32 v164, v71, v164
	v_mul_f32_e32 v165, v71, v165
	v_mul_f32_e32 v166, v71, v166
	v_mul_f32_e32 v167, v71, v167
	ds_write_b128 v209, v[164:167] offset:5120
	v_mul_f32_e32 v168, v72, v168
	v_mul_f32_e32 v169, v72, v169
	v_mul_f32_e32 v170, v72, v170
	v_mul_f32_e32 v171, v72, v171
	ds_write_b128 v209, v[168:171] offset:6144
	v_mul_f32_e32 v172, v73, v172
	v_mul_f32_e32 v173, v73, v173
	v_mul_f32_e32 v174, v73, v174
	v_mul_f32_e32 v175, v73, v175
	ds_write_b128 v209, v[172:175] offset:7168
	s_waitcnt lgkmcnt(0)
	s_barrier
; #define GAS __attribute__((address_space(1)))
; #define LAS __attribute__((address_space(3)))
; #define LDS_WAIT() asm volatile("s_waitcnt lgkmcnt(0)" ::: "memory")
;     const int pr = item >> 1, kb = 2 * (pr / nblk) + (item & 1), nb = pr % nblk, k0 = 64 * kb, n0 = 32 * nb;
;     const int nr = n0 + (lane & 31); const int sc = MAP == 1 ? src_col_in(nr) : nr;
;     float v[32];
; #pragma unroll
;     for (int i = 0; i < 32; ++i) v[i] = sc >= 0 ? W[(size_t)(k0 + 2 * i + (lane >> 5)) * Nsrc + sc] : 0.f;
; #pragma unroll
;     for (int i = 0; i < 32; ++i) { const int k = k0 + 2 * i + (lane >> 5); float x = v[i] * wscale; if (KS) x *= (k < ksplit ? ksA[k] : ksB[k - ksplit]); scr[(2 * i + (lane >> 5)) * 33 + (lane & 31)] = x; }
;     LDS_WAIT(); asm volatile("" ::: "memory");
;     const int c = lane & 7;
; #pragma unroll
;     for (int j = 0; j < 4; ++j) { const int n = (lane >> 3) + 8 * j; const LAS float* s = scr + (8 * c) * 33 + n;
;         const unsigned long long o = (unsigned long long)pg8::pk4_fp8(s[0 * 33], s[1 * 33], s[2 * 33], s[3 * 33]) | ((unsigned long long)pg8::pk4_fp8(s[4 * 33], s[5 * 33], s[6 * 33], s[7 * 33]) << 32);
;         *(GAS unsigned long long*)(WT + (size_t)(n0 + n) * K + k0 + 8 * c) = o; }
;     LDS_WAIT(); asm volatile("" ::: "memory");
; }
	s_add_u32 s8, s58, 0x2000
	s_addc_u32 s9, s59, 0
	global_load_dwordx4 v[144:147], v75, s[8:9]
	s_add_u32 s8, s8, 0x8000
	s_addc_u32 s9, s9, 0
	global_load_dwordx4 v[148:151], v75, s[8:9]
	s_add_u32 s8, s8, 0x8000
	s_addc_u32 s9, s9, 0
	global_load_dwordx4 v[152:155], v75, s[8:9]
	s_add_u32 s8, s8, 0x8000
	s_addc_u32 s9, s9, 0
	global_load_dwordx4 v[156:159], v75, s[8:9]
	s_add_u32 s8, s8, 0x8000
	s_addc_u32 s9, s9, 0
	global_load_dwordx4 v[160:163], v75, s[8:9]
	s_add_u32 s8, s8, 0x8000
	s_addc_u32 s9, s9, 0
	global_load_dwordx4 v[164:167], v75, s[8:9]
	s_add_u32 s8, s8, 0x8000
	s_addc_u32 s9, s9, 0
	global_load_dwordx4 v[168:171], v75, s[8:9]
	s_add_u32 s8, s8, 0x8000
	s_addc_u32 s9, s9, 0
	global_load_dwordx4 v[172:175], v75, s[8:9]
	s_mov_b64 s[6:7], s[60:61]
	ds_read_b32 v226, v211
	ds_read_b32 v227, v211 offset:512
	ds_read_b32 v228, v211 offset:1024
	ds_read_b32 v229, v211 offset:1536
	ds_read_b32 v230, v211 offset:2048
	ds_read_b32 v231, v211 offset:2560
	ds_read_b32 v232, v211 offset:3072
	ds_read_b32 v233, v211 offset:3584
	ds_read_b32 v234, v211 offset:4096
	ds_read_b32 v235, v211 offset:4608
	ds_read_b32 v236, v211 offset:5120
	ds_read_b32 v237, v211 offset:5632
	ds_read_b32 v238, v211 offset:6144
	ds_read_b32 v239, v211 offset:6656
	ds_read_b32 v240, v211 offset:7168
	ds_read_b32 v241, v211 offset:7680
	s_waitcnt lgkmcnt(0)
	v_max_f32_e32 v226, v226, v226
	v_max_f32_e32 v227, v227, v227
	v_max_f32_e32 v228, v228, v228
	v_max_f32_e32 v229, v229, v229
	v_max_f32_e32 v230, v230, v230
	v_max_f32_e32 v231, v231, v231
	v_max_f32_e32 v232, v232, v232
	v_max_f32_e32 v233, v233, v233
	v_max_f32_e32 v234, v234, v234
	v_max_f32_e32 v235, v235, v235
	v_max_f32_e32 v236, v236, v236
	v_max_f32_e32 v237, v237, v237
	v_max_f32_e32 v238, v238, v238
	v_max_f32_e32 v239, v239, v239
	v_max_f32_e32 v240, v240, v240
	v_max_f32_e32 v241, v241, v241
	v_med3_f32 v226, v226, s62, v95
	v_med3_f32 v227, v227, s62, v95
	v_med3_f32 v228, v228, s62, v95
	v_med3_f32 v229, v229, s62, v95
	v_med3_f32 v230, v230, s62, v95
	v_med3_f32 v231, v231, s62, v95
	v_med3_f32 v232, v232, s62, v95
	v_med3_f32 v233, v233, s62, v95
	v_med3_f32 v234, v234, s62, v95
	v_med3_f32 v235, v235, s62, v95
	v_med3_f32 v236, v236, s62, v95
	v_med3_f32 v237, v237, s62, v95
	v_med3_f32 v238, v238, s62, v95
	v_med3_f32 v239, v239, s62, v95
	v_med3_f32 v240, v240, s62, v95
	v_med3_f32 v241, v241, s62, v95
	v_mov_b32_e32 v242, 0
	v_mov_b32_e32 v243, 0
	v_mov_b32_e32 v244, 0
	v_mov_b32_e32 v245, 0
	v_cvt_pk_fp8_f32 v242, v226, v227
	v_cvt_pk_fp8_f32 v243, v230, v231
	v_cvt_pk_fp8_f32 v244, v234, v235
	v_cvt_pk_fp8_f32 v245, v238, v239
	v_cvt_pk_fp8_f32 v242, v228, v229 op_sel:[0,0,1]
	v_cvt_pk_fp8_f32 v243, v232, v233 op_sel:[0,0,1]
	v_cvt_pk_fp8_f32 v244, v236, v237 op_sel:[0,0,1]
	v_cvt_pk_fp8_f32 v245, v240, v241 op_sel:[0,0,1]
	s_nop 0
	global_store_dwordx4 v77, v[242:245], s[6:7]
	ds_read_b32 v226, v213
	ds_read_b32 v227, v213 offset:512
	ds_read_b32 v228, v213 offset:1024
	ds_read_b32 v229, v213 offset:1536
	ds_read_b32 v230, v213 offset:2048
	ds_read_b32 v231, v213 offset:2560
	ds_read_b32 v232, v213 offset:3072
	ds_read_b32 v233, v213 offset:3584
	ds_read_b32 v234, v213 offset:4096
	ds_read_b32 v235, v213 offset:4608
	ds_read_b32 v236, v213 offset:5120
	ds_read_b32 v237, v213 offset:5632
	ds_read_b32 v238, v213 offset:6144
	ds_read_b32 v239, v213 offset:6656
	ds_read_b32 v240, v213 offset:7168
	ds_read_b32 v241, v213 offset:7680
	s_waitcnt lgkmcnt(0)
	v_max_f32_e32 v226, v226, v226
	v_max_f32_e32 v227, v227, v227
	v_max_f32_e32 v228, v228, v228
	v_max_f32_e32 v229, v229, v229
	v_max_f32_e32 v230, v230, v230
	v_max_f32_e32 v231, v231, v231
	v_max_f32_e32 v232, v232, v232
	v_max_f32_e32 v233, v233, v233
	v_max_f32_e32 v234, v234, v234
	v_max_f32_e32 v235, v235, v235
	v_max_f32_e32 v236, v236, v236
	v_max_f32_e32 v237, v237, v237
	v_max_f32_e32 v238, v238, v238
	v_max_f32_e32 v239, v239, v239
	v_max_f32_e32 v240, v240, v240
	v_max_f32_e32 v241, v241, v241
	v_med3_f32 v226, v226, s62, v95
	v_med3_f32 v227, v227, s62, v95
	v_med3_f32 v228, v228, s62, v95
	v_med3_f32 v229, v229, s62, v95
	v_med3_f32 v230, v230, s62, v95
	v_med3_f32 v231, v231, s62, v95
	v_med3_f32 v232, v232, s62, v95
	v_med3_f32 v233, v233, s62, v95
	v_med3_f32 v234, v234, s62, v95
	v_med3_f32 v235, v235, s62, v95
	v_med3_f32 v236, v236, s62, v95
	v_med3_f32 v237, v237, s62, v95
	v_med3_f32 v238, v238, s62, v95
	v_med3_f32 v239, v239, s62, v95
	v_med3_f32 v240, v240, s62, v95
	v_med3_f32 v241, v241, s62, v95
	v_mov_b32_e32 v242, 0
	v_mov_b32_e32 v243, 0
	v_mov_b32_e32 v244, 0
	v_mov_b32_e32 v245, 0
	v_cvt_pk_fp8_f32 v242, v226, v227
	v_cvt_pk_fp8_f32 v243, v230, v231
	v_cvt_pk_fp8_f32 v244, v234, v235
	v_cvt_pk_fp8_f32 v245, v238, v239
	v_cvt_pk_fp8_f32 v242, v228, v229 op_sel:[0,0,1]
	v_cvt_pk_fp8_f32 v243, v232, v233 op_sel:[0,0,1]
	v_cvt_pk_fp8_f32 v244, v236, v237 op_sel:[0,0,1]
	v_cvt_pk_fp8_f32 v245, v240, v241 op_sel:[0,0,1]
	s_nop 0
	global_store_dwordx4 v78, v[242:245], s[6:7]
	s_waitcnt vmcnt(14)
	v_mul_f32_e32 v176, v66, v176
	v_mul_f32_e32 v177, v66, v177
	v_mul_f32_e32 v178, v66, v178
	v_mul_f32_e32 v179, v66, v179
	ds_write_b128 v210, v[176:179]
	v_mul_f32_e32 v180, v67, v180
	v_mul_f32_e32 v181, v67, v181
	v_mul_f32_e32 v182, v67, v182
	v_mul_f32_e32 v183, v67, v183
	ds_write_b128 v210, v[180:183] offset:1024
	v_mul_f32_e32 v184, v68, v184
	v_mul_f32_e32 v185, v68, v185
	v_mul_f32_e32 v186, v68, v186
	v_mul_f32_e32 v187, v68, v187
	ds_write_b128 v210, v[184:187] offset:2048
	v_mul_f32_e32 v188, v69, v188
	v_mul_f32_e32 v189, v69, v189
	v_mul_f32_e32 v190, v69, v190
	v_mul_f32_e32 v191, v69, v191
	ds_write_b128 v210, v[188:191] offset:3072
	v_mul_f32_e32 v192, v70, v192
	v_mul_f32_e32 v193, v70, v193
	v_mul_f32_e32 v194, v70, v194
	v_mul_f32_e32 v195, v70, v195
	ds_write_b128 v210, v[192:195] offset:4096
	v_mul_f32_e32 v196, v71, v196
	v_mul_f32_e32 v197, v71, v197
	v_mul_f32_e32 v198, v71, v198
	v_mul_f32_e32 v199, v71, v199
	ds_write_b128 v210, v[196:199] offset:5120
	v_mul_f32_e32 v200, v72, v200
	v_mul_f32_e32 v201, v72, v201
	v_mul_f32_e32 v202, v72, v202
	v_mul_f32_e32 v203, v72, v203
	ds_write_b128 v210, v[200:203] offset:6144
	v_mul_f32_e32 v204, v73, v204
	v_mul_f32_e32 v205, v73, v205
	v_mul_f32_e32 v206, v73, v206
	v_mul_f32_e32 v207, v73, v207
	ds_write_b128 v210, v[204:207] offset:7168
	s_waitcnt lgkmcnt(0)
	s_barrier
; #define GAS __attribute__((address_space(1)))
; #define LAS __attribute__((address_space(3)))
; #define LDS_WAIT() asm volatile("s_waitcnt lgkmcnt(0)" ::: "memory")
;     const int pr = item >> 1, kb = 2 * (pr / nblk) + (item & 1), nb = pr % nblk, k0 = 64 * kb, n0 = 32 * nb;
;     const int nr = n0 + (lane & 31); const int sc = MAP == 1 ? src_col_in(nr) : nr;
;     float v[32];
; #pragma unroll
;     for (int i = 0; i < 32; ++i) v[i] = sc >= 0 ? W[(size_t)(k0 + 2 * i + (lane >> 5)) * Nsrc + sc] : 0.f;
; #pragma unroll
;     for (int i = 0; i < 32; ++i) { const int k = k0 + 2 * i + (lane >> 5); float x = v[i] * wscale; if (KS) x *= (k < ksplit ? ksA[k] : ksB[k - ksplit]); scr[(2 * i + (lane >> 5)) * 33 + (lane & 31)] = x; }
;     LDS_WAIT(); asm volatile("" ::: "memory");
;     const int c = lane & 7;
; #pragma unroll
;     for (int j = 0; j < 4; ++j) { const int n = (lane >> 3) + 8 * j; const LAS float* s = scr + (8 * c) * 33 + n;
;         const unsigned long long o = (unsigned long long)pg8::pk4_fp8(s[0 * 33], s[1 * 33], s[2 * 33], s[3 * 33]) | ((unsigned long long)pg8::pk4_fp8(s[4 * 33], s[5 * 33], s[6 * 33], s[7 * 33]) << 32);
;         *(GAS unsigned long long*)(WT + (size_t)(n0 + n) * K + k0 + 8 * c) = o; }
;     LDS_WAIT(); asm volatile("" ::: "memory");
; }
	s_add_u32 s8, s58, 0x3000
	s_addc_u32 s9, s59, 0
	global_load_dwordx4 v[176:179], v75, s[8:9]
	s_add_u32 s8, s8, 0x8000
	s_addc_u32 s9, s9, 0
	global_load_dwordx4 v[180:183], v75, s[8:9]
	s_add_u32 s8, s8, 0x8000
	s_addc_u32 s9, s9, 0
	global_load_dwordx4 v[184:187], v75, s[8:9]
	s_add_u32 s8, s8, 0x8000
	s_addc_u32 s9, s9, 0
	global_load_dwordx4 v[188:191], v75, s[8:9]
	s_add_u32 s8, s8, 0x8000
	s_addc_u32 s9, s9, 0
	global_load_dwordx4 v[192:195], v75, s[8:9]
	s_add_u32 s8, s8, 0x8000
	s_addc_u32 s9, s9, 0
	global_load_dwordx4 v[196:199], v75, s[8:9]
	s_add_u32 s8, s8, 0x8000
	s_addc_u32 s9, s9, 0
	global_load_dwordx4 v[200:203], v75, s[8:9]
	s_add_u32 s8, s8, 0x8000
	s_addc_u32 s9, s9, 0
	global_load_dwordx4 v[204:207], v75, s[8:9]
	s_add_u32 s6, s60, 0x400000
	s_addc_u32 s7, s61, 0
	ds_read_b32 v226, v212
	ds_read_b32 v227, v212 offset:512
	ds_read_b32 v228, v212 offset:1024
	ds_read_b32 v229, v212 offset:1536
	ds_read_b32 v230, v212 offset:2048
	ds_read_b32 v231, v212 offset:2560
	ds_read_b32 v232, v212 offset:3072
	ds_read_b32 v233, v212 offset:3584
	ds_read_b32 v234, v212 offset:4096
	ds_read_b32 v235, v212 offset:4608
	ds_read_b32 v236, v212 offset:5120
	ds_read_b32 v237, v212 offset:5632
	ds_read_b32 v238, v212 offset:6144
	ds_read_b32 v239, v212 offset:6656
	ds_read_b32 v240, v212 offset:7168
	ds_read_b32 v241, v212 offset:7680
	s_waitcnt lgkmcnt(0)
	v_max_f32_e32 v226, v226, v226
	v_max_f32_e32 v227, v227, v227
	v_max_f32_e32 v228, v228, v228
	v_max_f32_e32 v229, v229, v229
	v_max_f32_e32 v230, v230, v230
	v_max_f32_e32 v231, v231, v231
	v_max_f32_e32 v232, v232, v232
	v_max_f32_e32 v233, v233, v233
	v_max_f32_e32 v234, v234, v234
	v_max_f32_e32 v235, v235, v235
	v_max_f32_e32 v236, v236, v236
	v_max_f32_e32 v237, v237, v237
	v_max_f32_e32 v238, v238, v238
	v_max_f32_e32 v239, v239, v239
	v_max_f32_e32 v240, v240, v240
	v_max_f32_e32 v241, v241, v241
	v_med3_f32 v226, v226, s62, v95
	v_med3_f32 v227, v227, s62, v95
	v_med3_f32 v228, v228, s62, v95
	v_med3_f32 v229, v229, s62, v95
	v_med3_f32 v230, v230, s62, v95
	v_med3_f32 v231, v231, s62, v95
	v_med3_f32 v232, v232, s62, v95
	v_med3_f32 v233, v233, s62, v95
	v_med3_f32 v234, v234, s62, v95
	v_med3_f32 v235, v235, s62, v95
	v_med3_f32 v236, v236, s62, v95
	v_med3_f32 v237, v237, s62, v95
	v_med3_f32 v238, v238, s62, v95
	v_med3_f32 v239, v239, s62, v95
	v_med3_f32 v240, v240, s62, v95
	v_med3_f32 v241, v241, s62, v95
	v_mov_b32_e32 v242, 0
	v_mov_b32_e32 v243, 0
	v_mov_b32_e32 v244, 0
	v_mov_b32_e32 v245, 0
	v_cvt_pk_fp8_f32 v242, v226, v227
	v_cvt_pk_fp8_f32 v243, v230, v231
	v_cvt_pk_fp8_f32 v244, v234, v235
	v_cvt_pk_fp8_f32 v245, v238, v239
	v_cvt_pk_fp8_f32 v242, v228, v229 op_sel:[0,0,1]
	v_cvt_pk_fp8_f32 v243, v232, v233 op_sel:[0,0,1]
	v_cvt_pk_fp8_f32 v244, v236, v237 op_sel:[0,0,1]
	v_cvt_pk_fp8_f32 v245, v240, v241 op_sel:[0,0,1]
	s_nop 0
	global_store_dwordx4 v77, v[242:245], s[6:7]
	ds_read_b32 v226, v214
	ds_read_b32 v227, v214 offset:512
	ds_read_b32 v228, v214 offset:1024
	ds_read_b32 v229, v214 offset:1536
	ds_read_b32 v230, v214 offset:2048
	ds_read_b32 v231, v214 offset:2560
	ds_read_b32 v232, v214 offset:3072
	ds_read_b32 v233, v214 offset:3584
	ds_read_b32 v234, v214 offset:4096
	ds_read_b32 v235, v214 offset:4608
	ds_read_b32 v236, v214 offset:5120
	ds_read_b32 v237, v214 offset:5632
	ds_read_b32 v238, v214 offset:6144
	ds_read_b32 v239, v214 offset:6656
	ds_read_b32 v240, v214 offset:7168
	ds_read_b32 v241, v214 offset:7680
	s_waitcnt lgkmcnt(0)
	v_max_f32_e32 v226, v226, v226
	v_max_f32_e32 v227, v227, v227
	v_max_f32_e32 v228, v228, v228
	v_max_f32_e32 v229, v229, v229
	v_max_f32_e32 v230, v230, v230
	v_max_f32_e32 v231, v231, v231
	v_max_f32_e32 v232, v232, v232
	v_max_f32_e32 v233, v233, v233
	v_max_f32_e32 v234, v234, v234
	v_max_f32_e32 v235, v235, v235
	v_max_f32_e32 v236, v236, v236
	v_max_f32_e32 v237, v237, v237
	v_max_f32_e32 v238, v238, v238
	v_max_f32_e32 v239, v239, v239
	v_max_f32_e32 v240, v240, v240
	v_max_f32_e32 v241, v241, v241
	v_med3_f32 v226, v226, s62, v95
	v_med3_f32 v227, v227, s62, v95
	v_med3_f32 v228, v228, s62, v95
	v_med3_f32 v229, v229, s62, v95
	v_med3_f32 v230, v230, s62, v95
	v_med3_f32 v231, v231, s62, v95
	v_med3_f32 v232, v232, s62, v95
	v_med3_f32 v233, v233, s62, v95
	v_med3_f32 v234, v234, s62, v95
	v_med3_f32 v235, v235, s62, v95
	v_med3_f32 v236, v236, s62, v95
	v_med3_f32 v237, v237, s62, v95
	v_med3_f32 v238, v238, s62, v95
	v_med3_f32 v239, v239, s62, v95
	v_med3_f32 v240, v240, s62, v95
	v_med3_f32 v241, v241, s62, v95
	v_mov_b32_e32 v242, 0
	v_mov_b32_e32 v243, 0
	v_mov_b32_e32 v244, 0
	v_mov_b32_e32 v245, 0
	v_cvt_pk_fp8_f32 v242, v226, v227
	v_cvt_pk_fp8_f32 v243, v230, v231
	v_cvt_pk_fp8_f32 v244, v234, v235
	v_cvt_pk_fp8_f32 v245, v238, v239
	v_cvt_pk_fp8_f32 v242, v228, v229 op_sel:[0,0,1]
	v_cvt_pk_fp8_f32 v243, v232, v233 op_sel:[0,0,1]
	v_cvt_pk_fp8_f32 v244, v236, v237 op_sel:[0,0,1]
	v_cvt_pk_fp8_f32 v245, v240, v241 op_sel:[0,0,1]
	s_nop 0
	global_store_dwordx4 v78, v[242:245], s[6:7]
	s_waitcnt vmcnt(12)
	v_mul_f32_e32 v144, v66, v144
	v_mul_f32_e32 v145, v66, v145
	v_mul_f32_e32 v146, v66, v146
	v_mul_f32_e32 v147, v66, v147
	ds_write_b128 v209, v[144:147]
	v_mul_f32_e32 v148, v67, v148
	v_mul_f32_e32 v149, v67, v149
	v_mul_f32_e32 v150, v67, v150
	v_mul_f32_e32 v151, v67, v151
	ds_write_b128 v209, v[148:151] offset:1024
	v_mul_f32_e32 v152, v68, v152
	v_mul_f32_e32 v153, v68, v153
	v_mul_f32_e32 v154, v68, v154
	v_mul_f32_e32 v155, v68, v155
	ds_write_b128 v209, v[152:155] offset:2048
	v_mul_f32_e32 v156, v69, v156
	v_mul_f32_e32 v157, v69, v157
	v_mul_f32_e32 v158, v69, v158
	v_mul_f32_e32 v159, v69, v159
	ds_write_b128 v209, v[156:159] offset:3072
	v_mul_f32_e32 v160, v70, v160
	v_mul_f32_e32 v161, v70, v161
	v_mul_f32_e32 v162, v70, v162
	v_mul_f32_e32 v163, v70, v163
	ds_write_b128 v209, v[160:163] offset:4096
	v_mul_f32_e32 v164, v71, v164
	v_mul_f32_e32 v165, v71, v165
	v_mul_f32_e32 v166, v71, v166
	v_mul_f32_e32 v167, v71, v167
	ds_write_b128 v209, v[164:167] offset:5120
	v_mul_f32_e32 v168, v72, v168
	v_mul_f32_e32 v169, v72, v169
	v_mul_f32_e32 v170, v72, v170
	v_mul_f32_e32 v171, v72, v171
	ds_write_b128 v209, v[168:171] offset:6144
	v_mul_f32_e32 v172, v73, v172
	v_mul_f32_e32 v173, v73, v173
	v_mul_f32_e32 v174, v73, v174
	v_mul_f32_e32 v175, v73, v175
	ds_write_b128 v209, v[172:175] offset:7168
	s_waitcnt lgkmcnt(0)
	s_barrier
; #define GAS __attribute__((address_space(1)))
; #define LAS __attribute__((address_space(3)))
; #define LDS_WAIT() asm volatile("s_waitcnt lgkmcnt(0)" ::: "memory")
;     const int pr = item >> 1, kb = 2 * (pr / nblk) + (item & 1), nb = pr % nblk, k0 = 64 * kb, n0 = 32 * nb;
;     const int nr = n0 + (lane & 31); const int sc = MAP == 1 ? src_col_in(nr) : nr;
;     float v[32];
; #pragma unroll
;     for (int i = 0; i < 32; ++i) v[i] = sc >= 0 ? W[(size_t)(k0 + 2 * i + (lane >> 5)) * Nsrc + sc] : 0.f;
; #pragma unroll
;     for (int i = 0; i < 32; ++i) { const int k = k0 + 2 * i + (lane >> 5); float x = v[i] * wscale; if (KS) x *= (k < ksplit ? ksA[k] : ksB[k - ksplit]); scr[(2 * i + (lane >> 5)) * 33 + (lane & 31)] = x; }
;     LDS_WAIT(); asm volatile("" ::: "memory");
;     const int c = lane & 7;
; #pragma unroll
;     for (int j = 0; j < 4; ++j) { const int n = (lane >> 3) + 8 * j; const LAS float* s = scr + (8 * c) * 33 + n;
;         const unsigned long long o = (unsigned long long)pg8::pk4_fp8(s[0 * 33], s[1 * 33], s[2 * 33], s[3 * 33]) | ((unsigned long long)pg8::pk4_fp8(s[4 * 33], s[5 * 33], s[6 * 33], s[7 * 33]) << 32);
;         *(GAS unsigned long long*)(WT + (size_t)(n0 + n) * K + k0 + 8 * c) = o; }
;     LDS_WAIT(); asm volatile("" ::: "memory");
; }
	s_add_u32 s6, s60, 0x800000
	s_addc_u32 s7, s61, 0
	ds_read_b32 v226, v211
	ds_read_b32 v227, v211 offset:512
	ds_read_b32 v228, v211 offset:1024
	ds_read_b32 v229, v211 offset:1536
	ds_read_b32 v230, v211 offset:2048
	ds_read_b32 v231, v211 offset:2560
	ds_read_b32 v232, v211 offset:3072
	ds_read_b32 v233, v211 offset:3584
	ds_read_b32 v234, v211 offset:4096
	ds_read_b32 v235, v211 offset:4608
	ds_read_b32 v236, v211 offset:5120
	ds_read_b32 v237, v211 offset:5632
	ds_read_b32 v238, v211 offset:6144
	ds_read_b32 v239, v211 offset:6656
	ds_read_b32 v240, v211 offset:7168
	ds_read_b32 v241, v211 offset:7680
	s_waitcnt lgkmcnt(0)
	v_max_f32_e32 v226, v226, v226
	v_max_f32_e32 v227, v227, v227
	v_max_f32_e32 v228, v228, v228
	v_max_f32_e32 v229, v229, v229
	v_max_f32_e32 v230, v230, v230
	v_max_f32_e32 v231, v231, v231
	v_max_f32_e32 v232, v232, v232
	v_max_f32_e32 v233, v233, v233
	v_max_f32_e32 v234, v234, v234
	v_max_f32_e32 v235, v235, v235
	v_max_f32_e32 v236, v236, v236
	v_max_f32_e32 v237, v237, v237
	v_max_f32_e32 v238, v238, v238
	v_max_f32_e32 v239, v239, v239
	v_max_f32_e32 v240, v240, v240
	v_max_f32_e32 v241, v241, v241
	v_med3_f32 v226, v226, s62, v95
	v_med3_f32 v227, v227, s62, v95
	v_med3_f32 v228, v228, s62, v95
	v_med3_f32 v229, v229, s62, v95
	v_med3_f32 v230, v230, s62, v95
	v_med3_f32 v231, v231, s62, v95
	v_med3_f32 v232, v232, s62, v95
	v_med3_f32 v233, v233, s62, v95
	v_med3_f32 v234, v234, s62, v95
	v_med3_f32 v235, v235, s62, v95
	v_med3_f32 v236, v236, s62, v95
	v_med3_f32 v237, v237, s62, v95
	v_med3_f32 v238, v238, s62, v95
	v_med3_f32 v239, v239, s62, v95
	v_med3_f32 v240, v240, s62, v95
	v_med3_f32 v241, v241, s62, v95
	v_mov_b32_e32 v242, 0
	v_mov_b32_e32 v243, 0
	v_mov_b32_e32 v244, 0
	v_mov_b32_e32 v245, 0
	v_cvt_pk_fp8_f32 v242, v226, v227
	v_cvt_pk_fp8_f32 v243, v230, v231
	v_cvt_pk_fp8_f32 v244, v234, v235
	v_cvt_pk_fp8_f32 v245, v238, v239
	v_cvt_pk_fp8_f32 v242, v228, v229 op_sel:[0,0,1]
	v_cvt_pk_fp8_f32 v243, v232, v233 op_sel:[0,0,1]
	v_cvt_pk_fp8_f32 v244, v236, v237 op_sel:[0,0,1]
	v_cvt_pk_fp8_f32 v245, v240, v241 op_sel:[0,0,1]
	s_nop 0
	global_store_dwordx4 v77, v[242:245], s[6:7]
	ds_read_b32 v226, v213
	ds_read_b32 v227, v213 offset:512
	ds_read_b32 v228, v213 offset:1024
	ds_read_b32 v229, v213 offset:1536
	ds_read_b32 v230, v213 offset:2048
	ds_read_b32 v231, v213 offset:2560
	ds_read_b32 v232, v213 offset:3072
	ds_read_b32 v233, v213 offset:3584
	ds_read_b32 v234, v213 offset:4096
	ds_read_b32 v235, v213 offset:4608
	ds_read_b32 v236, v213 offset:5120
	ds_read_b32 v237, v213 offset:5632
	ds_read_b32 v238, v213 offset:6144
	ds_read_b32 v239, v213 offset:6656
	ds_read_b32 v240, v213 offset:7168
	ds_read_b32 v241, v213 offset:7680
	s_waitcnt lgkmcnt(0)
	v_max_f32_e32 v226, v226, v226
	v_max_f32_e32 v227, v227, v227
	v_max_f32_e32 v228, v228, v228
	v_max_f32_e32 v229, v229, v229
	v_max_f32_e32 v230, v230, v230
	v_max_f32_e32 v231, v231, v231
	v_max_f32_e32 v232, v232, v232
	v_max_f32_e32 v233, v233, v233
	v_max_f32_e32 v234, v234, v234
	v_max_f32_e32 v235, v235, v235
	v_max_f32_e32 v236, v236, v236
	v_max_f32_e32 v237, v237, v237
	v_max_f32_e32 v238, v238, v238
	v_max_f32_e32 v239, v239, v239
	v_max_f32_e32 v240, v240, v240
	v_max_f32_e32 v241, v241, v241
	v_med3_f32 v226, v226, s62, v95
	v_med3_f32 v227, v227, s62, v95
	v_med3_f32 v228, v228, s62, v95
	v_med3_f32 v229, v229, s62, v95
	v_med3_f32 v230, v230, s62, v95
	v_med3_f32 v231, v231, s62, v95
	v_med3_f32 v232, v232, s62, v95
	v_med3_f32 v233, v233, s62, v95
	v_med3_f32 v234, v234, s62, v95
	v_med3_f32 v235, v235, s62, v95
	v_med3_f32 v236, v236, s62, v95
	v_med3_f32 v237, v237, s62, v95
	v_med3_f32 v238, v238, s62, v95
	v_med3_f32 v239, v239, s62, v95
	v_med3_f32 v240, v240, s62, v95
	v_med3_f32 v241, v241, s62, v95
	v_mov_b32_e32 v242, 0
	v_mov_b32_e32 v243, 0
	v_mov_b32_e32 v244, 0
	v_mov_b32_e32 v245, 0
	v_cvt_pk_fp8_f32 v242, v226, v227
	v_cvt_pk_fp8_f32 v243, v230, v231
	v_cvt_pk_fp8_f32 v244, v234, v235
	v_cvt_pk_fp8_f32 v245, v238, v239
	v_cvt_pk_fp8_f32 v242, v228, v229 op_sel:[0,0,1]
	v_cvt_pk_fp8_f32 v243, v232, v233 op_sel:[0,0,1]
	v_cvt_pk_fp8_f32 v244, v236, v237 op_sel:[0,0,1]
	v_cvt_pk_fp8_f32 v245, v240, v241 op_sel:[0,0,1]
	s_nop 0
	global_store_dwordx4 v78, v[242:245], s[6:7]
	s_waitcnt vmcnt(4)
	v_mul_f32_e32 v176, v66, v176
	v_mul_f32_e32 v177, v66, v177
	v_mul_f32_e32 v178, v66, v178
	v_mul_f32_e32 v179, v66, v179
	ds_write_b128 v210, v[176:179]
	v_mul_f32_e32 v180, v67, v180
	v_mul_f32_e32 v181, v67, v181
	v_mul_f32_e32 v182, v67, v182
	v_mul_f32_e32 v183, v67, v183
	ds_write_b128 v210, v[180:183] offset:1024
	v_mul_f32_e32 v184, v68, v184
	v_mul_f32_e32 v185, v68, v185
	v_mul_f32_e32 v186, v68, v186
	v_mul_f32_e32 v187, v68, v187
	ds_write_b128 v210, v[184:187] offset:2048
	v_mul_f32_e32 v188, v69, v188
	v_mul_f32_e32 v189, v69, v189
	v_mul_f32_e32 v190, v69, v190
	v_mul_f32_e32 v191, v69, v191
	ds_write_b128 v210, v[188:191] offset:3072
	v_mul_f32_e32 v192, v70, v192
	v_mul_f32_e32 v193, v70, v193
	v_mul_f32_e32 v194, v70, v194
	v_mul_f32_e32 v195, v70, v195
	ds_write_b128 v210, v[192:195] offset:4096
	v_mul_f32_e32 v196, v71, v196
	v_mul_f32_e32 v197, v71, v197
	v_mul_f32_e32 v198, v71, v198
	v_mul_f32_e32 v199, v71, v199
	ds_write_b128 v210, v[196:199] offset:5120
	v_mul_f32_e32 v200, v72, v200
	v_mul_f32_e32 v201, v72, v201
	v_mul_f32_e32 v202, v72, v202
	v_mul_f32_e32 v203, v72, v203
	ds_write_b128 v210, v[200:203] offset:6144
	v_mul_f32_e32 v204, v73, v204
	v_mul_f32_e32 v205, v73, v205
	v_mul_f32_e32 v206, v73, v206
	v_mul_f32_e32 v207, v73, v207
	ds_write_b128 v210, v[204:207] offset:7168
	s_waitcnt lgkmcnt(0)
	s_barrier
; #define GAS __attribute__((address_space(1)))
; #define LAS __attribute__((address_space(3)))
; #define LDS_WAIT() asm volatile("s_waitcnt lgkmcnt(0)" ::: "memory")
;     const int pr = item >> 1, kb = 2 * (pr / nblk) + (item & 1), nb = pr % nblk, k0 = 64 * kb, n0 = 32 * nb;
;     const int nr = n0 + (lane & 31); const int sc = MAP == 1 ? src_col_in(nr) : nr;
;     float v[32];
; #pragma unroll
;     for (int i = 0; i < 32; ++i) v[i] = sc >= 0 ? W[(size_t)(k0 + 2 * i + (lane >> 5)) * Nsrc + sc] : 0.f;
; #pragma unroll
;     for (int i = 0; i < 32; ++i) { const int k = k0 + 2 * i + (lane >> 5); float x = v[i] * wscale; if (KS) x *= (k < ksplit ? ksA[k] : ksB[k - ksplit]); scr[(2 * i + (lane >> 5)) * 33 + (lane & 31)] = x; }
;     LDS_WAIT(); asm volatile("" ::: "memory");
;     const int c = lane & 7;
; #pragma unroll
;     for (int j = 0; j < 4; ++j) { const int n = (lane >> 3) + 8 * j; const LAS float* s = scr + (8 * c) * 33 + n;
;         const unsigned long long o = (unsigned long long)pg8::pk4_fp8(s[0 * 33], s[1 * 33], s[2 * 33], s[3 * 33]) | ((unsigned long long)pg8::pk4_fp8(s[4 * 33], s[5 * 33], s[6 * 33], s[7 * 33]) << 32);
;         *(GAS unsigned long long*)(WT + (size_t)(n0 + n) * K + k0 + 8 * c) = o; }
;     LDS_WAIT(); asm volatile("" ::: "memory");
; }
	s_add_u32 s6, s60, 0xc00000
	s_addc_u32 s7, s61, 0
	ds_read_b32 v226, v212
	ds_read_b32 v227, v212 offset:512
	ds_read_b32 v228, v212 offset:1024
	ds_read_b32 v229, v212 offset:1536
	ds_read_b32 v230, v212 offset:2048
	ds_read_b32 v231, v212 offset:2560
	ds_read_b32 v232, v212 offset:3072
	ds_read_b32 v233, v212 offset:3584
	ds_read_b32 v234, v212 offset:4096
	ds_read_b32 v235, v212 offset:4608
	ds_read_b32 v236, v212 offset:5120
	ds_read_b32 v237, v212 offset:5632
	ds_read_b32 v238, v212 offset:6144
	ds_read_b32 v239, v212 offset:6656
	ds_read_b32 v240, v212 offset:7168
	ds_read_b32 v241, v212 offset:7680
	s_waitcnt lgkmcnt(0)
	v_max_f32_e32 v226, v226, v226
	v_max_f32_e32 v227, v227, v227
	v_max_f32_e32 v228, v228, v228
	v_max_f32_e32 v229, v229, v229
	v_max_f32_e32 v230, v230, v230
	v_max_f32_e32 v231, v231, v231
	v_max_f32_e32 v232, v232, v232
	v_max_f32_e32 v233, v233, v233
	v_max_f32_e32 v234, v234, v234
	v_max_f32_e32 v235, v235, v235
	v_max_f32_e32 v236, v236, v236
	v_max_f32_e32 v237, v237, v237
	v_max_f32_e32 v238, v238, v238
	v_max_f32_e32 v239, v239, v239
	v_max_f32_e32 v240, v240, v240
	v_max_f32_e32 v241, v241, v241
	v_med3_f32 v226, v226, s62, v95
	v_med3_f32 v227, v227, s62, v95
	v_med3_f32 v228, v228, s62, v95
	v_med3_f32 v229, v229, s62, v95
	v_med3_f32 v230, v230, s62, v95
	v_med3_f32 v231, v231, s62, v95
	v_med3_f32 v232, v232, s62, v95
	v_med3_f32 v233, v233, s62, v95
	v_med3_f32 v234, v234, s62, v95
	v_med3_f32 v235, v235, s62, v95
	v_med3_f32 v236, v236, s62, v95
	v_med3_f32 v237, v237, s62, v95
	v_med3_f32 v238, v238, s62, v95
	v_med3_f32 v239, v239, s62, v95
	v_med3_f32 v240, v240, s62, v95
	v_med3_f32 v241, v241, s62, v95
	v_mov_b32_e32 v242, 0
	v_mov_b32_e32 v243, 0
	v_mov_b32_e32 v244, 0
	v_mov_b32_e32 v245, 0
	v_cvt_pk_fp8_f32 v242, v226, v227
	v_cvt_pk_fp8_f32 v243, v230, v231
	v_cvt_pk_fp8_f32 v244, v234, v235
	v_cvt_pk_fp8_f32 v245, v238, v239
	v_cvt_pk_fp8_f32 v242, v228, v229 op_sel:[0,0,1]
	v_cvt_pk_fp8_f32 v243, v232, v233 op_sel:[0,0,1]
	v_cvt_pk_fp8_f32 v244, v236, v237 op_sel:[0,0,1]
	v_cvt_pk_fp8_f32 v245, v240, v241 op_sel:[0,0,1]
	s_nop 0
	global_store_dwordx4 v77, v[242:245], s[6:7]
	ds_read_b32 v226, v214
	ds_read_b32 v227, v214 offset:512
	ds_read_b32 v228, v214 offset:1024
	ds_read_b32 v229, v214 offset:1536
	ds_read_b32 v230, v214 offset:2048
	ds_read_b32 v231, v214 offset:2560
	ds_read_b32 v232, v214 offset:3072
	ds_read_b32 v233, v214 offset:3584
	ds_read_b32 v234, v214 offset:4096
	ds_read_b32 v235, v214 offset:4608
	ds_read_b32 v236, v214 offset:5120
	ds_read_b32 v237, v214 offset:5632
	ds_read_b32 v238, v214 offset:6144
	ds_read_b32 v239, v214 offset:6656
	ds_read_b32 v240, v214 offset:7168
	ds_read_b32 v241, v214 offset:7680
	s_waitcnt lgkmcnt(0)
	v_max_f32_e32 v226, v226, v226
	v_max_f32_e32 v227, v227, v227
	v_max_f32_e32 v228, v228, v228
	v_max_f32_e32 v229, v229, v229
	v_max_f32_e32 v230, v230, v230
	v_max_f32_e32 v231, v231, v231
	v_max_f32_e32 v232, v232, v232
	v_max_f32_e32 v233, v233, v233
	v_max_f32_e32 v234, v234, v234
	v_max_f32_e32 v235, v235, v235
	v_max_f32_e32 v236, v236, v236
	v_max_f32_e32 v237, v237, v237
	v_max_f32_e32 v238, v238, v238
	v_max_f32_e32 v239, v239, v239
	v_max_f32_e32 v240, v240, v240
	v_max_f32_e32 v241, v241, v241
	v_med3_f32 v226, v226, s62, v95
	v_med3_f32 v227, v227, s62, v95
	v_med3_f32 v228, v228, s62, v95
	v_med3_f32 v229, v229, s62, v95
	v_med3_f32 v230, v230, s62, v95
	v_med3_f32 v231, v231, s62, v95
	v_med3_f32 v232, v232, s62, v95
	v_med3_f32 v233, v233, s62, v95
	v_med3_f32 v234, v234, s62, v95
	v_med3_f32 v235, v235, s62, v95
	v_med3_f32 v236, v236, s62, v95
	v_med3_f32 v237, v237, s62, v95
	v_med3_f32 v238, v238, s62, v95
	v_med3_f32 v239, v239, s62, v95
	v_med3_f32 v240, v240, s62, v95
	v_med3_f32 v241, v241, s62, v95
	v_mov_b32_e32 v242, 0
	v_mov_b32_e32 v243, 0
	v_mov_b32_e32 v244, 0
	v_mov_b32_e32 v245, 0
	v_cvt_pk_fp8_f32 v242, v226, v227
	v_cvt_pk_fp8_f32 v243, v230, v231
	v_cvt_pk_fp8_f32 v244, v234, v235
	v_cvt_pk_fp8_f32 v245, v238, v239
	v_cvt_pk_fp8_f32 v242, v228, v229 op_sel:[0,0,1]
	v_cvt_pk_fp8_f32 v243, v232, v233 op_sel:[0,0,1]
	v_cvt_pk_fp8_f32 v244, v236, v237 op_sel:[0,0,1]
	v_cvt_pk_fp8_f32 v245, v240, v241 op_sel:[0,0,1]
	s_nop 0
	global_store_dwordx4 v78, v[242:245], s[6:7]
	s_waitcnt lgkmcnt(0)
	s_barrier
; __global__ void __launch_bounds__(NWAVES * 64, 2) hybrid_fwd(Args args) {
;     ...
;     for (int L = 0; L < DEPTH; ++L) {
;         { unsigned long long wz = 0; asm volatile("" : "+s"(wz)); ws = args.ws + wz; }
;         bf16* Hres = (bf16*)(ws + WS_H);     static_assert(DEPTH == 2 && WO_F8_FROM == 1 && PROJ_F8_FROM == 1, "the phase instantiations below are written for this precision plan");
;         bf16* XN = (bf16*)(ws + WS_XN); bf16* PROJ = (bf16*)(ws + WS_PROJ); bf16* ACT = (bf16*)(ws + WS_ACT); unsigned char* CAT = (unsigned char*)(ws + WS_CAT);     const bool wo_f8 = L >= WO_F8_FROM;
;         float* ATT = (float*)(ws + WS_ATT); bf16* XBC = (bf16*)(ws + WS_XBC); bf16* Y = (bf16*)(ws + WS_Y);
;         bf16* KC = (bf16*)(ws + WS_KC); bf16* VC = (bf16*)(ws + WS_VC); float* DT = (float*)(ws + WS_DT); float* ADT = (float*)(ws + WS_ADT);
;         float* COS = (float*)(ws + WS_COS); float* SIN = (float*)(ws + WS_SIN); unsigned* BMP = (unsigned*)(ws + WS_BMP);
;         bf16* AO = (bf16*)(ws + WS_ACT);     float* STT = (float*)(ws + WS_ST); bf16* PREVB = (bf16*)(ws + WS_PREV);     float* ACSG = (float*)(ws + WS_ACSG); float* DEC = (float*)(ws + WS_DEC);
;         {
;             const bool split = (L < PROJ_F8_FROM) && (F.G == 256);
;             if (L >= PROJ_F8_FROM) { pg8::StaticOrder So; So.init(S, NPROJ, F.G, (int)blockIdx.x); pg8::Gemm g{XN, (const bf16*)(ws + WS_WIN + L * SZ_WIN), S, NPROJ, DM / 2};
	v_readlane_b32 s12, v253, 35
	v_readlane_b32 s18, v253, 41
	v_readlane_b32 s19, v253, 42
	s_add_u32 s81, s18, 0x1f600000
	s_addc_u32 s94, s19, 0
	s_add_u32 s24, s18, 0xf600000
	v_or_b32_e32 v2, 2, v6
	v_mov_b32_e32 v3, 0x630
	v_readlane_b32 s13, v253, 36
	v_readlane_b32 s14, v253, 37
	v_readlane_b32 s15, v253, 38
	s_addc_u32 s25, s19, 0
	v_mad_u32_u24 v58, v2, s0, v3
	v_mov_b32_e32 v3, 0xc60
	s_add_u32 s26, s18, 0xb600000
	v_mad_u32_u24 v59, v2, s0, v3
	v_readlane_b32 s0, v253, 19
	s_addc_u32 s27, s19, 0
	v_readlane_b32 s2, v253, 21
	v_readlane_b32 s10, v253, 29
	v_readlane_b32 s3, v253, 22
	v_readlane_b32 s11, v253, 30
	s_add_u32 s2, s10, 0x4000000
	v_readlane_b32 s40, v253, 3
	s_addc_u32 s3, s11, 0
	v_readlane_b32 s52, v253, 15
	v_readlane_b32 s53, v253, 16
	s_add_u32 s22, s52, 0x2000
	v_readlane_b32 s8, v253, 27
	s_addc_u32 s23, s53, 0
	v_readlane_b32 s9, v253, 28
	s_add_u32 s84, s8, 0x2000
	s_addc_u32 s85, s9, 0
	s_add_u32 s33, s18, 0x200000
	v_readlane_b32 s44, v253, 7
	s_addc_u32 s38, s19, 0
	v_mov_b32_e32 v9, v11
	v_readlane_b32 s1, v253, 20
	v_readlane_b32 s45, v253, 8
	s_add_u32 s86, s44, 0xb140000
	v_mul_u32_u24_e32 v57, 0x84, v2
	v_readlane_b32 s42, v253, 5
	v_lshl_add_u64 v[2:3], s[18:19], 0, v[8:9]
	s_mov_b64 s[0:1], 0xd600000
	s_addc_u32 s87, s45, 0
	v_readlane_b32 s12, v253, 31
	v_readlane_b32 s13, v253, 32
	v_readlane_b32 s14, v253, 33
	v_readlane_b32 s15, v253, 34
	v_readlane_b32 s43, v253, 6
	v_readlane_b32 s54, v253, 17
	v_readlane_b32 s55, v253, 18
	v_lshl_add_u64 v[12:13], v[2:3], 0, s[0:1]
	s_add_u32 s88, s42, 0x4000
	s_mov_b64 s[0:1], 0x5c00000
	v_readlane_b32 s41, v253, 4
	v_readlane_b32 s46, v253, 9
	v_readlane_b32 s47, v253, 10
	v_readlane_b32 s48, v253, 11
	v_readlane_b32 s49, v253, 12
	v_readlane_b32 s50, v253, 13
	s_addc_u32 s89, s43, 0
	v_lshlrev_b32_e32 v4, 6, v18
	v_lshl_add_u64 v[14:15], v[2:3], 0, s[0:1]
	s_lshl_b32 s0, s80, 5
	s_movk_i32 s12, 0xe000
	s_movk_i32 s14, 0xe008
	s_movk_i32 s18, 0xe010
	s_movk_i32 s78, 0xe018
	s_movk_i32 s92, 0xe0d0
	s_movk_i32 s28, 0xe0d8
	s_movk_i32 s34, 0xe0e0
	s_movk_i32 s52, 0xe0e8
	s_movk_i32 s54, 0xe0f0
	s_movk_i32 s56, 0xe0f8
	v_or_b32_e32 v26, 0x2000, v18
	v_or_b32_e32 v27, 0x4000, v18
	v_or_b32_e32 v28, 0x6000, v18
	v_or_b32_e32 v29, 0x8000, v18
	v_or_b32_e32 v30, 0xa000, v18
	v_or_b32_e32 v31, 0xc000, v18
	v_or_b32_e32 v32, 0xe000, v18
	v_or_b32_e32 v33, 0x10000, v18
	v_or_b32_e32 v34, 0x12000, v18
	v_or_b32_e32 v35, 0x14000, v18
	v_or_b32_e32 v36, 0x16000, v18
	v_or_b32_e32 v37, 0x18000, v18
	v_or_b32_e32 v38, 0x1a000, v18
	v_or_b32_e32 v39, 0x1c000, v18
	v_or_b32_e32 v40, 0x1e000, v18
	v_or_b32_e32 v41, 0x20000, v18
	v_or_b32_e32 v42, 0x22000, v18
	v_or_b32_e32 v43, 0x24000, v18
	v_or_b32_e32 v44, 0x26000, v18
	v_or_b32_e32 v45, 0x28000, v18
	v_or_b32_e32 v46, 0x2a000, v18
	v_or_b32_e32 v47, 0x2c000, v18
	v_or_b32_e32 v48, 0x2e000, v18
	v_or_b32_e32 v49, 0x30000, v18
	v_or_b32_e32 v50, 0x32000, v18
	v_or_b32_e32 v51, 0x34000, v18
	v_or_b32_e32 v52, 0x36000, v18
	v_or_b32_e32 v53, 0x38000, v18
	v_or_b32_e32 v54, 0x3a000, v18
	v_or_b32_e32 v55, 0x3c000, v18
	v_or_b32_e32 v56, 0x3e000, v18
	v_and_b32_e32 v60, 64, v4
	v_mov_b32_e32 v7, v11
	s_lshl_b32 s39, s80, 6
	s_add_i32 s40, s0, 0xfff4c000
	s_lshl_b32 s41, s83, 8
	s_lshl_b32 s42, s80, 4
	s_lshl_b32 s43, s83, 7
	s_mov_b32 s91, 0
	s_mov_b32 s44, 0xc3e00000
	s_movk_i32 s45, 0x7fff
	s_mov_b32 s46, 0xffff0000
	s_movk_i32 s47, 0x2c2f
	s_movk_i32 s48, 0x2c50
	s_mov_b32 s49, 0xb140
	v_add_u32_e32 v61, 0x400, v19
	v_add_u32_e32 v62, 0x800, v19
	v_add_u32_e32 v63, 0xc00, v19
	v_mov_b32_e32 v64, 0x43e00000
	s_mov_b32 s50, s80
	s_mov_b32 s13, -1
	s_mov_b32 s15, -1
	s_mov_b32 s19, -1
	s_mov_b32 s79, -1
	s_mov_b32 s93, -1
	s_mov_b32 s29, -1
	s_mov_b32 s35, -1
	s_mov_b32 s53, -1
	s_mov_b32 s55, -1
	s_mov_b32 s57, -1
	v_readlane_b32 s16, v253, 39
	v_readlane_b32 s17, v253, 40
	v_readlane_b32 s4, v253, 23
	v_readlane_b32 s5, v253, 24
	v_readlane_b32 s6, v253, 25
	v_readlane_b32 s7, v253, 26
	v_readlane_b32 s51, v253, 14
	s_branch .LBB0_15

; #define GAS __attribute__((address_space(1)))
; #define LAS __attribute__((address_space(3)))
; #define LDS_WAIT() asm volatile("s_waitcnt lgkmcnt(0)" ::: "memory")
;     const int pr = item >> 1, kb = 2 * (pr / nblk) + (item & 1), nb = pr % nblk, k0 = 64 * kb, n0 = 32 * nb;
;     const int nr = n0 + (lane & 31); const int sc = MAP == 1 ? src_col_in(nr) : nr;
;     float v[32];
; #pragma unroll
;     for (int i = 0; i < 32; ++i) v[i] = sc >= 0 ? W[(size_t)(k0 + 2 * i + (lane >> 5)) * Nsrc + sc] : 0.f;
; #pragma unroll
;     for (int i = 0; i < 32; ++i) { const int k = k0 + 2 * i + (lane >> 5); float x = v[i] * wscale; if (KS) x *= (k < ksplit ? ksA[k] : ksB[k - ksplit]); scr[(2 * i + (lane >> 5)) * 33 + (lane & 31)] = x; }
;     LDS_WAIT(); asm volatile("" ::: "memory");
;     const int c = lane & 7;
; #pragma unroll
;     for (int j = 0; j < 4; ++j) { const int n = (lane >> 3) + 8 * j; const LAS float* s = scr + (8 * c) * 33 + n;
;         const unsigned long long o = (unsigned long long)pg8::pk4_fp8(s[0 * 33], s[1 * 33], s[2 * 33], s[3 * 33]) | ((unsigned long long)pg8::pk4_fp8(s[4 * 33], s[5 * 33], s[6 * 33], s[7 * 33]) << 32);
;         *(GAS unsigned long long*)(WT + (size_t)(n0 + n) * K + k0 + 8 * c) = o; }
;     LDS_WAIT(); asm volatile("" ::: "memory");
; }
; __global__ void __launch_bounds__(NWAVES * 64, 2) hybrid_fwd(Args args) {
;     ...
;             p0_transpose_item_f8<false>(args.in[16] + (size_t)l * FF * DM, FF, DM, DM / 32, (unsigned char*)(ws + WS_WDN + l * SZ_WDN), 128.f, args.in[16], args.in[16], 0, scr, r, lane);
.LBB0_680:
	s_andn2_b64 vcc, exec, s[50:51]
	s_mov_b64 s[0:1], -1
	s_cbranch_vccnz .LBB0_579
	s_and_b64 vcc, exec, s[12:13]
	s_cbranch_vccz .Llite0_skip
	s_waitcnt vmcnt(0) lgkmcnt(0)
	s_barrier
	v_readlane_b32 s16, v253, 43
	s_sub_i32 s16, s16, 160
	v_and_b32_e32 v133, 63, v0
	v_lshrrev_b32_e32 v134, 6, v0
	v_lshrrev_b32_e32 v130, 5, v133
	v_lshl_add_u32 v131, v134, 4, v130
	v_and_b32_e32 v132, 31, v133
	v_xor_b32_e32 v132, v132, v134
	v_lshlrev_b32_e32 v132, 4, v132
	v_lshl_add_u32 v120, v131, 9, v132
	v_add_u32_e32 v121, 0x10000, v120
	v_and_b32_e32 v132, 31, v133
	v_lshlrev_b32_e32 v132, 4, v132
	s_mov_b32 s21, 0x4000
	v_mad_u32_u24 v126, v131, s21, v132
	v_and_b32_e32 v130, 7, v133
	v_lshrrev_b32_e32 v131, 5, v133
	v_lshl_add_u32 v131, v134, 2, v131
	v_xor_b32_e32 v131, v131, v130
	v_lshlrev_b32_e32 v131, 4, v131
	v_lshl_add_u32 v131, v130, 13, v131
	v_bfe_u32 v132, v133, 3, 2
	v_lshl_add_u32 v122, v132, 2, v131
	v_add_u32_e32 v123, 0x10000, v122
	v_and_b32_e32 v130, 7, v133
	v_lshrrev_b32_e32 v131, 5, v133
	v_lshl_add_u32 v131, v134, 2, v131
	v_add_u32_e32 v131, 2, v131
	v_xor_b32_e32 v131, v131, v130
	v_lshlrev_b32_e32 v131, 4, v131
	v_lshl_add_u32 v131, v130, 13, v131
	v_bfe_u32 v132, v133, 3, 2
	v_lshl_add_u32 v124, v132, 2, v131
	v_add_u32_e32 v125, 0x10000, v124
	v_lshrrev_b32_e32 v130, 3, v133
	v_lshl_add_u32 v130, v134, 4, v130
	v_and_b32_e32 v131, 7, v133
	v_lshlrev_b32_e32 v131, 4, v131
	v_lshl_add_u32 v127, v130, 14, v131
	v_lshrrev_b32_e32 v130, 3, v133
	v_lshl_add_u32 v130, v134, 4, v130
	v_add_u32_e32 v130, 8, v130
	v_and_b32_e32 v131, 7, v133
	v_lshlrev_b32_e32 v131, 4, v131
	v_lshl_add_u32 v128, v130, 14, v131
	v_mov_b32_e32 v129, 0x43e00000
	s_mov_b32 s20, 0xc3e00000
	v_readlane_b32 s2, v253, 35
	v_readlane_b32 s3, v253, 36
	v_readlane_b32 s4, v253, 41
	v_readlane_b32 s5, v253, 42
	s_add_u32 s2, s2, 0x10000000
	s_addc_u32 s3, s3, 0
	s_add_u32 s4, s4, 0x27600000
	s_addc_u32 s5, s5, 0
	s_add_i32 s17, s16, 0
	s_min_u32 s17, s17, 0x7ff
	s_lshr_b32 s18, s17, 5
	s_add_i32 s18, s18, 0
	s_and_b32 s19, s17, 31
	s_lshl_b32 s18, s18, 21
	s_lshl_b32 s19, s19, 9
	s_add_u32 s18, s18, s19
	s_add_u32 s10, s2, s18
	s_addc_u32 s11, s3, 0
	global_load_dwordx4 v[36:39], v126, s[10:11]
	s_add_u32 s10, s10, 0x8000
	s_addc_u32 s11, s11, 0
	global_load_dwordx4 v[40:43], v126, s[10:11]
	s_add_u32 s10, s10, 0x8000
	s_addc_u32 s11, s11, 0
	global_load_dwordx4 v[44:47], v126, s[10:11]
	s_add_u32 s10, s10, 0x8000
	s_addc_u32 s11, s11, 0
	global_load_dwordx4 v[48:51], v126, s[10:11]
	s_add_u32 s10, s10, 0x8000
	s_addc_u32 s11, s11, 0
	global_load_dwordx4 v[52:55], v126, s[10:11]
	s_add_u32 s10, s10, 0x8000
	s_addc_u32 s11, s11, 0
	global_load_dwordx4 v[56:59], v126, s[10:11]
	s_add_u32 s10, s10, 0x8000
	s_addc_u32 s11, s11, 0
	global_load_dwordx4 v[60:63], v126, s[10:11]
	s_add_u32 s10, s10, 0x8000
	s_addc_u32 s11, s11, 0
	global_load_dwordx4 v[64:67], v126, s[10:11]
	s_add_i32 s17, s16, 96
	s_min_u32 s17, s17, 0x7ff
	s_lshr_b32 s18, s17, 5
	s_add_i32 s18, s18, 0
	s_and_b32 s19, s17, 31
	s_lshl_b32 s18, s18, 21
	s_lshl_b32 s19, s19, 9
	s_add_u32 s18, s18, s19
	s_add_u32 s10, s2, s18
	s_addc_u32 s11, s3, 0
	global_load_dwordx4 v[68:71], v126, s[10:11]
	s_add_u32 s10, s10, 0x8000
	s_addc_u32 s11, s11, 0
	global_load_dwordx4 v[72:75], v126, s[10:11]
	s_add_u32 s10, s10, 0x8000
	s_addc_u32 s11, s11, 0
	global_load_dwordx4 v[76:79], v126, s[10:11]
	s_add_u32 s10, s10, 0x8000
	s_addc_u32 s11, s11, 0
	global_load_dwordx4 v[80:83], v126, s[10:11]
	s_add_u32 s10, s10, 0x8000
	s_addc_u32 s11, s11, 0
	global_load_dwordx4 v[84:87], v126, s[10:11]
	s_add_u32 s10, s10, 0x8000
	s_addc_u32 s11, s11, 0
	global_load_dwordx4 v[88:91], v126, s[10:11]
	s_add_u32 s10, s10, 0x8000
	s_addc_u32 s11, s11, 0
	global_load_dwordx4 v[92:95], v126, s[10:11]
	s_add_u32 s10, s10, 0x8000
	s_addc_u32 s11, s11, 0
	global_load_dwordx4 v[96:99], v126, s[10:11]
	s_waitcnt vmcnt(8)
	v_mul_f32_e32 v36, 0x43000000, v36
	v_mul_f32_e32 v37, 0x43000000, v37
	v_mul_f32_e32 v38, 0x43000000, v38
	v_mul_f32_e32 v39, 0x43000000, v39
	ds_write_b128 v120, v[36:39]
	v_mul_f32_e32 v40, 0x43000000, v40
	v_mul_f32_e32 v41, 0x43000000, v41
	v_mul_f32_e32 v42, 0x43000000, v42
	v_mul_f32_e32 v43, 0x43000000, v43
	ds_write_b128 v120, v[40:43] offset:1024
	v_mul_f32_e32 v44, 0x43000000, v44
	v_mul_f32_e32 v45, 0x43000000, v45
	v_mul_f32_e32 v46, 0x43000000, v46
	v_mul_f32_e32 v47, 0x43000000, v47
	ds_write_b128 v120, v[44:47] offset:2048
	v_mul_f32_e32 v48, 0x43000000, v48
	v_mul_f32_e32 v49, 0x43000000, v49
	v_mul_f32_e32 v50, 0x43000000, v50
	v_mul_f32_e32 v51, 0x43000000, v51
	ds_write_b128 v120, v[48:51] offset:3072
	v_mul_f32_e32 v52, 0x43000000, v52
	v_mul_f32_e32 v53, 0x43000000, v53
	v_mul_f32_e32 v54, 0x43000000, v54
	v_mul_f32_e32 v55, 0x43000000, v55
	ds_write_b128 v120, v[52:55] offset:4096
	v_mul_f32_e32 v56, 0x43000000, v56
	v_mul_f32_e32 v57, 0x43000000, v57
	v_mul_f32_e32 v58, 0x43000000, v58
	v_mul_f32_e32 v59, 0x43000000, v59
	ds_write_b128 v120, v[56:59] offset:5120
	v_mul_f32_e32 v60, 0x43000000, v60
	v_mul_f32_e32 v61, 0x43000000, v61
	v_mul_f32_e32 v62, 0x43000000, v62
	v_mul_f32_e32 v63, 0x43000000, v63
	ds_write_b128 v120, v[60:63] offset:6144
	v_mul_f32_e32 v64, 0x43000000, v64
	v_mul_f32_e32 v65, 0x43000000, v65
	v_mul_f32_e32 v66, 0x43000000, v66
	v_mul_f32_e32 v67, 0x43000000, v67
	ds_write_b128 v120, v[64:67] offset:7168
	s_waitcnt lgkmcnt(0)
	s_barrier
; #define GAS __attribute__((address_space(1)))
; #define LAS __attribute__((address_space(3)))
; #define LDS_WAIT() asm volatile("s_waitcnt lgkmcnt(0)" ::: "memory")
;     const int pr = item >> 1, kb = 2 * (pr / nblk) + (item & 1), nb = pr % nblk, k0 = 64 * kb, n0 = 32 * nb;
;     const int nr = n0 + (lane & 31); const int sc = MAP == 1 ? src_col_in(nr) : nr;
;     float v[32];
; #pragma unroll
;     for (int i = 0; i < 32; ++i) v[i] = sc >= 0 ? W[(size_t)(k0 + 2 * i + (lane >> 5)) * Nsrc + sc] : 0.f;
; #pragma unroll
;     for (int i = 0; i < 32; ++i) { const int k = k0 + 2 * i + (lane >> 5); float x = v[i] * wscale; if (KS) x *= (k < ksplit ? ksA[k] : ksB[k - ksplit]); scr[(2 * i + (lane >> 5)) * 33 + (lane & 31)] = x; }
;     LDS_WAIT(); asm volatile("" ::: "memory");
;     const int c = lane & 7;
; #pragma unroll
;     for (int j = 0; j < 4; ++j) { const int n = (lane >> 3) + 8 * j; const LAS float* s = scr + (8 * c) * 33 + n;
;         const unsigned long long o = (unsigned long long)pg8::pk4_fp8(s[0 * 33], s[1 * 33], s[2 * 33], s[3 * 33]) | ((unsigned long long)pg8::pk4_fp8(s[4 * 33], s[5 * 33], s[6 * 33], s[7 * 33]) << 32);
;         *(GAS unsigned long long*)(WT + (size_t)(n0 + n) * K + k0 + 8 * c) = o; }
;     LDS_WAIT(); asm volatile("" ::: "memory");
; }
	s_add_i32 s17, s16, 192
	s_min_u32 s17, s17, 0x7ff
	s_lshr_b32 s18, s17, 5
	s_add_i32 s18, s18, 0
	s_and_b32 s19, s17, 31
	s_lshl_b32 s18, s18, 21
	s_lshl_b32 s19, s19, 9
	s_add_u32 s18, s18, s19
	s_add_u32 s10, s2, s18
	s_addc_u32 s11, s3, 0
	global_load_dwordx4 v[36:39], v126, s[10:11]
	s_add_u32 s10, s10, 0x8000
	s_addc_u32 s11, s11, 0
	global_load_dwordx4 v[40:43], v126, s[10:11]
	s_add_u32 s10, s10, 0x8000
	s_addc_u32 s11, s11, 0
	global_load_dwordx4 v[44:47], v126, s[10:11]
	s_add_u32 s10, s10, 0x8000
	s_addc_u32 s11, s11, 0
	global_load_dwordx4 v[48:51], v126, s[10:11]
	s_add_u32 s10, s10, 0x8000
	s_addc_u32 s11, s11, 0
	global_load_dwordx4 v[52:55], v126, s[10:11]
	s_add_u32 s10, s10, 0x8000
	s_addc_u32 s11, s11, 0
	global_load_dwordx4 v[56:59], v126, s[10:11]
	s_add_u32 s10, s10, 0x8000
	s_addc_u32 s11, s11, 0
	global_load_dwordx4 v[60:63], v126, s[10:11]
	s_add_u32 s10, s10, 0x8000
	s_addc_u32 s11, s11, 0
	global_load_dwordx4 v[64:67], v126, s[10:11]
	s_add_i32 s17, s16, 0
	s_min_u32 s17, s17, 0x7ff
	s_lshr_b32 s18, s17, 5
	s_add_i32 s18, s18, 0
	s_and_b32 s19, s17, 31
	s_lshl_b32 s19, s19, 21
	s_lshl_b32 s18, s18, 7
	s_add_u32 s18, s18, s19
	s_add_u32 s14, s4, s18
	s_addc_u32 s15, s5, 0
	ds_read_b32 v100, v122
	ds_read_b32 v101, v122 offset:512
	ds_read_b32 v102, v122 offset:1024
	ds_read_b32 v103, v122 offset:1536
	ds_read_b32 v104, v122 offset:2048
	ds_read_b32 v105, v122 offset:2560
	ds_read_b32 v106, v122 offset:3072
	ds_read_b32 v107, v122 offset:3584
	ds_read_b32 v108, v122 offset:4096
	ds_read_b32 v109, v122 offset:4608
	ds_read_b32 v110, v122 offset:5120
	ds_read_b32 v111, v122 offset:5632
	ds_read_b32 v112, v122 offset:6144
	ds_read_b32 v113, v122 offset:6656
	ds_read_b32 v114, v122 offset:7168
	ds_read_b32 v115, v122 offset:7680
	s_waitcnt lgkmcnt(0)
	v_max_f32_e32 v100, v100, v100
	v_max_f32_e32 v101, v101, v101
	v_max_f32_e32 v102, v102, v102
	v_max_f32_e32 v103, v103, v103
	v_max_f32_e32 v104, v104, v104
	v_max_f32_e32 v105, v105, v105
	v_max_f32_e32 v106, v106, v106
	v_max_f32_e32 v107, v107, v107
	v_max_f32_e32 v108, v108, v108
	v_max_f32_e32 v109, v109, v109
	v_max_f32_e32 v110, v110, v110
	v_max_f32_e32 v111, v111, v111
	v_max_f32_e32 v112, v112, v112
	v_max_f32_e32 v113, v113, v113
	v_max_f32_e32 v114, v114, v114
	v_max_f32_e32 v115, v115, v115
	v_med3_f32 v100, v100, s20, v129
	v_med3_f32 v101, v101, s20, v129
	v_med3_f32 v102, v102, s20, v129
	v_med3_f32 v103, v103, s20, v129
	v_med3_f32 v104, v104, s20, v129
	v_med3_f32 v105, v105, s20, v129
	v_med3_f32 v106, v106, s20, v129
	v_med3_f32 v107, v107, s20, v129
	v_med3_f32 v108, v108, s20, v129
	v_med3_f32 v109, v109, s20, v129
	v_med3_f32 v110, v110, s20, v129
	v_med3_f32 v111, v111, s20, v129
	v_med3_f32 v112, v112, s20, v129
	v_med3_f32 v113, v113, s20, v129
	v_med3_f32 v114, v114, s20, v129
	v_med3_f32 v115, v115, s20, v129
	v_mov_b32_e32 v116, 0
	v_mov_b32_e32 v117, 0
	v_mov_b32_e32 v118, 0
	v_mov_b32_e32 v119, 0
	v_cvt_pk_fp8_f32 v116, v100, v101
	v_cvt_pk_fp8_f32 v117, v104, v105
	v_cvt_pk_fp8_f32 v118, v108, v109
	v_cvt_pk_fp8_f32 v119, v112, v113
	v_cvt_pk_fp8_f32 v116, v102, v103 op_sel:[0,0,1]
	v_cvt_pk_fp8_f32 v117, v106, v107 op_sel:[0,0,1]
	v_cvt_pk_fp8_f32 v118, v110, v111 op_sel:[0,0,1]
	v_cvt_pk_fp8_f32 v119, v114, v115 op_sel:[0,0,1]
	s_nop 0
	global_store_dwordx4 v127, v[116:119], s[14:15]
	ds_read_b32 v100, v124
	ds_read_b32 v101, v124 offset:512
	ds_read_b32 v102, v124 offset:1024
	ds_read_b32 v103, v124 offset:1536
	ds_read_b32 v104, v124 offset:2048
	ds_read_b32 v105, v124 offset:2560
	ds_read_b32 v106, v124 offset:3072
	ds_read_b32 v107, v124 offset:3584
	ds_read_b32 v108, v124 offset:4096
	ds_read_b32 v109, v124 offset:4608
	ds_read_b32 v110, v124 offset:5120
	ds_read_b32 v111, v124 offset:5632
	ds_read_b32 v112, v124 offset:6144
	ds_read_b32 v113, v124 offset:6656
	ds_read_b32 v114, v124 offset:7168
	ds_read_b32 v115, v124 offset:7680
	s_waitcnt lgkmcnt(0)
	v_max_f32_e32 v100, v100, v100
	v_max_f32_e32 v101, v101, v101
	v_max_f32_e32 v102, v102, v102
	v_max_f32_e32 v103, v103, v103
	v_max_f32_e32 v104, v104, v104
	v_max_f32_e32 v105, v105, v105
	v_max_f32_e32 v106, v106, v106
	v_max_f32_e32 v107, v107, v107
	v_max_f32_e32 v108, v108, v108
	v_max_f32_e32 v109, v109, v109
	v_max_f32_e32 v110, v110, v110
	v_max_f32_e32 v111, v111, v111
	v_max_f32_e32 v112, v112, v112
	v_max_f32_e32 v113, v113, v113
	v_max_f32_e32 v114, v114, v114
	v_max_f32_e32 v115, v115, v115
	v_med3_f32 v100, v100, s20, v129
	v_med3_f32 v101, v101, s20, v129
	v_med3_f32 v102, v102, s20, v129
	v_med3_f32 v103, v103, s20, v129
	v_med3_f32 v104, v104, s20, v129
	v_med3_f32 v105, v105, s20, v129
	v_med3_f32 v106, v106, s20, v129
	v_med3_f32 v107, v107, s20, v129
	v_med3_f32 v108, v108, s20, v129
	v_med3_f32 v109, v109, s20, v129
	v_med3_f32 v110, v110, s20, v129
	v_med3_f32 v111, v111, s20, v129
	v_med3_f32 v112, v112, s20, v129
	v_med3_f32 v113, v113, s20, v129
	v_med3_f32 v114, v114, s20, v129
	v_med3_f32 v115, v115, s20, v129
	v_mov_b32_e32 v116, 0
	v_mov_b32_e32 v117, 0
	v_mov_b32_e32 v118, 0
	v_mov_b32_e32 v119, 0
	v_cvt_pk_fp8_f32 v116, v100, v101
	v_cvt_pk_fp8_f32 v117, v104, v105
	v_cvt_pk_fp8_f32 v118, v108, v109
	v_cvt_pk_fp8_f32 v119, v112, v113
	v_cvt_pk_fp8_f32 v116, v102, v103 op_sel:[0,0,1]
	v_cvt_pk_fp8_f32 v117, v106, v107 op_sel:[0,0,1]
	v_cvt_pk_fp8_f32 v118, v110, v111 op_sel:[0,0,1]
	v_cvt_pk_fp8_f32 v119, v114, v115 op_sel:[0,0,1]
	s_nop 0
	global_store_dwordx4 v128, v[116:119], s[14:15]
	s_waitcnt vmcnt(10)
	v_mul_f32_e32 v68, 0x43000000, v68
	v_mul_f32_e32 v69, 0x43000000, v69
	v_mul_f32_e32 v70, 0x43000000, v70
	v_mul_f32_e32 v71, 0x43000000, v71
	ds_write_b128 v121, v[68:71]
	v_mul_f32_e32 v72, 0x43000000, v72
	v_mul_f32_e32 v73, 0x43000000, v73
	v_mul_f32_e32 v74, 0x43000000, v74
	v_mul_f32_e32 v75, 0x43000000, v75
	ds_write_b128 v121, v[72:75] offset:1024
	v_mul_f32_e32 v76, 0x43000000, v76
	v_mul_f32_e32 v77, 0x43000000, v77
	v_mul_f32_e32 v78, 0x43000000, v78
	v_mul_f32_e32 v79, 0x43000000, v79
	ds_write_b128 v121, v[76:79] offset:2048
	v_mul_f32_e32 v80, 0x43000000, v80
	v_mul_f32_e32 v81, 0x43000000, v81
	v_mul_f32_e32 v82, 0x43000000, v82
	v_mul_f32_e32 v83, 0x43000000, v83
	ds_write_b128 v121, v[80:83] offset:3072
	v_mul_f32_e32 v84, 0x43000000, v84
	v_mul_f32_e32 v85, 0x43000000, v85
	v_mul_f32_e32 v86, 0x43000000, v86
	v_mul_f32_e32 v87, 0x43000000, v87
	ds_write_b128 v121, v[84:87] offset:4096
	v_mul_f32_e32 v88, 0x43000000, v88
	v_mul_f32_e32 v89, 0x43000000, v89
	v_mul_f32_e32 v90, 0x43000000, v90
	v_mul_f32_e32 v91, 0x43000000, v91
	ds_write_b128 v121, v[88:91] offset:5120
	v_mul_f32_e32 v92, 0x43000000, v92
	v_mul_f32_e32 v93, 0x43000000, v93
	v_mul_f32_e32 v94, 0x43000000, v94
	v_mul_f32_e32 v95, 0x43000000, v95
	ds_write_b128 v121, v[92:95] offset:6144
	v_mul_f32_e32 v96, 0x43000000, v96
	v_mul_f32_e32 v97, 0x43000000, v97
	v_mul_f32_e32 v98, 0x43000000, v98
	v_mul_f32_e32 v99, 0x43000000, v99
	ds_write_b128 v121, v[96:99] offset:7168
	s_waitcnt lgkmcnt(0)
	s_barrier
; #define GAS __attribute__((address_space(1)))
; #define LAS __attribute__((address_space(3)))
; #define LDS_WAIT() asm volatile("s_waitcnt lgkmcnt(0)" ::: "memory")
;     const int pr = item >> 1, kb = 2 * (pr / nblk) + (item & 1), nb = pr % nblk, k0 = 64 * kb, n0 = 32 * nb;
;     const int nr = n0 + (lane & 31); const int sc = MAP == 1 ? src_col_in(nr) : nr;
;     float v[32];
; #pragma unroll
;     for (int i = 0; i < 32; ++i) v[i] = sc >= 0 ? W[(size_t)(k0 + 2 * i + (lane >> 5)) * Nsrc + sc] : 0.f;
; #pragma unroll
;     for (int i = 0; i < 32; ++i) { const int k = k0 + 2 * i + (lane >> 5); float x = v[i] * wscale; if (KS) x *= (k < ksplit ? ksA[k] : ksB[k - ksplit]); scr[(2 * i + (lane >> 5)) * 33 + (lane & 31)] = x; }
;     LDS_WAIT(); asm volatile("" ::: "memory");
;     const int c = lane & 7;
; #pragma unroll
;     for (int j = 0; j < 4; ++j) { const int n = (lane >> 3) + 8 * j; const LAS float* s = scr + (8 * c) * 33 + n;
;         const unsigned long long o = (unsigned long long)pg8::pk4_fp8(s[0 * 33], s[1 * 33], s[2 * 33], s[3 * 33]) | ((unsigned long long)pg8::pk4_fp8(s[4 * 33], s[5 * 33], s[6 * 33], s[7 * 33]) << 32);
;         *(GAS unsigned long long*)(WT + (size_t)(n0 + n) * K + k0 + 8 * c) = o; }
;     LDS_WAIT(); asm volatile("" ::: "memory");
; }
	s_add_i32 s17, s16, 288
	s_min_u32 s17, s17, 0x7ff
	s_lshr_b32 s18, s17, 5
	s_add_i32 s18, s18, 0
	s_and_b32 s19, s17, 31
	s_lshl_b32 s18, s18, 21
	s_lshl_b32 s19, s19, 9
	s_add_u32 s18, s18, s19
	s_add_u32 s10, s2, s18
	s_addc_u32 s11, s3, 0
	global_load_dwordx4 v[68:71], v126, s[10:11]
	s_add_u32 s10, s10, 0x8000
	s_addc_u32 s11, s11, 0
	global_load_dwordx4 v[72:75], v126, s[10:11]
	s_add_u32 s10, s10, 0x8000
	s_addc_u32 s11, s11, 0
	global_load_dwordx4 v[76:79], v126, s[10:11]
	s_add_u32 s10, s10, 0x8000
	s_addc_u32 s11, s11, 0
	global_load_dwordx4 v[80:83], v126, s[10:11]
	s_add_u32 s10, s10, 0x8000
	s_addc_u32 s11, s11, 0
	global_load_dwordx4 v[84:87], v126, s[10:11]
	s_add_u32 s10, s10, 0x8000
	s_addc_u32 s11, s11, 0
	global_load_dwordx4 v[88:91], v126, s[10:11]
	s_add_u32 s10, s10, 0x8000
	s_addc_u32 s11, s11, 0
	global_load_dwordx4 v[92:95], v126, s[10:11]
	s_add_u32 s10, s10, 0x8000
	s_addc_u32 s11, s11, 0
	global_load_dwordx4 v[96:99], v126, s[10:11]
	s_add_i32 s17, s16, 96
	s_min_u32 s17, s17, 0x7ff
	s_lshr_b32 s18, s17, 5
	s_add_i32 s18, s18, 0
	s_and_b32 s19, s17, 31
	s_lshl_b32 s19, s19, 21
	s_lshl_b32 s18, s18, 7
	s_add_u32 s18, s18, s19
	s_add_u32 s14, s4, s18
	s_addc_u32 s15, s5, 0
	ds_read_b32 v100, v123
	ds_read_b32 v101, v123 offset:512
	ds_read_b32 v102, v123 offset:1024
	ds_read_b32 v103, v123 offset:1536
	ds_read_b32 v104, v123 offset:2048
	ds_read_b32 v105, v123 offset:2560
	ds_read_b32 v106, v123 offset:3072
	ds_read_b32 v107, v123 offset:3584
	ds_read_b32 v108, v123 offset:4096
	ds_read_b32 v109, v123 offset:4608
	ds_read_b32 v110, v123 offset:5120
	ds_read_b32 v111, v123 offset:5632
	ds_read_b32 v112, v123 offset:6144
	ds_read_b32 v113, v123 offset:6656
	ds_read_b32 v114, v123 offset:7168
	ds_read_b32 v115, v123 offset:7680
	s_waitcnt lgkmcnt(0)
	v_max_f32_e32 v100, v100, v100
	v_max_f32_e32 v101, v101, v101
	v_max_f32_e32 v102, v102, v102
	v_max_f32_e32 v103, v103, v103
	v_max_f32_e32 v104, v104, v104
	v_max_f32_e32 v105, v105, v105
	v_max_f32_e32 v106, v106, v106
	v_max_f32_e32 v107, v107, v107
	v_max_f32_e32 v108, v108, v108
	v_max_f32_e32 v109, v109, v109
	v_max_f32_e32 v110, v110, v110
	v_max_f32_e32 v111, v111, v111
	v_max_f32_e32 v112, v112, v112
	v_max_f32_e32 v113, v113, v113
	v_max_f32_e32 v114, v114, v114
	v_max_f32_e32 v115, v115, v115
	v_med3_f32 v100, v100, s20, v129
	v_med3_f32 v101, v101, s20, v129
	v_med3_f32 v102, v102, s20, v129
	v_med3_f32 v103, v103, s20, v129
	v_med3_f32 v104, v104, s20, v129
	v_med3_f32 v105, v105, s20, v129
	v_med3_f32 v106, v106, s20, v129
	v_med3_f32 v107, v107, s20, v129
	v_med3_f32 v108, v108, s20, v129
	v_med3_f32 v109, v109, s20, v129
	v_med3_f32 v110, v110, s20, v129
	v_med3_f32 v111, v111, s20, v129
	v_med3_f32 v112, v112, s20, v129
	v_med3_f32 v113, v113, s20, v129
	v_med3_f32 v114, v114, s20, v129
	v_med3_f32 v115, v115, s20, v129
	v_mov_b32_e32 v116, 0
	v_mov_b32_e32 v117, 0
	v_mov_b32_e32 v118, 0
	v_mov_b32_e32 v119, 0
	v_cvt_pk_fp8_f32 v116, v100, v101
	v_cvt_pk_fp8_f32 v117, v104, v105
	v_cvt_pk_fp8_f32 v118, v108, v109
	v_cvt_pk_fp8_f32 v119, v112, v113
	v_cvt_pk_fp8_f32 v116, v102, v103 op_sel:[0,0,1]
	v_cvt_pk_fp8_f32 v117, v106, v107 op_sel:[0,0,1]
	v_cvt_pk_fp8_f32 v118, v110, v111 op_sel:[0,0,1]
	v_cvt_pk_fp8_f32 v119, v114, v115 op_sel:[0,0,1]
	s_nop 0
	global_store_dwordx4 v127, v[116:119], s[14:15]
	ds_read_b32 v100, v125
	ds_read_b32 v101, v125 offset:512
	ds_read_b32 v102, v125 offset:1024
	ds_read_b32 v103, v125 offset:1536
	ds_read_b32 v104, v125 offset:2048
	ds_read_b32 v105, v125 offset:2560
	ds_read_b32 v106, v125 offset:3072
	ds_read_b32 v107, v125 offset:3584
	ds_read_b32 v108, v125 offset:4096
	ds_read_b32 v109, v125 offset:4608
	ds_read_b32 v110, v125 offset:5120
	ds_read_b32 v111, v125 offset:5632
	ds_read_b32 v112, v125 offset:6144
	ds_read_b32 v113, v125 offset:6656
	ds_read_b32 v114, v125 offset:7168
	ds_read_b32 v115, v125 offset:7680
	s_waitcnt lgkmcnt(0)
	v_max_f32_e32 v100, v100, v100
	v_max_f32_e32 v101, v101, v101
	v_max_f32_e32 v102, v102, v102
	v_max_f32_e32 v103, v103, v103
	v_max_f32_e32 v104, v104, v104
	v_max_f32_e32 v105, v105, v105
	v_max_f32_e32 v106, v106, v106
	v_max_f32_e32 v107, v107, v107
	v_max_f32_e32 v108, v108, v108
	v_max_f32_e32 v109, v109, v109
	v_max_f32_e32 v110, v110, v110
	v_max_f32_e32 v111, v111, v111
	v_max_f32_e32 v112, v112, v112
	v_max_f32_e32 v113, v113, v113
	v_max_f32_e32 v114, v114, v114
	v_max_f32_e32 v115, v115, v115
	v_med3_f32 v100, v100, s20, v129
	v_med3_f32 v101, v101, s20, v129
	v_med3_f32 v102, v102, s20, v129
	v_med3_f32 v103, v103, s20, v129
	v_med3_f32 v104, v104, s20, v129
	v_med3_f32 v105, v105, s20, v129
	v_med3_f32 v106, v106, s20, v129
	v_med3_f32 v107, v107, s20, v129
	v_med3_f32 v108, v108, s20, v129
	v_med3_f32 v109, v109, s20, v129
	v_med3_f32 v110, v110, s20, v129
	v_med3_f32 v111, v111, s20, v129
	v_med3_f32 v112, v112, s20, v129
	v_med3_f32 v113, v113, s20, v129
	v_med3_f32 v114, v114, s20, v129
	v_med3_f32 v115, v115, s20, v129
	v_mov_b32_e32 v116, 0
	v_mov_b32_e32 v117, 0
	v_mov_b32_e32 v118, 0
	v_mov_b32_e32 v119, 0
	v_cvt_pk_fp8_f32 v116, v100, v101
	v_cvt_pk_fp8_f32 v117, v104, v105
	v_cvt_pk_fp8_f32 v118, v108, v109
	v_cvt_pk_fp8_f32 v119, v112, v113
	v_cvt_pk_fp8_f32 v116, v102, v103 op_sel:[0,0,1]
	v_cvt_pk_fp8_f32 v117, v106, v107 op_sel:[0,0,1]
	v_cvt_pk_fp8_f32 v118, v110, v111 op_sel:[0,0,1]
	v_cvt_pk_fp8_f32 v119, v114, v115 op_sel:[0,0,1]
	s_nop 0
	global_store_dwordx4 v128, v[116:119], s[14:15]
	s_waitcnt vmcnt(12)
	v_mul_f32_e32 v36, 0x43000000, v36
	v_mul_f32_e32 v37, 0x43000000, v37
	v_mul_f32_e32 v38, 0x43000000, v38
	v_mul_f32_e32 v39, 0x43000000, v39
	ds_write_b128 v120, v[36:39]
	v_mul_f32_e32 v40, 0x43000000, v40
	v_mul_f32_e32 v41, 0x43000000, v41
	v_mul_f32_e32 v42, 0x43000000, v42
	v_mul_f32_e32 v43, 0x43000000, v43
	ds_write_b128 v120, v[40:43] offset:1024
	v_mul_f32_e32 v44, 0x43000000, v44
	v_mul_f32_e32 v45, 0x43000000, v45
	v_mul_f32_e32 v46, 0x43000000, v46
	v_mul_f32_e32 v47, 0x43000000, v47
	ds_write_b128 v120, v[44:47] offset:2048
	v_mul_f32_e32 v48, 0x43000000, v48
	v_mul_f32_e32 v49, 0x43000000, v49
	v_mul_f32_e32 v50, 0x43000000, v50
	v_mul_f32_e32 v51, 0x43000000, v51
	ds_write_b128 v120, v[48:51] offset:3072
	v_mul_f32_e32 v52, 0x43000000, v52
	v_mul_f32_e32 v53, 0x43000000, v53
	v_mul_f32_e32 v54, 0x43000000, v54
	v_mul_f32_e32 v55, 0x43000000, v55
	ds_write_b128 v120, v[52:55] offset:4096
	v_mul_f32_e32 v56, 0x43000000, v56
	v_mul_f32_e32 v57, 0x43000000, v57
	v_mul_f32_e32 v58, 0x43000000, v58
	v_mul_f32_e32 v59, 0x43000000, v59
	ds_write_b128 v120, v[56:59] offset:5120
	v_mul_f32_e32 v60, 0x43000000, v60
	v_mul_f32_e32 v61, 0x43000000, v61
	v_mul_f32_e32 v62, 0x43000000, v62
	v_mul_f32_e32 v63, 0x43000000, v63
	ds_write_b128 v120, v[60:63] offset:6144
	v_mul_f32_e32 v64, 0x43000000, v64
	v_mul_f32_e32 v65, 0x43000000, v65
	v_mul_f32_e32 v66, 0x43000000, v66
	v_mul_f32_e32 v67, 0x43000000, v67
	ds_write_b128 v120, v[64:67] offset:7168
	s_waitcnt lgkmcnt(0)
	s_barrier
; #define GAS __attribute__((address_space(1)))
; #define LAS __attribute__((address_space(3)))
; #define LDS_WAIT() asm volatile("s_waitcnt lgkmcnt(0)" ::: "memory")
;     const int pr = item >> 1, kb = 2 * (pr / nblk) + (item & 1), nb = pr % nblk, k0 = 64 * kb, n0 = 32 * nb;
;     const int nr = n0 + (lane & 31); const int sc = MAP == 1 ? src_col_in(nr) : nr;
;     float v[32];
; #pragma unroll
;     for (int i = 0; i < 32; ++i) v[i] = sc >= 0 ? W[(size_t)(k0 + 2 * i + (lane >> 5)) * Nsrc + sc] : 0.f;
; #pragma unroll
;     for (int i = 0; i < 32; ++i) { const int k = k0 + 2 * i + (lane >> 5); float x = v[i] * wscale; if (KS) x *= (k < ksplit ? ksA[k] : ksB[k - ksplit]); scr[(2 * i + (lane >> 5)) * 33 + (lane & 31)] = x; }
;     LDS_WAIT(); asm volatile("" ::: "memory");
;     const int c = lane & 7;
; #pragma unroll
;     for (int j = 0; j < 4; ++j) { const int n = (lane >> 3) + 8 * j; const LAS float* s = scr + (8 * c) * 33 + n;
;         const unsigned long long o = (unsigned long long)pg8::pk4_fp8(s[0 * 33], s[1 * 33], s[2 * 33], s[3 * 33]) | ((unsigned long long)pg8::pk4_fp8(s[4 * 33], s[5 * 33], s[6 * 33], s[7 * 33]) << 32);
;         *(GAS unsigned long long*)(WT + (size_t)(n0 + n) * K + k0 + 8 * c) = o; }
;     LDS_WAIT(); asm volatile("" ::: "memory");
; }
	s_add_i32 s17, s16, 384
	s_min_u32 s17, s17, 0x7ff
	s_lshr_b32 s18, s17, 5
	s_add_i32 s18, s18, 0
	s_and_b32 s19, s17, 31
	s_lshl_b32 s18, s18, 21
	s_lshl_b32 s19, s19, 9
	s_add_u32 s18, s18, s19
	s_add_u32 s10, s2, s18
	s_addc_u32 s11, s3, 0
	global_load_dwordx4 v[36:39], v126, s[10:11]
	s_add_u32 s10, s10, 0x8000
	s_addc_u32 s11, s11, 0
	global_load_dwordx4 v[40:43], v126, s[10:11]
	s_add_u32 s10, s10, 0x8000
	s_addc_u32 s11, s11, 0
	global_load_dwordx4 v[44:47], v126, s[10:11]
	s_add_u32 s10, s10, 0x8000
	s_addc_u32 s11, s11, 0
	global_load_dwordx4 v[48:51], v126, s[10:11]
	s_add_u32 s10, s10, 0x8000
	s_addc_u32 s11, s11, 0
	global_load_dwordx4 v[52:55], v126, s[10:11]
	s_add_u32 s10, s10, 0x8000
	s_addc_u32 s11, s11, 0
	global_load_dwordx4 v[56:59], v126, s[10:11]
	s_add_u32 s10, s10, 0x8000
	s_addc_u32 s11, s11, 0
	global_load_dwordx4 v[60:63], v126, s[10:11]
	s_add_u32 s10, s10, 0x8000
	s_addc_u32 s11, s11, 0
	global_load_dwordx4 v[64:67], v126, s[10:11]
	s_add_i32 s17, s16, 192
	s_min_u32 s17, s17, 0x7ff
	s_lshr_b32 s18, s17, 5
	s_add_i32 s18, s18, 0
	s_and_b32 s19, s17, 31
	s_lshl_b32 s19, s19, 21
	s_lshl_b32 s18, s18, 7
	s_add_u32 s18, s18, s19
	s_add_u32 s14, s4, s18
	s_addc_u32 s15, s5, 0
	ds_read_b32 v100, v122
	ds_read_b32 v101, v122 offset:512
	ds_read_b32 v102, v122 offset:1024
	ds_read_b32 v103, v122 offset:1536
	ds_read_b32 v104, v122 offset:2048
	ds_read_b32 v105, v122 offset:2560
	ds_read_b32 v106, v122 offset:3072
	ds_read_b32 v107, v122 offset:3584
	ds_read_b32 v108, v122 offset:4096
	ds_read_b32 v109, v122 offset:4608
	ds_read_b32 v110, v122 offset:5120
	ds_read_b32 v111, v122 offset:5632
	ds_read_b32 v112, v122 offset:6144
	ds_read_b32 v113, v122 offset:6656
	ds_read_b32 v114, v122 offset:7168
	ds_read_b32 v115, v122 offset:7680
	s_waitcnt lgkmcnt(0)
	v_max_f32_e32 v100, v100, v100
	v_max_f32_e32 v101, v101, v101
	v_max_f32_e32 v102, v102, v102
	v_max_f32_e32 v103, v103, v103
	v_max_f32_e32 v104, v104, v104
	v_max_f32_e32 v105, v105, v105
	v_max_f32_e32 v106, v106, v106
	v_max_f32_e32 v107, v107, v107
	v_max_f32_e32 v108, v108, v108
	v_max_f32_e32 v109, v109, v109
	v_max_f32_e32 v110, v110, v110
	v_max_f32_e32 v111, v111, v111
	v_max_f32_e32 v112, v112, v112
	v_max_f32_e32 v113, v113, v113
	v_max_f32_e32 v114, v114, v114
	v_max_f32_e32 v115, v115, v115
	v_med3_f32 v100, v100, s20, v129
	v_med3_f32 v101, v101, s20, v129
	v_med3_f32 v102, v102, s20, v129
	v_med3_f32 v103, v103, s20, v129
	v_med3_f32 v104, v104, s20, v129
	v_med3_f32 v105, v105, s20, v129
	v_med3_f32 v106, v106, s20, v129
	v_med3_f32 v107, v107, s20, v129
	v_med3_f32 v108, v108, s20, v129
	v_med3_f32 v109, v109, s20, v129
	v_med3_f32 v110, v110, s20, v129
	v_med3_f32 v111, v111, s20, v129
	v_med3_f32 v112, v112, s20, v129
	v_med3_f32 v113, v113, s20, v129
	v_med3_f32 v114, v114, s20, v129
	v_med3_f32 v115, v115, s20, v129
	v_mov_b32_e32 v116, 0
	v_mov_b32_e32 v117, 0
	v_mov_b32_e32 v118, 0
	v_mov_b32_e32 v119, 0
	v_cvt_pk_fp8_f32 v116, v100, v101
	v_cvt_pk_fp8_f32 v117, v104, v105
	v_cvt_pk_fp8_f32 v118, v108, v109
	v_cvt_pk_fp8_f32 v119, v112, v113
	v_cvt_pk_fp8_f32 v116, v102, v103 op_sel:[0,0,1]
	v_cvt_pk_fp8_f32 v117, v106, v107 op_sel:[0,0,1]
	v_cvt_pk_fp8_f32 v118, v110, v111 op_sel:[0,0,1]
	v_cvt_pk_fp8_f32 v119, v114, v115 op_sel:[0,0,1]
	s_nop 0
	global_store_dwordx4 v127, v[116:119], s[14:15]
	ds_read_b32 v100, v124
	ds_read_b32 v101, v124 offset:512
	ds_read_b32 v102, v124 offset:1024
	ds_read_b32 v103, v124 offset:1536
	ds_read_b32 v104, v124 offset:2048
	ds_read_b32 v105, v124 offset:2560
	ds_read_b32 v106, v124 offset:3072
	ds_read_b32 v107, v124 offset:3584
	ds_read_b32 v108, v124 offset:4096
	ds_read_b32 v109, v124 offset:4608
	ds_read_b32 v110, v124 offset:5120
	ds_read_b32 v111, v124 offset:5632
	ds_read_b32 v112, v124 offset:6144
	ds_read_b32 v113, v124 offset:6656
	ds_read_b32 v114, v124 offset:7168
	ds_read_b32 v115, v124 offset:7680
	s_waitcnt lgkmcnt(0)
	v_max_f32_e32 v100, v100, v100
	v_max_f32_e32 v101, v101, v101
	v_max_f32_e32 v102, v102, v102
	v_max_f32_e32 v103, v103, v103
	v_max_f32_e32 v104, v104, v104
	v_max_f32_e32 v105, v105, v105
	v_max_f32_e32 v106, v106, v106
	v_max_f32_e32 v107, v107, v107
	v_max_f32_e32 v108, v108, v108
	v_max_f32_e32 v109, v109, v109
	v_max_f32_e32 v110, v110, v110
	v_max_f32_e32 v111, v111, v111
	v_max_f32_e32 v112, v112, v112
	v_max_f32_e32 v113, v113, v113
	v_max_f32_e32 v114, v114, v114
	v_max_f32_e32 v115, v115, v115
	v_med3_f32 v100, v100, s20, v129
	v_med3_f32 v101, v101, s20, v129
	v_med3_f32 v102, v102, s20, v129
	v_med3_f32 v103, v103, s20, v129
	v_med3_f32 v104, v104, s20, v129
	v_med3_f32 v105, v105, s20, v129
	v_med3_f32 v106, v106, s20, v129
	v_med3_f32 v107, v107, s20, v129
	v_med3_f32 v108, v108, s20, v129
	v_med3_f32 v109, v109, s20, v129
	v_med3_f32 v110, v110, s20, v129
	v_med3_f32 v111, v111, s20, v129
	v_med3_f32 v112, v112, s20, v129
	v_med3_f32 v113, v113, s20, v129
	v_med3_f32 v114, v114, s20, v129
	v_med3_f32 v115, v115, s20, v129
	v_mov_b32_e32 v116, 0
	v_mov_b32_e32 v117, 0
	v_mov_b32_e32 v118, 0
	v_mov_b32_e32 v119, 0
	v_cvt_pk_fp8_f32 v116, v100, v101
	v_cvt_pk_fp8_f32 v117, v104, v105
	v_cvt_pk_fp8_f32 v118, v108, v109
	v_cvt_pk_fp8_f32 v119, v112, v113
	v_cvt_pk_fp8_f32 v116, v102, v103 op_sel:[0,0,1]
	v_cvt_pk_fp8_f32 v117, v106, v107 op_sel:[0,0,1]
	v_cvt_pk_fp8_f32 v118, v110, v111 op_sel:[0,0,1]
	v_cvt_pk_fp8_f32 v119, v114, v115 op_sel:[0,0,1]
	s_nop 0
	global_store_dwordx4 v128, v[116:119], s[14:15]
	s_waitcnt vmcnt(12)
	v_mul_f32_e32 v68, 0x43000000, v68
	v_mul_f32_e32 v69, 0x43000000, v69
	v_mul_f32_e32 v70, 0x43000000, v70
	v_mul_f32_e32 v71, 0x43000000, v71
	ds_write_b128 v121, v[68:71]
	v_mul_f32_e32 v72, 0x43000000, v72
	v_mul_f32_e32 v73, 0x43000000, v73
	v_mul_f32_e32 v74, 0x43000000, v74
	v_mul_f32_e32 v75, 0x43000000, v75
	ds_write_b128 v121, v[72:75] offset:1024
	v_mul_f32_e32 v76, 0x43000000, v76
	v_mul_f32_e32 v77, 0x43000000, v77
	v_mul_f32_e32 v78, 0x43000000, v78
	v_mul_f32_e32 v79, 0x43000000, v79
	ds_write_b128 v121, v[76:79] offset:2048
	v_mul_f32_e32 v80, 0x43000000, v80
	v_mul_f32_e32 v81, 0x43000000, v81
	v_mul_f32_e32 v82, 0x43000000, v82
	v_mul_f32_e32 v83, 0x43000000, v83
	ds_write_b128 v121, v[80:83] offset:3072
	v_mul_f32_e32 v84, 0x43000000, v84
	v_mul_f32_e32 v85, 0x43000000, v85
	v_mul_f32_e32 v86, 0x43000000, v86
	v_mul_f32_e32 v87, 0x43000000, v87
	ds_write_b128 v121, v[84:87] offset:4096
	v_mul_f32_e32 v88, 0x43000000, v88
	v_mul_f32_e32 v89, 0x43000000, v89
	v_mul_f32_e32 v90, 0x43000000, v90
	v_mul_f32_e32 v91, 0x43000000, v91
	ds_write_b128 v121, v[88:91] offset:5120
	v_mul_f32_e32 v92, 0x43000000, v92
	v_mul_f32_e32 v93, 0x43000000, v93
	v_mul_f32_e32 v94, 0x43000000, v94
	v_mul_f32_e32 v95, 0x43000000, v95
	ds_write_b128 v121, v[92:95] offset:6144
	v_mul_f32_e32 v96, 0x43000000, v96
	v_mul_f32_e32 v97, 0x43000000, v97
	v_mul_f32_e32 v98, 0x43000000, v98
	v_mul_f32_e32 v99, 0x43000000, v99
	ds_write_b128 v121, v[96:99] offset:7168
	s_waitcnt lgkmcnt(0)
	s_barrier
; #define GAS __attribute__((address_space(1)))
; #define LAS __attribute__((address_space(3)))
; #define LDS_WAIT() asm volatile("s_waitcnt lgkmcnt(0)" ::: "memory")
;     const int pr = item >> 1, kb = 2 * (pr / nblk) + (item & 1), nb = pr % nblk, k0 = 64 * kb, n0 = 32 * nb;
;     const int nr = n0 + (lane & 31); const int sc = MAP == 1 ? src_col_in(nr) : nr;
;     float v[32];
; #pragma unroll
;     for (int i = 0; i < 32; ++i) v[i] = sc >= 0 ? W[(size_t)(k0 + 2 * i + (lane >> 5)) * Nsrc + sc] : 0.f;
; #pragma unroll
;     for (int i = 0; i < 32; ++i) { const int k = k0 + 2 * i + (lane >> 5); float x = v[i] * wscale; if (KS) x *= (k < ksplit ? ksA[k] : ksB[k - ksplit]); scr[(2 * i + (lane >> 5)) * 33 + (lane & 31)] = x; }
;     LDS_WAIT(); asm volatile("" ::: "memory");
;     const int c = lane & 7;
; #pragma unroll
;     for (int j = 0; j < 4; ++j) { const int n = (lane >> 3) + 8 * j; const LAS float* s = scr + (8 * c) * 33 + n;
;         const unsigned long long o = (unsigned long long)pg8::pk4_fp8(s[0 * 33], s[1 * 33], s[2 * 33], s[3 * 33]) | ((unsigned long long)pg8::pk4_fp8(s[4 * 33], s[5 * 33], s[6 * 33], s[7 * 33]) << 32);
;         *(GAS unsigned long long*)(WT + (size_t)(n0 + n) * K + k0 + 8 * c) = o; }
;     LDS_WAIT(); asm volatile("" ::: "memory");
; }
	s_add_i32 s17, s16, 480
	s_min_u32 s17, s17, 0x7ff
	s_lshr_b32 s18, s17, 5
	s_add_i32 s18, s18, 0
	s_and_b32 s19, s17, 31
	s_lshl_b32 s18, s18, 21
	s_lshl_b32 s19, s19, 9
	s_add_u32 s18, s18, s19
	s_add_u32 s10, s2, s18
	s_addc_u32 s11, s3, 0
	global_load_dwordx4 v[68:71], v126, s[10:11]
	s_add_u32 s10, s10, 0x8000
	s_addc_u32 s11, s11, 0
	global_load_dwordx4 v[72:75], v126, s[10:11]
	s_add_u32 s10, s10, 0x8000
	s_addc_u32 s11, s11, 0
	global_load_dwordx4 v[76:79], v126, s[10:11]
	s_add_u32 s10, s10, 0x8000
	s_addc_u32 s11, s11, 0
	global_load_dwordx4 v[80:83], v126, s[10:11]
	s_add_u32 s10, s10, 0x8000
	s_addc_u32 s11, s11, 0
	global_load_dwordx4 v[84:87], v126, s[10:11]
	s_add_u32 s10, s10, 0x8000
	s_addc_u32 s11, s11, 0
	global_load_dwordx4 v[88:91], v126, s[10:11]
	s_add_u32 s10, s10, 0x8000
	s_addc_u32 s11, s11, 0
	global_load_dwordx4 v[92:95], v126, s[10:11]
	s_add_u32 s10, s10, 0x8000
	s_addc_u32 s11, s11, 0
	global_load_dwordx4 v[96:99], v126, s[10:11]
	s_add_i32 s17, s16, 288
	s_min_u32 s17, s17, 0x7ff
	s_lshr_b32 s18, s17, 5
	s_add_i32 s18, s18, 0
	s_and_b32 s19, s17, 31
	s_lshl_b32 s19, s19, 21
	s_lshl_b32 s18, s18, 7
	s_add_u32 s18, s18, s19
	s_add_u32 s14, s4, s18
	s_addc_u32 s15, s5, 0
	ds_read_b32 v100, v123
	ds_read_b32 v101, v123 offset:512
	ds_read_b32 v102, v123 offset:1024
	ds_read_b32 v103, v123 offset:1536
	ds_read_b32 v104, v123 offset:2048
	ds_read_b32 v105, v123 offset:2560
	ds_read_b32 v106, v123 offset:3072
	ds_read_b32 v107, v123 offset:3584
	ds_read_b32 v108, v123 offset:4096
	ds_read_b32 v109, v123 offset:4608
	ds_read_b32 v110, v123 offset:5120
	ds_read_b32 v111, v123 offset:5632
	ds_read_b32 v112, v123 offset:6144
	ds_read_b32 v113, v123 offset:6656
	ds_read_b32 v114, v123 offset:7168
	ds_read_b32 v115, v123 offset:7680
	s_waitcnt lgkmcnt(0)
	v_max_f32_e32 v100, v100, v100
	v_max_f32_e32 v101, v101, v101
	v_max_f32_e32 v102, v102, v102
	v_max_f32_e32 v103, v103, v103
	v_max_f32_e32 v104, v104, v104
	v_max_f32_e32 v105, v105, v105
	v_max_f32_e32 v106, v106, v106
	v_max_f32_e32 v107, v107, v107
	v_max_f32_e32 v108, v108, v108
	v_max_f32_e32 v109, v109, v109
	v_max_f32_e32 v110, v110, v110
	v_max_f32_e32 v111, v111, v111
	v_max_f32_e32 v112, v112, v112
	v_max_f32_e32 v113, v113, v113
	v_max_f32_e32 v114, v114, v114
	v_max_f32_e32 v115, v115, v115
	v_med3_f32 v100, v100, s20, v129
	v_med3_f32 v101, v101, s20, v129
	v_med3_f32 v102, v102, s20, v129
	v_med3_f32 v103, v103, s20, v129
	v_med3_f32 v104, v104, s20, v129
	v_med3_f32 v105, v105, s20, v129
	v_med3_f32 v106, v106, s20, v129
	v_med3_f32 v107, v107, s20, v129
	v_med3_f32 v108, v108, s20, v129
	v_med3_f32 v109, v109, s20, v129
	v_med3_f32 v110, v110, s20, v129
	v_med3_f32 v111, v111, s20, v129
	v_med3_f32 v112, v112, s20, v129
	v_med3_f32 v113, v113, s20, v129
	v_med3_f32 v114, v114, s20, v129
	v_med3_f32 v115, v115, s20, v129
	v_mov_b32_e32 v116, 0
	v_mov_b32_e32 v117, 0
	v_mov_b32_e32 v118, 0
	v_mov_b32_e32 v119, 0
	v_cvt_pk_fp8_f32 v116, v100, v101
	v_cvt_pk_fp8_f32 v117, v104, v105
	v_cvt_pk_fp8_f32 v118, v108, v109
	v_cvt_pk_fp8_f32 v119, v112, v113
	v_cvt_pk_fp8_f32 v116, v102, v103 op_sel:[0,0,1]
	v_cvt_pk_fp8_f32 v117, v106, v107 op_sel:[0,0,1]
	v_cvt_pk_fp8_f32 v118, v110, v111 op_sel:[0,0,1]
	v_cvt_pk_fp8_f32 v119, v114, v115 op_sel:[0,0,1]
	s_nop 0
	global_store_dwordx4 v127, v[116:119], s[14:15]
	ds_read_b32 v100, v125
	ds_read_b32 v101, v125 offset:512
	ds_read_b32 v102, v125 offset:1024
	ds_read_b32 v103, v125 offset:1536
	ds_read_b32 v104, v125 offset:2048
	ds_read_b32 v105, v125 offset:2560
	ds_read_b32 v106, v125 offset:3072
	ds_read_b32 v107, v125 offset:3584
	ds_read_b32 v108, v125 offset:4096
	ds_read_b32 v109, v125 offset:4608
	ds_read_b32 v110, v125 offset:5120
	ds_read_b32 v111, v125 offset:5632
	ds_read_b32 v112, v125 offset:6144
	ds_read_b32 v113, v125 offset:6656
	ds_read_b32 v114, v125 offset:7168
	ds_read_b32 v115, v125 offset:7680
	s_waitcnt lgkmcnt(0)
	v_max_f32_e32 v100, v100, v100
	v_max_f32_e32 v101, v101, v101
	v_max_f32_e32 v102, v102, v102
	v_max_f32_e32 v103, v103, v103
	v_max_f32_e32 v104, v104, v104
	v_max_f32_e32 v105, v105, v105
	v_max_f32_e32 v106, v106, v106
	v_max_f32_e32 v107, v107, v107
	v_max_f32_e32 v108, v108, v108
	v_max_f32_e32 v109, v109, v109
	v_max_f32_e32 v110, v110, v110
	v_max_f32_e32 v111, v111, v111
	v_max_f32_e32 v112, v112, v112
	v_max_f32_e32 v113, v113, v113
	v_max_f32_e32 v114, v114, v114
	v_max_f32_e32 v115, v115, v115
	v_med3_f32 v100, v100, s20, v129
	v_med3_f32 v101, v101, s20, v129
	v_med3_f32 v102, v102, s20, v129
	v_med3_f32 v103, v103, s20, v129
	v_med3_f32 v104, v104, s20, v129
	v_med3_f32 v105, v105, s20, v129
	v_med3_f32 v106, v106, s20, v129
	v_med3_f32 v107, v107, s20, v129
	v_med3_f32 v108, v108, s20, v129
	v_med3_f32 v109, v109, s20, v129
	v_med3_f32 v110, v110, s20, v129
	v_med3_f32 v111, v111, s20, v129
	v_med3_f32 v112, v112, s20, v129
	v_med3_f32 v113, v113, s20, v129
	v_med3_f32 v114, v114, s20, v129
	v_med3_f32 v115, v115, s20, v129
	v_mov_b32_e32 v116, 0
	v_mov_b32_e32 v117, 0
	v_mov_b32_e32 v118, 0
	v_mov_b32_e32 v119, 0
	v_cvt_pk_fp8_f32 v116, v100, v101
	v_cvt_pk_fp8_f32 v117, v104, v105
	v_cvt_pk_fp8_f32 v118, v108, v109
	v_cvt_pk_fp8_f32 v119, v112, v113
	v_cvt_pk_fp8_f32 v116, v102, v103 op_sel:[0,0,1]
	v_cvt_pk_fp8_f32 v117, v106, v107 op_sel:[0,0,1]
	v_cvt_pk_fp8_f32 v118, v110, v111 op_sel:[0,0,1]
	v_cvt_pk_fp8_f32 v119, v114, v115 op_sel:[0,0,1]
	s_nop 0
	global_store_dwordx4 v128, v[116:119], s[14:15]
	s_waitcnt vmcnt(12)
	v_mul_f32_e32 v36, 0x43000000, v36
	v_mul_f32_e32 v37, 0x43000000, v37
	v_mul_f32_e32 v38, 0x43000000, v38
	v_mul_f32_e32 v39, 0x43000000, v39
	ds_write_b128 v120, v[36:39]
	v_mul_f32_e32 v40, 0x43000000, v40
	v_mul_f32_e32 v41, 0x43000000, v41
	v_mul_f32_e32 v42, 0x43000000, v42
	v_mul_f32_e32 v43, 0x43000000, v43
	ds_write_b128 v120, v[40:43] offset:1024
	v_mul_f32_e32 v44, 0x43000000, v44
	v_mul_f32_e32 v45, 0x43000000, v45
	v_mul_f32_e32 v46, 0x43000000, v46
	v_mul_f32_e32 v47, 0x43000000, v47
	ds_write_b128 v120, v[44:47] offset:2048
	v_mul_f32_e32 v48, 0x43000000, v48
	v_mul_f32_e32 v49, 0x43000000, v49
	v_mul_f32_e32 v50, 0x43000000, v50
	v_mul_f32_e32 v51, 0x43000000, v51
	ds_write_b128 v120, v[48:51] offset:3072
	v_mul_f32_e32 v52, 0x43000000, v52
	v_mul_f32_e32 v53, 0x43000000, v53
	v_mul_f32_e32 v54, 0x43000000, v54
	v_mul_f32_e32 v55, 0x43000000, v55
	ds_write_b128 v120, v[52:55] offset:4096
	v_mul_f32_e32 v56, 0x43000000, v56
	v_mul_f32_e32 v57, 0x43000000, v57
	v_mul_f32_e32 v58, 0x43000000, v58
	v_mul_f32_e32 v59, 0x43000000, v59
	ds_write_b128 v120, v[56:59] offset:5120
	v_mul_f32_e32 v60, 0x43000000, v60
	v_mul_f32_e32 v61, 0x43000000, v61
	v_mul_f32_e32 v62, 0x43000000, v62
	v_mul_f32_e32 v63, 0x43000000, v63
	ds_write_b128 v120, v[60:63] offset:6144
	v_mul_f32_e32 v64, 0x43000000, v64
	v_mul_f32_e32 v65, 0x43000000, v65
	v_mul_f32_e32 v66, 0x43000000, v66
	v_mul_f32_e32 v67, 0x43000000, v67
	ds_write_b128 v120, v[64:67] offset:7168
	s_waitcnt lgkmcnt(0)
	s_barrier
; #define GAS __attribute__((address_space(1)))
; #define LAS __attribute__((address_space(3)))
; #define LDS_WAIT() asm volatile("s_waitcnt lgkmcnt(0)" ::: "memory")
;     const int pr = item >> 1, kb = 2 * (pr / nblk) + (item & 1), nb = pr % nblk, k0 = 64 * kb, n0 = 32 * nb;
;     const int nr = n0 + (lane & 31); const int sc = MAP == 1 ? src_col_in(nr) : nr;
;     float v[32];
; #pragma unroll
;     for (int i = 0; i < 32; ++i) v[i] = sc >= 0 ? W[(size_t)(k0 + 2 * i + (lane >> 5)) * Nsrc + sc] : 0.f;
; #pragma unroll
;     for (int i = 0; i < 32; ++i) { const int k = k0 + 2 * i + (lane >> 5); float x = v[i] * wscale; if (KS) x *= (k < ksplit ? ksA[k] : ksB[k - ksplit]); scr[(2 * i + (lane >> 5)) * 33 + (lane & 31)] = x; }
;     LDS_WAIT(); asm volatile("" ::: "memory");
;     const int c = lane & 7;
; #pragma unroll
;     for (int j = 0; j < 4; ++j) { const int n = (lane >> 3) + 8 * j; const LAS float* s = scr + (8 * c) * 33 + n;
;         const unsigned long long o = (unsigned long long)pg8::pk4_fp8(s[0 * 33], s[1 * 33], s[2 * 33], s[3 * 33]) | ((unsigned long long)pg8::pk4_fp8(s[4 * 33], s[5 * 33], s[6 * 33], s[7 * 33]) << 32);
;         *(GAS unsigned long long*)(WT + (size_t)(n0 + n) * K + k0 + 8 * c) = o; }
;     LDS_WAIT(); asm volatile("" ::: "memory");
; }
	s_add_i32 s17, s16, 576
	s_min_u32 s17, s17, 0x7ff
	s_lshr_b32 s18, s17, 5
	s_add_i32 s18, s18, 0
	s_and_b32 s19, s17, 31
	s_lshl_b32 s18, s18, 21
	s_lshl_b32 s19, s19, 9
	s_add_u32 s18, s18, s19
	s_add_u32 s10, s2, s18
	s_addc_u32 s11, s3, 0
	global_load_dwordx4 v[36:39], v126, s[10:11]
	s_add_u32 s10, s10, 0x8000
	s_addc_u32 s11, s11, 0
	global_load_dwordx4 v[40:43], v126, s[10:11]
	s_add_u32 s10, s10, 0x8000
	s_addc_u32 s11, s11, 0
	global_load_dwordx4 v[44:47], v126, s[10:11]
	s_add_u32 s10, s10, 0x8000
	s_addc_u32 s11, s11, 0
	global_load_dwordx4 v[48:51], v126, s[10:11]
	s_add_u32 s10, s10, 0x8000
	s_addc_u32 s11, s11, 0
	global_load_dwordx4 v[52:55], v126, s[10:11]
	s_add_u32 s10, s10, 0x8000
	s_addc_u32 s11, s11, 0
	global_load_dwordx4 v[56:59], v126, s[10:11]
	s_add_u32 s10, s10, 0x8000
	s_addc_u32 s11, s11, 0
	global_load_dwordx4 v[60:63], v126, s[10:11]
	s_add_u32 s10, s10, 0x8000
	s_addc_u32 s11, s11, 0
	global_load_dwordx4 v[64:67], v126, s[10:11]
	s_add_i32 s17, s16, 384
	s_min_u32 s17, s17, 0x7ff
	s_lshr_b32 s18, s17, 5
	s_add_i32 s18, s18, 0
	s_and_b32 s19, s17, 31
	s_lshl_b32 s19, s19, 21
	s_lshl_b32 s18, s18, 7
	s_add_u32 s18, s18, s19
	s_add_u32 s14, s4, s18
	s_addc_u32 s15, s5, 0
	ds_read_b32 v100, v122
	ds_read_b32 v101, v122 offset:512
	ds_read_b32 v102, v122 offset:1024
	ds_read_b32 v103, v122 offset:1536
	ds_read_b32 v104, v122 offset:2048
	ds_read_b32 v105, v122 offset:2560
	ds_read_b32 v106, v122 offset:3072
	ds_read_b32 v107, v122 offset:3584
	ds_read_b32 v108, v122 offset:4096
	ds_read_b32 v109, v122 offset:4608
	ds_read_b32 v110, v122 offset:5120
	ds_read_b32 v111, v122 offset:5632
	ds_read_b32 v112, v122 offset:6144
	ds_read_b32 v113, v122 offset:6656
	ds_read_b32 v114, v122 offset:7168
	ds_read_b32 v115, v122 offset:7680
	s_waitcnt lgkmcnt(0)
	v_max_f32_e32 v100, v100, v100
	v_max_f32_e32 v101, v101, v101
	v_max_f32_e32 v102, v102, v102
	v_max_f32_e32 v103, v103, v103
	v_max_f32_e32 v104, v104, v104
	v_max_f32_e32 v105, v105, v105
	v_max_f32_e32 v106, v106, v106
	v_max_f32_e32 v107, v107, v107
	v_max_f32_e32 v108, v108, v108
	v_max_f32_e32 v109, v109, v109
	v_max_f32_e32 v110, v110, v110
	v_max_f32_e32 v111, v111, v111
	v_max_f32_e32 v112, v112, v112
	v_max_f32_e32 v113, v113, v113
	v_max_f32_e32 v114, v114, v114
	v_max_f32_e32 v115, v115, v115
	v_med3_f32 v100, v100, s20, v129
	v_med3_f32 v101, v101, s20, v129
	v_med3_f32 v102, v102, s20, v129
	v_med3_f32 v103, v103, s20, v129
	v_med3_f32 v104, v104, s20, v129
	v_med3_f32 v105, v105, s20, v129
	v_med3_f32 v106, v106, s20, v129
	v_med3_f32 v107, v107, s20, v129
	v_med3_f32 v108, v108, s20, v129
	v_med3_f32 v109, v109, s20, v129
	v_med3_f32 v110, v110, s20, v129
	v_med3_f32 v111, v111, s20, v129
	v_med3_f32 v112, v112, s20, v129
	v_med3_f32 v113, v113, s20, v129
	v_med3_f32 v114, v114, s20, v129
	v_med3_f32 v115, v115, s20, v129
	v_mov_b32_e32 v116, 0
	v_mov_b32_e32 v117, 0
	v_mov_b32_e32 v118, 0
	v_mov_b32_e32 v119, 0
	v_cvt_pk_fp8_f32 v116, v100, v101
	v_cvt_pk_fp8_f32 v117, v104, v105
	v_cvt_pk_fp8_f32 v118, v108, v109
	v_cvt_pk_fp8_f32 v119, v112, v113
	v_cvt_pk_fp8_f32 v116, v102, v103 op_sel:[0,0,1]
	v_cvt_pk_fp8_f32 v117, v106, v107 op_sel:[0,0,1]
	v_cvt_pk_fp8_f32 v118, v110, v111 op_sel:[0,0,1]
	v_cvt_pk_fp8_f32 v119, v114, v115 op_sel:[0,0,1]
	s_nop 0
	global_store_dwordx4 v127, v[116:119], s[14:15]
	ds_read_b32 v100, v124
	ds_read_b32 v101, v124 offset:512
	ds_read_b32 v102, v124 offset:1024
	ds_read_b32 v103, v124 offset:1536
	ds_read_b32 v104, v124 offset:2048
	ds_read_b32 v105, v124 offset:2560
	ds_read_b32 v106, v124 offset:3072
	ds_read_b32 v107, v124 offset:3584
	ds_read_b32 v108, v124 offset:4096
	ds_read_b32 v109, v124 offset:4608
	ds_read_b32 v110, v124 offset:5120
	ds_read_b32 v111, v124 offset:5632
	ds_read_b32 v112, v124 offset:6144
	ds_read_b32 v113, v124 offset:6656
	ds_read_b32 v114, v124 offset:7168
	ds_read_b32 v115, v124 offset:7680
	s_waitcnt lgkmcnt(0)
	v_max_f32_e32 v100, v100, v100
	v_max_f32_e32 v101, v101, v101
	v_max_f32_e32 v102, v102, v102
	v_max_f32_e32 v103, v103, v103
	v_max_f32_e32 v104, v104, v104
	v_max_f32_e32 v105, v105, v105
	v_max_f32_e32 v106, v106, v106
	v_max_f32_e32 v107, v107, v107
	v_max_f32_e32 v108, v108, v108
	v_max_f32_e32 v109, v109, v109
	v_max_f32_e32 v110, v110, v110
	v_max_f32_e32 v111, v111, v111
	v_max_f32_e32 v112, v112, v112
	v_max_f32_e32 v113, v113, v113
	v_max_f32_e32 v114, v114, v114
	v_max_f32_e32 v115, v115, v115
	v_med3_f32 v100, v100, s20, v129
	v_med3_f32 v101, v101, s20, v129
	v_med3_f32 v102, v102, s20, v129
	v_med3_f32 v103, v103, s20, v129
	v_med3_f32 v104, v104, s20, v129
	v_med3_f32 v105, v105, s20, v129
	v_med3_f32 v106, v106, s20, v129
	v_med3_f32 v107, v107, s20, v129
	v_med3_f32 v108, v108, s20, v129
	v_med3_f32 v109, v109, s20, v129
	v_med3_f32 v110, v110, s20, v129
	v_med3_f32 v111, v111, s20, v129
	v_med3_f32 v112, v112, s20, v129
	v_med3_f32 v113, v113, s20, v129
	v_med3_f32 v114, v114, s20, v129
	v_med3_f32 v115, v115, s20, v129
	v_mov_b32_e32 v116, 0
	v_mov_b32_e32 v117, 0
	v_mov_b32_e32 v118, 0
	v_mov_b32_e32 v119, 0
	v_cvt_pk_fp8_f32 v116, v100, v101
	v_cvt_pk_fp8_f32 v117, v104, v105
	v_cvt_pk_fp8_f32 v118, v108, v109
	v_cvt_pk_fp8_f32 v119, v112, v113
	v_cvt_pk_fp8_f32 v116, v102, v103 op_sel:[0,0,1]
	v_cvt_pk_fp8_f32 v117, v106, v107 op_sel:[0,0,1]
	v_cvt_pk_fp8_f32 v118, v110, v111 op_sel:[0,0,1]
	v_cvt_pk_fp8_f32 v119, v114, v115 op_sel:[0,0,1]
	s_nop 0
	global_store_dwordx4 v128, v[116:119], s[14:15]
	s_waitcnt vmcnt(12)
	v_mul_f32_e32 v68, 0x43000000, v68
	v_mul_f32_e32 v69, 0x43000000, v69
	v_mul_f32_e32 v70, 0x43000000, v70
	v_mul_f32_e32 v71, 0x43000000, v71
	ds_write_b128 v121, v[68:71]
	v_mul_f32_e32 v72, 0x43000000, v72
	v_mul_f32_e32 v73, 0x43000000, v73
	v_mul_f32_e32 v74, 0x43000000, v74
	v_mul_f32_e32 v75, 0x43000000, v75
	ds_write_b128 v121, v[72:75] offset:1024
	v_mul_f32_e32 v76, 0x43000000, v76
	v_mul_f32_e32 v77, 0x43000000, v77
	v_mul_f32_e32 v78, 0x43000000, v78
	v_mul_f32_e32 v79, 0x43000000, v79
	ds_write_b128 v121, v[76:79] offset:2048
	v_mul_f32_e32 v80, 0x43000000, v80
	v_mul_f32_e32 v81, 0x43000000, v81
	v_mul_f32_e32 v82, 0x43000000, v82
	v_mul_f32_e32 v83, 0x43000000, v83
	ds_write_b128 v121, v[80:83] offset:3072
	v_mul_f32_e32 v84, 0x43000000, v84
	v_mul_f32_e32 v85, 0x43000000, v85
	v_mul_f32_e32 v86, 0x43000000, v86
	v_mul_f32_e32 v87, 0x43000000, v87
	ds_write_b128 v121, v[84:87] offset:4096
	v_mul_f32_e32 v88, 0x43000000, v88
	v_mul_f32_e32 v89, 0x43000000, v89
	v_mul_f32_e32 v90, 0x43000000, v90
	v_mul_f32_e32 v91, 0x43000000, v91
	ds_write_b128 v121, v[88:91] offset:5120
	v_mul_f32_e32 v92, 0x43000000, v92
	v_mul_f32_e32 v93, 0x43000000, v93
	v_mul_f32_e32 v94, 0x43000000, v94
	v_mul_f32_e32 v95, 0x43000000, v95
	ds_write_b128 v121, v[92:95] offset:6144
	v_mul_f32_e32 v96, 0x43000000, v96
	v_mul_f32_e32 v97, 0x43000000, v97
	v_mul_f32_e32 v98, 0x43000000, v98
	v_mul_f32_e32 v99, 0x43000000, v99
	ds_write_b128 v121, v[96:99] offset:7168
	s_waitcnt lgkmcnt(0)
	s_barrier
; #define GAS __attribute__((address_space(1)))
; #define LAS __attribute__((address_space(3)))
; #define LDS_WAIT() asm volatile("s_waitcnt lgkmcnt(0)" ::: "memory")
;     const int pr = item >> 1, kb = 2 * (pr / nblk) + (item & 1), nb = pr % nblk, k0 = 64 * kb, n0 = 32 * nb;
;     const int nr = n0 + (lane & 31); const int sc = MAP == 1 ? src_col_in(nr) : nr;
;     float v[32];
; #pragma unroll
;     for (int i = 0; i < 32; ++i) v[i] = sc >= 0 ? W[(size_t)(k0 + 2 * i + (lane >> 5)) * Nsrc + sc] : 0.f;
; #pragma unroll
;     for (int i = 0; i < 32; ++i) { const int k = k0 + 2 * i + (lane >> 5); float x = v[i] * wscale; if (KS) x *= (k < ksplit ? ksA[k] : ksB[k - ksplit]); scr[(2 * i + (lane >> 5)) * 33 + (lane & 31)] = x; }
;     LDS_WAIT(); asm volatile("" ::: "memory");
;     const int c = lane & 7;
; #pragma unroll
;     for (int j = 0; j < 4; ++j) { const int n = (lane >> 3) + 8 * j; const LAS float* s = scr + (8 * c) * 33 + n;
;         const unsigned long long o = (unsigned long long)pg8::pk4_fp8(s[0 * 33], s[1 * 33], s[2 * 33], s[3 * 33]) | ((unsigned long long)pg8::pk4_fp8(s[4 * 33], s[5 * 33], s[6 * 33], s[7 * 33]) << 32);
;         *(GAS unsigned long long*)(WT + (size_t)(n0 + n) * K + k0 + 8 * c) = o; }
;     LDS_WAIT(); asm volatile("" ::: "memory");
; }
	s_add_i32 s17, s16, 672
	s_min_u32 s17, s17, 0x7ff
	s_lshr_b32 s18, s17, 5
	s_add_i32 s18, s18, 0
	s_and_b32 s19, s17, 31
	s_lshl_b32 s18, s18, 21
	s_lshl_b32 s19, s19, 9
	s_add_u32 s18, s18, s19
	s_add_u32 s10, s2, s18
	s_addc_u32 s11, s3, 0
	global_load_dwordx4 v[68:71], v126, s[10:11]
	s_add_u32 s10, s10, 0x8000
	s_addc_u32 s11, s11, 0
	global_load_dwordx4 v[72:75], v126, s[10:11]
	s_add_u32 s10, s10, 0x8000
	s_addc_u32 s11, s11, 0
	global_load_dwordx4 v[76:79], v126, s[10:11]
	s_add_u32 s10, s10, 0x8000
	s_addc_u32 s11, s11, 0
	global_load_dwordx4 v[80:83], v126, s[10:11]
	s_add_u32 s10, s10, 0x8000
	s_addc_u32 s11, s11, 0
	global_load_dwordx4 v[84:87], v126, s[10:11]
	s_add_u32 s10, s10, 0x8000
	s_addc_u32 s11, s11, 0
	global_load_dwordx4 v[88:91], v126, s[10:11]
	s_add_u32 s10, s10, 0x8000
	s_addc_u32 s11, s11, 0
	global_load_dwordx4 v[92:95], v126, s[10:11]
	s_add_u32 s10, s10, 0x8000
	s_addc_u32 s11, s11, 0
	global_load_dwordx4 v[96:99], v126, s[10:11]
	s_add_i32 s17, s16, 480
	s_min_u32 s17, s17, 0x7ff
	s_lshr_b32 s18, s17, 5
	s_add_i32 s18, s18, 0
	s_and_b32 s19, s17, 31
	s_lshl_b32 s19, s19, 21
	s_lshl_b32 s18, s18, 7
	s_add_u32 s18, s18, s19
	s_add_u32 s14, s4, s18
	s_addc_u32 s15, s5, 0
	ds_read_b32 v100, v123
	ds_read_b32 v101, v123 offset:512
	ds_read_b32 v102, v123 offset:1024
	ds_read_b32 v103, v123 offset:1536
	ds_read_b32 v104, v123 offset:2048
	ds_read_b32 v105, v123 offset:2560
	ds_read_b32 v106, v123 offset:3072
	ds_read_b32 v107, v123 offset:3584
	ds_read_b32 v108, v123 offset:4096
	ds_read_b32 v109, v123 offset:4608
	ds_read_b32 v110, v123 offset:5120
	ds_read_b32 v111, v123 offset:5632
	ds_read_b32 v112, v123 offset:6144
	ds_read_b32 v113, v123 offset:6656
	ds_read_b32 v114, v123 offset:7168
	ds_read_b32 v115, v123 offset:7680
	s_waitcnt lgkmcnt(0)
	v_max_f32_e32 v100, v100, v100
	v_max_f32_e32 v101, v101, v101
	v_max_f32_e32 v102, v102, v102
	v_max_f32_e32 v103, v103, v103
	v_max_f32_e32 v104, v104, v104
	v_max_f32_e32 v105, v105, v105
	v_max_f32_e32 v106, v106, v106
	v_max_f32_e32 v107, v107, v107
	v_max_f32_e32 v108, v108, v108
	v_max_f32_e32 v109, v109, v109
	v_max_f32_e32 v110, v110, v110
	v_max_f32_e32 v111, v111, v111
	v_max_f32_e32 v112, v112, v112
	v_max_f32_e32 v113, v113, v113
	v_max_f32_e32 v114, v114, v114
	v_max_f32_e32 v115, v115, v115
	v_med3_f32 v100, v100, s20, v129
	v_med3_f32 v101, v101, s20, v129
	v_med3_f32 v102, v102, s20, v129
	v_med3_f32 v103, v103, s20, v129
	v_med3_f32 v104, v104, s20, v129
	v_med3_f32 v105, v105, s20, v129
	v_med3_f32 v106, v106, s20, v129
	v_med3_f32 v107, v107, s20, v129
	v_med3_f32 v108, v108, s20, v129
	v_med3_f32 v109, v109, s20, v129
	v_med3_f32 v110, v110, s20, v129
	v_med3_f32 v111, v111, s20, v129
	v_med3_f32 v112, v112, s20, v129
	v_med3_f32 v113, v113, s20, v129
	v_med3_f32 v114, v114, s20, v129
	v_med3_f32 v115, v115, s20, v129
	v_mov_b32_e32 v116, 0
	v_mov_b32_e32 v117, 0
	v_mov_b32_e32 v118, 0
	v_mov_b32_e32 v119, 0
	v_cvt_pk_fp8_f32 v116, v100, v101
	v_cvt_pk_fp8_f32 v117, v104, v105
	v_cvt_pk_fp8_f32 v118, v108, v109
	v_cvt_pk_fp8_f32 v119, v112, v113
	v_cvt_pk_fp8_f32 v116, v102, v103 op_sel:[0,0,1]
	v_cvt_pk_fp8_f32 v117, v106, v107 op_sel:[0,0,1]
	v_cvt_pk_fp8_f32 v118, v110, v111 op_sel:[0,0,1]
	v_cvt_pk_fp8_f32 v119, v114, v115 op_sel:[0,0,1]
	s_nop 0
	global_store_dwordx4 v127, v[116:119], s[14:15]
	ds_read_b32 v100, v125
	ds_read_b32 v101, v125 offset:512
	ds_read_b32 v102, v125 offset:1024
	ds_read_b32 v103, v125 offset:1536
	ds_read_b32 v104, v125 offset:2048
	ds_read_b32 v105, v125 offset:2560
	ds_read_b32 v106, v125 offset:3072
	ds_read_b32 v107, v125 offset:3584
	ds_read_b32 v108, v125 offset:4096
	ds_read_b32 v109, v125 offset:4608
	ds_read_b32 v110, v125 offset:5120
	ds_read_b32 v111, v125 offset:5632
	ds_read_b32 v112, v125 offset:6144
	ds_read_b32 v113, v125 offset:6656
	ds_read_b32 v114, v125 offset:7168
	ds_read_b32 v115, v125 offset:7680
	s_waitcnt lgkmcnt(0)
	v_max_f32_e32 v100, v100, v100
	v_max_f32_e32 v101, v101, v101
	v_max_f32_e32 v102, v102, v102
	v_max_f32_e32 v103, v103, v103
	v_max_f32_e32 v104, v104, v104
	v_max_f32_e32 v105, v105, v105
	v_max_f32_e32 v106, v106, v106
	v_max_f32_e32 v107, v107, v107
	v_max_f32_e32 v108, v108, v108
	v_max_f32_e32 v109, v109, v109
	v_max_f32_e32 v110, v110, v110
	v_max_f32_e32 v111, v111, v111
	v_max_f32_e32 v112, v112, v112
	v_max_f32_e32 v113, v113, v113
	v_max_f32_e32 v114, v114, v114
	v_max_f32_e32 v115, v115, v115
	v_med3_f32 v100, v100, s20, v129
	v_med3_f32 v101, v101, s20, v129
	v_med3_f32 v102, v102, s20, v129
	v_med3_f32 v103, v103, s20, v129
	v_med3_f32 v104, v104, s20, v129
	v_med3_f32 v105, v105, s20, v129
	v_med3_f32 v106, v106, s20, v129
	v_med3_f32 v107, v107, s20, v129
	v_med3_f32 v108, v108, s20, v129
	v_med3_f32 v109, v109, s20, v129
	v_med3_f32 v110, v110, s20, v129
	v_med3_f32 v111, v111, s20, v129
	v_med3_f32 v112, v112, s20, v129
	v_med3_f32 v113, v113, s20, v129
	v_med3_f32 v114, v114, s20, v129
	v_med3_f32 v115, v115, s20, v129
	v_mov_b32_e32 v116, 0
	v_mov_b32_e32 v117, 0
	v_mov_b32_e32 v118, 0
	v_mov_b32_e32 v119, 0
	v_cvt_pk_fp8_f32 v116, v100, v101
	v_cvt_pk_fp8_f32 v117, v104, v105
	v_cvt_pk_fp8_f32 v118, v108, v109
	v_cvt_pk_fp8_f32 v119, v112, v113
	v_cvt_pk_fp8_f32 v116, v102, v103 op_sel:[0,0,1]
	v_cvt_pk_fp8_f32 v117, v106, v107 op_sel:[0,0,1]
	v_cvt_pk_fp8_f32 v118, v110, v111 op_sel:[0,0,1]
	v_cvt_pk_fp8_f32 v119, v114, v115 op_sel:[0,0,1]
	s_nop 0
	global_store_dwordx4 v128, v[116:119], s[14:15]
	s_waitcnt vmcnt(12)
	v_mul_f32_e32 v36, 0x43000000, v36
	v_mul_f32_e32 v37, 0x43000000, v37
	v_mul_f32_e32 v38, 0x43000000, v38
	v_mul_f32_e32 v39, 0x43000000, v39
	ds_write_b128 v120, v[36:39]
	v_mul_f32_e32 v40, 0x43000000, v40
	v_mul_f32_e32 v41, 0x43000000, v41
	v_mul_f32_e32 v42, 0x43000000, v42
	v_mul_f32_e32 v43, 0x43000000, v43
	ds_write_b128 v120, v[40:43] offset:1024
	v_mul_f32_e32 v44, 0x43000000, v44
	v_mul_f32_e32 v45, 0x43000000, v45
	v_mul_f32_e32 v46, 0x43000000, v46
	v_mul_f32_e32 v47, 0x43000000, v47
	ds_write_b128 v120, v[44:47] offset:2048
	v_mul_f32_e32 v48, 0x43000000, v48
	v_mul_f32_e32 v49, 0x43000000, v49
	v_mul_f32_e32 v50, 0x43000000, v50
	v_mul_f32_e32 v51, 0x43000000, v51
	ds_write_b128 v120, v[48:51] offset:3072
	v_mul_f32_e32 v52, 0x43000000, v52
	v_mul_f32_e32 v53, 0x43000000, v53
	v_mul_f32_e32 v54, 0x43000000, v54
	v_mul_f32_e32 v55, 0x43000000, v55
	ds_write_b128 v120, v[52:55] offset:4096
	v_mul_f32_e32 v56, 0x43000000, v56
	v_mul_f32_e32 v57, 0x43000000, v57
	v_mul_f32_e32 v58, 0x43000000, v58
	v_mul_f32_e32 v59, 0x43000000, v59
	ds_write_b128 v120, v[56:59] offset:5120
	v_mul_f32_e32 v60, 0x43000000, v60
	v_mul_f32_e32 v61, 0x43000000, v61
	v_mul_f32_e32 v62, 0x43000000, v62
	v_mul_f32_e32 v63, 0x43000000, v63
	ds_write_b128 v120, v[60:63] offset:6144
	v_mul_f32_e32 v64, 0x43000000, v64
	v_mul_f32_e32 v65, 0x43000000, v65
	v_mul_f32_e32 v66, 0x43000000, v66
	v_mul_f32_e32 v67, 0x43000000, v67
	ds_write_b128 v120, v[64:67] offset:7168
	s_waitcnt lgkmcnt(0)
	s_barrier
; #define GAS __attribute__((address_space(1)))
; #define LAS __attribute__((address_space(3)))
; #define LDS_WAIT() asm volatile("s_waitcnt lgkmcnt(0)" ::: "memory")
;     const int pr = item >> 1, kb = 2 * (pr / nblk) + (item & 1), nb = pr % nblk, k0 = 64 * kb, n0 = 32 * nb;
;     const int nr = n0 + (lane & 31); const int sc = MAP == 1 ? src_col_in(nr) : nr;
;     float v[32];
; #pragma unroll
;     for (int i = 0; i < 32; ++i) v[i] = sc >= 0 ? W[(size_t)(k0 + 2 * i + (lane >> 5)) * Nsrc + sc] : 0.f;
; #pragma unroll
;     for (int i = 0; i < 32; ++i) { const int k = k0 + 2 * i + (lane >> 5); float x = v[i] * wscale; if (KS) x *= (k < ksplit ? ksA[k] : ksB[k - ksplit]); scr[(2 * i + (lane >> 5)) * 33 + (lane & 31)] = x; }
;     LDS_WAIT(); asm volatile("" ::: "memory");
;     const int c = lane & 7;
; #pragma unroll
;     for (int j = 0; j < 4; ++j) { const int n = (lane >> 3) + 8 * j; const LAS float* s = scr + (8 * c) * 33 + n;
;         const unsigned long long o = (unsigned long long)pg8::pk4_fp8(s[0 * 33], s[1 * 33], s[2 * 33], s[3 * 33]) | ((unsigned long long)pg8::pk4_fp8(s[4 * 33], s[5 * 33], s[6 * 33], s[7 * 33]) << 32);
;         *(GAS unsigned long long*)(WT + (size_t)(n0 + n) * K + k0 + 8 * c) = o; }
;     LDS_WAIT(); asm volatile("" ::: "memory");
	s_add_i32 s17, s16, 768
	s_min_u32 s17, s17, 0x7ff
	s_lshr_b32 s18, s17, 5
	s_add_i32 s18, s18, 0
	s_and_b32 s19, s17, 31
	s_lshl_b32 s18, s18, 21
	s_lshl_b32 s19, s19, 9
	s_add_u32 s18, s18, s19
	s_add_u32 s10, s2, s18
	s_addc_u32 s11, s3, 0
	global_load_dwordx4 v[36:39], v126, s[10:11]
	s_add_u32 s10, s10, 0x8000
	s_addc_u32 s11, s11, 0
	global_load_dwordx4 v[40:43], v126, s[10:11]
	s_add_u32 s10, s10, 0x8000
	s_addc_u32 s11, s11, 0
	global_load_dwordx4 v[44:47], v126, s[10:11]
	s_add_u32 s10, s10, 0x8000
	s_addc_u32 s11, s11, 0
	global_load_dwordx4 v[48:51], v126, s[10:11]
	s_add_u32 s10, s10, 0x8000
	s_addc_u32 s11, s11, 0
	global_load_dwordx4 v[52:55], v126, s[10:11]
	s_add_u32 s10, s10, 0x8000
	s_addc_u32 s11, s11, 0
	global_load_dwordx4 v[56:59], v126, s[10:11]
	s_add_u32 s10, s10, 0x8000
	s_addc_u32 s11, s11, 0
	global_load_dwordx4 v[60:63], v126, s[10:11]
	s_add_u32 s10, s10, 0x8000
	s_addc_u32 s11, s11, 0
	global_load_dwordx4 v[64:67], v126, s[10:11]
	s_add_i32 s17, s16, 576
	s_min_u32 s17, s17, 0x7ff
	s_lshr_b32 s18, s17, 5
	s_add_i32 s18, s18, 0
	s_and_b32 s19, s17, 31
	s_lshl_b32 s19, s19, 21
	s_lshl_b32 s18, s18, 7
	s_add_u32 s18, s18, s19
	s_add_u32 s14, s4, s18
	s_addc_u32 s15, s5, 0
	ds_read_b32 v100, v122
	ds_read_b32 v101, v122 offset:512
	ds_read_b32 v102, v122 offset:1024
	ds_read_b32 v103, v122 offset:1536
	ds_read_b32 v104, v122 offset:2048
	ds_read_b32 v105, v122 offset:2560
	ds_read_b32 v106, v122 offset:3072
	ds_read_b32 v107, v122 offset:3584
	ds_read_b32 v108, v122 offset:4096
	ds_read_b32 v109, v122 offset:4608
	ds_read_b32 v110, v122 offset:5120
	ds_read_b32 v111, v122 offset:5632
	ds_read_b32 v112, v122 offset:6144
	ds_read_b32 v113, v122 offset:6656
	ds_read_b32 v114, v122 offset:7168
	ds_read_b32 v115, v122 offset:7680
	s_waitcnt lgkmcnt(0)
	v_max_f32_e32 v100, v100, v100
	v_max_f32_e32 v101, v101, v101
	v_max_f32_e32 v102, v102, v102
	v_max_f32_e32 v103, v103, v103
	v_max_f32_e32 v104, v104, v104
	v_max_f32_e32 v105, v105, v105
	v_max_f32_e32 v106, v106, v106
	v_max_f32_e32 v107, v107, v107
	v_max_f32_e32 v108, v108, v108
	v_max_f32_e32 v109, v109, v109
	v_max_f32_e32 v110, v110, v110
	v_max_f32_e32 v111, v111, v111
	v_max_f32_e32 v112, v112, v112
	v_max_f32_e32 v113, v113, v113
	v_max_f32_e32 v114, v114, v114
	v_max_f32_e32 v115, v115, v115
	v_med3_f32 v100, v100, s20, v129
	v_med3_f32 v101, v101, s20, v129
	v_med3_f32 v102, v102, s20, v129
	v_med3_f32 v103, v103, s20, v129
	v_med3_f32 v104, v104, s20, v129
	v_med3_f32 v105, v105, s20, v129
	v_med3_f32 v106, v106, s20, v129
	v_med3_f32 v107, v107, s20, v129
	v_med3_f32 v108, v108, s20, v129
	v_med3_f32 v109, v109, s20, v129
	v_med3_f32 v110, v110, s20, v129
	v_med3_f32 v111, v111, s20, v129
	v_med3_f32 v112, v112, s20, v129
	v_med3_f32 v113, v113, s20, v129
	v_med3_f32 v114, v114, s20, v129
	v_med3_f32 v115, v115, s20, v129
	v_mov_b32_e32 v116, 0
	v_mov_b32_e32 v117, 0
	v_mov_b32_e32 v118, 0
	v_mov_b32_e32 v119, 0
	v_cvt_pk_fp8_f32 v116, v100, v101
	v_cvt_pk_fp8_f32 v117, v104, v105
	v_cvt_pk_fp8_f32 v118, v108, v109
	v_cvt_pk_fp8_f32 v119, v112, v113
	v_cvt_pk_fp8_f32 v116, v102, v103 op_sel:[0,0,1]
	v_cvt_pk_fp8_f32 v117, v106, v107 op_sel:[0,0,1]
	v_cvt_pk_fp8_f32 v118, v110, v111 op_sel:[0,0,1]
	v_cvt_pk_fp8_f32 v119, v114, v115 op_sel:[0,0,1]
	s_nop 0
	global_store_dwordx4 v127, v[116:119], s[14:15]
	ds_read_b32 v100, v124
	ds_read_b32 v101, v124 offset:512
	ds_read_b32 v102, v124 offset:1024
	ds_read_b32 v103, v124 offset:1536
	ds_read_b32 v104, v124 offset:2048
	ds_read_b32 v105, v124 offset:2560
	ds_read_b32 v106, v124 offset:3072
	ds_read_b32 v107, v124 offset:3584
	ds_read_b32 v108, v124 offset:4096
	ds_read_b32 v109, v124 offset:4608
	ds_read_b32 v110, v124 offset:5120
	ds_read_b32 v111, v124 offset:5632
	ds_read_b32 v112, v124 offset:6144
	ds_read_b32 v113, v124 offset:6656
	ds_read_b32 v114, v124 offset:7168
	ds_read_b32 v115, v124 offset:7680
	s_waitcnt lgkmcnt(0)
	v_max_f32_e32 v100, v100, v100
	v_max_f32_e32 v101, v101, v101
	v_max_f32_e32 v102, v102, v102
	v_max_f32_e32 v103, v103, v103
	v_max_f32_e32 v104, v104, v104
	v_max_f32_e32 v105, v105, v105
	v_max_f32_e32 v106, v106, v106
	v_max_f32_e32 v107, v107, v107
	v_max_f32_e32 v108, v108, v108
	v_max_f32_e32 v109, v109, v109
	v_max_f32_e32 v110, v110, v110
	v_max_f32_e32 v111, v111, v111
	v_max_f32_e32 v112, v112, v112
	v_max_f32_e32 v113, v113, v113
	v_max_f32_e32 v114, v114, v114
	v_max_f32_e32 v115, v115, v115
	v_med3_f32 v100, v100, s20, v129
	v_med3_f32 v101, v101, s20, v129
	v_med3_f32 v102, v102, s20, v129
	v_med3_f32 v103, v103, s20, v129
	v_med3_f32 v104, v104, s20, v129
	v_med3_f32 v105, v105, s20, v129
	v_med3_f32 v106, v106, s20, v129
	v_med3_f32 v107, v107, s20, v129
	v_med3_f32 v108, v108, s20, v129
	v_med3_f32 v109, v109, s20, v129
	v_med3_f32 v110, v110, s20, v129
	v_med3_f32 v111, v111, s20, v129
	v_med3_f32 v112, v112, s20, v129
	v_med3_f32 v113, v113, s20, v129
	v_med3_f32 v114, v114, s20, v129
	v_med3_f32 v115, v115, s20, v129
	v_mov_b32_e32 v116, 0
	v_mov_b32_e32 v117, 0
	v_mov_b32_e32 v118, 0
	v_mov_b32_e32 v119, 0
	v_cvt_pk_fp8_f32 v116, v100, v101
	v_cvt_pk_fp8_f32 v117, v104, v105
	v_cvt_pk_fp8_f32 v118, v108, v109
	v_cvt_pk_fp8_f32 v119, v112, v113
	v_cvt_pk_fp8_f32 v116, v102, v103 op_sel:[0,0,1]
	v_cvt_pk_fp8_f32 v117, v106, v107 op_sel:[0,0,1]
	v_cvt_pk_fp8_f32 v118, v110, v111 op_sel:[0,0,1]
	v_cvt_pk_fp8_f32 v119, v114, v115 op_sel:[0,0,1]
	s_nop 0
	global_store_dwordx4 v128, v[116:119], s[14:15]
	s_waitcnt vmcnt(12)
	v_mul_f32_e32 v68, 0x43000000, v68
	v_mul_f32_e32 v69, 0x43000000, v69
	v_mul_f32_e32 v70, 0x43000000, v70
	v_mul_f32_e32 v71, 0x43000000, v71
	ds_write_b128 v121, v[68:71]
	v_mul_f32_e32 v72, 0x43000000, v72
	v_mul_f32_e32 v73, 0x43000000, v73
	v_mul_f32_e32 v74, 0x43000000, v74
	v_mul_f32_e32 v75, 0x43000000, v75
	ds_write_b128 v121, v[72:75] offset:1024
	v_mul_f32_e32 v76, 0x43000000, v76
	v_mul_f32_e32 v77, 0x43000000, v77
	v_mul_f32_e32 v78, 0x43000000, v78
	v_mul_f32_e32 v79, 0x43000000, v79
	ds_write_b128 v121, v[76:79] offset:2048
	v_mul_f32_e32 v80, 0x43000000, v80
	v_mul_f32_e32 v81, 0x43000000, v81
	v_mul_f32_e32 v82, 0x43000000, v82
	v_mul_f32_e32 v83, 0x43000000, v83
	ds_write_b128 v121, v[80:83] offset:3072
	v_mul_f32_e32 v84, 0x43000000, v84
	v_mul_f32_e32 v85, 0x43000000, v85
	v_mul_f32_e32 v86, 0x43000000, v86
	v_mul_f32_e32 v87, 0x43000000, v87
	ds_write_b128 v121, v[84:87] offset:4096
	v_mul_f32_e32 v88, 0x43000000, v88
	v_mul_f32_e32 v89, 0x43000000, v89
	v_mul_f32_e32 v90, 0x43000000, v90
	v_mul_f32_e32 v91, 0x43000000, v91
	ds_write_b128 v121, v[88:91] offset:5120
	v_mul_f32_e32 v92, 0x43000000, v92
	v_mul_f32_e32 v93, 0x43000000, v93
	v_mul_f32_e32 v94, 0x43000000, v94
	v_mul_f32_e32 v95, 0x43000000, v95
	ds_write_b128 v121, v[92:95] offset:6144
	v_mul_f32_e32 v96, 0x43000000, v96
	v_mul_f32_e32 v97, 0x43000000, v97
	v_mul_f32_e32 v98, 0x43000000, v98
	v_mul_f32_e32 v99, 0x43000000, v99
	ds_write_b128 v121, v[96:99] offset:7168
	s_waitcnt lgkmcnt(0)
	s_barrier
; #define GAS __attribute__((address_space(1)))
; #define LAS __attribute__((address_space(3)))
; #define LDS_WAIT() asm volatile("s_waitcnt lgkmcnt(0)" ::: "memory")
;     const int pr = item >> 1, kb = 2 * (pr / nblk) + (item & 1), nb = pr % nblk, k0 = 64 * kb, n0 = 32 * nb;
;     const int nr = n0 + (lane & 31); const int sc = MAP == 1 ? src_col_in(nr) : nr;
;     float v[32];
; #pragma unroll
;     for (int i = 0; i < 32; ++i) v[i] = sc >= 0 ? W[(size_t)(k0 + 2 * i + (lane >> 5)) * Nsrc + sc] : 0.f;
; #pragma unroll
;     for (int i = 0; i < 32; ++i) { const int k = k0 + 2 * i + (lane >> 5); float x = v[i] * wscale; if (KS) x *= (k < ksplit ? ksA[k] : ksB[k - ksplit]); scr[(2 * i + (lane >> 5)) * 33 + (lane & 31)] = x; }
;     LDS_WAIT(); asm volatile("" ::: "memory");
;     const int c = lane & 7;
; #pragma unroll
;     for (int j = 0; j < 4; ++j) { const int n = (lane >> 3) + 8 * j; const LAS float* s = scr + (8 * c) * 33 + n;
;         const unsigned long long o = (unsigned long long)pg8::pk4_fp8(s[0 * 33], s[1 * 33], s[2 * 33], s[3 * 33]) | ((unsigned long long)pg8::pk4_fp8(s[4 * 33], s[5 * 33], s[6 * 33], s[7 * 33]) << 32);
;         *(GAS unsigned long long*)(WT + (size_t)(n0 + n) * K + k0 + 8 * c) = o; }
;     LDS_WAIT(); asm volatile("" ::: "memory");
	s_add_i32 s17, s16, 864
	s_min_u32 s17, s17, 0x7ff
	s_lshr_b32 s18, s17, 5
	s_add_i32 s18, s18, 0
	s_and_b32 s19, s17, 31
	s_lshl_b32 s18, s18, 21
	s_lshl_b32 s19, s19, 9
	s_add_u32 s18, s18, s19
	s_add_u32 s10, s2, s18
	s_addc_u32 s11, s3, 0
	global_load_dwordx4 v[68:71], v126, s[10:11]
	s_add_u32 s10, s10, 0x8000
	s_addc_u32 s11, s11, 0
	global_load_dwordx4 v[72:75], v126, s[10:11]
	s_add_u32 s10, s10, 0x8000
	s_addc_u32 s11, s11, 0
	global_load_dwordx4 v[76:79], v126, s[10:11]
	s_add_u32 s10, s10, 0x8000
	s_addc_u32 s11, s11, 0
	global_load_dwordx4 v[80:83], v126, s[10:11]
	s_add_u32 s10, s10, 0x8000
	s_addc_u32 s11, s11, 0
	global_load_dwordx4 v[84:87], v126, s[10:11]
	s_add_u32 s10, s10, 0x8000
	s_addc_u32 s11, s11, 0
	global_load_dwordx4 v[88:91], v126, s[10:11]
	s_add_u32 s10, s10, 0x8000
	s_addc_u32 s11, s11, 0
	global_load_dwordx4 v[92:95], v126, s[10:11]
	s_add_u32 s10, s10, 0x8000
	s_addc_u32 s11, s11, 0
	global_load_dwordx4 v[96:99], v126, s[10:11]
	s_add_i32 s17, s16, 672
	s_min_u32 s17, s17, 0x7ff
	s_lshr_b32 s18, s17, 5
	s_add_i32 s18, s18, 0
	s_and_b32 s19, s17, 31
	s_lshl_b32 s19, s19, 21
	s_lshl_b32 s18, s18, 7
	s_add_u32 s18, s18, s19
	s_add_u32 s14, s4, s18
	s_addc_u32 s15, s5, 0
	ds_read_b32 v100, v123
	ds_read_b32 v101, v123 offset:512
	ds_read_b32 v102, v123 offset:1024
	ds_read_b32 v103, v123 offset:1536
	ds_read_b32 v104, v123 offset:2048
	ds_read_b32 v105, v123 offset:2560
	ds_read_b32 v106, v123 offset:3072
	ds_read_b32 v107, v123 offset:3584
	ds_read_b32 v108, v123 offset:4096
	ds_read_b32 v109, v123 offset:4608
	ds_read_b32 v110, v123 offset:5120
	ds_read_b32 v111, v123 offset:5632
	ds_read_b32 v112, v123 offset:6144
	ds_read_b32 v113, v123 offset:6656
	ds_read_b32 v114, v123 offset:7168
	ds_read_b32 v115, v123 offset:7680
	s_waitcnt lgkmcnt(0)
	v_max_f32_e32 v100, v100, v100
	v_max_f32_e32 v101, v101, v101
	v_max_f32_e32 v102, v102, v102
	v_max_f32_e32 v103, v103, v103
	v_max_f32_e32 v104, v104, v104
	v_max_f32_e32 v105, v105, v105
	v_max_f32_e32 v106, v106, v106
	v_max_f32_e32 v107, v107, v107
	v_max_f32_e32 v108, v108, v108
	v_max_f32_e32 v109, v109, v109
	v_max_f32_e32 v110, v110, v110
	v_max_f32_e32 v111, v111, v111
	v_max_f32_e32 v112, v112, v112
	v_max_f32_e32 v113, v113, v113
	v_max_f32_e32 v114, v114, v114
	v_max_f32_e32 v115, v115, v115
	v_med3_f32 v100, v100, s20, v129
	v_med3_f32 v101, v101, s20, v129
	v_med3_f32 v102, v102, s20, v129
	v_med3_f32 v103, v103, s20, v129
	v_med3_f32 v104, v104, s20, v129
	v_med3_f32 v105, v105, s20, v129
	v_med3_f32 v106, v106, s20, v129
	v_med3_f32 v107, v107, s20, v129
	v_med3_f32 v108, v108, s20, v129
	v_med3_f32 v109, v109, s20, v129
	v_med3_f32 v110, v110, s20, v129
	v_med3_f32 v111, v111, s20, v129
	v_med3_f32 v112, v112, s20, v129
	v_med3_f32 v113, v113, s20, v129
	v_med3_f32 v114, v114, s20, v129
	v_med3_f32 v115, v115, s20, v129
	v_mov_b32_e32 v116, 0
	v_mov_b32_e32 v117, 0
	v_mov_b32_e32 v118, 0
	v_mov_b32_e32 v119, 0
	v_cvt_pk_fp8_f32 v116, v100, v101
	v_cvt_pk_fp8_f32 v117, v104, v105
	v_cvt_pk_fp8_f32 v118, v108, v109
	v_cvt_pk_fp8_f32 v119, v112, v113
	v_cvt_pk_fp8_f32 v116, v102, v103 op_sel:[0,0,1]
	v_cvt_pk_fp8_f32 v117, v106, v107 op_sel:[0,0,1]
	v_cvt_pk_fp8_f32 v118, v110, v111 op_sel:[0,0,1]
	v_cvt_pk_fp8_f32 v119, v114, v115 op_sel:[0,0,1]
	s_nop 0
	global_store_dwordx4 v127, v[116:119], s[14:15]
	ds_read_b32 v100, v125
	ds_read_b32 v101, v125 offset:512
	ds_read_b32 v102, v125 offset:1024
	ds_read_b32 v103, v125 offset:1536
	ds_read_b32 v104, v125 offset:2048
	ds_read_b32 v105, v125 offset:2560
	ds_read_b32 v106, v125 offset:3072
	ds_read_b32 v107, v125 offset:3584
	ds_read_b32 v108, v125 offset:4096
	ds_read_b32 v109, v125 offset:4608
	ds_read_b32 v110, v125 offset:5120
	ds_read_b32 v111, v125 offset:5632
	ds_read_b32 v112, v125 offset:6144
	ds_read_b32 v113, v125 offset:6656
	ds_read_b32 v114, v125 offset:7168
	ds_read_b32 v115, v125 offset:7680
	s_waitcnt lgkmcnt(0)
	v_max_f32_e32 v100, v100, v100
	v_max_f32_e32 v101, v101, v101
	v_max_f32_e32 v102, v102, v102
	v_max_f32_e32 v103, v103, v103
	v_max_f32_e32 v104, v104, v104
	v_max_f32_e32 v105, v105, v105
	v_max_f32_e32 v106, v106, v106
	v_max_f32_e32 v107, v107, v107
	v_max_f32_e32 v108, v108, v108
	v_max_f32_e32 v109, v109, v109
	v_max_f32_e32 v110, v110, v110
	v_max_f32_e32 v111, v111, v111
	v_max_f32_e32 v112, v112, v112
	v_max_f32_e32 v113, v113, v113
	v_max_f32_e32 v114, v114, v114
	v_max_f32_e32 v115, v115, v115
	v_med3_f32 v100, v100, s20, v129
	v_med3_f32 v101, v101, s20, v129
	v_med3_f32 v102, v102, s20, v129
	v_med3_f32 v103, v103, s20, v129
	v_med3_f32 v104, v104, s20, v129
	v_med3_f32 v105, v105, s20, v129
	v_med3_f32 v106, v106, s20, v129
	v_med3_f32 v107, v107, s20, v129
	v_med3_f32 v108, v108, s20, v129
	v_med3_f32 v109, v109, s20, v129
	v_med3_f32 v110, v110, s20, v129
	v_med3_f32 v111, v111, s20, v129
	v_med3_f32 v112, v112, s20, v129
	v_med3_f32 v113, v113, s20, v129
	v_med3_f32 v114, v114, s20, v129
	v_med3_f32 v115, v115, s20, v129
	v_mov_b32_e32 v116, 0
	v_mov_b32_e32 v117, 0
	v_mov_b32_e32 v118, 0
	v_mov_b32_e32 v119, 0
	v_cvt_pk_fp8_f32 v116, v100, v101
	v_cvt_pk_fp8_f32 v117, v104, v105
	v_cvt_pk_fp8_f32 v118, v108, v109
	v_cvt_pk_fp8_f32 v119, v112, v113
	v_cvt_pk_fp8_f32 v116, v102, v103 op_sel:[0,0,1]
	v_cvt_pk_fp8_f32 v117, v106, v107 op_sel:[0,0,1]
	v_cvt_pk_fp8_f32 v118, v110, v111 op_sel:[0,0,1]
	v_cvt_pk_fp8_f32 v119, v114, v115 op_sel:[0,0,1]
	s_nop 0
	global_store_dwordx4 v128, v[116:119], s[14:15]
	s_waitcnt vmcnt(12)
	v_mul_f32_e32 v36, 0x43000000, v36
	v_mul_f32_e32 v37, 0x43000000, v37
	v_mul_f32_e32 v38, 0x43000000, v38
	v_mul_f32_e32 v39, 0x43000000, v39
	ds_write_b128 v120, v[36:39]
	v_mul_f32_e32 v40, 0x43000000, v40
	v_mul_f32_e32 v41, 0x43000000, v41
	v_mul_f32_e32 v42, 0x43000000, v42
	v_mul_f32_e32 v43, 0x43000000, v43
	ds_write_b128 v120, v[40:43] offset:1024
	v_mul_f32_e32 v44, 0x43000000, v44
	v_mul_f32_e32 v45, 0x43000000, v45
	v_mul_f32_e32 v46, 0x43000000, v46
	v_mul_f32_e32 v47, 0x43000000, v47
	ds_write_b128 v120, v[44:47] offset:2048
	v_mul_f32_e32 v48, 0x43000000, v48
	v_mul_f32_e32 v49, 0x43000000, v49
	v_mul_f32_e32 v50, 0x43000000, v50
	v_mul_f32_e32 v51, 0x43000000, v51
	ds_write_b128 v120, v[48:51] offset:3072
	v_mul_f32_e32 v52, 0x43000000, v52
	v_mul_f32_e32 v53, 0x43000000, v53
	v_mul_f32_e32 v54, 0x43000000, v54
	v_mul_f32_e32 v55, 0x43000000, v55
	ds_write_b128 v120, v[52:55] offset:4096
	v_mul_f32_e32 v56, 0x43000000, v56
	v_mul_f32_e32 v57, 0x43000000, v57
	v_mul_f32_e32 v58, 0x43000000, v58
	v_mul_f32_e32 v59, 0x43000000, v59
	ds_write_b128 v120, v[56:59] offset:5120
	v_mul_f32_e32 v60, 0x43000000, v60
	v_mul_f32_e32 v61, 0x43000000, v61
	v_mul_f32_e32 v62, 0x43000000, v62
	v_mul_f32_e32 v63, 0x43000000, v63
	ds_write_b128 v120, v[60:63] offset:6144
	v_mul_f32_e32 v64, 0x43000000, v64
	v_mul_f32_e32 v65, 0x43000000, v65
	v_mul_f32_e32 v66, 0x43000000, v66
	v_mul_f32_e32 v67, 0x43000000, v67
	ds_write_b128 v120, v[64:67] offset:7168
	s_waitcnt lgkmcnt(0)
	s_barrier
; #define GAS __attribute__((address_space(1)))
; #define LAS __attribute__((address_space(3)))
; #define LDS_WAIT() asm volatile("s_waitcnt lgkmcnt(0)" ::: "memory")
;     const int pr = item >> 1, kb = 2 * (pr / nblk) + (item & 1), nb = pr % nblk, k0 = 64 * kb, n0 = 32 * nb;
;     const int nr = n0 + (lane & 31); const int sc = MAP == 1 ? src_col_in(nr) : nr;
;     float v[32];
; #pragma unroll
;     for (int i = 0; i < 32; ++i) v[i] = sc >= 0 ? W[(size_t)(k0 + 2 * i + (lane >> 5)) * Nsrc + sc] : 0.f;
; #pragma unroll
;     for (int i = 0; i < 32; ++i) { const int k = k0 + 2 * i + (lane >> 5); float x = v[i] * wscale; if (KS) x *= (k < ksplit ? ksA[k] : ksB[k - ksplit]); scr[(2 * i + (lane >> 5)) * 33 + (lane & 31)] = x; }
;     LDS_WAIT(); asm volatile("" ::: "memory");
;     const int c = lane & 7;
; #pragma unroll
;     for (int j = 0; j < 4; ++j) { const int n = (lane >> 3) + 8 * j; const LAS float* s = scr + (8 * c) * 33 + n;
;         const unsigned long long o = (unsigned long long)pg8::pk4_fp8(s[0 * 33], s[1 * 33], s[2 * 33], s[3 * 33]) | ((unsigned long long)pg8::pk4_fp8(s[4 * 33], s[5 * 33], s[6 * 33], s[7 * 33]) << 32);
;         *(GAS unsigned long long*)(WT + (size_t)(n0 + n) * K + k0 + 8 * c) = o; }
;     LDS_WAIT(); asm volatile("" ::: "memory");
	s_add_i32 s17, s16, 960
	s_min_u32 s17, s17, 0x7ff
	s_lshr_b32 s18, s17, 5
	s_add_i32 s18, s18, 0
	s_and_b32 s19, s17, 31
	s_lshl_b32 s18, s18, 21
	s_lshl_b32 s19, s19, 9
	s_add_u32 s18, s18, s19
	s_add_u32 s10, s2, s18
	s_addc_u32 s11, s3, 0
	global_load_dwordx4 v[36:39], v126, s[10:11]
	s_add_u32 s10, s10, 0x8000
	s_addc_u32 s11, s11, 0
	global_load_dwordx4 v[40:43], v126, s[10:11]
	s_add_u32 s10, s10, 0x8000
	s_addc_u32 s11, s11, 0
	global_load_dwordx4 v[44:47], v126, s[10:11]
	s_add_u32 s10, s10, 0x8000
	s_addc_u32 s11, s11, 0
	global_load_dwordx4 v[48:51], v126, s[10:11]
	s_add_u32 s10, s10, 0x8000
	s_addc_u32 s11, s11, 0
	global_load_dwordx4 v[52:55], v126, s[10:11]
	s_add_u32 s10, s10, 0x8000
	s_addc_u32 s11, s11, 0
	global_load_dwordx4 v[56:59], v126, s[10:11]
	s_add_u32 s10, s10, 0x8000
	s_addc_u32 s11, s11, 0
	global_load_dwordx4 v[60:63], v126, s[10:11]
	s_add_u32 s10, s10, 0x8000
	s_addc_u32 s11, s11, 0
	global_load_dwordx4 v[64:67], v126, s[10:11]
	s_add_i32 s17, s16, 768
	s_min_u32 s17, s17, 0x7ff
	s_lshr_b32 s18, s17, 5
	s_add_i32 s18, s18, 0
	s_and_b32 s19, s17, 31
	s_lshl_b32 s19, s19, 21
	s_lshl_b32 s18, s18, 7
	s_add_u32 s18, s18, s19
	s_add_u32 s14, s4, s18
	s_addc_u32 s15, s5, 0
	ds_read_b32 v100, v122
	ds_read_b32 v101, v122 offset:512
	ds_read_b32 v102, v122 offset:1024
	ds_read_b32 v103, v122 offset:1536
	ds_read_b32 v104, v122 offset:2048
	ds_read_b32 v105, v122 offset:2560
	ds_read_b32 v106, v122 offset:3072
	ds_read_b32 v107, v122 offset:3584
	ds_read_b32 v108, v122 offset:4096
	ds_read_b32 v109, v122 offset:4608
	ds_read_b32 v110, v122 offset:5120
	ds_read_b32 v111, v122 offset:5632
	ds_read_b32 v112, v122 offset:6144
	ds_read_b32 v113, v122 offset:6656
	ds_read_b32 v114, v122 offset:7168
	ds_read_b32 v115, v122 offset:7680
	s_waitcnt lgkmcnt(0)
	v_max_f32_e32 v100, v100, v100
	v_max_f32_e32 v101, v101, v101
	v_max_f32_e32 v102, v102, v102
	v_max_f32_e32 v103, v103, v103
	v_max_f32_e32 v104, v104, v104
	v_max_f32_e32 v105, v105, v105
	v_max_f32_e32 v106, v106, v106
	v_max_f32_e32 v107, v107, v107
	v_max_f32_e32 v108, v108, v108
	v_max_f32_e32 v109, v109, v109
	v_max_f32_e32 v110, v110, v110
	v_max_f32_e32 v111, v111, v111
	v_max_f32_e32 v112, v112, v112
	v_max_f32_e32 v113, v113, v113
	v_max_f32_e32 v114, v114, v114
	v_max_f32_e32 v115, v115, v115
	v_med3_f32 v100, v100, s20, v129
	v_med3_f32 v101, v101, s20, v129
	v_med3_f32 v102, v102, s20, v129
	v_med3_f32 v103, v103, s20, v129
	v_med3_f32 v104, v104, s20, v129
	v_med3_f32 v105, v105, s20, v129
	v_med3_f32 v106, v106, s20, v129
	v_med3_f32 v107, v107, s20, v129
	v_med3_f32 v108, v108, s20, v129
	v_med3_f32 v109, v109, s20, v129
	v_med3_f32 v110, v110, s20, v129
	v_med3_f32 v111, v111, s20, v129
	v_med3_f32 v112, v112, s20, v129
	v_med3_f32 v113, v113, s20, v129
	v_med3_f32 v114, v114, s20, v129
	v_med3_f32 v115, v115, s20, v129
	v_mov_b32_e32 v116, 0
	v_mov_b32_e32 v117, 0
	v_mov_b32_e32 v118, 0
	v_mov_b32_e32 v119, 0
	v_cvt_pk_fp8_f32 v116, v100, v101
	v_cvt_pk_fp8_f32 v117, v104, v105
	v_cvt_pk_fp8_f32 v118, v108, v109
	v_cvt_pk_fp8_f32 v119, v112, v113
	v_cvt_pk_fp8_f32 v116, v102, v103 op_sel:[0,0,1]
	v_cvt_pk_fp8_f32 v117, v106, v107 op_sel:[0,0,1]
	v_cvt_pk_fp8_f32 v118, v110, v111 op_sel:[0,0,1]
	v_cvt_pk_fp8_f32 v119, v114, v115 op_sel:[0,0,1]
	s_nop 0
	global_store_dwordx4 v127, v[116:119], s[14:15]
	ds_read_b32 v100, v124
	ds_read_b32 v101, v124 offset:512
	ds_read_b32 v102, v124 offset:1024
	ds_read_b32 v103, v124 offset:1536
	ds_read_b32 v104, v124 offset:2048
	ds_read_b32 v105, v124 offset:2560
	ds_read_b32 v106, v124 offset:3072
	ds_read_b32 v107, v124 offset:3584
	ds_read_b32 v108, v124 offset:4096
	ds_read_b32 v109, v124 offset:4608
	ds_read_b32 v110, v124 offset:5120
	ds_read_b32 v111, v124 offset:5632
	ds_read_b32 v112, v124 offset:6144
	ds_read_b32 v113, v124 offset:6656
	ds_read_b32 v114, v124 offset:7168
	ds_read_b32 v115, v124 offset:7680
	s_waitcnt lgkmcnt(0)
	v_max_f32_e32 v100, v100, v100
	v_max_f32_e32 v101, v101, v101
	v_max_f32_e32 v102, v102, v102
	v_max_f32_e32 v103, v103, v103
	v_max_f32_e32 v104, v104, v104
	v_max_f32_e32 v105, v105, v105
	v_max_f32_e32 v106, v106, v106
	v_max_f32_e32 v107, v107, v107
	v_max_f32_e32 v108, v108, v108
	v_max_f32_e32 v109, v109, v109
	v_max_f32_e32 v110, v110, v110
	v_max_f32_e32 v111, v111, v111
	v_max_f32_e32 v112, v112, v112
	v_max_f32_e32 v113, v113, v113
	v_max_f32_e32 v114, v114, v114
	v_max_f32_e32 v115, v115, v115
	v_med3_f32 v100, v100, s20, v129
	v_med3_f32 v101, v101, s20, v129
	v_med3_f32 v102, v102, s20, v129
	v_med3_f32 v103, v103, s20, v129
	v_med3_f32 v104, v104, s20, v129
	v_med3_f32 v105, v105, s20, v129
	v_med3_f32 v106, v106, s20, v129
	v_med3_f32 v107, v107, s20, v129
	v_med3_f32 v108, v108, s20, v129
	v_med3_f32 v109, v109, s20, v129
	v_med3_f32 v110, v110, s20, v129
	v_med3_f32 v111, v111, s20, v129
	v_med3_f32 v112, v112, s20, v129
	v_med3_f32 v113, v113, s20, v129
	v_med3_f32 v114, v114, s20, v129
	v_med3_f32 v115, v115, s20, v129
	v_mov_b32_e32 v116, 0
	v_mov_b32_e32 v117, 0
	v_mov_b32_e32 v118, 0
	v_mov_b32_e32 v119, 0
	v_cvt_pk_fp8_f32 v116, v100, v101
	v_cvt_pk_fp8_f32 v117, v104, v105
	v_cvt_pk_fp8_f32 v118, v108, v109
	v_cvt_pk_fp8_f32 v119, v112, v113
	v_cvt_pk_fp8_f32 v116, v102, v103 op_sel:[0,0,1]
	v_cvt_pk_fp8_f32 v117, v106, v107 op_sel:[0,0,1]
	v_cvt_pk_fp8_f32 v118, v110, v111 op_sel:[0,0,1]
	v_cvt_pk_fp8_f32 v119, v114, v115 op_sel:[0,0,1]
	s_nop 0
	global_store_dwordx4 v128, v[116:119], s[14:15]
	s_waitcnt vmcnt(12)
	v_mul_f32_e32 v68, 0x43000000, v68
	v_mul_f32_e32 v69, 0x43000000, v69
	v_mul_f32_e32 v70, 0x43000000, v70
	v_mul_f32_e32 v71, 0x43000000, v71
	ds_write_b128 v121, v[68:71]
	v_mul_f32_e32 v72, 0x43000000, v72
	v_mul_f32_e32 v73, 0x43000000, v73
	v_mul_f32_e32 v74, 0x43000000, v74
	v_mul_f32_e32 v75, 0x43000000, v75
	ds_write_b128 v121, v[72:75] offset:1024
	v_mul_f32_e32 v76, 0x43000000, v76
	v_mul_f32_e32 v77, 0x43000000, v77
	v_mul_f32_e32 v78, 0x43000000, v78
	v_mul_f32_e32 v79, 0x43000000, v79
	ds_write_b128 v121, v[76:79] offset:2048
	v_mul_f32_e32 v80, 0x43000000, v80
	v_mul_f32_e32 v81, 0x43000000, v81
	v_mul_f32_e32 v82, 0x43000000, v82
	v_mul_f32_e32 v83, 0x43000000, v83
	ds_write_b128 v121, v[80:83] offset:3072
	v_mul_f32_e32 v84, 0x43000000, v84
	v_mul_f32_e32 v85, 0x43000000, v85
	v_mul_f32_e32 v86, 0x43000000, v86
	v_mul_f32_e32 v87, 0x43000000, v87
	ds_write_b128 v121, v[84:87] offset:4096
	v_mul_f32_e32 v88, 0x43000000, v88
	v_mul_f32_e32 v89, 0x43000000, v89
	v_mul_f32_e32 v90, 0x43000000, v90
	v_mul_f32_e32 v91, 0x43000000, v91
	ds_write_b128 v121, v[88:91] offset:5120
	v_mul_f32_e32 v92, 0x43000000, v92
	v_mul_f32_e32 v93, 0x43000000, v93
	v_mul_f32_e32 v94, 0x43000000, v94
	v_mul_f32_e32 v95, 0x43000000, v95
	ds_write_b128 v121, v[92:95] offset:6144
	v_mul_f32_e32 v96, 0x43000000, v96
	v_mul_f32_e32 v97, 0x43000000, v97
	v_mul_f32_e32 v98, 0x43000000, v98
	v_mul_f32_e32 v99, 0x43000000, v99
	ds_write_b128 v121, v[96:99] offset:7168
	s_waitcnt lgkmcnt(0)
	s_barrier
; #define GAS __attribute__((address_space(1)))
; #define LAS __attribute__((address_space(3)))
; #define LDS_WAIT() asm volatile("s_waitcnt lgkmcnt(0)" ::: "memory")
;     const int pr = item >> 1, kb = 2 * (pr / nblk) + (item & 1), nb = pr % nblk, k0 = 64 * kb, n0 = 32 * nb;
;     const int nr = n0 + (lane & 31); const int sc = MAP == 1 ? src_col_in(nr) : nr;
;     float v[32];
; #pragma unroll
;     for (int i = 0; i < 32; ++i) v[i] = sc >= 0 ? W[(size_t)(k0 + 2 * i + (lane >> 5)) * Nsrc + sc] : 0.f;
; #pragma unroll
;     for (int i = 0; i < 32; ++i) { const int k = k0 + 2 * i + (lane >> 5); float x = v[i] * wscale; if (KS) x *= (k < ksplit ? ksA[k] : ksB[k - ksplit]); scr[(2 * i + (lane >> 5)) * 33 + (lane & 31)] = x; }
;     LDS_WAIT(); asm volatile("" ::: "memory");
;     const int c = lane & 7;
; #pragma unroll
;     for (int j = 0; j < 4; ++j) { const int n = (lane >> 3) + 8 * j; const LAS float* s = scr + (8 * c) * 33 + n;
;         const unsigned long long o = (unsigned long long)pg8::pk4_fp8(s[0 * 33], s[1 * 33], s[2 * 33], s[3 * 33]) | ((unsigned long long)pg8::pk4_fp8(s[4 * 33], s[5 * 33], s[6 * 33], s[7 * 33]) << 32);
;         *(GAS unsigned long long*)(WT + (size_t)(n0 + n) * K + k0 + 8 * c) = o; }
;     LDS_WAIT(); asm volatile("" ::: "memory");
	s_add_i32 s17, s16, 1056
	s_min_u32 s17, s17, 0x7ff
	s_lshr_b32 s18, s17, 5
	s_add_i32 s18, s18, 0
	s_and_b32 s19, s17, 31
	s_lshl_b32 s18, s18, 21
	s_lshl_b32 s19, s19, 9
	s_add_u32 s18, s18, s19
	s_add_u32 s10, s2, s18
	s_addc_u32 s11, s3, 0
	global_load_dwordx4 v[68:71], v126, s[10:11]
	s_add_u32 s10, s10, 0x8000
	s_addc_u32 s11, s11, 0
	global_load_dwordx4 v[72:75], v126, s[10:11]
	s_add_u32 s10, s10, 0x8000
	s_addc_u32 s11, s11, 0
	global_load_dwordx4 v[76:79], v126, s[10:11]
	s_add_u32 s10, s10, 0x8000
	s_addc_u32 s11, s11, 0
	global_load_dwordx4 v[80:83], v126, s[10:11]
	s_add_u32 s10, s10, 0x8000
	s_addc_u32 s11, s11, 0
	global_load_dwordx4 v[84:87], v126, s[10:11]
	s_add_u32 s10, s10, 0x8000
	s_addc_u32 s11, s11, 0
	global_load_dwordx4 v[88:91], v126, s[10:11]
	s_add_u32 s10, s10, 0x8000
	s_addc_u32 s11, s11, 0
	global_load_dwordx4 v[92:95], v126, s[10:11]
	s_add_u32 s10, s10, 0x8000
	s_addc_u32 s11, s11, 0
	global_load_dwordx4 v[96:99], v126, s[10:11]
	s_add_i32 s17, s16, 864
	s_min_u32 s17, s17, 0x7ff
	s_lshr_b32 s18, s17, 5
	s_add_i32 s18, s18, 0
	s_and_b32 s19, s17, 31
	s_lshl_b32 s19, s19, 21
	s_lshl_b32 s18, s18, 7
	s_add_u32 s18, s18, s19
	s_add_u32 s14, s4, s18
	s_addc_u32 s15, s5, 0
	ds_read_b32 v100, v123
	ds_read_b32 v101, v123 offset:512
	ds_read_b32 v102, v123 offset:1024
	ds_read_b32 v103, v123 offset:1536
	ds_read_b32 v104, v123 offset:2048
	ds_read_b32 v105, v123 offset:2560
	ds_read_b32 v106, v123 offset:3072
	ds_read_b32 v107, v123 offset:3584
	ds_read_b32 v108, v123 offset:4096
	ds_read_b32 v109, v123 offset:4608
	ds_read_b32 v110, v123 offset:5120
	ds_read_b32 v111, v123 offset:5632
	ds_read_b32 v112, v123 offset:6144
	ds_read_b32 v113, v123 offset:6656
	ds_read_b32 v114, v123 offset:7168
	ds_read_b32 v115, v123 offset:7680
	s_waitcnt lgkmcnt(0)
	v_max_f32_e32 v100, v100, v100
	v_max_f32_e32 v101, v101, v101
	v_max_f32_e32 v102, v102, v102
	v_max_f32_e32 v103, v103, v103
	v_max_f32_e32 v104, v104, v104
	v_max_f32_e32 v105, v105, v105
	v_max_f32_e32 v106, v106, v106
	v_max_f32_e32 v107, v107, v107
	v_max_f32_e32 v108, v108, v108
	v_max_f32_e32 v109, v109, v109
	v_max_f32_e32 v110, v110, v110
	v_max_f32_e32 v111, v111, v111
	v_max_f32_e32 v112, v112, v112
	v_max_f32_e32 v113, v113, v113
	v_max_f32_e32 v114, v114, v114
	v_max_f32_e32 v115, v115, v115
	v_med3_f32 v100, v100, s20, v129
	v_med3_f32 v101, v101, s20, v129
	v_med3_f32 v102, v102, s20, v129
	v_med3_f32 v103, v103, s20, v129
	v_med3_f32 v104, v104, s20, v129
	v_med3_f32 v105, v105, s20, v129
	v_med3_f32 v106, v106, s20, v129
	v_med3_f32 v107, v107, s20, v129
	v_med3_f32 v108, v108, s20, v129
	v_med3_f32 v109, v109, s20, v129
	v_med3_f32 v110, v110, s20, v129
	v_med3_f32 v111, v111, s20, v129
	v_med3_f32 v112, v112, s20, v129
	v_med3_f32 v113, v113, s20, v129
	v_med3_f32 v114, v114, s20, v129
	v_med3_f32 v115, v115, s20, v129
	v_mov_b32_e32 v116, 0
	v_mov_b32_e32 v117, 0
	v_mov_b32_e32 v118, 0
	v_mov_b32_e32 v119, 0
	v_cvt_pk_fp8_f32 v116, v100, v101
	v_cvt_pk_fp8_f32 v117, v104, v105
	v_cvt_pk_fp8_f32 v118, v108, v109
	v_cvt_pk_fp8_f32 v119, v112, v113
	v_cvt_pk_fp8_f32 v116, v102, v103 op_sel:[0,0,1]
	v_cvt_pk_fp8_f32 v117, v106, v107 op_sel:[0,0,1]
	v_cvt_pk_fp8_f32 v118, v110, v111 op_sel:[0,0,1]
	v_cvt_pk_fp8_f32 v119, v114, v115 op_sel:[0,0,1]
	s_nop 0
	global_store_dwordx4 v127, v[116:119], s[14:15]
	ds_read_b32 v100, v125
	ds_read_b32 v101, v125 offset:512
	ds_read_b32 v102, v125 offset:1024
	ds_read_b32 v103, v125 offset:1536
	ds_read_b32 v104, v125 offset:2048
	ds_read_b32 v105, v125 offset:2560
	ds_read_b32 v106, v125 offset:3072
	ds_read_b32 v107, v125 offset:3584
	ds_read_b32 v108, v125 offset:4096
	ds_read_b32 v109, v125 offset:4608
	ds_read_b32 v110, v125 offset:5120
	ds_read_b32 v111, v125 offset:5632
	ds_read_b32 v112, v125 offset:6144
	ds_read_b32 v113, v125 offset:6656
	ds_read_b32 v114, v125 offset:7168
	ds_read_b32 v115, v125 offset:7680
	s_waitcnt lgkmcnt(0)
	v_max_f32_e32 v100, v100, v100
	v_max_f32_e32 v101, v101, v101
	v_max_f32_e32 v102, v102, v102
	v_max_f32_e32 v103, v103, v103
	v_max_f32_e32 v104, v104, v104
	v_max_f32_e32 v105, v105, v105
	v_max_f32_e32 v106, v106, v106
	v_max_f32_e32 v107, v107, v107
	v_max_f32_e32 v108, v108, v108
	v_max_f32_e32 v109, v109, v109
	v_max_f32_e32 v110, v110, v110
	v_max_f32_e32 v111, v111, v111
	v_max_f32_e32 v112, v112, v112
	v_max_f32_e32 v113, v113, v113
	v_max_f32_e32 v114, v114, v114
	v_max_f32_e32 v115, v115, v115
	v_med3_f32 v100, v100, s20, v129
	v_med3_f32 v101, v101, s20, v129
	v_med3_f32 v102, v102, s20, v129
	v_med3_f32 v103, v103, s20, v129
	v_med3_f32 v104, v104, s20, v129
	v_med3_f32 v105, v105, s20, v129
	v_med3_f32 v106, v106, s20, v129
	v_med3_f32 v107, v107, s20, v129
	v_med3_f32 v108, v108, s20, v129
	v_med3_f32 v109, v109, s20, v129
	v_med3_f32 v110, v110, s20, v129
	v_med3_f32 v111, v111, s20, v129
	v_med3_f32 v112, v112, s20, v129
	v_med3_f32 v113, v113, s20, v129
	v_med3_f32 v114, v114, s20, v129
	v_med3_f32 v115, v115, s20, v129
	v_mov_b32_e32 v116, 0
	v_mov_b32_e32 v117, 0
	v_mov_b32_e32 v118, 0
	v_mov_b32_e32 v119, 0
	v_cvt_pk_fp8_f32 v116, v100, v101
	v_cvt_pk_fp8_f32 v117, v104, v105
	v_cvt_pk_fp8_f32 v118, v108, v109
	v_cvt_pk_fp8_f32 v119, v112, v113
	v_cvt_pk_fp8_f32 v116, v102, v103 op_sel:[0,0,1]
	v_cvt_pk_fp8_f32 v117, v106, v107 op_sel:[0,0,1]
	v_cvt_pk_fp8_f32 v118, v110, v111 op_sel:[0,0,1]
	v_cvt_pk_fp8_f32 v119, v114, v115 op_sel:[0,0,1]
	s_nop 0
	global_store_dwordx4 v128, v[116:119], s[14:15]
	s_waitcnt vmcnt(12)
	v_mul_f32_e32 v36, 0x43000000, v36
	v_mul_f32_e32 v37, 0x43000000, v37
	v_mul_f32_e32 v38, 0x43000000, v38
	v_mul_f32_e32 v39, 0x43000000, v39
	ds_write_b128 v120, v[36:39]
	v_mul_f32_e32 v40, 0x43000000, v40
	v_mul_f32_e32 v41, 0x43000000, v41
	v_mul_f32_e32 v42, 0x43000000, v42
	v_mul_f32_e32 v43, 0x43000000, v43
	ds_write_b128 v120, v[40:43] offset:1024
	v_mul_f32_e32 v44, 0x43000000, v44
	v_mul_f32_e32 v45, 0x43000000, v45
	v_mul_f32_e32 v46, 0x43000000, v46
	v_mul_f32_e32 v47, 0x43000000, v47
	ds_write_b128 v120, v[44:47] offset:2048
	v_mul_f32_e32 v48, 0x43000000, v48
	v_mul_f32_e32 v49, 0x43000000, v49
	v_mul_f32_e32 v50, 0x43000000, v50
	v_mul_f32_e32 v51, 0x43000000, v51
	ds_write_b128 v120, v[48:51] offset:3072
	v_mul_f32_e32 v52, 0x43000000, v52
	v_mul_f32_e32 v53, 0x43000000, v53
	v_mul_f32_e32 v54, 0x43000000, v54
	v_mul_f32_e32 v55, 0x43000000, v55
	ds_write_b128 v120, v[52:55] offset:4096
	v_mul_f32_e32 v56, 0x43000000, v56
	v_mul_f32_e32 v57, 0x43000000, v57
	v_mul_f32_e32 v58, 0x43000000, v58
	v_mul_f32_e32 v59, 0x43000000, v59
	ds_write_b128 v120, v[56:59] offset:5120
	v_mul_f32_e32 v60, 0x43000000, v60
	v_mul_f32_e32 v61, 0x43000000, v61
	v_mul_f32_e32 v62, 0x43000000, v62
	v_mul_f32_e32 v63, 0x43000000, v63
	ds_write_b128 v120, v[60:63] offset:6144
	v_mul_f32_e32 v64, 0x43000000, v64
	v_mul_f32_e32 v65, 0x43000000, v65
	v_mul_f32_e32 v66, 0x43000000, v66
	v_mul_f32_e32 v67, 0x43000000, v67
	ds_write_b128 v120, v[64:67] offset:7168
	s_waitcnt lgkmcnt(0)
	s_barrier
; #define GAS __attribute__((address_space(1)))
; #define LAS __attribute__((address_space(3)))
; #define LDS_WAIT() asm volatile("s_waitcnt lgkmcnt(0)" ::: "memory")
;     const int pr = item >> 1, kb = 2 * (pr / nblk) + (item & 1), nb = pr % nblk, k0 = 64 * kb, n0 = 32 * nb;
;     const int nr = n0 + (lane & 31); const int sc = MAP == 1 ? src_col_in(nr) : nr;
;     float v[32];
; #pragma unroll
;     for (int i = 0; i < 32; ++i) v[i] = sc >= 0 ? W[(size_t)(k0 + 2 * i + (lane >> 5)) * Nsrc + sc] : 0.f;
; #pragma unroll
;     for (int i = 0; i < 32; ++i) { const int k = k0 + 2 * i + (lane >> 5); float x = v[i] * wscale; if (KS) x *= (k < ksplit ? ksA[k] : ksB[k - ksplit]); scr[(2 * i + (lane >> 5)) * 33 + (lane & 31)] = x; }
;     LDS_WAIT(); asm volatile("" ::: "memory");
;     const int c = lane & 7;
; #pragma unroll
;     for (int j = 0; j < 4; ++j) { const int n = (lane >> 3) + 8 * j; const LAS float* s = scr + (8 * c) * 33 + n;
;         const unsigned long long o = (unsigned long long)pg8::pk4_fp8(s[0 * 33], s[1 * 33], s[2 * 33], s[3 * 33]) | ((unsigned long long)pg8::pk4_fp8(s[4 * 33], s[5 * 33], s[6 * 33], s[7 * 33]) << 32);
;         *(GAS unsigned long long*)(WT + (size_t)(n0 + n) * K + k0 + 8 * c) = o; }
;     LDS_WAIT(); asm volatile("" ::: "memory");
	s_add_i32 s17, s16, 1152
	s_min_u32 s17, s17, 0x7ff
	s_lshr_b32 s18, s17, 5
	s_add_i32 s18, s18, 0
	s_and_b32 s19, s17, 31
	s_lshl_b32 s18, s18, 21
	s_lshl_b32 s19, s19, 9
	s_add_u32 s18, s18, s19
	s_add_u32 s10, s2, s18
	s_addc_u32 s11, s3, 0
	global_load_dwordx4 v[36:39], v126, s[10:11]
	s_add_u32 s10, s10, 0x8000
	s_addc_u32 s11, s11, 0
	global_load_dwordx4 v[40:43], v126, s[10:11]
	s_add_u32 s10, s10, 0x8000
	s_addc_u32 s11, s11, 0
	global_load_dwordx4 v[44:47], v126, s[10:11]
	s_add_u32 s10, s10, 0x8000
	s_addc_u32 s11, s11, 0
	global_load_dwordx4 v[48:51], v126, s[10:11]
	s_add_u32 s10, s10, 0x8000
	s_addc_u32 s11, s11, 0
	global_load_dwordx4 v[52:55], v126, s[10:11]
	s_add_u32 s10, s10, 0x8000
	s_addc_u32 s11, s11, 0
	global_load_dwordx4 v[56:59], v126, s[10:11]
	s_add_u32 s10, s10, 0x8000
	s_addc_u32 s11, s11, 0
	global_load_dwordx4 v[60:63], v126, s[10:11]
	s_add_u32 s10, s10, 0x8000
	s_addc_u32 s11, s11, 0
	global_load_dwordx4 v[64:67], v126, s[10:11]
	s_add_i32 s17, s16, 960
	s_min_u32 s17, s17, 0x7ff
	s_lshr_b32 s18, s17, 5
	s_add_i32 s18, s18, 0
	s_and_b32 s19, s17, 31
	s_lshl_b32 s19, s19, 21
	s_lshl_b32 s18, s18, 7
	s_add_u32 s18, s18, s19
	s_add_u32 s14, s4, s18
	s_addc_u32 s15, s5, 0
	ds_read_b32 v100, v122
	ds_read_b32 v101, v122 offset:512
	ds_read_b32 v102, v122 offset:1024
	ds_read_b32 v103, v122 offset:1536
	ds_read_b32 v104, v122 offset:2048
	ds_read_b32 v105, v122 offset:2560
	ds_read_b32 v106, v122 offset:3072
	ds_read_b32 v107, v122 offset:3584
	ds_read_b32 v108, v122 offset:4096
	ds_read_b32 v109, v122 offset:4608
	ds_read_b32 v110, v122 offset:5120
	ds_read_b32 v111, v122 offset:5632
	ds_read_b32 v112, v122 offset:6144
	ds_read_b32 v113, v122 offset:6656
	ds_read_b32 v114, v122 offset:7168
	ds_read_b32 v115, v122 offset:7680
	s_waitcnt lgkmcnt(0)
	v_max_f32_e32 v100, v100, v100
	v_max_f32_e32 v101, v101, v101
	v_max_f32_e32 v102, v102, v102
	v_max_f32_e32 v103, v103, v103
	v_max_f32_e32 v104, v104, v104
	v_max_f32_e32 v105, v105, v105
	v_max_f32_e32 v106, v106, v106
	v_max_f32_e32 v107, v107, v107
	v_max_f32_e32 v108, v108, v108
	v_max_f32_e32 v109, v109, v109
	v_max_f32_e32 v110, v110, v110
	v_max_f32_e32 v111, v111, v111
	v_max_f32_e32 v112, v112, v112
	v_max_f32_e32 v113, v113, v113
	v_max_f32_e32 v114, v114, v114
	v_max_f32_e32 v115, v115, v115
	v_med3_f32 v100, v100, s20, v129
	v_med3_f32 v101, v101, s20, v129
	v_med3_f32 v102, v102, s20, v129
	v_med3_f32 v103, v103, s20, v129
	v_med3_f32 v104, v104, s20, v129
	v_med3_f32 v105, v105, s20, v129
	v_med3_f32 v106, v106, s20, v129
	v_med3_f32 v107, v107, s20, v129
	v_med3_f32 v108, v108, s20, v129
	v_med3_f32 v109, v109, s20, v129
	v_med3_f32 v110, v110, s20, v129
	v_med3_f32 v111, v111, s20, v129
	v_med3_f32 v112, v112, s20, v129
	v_med3_f32 v113, v113, s20, v129
	v_med3_f32 v114, v114, s20, v129
	v_med3_f32 v115, v115, s20, v129
	v_mov_b32_e32 v116, 0
	v_mov_b32_e32 v117, 0
	v_mov_b32_e32 v118, 0
	v_mov_b32_e32 v119, 0
	v_cvt_pk_fp8_f32 v116, v100, v101
	v_cvt_pk_fp8_f32 v117, v104, v105
	v_cvt_pk_fp8_f32 v118, v108, v109
	v_cvt_pk_fp8_f32 v119, v112, v113
	v_cvt_pk_fp8_f32 v116, v102, v103 op_sel:[0,0,1]
	v_cvt_pk_fp8_f32 v117, v106, v107 op_sel:[0,0,1]
	v_cvt_pk_fp8_f32 v118, v110, v111 op_sel:[0,0,1]
	v_cvt_pk_fp8_f32 v119, v114, v115 op_sel:[0,0,1]
	s_nop 0
	global_store_dwordx4 v127, v[116:119], s[14:15]
	ds_read_b32 v100, v124
	ds_read_b32 v101, v124 offset:512
	ds_read_b32 v102, v124 offset:1024
	ds_read_b32 v103, v124 offset:1536
	ds_read_b32 v104, v124 offset:2048
	ds_read_b32 v105, v124 offset:2560
	ds_read_b32 v106, v124 offset:3072
	ds_read_b32 v107, v124 offset:3584
	ds_read_b32 v108, v124 offset:4096
	ds_read_b32 v109, v124 offset:4608
	ds_read_b32 v110, v124 offset:5120
	ds_read_b32 v111, v124 offset:5632
	ds_read_b32 v112, v124 offset:6144
	ds_read_b32 v113, v124 offset:6656
	ds_read_b32 v114, v124 offset:7168
	ds_read_b32 v115, v124 offset:7680
	s_waitcnt lgkmcnt(0)
	v_max_f32_e32 v100, v100, v100
	v_max_f32_e32 v101, v101, v101
	v_max_f32_e32 v102, v102, v102
	v_max_f32_e32 v103, v103, v103
	v_max_f32_e32 v104, v104, v104
	v_max_f32_e32 v105, v105, v105
	v_max_f32_e32 v106, v106, v106
	v_max_f32_e32 v107, v107, v107
	v_max_f32_e32 v108, v108, v108
	v_max_f32_e32 v109, v109, v109
	v_max_f32_e32 v110, v110, v110
	v_max_f32_e32 v111, v111, v111
	v_max_f32_e32 v112, v112, v112
	v_max_f32_e32 v113, v113, v113
	v_max_f32_e32 v114, v114, v114
	v_max_f32_e32 v115, v115, v115
	v_med3_f32 v100, v100, s20, v129
	v_med3_f32 v101, v101, s20, v129
	v_med3_f32 v102, v102, s20, v129
	v_med3_f32 v103, v103, s20, v129
	v_med3_f32 v104, v104, s20, v129
	v_med3_f32 v105, v105, s20, v129
	v_med3_f32 v106, v106, s20, v129
	v_med3_f32 v107, v107, s20, v129
	v_med3_f32 v108, v108, s20, v129
	v_med3_f32 v109, v109, s20, v129
	v_med3_f32 v110, v110, s20, v129
	v_med3_f32 v111, v111, s20, v129
	v_med3_f32 v112, v112, s20, v129
	v_med3_f32 v113, v113, s20, v129
	v_med3_f32 v114, v114, s20, v129
	v_med3_f32 v115, v115, s20, v129
	v_mov_b32_e32 v116, 0
	v_mov_b32_e32 v117, 0
	v_mov_b32_e32 v118, 0
	v_mov_b32_e32 v119, 0
	v_cvt_pk_fp8_f32 v116, v100, v101
	v_cvt_pk_fp8_f32 v117, v104, v105
	v_cvt_pk_fp8_f32 v118, v108, v109
	v_cvt_pk_fp8_f32 v119, v112, v113
	v_cvt_pk_fp8_f32 v116, v102, v103 op_sel:[0,0,1]
	v_cvt_pk_fp8_f32 v117, v106, v107 op_sel:[0,0,1]
	v_cvt_pk_fp8_f32 v118, v110, v111 op_sel:[0,0,1]
	v_cvt_pk_fp8_f32 v119, v114, v115 op_sel:[0,0,1]
	s_nop 0
	global_store_dwordx4 v128, v[116:119], s[14:15]
	s_waitcnt vmcnt(12)
	v_mul_f32_e32 v68, 0x43000000, v68
	v_mul_f32_e32 v69, 0x43000000, v69
	v_mul_f32_e32 v70, 0x43000000, v70
	v_mul_f32_e32 v71, 0x43000000, v71
	ds_write_b128 v121, v[68:71]
	v_mul_f32_e32 v72, 0x43000000, v72
	v_mul_f32_e32 v73, 0x43000000, v73
	v_mul_f32_e32 v74, 0x43000000, v74
	v_mul_f32_e32 v75, 0x43000000, v75
	ds_write_b128 v121, v[72:75] offset:1024
	v_mul_f32_e32 v76, 0x43000000, v76
	v_mul_f32_e32 v77, 0x43000000, v77
	v_mul_f32_e32 v78, 0x43000000, v78
	v_mul_f32_e32 v79, 0x43000000, v79
	ds_write_b128 v121, v[76:79] offset:2048
	v_mul_f32_e32 v80, 0x43000000, v80
	v_mul_f32_e32 v81, 0x43000000, v81
	v_mul_f32_e32 v82, 0x43000000, v82
	v_mul_f32_e32 v83, 0x43000000, v83
	ds_write_b128 v121, v[80:83] offset:3072
	v_mul_f32_e32 v84, 0x43000000, v84
	v_mul_f32_e32 v85, 0x43000000, v85
	v_mul_f32_e32 v86, 0x43000000, v86
	v_mul_f32_e32 v87, 0x43000000, v87
	ds_write_b128 v121, v[84:87] offset:4096
	v_mul_f32_e32 v88, 0x43000000, v88
	v_mul_f32_e32 v89, 0x43000000, v89
	v_mul_f32_e32 v90, 0x43000000, v90
	v_mul_f32_e32 v91, 0x43000000, v91
	ds_write_b128 v121, v[88:91] offset:5120
	v_mul_f32_e32 v92, 0x43000000, v92
	v_mul_f32_e32 v93, 0x43000000, v93
	v_mul_f32_e32 v94, 0x43000000, v94
	v_mul_f32_e32 v95, 0x43000000, v95
	ds_write_b128 v121, v[92:95] offset:6144
	v_mul_f32_e32 v96, 0x43000000, v96
	v_mul_f32_e32 v97, 0x43000000, v97
	v_mul_f32_e32 v98, 0x43000000, v98
	v_mul_f32_e32 v99, 0x43000000, v99
	ds_write_b128 v121, v[96:99] offset:7168
	s_waitcnt lgkmcnt(0)
	s_barrier
; #define GAS __attribute__((address_space(1)))
; #define LAS __attribute__((address_space(3)))
; #define LDS_WAIT() asm volatile("s_waitcnt lgkmcnt(0)" ::: "memory")
;     const int pr = item >> 1, kb = 2 * (pr / nblk) + (item & 1), nb = pr % nblk, k0 = 64 * kb, n0 = 32 * nb;
;     const int nr = n0 + (lane & 31); const int sc = MAP == 1 ? src_col_in(nr) : nr;
;     float v[32];
; #pragma unroll
;     for (int i = 0; i < 32; ++i) v[i] = sc >= 0 ? W[(size_t)(k0 + 2 * i + (lane >> 5)) * Nsrc + sc] : 0.f;
; #pragma unroll
;     for (int i = 0; i < 32; ++i) { const int k = k0 + 2 * i + (lane >> 5); float x = v[i] * wscale; if (KS) x *= (k < ksplit ? ksA[k] : ksB[k - ksplit]); scr[(2 * i + (lane >> 5)) * 33 + (lane & 31)] = x; }
;     LDS_WAIT(); asm volatile("" ::: "memory");
;     const int c = lane & 7;
; #pragma unroll
;     for (int j = 0; j < 4; ++j) { const int n = (lane >> 3) + 8 * j; const LAS float* s = scr + (8 * c) * 33 + n;
;         const unsigned long long o = (unsigned long long)pg8::pk4_fp8(s[0 * 33], s[1 * 33], s[2 * 33], s[3 * 33]) | ((unsigned long long)pg8::pk4_fp8(s[4 * 33], s[5 * 33], s[6 * 33], s[7 * 33]) << 32);
;         *(GAS unsigned long long*)(WT + (size_t)(n0 + n) * K + k0 + 8 * c) = o; }
;     LDS_WAIT(); asm volatile("" ::: "memory");
	s_add_i32 s17, s16, 1248
	s_min_u32 s17, s17, 0x7ff
	s_lshr_b32 s18, s17, 5
	s_add_i32 s18, s18, 0
	s_and_b32 s19, s17, 31
	s_lshl_b32 s18, s18, 21
	s_lshl_b32 s19, s19, 9
	s_add_u32 s18, s18, s19
	s_add_u32 s10, s2, s18
	s_addc_u32 s11, s3, 0
	global_load_dwordx4 v[68:71], v126, s[10:11]
	s_add_u32 s10, s10, 0x8000
	s_addc_u32 s11, s11, 0
	global_load_dwordx4 v[72:75], v126, s[10:11]
	s_add_u32 s10, s10, 0x8000
	s_addc_u32 s11, s11, 0
	global_load_dwordx4 v[76:79], v126, s[10:11]
	s_add_u32 s10, s10, 0x8000
	s_addc_u32 s11, s11, 0
	global_load_dwordx4 v[80:83], v126, s[10:11]
	s_add_u32 s10, s10, 0x8000
	s_addc_u32 s11, s11, 0
	global_load_dwordx4 v[84:87], v126, s[10:11]
	s_add_u32 s10, s10, 0x8000
	s_addc_u32 s11, s11, 0
	global_load_dwordx4 v[88:91], v126, s[10:11]
	s_add_u32 s10, s10, 0x8000
	s_addc_u32 s11, s11, 0
	global_load_dwordx4 v[92:95], v126, s[10:11]
	s_add_u32 s10, s10, 0x8000
	s_addc_u32 s11, s11, 0
	global_load_dwordx4 v[96:99], v126, s[10:11]
	s_add_i32 s17, s16, 1056
	s_min_u32 s17, s17, 0x7ff
	s_lshr_b32 s18, s17, 5
	s_add_i32 s18, s18, 0
	s_and_b32 s19, s17, 31
	s_lshl_b32 s19, s19, 21
	s_lshl_b32 s18, s18, 7
	s_add_u32 s18, s18, s19
	s_add_u32 s14, s4, s18
	s_addc_u32 s15, s5, 0
	ds_read_b32 v100, v123
	ds_read_b32 v101, v123 offset:512
	ds_read_b32 v102, v123 offset:1024
	ds_read_b32 v103, v123 offset:1536
	ds_read_b32 v104, v123 offset:2048
	ds_read_b32 v105, v123 offset:2560
	ds_read_b32 v106, v123 offset:3072
	ds_read_b32 v107, v123 offset:3584
	ds_read_b32 v108, v123 offset:4096
	ds_read_b32 v109, v123 offset:4608
	ds_read_b32 v110, v123 offset:5120
	ds_read_b32 v111, v123 offset:5632
	ds_read_b32 v112, v123 offset:6144
	ds_read_b32 v113, v123 offset:6656
	ds_read_b32 v114, v123 offset:7168
	ds_read_b32 v115, v123 offset:7680
	s_waitcnt lgkmcnt(0)
	v_max_f32_e32 v100, v100, v100
	v_max_f32_e32 v101, v101, v101
	v_max_f32_e32 v102, v102, v102
	v_max_f32_e32 v103, v103, v103
	v_max_f32_e32 v104, v104, v104
	v_max_f32_e32 v105, v105, v105
	v_max_f32_e32 v106, v106, v106
	v_max_f32_e32 v107, v107, v107
	v_max_f32_e32 v108, v108, v108
	v_max_f32_e32 v109, v109, v109
	v_max_f32_e32 v110, v110, v110
	v_max_f32_e32 v111, v111, v111
	v_max_f32_e32 v112, v112, v112
	v_max_f32_e32 v113, v113, v113
	v_max_f32_e32 v114, v114, v114
	v_max_f32_e32 v115, v115, v115
	v_med3_f32 v100, v100, s20, v129
	v_med3_f32 v101, v101, s20, v129
	v_med3_f32 v102, v102, s20, v129
	v_med3_f32 v103, v103, s20, v129
	v_med3_f32 v104, v104, s20, v129
	v_med3_f32 v105, v105, s20, v129
	v_med3_f32 v106, v106, s20, v129
	v_med3_f32 v107, v107, s20, v129
	v_med3_f32 v108, v108, s20, v129
	v_med3_f32 v109, v109, s20, v129
	v_med3_f32 v110, v110, s20, v129
	v_med3_f32 v111, v111, s20, v129
	v_med3_f32 v112, v112, s20, v129
	v_med3_f32 v113, v113, s20, v129
	v_med3_f32 v114, v114, s20, v129
	v_med3_f32 v115, v115, s20, v129
	v_mov_b32_e32 v116, 0
	v_mov_b32_e32 v117, 0
	v_mov_b32_e32 v118, 0
	v_mov_b32_e32 v119, 0
	v_cvt_pk_fp8_f32 v116, v100, v101
	v_cvt_pk_fp8_f32 v117, v104, v105
	v_cvt_pk_fp8_f32 v118, v108, v109
	v_cvt_pk_fp8_f32 v119, v112, v113
	v_cvt_pk_fp8_f32 v116, v102, v103 op_sel:[0,0,1]
	v_cvt_pk_fp8_f32 v117, v106, v107 op_sel:[0,0,1]
	v_cvt_pk_fp8_f32 v118, v110, v111 op_sel:[0,0,1]
	v_cvt_pk_fp8_f32 v119, v114, v115 op_sel:[0,0,1]
	s_nop 0
	global_store_dwordx4 v127, v[116:119], s[14:15]
	ds_read_b32 v100, v125
	ds_read_b32 v101, v125 offset:512
	ds_read_b32 v102, v125 offset:1024
	ds_read_b32 v103, v125 offset:1536
	ds_read_b32 v104, v125 offset:2048
	ds_read_b32 v105, v125 offset:2560
	ds_read_b32 v106, v125 offset:3072
	ds_read_b32 v107, v125 offset:3584
	ds_read_b32 v108, v125 offset:4096
	ds_read_b32 v109, v125 offset:4608
	ds_read_b32 v110, v125 offset:5120
	ds_read_b32 v111, v125 offset:5632
	ds_read_b32 v112, v125 offset:6144
	ds_read_b32 v113, v125 offset:6656
	ds_read_b32 v114, v125 offset:7168
	ds_read_b32 v115, v125 offset:7680
	s_waitcnt lgkmcnt(0)
	v_max_f32_e32 v100, v100, v100
	v_max_f32_e32 v101, v101, v101
	v_max_f32_e32 v102, v102, v102
	v_max_f32_e32 v103, v103, v103
	v_max_f32_e32 v104, v104, v104
	v_max_f32_e32 v105, v105, v105
	v_max_f32_e32 v106, v106, v106
	v_max_f32_e32 v107, v107, v107
	v_max_f32_e32 v108, v108, v108
	v_max_f32_e32 v109, v109, v109
	v_max_f32_e32 v110, v110, v110
	v_max_f32_e32 v111, v111, v111
	v_max_f32_e32 v112, v112, v112
	v_max_f32_e32 v113, v113, v113
	v_max_f32_e32 v114, v114, v114
	v_max_f32_e32 v115, v115, v115
	v_med3_f32 v100, v100, s20, v129
	v_med3_f32 v101, v101, s20, v129
	v_med3_f32 v102, v102, s20, v129
	v_med3_f32 v103, v103, s20, v129
	v_med3_f32 v104, v104, s20, v129
	v_med3_f32 v105, v105, s20, v129
	v_med3_f32 v106, v106, s20, v129
	v_med3_f32 v107, v107, s20, v129
	v_med3_f32 v108, v108, s20, v129
	v_med3_f32 v109, v109, s20, v129
	v_med3_f32 v110, v110, s20, v129
	v_med3_f32 v111, v111, s20, v129
	v_med3_f32 v112, v112, s20, v129
	v_med3_f32 v113, v113, s20, v129
	v_med3_f32 v114, v114, s20, v129
	v_med3_f32 v115, v115, s20, v129
	v_mov_b32_e32 v116, 0
	v_mov_b32_e32 v117, 0
	v_mov_b32_e32 v118, 0
	v_mov_b32_e32 v119, 0
	v_cvt_pk_fp8_f32 v116, v100, v101
	v_cvt_pk_fp8_f32 v117, v104, v105
	v_cvt_pk_fp8_f32 v118, v108, v109
	v_cvt_pk_fp8_f32 v119, v112, v113
	v_cvt_pk_fp8_f32 v116, v102, v103 op_sel:[0,0,1]
	v_cvt_pk_fp8_f32 v117, v106, v107 op_sel:[0,0,1]
	v_cvt_pk_fp8_f32 v118, v110, v111 op_sel:[0,0,1]
	v_cvt_pk_fp8_f32 v119, v114, v115 op_sel:[0,0,1]
	s_nop 0
	global_store_dwordx4 v128, v[116:119], s[14:15]
	s_waitcnt vmcnt(12)
	v_mul_f32_e32 v36, 0x43000000, v36
	v_mul_f32_e32 v37, 0x43000000, v37
	v_mul_f32_e32 v38, 0x43000000, v38
	v_mul_f32_e32 v39, 0x43000000, v39
	ds_write_b128 v120, v[36:39]
	v_mul_f32_e32 v40, 0x43000000, v40
	v_mul_f32_e32 v41, 0x43000000, v41
	v_mul_f32_e32 v42, 0x43000000, v42
	v_mul_f32_e32 v43, 0x43000000, v43
	ds_write_b128 v120, v[40:43] offset:1024
	v_mul_f32_e32 v44, 0x43000000, v44
	v_mul_f32_e32 v45, 0x43000000, v45
	v_mul_f32_e32 v46, 0x43000000, v46
	v_mul_f32_e32 v47, 0x43000000, v47
	ds_write_b128 v120, v[44:47] offset:2048
	v_mul_f32_e32 v48, 0x43000000, v48
	v_mul_f32_e32 v49, 0x43000000, v49
	v_mul_f32_e32 v50, 0x43000000, v50
	v_mul_f32_e32 v51, 0x43000000, v51
	ds_write_b128 v120, v[48:51] offset:3072
	v_mul_f32_e32 v52, 0x43000000, v52
	v_mul_f32_e32 v53, 0x43000000, v53
	v_mul_f32_e32 v54, 0x43000000, v54
	v_mul_f32_e32 v55, 0x43000000, v55
	ds_write_b128 v120, v[52:55] offset:4096
	v_mul_f32_e32 v56, 0x43000000, v56
	v_mul_f32_e32 v57, 0x43000000, v57
	v_mul_f32_e32 v58, 0x43000000, v58
	v_mul_f32_e32 v59, 0x43000000, v59
	ds_write_b128 v120, v[56:59] offset:5120
	v_mul_f32_e32 v60, 0x43000000, v60
	v_mul_f32_e32 v61, 0x43000000, v61
	v_mul_f32_e32 v62, 0x43000000, v62
	v_mul_f32_e32 v63, 0x43000000, v63
	ds_write_b128 v120, v[60:63] offset:6144
	v_mul_f32_e32 v64, 0x43000000, v64
	v_mul_f32_e32 v65, 0x43000000, v65
	v_mul_f32_e32 v66, 0x43000000, v66
	v_mul_f32_e32 v67, 0x43000000, v67
	ds_write_b128 v120, v[64:67] offset:7168
	s_waitcnt lgkmcnt(0)
	s_barrier
; #define GAS __attribute__((address_space(1)))
; #define LAS __attribute__((address_space(3)))
; #define LDS_WAIT() asm volatile("s_waitcnt lgkmcnt(0)" ::: "memory")
;     const int pr = item >> 1, kb = 2 * (pr / nblk) + (item & 1), nb = pr % nblk, k0 = 64 * kb, n0 = 32 * nb;
;     const int nr = n0 + (lane & 31); const int sc = MAP == 1 ? src_col_in(nr) : nr;
;     float v[32];
; #pragma unroll
;     for (int i = 0; i < 32; ++i) v[i] = sc >= 0 ? W[(size_t)(k0 + 2 * i + (lane >> 5)) * Nsrc + sc] : 0.f;
; #pragma unroll
;     for (int i = 0; i < 32; ++i) { const int k = k0 + 2 * i + (lane >> 5); float x = v[i] * wscale; if (KS) x *= (k < ksplit ? ksA[k] : ksB[k - ksplit]); scr[(2 * i + (lane >> 5)) * 33 + (lane & 31)] = x; }
;     LDS_WAIT(); asm volatile("" ::: "memory");
;     const int c = lane & 7;
; #pragma unroll
;     for (int j = 0; j < 4; ++j) { const int n = (lane >> 3) + 8 * j; const LAS float* s = scr + (8 * c) * 33 + n;
;         const unsigned long long o = (unsigned long long)pg8::pk4_fp8(s[0 * 33], s[1 * 33], s[2 * 33], s[3 * 33]) | ((unsigned long long)pg8::pk4_fp8(s[4 * 33], s[5 * 33], s[6 * 33], s[7 * 33]) << 32);
;         *(GAS unsigned long long*)(WT + (size_t)(n0 + n) * K + k0 + 8 * c) = o; }
;     LDS_WAIT(); asm volatile("" ::: "memory");
	s_add_i32 s17, s16, 1344
	s_min_u32 s17, s17, 0x7ff
	s_lshr_b32 s18, s17, 5
	s_add_i32 s18, s18, 0
	s_and_b32 s19, s17, 31
	s_lshl_b32 s18, s18, 21
	s_lshl_b32 s19, s19, 9
	s_add_u32 s18, s18, s19
	s_add_u32 s10, s2, s18
	s_addc_u32 s11, s3, 0
	global_load_dwordx4 v[36:39], v126, s[10:11]
	s_add_u32 s10, s10, 0x8000
	s_addc_u32 s11, s11, 0
	global_load_dwordx4 v[40:43], v126, s[10:11]
	s_add_u32 s10, s10, 0x8000
	s_addc_u32 s11, s11, 0
	global_load_dwordx4 v[44:47], v126, s[10:11]
	s_add_u32 s10, s10, 0x8000
	s_addc_u32 s11, s11, 0
	global_load_dwordx4 v[48:51], v126, s[10:11]
	s_add_u32 s10, s10, 0x8000
	s_addc_u32 s11, s11, 0
	global_load_dwordx4 v[52:55], v126, s[10:11]
	s_add_u32 s10, s10, 0x8000
	s_addc_u32 s11, s11, 0
	global_load_dwordx4 v[56:59], v126, s[10:11]
	s_add_u32 s10, s10, 0x8000
	s_addc_u32 s11, s11, 0
	global_load_dwordx4 v[60:63], v126, s[10:11]
	s_add_u32 s10, s10, 0x8000
	s_addc_u32 s11, s11, 0
	global_load_dwordx4 v[64:67], v126, s[10:11]
	s_add_i32 s17, s16, 1152
	s_min_u32 s17, s17, 0x7ff
	s_lshr_b32 s18, s17, 5
	s_add_i32 s18, s18, 0
	s_and_b32 s19, s17, 31
	s_lshl_b32 s19, s19, 21
	s_lshl_b32 s18, s18, 7
	s_add_u32 s18, s18, s19
	s_add_u32 s14, s4, s18
	s_addc_u32 s15, s5, 0
	ds_read_b32 v100, v122
	ds_read_b32 v101, v122 offset:512
	ds_read_b32 v102, v122 offset:1024
	ds_read_b32 v103, v122 offset:1536
	ds_read_b32 v104, v122 offset:2048
	ds_read_b32 v105, v122 offset:2560
	ds_read_b32 v106, v122 offset:3072
	ds_read_b32 v107, v122 offset:3584
	ds_read_b32 v108, v122 offset:4096
	ds_read_b32 v109, v122 offset:4608
	ds_read_b32 v110, v122 offset:5120
	ds_read_b32 v111, v122 offset:5632
	ds_read_b32 v112, v122 offset:6144
	ds_read_b32 v113, v122 offset:6656
	ds_read_b32 v114, v122 offset:7168
	ds_read_b32 v115, v122 offset:7680
	s_waitcnt lgkmcnt(0)
	v_max_f32_e32 v100, v100, v100
	v_max_f32_e32 v101, v101, v101
	v_max_f32_e32 v102, v102, v102
	v_max_f32_e32 v103, v103, v103
	v_max_f32_e32 v104, v104, v104
	v_max_f32_e32 v105, v105, v105
	v_max_f32_e32 v106, v106, v106
	v_max_f32_e32 v107, v107, v107
	v_max_f32_e32 v108, v108, v108
	v_max_f32_e32 v109, v109, v109
	v_max_f32_e32 v110, v110, v110
	v_max_f32_e32 v111, v111, v111
	v_max_f32_e32 v112, v112, v112
	v_max_f32_e32 v113, v113, v113
	v_max_f32_e32 v114, v114, v114
	v_max_f32_e32 v115, v115, v115
	v_med3_f32 v100, v100, s20, v129
	v_med3_f32 v101, v101, s20, v129
	v_med3_f32 v102, v102, s20, v129
	v_med3_f32 v103, v103, s20, v129
	v_med3_f32 v104, v104, s20, v129
	v_med3_f32 v105, v105, s20, v129
	v_med3_f32 v106, v106, s20, v129
	v_med3_f32 v107, v107, s20, v129
	v_med3_f32 v108, v108, s20, v129
	v_med3_f32 v109, v109, s20, v129
	v_med3_f32 v110, v110, s20, v129
	v_med3_f32 v111, v111, s20, v129
	v_med3_f32 v112, v112, s20, v129
	v_med3_f32 v113, v113, s20, v129
	v_med3_f32 v114, v114, s20, v129
	v_med3_f32 v115, v115, s20, v129
	v_mov_b32_e32 v116, 0
	v_mov_b32_e32 v117, 0
	v_mov_b32_e32 v118, 0
	v_mov_b32_e32 v119, 0
	v_cvt_pk_fp8_f32 v116, v100, v101
	v_cvt_pk_fp8_f32 v117, v104, v105
	v_cvt_pk_fp8_f32 v118, v108, v109
	v_cvt_pk_fp8_f32 v119, v112, v113
	v_cvt_pk_fp8_f32 v116, v102, v103 op_sel:[0,0,1]
	v_cvt_pk_fp8_f32 v117, v106, v107 op_sel:[0,0,1]
	v_cvt_pk_fp8_f32 v118, v110, v111 op_sel:[0,0,1]
	v_cvt_pk_fp8_f32 v119, v114, v115 op_sel:[0,0,1]
	s_nop 0
	global_store_dwordx4 v127, v[116:119], s[14:15]
	ds_read_b32 v100, v124
	ds_read_b32 v101, v124 offset:512
	ds_read_b32 v102, v124 offset:1024
	ds_read_b32 v103, v124 offset:1536
	ds_read_b32 v104, v124 offset:2048
	ds_read_b32 v105, v124 offset:2560
	ds_read_b32 v106, v124 offset:3072
	ds_read_b32 v107, v124 offset:3584
	ds_read_b32 v108, v124 offset:4096
	ds_read_b32 v109, v124 offset:4608
	ds_read_b32 v110, v124 offset:5120
	ds_read_b32 v111, v124 offset:5632
	ds_read_b32 v112, v124 offset:6144
	ds_read_b32 v113, v124 offset:6656
	ds_read_b32 v114, v124 offset:7168
	ds_read_b32 v115, v124 offset:7680
	s_waitcnt lgkmcnt(0)
	v_max_f32_e32 v100, v100, v100
	v_max_f32_e32 v101, v101, v101
	v_max_f32_e32 v102, v102, v102
	v_max_f32_e32 v103, v103, v103
	v_max_f32_e32 v104, v104, v104
	v_max_f32_e32 v105, v105, v105
	v_max_f32_e32 v106, v106, v106
	v_max_f32_e32 v107, v107, v107
	v_max_f32_e32 v108, v108, v108
	v_max_f32_e32 v109, v109, v109
	v_max_f32_e32 v110, v110, v110
	v_max_f32_e32 v111, v111, v111
	v_max_f32_e32 v112, v112, v112
	v_max_f32_e32 v113, v113, v113
	v_max_f32_e32 v114, v114, v114
	v_max_f32_e32 v115, v115, v115
	v_med3_f32 v100, v100, s20, v129
	v_med3_f32 v101, v101, s20, v129
	v_med3_f32 v102, v102, s20, v129
	v_med3_f32 v103, v103, s20, v129
	v_med3_f32 v104, v104, s20, v129
	v_med3_f32 v105, v105, s20, v129
	v_med3_f32 v106, v106, s20, v129
	v_med3_f32 v107, v107, s20, v129
	v_med3_f32 v108, v108, s20, v129
	v_med3_f32 v109, v109, s20, v129
	v_med3_f32 v110, v110, s20, v129
	v_med3_f32 v111, v111, s20, v129
	v_med3_f32 v112, v112, s20, v129
	v_med3_f32 v113, v113, s20, v129
	v_med3_f32 v114, v114, s20, v129
	v_med3_f32 v115, v115, s20, v129
	v_mov_b32_e32 v116, 0
	v_mov_b32_e32 v117, 0
	v_mov_b32_e32 v118, 0
	v_mov_b32_e32 v119, 0
	v_cvt_pk_fp8_f32 v116, v100, v101
	v_cvt_pk_fp8_f32 v117, v104, v105
	v_cvt_pk_fp8_f32 v118, v108, v109
	v_cvt_pk_fp8_f32 v119, v112, v113
	v_cvt_pk_fp8_f32 v116, v102, v103 op_sel:[0,0,1]
	v_cvt_pk_fp8_f32 v117, v106, v107 op_sel:[0,0,1]
	v_cvt_pk_fp8_f32 v118, v110, v111 op_sel:[0,0,1]
	v_cvt_pk_fp8_f32 v119, v114, v115 op_sel:[0,0,1]
	s_nop 0
	global_store_dwordx4 v128, v[116:119], s[14:15]
	s_waitcnt vmcnt(12)
	v_mul_f32_e32 v68, 0x43000000, v68
	v_mul_f32_e32 v69, 0x43000000, v69
	v_mul_f32_e32 v70, 0x43000000, v70
	v_mul_f32_e32 v71, 0x43000000, v71
	ds_write_b128 v121, v[68:71]
	v_mul_f32_e32 v72, 0x43000000, v72
	v_mul_f32_e32 v73, 0x43000000, v73
	v_mul_f32_e32 v74, 0x43000000, v74
	v_mul_f32_e32 v75, 0x43000000, v75
	ds_write_b128 v121, v[72:75] offset:1024
	v_mul_f32_e32 v76, 0x43000000, v76
	v_mul_f32_e32 v77, 0x43000000, v77
	v_mul_f32_e32 v78, 0x43000000, v78
	v_mul_f32_e32 v79, 0x43000000, v79
	ds_write_b128 v121, v[76:79] offset:2048
	v_mul_f32_e32 v80, 0x43000000, v80
	v_mul_f32_e32 v81, 0x43000000, v81
	v_mul_f32_e32 v82, 0x43000000, v82
	v_mul_f32_e32 v83, 0x43000000, v83
	ds_write_b128 v121, v[80:83] offset:3072
	v_mul_f32_e32 v84, 0x43000000, v84
	v_mul_f32_e32 v85, 0x43000000, v85
	v_mul_f32_e32 v86, 0x43000000, v86
	v_mul_f32_e32 v87, 0x43000000, v87
	ds_write_b128 v121, v[84:87] offset:4096
	v_mul_f32_e32 v88, 0x43000000, v88
	v_mul_f32_e32 v89, 0x43000000, v89
	v_mul_f32_e32 v90, 0x43000000, v90
	v_mul_f32_e32 v91, 0x43000000, v91
	ds_write_b128 v121, v[88:91] offset:5120
	v_mul_f32_e32 v92, 0x43000000, v92
	v_mul_f32_e32 v93, 0x43000000, v93
	v_mul_f32_e32 v94, 0x43000000, v94
	v_mul_f32_e32 v95, 0x43000000, v95
	ds_write_b128 v121, v[92:95] offset:6144
	v_mul_f32_e32 v96, 0x43000000, v96
	v_mul_f32_e32 v97, 0x43000000, v97
	v_mul_f32_e32 v98, 0x43000000, v98
	v_mul_f32_e32 v99, 0x43000000, v99
	ds_write_b128 v121, v[96:99] offset:7168
	s_waitcnt lgkmcnt(0)
	s_barrier
; #define GAS __attribute__((address_space(1)))
; #define LAS __attribute__((address_space(3)))
; #define LDS_WAIT() asm volatile("s_waitcnt lgkmcnt(0)" ::: "memory")
;     const int pr = item >> 1, kb = 2 * (pr / nblk) + (item & 1), nb = pr % nblk, k0 = 64 * kb, n0 = 32 * nb;
;     const int nr = n0 + (lane & 31); const int sc = MAP == 1 ? src_col_in(nr) : nr;
;     float v[32];
; #pragma unroll
;     for (int i = 0; i < 32; ++i) v[i] = sc >= 0 ? W[(size_t)(k0 + 2 * i + (lane >> 5)) * Nsrc + sc] : 0.f;
; #pragma unroll
;     for (int i = 0; i < 32; ++i) { const int k = k0 + 2 * i + (lane >> 5); float x = v[i] * wscale; if (KS) x *= (k < ksplit ? ksA[k] : ksB[k - ksplit]); scr[(2 * i + (lane >> 5)) * 33 + (lane & 31)] = x; }
;     LDS_WAIT(); asm volatile("" ::: "memory");
;     const int c = lane & 7;
; #pragma unroll
;     for (int j = 0; j < 4; ++j) { const int n = (lane >> 3) + 8 * j; const LAS float* s = scr + (8 * c) * 33 + n;
;         const unsigned long long o = (unsigned long long)pg8::pk4_fp8(s[0 * 33], s[1 * 33], s[2 * 33], s[3 * 33]) | ((unsigned long long)pg8::pk4_fp8(s[4 * 33], s[5 * 33], s[6 * 33], s[7 * 33]) << 32);
;         *(GAS unsigned long long*)(WT + (size_t)(n0 + n) * K + k0 + 8 * c) = o; }
;     LDS_WAIT(); asm volatile("" ::: "memory");
	s_add_i32 s17, s16, 1440
	s_min_u32 s17, s17, 0x7ff
	s_lshr_b32 s18, s17, 5
	s_add_i32 s18, s18, 0
	s_and_b32 s19, s17, 31
	s_lshl_b32 s18, s18, 21
	s_lshl_b32 s19, s19, 9
	s_add_u32 s18, s18, s19
	s_add_u32 s10, s2, s18
	s_addc_u32 s11, s3, 0
	global_load_dwordx4 v[68:71], v126, s[10:11]
	s_add_u32 s10, s10, 0x8000
	s_addc_u32 s11, s11, 0
	global_load_dwordx4 v[72:75], v126, s[10:11]
	s_add_u32 s10, s10, 0x8000
	s_addc_u32 s11, s11, 0
	global_load_dwordx4 v[76:79], v126, s[10:11]
	s_add_u32 s10, s10, 0x8000
	s_addc_u32 s11, s11, 0
	global_load_dwordx4 v[80:83], v126, s[10:11]
	s_add_u32 s10, s10, 0x8000
	s_addc_u32 s11, s11, 0
	global_load_dwordx4 v[84:87], v126, s[10:11]
	s_add_u32 s10, s10, 0x8000
	s_addc_u32 s11, s11, 0
	global_load_dwordx4 v[88:91], v126, s[10:11]
	s_add_u32 s10, s10, 0x8000
	s_addc_u32 s11, s11, 0
	global_load_dwordx4 v[92:95], v126, s[10:11]
	s_add_u32 s10, s10, 0x8000
	s_addc_u32 s11, s11, 0
	global_load_dwordx4 v[96:99], v126, s[10:11]
	s_add_i32 s17, s16, 1248
	s_min_u32 s17, s17, 0x7ff
	s_lshr_b32 s18, s17, 5
	s_add_i32 s18, s18, 0
	s_and_b32 s19, s17, 31
	s_lshl_b32 s19, s19, 21
	s_lshl_b32 s18, s18, 7
	s_add_u32 s18, s18, s19
	s_add_u32 s14, s4, s18
	s_addc_u32 s15, s5, 0
	ds_read_b32 v100, v123
	ds_read_b32 v101, v123 offset:512
	ds_read_b32 v102, v123 offset:1024
	ds_read_b32 v103, v123 offset:1536
	ds_read_b32 v104, v123 offset:2048
	ds_read_b32 v105, v123 offset:2560
	ds_read_b32 v106, v123 offset:3072
	ds_read_b32 v107, v123 offset:3584
	ds_read_b32 v108, v123 offset:4096
	ds_read_b32 v109, v123 offset:4608
	ds_read_b32 v110, v123 offset:5120
	ds_read_b32 v111, v123 offset:5632
	ds_read_b32 v112, v123 offset:6144
	ds_read_b32 v113, v123 offset:6656
	ds_read_b32 v114, v123 offset:7168
	ds_read_b32 v115, v123 offset:7680
	s_waitcnt lgkmcnt(0)
	v_max_f32_e32 v100, v100, v100
	v_max_f32_e32 v101, v101, v101
	v_max_f32_e32 v102, v102, v102
	v_max_f32_e32 v103, v103, v103
	v_max_f32_e32 v104, v104, v104
	v_max_f32_e32 v105, v105, v105
	v_max_f32_e32 v106, v106, v106
	v_max_f32_e32 v107, v107, v107
	v_max_f32_e32 v108, v108, v108
	v_max_f32_e32 v109, v109, v109
	v_max_f32_e32 v110, v110, v110
	v_max_f32_e32 v111, v111, v111
	v_max_f32_e32 v112, v112, v112
	v_max_f32_e32 v113, v113, v113
	v_max_f32_e32 v114, v114, v114
	v_max_f32_e32 v115, v115, v115
	v_med3_f32 v100, v100, s20, v129
	v_med3_f32 v101, v101, s20, v129
	v_med3_f32 v102, v102, s20, v129
	v_med3_f32 v103, v103, s20, v129
	v_med3_f32 v104, v104, s20, v129
	v_med3_f32 v105, v105, s20, v129
	v_med3_f32 v106, v106, s20, v129
	v_med3_f32 v107, v107, s20, v129
	v_med3_f32 v108, v108, s20, v129
	v_med3_f32 v109, v109, s20, v129
	v_med3_f32 v110, v110, s20, v129
	v_med3_f32 v111, v111, s20, v129
	v_med3_f32 v112, v112, s20, v129
	v_med3_f32 v113, v113, s20, v129
	v_med3_f32 v114, v114, s20, v129
	v_med3_f32 v115, v115, s20, v129
	v_mov_b32_e32 v116, 0
	v_mov_b32_e32 v117, 0
	v_mov_b32_e32 v118, 0
	v_mov_b32_e32 v119, 0
	v_cvt_pk_fp8_f32 v116, v100, v101
	v_cvt_pk_fp8_f32 v117, v104, v105
	v_cvt_pk_fp8_f32 v118, v108, v109
	v_cvt_pk_fp8_f32 v119, v112, v113
	v_cvt_pk_fp8_f32 v116, v102, v103 op_sel:[0,0,1]
	v_cvt_pk_fp8_f32 v117, v106, v107 op_sel:[0,0,1]
	v_cvt_pk_fp8_f32 v118, v110, v111 op_sel:[0,0,1]
	v_cvt_pk_fp8_f32 v119, v114, v115 op_sel:[0,0,1]
	s_nop 0
	global_store_dwordx4 v127, v[116:119], s[14:15]
	ds_read_b32 v100, v125
	ds_read_b32 v101, v125 offset:512
	ds_read_b32 v102, v125 offset:1024
	ds_read_b32 v103, v125 offset:1536
	ds_read_b32 v104, v125 offset:2048
	ds_read_b32 v105, v125 offset:2560
	ds_read_b32 v106, v125 offset:3072
	ds_read_b32 v107, v125 offset:3584
	ds_read_b32 v108, v125 offset:4096
	ds_read_b32 v109, v125 offset:4608
	ds_read_b32 v110, v125 offset:5120
	ds_read_b32 v111, v125 offset:5632
	ds_read_b32 v112, v125 offset:6144
	ds_read_b32 v113, v125 offset:6656
	ds_read_b32 v114, v125 offset:7168
	ds_read_b32 v115, v125 offset:7680
	s_waitcnt lgkmcnt(0)
	v_max_f32_e32 v100, v100, v100
	v_max_f32_e32 v101, v101, v101
	v_max_f32_e32 v102, v102, v102
	v_max_f32_e32 v103, v103, v103
	v_max_f32_e32 v104, v104, v104
	v_max_f32_e32 v105, v105, v105
	v_max_f32_e32 v106, v106, v106
	v_max_f32_e32 v107, v107, v107
	v_max_f32_e32 v108, v108, v108
	v_max_f32_e32 v109, v109, v109
	v_max_f32_e32 v110, v110, v110
	v_max_f32_e32 v111, v111, v111
	v_max_f32_e32 v112, v112, v112
	v_max_f32_e32 v113, v113, v113
	v_max_f32_e32 v114, v114, v114
	v_max_f32_e32 v115, v115, v115
	v_med3_f32 v100, v100, s20, v129
	v_med3_f32 v101, v101, s20, v129
	v_med3_f32 v102, v102, s20, v129
	v_med3_f32 v103, v103, s20, v129
	v_med3_f32 v104, v104, s20, v129
	v_med3_f32 v105, v105, s20, v129
	v_med3_f32 v106, v106, s20, v129
	v_med3_f32 v107, v107, s20, v129
	v_med3_f32 v108, v108, s20, v129
	v_med3_f32 v109, v109, s20, v129
	v_med3_f32 v110, v110, s20, v129
	v_med3_f32 v111, v111, s20, v129
	v_med3_f32 v112, v112, s20, v129
	v_med3_f32 v113, v113, s20, v129
	v_med3_f32 v114, v114, s20, v129
	v_med3_f32 v115, v115, s20, v129
	v_mov_b32_e32 v116, 0
	v_mov_b32_e32 v117, 0
	v_mov_b32_e32 v118, 0
	v_mov_b32_e32 v119, 0
	v_cvt_pk_fp8_f32 v116, v100, v101
	v_cvt_pk_fp8_f32 v117, v104, v105
	v_cvt_pk_fp8_f32 v118, v108, v109
	v_cvt_pk_fp8_f32 v119, v112, v113
	v_cvt_pk_fp8_f32 v116, v102, v103 op_sel:[0,0,1]
	v_cvt_pk_fp8_f32 v117, v106, v107 op_sel:[0,0,1]
	v_cvt_pk_fp8_f32 v118, v110, v111 op_sel:[0,0,1]
	v_cvt_pk_fp8_f32 v119, v114, v115 op_sel:[0,0,1]
	s_nop 0
	global_store_dwordx4 v128, v[116:119], s[14:15]
	s_waitcnt vmcnt(12)
	v_mul_f32_e32 v36, 0x43000000, v36
	v_mul_f32_e32 v37, 0x43000000, v37
	v_mul_f32_e32 v38, 0x43000000, v38
	v_mul_f32_e32 v39, 0x43000000, v39
	ds_write_b128 v120, v[36:39]
	v_mul_f32_e32 v40, 0x43000000, v40
	v_mul_f32_e32 v41, 0x43000000, v41
	v_mul_f32_e32 v42, 0x43000000, v42
	v_mul_f32_e32 v43, 0x43000000, v43
	ds_write_b128 v120, v[40:43] offset:1024
	v_mul_f32_e32 v44, 0x43000000, v44
	v_mul_f32_e32 v45, 0x43000000, v45
	v_mul_f32_e32 v46, 0x43000000, v46
	v_mul_f32_e32 v47, 0x43000000, v47
	ds_write_b128 v120, v[44:47] offset:2048
	v_mul_f32_e32 v48, 0x43000000, v48
	v_mul_f32_e32 v49, 0x43000000, v49
	v_mul_f32_e32 v50, 0x43000000, v50
	v_mul_f32_e32 v51, 0x43000000, v51
	ds_write_b128 v120, v[48:51] offset:3072
	v_mul_f32_e32 v52, 0x43000000, v52
	v_mul_f32_e32 v53, 0x43000000, v53
	v_mul_f32_e32 v54, 0x43000000, v54
	v_mul_f32_e32 v55, 0x43000000, v55
	ds_write_b128 v120, v[52:55] offset:4096
	v_mul_f32_e32 v56, 0x43000000, v56
	v_mul_f32_e32 v57, 0x43000000, v57
	v_mul_f32_e32 v58, 0x43000000, v58
	v_mul_f32_e32 v59, 0x43000000, v59
	ds_write_b128 v120, v[56:59] offset:5120
	v_mul_f32_e32 v60, 0x43000000, v60
	v_mul_f32_e32 v61, 0x43000000, v61
	v_mul_f32_e32 v62, 0x43000000, v62
	v_mul_f32_e32 v63, 0x43000000, v63
	ds_write_b128 v120, v[60:63] offset:6144
	v_mul_f32_e32 v64, 0x43000000, v64
	v_mul_f32_e32 v65, 0x43000000, v65
	v_mul_f32_e32 v66, 0x43000000, v66
	v_mul_f32_e32 v67, 0x43000000, v67
	ds_write_b128 v120, v[64:67] offset:7168
	s_waitcnt lgkmcnt(0)
	s_barrier
; #define GAS __attribute__((address_space(1)))
; #define LAS __attribute__((address_space(3)))
; #define LDS_WAIT() asm volatile("s_waitcnt lgkmcnt(0)" ::: "memory")
;     const int pr = item >> 1, kb = 2 * (pr / nblk) + (item & 1), nb = pr % nblk, k0 = 64 * kb, n0 = 32 * nb;
;     const int nr = n0 + (lane & 31); const int sc = MAP == 1 ? src_col_in(nr) : nr;
;     float v[32];
; #pragma unroll
;     for (int i = 0; i < 32; ++i) v[i] = sc >= 0 ? W[(size_t)(k0 + 2 * i + (lane >> 5)) * Nsrc + sc] : 0.f;
; #pragma unroll
;     for (int i = 0; i < 32; ++i) { const int k = k0 + 2 * i + (lane >> 5); float x = v[i] * wscale; if (KS) x *= (k < ksplit ? ksA[k] : ksB[k - ksplit]); scr[(2 * i + (lane >> 5)) * 33 + (lane & 31)] = x; }
;     LDS_WAIT(); asm volatile("" ::: "memory");
;     const int c = lane & 7;
; #pragma unroll
;     for (int j = 0; j < 4; ++j) { const int n = (lane >> 3) + 8 * j; const LAS float* s = scr + (8 * c) * 33 + n;
;         const unsigned long long o = (unsigned long long)pg8::pk4_fp8(s[0 * 33], s[1 * 33], s[2 * 33], s[3 * 33]) | ((unsigned long long)pg8::pk4_fp8(s[4 * 33], s[5 * 33], s[6 * 33], s[7 * 33]) << 32);
;         *(GAS unsigned long long*)(WT + (size_t)(n0 + n) * K + k0 + 8 * c) = o; }
;     LDS_WAIT(); asm volatile("" ::: "memory");
	s_add_i32 s17, s16, 1536
	s_min_u32 s17, s17, 0x7ff
	s_lshr_b32 s18, s17, 5
	s_add_i32 s18, s18, 0
	s_and_b32 s19, s17, 31
	s_lshl_b32 s18, s18, 21
	s_lshl_b32 s19, s19, 9
	s_add_u32 s18, s18, s19
	s_add_u32 s10, s2, s18
	s_addc_u32 s11, s3, 0
	global_load_dwordx4 v[36:39], v126, s[10:11]
	s_add_u32 s10, s10, 0x8000
	s_addc_u32 s11, s11, 0
	global_load_dwordx4 v[40:43], v126, s[10:11]
	s_add_u32 s10, s10, 0x8000
	s_addc_u32 s11, s11, 0
	global_load_dwordx4 v[44:47], v126, s[10:11]
	s_add_u32 s10, s10, 0x8000
	s_addc_u32 s11, s11, 0
	global_load_dwordx4 v[48:51], v126, s[10:11]
	s_add_u32 s10, s10, 0x8000
	s_addc_u32 s11, s11, 0
	global_load_dwordx4 v[52:55], v126, s[10:11]
	s_add_u32 s10, s10, 0x8000
	s_addc_u32 s11, s11, 0
	global_load_dwordx4 v[56:59], v126, s[10:11]
	s_add_u32 s10, s10, 0x8000
	s_addc_u32 s11, s11, 0
	global_load_dwordx4 v[60:63], v126, s[10:11]
	s_add_u32 s10, s10, 0x8000
	s_addc_u32 s11, s11, 0
	global_load_dwordx4 v[64:67], v126, s[10:11]
	s_add_i32 s17, s16, 1344
	s_min_u32 s17, s17, 0x7ff
	s_lshr_b32 s18, s17, 5
	s_add_i32 s18, s18, 0
	s_and_b32 s19, s17, 31
	s_lshl_b32 s19, s19, 21
	s_lshl_b32 s18, s18, 7
	s_add_u32 s18, s18, s19
	s_add_u32 s14, s4, s18
	s_addc_u32 s15, s5, 0
	ds_read_b32 v100, v122
	ds_read_b32 v101, v122 offset:512
	ds_read_b32 v102, v122 offset:1024
	ds_read_b32 v103, v122 offset:1536
	ds_read_b32 v104, v122 offset:2048
	ds_read_b32 v105, v122 offset:2560
	ds_read_b32 v106, v122 offset:3072
	ds_read_b32 v107, v122 offset:3584
	ds_read_b32 v108, v122 offset:4096
	ds_read_b32 v109, v122 offset:4608
	ds_read_b32 v110, v122 offset:5120
	ds_read_b32 v111, v122 offset:5632
	ds_read_b32 v112, v122 offset:6144
	ds_read_b32 v113, v122 offset:6656
	ds_read_b32 v114, v122 offset:7168
	ds_read_b32 v115, v122 offset:7680
	s_waitcnt lgkmcnt(0)
	v_max_f32_e32 v100, v100, v100
	v_max_f32_e32 v101, v101, v101
	v_max_f32_e32 v102, v102, v102
	v_max_f32_e32 v103, v103, v103
	v_max_f32_e32 v104, v104, v104
	v_max_f32_e32 v105, v105, v105
	v_max_f32_e32 v106, v106, v106
	v_max_f32_e32 v107, v107, v107
	v_max_f32_e32 v108, v108, v108
	v_max_f32_e32 v109, v109, v109
	v_max_f32_e32 v110, v110, v110
	v_max_f32_e32 v111, v111, v111
	v_max_f32_e32 v112, v112, v112
	v_max_f32_e32 v113, v113, v113
	v_max_f32_e32 v114, v114, v114
	v_max_f32_e32 v115, v115, v115
	v_med3_f32 v100, v100, s20, v129
	v_med3_f32 v101, v101, s20, v129
	v_med3_f32 v102, v102, s20, v129
	v_med3_f32 v103, v103, s20, v129
	v_med3_f32 v104, v104, s20, v129
	v_med3_f32 v105, v105, s20, v129
	v_med3_f32 v106, v106, s20, v129
	v_med3_f32 v107, v107, s20, v129
	v_med3_f32 v108, v108, s20, v129
	v_med3_f32 v109, v109, s20, v129
	v_med3_f32 v110, v110, s20, v129
	v_med3_f32 v111, v111, s20, v129
	v_med3_f32 v112, v112, s20, v129
	v_med3_f32 v113, v113, s20, v129
	v_med3_f32 v114, v114, s20, v129
	v_med3_f32 v115, v115, s20, v129
	v_mov_b32_e32 v116, 0
	v_mov_b32_e32 v117, 0
	v_mov_b32_e32 v118, 0
	v_mov_b32_e32 v119, 0
	v_cvt_pk_fp8_f32 v116, v100, v101
	v_cvt_pk_fp8_f32 v117, v104, v105
	v_cvt_pk_fp8_f32 v118, v108, v109
	v_cvt_pk_fp8_f32 v119, v112, v113
	v_cvt_pk_fp8_f32 v116, v102, v103 op_sel:[0,0,1]
	v_cvt_pk_fp8_f32 v117, v106, v107 op_sel:[0,0,1]
	v_cvt_pk_fp8_f32 v118, v110, v111 op_sel:[0,0,1]
	v_cvt_pk_fp8_f32 v119, v114, v115 op_sel:[0,0,1]
	s_nop 0
	global_store_dwordx4 v127, v[116:119], s[14:15]
	ds_read_b32 v100, v124
	ds_read_b32 v101, v124 offset:512
	ds_read_b32 v102, v124 offset:1024
	ds_read_b32 v103, v124 offset:1536
	ds_read_b32 v104, v124 offset:2048
	ds_read_b32 v105, v124 offset:2560
	ds_read_b32 v106, v124 offset:3072
	ds_read_b32 v107, v124 offset:3584
	ds_read_b32 v108, v124 offset:4096
	ds_read_b32 v109, v124 offset:4608
	ds_read_b32 v110, v124 offset:5120
	ds_read_b32 v111, v124 offset:5632
	ds_read_b32 v112, v124 offset:6144
	ds_read_b32 v113, v124 offset:6656
	ds_read_b32 v114, v124 offset:7168
	ds_read_b32 v115, v124 offset:7680
	s_waitcnt lgkmcnt(0)
	v_max_f32_e32 v100, v100, v100
	v_max_f32_e32 v101, v101, v101
	v_max_f32_e32 v102, v102, v102
	v_max_f32_e32 v103, v103, v103
	v_max_f32_e32 v104, v104, v104
	v_max_f32_e32 v105, v105, v105
	v_max_f32_e32 v106, v106, v106
	v_max_f32_e32 v107, v107, v107
	v_max_f32_e32 v108, v108, v108
	v_max_f32_e32 v109, v109, v109
	v_max_f32_e32 v110, v110, v110
	v_max_f32_e32 v111, v111, v111
	v_max_f32_e32 v112, v112, v112
	v_max_f32_e32 v113, v113, v113
	v_max_f32_e32 v114, v114, v114
	v_max_f32_e32 v115, v115, v115
	v_med3_f32 v100, v100, s20, v129
	v_med3_f32 v101, v101, s20, v129
	v_med3_f32 v102, v102, s20, v129
	v_med3_f32 v103, v103, s20, v129
	v_med3_f32 v104, v104, s20, v129
	v_med3_f32 v105, v105, s20, v129
	v_med3_f32 v106, v106, s20, v129
	v_med3_f32 v107, v107, s20, v129
	v_med3_f32 v108, v108, s20, v129
	v_med3_f32 v109, v109, s20, v129
	v_med3_f32 v110, v110, s20, v129
	v_med3_f32 v111, v111, s20, v129
	v_med3_f32 v112, v112, s20, v129
	v_med3_f32 v113, v113, s20, v129
	v_med3_f32 v114, v114, s20, v129
	v_med3_f32 v115, v115, s20, v129
	v_mov_b32_e32 v116, 0
	v_mov_b32_e32 v117, 0
	v_mov_b32_e32 v118, 0
	v_mov_b32_e32 v119, 0
	v_cvt_pk_fp8_f32 v116, v100, v101
	v_cvt_pk_fp8_f32 v117, v104, v105
	v_cvt_pk_fp8_f32 v118, v108, v109
	v_cvt_pk_fp8_f32 v119, v112, v113
	v_cvt_pk_fp8_f32 v116, v102, v103 op_sel:[0,0,1]
	v_cvt_pk_fp8_f32 v117, v106, v107 op_sel:[0,0,1]
	v_cvt_pk_fp8_f32 v118, v110, v111 op_sel:[0,0,1]
	v_cvt_pk_fp8_f32 v119, v114, v115 op_sel:[0,0,1]
	s_nop 0
	global_store_dwordx4 v128, v[116:119], s[14:15]
	s_waitcnt vmcnt(12)
	v_mul_f32_e32 v68, 0x43000000, v68
	v_mul_f32_e32 v69, 0x43000000, v69
	v_mul_f32_e32 v70, 0x43000000, v70
	v_mul_f32_e32 v71, 0x43000000, v71
	ds_write_b128 v121, v[68:71]
	v_mul_f32_e32 v72, 0x43000000, v72
	v_mul_f32_e32 v73, 0x43000000, v73
	v_mul_f32_e32 v74, 0x43000000, v74
	v_mul_f32_e32 v75, 0x43000000, v75
	ds_write_b128 v121, v[72:75] offset:1024
	v_mul_f32_e32 v76, 0x43000000, v76
	v_mul_f32_e32 v77, 0x43000000, v77
	v_mul_f32_e32 v78, 0x43000000, v78
	v_mul_f32_e32 v79, 0x43000000, v79
	ds_write_b128 v121, v[76:79] offset:2048
	v_mul_f32_e32 v80, 0x43000000, v80
	v_mul_f32_e32 v81, 0x43000000, v81
	v_mul_f32_e32 v82, 0x43000000, v82
	v_mul_f32_e32 v83, 0x43000000, v83
	ds_write_b128 v121, v[80:83] offset:3072
	v_mul_f32_e32 v84, 0x43000000, v84
	v_mul_f32_e32 v85, 0x43000000, v85
	v_mul_f32_e32 v86, 0x43000000, v86
	v_mul_f32_e32 v87, 0x43000000, v87
	ds_write_b128 v121, v[84:87] offset:4096
	v_mul_f32_e32 v88, 0x43000000, v88
	v_mul_f32_e32 v89, 0x43000000, v89
	v_mul_f32_e32 v90, 0x43000000, v90
	v_mul_f32_e32 v91, 0x43000000, v91
	ds_write_b128 v121, v[88:91] offset:5120
	v_mul_f32_e32 v92, 0x43000000, v92
	v_mul_f32_e32 v93, 0x43000000, v93
	v_mul_f32_e32 v94, 0x43000000, v94
	v_mul_f32_e32 v95, 0x43000000, v95
	ds_write_b128 v121, v[92:95] offset:6144
	v_mul_f32_e32 v96, 0x43000000, v96
	v_mul_f32_e32 v97, 0x43000000, v97
	v_mul_f32_e32 v98, 0x43000000, v98
	v_mul_f32_e32 v99, 0x43000000, v99
	ds_write_b128 v121, v[96:99] offset:7168
	s_waitcnt lgkmcnt(0)
	s_barrier
; #define GAS __attribute__((address_space(1)))
; #define LAS __attribute__((address_space(3)))
; #define LDS_WAIT() asm volatile("s_waitcnt lgkmcnt(0)" ::: "memory")
;     const int pr = item >> 1, kb = 2 * (pr / nblk) + (item & 1), nb = pr % nblk, k0 = 64 * kb, n0 = 32 * nb;
;     const int nr = n0 + (lane & 31); const int sc = MAP == 1 ? src_col_in(nr) : nr;
;     float v[32];
; #pragma unroll
;     for (int i = 0; i < 32; ++i) v[i] = sc >= 0 ? W[(size_t)(k0 + 2 * i + (lane >> 5)) * Nsrc + sc] : 0.f;
; #pragma unroll
;     for (int i = 0; i < 32; ++i) { const int k = k0 + 2 * i + (lane >> 5); float x = v[i] * wscale; if (KS) x *= (k < ksplit ? ksA[k] : ksB[k - ksplit]); scr[(2 * i + (lane >> 5)) * 33 + (lane & 31)] = x; }
;     LDS_WAIT(); asm volatile("" ::: "memory");
;     const int c = lane & 7;
; #pragma unroll
;     for (int j = 0; j < 4; ++j) { const int n = (lane >> 3) + 8 * j; const LAS float* s = scr + (8 * c) * 33 + n;
;         const unsigned long long o = (unsigned long long)pg8::pk4_fp8(s[0 * 33], s[1 * 33], s[2 * 33], s[3 * 33]) | ((unsigned long long)pg8::pk4_fp8(s[4 * 33], s[5 * 33], s[6 * 33], s[7 * 33]) << 32);
;         *(GAS unsigned long long*)(WT + (size_t)(n0 + n) * K + k0 + 8 * c) = o; }
;     LDS_WAIT(); asm volatile("" ::: "memory");
	s_add_i32 s17, s16, 1632
	s_min_u32 s17, s17, 0x7ff
	s_lshr_b32 s18, s17, 5
	s_add_i32 s18, s18, 0
	s_and_b32 s19, s17, 31
	s_lshl_b32 s18, s18, 21
	s_lshl_b32 s19, s19, 9
	s_add_u32 s18, s18, s19
	s_add_u32 s10, s2, s18
	s_addc_u32 s11, s3, 0
	global_load_dwordx4 v[68:71], v126, s[10:11]
	s_add_u32 s10, s10, 0x8000
	s_addc_u32 s11, s11, 0
	global_load_dwordx4 v[72:75], v126, s[10:11]
	s_add_u32 s10, s10, 0x8000
	s_addc_u32 s11, s11, 0
	global_load_dwordx4 v[76:79], v126, s[10:11]
	s_add_u32 s10, s10, 0x8000
	s_addc_u32 s11, s11, 0
	global_load_dwordx4 v[80:83], v126, s[10:11]
	s_add_u32 s10, s10, 0x8000
	s_addc_u32 s11, s11, 0
	global_load_dwordx4 v[84:87], v126, s[10:11]
	s_add_u32 s10, s10, 0x8000
	s_addc_u32 s11, s11, 0
	global_load_dwordx4 v[88:91], v126, s[10:11]
	s_add_u32 s10, s10, 0x8000
	s_addc_u32 s11, s11, 0
	global_load_dwordx4 v[92:95], v126, s[10:11]
	s_add_u32 s10, s10, 0x8000
	s_addc_u32 s11, s11, 0
	global_load_dwordx4 v[96:99], v126, s[10:11]
	s_add_i32 s17, s16, 1440
	s_min_u32 s17, s17, 0x7ff
	s_lshr_b32 s18, s17, 5
	s_add_i32 s18, s18, 0
	s_and_b32 s19, s17, 31
	s_lshl_b32 s19, s19, 21
	s_lshl_b32 s18, s18, 7
	s_add_u32 s18, s18, s19
	s_add_u32 s14, s4, s18
	s_addc_u32 s15, s5, 0
	ds_read_b32 v100, v123
	ds_read_b32 v101, v123 offset:512
	ds_read_b32 v102, v123 offset:1024
	ds_read_b32 v103, v123 offset:1536
	ds_read_b32 v104, v123 offset:2048
	ds_read_b32 v105, v123 offset:2560
	ds_read_b32 v106, v123 offset:3072
	ds_read_b32 v107, v123 offset:3584
	ds_read_b32 v108, v123 offset:4096
	ds_read_b32 v109, v123 offset:4608
	ds_read_b32 v110, v123 offset:5120
	ds_read_b32 v111, v123 offset:5632
	ds_read_b32 v112, v123 offset:6144
	ds_read_b32 v113, v123 offset:6656
	ds_read_b32 v114, v123 offset:7168
	ds_read_b32 v115, v123 offset:7680
	s_waitcnt lgkmcnt(0)
	v_max_f32_e32 v100, v100, v100
	v_max_f32_e32 v101, v101, v101
	v_max_f32_e32 v102, v102, v102
	v_max_f32_e32 v103, v103, v103
	v_max_f32_e32 v104, v104, v104
	v_max_f32_e32 v105, v105, v105
	v_max_f32_e32 v106, v106, v106
	v_max_f32_e32 v107, v107, v107
	v_max_f32_e32 v108, v108, v108
	v_max_f32_e32 v109, v109, v109
	v_max_f32_e32 v110, v110, v110
	v_max_f32_e32 v111, v111, v111
	v_max_f32_e32 v112, v112, v112
	v_max_f32_e32 v113, v113, v113
	v_max_f32_e32 v114, v114, v114
	v_max_f32_e32 v115, v115, v115
	v_med3_f32 v100, v100, s20, v129
	v_med3_f32 v101, v101, s20, v129
	v_med3_f32 v102, v102, s20, v129
	v_med3_f32 v103, v103, s20, v129
	v_med3_f32 v104, v104, s20, v129
	v_med3_f32 v105, v105, s20, v129
	v_med3_f32 v106, v106, s20, v129
	v_med3_f32 v107, v107, s20, v129
	v_med3_f32 v108, v108, s20, v129
	v_med3_f32 v109, v109, s20, v129
	v_med3_f32 v110, v110, s20, v129
	v_med3_f32 v111, v111, s20, v129
	v_med3_f32 v112, v112, s20, v129
	v_med3_f32 v113, v113, s20, v129
	v_med3_f32 v114, v114, s20, v129
	v_med3_f32 v115, v115, s20, v129
	v_mov_b32_e32 v116, 0
	v_mov_b32_e32 v117, 0
	v_mov_b32_e32 v118, 0
	v_mov_b32_e32 v119, 0
	v_cvt_pk_fp8_f32 v116, v100, v101
	v_cvt_pk_fp8_f32 v117, v104, v105
	v_cvt_pk_fp8_f32 v118, v108, v109
	v_cvt_pk_fp8_f32 v119, v112, v113
	v_cvt_pk_fp8_f32 v116, v102, v103 op_sel:[0,0,1]
	v_cvt_pk_fp8_f32 v117, v106, v107 op_sel:[0,0,1]
	v_cvt_pk_fp8_f32 v118, v110, v111 op_sel:[0,0,1]
	v_cvt_pk_fp8_f32 v119, v114, v115 op_sel:[0,0,1]
	s_nop 0
	global_store_dwordx4 v127, v[116:119], s[14:15]
	ds_read_b32 v100, v125
	ds_read_b32 v101, v125 offset:512
	ds_read_b32 v102, v125 offset:1024
	ds_read_b32 v103, v125 offset:1536
	ds_read_b32 v104, v125 offset:2048
	ds_read_b32 v105, v125 offset:2560
	ds_read_b32 v106, v125 offset:3072
	ds_read_b32 v107, v125 offset:3584
	ds_read_b32 v108, v125 offset:4096
	ds_read_b32 v109, v125 offset:4608
	ds_read_b32 v110, v125 offset:5120
	ds_read_b32 v111, v125 offset:5632
	ds_read_b32 v112, v125 offset:6144
	ds_read_b32 v113, v125 offset:6656
	ds_read_b32 v114, v125 offset:7168
	ds_read_b32 v115, v125 offset:7680
	s_waitcnt lgkmcnt(0)
	v_max_f32_e32 v100, v100, v100
	v_max_f32_e32 v101, v101, v101
	v_max_f32_e32 v102, v102, v102
	v_max_f32_e32 v103, v103, v103
	v_max_f32_e32 v104, v104, v104
	v_max_f32_e32 v105, v105, v105
	v_max_f32_e32 v106, v106, v106
	v_max_f32_e32 v107, v107, v107
	v_max_f32_e32 v108, v108, v108
	v_max_f32_e32 v109, v109, v109
	v_max_f32_e32 v110, v110, v110
	v_max_f32_e32 v111, v111, v111
	v_max_f32_e32 v112, v112, v112
	v_max_f32_e32 v113, v113, v113
	v_max_f32_e32 v114, v114, v114
	v_max_f32_e32 v115, v115, v115
	v_med3_f32 v100, v100, s20, v129
	v_med3_f32 v101, v101, s20, v129
	v_med3_f32 v102, v102, s20, v129
	v_med3_f32 v103, v103, s20, v129
	v_med3_f32 v104, v104, s20, v129
	v_med3_f32 v105, v105, s20, v129
	v_med3_f32 v106, v106, s20, v129
	v_med3_f32 v107, v107, s20, v129
	v_med3_f32 v108, v108, s20, v129
	v_med3_f32 v109, v109, s20, v129
	v_med3_f32 v110, v110, s20, v129
	v_med3_f32 v111, v111, s20, v129
	v_med3_f32 v112, v112, s20, v129
	v_med3_f32 v113, v113, s20, v129
	v_med3_f32 v114, v114, s20, v129
	v_med3_f32 v115, v115, s20, v129
	v_mov_b32_e32 v116, 0
	v_mov_b32_e32 v117, 0
	v_mov_b32_e32 v118, 0
	v_mov_b32_e32 v119, 0
	v_cvt_pk_fp8_f32 v116, v100, v101
	v_cvt_pk_fp8_f32 v117, v104, v105
	v_cvt_pk_fp8_f32 v118, v108, v109
	v_cvt_pk_fp8_f32 v119, v112, v113
	v_cvt_pk_fp8_f32 v116, v102, v103 op_sel:[0,0,1]
	v_cvt_pk_fp8_f32 v117, v106, v107 op_sel:[0,0,1]
	v_cvt_pk_fp8_f32 v118, v110, v111 op_sel:[0,0,1]
	v_cvt_pk_fp8_f32 v119, v114, v115 op_sel:[0,0,1]
	s_nop 0
	global_store_dwordx4 v128, v[116:119], s[14:15]
	s_waitcnt vmcnt(12)
	v_mul_f32_e32 v36, 0x43000000, v36
	v_mul_f32_e32 v37, 0x43000000, v37
	v_mul_f32_e32 v38, 0x43000000, v38
	v_mul_f32_e32 v39, 0x43000000, v39
	ds_write_b128 v120, v[36:39]
	v_mul_f32_e32 v40, 0x43000000, v40
	v_mul_f32_e32 v41, 0x43000000, v41
	v_mul_f32_e32 v42, 0x43000000, v42
	v_mul_f32_e32 v43, 0x43000000, v43
	ds_write_b128 v120, v[40:43] offset:1024
	v_mul_f32_e32 v44, 0x43000000, v44
	v_mul_f32_e32 v45, 0x43000000, v45
	v_mul_f32_e32 v46, 0x43000000, v46
	v_mul_f32_e32 v47, 0x43000000, v47
	ds_write_b128 v120, v[44:47] offset:2048
	v_mul_f32_e32 v48, 0x43000000, v48
	v_mul_f32_e32 v49, 0x43000000, v49
	v_mul_f32_e32 v50, 0x43000000, v50
	v_mul_f32_e32 v51, 0x43000000, v51
	ds_write_b128 v120, v[48:51] offset:3072
	v_mul_f32_e32 v52, 0x43000000, v52
	v_mul_f32_e32 v53, 0x43000000, v53
	v_mul_f32_e32 v54, 0x43000000, v54
	v_mul_f32_e32 v55, 0x43000000, v55
	ds_write_b128 v120, v[52:55] offset:4096
	v_mul_f32_e32 v56, 0x43000000, v56
	v_mul_f32_e32 v57, 0x43000000, v57
	v_mul_f32_e32 v58, 0x43000000, v58
	v_mul_f32_e32 v59, 0x43000000, v59
	ds_write_b128 v120, v[56:59] offset:5120
	v_mul_f32_e32 v60, 0x43000000, v60
	v_mul_f32_e32 v61, 0x43000000, v61
	v_mul_f32_e32 v62, 0x43000000, v62
	v_mul_f32_e32 v63, 0x43000000, v63
	ds_write_b128 v120, v[60:63] offset:6144
	v_mul_f32_e32 v64, 0x43000000, v64
	v_mul_f32_e32 v65, 0x43000000, v65
	v_mul_f32_e32 v66, 0x43000000, v66
	v_mul_f32_e32 v67, 0x43000000, v67
	ds_write_b128 v120, v[64:67] offset:7168
	s_waitcnt lgkmcnt(0)
	s_barrier
; #define GAS __attribute__((address_space(1)))
; #define LAS __attribute__((address_space(3)))
; #define LDS_WAIT() asm volatile("s_waitcnt lgkmcnt(0)" ::: "memory")
;     const int pr = item >> 1, kb = 2 * (pr / nblk) + (item & 1), nb = pr % nblk, k0 = 64 * kb, n0 = 32 * nb;
;     const int nr = n0 + (lane & 31); const int sc = MAP == 1 ? src_col_in(nr) : nr;
;     float v[32];
; #pragma unroll
;     for (int i = 0; i < 32; ++i) v[i] = sc >= 0 ? W[(size_t)(k0 + 2 * i + (lane >> 5)) * Nsrc + sc] : 0.f;
; #pragma unroll
;     for (int i = 0; i < 32; ++i) { const int k = k0 + 2 * i + (lane >> 5); float x = v[i] * wscale; if (KS) x *= (k < ksplit ? ksA[k] : ksB[k - ksplit]); scr[(2 * i + (lane >> 5)) * 33 + (lane & 31)] = x; }
;     LDS_WAIT(); asm volatile("" ::: "memory");
;     const int c = lane & 7;
; #pragma unroll
;     for (int j = 0; j < 4; ++j) { const int n = (lane >> 3) + 8 * j; const LAS float* s = scr + (8 * c) * 33 + n;
;         const unsigned long long o = (unsigned long long)pg8::pk4_fp8(s[0 * 33], s[1 * 33], s[2 * 33], s[3 * 33]) | ((unsigned long long)pg8::pk4_fp8(s[4 * 33], s[5 * 33], s[6 * 33], s[7 * 33]) << 32);
;         *(GAS unsigned long long*)(WT + (size_t)(n0 + n) * K + k0 + 8 * c) = o; }
;     LDS_WAIT(); asm volatile("" ::: "memory");
	s_add_i32 s17, s16, 1728
	s_min_u32 s17, s17, 0x7ff
	s_lshr_b32 s18, s17, 5
	s_add_i32 s18, s18, 0
	s_and_b32 s19, s17, 31
	s_lshl_b32 s18, s18, 21
	s_lshl_b32 s19, s19, 9
	s_add_u32 s18, s18, s19
	s_add_u32 s10, s2, s18
	s_addc_u32 s11, s3, 0
	global_load_dwordx4 v[36:39], v126, s[10:11]
	s_add_u32 s10, s10, 0x8000
	s_addc_u32 s11, s11, 0
	global_load_dwordx4 v[40:43], v126, s[10:11]
	s_add_u32 s10, s10, 0x8000
	s_addc_u32 s11, s11, 0
	global_load_dwordx4 v[44:47], v126, s[10:11]
	s_add_u32 s10, s10, 0x8000
	s_addc_u32 s11, s11, 0
	global_load_dwordx4 v[48:51], v126, s[10:11]
	s_add_u32 s10, s10, 0x8000
	s_addc_u32 s11, s11, 0
	global_load_dwordx4 v[52:55], v126, s[10:11]
	s_add_u32 s10, s10, 0x8000
	s_addc_u32 s11, s11, 0
	global_load_dwordx4 v[56:59], v126, s[10:11]
	s_add_u32 s10, s10, 0x8000
	s_addc_u32 s11, s11, 0
	global_load_dwordx4 v[60:63], v126, s[10:11]
	s_add_u32 s10, s10, 0x8000
	s_addc_u32 s11, s11, 0
	global_load_dwordx4 v[64:67], v126, s[10:11]
	s_add_i32 s17, s16, 1536
	s_min_u32 s17, s17, 0x7ff
	s_lshr_b32 s18, s17, 5
	s_add_i32 s18, s18, 0
	s_and_b32 s19, s17, 31
	s_lshl_b32 s19, s19, 21
	s_lshl_b32 s18, s18, 7
	s_add_u32 s18, s18, s19
	s_add_u32 s14, s4, s18
	s_addc_u32 s15, s5, 0
	ds_read_b32 v100, v122
	ds_read_b32 v101, v122 offset:512
	ds_read_b32 v102, v122 offset:1024
	ds_read_b32 v103, v122 offset:1536
	ds_read_b32 v104, v122 offset:2048
	ds_read_b32 v105, v122 offset:2560
	ds_read_b32 v106, v122 offset:3072
	ds_read_b32 v107, v122 offset:3584
	ds_read_b32 v108, v122 offset:4096
	ds_read_b32 v109, v122 offset:4608
	ds_read_b32 v110, v122 offset:5120
	ds_read_b32 v111, v122 offset:5632
	ds_read_b32 v112, v122 offset:6144
	ds_read_b32 v113, v122 offset:6656
	ds_read_b32 v114, v122 offset:7168
	ds_read_b32 v115, v122 offset:7680
	s_waitcnt lgkmcnt(0)
	v_max_f32_e32 v100, v100, v100
	v_max_f32_e32 v101, v101, v101
	v_max_f32_e32 v102, v102, v102
	v_max_f32_e32 v103, v103, v103
	v_max_f32_e32 v104, v104, v104
	v_max_f32_e32 v105, v105, v105
	v_max_f32_e32 v106, v106, v106
	v_max_f32_e32 v107, v107, v107
	v_max_f32_e32 v108, v108, v108
	v_max_f32_e32 v109, v109, v109
	v_max_f32_e32 v110, v110, v110
	v_max_f32_e32 v111, v111, v111
	v_max_f32_e32 v112, v112, v112
	v_max_f32_e32 v113, v113, v113
	v_max_f32_e32 v114, v114, v114
	v_max_f32_e32 v115, v115, v115
	v_med3_f32 v100, v100, s20, v129
	v_med3_f32 v101, v101, s20, v129
	v_med3_f32 v102, v102, s20, v129
	v_med3_f32 v103, v103, s20, v129
	v_med3_f32 v104, v104, s20, v129
	v_med3_f32 v105, v105, s20, v129
	v_med3_f32 v106, v106, s20, v129
	v_med3_f32 v107, v107, s20, v129
	v_med3_f32 v108, v108, s20, v129
	v_med3_f32 v109, v109, s20, v129
	v_med3_f32 v110, v110, s20, v129
	v_med3_f32 v111, v111, s20, v129
	v_med3_f32 v112, v112, s20, v129
	v_med3_f32 v113, v113, s20, v129
	v_med3_f32 v114, v114, s20, v129
	v_med3_f32 v115, v115, s20, v129
	v_mov_b32_e32 v116, 0
	v_mov_b32_e32 v117, 0
	v_mov_b32_e32 v118, 0
	v_mov_b32_e32 v119, 0
	v_cvt_pk_fp8_f32 v116, v100, v101
	v_cvt_pk_fp8_f32 v117, v104, v105
	v_cvt_pk_fp8_f32 v118, v108, v109
	v_cvt_pk_fp8_f32 v119, v112, v113
	v_cvt_pk_fp8_f32 v116, v102, v103 op_sel:[0,0,1]
	v_cvt_pk_fp8_f32 v117, v106, v107 op_sel:[0,0,1]
	v_cvt_pk_fp8_f32 v118, v110, v111 op_sel:[0,0,1]
	v_cvt_pk_fp8_f32 v119, v114, v115 op_sel:[0,0,1]
	s_nop 0
	global_store_dwordx4 v127, v[116:119], s[14:15]
	ds_read_b32 v100, v124
	ds_read_b32 v101, v124 offset:512
	ds_read_b32 v102, v124 offset:1024
	ds_read_b32 v103, v124 offset:1536
	ds_read_b32 v104, v124 offset:2048
	ds_read_b32 v105, v124 offset:2560
	ds_read_b32 v106, v124 offset:3072
	ds_read_b32 v107, v124 offset:3584
	ds_read_b32 v108, v124 offset:4096
	ds_read_b32 v109, v124 offset:4608
	ds_read_b32 v110, v124 offset:5120
	ds_read_b32 v111, v124 offset:5632
	ds_read_b32 v112, v124 offset:6144
	ds_read_b32 v113, v124 offset:6656
	ds_read_b32 v114, v124 offset:7168
	ds_read_b32 v115, v124 offset:7680
	s_waitcnt lgkmcnt(0)
	v_max_f32_e32 v100, v100, v100
	v_max_f32_e32 v101, v101, v101
	v_max_f32_e32 v102, v102, v102
	v_max_f32_e32 v103, v103, v103
	v_max_f32_e32 v104, v104, v104
	v_max_f32_e32 v105, v105, v105
	v_max_f32_e32 v106, v106, v106
	v_max_f32_e32 v107, v107, v107
	v_max_f32_e32 v108, v108, v108
	v_max_f32_e32 v109, v109, v109
	v_max_f32_e32 v110, v110, v110
	v_max_f32_e32 v111, v111, v111
	v_max_f32_e32 v112, v112, v112
	v_max_f32_e32 v113, v113, v113
	v_max_f32_e32 v114, v114, v114
	v_max_f32_e32 v115, v115, v115
	v_med3_f32 v100, v100, s20, v129
	v_med3_f32 v101, v101, s20, v129
	v_med3_f32 v102, v102, s20, v129
	v_med3_f32 v103, v103, s20, v129
	v_med3_f32 v104, v104, s20, v129
	v_med3_f32 v105, v105, s20, v129
	v_med3_f32 v106, v106, s20, v129
	v_med3_f32 v107, v107, s20, v129
	v_med3_f32 v108, v108, s20, v129
	v_med3_f32 v109, v109, s20, v129
	v_med3_f32 v110, v110, s20, v129
	v_med3_f32 v111, v111, s20, v129
	v_med3_f32 v112, v112, s20, v129
	v_med3_f32 v113, v113, s20, v129
	v_med3_f32 v114, v114, s20, v129
	v_med3_f32 v115, v115, s20, v129
	v_mov_b32_e32 v116, 0
	v_mov_b32_e32 v117, 0
	v_mov_b32_e32 v118, 0
	v_mov_b32_e32 v119, 0
	v_cvt_pk_fp8_f32 v116, v100, v101
	v_cvt_pk_fp8_f32 v117, v104, v105
	v_cvt_pk_fp8_f32 v118, v108, v109
	v_cvt_pk_fp8_f32 v119, v112, v113
	v_cvt_pk_fp8_f32 v116, v102, v103 op_sel:[0,0,1]
	v_cvt_pk_fp8_f32 v117, v106, v107 op_sel:[0,0,1]
	v_cvt_pk_fp8_f32 v118, v110, v111 op_sel:[0,0,1]
	v_cvt_pk_fp8_f32 v119, v114, v115 op_sel:[0,0,1]
	s_nop 0
	global_store_dwordx4 v128, v[116:119], s[14:15]
	s_waitcnt vmcnt(12)
	v_mul_f32_e32 v68, 0x43000000, v68
	v_mul_f32_e32 v69, 0x43000000, v69
	v_mul_f32_e32 v70, 0x43000000, v70
	v_mul_f32_e32 v71, 0x43000000, v71
	ds_write_b128 v121, v[68:71]
	v_mul_f32_e32 v72, 0x43000000, v72
	v_mul_f32_e32 v73, 0x43000000, v73
	v_mul_f32_e32 v74, 0x43000000, v74
	v_mul_f32_e32 v75, 0x43000000, v75
	ds_write_b128 v121, v[72:75] offset:1024
	v_mul_f32_e32 v76, 0x43000000, v76
	v_mul_f32_e32 v77, 0x43000000, v77
	v_mul_f32_e32 v78, 0x43000000, v78
	v_mul_f32_e32 v79, 0x43000000, v79
	ds_write_b128 v121, v[76:79] offset:2048
	v_mul_f32_e32 v80, 0x43000000, v80
	v_mul_f32_e32 v81, 0x43000000, v81
	v_mul_f32_e32 v82, 0x43000000, v82
	v_mul_f32_e32 v83, 0x43000000, v83
	ds_write_b128 v121, v[80:83] offset:3072
	v_mul_f32_e32 v84, 0x43000000, v84
	v_mul_f32_e32 v85, 0x43000000, v85
	v_mul_f32_e32 v86, 0x43000000, v86
	v_mul_f32_e32 v87, 0x43000000, v87
	ds_write_b128 v121, v[84:87] offset:4096
	v_mul_f32_e32 v88, 0x43000000, v88
	v_mul_f32_e32 v89, 0x43000000, v89
	v_mul_f32_e32 v90, 0x43000000, v90
	v_mul_f32_e32 v91, 0x43000000, v91
	ds_write_b128 v121, v[88:91] offset:5120
	v_mul_f32_e32 v92, 0x43000000, v92
	v_mul_f32_e32 v93, 0x43000000, v93
	v_mul_f32_e32 v94, 0x43000000, v94
	v_mul_f32_e32 v95, 0x43000000, v95
	ds_write_b128 v121, v[92:95] offset:6144
	v_mul_f32_e32 v96, 0x43000000, v96
	v_mul_f32_e32 v97, 0x43000000, v97
	v_mul_f32_e32 v98, 0x43000000, v98
	v_mul_f32_e32 v99, 0x43000000, v99
	ds_write_b128 v121, v[96:99] offset:7168
	s_waitcnt lgkmcnt(0)
	s_barrier
; #define GAS __attribute__((address_space(1)))
; #define LAS __attribute__((address_space(3)))
; #define LDS_WAIT() asm volatile("s_waitcnt lgkmcnt(0)" ::: "memory")
;     const int pr = item >> 1, kb = 2 * (pr / nblk) + (item & 1), nb = pr % nblk, k0 = 64 * kb, n0 = 32 * nb;
;     const int nr = n0 + (lane & 31); const int sc = MAP == 1 ? src_col_in(nr) : nr;
;     float v[32];
; #pragma unroll
;     for (int i = 0; i < 32; ++i) v[i] = sc >= 0 ? W[(size_t)(k0 + 2 * i + (lane >> 5)) * Nsrc + sc] : 0.f;
; #pragma unroll
;     for (int i = 0; i < 32; ++i) { const int k = k0 + 2 * i + (lane >> 5); float x = v[i] * wscale; if (KS) x *= (k < ksplit ? ksA[k] : ksB[k - ksplit]); scr[(2 * i + (lane >> 5)) * 33 + (lane & 31)] = x; }
;     LDS_WAIT(); asm volatile("" ::: "memory");
;     const int c = lane & 7;
; #pragma unroll
;     for (int j = 0; j < 4; ++j) { const int n = (lane >> 3) + 8 * j; const LAS float* s = scr + (8 * c) * 33 + n;
;         const unsigned long long o = (unsigned long long)pg8::pk4_fp8(s[0 * 33], s[1 * 33], s[2 * 33], s[3 * 33]) | ((unsigned long long)pg8::pk4_fp8(s[4 * 33], s[5 * 33], s[6 * 33], s[7 * 33]) << 32);
;         *(GAS unsigned long long*)(WT + (size_t)(n0 + n) * K + k0 + 8 * c) = o; }
;     LDS_WAIT(); asm volatile("" ::: "memory");
	s_add_i32 s17, s16, 1824
	s_min_u32 s17, s17, 0x7ff
	s_lshr_b32 s18, s17, 5
	s_add_i32 s18, s18, 0
	s_and_b32 s19, s17, 31
	s_lshl_b32 s18, s18, 21
	s_lshl_b32 s19, s19, 9
	s_add_u32 s18, s18, s19
	s_add_u32 s10, s2, s18
	s_addc_u32 s11, s3, 0
	global_load_dwordx4 v[68:71], v126, s[10:11]
	s_add_u32 s10, s10, 0x8000
	s_addc_u32 s11, s11, 0
	global_load_dwordx4 v[72:75], v126, s[10:11]
	s_add_u32 s10, s10, 0x8000
	s_addc_u32 s11, s11, 0
	global_load_dwordx4 v[76:79], v126, s[10:11]
	s_add_u32 s10, s10, 0x8000
	s_addc_u32 s11, s11, 0
	global_load_dwordx4 v[80:83], v126, s[10:11]
	s_add_u32 s10, s10, 0x8000
	s_addc_u32 s11, s11, 0
	global_load_dwordx4 v[84:87], v126, s[10:11]
	s_add_u32 s10, s10, 0x8000
	s_addc_u32 s11, s11, 0
	global_load_dwordx4 v[88:91], v126, s[10:11]
	s_add_u32 s10, s10, 0x8000
	s_addc_u32 s11, s11, 0
	global_load_dwordx4 v[92:95], v126, s[10:11]
	s_add_u32 s10, s10, 0x8000
	s_addc_u32 s11, s11, 0
	global_load_dwordx4 v[96:99], v126, s[10:11]
	s_add_i32 s17, s16, 1632
	s_min_u32 s17, s17, 0x7ff
	s_lshr_b32 s18, s17, 5
	s_add_i32 s18, s18, 0
	s_and_b32 s19, s17, 31
	s_lshl_b32 s19, s19, 21
	s_lshl_b32 s18, s18, 7
	s_add_u32 s18, s18, s19
	s_add_u32 s14, s4, s18
	s_addc_u32 s15, s5, 0
	ds_read_b32 v100, v123
	ds_read_b32 v101, v123 offset:512
	ds_read_b32 v102, v123 offset:1024
	ds_read_b32 v103, v123 offset:1536
	ds_read_b32 v104, v123 offset:2048
	ds_read_b32 v105, v123 offset:2560
	ds_read_b32 v106, v123 offset:3072
	ds_read_b32 v107, v123 offset:3584
	ds_read_b32 v108, v123 offset:4096
	ds_read_b32 v109, v123 offset:4608
	ds_read_b32 v110, v123 offset:5120
	ds_read_b32 v111, v123 offset:5632
	ds_read_b32 v112, v123 offset:6144
	ds_read_b32 v113, v123 offset:6656
	ds_read_b32 v114, v123 offset:7168
	ds_read_b32 v115, v123 offset:7680
	s_waitcnt lgkmcnt(0)
	v_max_f32_e32 v100, v100, v100
	v_max_f32_e32 v101, v101, v101
	v_max_f32_e32 v102, v102, v102
	v_max_f32_e32 v103, v103, v103
	v_max_f32_e32 v104, v104, v104
	v_max_f32_e32 v105, v105, v105
	v_max_f32_e32 v106, v106, v106
	v_max_f32_e32 v107, v107, v107
	v_max_f32_e32 v108, v108, v108
	v_max_f32_e32 v109, v109, v109
	v_max_f32_e32 v110, v110, v110
	v_max_f32_e32 v111, v111, v111
	v_max_f32_e32 v112, v112, v112
	v_max_f32_e32 v113, v113, v113
	v_max_f32_e32 v114, v114, v114
	v_max_f32_e32 v115, v115, v115
	v_med3_f32 v100, v100, s20, v129
	v_med3_f32 v101, v101, s20, v129
	v_med3_f32 v102, v102, s20, v129
	v_med3_f32 v103, v103, s20, v129
	v_med3_f32 v104, v104, s20, v129
	v_med3_f32 v105, v105, s20, v129
	v_med3_f32 v106, v106, s20, v129
	v_med3_f32 v107, v107, s20, v129
	v_med3_f32 v108, v108, s20, v129
	v_med3_f32 v109, v109, s20, v129
	v_med3_f32 v110, v110, s20, v129
	v_med3_f32 v111, v111, s20, v129
	v_med3_f32 v112, v112, s20, v129
	v_med3_f32 v113, v113, s20, v129
	v_med3_f32 v114, v114, s20, v129
	v_med3_f32 v115, v115, s20, v129
	v_mov_b32_e32 v116, 0
	v_mov_b32_e32 v117, 0
	v_mov_b32_e32 v118, 0
	v_mov_b32_e32 v119, 0
	v_cvt_pk_fp8_f32 v116, v100, v101
	v_cvt_pk_fp8_f32 v117, v104, v105
	v_cvt_pk_fp8_f32 v118, v108, v109
	v_cvt_pk_fp8_f32 v119, v112, v113
	v_cvt_pk_fp8_f32 v116, v102, v103 op_sel:[0,0,1]
	v_cvt_pk_fp8_f32 v117, v106, v107 op_sel:[0,0,1]
	v_cvt_pk_fp8_f32 v118, v110, v111 op_sel:[0,0,1]
	v_cvt_pk_fp8_f32 v119, v114, v115 op_sel:[0,0,1]
	s_nop 0
	global_store_dwordx4 v127, v[116:119], s[14:15]
	ds_read_b32 v100, v125
	ds_read_b32 v101, v125 offset:512
	ds_read_b32 v102, v125 offset:1024
	ds_read_b32 v103, v125 offset:1536
	ds_read_b32 v104, v125 offset:2048
	ds_read_b32 v105, v125 offset:2560
	ds_read_b32 v106, v125 offset:3072
	ds_read_b32 v107, v125 offset:3584
	ds_read_b32 v108, v125 offset:4096
	ds_read_b32 v109, v125 offset:4608
	ds_read_b32 v110, v125 offset:5120
	ds_read_b32 v111, v125 offset:5632
	ds_read_b32 v112, v125 offset:6144
	ds_read_b32 v113, v125 offset:6656
	ds_read_b32 v114, v125 offset:7168
	ds_read_b32 v115, v125 offset:7680
	s_waitcnt lgkmcnt(0)
	v_max_f32_e32 v100, v100, v100
	v_max_f32_e32 v101, v101, v101
	v_max_f32_e32 v102, v102, v102
	v_max_f32_e32 v103, v103, v103
	v_max_f32_e32 v104, v104, v104
	v_max_f32_e32 v105, v105, v105
	v_max_f32_e32 v106, v106, v106
	v_max_f32_e32 v107, v107, v107
	v_max_f32_e32 v108, v108, v108
	v_max_f32_e32 v109, v109, v109
	v_max_f32_e32 v110, v110, v110
	v_max_f32_e32 v111, v111, v111
	v_max_f32_e32 v112, v112, v112
	v_max_f32_e32 v113, v113, v113
	v_max_f32_e32 v114, v114, v114
	v_max_f32_e32 v115, v115, v115
	v_med3_f32 v100, v100, s20, v129
	v_med3_f32 v101, v101, s20, v129
	v_med3_f32 v102, v102, s20, v129
	v_med3_f32 v103, v103, s20, v129
	v_med3_f32 v104, v104, s20, v129
	v_med3_f32 v105, v105, s20, v129
	v_med3_f32 v106, v106, s20, v129
	v_med3_f32 v107, v107, s20, v129
	v_med3_f32 v108, v108, s20, v129
	v_med3_f32 v109, v109, s20, v129
	v_med3_f32 v110, v110, s20, v129
	v_med3_f32 v111, v111, s20, v129
	v_med3_f32 v112, v112, s20, v129
	v_med3_f32 v113, v113, s20, v129
	v_med3_f32 v114, v114, s20, v129
	v_med3_f32 v115, v115, s20, v129
	v_mov_b32_e32 v116, 0
	v_mov_b32_e32 v117, 0
	v_mov_b32_e32 v118, 0
	v_mov_b32_e32 v119, 0
	v_cvt_pk_fp8_f32 v116, v100, v101
	v_cvt_pk_fp8_f32 v117, v104, v105
	v_cvt_pk_fp8_f32 v118, v108, v109
	v_cvt_pk_fp8_f32 v119, v112, v113
	v_cvt_pk_fp8_f32 v116, v102, v103 op_sel:[0,0,1]
	v_cvt_pk_fp8_f32 v117, v106, v107 op_sel:[0,0,1]
	v_cvt_pk_fp8_f32 v118, v110, v111 op_sel:[0,0,1]
	v_cvt_pk_fp8_f32 v119, v114, v115 op_sel:[0,0,1]
	s_nop 0
	global_store_dwordx4 v128, v[116:119], s[14:15]
	s_waitcnt vmcnt(12)
	v_mul_f32_e32 v36, 0x43000000, v36
	v_mul_f32_e32 v37, 0x43000000, v37
	v_mul_f32_e32 v38, 0x43000000, v38
	v_mul_f32_e32 v39, 0x43000000, v39
	ds_write_b128 v120, v[36:39]
	v_mul_f32_e32 v40, 0x43000000, v40
	v_mul_f32_e32 v41, 0x43000000, v41
	v_mul_f32_e32 v42, 0x43000000, v42
	v_mul_f32_e32 v43, 0x43000000, v43
	ds_write_b128 v120, v[40:43] offset:1024
	v_mul_f32_e32 v44, 0x43000000, v44
	v_mul_f32_e32 v45, 0x43000000, v45
	v_mul_f32_e32 v46, 0x43000000, v46
	v_mul_f32_e32 v47, 0x43000000, v47
	ds_write_b128 v120, v[44:47] offset:2048
	v_mul_f32_e32 v48, 0x43000000, v48
	v_mul_f32_e32 v49, 0x43000000, v49
	v_mul_f32_e32 v50, 0x43000000, v50
	v_mul_f32_e32 v51, 0x43000000, v51
	ds_write_b128 v120, v[48:51] offset:3072
	v_mul_f32_e32 v52, 0x43000000, v52
	v_mul_f32_e32 v53, 0x43000000, v53
	v_mul_f32_e32 v54, 0x43000000, v54
	v_mul_f32_e32 v55, 0x43000000, v55
	ds_write_b128 v120, v[52:55] offset:4096
	v_mul_f32_e32 v56, 0x43000000, v56
	v_mul_f32_e32 v57, 0x43000000, v57
	v_mul_f32_e32 v58, 0x43000000, v58
	v_mul_f32_e32 v59, 0x43000000, v59
	ds_write_b128 v120, v[56:59] offset:5120
	v_mul_f32_e32 v60, 0x43000000, v60
	v_mul_f32_e32 v61, 0x43000000, v61
	v_mul_f32_e32 v62, 0x43000000, v62
	v_mul_f32_e32 v63, 0x43000000, v63
	ds_write_b128 v120, v[60:63] offset:6144
	v_mul_f32_e32 v64, 0x43000000, v64
	v_mul_f32_e32 v65, 0x43000000, v65
	v_mul_f32_e32 v66, 0x43000000, v66
	v_mul_f32_e32 v67, 0x43000000, v67
	ds_write_b128 v120, v[64:67] offset:7168
	s_waitcnt lgkmcnt(0)
	s_barrier
; #define GAS __attribute__((address_space(1)))
; #define LAS __attribute__((address_space(3)))
; #define LDS_WAIT() asm volatile("s_waitcnt lgkmcnt(0)" ::: "memory")
;     const int pr = item >> 1, kb = 2 * (pr / nblk) + (item & 1), nb = pr % nblk, k0 = 64 * kb, n0 = 32 * nb;
;     const int nr = n0 + (lane & 31); const int sc = MAP == 1 ? src_col_in(nr) : nr;
;     float v[32];
; #pragma unroll
;     for (int i = 0; i < 32; ++i) v[i] = sc >= 0 ? W[(size_t)(k0 + 2 * i + (lane >> 5)) * Nsrc + sc] : 0.f;
; #pragma unroll
;     for (int i = 0; i < 32; ++i) { const int k = k0 + 2 * i + (lane >> 5); float x = v[i] * wscale; if (KS) x *= (k < ksplit ? ksA[k] : ksB[k - ksplit]); scr[(2 * i + (lane >> 5)) * 33 + (lane & 31)] = x; }
;     LDS_WAIT(); asm volatile("" ::: "memory");
;     const int c = lane & 7;
; #pragma unroll
;     for (int j = 0; j < 4; ++j) { const int n = (lane >> 3) + 8 * j; const LAS float* s = scr + (8 * c) * 33 + n;
;         const unsigned long long o = (unsigned long long)pg8::pk4_fp8(s[0 * 33], s[1 * 33], s[2 * 33], s[3 * 33]) | ((unsigned long long)pg8::pk4_fp8(s[4 * 33], s[5 * 33], s[6 * 33], s[7 * 33]) << 32);
;         *(GAS unsigned long long*)(WT + (size_t)(n0 + n) * K + k0 + 8 * c) = o; }
;     LDS_WAIT(); asm volatile("" ::: "memory");
	s_add_i32 s17, s16, 1920
	s_min_u32 s17, s17, 0x7ff
	s_lshr_b32 s18, s17, 5
	s_add_i32 s18, s18, 0
	s_and_b32 s19, s17, 31
	s_lshl_b32 s18, s18, 21
	s_lshl_b32 s19, s19, 9
	s_add_u32 s18, s18, s19
	s_add_u32 s10, s2, s18
	s_addc_u32 s11, s3, 0
	global_load_dwordx4 v[36:39], v126, s[10:11]
	s_add_u32 s10, s10, 0x8000
	s_addc_u32 s11, s11, 0
	global_load_dwordx4 v[40:43], v126, s[10:11]
	s_add_u32 s10, s10, 0x8000
	s_addc_u32 s11, s11, 0
	global_load_dwordx4 v[44:47], v126, s[10:11]
	s_add_u32 s10, s10, 0x8000
	s_addc_u32 s11, s11, 0
	global_load_dwordx4 v[48:51], v126, s[10:11]
	s_add_u32 s10, s10, 0x8000
	s_addc_u32 s11, s11, 0
	global_load_dwordx4 v[52:55], v126, s[10:11]
	s_add_u32 s10, s10, 0x8000
	s_addc_u32 s11, s11, 0
	global_load_dwordx4 v[56:59], v126, s[10:11]
	s_add_u32 s10, s10, 0x8000
	s_addc_u32 s11, s11, 0
	global_load_dwordx4 v[60:63], v126, s[10:11]
	s_add_u32 s10, s10, 0x8000
	s_addc_u32 s11, s11, 0
	global_load_dwordx4 v[64:67], v126, s[10:11]
	s_add_i32 s17, s16, 1728
	s_min_u32 s17, s17, 0x7ff
	s_lshr_b32 s18, s17, 5
	s_add_i32 s18, s18, 0
	s_and_b32 s19, s17, 31
	s_lshl_b32 s19, s19, 21
	s_lshl_b32 s18, s18, 7
	s_add_u32 s18, s18, s19
	s_add_u32 s14, s4, s18
	s_addc_u32 s15, s5, 0
	ds_read_b32 v100, v122
	ds_read_b32 v101, v122 offset:512
	ds_read_b32 v102, v122 offset:1024
	ds_read_b32 v103, v122 offset:1536
	ds_read_b32 v104, v122 offset:2048
	ds_read_b32 v105, v122 offset:2560
	ds_read_b32 v106, v122 offset:3072
	ds_read_b32 v107, v122 offset:3584
	ds_read_b32 v108, v122 offset:4096
	ds_read_b32 v109, v122 offset:4608
	ds_read_b32 v110, v122 offset:5120
	ds_read_b32 v111, v122 offset:5632
	ds_read_b32 v112, v122 offset:6144
	ds_read_b32 v113, v122 offset:6656
	ds_read_b32 v114, v122 offset:7168
	ds_read_b32 v115, v122 offset:7680
	s_waitcnt lgkmcnt(0)
	v_max_f32_e32 v100, v100, v100
	v_max_f32_e32 v101, v101, v101
	v_max_f32_e32 v102, v102, v102
	v_max_f32_e32 v103, v103, v103
	v_max_f32_e32 v104, v104, v104
	v_max_f32_e32 v105, v105, v105
	v_max_f32_e32 v106, v106, v106
	v_max_f32_e32 v107, v107, v107
	v_max_f32_e32 v108, v108, v108
	v_max_f32_e32 v109, v109, v109
	v_max_f32_e32 v110, v110, v110
	v_max_f32_e32 v111, v111, v111
	v_max_f32_e32 v112, v112, v112
	v_max_f32_e32 v113, v113, v113
	v_max_f32_e32 v114, v114, v114
	v_max_f32_e32 v115, v115, v115
	v_med3_f32 v100, v100, s20, v129
	v_med3_f32 v101, v101, s20, v129
	v_med3_f32 v102, v102, s20, v129
	v_med3_f32 v103, v103, s20, v129
	v_med3_f32 v104, v104, s20, v129
	v_med3_f32 v105, v105, s20, v129
	v_med3_f32 v106, v106, s20, v129
	v_med3_f32 v107, v107, s20, v129
	v_med3_f32 v108, v108, s20, v129
	v_med3_f32 v109, v109, s20, v129
	v_med3_f32 v110, v110, s20, v129
	v_med3_f32 v111, v111, s20, v129
	v_med3_f32 v112, v112, s20, v129
	v_med3_f32 v113, v113, s20, v129
	v_med3_f32 v114, v114, s20, v129
	v_med3_f32 v115, v115, s20, v129
	v_mov_b32_e32 v116, 0
	v_mov_b32_e32 v117, 0
	v_mov_b32_e32 v118, 0
	v_mov_b32_e32 v119, 0
	v_cvt_pk_fp8_f32 v116, v100, v101
	v_cvt_pk_fp8_f32 v117, v104, v105
	v_cvt_pk_fp8_f32 v118, v108, v109
	v_cvt_pk_fp8_f32 v119, v112, v113
	v_cvt_pk_fp8_f32 v116, v102, v103 op_sel:[0,0,1]
	v_cvt_pk_fp8_f32 v117, v106, v107 op_sel:[0,0,1]
	v_cvt_pk_fp8_f32 v118, v110, v111 op_sel:[0,0,1]
	v_cvt_pk_fp8_f32 v119, v114, v115 op_sel:[0,0,1]
	s_nop 0
	global_store_dwordx4 v127, v[116:119], s[14:15]
	ds_read_b32 v100, v124
	ds_read_b32 v101, v124 offset:512
	ds_read_b32 v102, v124 offset:1024
	ds_read_b32 v103, v124 offset:1536
	ds_read_b32 v104, v124 offset:2048
	ds_read_b32 v105, v124 offset:2560
	ds_read_b32 v106, v124 offset:3072
	ds_read_b32 v107, v124 offset:3584
	ds_read_b32 v108, v124 offset:4096
	ds_read_b32 v109, v124 offset:4608
	ds_read_b32 v110, v124 offset:5120
	ds_read_b32 v111, v124 offset:5632
	ds_read_b32 v112, v124 offset:6144
	ds_read_b32 v113, v124 offset:6656
	ds_read_b32 v114, v124 offset:7168
	ds_read_b32 v115, v124 offset:7680
	s_waitcnt lgkmcnt(0)
	v_max_f32_e32 v100, v100, v100
	v_max_f32_e32 v101, v101, v101
	v_max_f32_e32 v102, v102, v102
	v_max_f32_e32 v103, v103, v103
	v_max_f32_e32 v104, v104, v104
	v_max_f32_e32 v105, v105, v105
	v_max_f32_e32 v106, v106, v106
	v_max_f32_e32 v107, v107, v107
	v_max_f32_e32 v108, v108, v108
	v_max_f32_e32 v109, v109, v109
	v_max_f32_e32 v110, v110, v110
	v_max_f32_e32 v111, v111, v111
	v_max_f32_e32 v112, v112, v112
	v_max_f32_e32 v113, v113, v113
	v_max_f32_e32 v114, v114, v114
	v_max_f32_e32 v115, v115, v115
	v_med3_f32 v100, v100, s20, v129
	v_med3_f32 v101, v101, s20, v129
	v_med3_f32 v102, v102, s20, v129
	v_med3_f32 v103, v103, s20, v129
	v_med3_f32 v104, v104, s20, v129
	v_med3_f32 v105, v105, s20, v129
	v_med3_f32 v106, v106, s20, v129
	v_med3_f32 v107, v107, s20, v129
	v_med3_f32 v108, v108, s20, v129
	v_med3_f32 v109, v109, s20, v129
	v_med3_f32 v110, v110, s20, v129
	v_med3_f32 v111, v111, s20, v129
	v_med3_f32 v112, v112, s20, v129
	v_med3_f32 v113, v113, s20, v129
	v_med3_f32 v114, v114, s20, v129
	v_med3_f32 v115, v115, s20, v129
	v_mov_b32_e32 v116, 0
	v_mov_b32_e32 v117, 0
	v_mov_b32_e32 v118, 0
	v_mov_b32_e32 v119, 0
	v_cvt_pk_fp8_f32 v116, v100, v101
	v_cvt_pk_fp8_f32 v117, v104, v105
	v_cvt_pk_fp8_f32 v118, v108, v109
	v_cvt_pk_fp8_f32 v119, v112, v113
	v_cvt_pk_fp8_f32 v116, v102, v103 op_sel:[0,0,1]
	v_cvt_pk_fp8_f32 v117, v106, v107 op_sel:[0,0,1]
	v_cvt_pk_fp8_f32 v118, v110, v111 op_sel:[0,0,1]
	v_cvt_pk_fp8_f32 v119, v114, v115 op_sel:[0,0,1]
	s_nop 0
	global_store_dwordx4 v128, v[116:119], s[14:15]
	s_waitcnt vmcnt(12)
	v_mul_f32_e32 v68, 0x43000000, v68
	v_mul_f32_e32 v69, 0x43000000, v69
	v_mul_f32_e32 v70, 0x43000000, v70
	v_mul_f32_e32 v71, 0x43000000, v71
	ds_write_b128 v121, v[68:71]
	v_mul_f32_e32 v72, 0x43000000, v72
	v_mul_f32_e32 v73, 0x43000000, v73
	v_mul_f32_e32 v74, 0x43000000, v74
	v_mul_f32_e32 v75, 0x43000000, v75
	ds_write_b128 v121, v[72:75] offset:1024
	v_mul_f32_e32 v76, 0x43000000, v76
	v_mul_f32_e32 v77, 0x43000000, v77
	v_mul_f32_e32 v78, 0x43000000, v78
	v_mul_f32_e32 v79, 0x43000000, v79
	ds_write_b128 v121, v[76:79] offset:2048
	v_mul_f32_e32 v80, 0x43000000, v80
	v_mul_f32_e32 v81, 0x43000000, v81
	v_mul_f32_e32 v82, 0x43000000, v82
	v_mul_f32_e32 v83, 0x43000000, v83
	ds_write_b128 v121, v[80:83] offset:3072
	v_mul_f32_e32 v84, 0x43000000, v84
	v_mul_f32_e32 v85, 0x43000000, v85
	v_mul_f32_e32 v86, 0x43000000, v86
	v_mul_f32_e32 v87, 0x43000000, v87
	ds_write_b128 v121, v[84:87] offset:4096
	v_mul_f32_e32 v88, 0x43000000, v88
	v_mul_f32_e32 v89, 0x43000000, v89
	v_mul_f32_e32 v90, 0x43000000, v90
	v_mul_f32_e32 v91, 0x43000000, v91
	ds_write_b128 v121, v[88:91] offset:5120
	v_mul_f32_e32 v92, 0x43000000, v92
	v_mul_f32_e32 v93, 0x43000000, v93
	v_mul_f32_e32 v94, 0x43000000, v94
	v_mul_f32_e32 v95, 0x43000000, v95
	ds_write_b128 v121, v[92:95] offset:6144
	v_mul_f32_e32 v96, 0x43000000, v96
	v_mul_f32_e32 v97, 0x43000000, v97
	v_mul_f32_e32 v98, 0x43000000, v98
	v_mul_f32_e32 v99, 0x43000000, v99
	ds_write_b128 v121, v[96:99] offset:7168
	s_waitcnt lgkmcnt(0)
	s_barrier
; #define GAS __attribute__((address_space(1)))
; #define LAS __attribute__((address_space(3)))
; #define LDS_WAIT() asm volatile("s_waitcnt lgkmcnt(0)" ::: "memory")
;     const int pr = item >> 1, kb = 2 * (pr / nblk) + (item & 1), nb = pr % nblk, k0 = 64 * kb, n0 = 32 * nb;
;     const int nr = n0 + (lane & 31); const int sc = MAP == 1 ? src_col_in(nr) : nr;
;     float v[32];
; #pragma unroll
;     for (int i = 0; i < 32; ++i) v[i] = sc >= 0 ? W[(size_t)(k0 + 2 * i + (lane >> 5)) * Nsrc + sc] : 0.f;
; #pragma unroll
;     for (int i = 0; i < 32; ++i) { const int k = k0 + 2 * i + (lane >> 5); float x = v[i] * wscale; if (KS) x *= (k < ksplit ? ksA[k] : ksB[k - ksplit]); scr[(2 * i + (lane >> 5)) * 33 + (lane & 31)] = x; }
;     LDS_WAIT(); asm volatile("" ::: "memory");
;     const int c = lane & 7;
; #pragma unroll
;     for (int j = 0; j < 4; ++j) { const int n = (lane >> 3) + 8 * j; const LAS float* s = scr + (8 * c) * 33 + n;
;         const unsigned long long o = (unsigned long long)pg8::pk4_fp8(s[0 * 33], s[1 * 33], s[2 * 33], s[3 * 33]) | ((unsigned long long)pg8::pk4_fp8(s[4 * 33], s[5 * 33], s[6 * 33], s[7 * 33]) << 32);
;         *(GAS unsigned long long*)(WT + (size_t)(n0 + n) * K + k0 + 8 * c) = o; }
;     LDS_WAIT(); asm volatile("" ::: "memory");
	s_add_i32 s17, s16, 2016
	s_min_u32 s17, s17, 0x7ff
	s_lshr_b32 s18, s17, 5
	s_add_i32 s18, s18, 0
	s_and_b32 s19, s17, 31
	s_lshl_b32 s18, s18, 21
	s_lshl_b32 s19, s19, 9
	s_add_u32 s18, s18, s19
	s_add_u32 s10, s2, s18
	s_addc_u32 s11, s3, 0
	global_load_dwordx4 v[68:71], v126, s[10:11]
	s_add_u32 s10, s10, 0x8000
	s_addc_u32 s11, s11, 0
	global_load_dwordx4 v[72:75], v126, s[10:11]
	s_add_u32 s10, s10, 0x8000
	s_addc_u32 s11, s11, 0
	global_load_dwordx4 v[76:79], v126, s[10:11]
	s_add_u32 s10, s10, 0x8000
	s_addc_u32 s11, s11, 0
	global_load_dwordx4 v[80:83], v126, s[10:11]
	s_add_u32 s10, s10, 0x8000
	s_addc_u32 s11, s11, 0
	global_load_dwordx4 v[84:87], v126, s[10:11]
	s_add_u32 s10, s10, 0x8000
	s_addc_u32 s11, s11, 0
	global_load_dwordx4 v[88:91], v126, s[10:11]
	s_add_u32 s10, s10, 0x8000
	s_addc_u32 s11, s11, 0
	global_load_dwordx4 v[92:95], v126, s[10:11]
	s_add_u32 s10, s10, 0x8000
	s_addc_u32 s11, s11, 0
	global_load_dwordx4 v[96:99], v126, s[10:11]
	s_add_i32 s17, s16, 1824
	s_min_u32 s17, s17, 0x7ff
	s_lshr_b32 s18, s17, 5
	s_add_i32 s18, s18, 0
	s_and_b32 s19, s17, 31
	s_lshl_b32 s19, s19, 21
	s_lshl_b32 s18, s18, 7
	s_add_u32 s18, s18, s19
	s_add_u32 s14, s4, s18
	s_addc_u32 s15, s5, 0
	ds_read_b32 v100, v123
	ds_read_b32 v101, v123 offset:512
	ds_read_b32 v102, v123 offset:1024
	ds_read_b32 v103, v123 offset:1536
	ds_read_b32 v104, v123 offset:2048
	ds_read_b32 v105, v123 offset:2560
	ds_read_b32 v106, v123 offset:3072
	ds_read_b32 v107, v123 offset:3584
	ds_read_b32 v108, v123 offset:4096
	ds_read_b32 v109, v123 offset:4608
	ds_read_b32 v110, v123 offset:5120
	ds_read_b32 v111, v123 offset:5632
	ds_read_b32 v112, v123 offset:6144
	ds_read_b32 v113, v123 offset:6656
	ds_read_b32 v114, v123 offset:7168
	ds_read_b32 v115, v123 offset:7680
	s_waitcnt lgkmcnt(0)
	v_max_f32_e32 v100, v100, v100
	v_max_f32_e32 v101, v101, v101
	v_max_f32_e32 v102, v102, v102
	v_max_f32_e32 v103, v103, v103
	v_max_f32_e32 v104, v104, v104
	v_max_f32_e32 v105, v105, v105
	v_max_f32_e32 v106, v106, v106
	v_max_f32_e32 v107, v107, v107
	v_max_f32_e32 v108, v108, v108
	v_max_f32_e32 v109, v109, v109
	v_max_f32_e32 v110, v110, v110
	v_max_f32_e32 v111, v111, v111
	v_max_f32_e32 v112, v112, v112
	v_max_f32_e32 v113, v113, v113
	v_max_f32_e32 v114, v114, v114
	v_max_f32_e32 v115, v115, v115
	v_med3_f32 v100, v100, s20, v129
	v_med3_f32 v101, v101, s20, v129
	v_med3_f32 v102, v102, s20, v129
	v_med3_f32 v103, v103, s20, v129
	v_med3_f32 v104, v104, s20, v129
	v_med3_f32 v105, v105, s20, v129
	v_med3_f32 v106, v106, s20, v129
	v_med3_f32 v107, v107, s20, v129
	v_med3_f32 v108, v108, s20, v129
	v_med3_f32 v109, v109, s20, v129
	v_med3_f32 v110, v110, s20, v129
	v_med3_f32 v111, v111, s20, v129
	v_med3_f32 v112, v112, s20, v129
	v_med3_f32 v113, v113, s20, v129
	v_med3_f32 v114, v114, s20, v129
	v_med3_f32 v115, v115, s20, v129
	v_mov_b32_e32 v116, 0
	v_mov_b32_e32 v117, 0
	v_mov_b32_e32 v118, 0
	v_mov_b32_e32 v119, 0
	v_cvt_pk_fp8_f32 v116, v100, v101
	v_cvt_pk_fp8_f32 v117, v104, v105
	v_cvt_pk_fp8_f32 v118, v108, v109
	v_cvt_pk_fp8_f32 v119, v112, v113
	v_cvt_pk_fp8_f32 v116, v102, v103 op_sel:[0,0,1]
	v_cvt_pk_fp8_f32 v117, v106, v107 op_sel:[0,0,1]
	v_cvt_pk_fp8_f32 v118, v110, v111 op_sel:[0,0,1]
	v_cvt_pk_fp8_f32 v119, v114, v115 op_sel:[0,0,1]
	s_nop 0
	global_store_dwordx4 v127, v[116:119], s[14:15]
	ds_read_b32 v100, v125
	ds_read_b32 v101, v125 offset:512
	ds_read_b32 v102, v125 offset:1024
	ds_read_b32 v103, v125 offset:1536
	ds_read_b32 v104, v125 offset:2048
	ds_read_b32 v105, v125 offset:2560
	ds_read_b32 v106, v125 offset:3072
	ds_read_b32 v107, v125 offset:3584
	ds_read_b32 v108, v125 offset:4096
	ds_read_b32 v109, v125 offset:4608
	ds_read_b32 v110, v125 offset:5120
	ds_read_b32 v111, v125 offset:5632
	ds_read_b32 v112, v125 offset:6144
	ds_read_b32 v113, v125 offset:6656
	ds_read_b32 v114, v125 offset:7168
	ds_read_b32 v115, v125 offset:7680
	s_waitcnt lgkmcnt(0)
	v_max_f32_e32 v100, v100, v100
	v_max_f32_e32 v101, v101, v101
	v_max_f32_e32 v102, v102, v102
	v_max_f32_e32 v103, v103, v103
	v_max_f32_e32 v104, v104, v104
	v_max_f32_e32 v105, v105, v105
	v_max_f32_e32 v106, v106, v106
	v_max_f32_e32 v107, v107, v107
	v_max_f32_e32 v108, v108, v108
	v_max_f32_e32 v109, v109, v109
	v_max_f32_e32 v110, v110, v110
	v_max_f32_e32 v111, v111, v111
	v_max_f32_e32 v112, v112, v112
	v_max_f32_e32 v113, v113, v113
	v_max_f32_e32 v114, v114, v114
	v_max_f32_e32 v115, v115, v115
	v_med3_f32 v100, v100, s20, v129
	v_med3_f32 v101, v101, s20, v129
	v_med3_f32 v102, v102, s20, v129
	v_med3_f32 v103, v103, s20, v129
	v_med3_f32 v104, v104, s20, v129
	v_med3_f32 v105, v105, s20, v129
	v_med3_f32 v106, v106, s20, v129
	v_med3_f32 v107, v107, s20, v129
	v_med3_f32 v108, v108, s20, v129
	v_med3_f32 v109, v109, s20, v129
	v_med3_f32 v110, v110, s20, v129
	v_med3_f32 v111, v111, s20, v129
	v_med3_f32 v112, v112, s20, v129
	v_med3_f32 v113, v113, s20, v129
	v_med3_f32 v114, v114, s20, v129
	v_med3_f32 v115, v115, s20, v129
	v_mov_b32_e32 v116, 0
	v_mov_b32_e32 v117, 0
	v_mov_b32_e32 v118, 0
	v_mov_b32_e32 v119, 0
	v_cvt_pk_fp8_f32 v116, v100, v101
	v_cvt_pk_fp8_f32 v117, v104, v105
	v_cvt_pk_fp8_f32 v118, v108, v109
	v_cvt_pk_fp8_f32 v119, v112, v113
	v_cvt_pk_fp8_f32 v116, v102, v103 op_sel:[0,0,1]
	v_cvt_pk_fp8_f32 v117, v106, v107 op_sel:[0,0,1]
	v_cvt_pk_fp8_f32 v118, v110, v111 op_sel:[0,0,1]
	v_cvt_pk_fp8_f32 v119, v114, v115 op_sel:[0,0,1]
	s_nop 0
	global_store_dwordx4 v128, v[116:119], s[14:15]
	s_waitcnt vmcnt(12)
	v_mul_f32_e32 v36, 0x43000000, v36
	v_mul_f32_e32 v37, 0x43000000, v37
	v_mul_f32_e32 v38, 0x43000000, v38
	v_mul_f32_e32 v39, 0x43000000, v39
	ds_write_b128 v120, v[36:39]
	v_mul_f32_e32 v40, 0x43000000, v40
	v_mul_f32_e32 v41, 0x43000000, v41
	v_mul_f32_e32 v42, 0x43000000, v42
	v_mul_f32_e32 v43, 0x43000000, v43
	ds_write_b128 v120, v[40:43] offset:1024
	v_mul_f32_e32 v44, 0x43000000, v44
	v_mul_f32_e32 v45, 0x43000000, v45
	v_mul_f32_e32 v46, 0x43000000, v46
	v_mul_f32_e32 v47, 0x43000000, v47
	ds_write_b128 v120, v[44:47] offset:2048
	v_mul_f32_e32 v48, 0x43000000, v48
	v_mul_f32_e32 v49, 0x43000000, v49
	v_mul_f32_e32 v50, 0x43000000, v50
	v_mul_f32_e32 v51, 0x43000000, v51
	ds_write_b128 v120, v[48:51] offset:3072
	v_mul_f32_e32 v52, 0x43000000, v52
	v_mul_f32_e32 v53, 0x43000000, v53
	v_mul_f32_e32 v54, 0x43000000, v54
	v_mul_f32_e32 v55, 0x43000000, v55
	ds_write_b128 v120, v[52:55] offset:4096
	v_mul_f32_e32 v56, 0x43000000, v56
	v_mul_f32_e32 v57, 0x43000000, v57
	v_mul_f32_e32 v58, 0x43000000, v58
	v_mul_f32_e32 v59, 0x43000000, v59
	ds_write_b128 v120, v[56:59] offset:5120
	v_mul_f32_e32 v60, 0x43000000, v60
	v_mul_f32_e32 v61, 0x43000000, v61
	v_mul_f32_e32 v62, 0x43000000, v62
	v_mul_f32_e32 v63, 0x43000000, v63
	ds_write_b128 v120, v[60:63] offset:6144
	v_mul_f32_e32 v64, 0x43000000, v64
	v_mul_f32_e32 v65, 0x43000000, v65
	v_mul_f32_e32 v66, 0x43000000, v66
	v_mul_f32_e32 v67, 0x43000000, v67
	ds_write_b128 v120, v[64:67] offset:7168
	s_waitcnt lgkmcnt(0)
	s_barrier
; #define GAS __attribute__((address_space(1)))
; #define LAS __attribute__((address_space(3)))
; #define LDS_WAIT() asm volatile("s_waitcnt lgkmcnt(0)" ::: "memory")
;     const int pr = item >> 1, kb = 2 * (pr / nblk) + (item & 1), nb = pr % nblk, k0 = 64 * kb, n0 = 32 * nb;
;     const int nr = n0 + (lane & 31); const int sc = MAP == 1 ? src_col_in(nr) : nr;
;     float v[32];
; #pragma unroll
;     for (int i = 0; i < 32; ++i) v[i] = sc >= 0 ? W[(size_t)(k0 + 2 * i + (lane >> 5)) * Nsrc + sc] : 0.f;
; #pragma unroll
;     for (int i = 0; i < 32; ++i) { const int k = k0 + 2 * i + (lane >> 5); float x = v[i] * wscale; if (KS) x *= (k < ksplit ? ksA[k] : ksB[k - ksplit]); scr[(2 * i + (lane >> 5)) * 33 + (lane & 31)] = x; }
;     LDS_WAIT(); asm volatile("" ::: "memory");
;     const int c = lane & 7;
; #pragma unroll
;     for (int j = 0; j < 4; ++j) { const int n = (lane >> 3) + 8 * j; const LAS float* s = scr + (8 * c) * 33 + n;
;         const unsigned long long o = (unsigned long long)pg8::pk4_fp8(s[0 * 33], s[1 * 33], s[2 * 33], s[3 * 33]) | ((unsigned long long)pg8::pk4_fp8(s[4 * 33], s[5 * 33], s[6 * 33], s[7 * 33]) << 32);
;         *(GAS unsigned long long*)(WT + (size_t)(n0 + n) * K + k0 + 8 * c) = o; }
;     LDS_WAIT(); asm volatile("" ::: "memory");
	s_add_i32 s17, s16, 1920
	s_min_u32 s17, s17, 0x7ff
	s_lshr_b32 s18, s17, 5
	s_add_i32 s18, s18, 0
	s_and_b32 s19, s17, 31
	s_lshl_b32 s19, s19, 21
	s_lshl_b32 s18, s18, 7
	s_add_u32 s18, s18, s19
	s_add_u32 s14, s4, s18
	s_addc_u32 s15, s5, 0
	ds_read_b32 v100, v122
	ds_read_b32 v101, v122 offset:512
	ds_read_b32 v102, v122 offset:1024
	ds_read_b32 v103, v122 offset:1536
	ds_read_b32 v104, v122 offset:2048
	ds_read_b32 v105, v122 offset:2560
	ds_read_b32 v106, v122 offset:3072
	ds_read_b32 v107, v122 offset:3584
	ds_read_b32 v108, v122 offset:4096
	ds_read_b32 v109, v122 offset:4608
	ds_read_b32 v110, v122 offset:5120
	ds_read_b32 v111, v122 offset:5632
	ds_read_b32 v112, v122 offset:6144
	ds_read_b32 v113, v122 offset:6656
	ds_read_b32 v114, v122 offset:7168
	ds_read_b32 v115, v122 offset:7680
	s_waitcnt lgkmcnt(0)
	v_max_f32_e32 v100, v100, v100
	v_max_f32_e32 v101, v101, v101
	v_max_f32_e32 v102, v102, v102
	v_max_f32_e32 v103, v103, v103
	v_max_f32_e32 v104, v104, v104
	v_max_f32_e32 v105, v105, v105
	v_max_f32_e32 v106, v106, v106
	v_max_f32_e32 v107, v107, v107
	v_max_f32_e32 v108, v108, v108
	v_max_f32_e32 v109, v109, v109
	v_max_f32_e32 v110, v110, v110
	v_max_f32_e32 v111, v111, v111
	v_max_f32_e32 v112, v112, v112
	v_max_f32_e32 v113, v113, v113
	v_max_f32_e32 v114, v114, v114
	v_max_f32_e32 v115, v115, v115
	v_med3_f32 v100, v100, s20, v129
	v_med3_f32 v101, v101, s20, v129
	v_med3_f32 v102, v102, s20, v129
	v_med3_f32 v103, v103, s20, v129
	v_med3_f32 v104, v104, s20, v129
	v_med3_f32 v105, v105, s20, v129
	v_med3_f32 v106, v106, s20, v129
	v_med3_f32 v107, v107, s20, v129
	v_med3_f32 v108, v108, s20, v129
	v_med3_f32 v109, v109, s20, v129
	v_med3_f32 v110, v110, s20, v129
	v_med3_f32 v111, v111, s20, v129
	v_med3_f32 v112, v112, s20, v129
	v_med3_f32 v113, v113, s20, v129
	v_med3_f32 v114, v114, s20, v129
	v_med3_f32 v115, v115, s20, v129
	v_mov_b32_e32 v116, 0
	v_mov_b32_e32 v117, 0
	v_mov_b32_e32 v118, 0
	v_mov_b32_e32 v119, 0
	v_cvt_pk_fp8_f32 v116, v100, v101
	v_cvt_pk_fp8_f32 v117, v104, v105
	v_cvt_pk_fp8_f32 v118, v108, v109
	v_cvt_pk_fp8_f32 v119, v112, v113
	v_cvt_pk_fp8_f32 v116, v102, v103 op_sel:[0,0,1]
	v_cvt_pk_fp8_f32 v117, v106, v107 op_sel:[0,0,1]
	v_cvt_pk_fp8_f32 v118, v110, v111 op_sel:[0,0,1]
	v_cvt_pk_fp8_f32 v119, v114, v115 op_sel:[0,0,1]
	s_nop 0
	global_store_dwordx4 v127, v[116:119], s[14:15]
	ds_read_b32 v100, v124
	ds_read_b32 v101, v124 offset:512
	ds_read_b32 v102, v124 offset:1024
	ds_read_b32 v103, v124 offset:1536
	ds_read_b32 v104, v124 offset:2048
	ds_read_b32 v105, v124 offset:2560
	ds_read_b32 v106, v124 offset:3072
	ds_read_b32 v107, v124 offset:3584
	ds_read_b32 v108, v124 offset:4096
	ds_read_b32 v109, v124 offset:4608
	ds_read_b32 v110, v124 offset:5120
	ds_read_b32 v111, v124 offset:5632
	ds_read_b32 v112, v124 offset:6144
	ds_read_b32 v113, v124 offset:6656
	ds_read_b32 v114, v124 offset:7168
	ds_read_b32 v115, v124 offset:7680
	s_waitcnt lgkmcnt(0)
	v_max_f32_e32 v100, v100, v100
	v_max_f32_e32 v101, v101, v101
	v_max_f32_e32 v102, v102, v102
	v_max_f32_e32 v103, v103, v103
	v_max_f32_e32 v104, v104, v104
	v_max_f32_e32 v105, v105, v105
	v_max_f32_e32 v106, v106, v106
	v_max_f32_e32 v107, v107, v107
	v_max_f32_e32 v108, v108, v108
	v_max_f32_e32 v109, v109, v109
	v_max_f32_e32 v110, v110, v110
	v_max_f32_e32 v111, v111, v111
	v_max_f32_e32 v112, v112, v112
	v_max_f32_e32 v113, v113, v113
	v_max_f32_e32 v114, v114, v114
	v_max_f32_e32 v115, v115, v115
	v_med3_f32 v100, v100, s20, v129
	v_med3_f32 v101, v101, s20, v129
	v_med3_f32 v102, v102, s20, v129
	v_med3_f32 v103, v103, s20, v129
	v_med3_f32 v104, v104, s20, v129
	v_med3_f32 v105, v105, s20, v129
	v_med3_f32 v106, v106, s20, v129
	v_med3_f32 v107, v107, s20, v129
	v_med3_f32 v108, v108, s20, v129
	v_med3_f32 v109, v109, s20, v129
	v_med3_f32 v110, v110, s20, v129
	v_med3_f32 v111, v111, s20, v129
	v_med3_f32 v112, v112, s20, v129
	v_med3_f32 v113, v113, s20, v129
	v_med3_f32 v114, v114, s20, v129
	v_med3_f32 v115, v115, s20, v129
	v_mov_b32_e32 v116, 0
	v_mov_b32_e32 v117, 0
	v_mov_b32_e32 v118, 0
	v_mov_b32_e32 v119, 0
	v_cvt_pk_fp8_f32 v116, v100, v101
	v_cvt_pk_fp8_f32 v117, v104, v105
	v_cvt_pk_fp8_f32 v118, v108, v109
	v_cvt_pk_fp8_f32 v119, v112, v113
	v_cvt_pk_fp8_f32 v116, v102, v103 op_sel:[0,0,1]
	v_cvt_pk_fp8_f32 v117, v106, v107 op_sel:[0,0,1]
	v_cvt_pk_fp8_f32 v118, v110, v111 op_sel:[0,0,1]
	v_cvt_pk_fp8_f32 v119, v114, v115 op_sel:[0,0,1]
	s_nop 0
	global_store_dwordx4 v128, v[116:119], s[14:15]
	s_waitcnt vmcnt(4)
	v_mul_f32_e32 v68, 0x43000000, v68
	v_mul_f32_e32 v69, 0x43000000, v69
	v_mul_f32_e32 v70, 0x43000000, v70
	v_mul_f32_e32 v71, 0x43000000, v71
	ds_write_b128 v121, v[68:71]
	v_mul_f32_e32 v72, 0x43000000, v72
	v_mul_f32_e32 v73, 0x43000000, v73
	v_mul_f32_e32 v74, 0x43000000, v74
	v_mul_f32_e32 v75, 0x43000000, v75
	ds_write_b128 v121, v[72:75] offset:1024
	v_mul_f32_e32 v76, 0x43000000, v76
	v_mul_f32_e32 v77, 0x43000000, v77
	v_mul_f32_e32 v78, 0x43000000, v78
	v_mul_f32_e32 v79, 0x43000000, v79
	ds_write_b128 v121, v[76:79] offset:2048
	v_mul_f32_e32 v80, 0x43000000, v80
	v_mul_f32_e32 v81, 0x43000000, v81
	v_mul_f32_e32 v82, 0x43000000, v82
	v_mul_f32_e32 v83, 0x43000000, v83
	ds_write_b128 v121, v[80:83] offset:3072
	v_mul_f32_e32 v84, 0x43000000, v84
	v_mul_f32_e32 v85, 0x43000000, v85
	v_mul_f32_e32 v86, 0x43000000, v86
	v_mul_f32_e32 v87, 0x43000000, v87
	ds_write_b128 v121, v[84:87] offset:4096
	v_mul_f32_e32 v88, 0x43000000, v88
	v_mul_f32_e32 v89, 0x43000000, v89
	v_mul_f32_e32 v90, 0x43000000, v90
	v_mul_f32_e32 v91, 0x43000000, v91
	ds_write_b128 v121, v[88:91] offset:5120
	v_mul_f32_e32 v92, 0x43000000, v92
	v_mul_f32_e32 v93, 0x43000000, v93
	v_mul_f32_e32 v94, 0x43000000, v94
	v_mul_f32_e32 v95, 0x43000000, v95
	ds_write_b128 v121, v[92:95] offset:6144
	v_mul_f32_e32 v96, 0x43000000, v96
	v_mul_f32_e32 v97, 0x43000000, v97
	v_mul_f32_e32 v98, 0x43000000, v98
	v_mul_f32_e32 v99, 0x43000000, v99
	ds_write_b128 v121, v[96:99] offset:7168
	s_waitcnt lgkmcnt(0)
	s_barrier
; __device__ __forceinline__ void xcd_barrier(const XcdBarrier& b) {
;     asm volatile("s_waitcnt vmcnt(0)" ::: "memory");
;     __syncthreads();
;     if (threadIdx.x == 0) {
;         unsigned* bar = b.bar;
;         __builtin_amdgcn_s_waitcnt(0);
;         unsigned nloc = b.st[0], nx = b.st[1];
;         if (nloc == 0u) { xcd_barrier_complete(bar, b.x, nloc, nx); b.st[0] = nloc; b.st[1] = nx; }
;         const unsigned old = xb_add(&bar[XB_XSUB(b.x)], 1u);
;         const unsigned gen = old / nloc;
;         if (old + 1u == (gen + 1u) * nloc) {
;             __builtin_amdgcn_fence(__ATOMIC_RELEASE, "agent");
;             asm volatile("s_waitcnt vmcnt(0)" ::: "memory");
;             const unsigned og = xb_add(&bar[XB_TOP], 1u);
;             const unsigned tg = og / nx;
;             if (og + 1u == (tg + 1u) * nx) xb_add(&bar[XB_TOPGEN], 1u);
;             else XB_SPIN(xb_ld(&bar[XB_TOPGEN]) == tg, bar);
;             __builtin_amdgcn_fence(__ATOMIC_ACQUIRE, "agent");
;             xb_add(&bar[XB_XGEN(b.x)], 1u);
;             asm volatile("s_waitcnt vmcnt(0)" ::: "memory");
;         } else {
;             XB_SPIN(xb_ld(&bar[XB_XGEN(b.x)]) == gen, bar);
;             __builtin_amdgcn_fence(__ATOMIC_ACQUIRE, "agent");
;     const int pr = item >> 1, kb = 2 * (pr / nblk) + (item & 1), nb = pr % nblk, k0 = 64 * kb, n0 = 32 * nb;
;     const int nr = n0 + (lane & 31); const int sc = MAP == 1 ? src_col_in(nr) : nr;
;     float v[32];
; #pragma unroll
;     for (int i = 0; i < 32; ++i) v[i] = sc >= 0 ? W[(size_t)(k0 + 2 * i + (lane >> 5)) * Nsrc + sc] : 0.f;
; #pragma unroll
;     for (int i = 0; i < 32; ++i) { const int k = k0 + 2 * i + (lane >> 5); float x = v[i] * wscale; if (KS) x *= (k < ksplit ? ksA[k] : ksB[k - ksplit]); scr[(2 * i + (lane >> 5)) * 33 + (lane & 31)] = x; }
;     LDS_WAIT(); asm volatile("" ::: "memory");
;     const int c = lane & 7;
; #pragma unroll
;     for (int j = 0; j < 4; ++j) { const int n = (lane >> 3) + 8 * j; const LAS float* s = scr + (8 * c) * 33 + n;
;         const unsigned long long o = (unsigned long long)pg8::pk4_fp8(s[0 * 33], s[1 * 33], s[2 * 33], s[3 * 33]) | ((unsigned long long)pg8::pk4_fp8(s[4 * 33], s[5 * 33], s[6 * 33], s[7 * 33]) << 32);
;         *(GAS unsigned long long*)(WT + (size_t)(n0 + n) * K + k0 + 8 * c) = o; }
;     LDS_WAIT(); asm volatile("" ::: "memory");
	s_add_i32 s17, s16, 2016
	s_min_u32 s17, s17, 0x7ff
	s_lshr_b32 s18, s17, 5
	s_add_i32 s18, s18, 0
	s_and_b32 s19, s17, 31
	s_lshl_b32 s19, s19, 21
	s_lshl_b32 s18, s18, 7
	s_add_u32 s18, s18, s19
	s_add_u32 s14, s4, s18
	s_addc_u32 s15, s5, 0
	ds_read_b32 v100, v123
	ds_read_b32 v101, v123 offset:512
	ds_read_b32 v102, v123 offset:1024
	ds_read_b32 v103, v123 offset:1536
	ds_read_b32 v104, v123 offset:2048
	ds_read_b32 v105, v123 offset:2560
	ds_read_b32 v106, v123 offset:3072
	ds_read_b32 v107, v123 offset:3584
	ds_read_b32 v108, v123 offset:4096
	ds_read_b32 v109, v123 offset:4608
	ds_read_b32 v110, v123 offset:5120
	ds_read_b32 v111, v123 offset:5632
	ds_read_b32 v112, v123 offset:6144
	ds_read_b32 v113, v123 offset:6656
	ds_read_b32 v114, v123 offset:7168
	ds_read_b32 v115, v123 offset:7680
	s_waitcnt lgkmcnt(0)
	v_max_f32_e32 v100, v100, v100
	v_max_f32_e32 v101, v101, v101
	v_max_f32_e32 v102, v102, v102
	v_max_f32_e32 v103, v103, v103
	v_max_f32_e32 v104, v104, v104
	v_max_f32_e32 v105, v105, v105
	v_max_f32_e32 v106, v106, v106
	v_max_f32_e32 v107, v107, v107
	v_max_f32_e32 v108, v108, v108
	v_max_f32_e32 v109, v109, v109
	v_max_f32_e32 v110, v110, v110
	v_max_f32_e32 v111, v111, v111
	v_max_f32_e32 v112, v112, v112
	v_max_f32_e32 v113, v113, v113
	v_max_f32_e32 v114, v114, v114
	v_max_f32_e32 v115, v115, v115
	v_med3_f32 v100, v100, s20, v129
	v_med3_f32 v101, v101, s20, v129
	v_med3_f32 v102, v102, s20, v129
	v_med3_f32 v103, v103, s20, v129
	v_med3_f32 v104, v104, s20, v129
	v_med3_f32 v105, v105, s20, v129
	v_med3_f32 v106, v106, s20, v129
	v_med3_f32 v107, v107, s20, v129
	v_med3_f32 v108, v108, s20, v129
	v_med3_f32 v109, v109, s20, v129
	v_med3_f32 v110, v110, s20, v129
	v_med3_f32 v111, v111, s20, v129
	v_med3_f32 v112, v112, s20, v129
	v_med3_f32 v113, v113, s20, v129
	v_med3_f32 v114, v114, s20, v129
	v_med3_f32 v115, v115, s20, v129
	v_mov_b32_e32 v116, 0
	v_mov_b32_e32 v117, 0
	v_mov_b32_e32 v118, 0
	v_mov_b32_e32 v119, 0
	v_cvt_pk_fp8_f32 v116, v100, v101
	v_cvt_pk_fp8_f32 v117, v104, v105
	v_cvt_pk_fp8_f32 v118, v108, v109
	v_cvt_pk_fp8_f32 v119, v112, v113
	v_cvt_pk_fp8_f32 v116, v102, v103 op_sel:[0,0,1]
	v_cvt_pk_fp8_f32 v117, v106, v107 op_sel:[0,0,1]
	v_cvt_pk_fp8_f32 v118, v110, v111 op_sel:[0,0,1]
	v_cvt_pk_fp8_f32 v119, v114, v115 op_sel:[0,0,1]
	s_nop 0
	global_store_dwordx4 v127, v[116:119], s[14:15]
	ds_read_b32 v100, v125
	ds_read_b32 v101, v125 offset:512
	ds_read_b32 v102, v125 offset:1024
	ds_read_b32 v103, v125 offset:1536
	ds_read_b32 v104, v125 offset:2048
	ds_read_b32 v105, v125 offset:2560
	ds_read_b32 v106, v125 offset:3072
	ds_read_b32 v107, v125 offset:3584
	ds_read_b32 v108, v125 offset:4096
	ds_read_b32 v109, v125 offset:4608
	ds_read_b32 v110, v125 offset:5120
	ds_read_b32 v111, v125 offset:5632
	ds_read_b32 v112, v125 offset:6144
	ds_read_b32 v113, v125 offset:6656
	ds_read_b32 v114, v125 offset:7168
	ds_read_b32 v115, v125 offset:7680
	s_waitcnt lgkmcnt(0)
	v_max_f32_e32 v100, v100, v100
	v_max_f32_e32 v101, v101, v101
	v_max_f32_e32 v102, v102, v102
	v_max_f32_e32 v103, v103, v103
	v_max_f32_e32 v104, v104, v104
	v_max_f32_e32 v105, v105, v105
	v_max_f32_e32 v106, v106, v106
	v_max_f32_e32 v107, v107, v107
	v_max_f32_e32 v108, v108, v108
	v_max_f32_e32 v109, v109, v109
	v_max_f32_e32 v110, v110, v110
	v_max_f32_e32 v111, v111, v111
	v_max_f32_e32 v112, v112, v112
	v_max_f32_e32 v113, v113, v113
	v_max_f32_e32 v114, v114, v114
	v_max_f32_e32 v115, v115, v115
	v_med3_f32 v100, v100, s20, v129
	v_med3_f32 v101, v101, s20, v129
	v_med3_f32 v102, v102, s20, v129
	v_med3_f32 v103, v103, s20, v129
	v_med3_f32 v104, v104, s20, v129
	v_med3_f32 v105, v105, s20, v129
	v_med3_f32 v106, v106, s20, v129
	v_med3_f32 v107, v107, s20, v129
	v_med3_f32 v108, v108, s20, v129
	v_med3_f32 v109, v109, s20, v129
	v_med3_f32 v110, v110, s20, v129
	v_med3_f32 v111, v111, s20, v129
	v_med3_f32 v112, v112, s20, v129
	v_med3_f32 v113, v113, s20, v129
	v_med3_f32 v114, v114, s20, v129
	v_med3_f32 v115, v115, s20, v129
	v_mov_b32_e32 v116, 0
	v_mov_b32_e32 v117, 0
	v_mov_b32_e32 v118, 0
	v_mov_b32_e32 v119, 0
	v_cvt_pk_fp8_f32 v116, v100, v101
	v_cvt_pk_fp8_f32 v117, v104, v105
	v_cvt_pk_fp8_f32 v118, v108, v109
	v_cvt_pk_fp8_f32 v119, v112, v113
	v_cvt_pk_fp8_f32 v116, v102, v103 op_sel:[0,0,1]
	v_cvt_pk_fp8_f32 v117, v106, v107 op_sel:[0,0,1]
	v_cvt_pk_fp8_f32 v118, v110, v111 op_sel:[0,0,1]
	v_cvt_pk_fp8_f32 v119, v114, v115 op_sel:[0,0,1]
	s_nop 0
	global_store_dwordx4 v128, v[116:119], s[14:15]
	s_waitcnt vmcnt(0) lgkmcnt(0)
	s_barrier
.Llite0_skip:
	s_mov_b64 s[2:3], 0
	s_getreg_b32 s4, hwreg(HW_REG_XCC_ID, 0, 4)
	s_waitcnt vmcnt(0)
	v_readlane_b32 s6, v253, 44
	v_readlane_b32 s7, v253, 45
	s_waitcnt vmcnt(0)
	s_barrier
	s_and_saveexec_b64 s[0:1], s[6:7]
	s_cbranch_execz .LBB0_578
	v_readlane_b32 s5, v254, 56
	s_waitcnt vmcnt(0) expcnt(0) lgkmcnt(0)
	s_mov_b32 s59, s49
	v_mov_b32_e32 v1, s5
	ds_read_b32 v4, v1
	v_readlane_b32 s5, v254, 57
	s_mov_b32 s58, s48
	s_mov_b64 s[48:49], s[12:13]
	s_mov_b64 s[96:97], s[8:9]
	v_readlane_b32 s8, v253, 35
	v_mov_b32_e32 v1, s5
	v_readlane_b32 s9, v253, 36
	v_readlane_b32 s10, v253, 37
	v_readlane_b32 s11, v253, 38
	v_readlane_b32 s12, v253, 39
	v_readlane_b32 s13, v253, 40
	ds_read_b32 v2, v1
	v_readlane_b32 s14, v253, 41
	v_readlane_b32 s15, v253, 42
	s_mov_b64 s[8:9], s[12:13]
	s_mov_b64 s[10:11], s[14:15]
	s_add_u32 s2, s10, s2
	s_waitcnt lgkmcnt(1)
	v_cmp_ne_u32_e32 vcc, 0, v4
	s_addc_u32 s3, s11, s3
	s_and_b32 s26, s4, 15
	s_cbranch_vccnz .LBB0_697
	v_readlane_b32 s4, v253, 0
	v_readlane_b32 s5, v253, 1
	s_load_dwordx2 s[16:17], s[4:5], 0x4
	s_add_u32 s4, s2, 0x4200
	s_addc_u32 s5, s3, 0
	s_add_u32 s10, s2, 0x4400
	s_addc_u32 s11, s3, 0
	s_waitcnt lgkmcnt(0)
	s_mul_i32 s27, s16, s83
	s_add_u32 s16, s2, 0x4500
	s_mul_i32 s27, s27, s17
	s_addc_u32 s17, s3, 0
	s_add_u32 s18, s2, 0x4600
	s_addc_u32 s19, s3, 0
	s_add_u32 s20, s2, 0x4700
	s_addc_u32 s21, s3, 0
	s_add_u32 s30, s2, 0x4800
	s_addc_u32 s31, s3, 0
	s_add_u32 s34, s2, 0x4900
	s_addc_u32 s35, s3, 0
	s_add_u32 s36, s2, 0x4a00
	s_addc_u32 s37, s3, 0
	s_add_u32 s50, s2, 0x4b00
	s_addc_u32 s51, s3, 0
	s_add_u32 s52, s2, 0x4c00
	s_addc_u32 s53, s3, 0
	s_add_u32 s54, s2, 0x4d00
	s_addc_u32 s55, s3, 0
	s_add_u32 s60, s2, 0x4e00
	s_addc_u32 s61, s3, 0
	s_add_u32 s62, s2, 0x4f00
	s_addc_u32 s63, s3, 0
	s_add_u32 s70, s2, 0x5000
	s_addc_u32 s71, s3, 0
	s_add_u32 s78, s2, 0x5100
	s_addc_u32 s79, s3, 0
	s_add_u32 s90, s2, 0x5200
	s_addc_u32 s91, s3, 0
	s_add_u32 s92, s2, 0x5300
	s_addc_u32 s93, s3, 0
	s_mov_b32 s42, 1
	s_branch .LBB0_685
